# all packed f32 VALU ops (v_pk_mul/add/fma_f32) split into two single f32 ops each, bit-identical math
# speedup vs baseline: 1.0015x; 1.0014x over previous
; __device__ __forceinline__ float row_rstd(const float* ssq, unsigned row) {
;     const float* p = ssq + (size_t)(row * 16u);
;     const f32x4 a = *(const f32x4*)(p), b = *(const f32x4*)(p + 4), c = *(const f32x4*)(p + 8), d = *(const f32x4*)(p + 12);
;     const float s = ((a[0] + a[1]) + (a[2] + a[3])) + ((b[0] + b[1]) + (b[2] + b[3])) + ((c[0] + c[1]) + (c[2] + c[3])) + ((d[0] + d[1]) + (d[2] + d[3]));
;     return 1.0f / sqrtf(s * (1.0f / 1024.0f) + RMS_EPS);
; template <class Sched>
; __device__ __forceinline__ int prep_tables(const Sched& S, PG8_LAS float* tab, const unsigned char* ws, const float* qg, const float* kg  , int tid) {
;     ...
;     { const int pm = (tid >> 8) ? pmB : pmA; if (pm >= 0) tab[tid] = row_rstd((const float*)(ws + E_SSQ), (unsigned)(pm * BM + (tid & 255))); }
.LBB0_40:
	s_movk_i32 s0, 0x100
	v_mov_b32_e32 v0, s12
	v_mov_b32_e32 v2, s29
	v_cmp_gt_u32_e32 vcc, s0, v232
	s_nop 1
	v_cndmask_b32_e32 v0, v0, v2, vcc
	v_cmp_gt_i32_e32 vcc, 0, v0
	s_and_saveexec_b64 s[0:1], vcc
	s_xor_b64 s[0:1], exec, s[0:1]
	v_lshlrev_b32_e32 v2, 4, v232
	s_andn2_saveexec_b64 s[8:9], s[0:1]
	s_cbranch_execz .LBB0_44
	v_lshlrev_b32_e32 v2, 4, v232
	v_and_b32_e32 v3, 0xff0, v2
	v_lshl_or_b32 v0, v0, 12, v3
	v_lshl_add_u64 v[4:5], v[0:1], 2, s[74:75]
	s_mov_b64 s[0:1], 0x3400000
	v_lshl_add_u64 v[16:17], v[4:5], 0, s[0:1]
	v_add_co_u32_e32 v4, vcc, 0x3400000, v4
	s_mov_b32 s0, 0xf800000
	s_nop 0
	v_addc_co_u32_e32 v5, vcc, 0, v5, vcc
	flat_load_dwordx4 v[4:7], v[4:5]
	s_nop 0
	flat_load_dwordx4 v[8:11], v[16:17] offset:16
	flat_load_dwordx4 v[12:15], v[16:17] offset:32
	s_nop 0
	flat_load_dwordx4 v[16:19], v[16:17] offset:48
	s_waitcnt vmcnt(0) lgkmcnt(0)
	v_mov_b32_e32 v20, v5
	v_mov_b32_e32 v21, v6
	v_mov_b32_e32 v5, v7
	v_mov_b32_e32 v6, v9
	v_mov_b32_e32 v7, v10
	v_mov_b32_e32 v9, v11
	v_add_f32_e32 v4, v20, v4
	v_add_f32_e32 v5, v21, v5
	v_add_f32_e32 v6, v6, v8
	v_add_f32_e32 v7, v7, v9
	v_pk_add_f32 v[4:5], v[4:5], v[4:5] op_sel:[0,1] op_sel_hi:[1,0]
	v_pk_add_f32 v[6:7], v[6:7], v[6:7] op_sel:[0,1] op_sel_hi:[1,0]
	v_add_f32_e32 v8, v12, v13
	v_add_f32_e32 v10, v14, v15
	v_mov_b32_e32 v5, v16
	v_mov_b32_e32 v7, v17
	v_mov_b32_e32 v9, v18
	v_mov_b32_e32 v11, v19
	v_add_f32_e32 v4, v4, v6
	v_add_f32_e32 v5, v5, v7
	v_add_f32_e32 v6, v8, v10
	v_add_f32_e32 v7, v9, v11
	s_nop 0
	v_add_f32_e32 v4, v4, v6
	v_add_f32_e32 v5, v5, v7
	s_nop 0
	v_add_f32_e32 v0, v4, v5
	v_fmamk_f32 v0, v0, 0x3a800000, v215
	v_cmp_gt_f32_e32 vcc, s0, v0
	v_mul_f32_e32 v3, 0x4f800000, v0
	s_nop 0
	v_cndmask_b32_e32 v0, v0, v3, vcc
	v_sqrt_f32_e32 v3, v0
	s_nop 0
	v_add_u32_e32 v4, -1, v3
	v_fma_f32 v5, -v4, v3, v0
	v_cmp_ge_f32_e64 s[0:1], 0, v5
	v_add_u32_e32 v5, 1, v3
	s_nop 0
	v_cndmask_b32_e64 v4, v3, v4, s[0:1]
	v_fma_f32 v3, -v5, v3, v0
	v_cmp_lt_f32_e64 s[0:1], 0, v3
	s_nop 1
	v_cndmask_b32_e64 v3, v4, v5, s[0:1]
	v_mul_f32_e32 v4, 0x37800000, v3
	v_cndmask_b32_e32 v3, v3, v4, vcc
	v_cmp_class_f32_e32 vcc, v0, v216
	s_nop 1
	v_cndmask_b32_e32 v0, v3, v0, vcc
	v_div_scale_f32 v3, s[0:1], v0, v0, 1.0
	v_rcp_f32_e32 v4, v3
	s_nop 0
	v_fma_f32 v5, -v3, v4, 1.0
	v_fmac_f32_e32 v4, v5, v4
	v_div_scale_f32 v5, vcc, 1.0, v0, 1.0
	v_mul_f32_e32 v6, v5, v4
	v_fma_f32 v7, -v3, v6, v5
	v_fmac_f32_e32 v6, v7, v4
	v_fma_f32 v3, -v3, v6, v5
	v_div_fmas_f32 v3, v3, v4, v6
	v_div_fixup_f32 v0, v3, v0, 1.0
	v_lshl_add_u32 v3, v232, 2, v238
	ds_write_b32 v3, v0

; #define PG8_GAS __attribute__((address_space(1)))
; #define PG8_PACK8(y0, y1) (u32x4){cvt_pk_bf16((y0)[0], (y0)[1]), cvt_pk_bf16((y0)[2], (y0)[3]), cvt_pk_bf16((y1)[0], (y1)[1]), cvt_pk_bf16((y1)[2], (y1)[3])}
;     __device__ __forceinline__ void operator()(const f32x4 (&acc)[2][2][4][2], const Unit& u, int ui, int wr, int wc, int fr, int fq) const {
;     ...
; #pragma unroll
;         for (int ai = 0; ai < 2; ++ai)
; #pragma unroll
;             for (int m = 0; m < 4; ++m) {
;                 const unsigned row = row0 + ai * HALF + m * 16; const float rs = rsv[ai][m];
; #pragma unroll
;                 for (int bj = 0; bj < 2; ++bj) {
;                     f32x4 y0 = acc[ai][bj][m][0] * rs, y1 = acc[ai][bj][m][1] * rs;
; #pragma unroll
;                     for (int e = 0; e < 4; ++e) { const float a = fmaxf(y0[e], 0.f), b = fmaxf(y1[e], 0.f); y0[e] = a * a; y1[e] = b * b; }
;                     const u32x4 hw = PG8_PACK8(y0, y1);
;     ...
;                     if (probe_mode == 1) { asm volatile("" :: "v"(hw)); } else
;     ...
;                     *(PG8_GAS u32x4*)((PG8_GAS unsigned char*)ws + E_QKVO + (size_t)((unsigned)(u.pm >> 4) * (24u << 20) + (unsigned)(u.pn >> 2) * (8u << 20) + row * 2048u + (colp + bj * HALF) * 2u)) = hw;
.LBB0_64:
	s_lshl_b32 s13, s51, 9
	s_cmp_eq_u32 s20, s29
	s_cselect_b32 s15, 0, 0x400
	v_add_u32_e32 v140, s15, v145
	ds_read2_b32 v[164:165], v140 offset1:16
	ds_read2_b32 v[166:167], v140 offset0:32 offset1:48
	ds_read2_b32 v[142:143], v140 offset0:128 offset1:144
	ds_read2_b32 v[140:141], v140 offset0:160 offset1:176
	s_lshl_b32 s22, s51, 21
	s_lshr_b32 s15, s20, 4
	s_and_b32 s22, s22, 0xff800000
	s_lshl_b32 s20, s20, 19
	s_waitcnt lgkmcnt(0)
	v_mul_f32_e32 v122, v122, v164
	v_mul_f32_e32 v123, v123, v164
	s_add_i32 s22, s22, s20
	v_mul_f32_e32 v126, v126, v164
	v_mul_f32_e32 v127, v127, v164
	v_mul_f32_e32 v124, v124, v164
	v_mul_f32_e32 v125, v125, v164
	v_max_f32_e32 v122, 0, v122
	s_and_b32 s13, s13, 0x600
	v_add_u32_e32 v163, s22, v146
	v_mul_f32_e32 v128, v128, v164
	v_mul_f32_e32 v129, v129, v164
	v_mul_f32_e32 v168, v122, v122
	v_max_f32_e32 v122, 0, v127
	v_max_f32_e32 v123, 0, v123
	v_max_f32_e32 v124, 0, v124
	s_mul_i32 s15, s15, 0x1800000
	v_or_b32_e32 v163, s13, v163
	v_max_f32_e32 v126, 0, v126
	v_mul_f32_e32 v122, v122, v122
	v_mul_f32_e32 v127, v123, v123
	v_max_f32_e32 v123, 0, v128
	v_mul_f32_e32 v128, v124, v124
	v_max_f32_e32 v124, 0, v129
	v_max_f32_e32 v125, 0, v125
	v_mul_f32_e32 v114, v114, v164
	v_mul_f32_e32 v115, v115, v164
	v_add_u32_e32 v163, s15, v163
	v_mul_f32_e32 v126, v126, v126
	v_mul_f32_e32 v123, v123, v123
	v_mul_f32_e32 v124, v124, v124
	v_mul_f32_e32 v125, v125, v125
	v_cvt_pk_bf16_f32 v122, v126, v122
	v_mul_f32_e32 v120, v120, v164
	v_mul_f32_e32 v121, v121, v164
	v_mul_f32_e32 v118, v118, v164
	v_mul_f32_e32 v119, v119, v164
	v_mul_f32_e32 v116, v116, v164
	v_mul_f32_e32 v117, v117, v164
	v_max_f32_e32 v114, 0, v114
	v_max_f32_e32 v115, 0, v115
	v_cvt_pk_bf16_f32 v123, v123, v124
	v_cvt_pk_bf16_f32 v124, v168, v127
	v_cvt_pk_bf16_f32 v125, v128, v125
	global_store_dwordx4 v163, v[122:125], s[10:11] nt
	v_max_f32_e32 v118, 0, v118
	v_max_f32_e32 v116, 0, v116
	v_mul_f32_e32 v122, v114, v114
	v_max_f32_e32 v114, 0, v119
	v_mul_f32_e32 v119, v115, v115
	v_max_f32_e32 v115, 0, v120
	v_mul_f32_e32 v118, v118, v118
	v_mul_f32_e32 v114, v114, v114
	v_mul_f32_e32 v115, v115, v115
	v_mul_f32_e32 v120, v116, v116
	v_max_f32_e32 v116, 0, v121
	v_max_f32_e32 v117, 0, v117
	v_mul_f32_e32 v116, v116, v116
	v_mul_f32_e32 v117, v117, v117
	v_cvt_pk_bf16_f32 v114, v118, v114
	v_cvt_pk_bf16_f32 v115, v115, v116
	v_or_b32_e32 v118, 0x100, v163
	v_cvt_pk_bf16_f32 v116, v122, v119
	v_cvt_pk_bf16_f32 v117, v120, v117
	global_store_dwordx4 v118, v[114:117], s[10:11] nt
	v_mul_f32_e32 v90, v90, v166
	v_mul_f32_e32 v91, v91, v166
	v_mul_f32_e32 v94, v94, v166
	v_mul_f32_e32 v95, v95, v166
	v_or_b32_e32 v115, 0x8000, v163
	v_mov_b32_e32 v114, v165
	v_mul_f32_e32 v106, v106, v114
	v_mul_f32_e32 v107, v107, v114
	v_mul_f32_e32 v110, v110, v114
	v_mul_f32_e32 v111, v111, v114
	v_mul_f32_e32 v108, v108, v114
	v_mul_f32_e32 v109, v109, v114
	v_max_f32_e32 v106, 0, v106
	v_mul_f32_e32 v112, v112, v114
	v_mul_f32_e32 v113, v113, v114
	v_mul_f32_e32 v116, v106, v106
	v_max_f32_e32 v106, 0, v111
	v_max_f32_e32 v107, 0, v107
	v_max_f32_e32 v108, 0, v108
	v_max_f32_e32 v110, 0, v110
	v_mul_f32_e32 v106, v106, v106
	v_mul_f32_e32 v111, v107, v107
	v_max_f32_e32 v107, 0, v112
	v_mul_f32_e32 v112, v108, v108
	v_max_f32_e32 v108, 0, v113
	v_max_f32_e32 v109, 0, v109
	v_mul_f32_e32 v98, v98, v114
	v_mul_f32_e32 v99, v99, v114
	v_mul_f32_e32 v110, v110, v110
	v_mul_f32_e32 v107, v107, v107
	v_mul_f32_e32 v108, v108, v108
	v_mul_f32_e32 v109, v109, v109
	v_cvt_pk_bf16_f32 v106, v110, v106
	v_mul_f32_e32 v104, v104, v114
	v_mul_f32_e32 v105, v105, v114
	v_mul_f32_e32 v102, v102, v114
	v_mul_f32_e32 v103, v103, v114
	v_mul_f32_e32 v100, v100, v114
	v_mul_f32_e32 v101, v101, v114
	v_max_f32_e32 v98, 0, v98
	v_max_f32_e32 v99, 0, v99
	v_cvt_pk_bf16_f32 v107, v107, v108
	v_cvt_pk_bf16_f32 v108, v116, v111
	v_cvt_pk_bf16_f32 v109, v112, v109
	global_store_dwordx4 v115, v[106:109], s[10:11] nt
	v_max_f32_e32 v102, 0, v102
	v_max_f32_e32 v100, 0, v100
	v_mul_f32_e32 v106, v98, v98
	v_max_f32_e32 v98, 0, v103
	v_mul_f32_e32 v103, v99, v99
	v_max_f32_e32 v99, 0, v104
	v_mul_f32_e32 v102, v102, v102
	v_mul_f32_e32 v98, v98, v98
	v_mul_f32_e32 v99, v99, v99
	v_mul_f32_e32 v104, v100, v100
	v_max_f32_e32 v100, 0, v105
	v_max_f32_e32 v101, 0, v101
	v_mul_f32_e32 v100, v100, v100
	v_mul_f32_e32 v101, v101, v101
	v_cvt_pk_bf16_f32 v98, v102, v98
	v_cvt_pk_bf16_f32 v99, v99, v100
	v_or_b32_e32 v102, 0x8100, v163
	v_mul_f32_e32 v92, v92, v166
	v_mul_f32_e32 v93, v93, v166
	v_max_f32_e32 v90, 0, v90
	v_cvt_pk_bf16_f32 v100, v106, v103
	v_cvt_pk_bf16_f32 v101, v104, v101
	global_store_dwordx4 v102, v[98:101], s[10:11] nt
	v_mul_f32_e32 v96, v96, v166
	v_mul_f32_e32 v97, v97, v166
	v_max_f32_e32 v91, 0, v91
	v_mul_f32_e32 v99, v90, v90
	v_max_f32_e32 v90, 0, v95
	v_max_f32_e32 v92, 0, v92
	v_max_f32_e32 v94, 0, v94
	v_mul_f32_e32 v90, v90, v90
	v_mul_f32_e32 v95, v91, v91
	v_max_f32_e32 v91, 0, v96
	v_mul_f32_e32 v96, v92, v92
	v_max_f32_e32 v92, 0, v97
	v_max_f32_e32 v93, 0, v93
	v_mul_f32_e32 v82, v82, v166
	v_mul_f32_e32 v83, v83, v166
	v_or_b32_e32 v98, 0x10000, v163
	v_mul_f32_e32 v94, v94, v94
	v_mul_f32_e32 v91, v91, v91
	v_mul_f32_e32 v92, v92, v92
	v_mul_f32_e32 v93, v93, v93
	v_cvt_pk_bf16_f32 v90, v94, v90
	v_mul_f32_e32 v88, v88, v166
	v_mul_f32_e32 v89, v89, v166
	v_mul_f32_e32 v86, v86, v166
	v_mul_f32_e32 v87, v87, v166
	v_mul_f32_e32 v84, v84, v166
	v_mul_f32_e32 v85, v85, v166
	v_max_f32_e32 v82, 0, v82
	v_max_f32_e32 v83, 0, v83
	v_cvt_pk_bf16_f32 v91, v91, v92
	v_cvt_pk_bf16_f32 v92, v99, v95
	v_cvt_pk_bf16_f32 v93, v96, v93
; #define PG8_GAS __attribute__((address_space(1)))
; #define PG8_PACK8(y0, y1) (u32x4){cvt_pk_bf16((y0)[0], (y0)[1]), cvt_pk_bf16((y0)[2], (y0)[3]), cvt_pk_bf16((y1)[0], (y1)[1]), cvt_pk_bf16((y1)[2], (y1)[3])}
;     __device__ __forceinline__ void operator()(const f32x4 (&acc)[2][2][4][2], const Unit& u, int ui, int wr, int wc, int fr, int fq) const {
;     ...
; #pragma unroll
;         for (int ai = 0; ai < 2; ++ai)
; #pragma unroll
;             for (int m = 0; m < 4; ++m) {
;                 const unsigned row = row0 + ai * HALF + m * 16; const float rs = rsv[ai][m];
; #pragma unroll
;                 for (int bj = 0; bj < 2; ++bj) {
;                     f32x4 y0 = acc[ai][bj][m][0] * rs, y1 = acc[ai][bj][m][1] * rs;
; #pragma unroll
;                     for (int e = 0; e < 4; ++e) { const float a = fmaxf(y0[e], 0.f), b = fmaxf(y1[e], 0.f); y0[e] = a * a; y1[e] = b * b; }
;                     const u32x4 hw = PG8_PACK8(y0, y1);
;     ...
;                     if (probe_mode == 1) { asm volatile("" :: "v"(hw)); } else
;     ...
;                     *(PG8_GAS u32x4*)((PG8_GAS unsigned char*)ws + E_QKVO + (size_t)((unsigned)(u.pm >> 4) * (24u << 20) + (unsigned)(u.pn >> 2) * (8u << 20) + row * 2048u + (colp + bj * HALF) * 2u)) = hw;
	global_store_dwordx4 v98, v[90:93], s[10:11] nt
	v_max_f32_e32 v86, 0, v86
	v_max_f32_e32 v84, 0, v84
	v_mul_f32_e32 v90, v82, v82
	v_max_f32_e32 v82, 0, v87
	v_mul_f32_e32 v87, v83, v83
	v_max_f32_e32 v83, 0, v88
	v_mul_f32_e32 v86, v86, v86
	v_mul_f32_e32 v82, v82, v82
	v_mul_f32_e32 v83, v83, v83
	v_mul_f32_e32 v88, v84, v84
	v_max_f32_e32 v84, 0, v89
	v_max_f32_e32 v85, 0, v85
	v_mul_f32_e32 v84, v84, v84
	v_mul_f32_e32 v85, v85, v85
	v_cvt_pk_bf16_f32 v82, v86, v82
	v_cvt_pk_bf16_f32 v83, v83, v84
	v_or_b32_e32 v86, 0x10100, v163
	v_cvt_pk_bf16_f32 v84, v90, v87
	v_cvt_pk_bf16_f32 v85, v88, v85
	global_store_dwordx4 v86, v[82:85], s[10:11] nt
	v_mul_f32_e32 v58, v58, v142
	v_mul_f32_e32 v59, v59, v142
	v_mul_f32_e32 v62, v62, v142
	v_mul_f32_e32 v63, v63, v142
	v_or_b32_e32 v83, 0x18000, v163
	v_mov_b32_e32 v82, v167
	v_mul_f32_e32 v74, v74, v82
	v_mul_f32_e32 v75, v75, v82
	v_mul_f32_e32 v78, v78, v82
	v_mul_f32_e32 v79, v79, v82
	v_mul_f32_e32 v76, v76, v82
	v_mul_f32_e32 v77, v77, v82
	v_max_f32_e32 v74, 0, v74
	v_mul_f32_e32 v80, v80, v82
	v_mul_f32_e32 v81, v81, v82
	v_mul_f32_e32 v84, v74, v74
	v_max_f32_e32 v74, 0, v79
	v_max_f32_e32 v75, 0, v75
	v_max_f32_e32 v76, 0, v76
	v_max_f32_e32 v78, 0, v78
	v_mul_f32_e32 v74, v74, v74
	v_mul_f32_e32 v79, v75, v75
	v_max_f32_e32 v75, 0, v80
	v_mul_f32_e32 v80, v76, v76
	v_max_f32_e32 v76, 0, v81
	v_max_f32_e32 v77, 0, v77
	v_mul_f32_e32 v66, v66, v82
	v_mul_f32_e32 v67, v67, v82
	v_mul_f32_e32 v78, v78, v78
	v_mul_f32_e32 v75, v75, v75
	v_mul_f32_e32 v76, v76, v76
	v_mul_f32_e32 v77, v77, v77
	v_cvt_pk_bf16_f32 v74, v78, v74
	v_mul_f32_e32 v72, v72, v82
	v_mul_f32_e32 v73, v73, v82
	v_mul_f32_e32 v70, v70, v82
	v_mul_f32_e32 v71, v71, v82
	v_mul_f32_e32 v68, v68, v82
	v_mul_f32_e32 v69, v69, v82
	v_max_f32_e32 v66, 0, v66
	v_max_f32_e32 v67, 0, v67
	v_cvt_pk_bf16_f32 v75, v75, v76
	v_cvt_pk_bf16_f32 v76, v84, v79
	v_cvt_pk_bf16_f32 v77, v80, v77
	global_store_dwordx4 v83, v[74:77], s[10:11]
	v_max_f32_e32 v70, 0, v70
	v_max_f32_e32 v68, 0, v68
	v_mul_f32_e32 v74, v66, v66
	v_max_f32_e32 v66, 0, v71
	v_mul_f32_e32 v71, v67, v67
	v_max_f32_e32 v67, 0, v72
	v_mul_f32_e32 v70, v70, v70
	v_mul_f32_e32 v66, v66, v66
	v_mul_f32_e32 v67, v67, v67
	v_mul_f32_e32 v72, v68, v68
	v_max_f32_e32 v68, 0, v73
	v_max_f32_e32 v69, 0, v69
	v_mul_f32_e32 v68, v68, v68
	v_mul_f32_e32 v69, v69, v69
	v_cvt_pk_bf16_f32 v66, v70, v66
	v_cvt_pk_bf16_f32 v67, v67, v68
	v_or_b32_e32 v70, 0x18100, v163
	v_mul_f32_e32 v60, v60, v142
	v_mul_f32_e32 v61, v61, v142
	v_max_f32_e32 v58, 0, v58
	v_cvt_pk_bf16_f32 v68, v74, v71
	v_cvt_pk_bf16_f32 v69, v72, v69
	global_store_dwordx4 v70, v[66:69], s[10:11]
	v_mul_f32_e32 v64, v64, v142
	v_mul_f32_e32 v65, v65, v142
	v_max_f32_e32 v59, 0, v59
	v_mul_f32_e32 v67, v58, v58
	v_max_f32_e32 v58, 0, v63
	v_max_f32_e32 v60, 0, v60
	v_max_f32_e32 v62, 0, v62
	v_mul_f32_e32 v58, v58, v58
	v_mul_f32_e32 v63, v59, v59
	v_max_f32_e32 v59, 0, v64
	v_mul_f32_e32 v64, v60, v60
	v_max_f32_e32 v60, 0, v65
	v_max_f32_e32 v61, 0, v61
	v_mul_f32_e32 v50, v50, v142
	v_mul_f32_e32 v51, v51, v142
	v_add_u32_e32 v66, 0x40000, v163
	v_mul_f32_e32 v62, v62, v62
	v_mul_f32_e32 v59, v59, v59
	v_mul_f32_e32 v60, v60, v60
	v_mul_f32_e32 v61, v61, v61
	v_cvt_pk_bf16_f32 v58, v62, v58
	v_mul_f32_e32 v56, v56, v142
	v_mul_f32_e32 v57, v57, v142
	v_mul_f32_e32 v54, v54, v142
	v_mul_f32_e32 v55, v55, v142
	v_mul_f32_e32 v52, v52, v142
	v_mul_f32_e32 v53, v53, v142
	v_max_f32_e32 v50, 0, v50
	v_max_f32_e32 v51, 0, v51
	v_cvt_pk_bf16_f32 v59, v59, v60
	v_cvt_pk_bf16_f32 v60, v67, v63
	v_cvt_pk_bf16_f32 v61, v64, v61
	global_store_dwordx4 v66, v[58:61], s[10:11]
	v_max_f32_e32 v54, 0, v54
	v_max_f32_e32 v52, 0, v52
	v_mul_f32_e32 v58, v50, v50
	v_max_f32_e32 v50, 0, v55
	v_mul_f32_e32 v55, v51, v51
	v_max_f32_e32 v51, 0, v56
	v_mul_f32_e32 v54, v54, v54
	v_mul_f32_e32 v50, v50, v50
	v_mul_f32_e32 v51, v51, v51
	v_mul_f32_e32 v56, v52, v52
	v_max_f32_e32 v52, 0, v57
	v_max_f32_e32 v53, 0, v53
	v_mul_f32_e32 v52, v52, v52
	v_mul_f32_e32 v53, v53, v53
	v_cvt_pk_bf16_f32 v50, v54, v50
	v_cvt_pk_bf16_f32 v51, v51, v52
	v_add_u32_e32 v54, 0x40100, v163
	v_cvt_pk_bf16_f32 v52, v58, v55
	v_cvt_pk_bf16_f32 v53, v56, v53
	global_store_dwordx4 v54, v[50:53], s[10:11]
	v_mul_f32_e32 v26, v26, v140
	v_mul_f32_e32 v27, v27, v140
	v_mul_f32_e32 v30, v30, v140
	v_mul_f32_e32 v31, v31, v140
	v_add_u32_e32 v51, 0x48000, v163
	v_mov_b32_e32 v50, v143
	v_mul_f32_e32 v42, v42, v50
	v_mul_f32_e32 v43, v43, v50
	v_mul_f32_e32 v46, v46, v50
	v_mul_f32_e32 v47, v47, v50
	v_mul_f32_e32 v44, v44, v50
	v_mul_f32_e32 v45, v45, v50
	v_max_f32_e32 v42, 0, v42
	v_mul_f32_e32 v48, v48, v50
	v_mul_f32_e32 v49, v49, v50
	v_mul_f32_e32 v52, v42, v42
	v_max_f32_e32 v42, 0, v47
	v_max_f32_e32 v43, 0, v43
	v_max_f32_e32 v44, 0, v44
	v_max_f32_e32 v46, 0, v46
	v_mul_f32_e32 v42, v42, v42
	v_mul_f32_e32 v47, v43, v43
; #define PG8_GAS __attribute__((address_space(1)))
; #define PG8_PACK8(y0, y1) (u32x4){cvt_pk_bf16((y0)[0], (y0)[1]), cvt_pk_bf16((y0)[2], (y0)[3]), cvt_pk_bf16((y1)[0], (y1)[1]), cvt_pk_bf16((y1)[2], (y1)[3])}
; #define PG8_BAR __builtin_amdgcn_s_barrier()
;     __device__ __forceinline__ void operator()(const f32x4 (&acc)[2][2][4][2], const Unit& u, int ui, int wr, int wc, int fr, int fq) const {
;     ...
;                 for (int bj = 0; bj < 2; ++bj) {
;                     f32x4 y0 = acc[ai][bj][m][0] * rs, y1 = acc[ai][bj][m][1] * rs;
; #pragma unroll
;                     for (int e = 0; e < 4; ++e) { const float a = fmaxf(y0[e], 0.f), b = fmaxf(y1[e], 0.f); y0[e] = a * a; y1[e] = b * b; }
;                     const u32x4 hw = PG8_PACK8(y0, y1);
;     ...
;                     if (probe_mode == 1) { asm volatile("" :: "v"(hw)); } else
;     ...
;                     *(PG8_GAS u32x4*)((PG8_GAS unsigned char*)ws + E_QKVO + (size_t)((unsigned)(u.pm >> 4) * (24u << 20) + (unsigned)(u.pn >> 2) * (8u << 20) + row * 2048u + (colp + bj * HALF) * 2u)) = hw;
; template <class Epi, class Sched, bool ALIGN_EPI = false, bool SP2 = false>
; __device__ __forceinline__ void gemm_phase(PG8_LAS unsigned char* lds, const Gemm g, const Sched& S, const Epi& E, const int tid) {
;     ...
;         if (!has_next) break;
; #pragma unroll
;         for (int a = 0; a < 2; ++a)
; #pragma unroll
;             for (int b = 0; b < 2; ++b)
; #pragma unroll
;                 for (int m = 0; m < 4; ++m)
; #pragma unroll
;                     for (int n = 0; n < 2; ++n) acc[a][b][m][n] = (f32x4){0.f, 0.f, 0.f, 0.f};
;         cur = nxt; cA = nA; cB = nB; ++ui;
;         if constexpr (ALIGN_EPI) { if (wr == 1) PG8_BAR; }
	v_max_f32_e32 v43, 0, v48
	v_mul_f32_e32 v48, v44, v44
	v_max_f32_e32 v44, 0, v49
	v_max_f32_e32 v45, 0, v45
	v_mul_f32_e32 v34, v34, v50
	v_mul_f32_e32 v35, v35, v50
	v_mul_f32_e32 v46, v46, v46
	v_mul_f32_e32 v43, v43, v43
	v_mul_f32_e32 v44, v44, v44
	v_mul_f32_e32 v45, v45, v45
	v_cvt_pk_bf16_f32 v42, v46, v42
	v_mul_f32_e32 v40, v40, v50
	v_mul_f32_e32 v41, v41, v50
	v_mul_f32_e32 v38, v38, v50
	v_mul_f32_e32 v39, v39, v50
	v_mul_f32_e32 v36, v36, v50
	v_mul_f32_e32 v37, v37, v50
	v_max_f32_e32 v34, 0, v34
	v_max_f32_e32 v35, 0, v35
	v_cvt_pk_bf16_f32 v43, v43, v44
	v_cvt_pk_bf16_f32 v44, v52, v47
	v_cvt_pk_bf16_f32 v45, v48, v45
	global_store_dwordx4 v51, v[42:45], s[10:11]
	v_max_f32_e32 v38, 0, v38
	v_max_f32_e32 v36, 0, v36
	v_mul_f32_e32 v42, v34, v34
	v_max_f32_e32 v34, 0, v39
	v_mul_f32_e32 v39, v35, v35
	v_max_f32_e32 v35, 0, v40
	v_mul_f32_e32 v38, v38, v38
	v_mul_f32_e32 v34, v34, v34
	v_mul_f32_e32 v35, v35, v35
	v_mul_f32_e32 v40, v36, v36
	v_max_f32_e32 v36, 0, v41
	v_max_f32_e32 v37, 0, v37
	v_mul_f32_e32 v36, v36, v36
	v_mul_f32_e32 v37, v37, v37
	v_cvt_pk_bf16_f32 v34, v38, v34
	v_cvt_pk_bf16_f32 v35, v35, v36
	v_add_u32_e32 v38, 0x48100, v163
	v_mul_f32_e32 v28, v28, v140
	v_mul_f32_e32 v29, v29, v140
	v_max_f32_e32 v26, 0, v26
	v_cvt_pk_bf16_f32 v36, v42, v39
	v_cvt_pk_bf16_f32 v37, v40, v37
	global_store_dwordx4 v38, v[34:37], s[10:11]
	v_mul_f32_e32 v32, v32, v140
	v_mul_f32_e32 v33, v33, v140
	v_max_f32_e32 v27, 0, v27
	v_mul_f32_e32 v35, v26, v26
	v_max_f32_e32 v26, 0, v31
	v_max_f32_e32 v28, 0, v28
	v_max_f32_e32 v30, 0, v30
	v_mul_f32_e32 v26, v26, v26
	v_mul_f32_e32 v31, v27, v27
	v_max_f32_e32 v27, 0, v32
	v_mul_f32_e32 v32, v28, v28
	v_max_f32_e32 v28, 0, v33
	v_max_f32_e32 v29, 0, v29
	v_mul_f32_e32 v18, v18, v140
	v_mul_f32_e32 v19, v19, v140
	v_add_u32_e32 v34, 0x50000, v163
	v_mul_f32_e32 v30, v30, v30
	v_mul_f32_e32 v27, v27, v27
	v_mul_f32_e32 v28, v28, v28
	v_mul_f32_e32 v29, v29, v29
	v_cvt_pk_bf16_f32 v26, v30, v26
	v_mul_f32_e32 v24, v24, v140
	v_mul_f32_e32 v25, v25, v140
	v_mul_f32_e32 v22, v22, v140
	v_mul_f32_e32 v23, v23, v140
	v_mul_f32_e32 v20, v20, v140
	v_mul_f32_e32 v21, v21, v140
	v_max_f32_e32 v18, 0, v18
	v_max_f32_e32 v19, 0, v19
	v_cvt_pk_bf16_f32 v27, v27, v28
	v_cvt_pk_bf16_f32 v28, v35, v31
	v_cvt_pk_bf16_f32 v29, v32, v29
	global_store_dwordx4 v34, v[26:29], s[10:11]
	v_max_f32_e32 v22, 0, v22
	v_max_f32_e32 v20, 0, v20
	v_mul_f32_e32 v26, v18, v18
	v_max_f32_e32 v18, 0, v23
	v_mul_f32_e32 v23, v19, v19
	v_max_f32_e32 v19, 0, v24
	v_mul_f32_e32 v22, v22, v22
	v_mul_f32_e32 v18, v18, v18
	v_mul_f32_e32 v19, v19, v19
	v_mul_f32_e32 v24, v20, v20
	v_max_f32_e32 v20, 0, v25
	v_max_f32_e32 v21, 0, v21
	v_mul_f32_e32 v20, v20, v20
	v_mul_f32_e32 v21, v21, v21
	v_cvt_pk_bf16_f32 v18, v22, v18
	v_cvt_pk_bf16_f32 v19, v19, v20
	v_add_u32_e32 v22, 0x50100, v163
	v_cvt_pk_bf16_f32 v20, v26, v23
	v_cvt_pk_bf16_f32 v21, v24, v21
	global_store_dwordx4 v22, v[18:21], s[10:11]
	s_andn2_b64 vcc, exec, s[0:1]
	s_mov_b64 s[0:1], -1
	v_add_u32_e32 v19, 0x58000, v163
	v_mov_b32_e32 v18, v141
	v_mul_f32_e32 v10, v10, v18
	v_mul_f32_e32 v11, v11, v18
	v_mul_f32_e32 v14, v14, v18
	v_mul_f32_e32 v15, v15, v18
	v_mul_f32_e32 v12, v12, v18
	v_mul_f32_e32 v13, v13, v18
	v_max_f32_e32 v10, 0, v10
	v_mul_f32_e32 v16, v16, v18
	v_mul_f32_e32 v17, v17, v18
	v_mul_f32_e32 v20, v10, v10
	v_max_f32_e32 v10, 0, v15
	v_max_f32_e32 v11, 0, v11
	v_max_f32_e32 v12, 0, v12
	v_max_f32_e32 v14, 0, v14
	v_mul_f32_e32 v10, v10, v10
	v_mul_f32_e32 v15, v11, v11
	v_max_f32_e32 v11, 0, v16
	v_mul_f32_e32 v16, v12, v12
	v_max_f32_e32 v12, 0, v17
	v_max_f32_e32 v13, 0, v13
	v_mul_f32_e32 v2, v2, v18
	v_mul_f32_e32 v3, v3, v18
	v_mul_f32_e32 v14, v14, v14
	v_mul_f32_e32 v11, v11, v11
	v_mul_f32_e32 v12, v12, v12
	v_mul_f32_e32 v13, v13, v13
	v_cvt_pk_bf16_f32 v10, v14, v10
	v_mul_f32_e32 v6, v6, v18
	v_mul_f32_e32 v7, v7, v18
	v_mul_f32_e32 v4, v4, v18
	v_mul_f32_e32 v5, v5, v18
	v_max_f32_e32 v2, 0, v2
	v_cvt_pk_bf16_f32 v11, v11, v12
	v_cvt_pk_bf16_f32 v12, v20, v15
	v_cvt_pk_bf16_f32 v13, v16, v13
	global_store_dwordx4 v19, v[10:13], s[10:11]
	v_mul_f32_e32 v8, v8, v18
	v_mul_f32_e32 v9, v9, v18
	v_max_f32_e32 v6, 0, v6
	v_mul_f32_e32 v10, v2, v2
	v_max_f32_e32 v2, 0, v7
	v_max_f32_e32 v3, 0, v3
	v_max_f32_e32 v4, 0, v4
	v_mul_f32_e32 v6, v6, v6
	v_mul_f32_e32 v2, v2, v2
	v_mul_f32_e32 v7, v3, v3
	v_max_f32_e32 v3, 0, v8
	v_mul_f32_e32 v8, v4, v4
	v_max_f32_e32 v4, 0, v9
	v_max_f32_e32 v5, 0, v5
	v_mul_f32_e32 v3, v3, v3
	v_mul_f32_e32 v4, v4, v4
	v_mul_f32_e32 v5, v5, v5
	v_cvt_pk_bf16_f32 v2, v6, v2
	v_add_u32_e32 v6, 0x58100, v163
	v_cvt_pk_bf16_f32 v3, v3, v4
	v_cvt_pk_bf16_f32 v4, v10, v7
	v_cvt_pk_bf16_f32 v5, v8, v5
	global_store_dwordx4 v6, v[2:5], s[10:11]
	s_mov_b32 s100, 2
	s_cbranch_vccnz .LBB0_53
	s_andn2_b64 vcc, exec, s[6:7]
	s_cbranch_vccnz .LBB0_52
	s_barrier
	s_branch .LBB0_52

; __device__ __forceinline__ void unpack8(const v4u w, float* f) { f[0] = bflo(w.x); f[1] = bfhi(w.x); f[2] = bflo(w.y); f[3] = bfhi(w.y); f[4] = bflo(w.z); f[5] = bfhi(w.z); f[6] = bflo(w.w); f[7] = bfhi(w.w); }
; __device__ __forceinline__ void norm_compute(const NormRow& R, int lane, v4u& ya, v4u& yc) {
;     ...
;     else { float f0[8], f1[8], f2[8]; unpack8(R.d0, f0); unpack8(R.d1, f1); unpack8(R.d2, f2);
;         const float inv = 1.0f / (R.l0 + R.l1 + R.l2);
; #pragma unroll
;         for (int e = 0; e < 8; ++e) fc[e] = (f0[e] + f1[e] + f2[e]) * inv; }
.LBB0_95:
	s_or_b64 exec, exec, s[12:13]
	s_and_saveexec_b64 s[12:13], s[38:39]
	s_xor_b64 s[12:13], exec, s[12:13]
	s_cbranch_execz .LBB0_97
	s_waitcnt vmcnt(0) lgkmcnt(0)
	v_add_f32_e32 v115, v173, v174
	v_add_f32_e32 v115, v115, v175
	v_div_scale_f32 v116, s[20:21], v115, v115, 1.0
	v_rcp_f32_e32 v117, v116
	v_and_b32_e32 v125, 0xffff0000, v86
	v_lshlrev_b32_e32 v126, 16, v90
	v_and_b32_e32 v127, 0xffff0000, v90
	v_fma_f32 v122, -v116, v117, 1.0
	v_fmac_f32_e32 v117, v122, v117
	v_div_scale_f32 v122, vcc, 1.0, v115, 1.0
	v_mul_f32_e32 v123, v122, v117
	v_fma_f32 v124, -v116, v123, v122
	v_fmac_f32_e32 v123, v124, v117
	v_fma_f32 v116, -v116, v123, v122
	v_div_fmas_f32 v116, v116, v117, v123
	v_div_fixup_f32 v122, v116, v115, 1.0
	v_lshlrev_b32_e32 v116, 16, v82
	v_and_b32_e32 v117, 0xffff0000, v82
	v_lshlrev_b32_e32 v124, 16, v86
	v_add_f32_e32 v116, v124, v116
	v_add_f32_e32 v117, v125, v117
	v_lshlrev_b32_e32 v128, 16, v91
	v_add_f32_e32 v116, v116, v126
	v_add_f32_e32 v117, v117, v127
	v_lshlrev_b32_e32 v126, 16, v87
	v_mul_f32_e32 v124, v116, v122
	v_mul_f32_e32 v125, v117, v122
	v_lshlrev_b32_e32 v116, 16, v83
	v_and_b32_e32 v117, 0xffff0000, v83
	v_and_b32_e32 v127, 0xffff0000, v87
	v_and_b32_e32 v129, 0xffff0000, v91
	v_add_f32_e32 v116, v126, v116
	v_add_f32_e32 v117, v127, v117
	v_lshlrev_b32_e32 v118, 16, v85
	v_lshlrev_b32_e32 v120, 16, v89
	v_and_b32_e32 v119, 0xffff0000, v85
	v_and_b32_e32 v121, 0xffff0000, v89
	v_add_f32_e32 v116, v116, v128
	v_add_f32_e32 v117, v117, v129
	v_lshlrev_b32_e32 v126, 16, v84
	v_and_b32_e32 v127, 0xffff0000, v84
	v_lshlrev_b32_e32 v128, 16, v88
	v_and_b32_e32 v129, 0xffff0000, v88
	v_lshlrev_b32_e32 v130, 16, v92
	v_and_b32_e32 v131, 0xffff0000, v92
	v_add_f32_e32 v126, v128, v126
	v_add_f32_e32 v127, v129, v127
	v_lshlrev_b32_e32 v128, 16, v93
	v_and_b32_e32 v129, 0xffff0000, v93
	v_add_f32_e32 v118, v120, v118
	v_add_f32_e32 v119, v121, v119
	v_add_f32_e32 v126, v126, v130
	v_add_f32_e32 v127, v127, v131
	v_add_f32_e32 v118, v118, v128
	v_add_f32_e32 v119, v119, v129
	v_mul_f32_e32 v116, v116, v122
	v_mul_f32_e32 v117, v117, v122
	v_mul_f32_e32 v126, v126, v122
	v_mul_f32_e32 v127, v127, v122
	v_mul_f32_e32 v128, v118, v122
	v_mul_f32_e32 v129, v119, v122
	v_mov_b32_e32 v130, v126
	v_mov_b32_e32 v131, v128
	v_mov_b32_e32 v128, v127
	v_mov_b32_e32 v133, v116
	v_mov_b32_e32 v116, v125
	v_mov_b32_e32 v132, v124
	s_andn2_saveexec_b64 s[12:13], s[12:13]
	s_cbranch_execnz .LBB0_98
	s_branch .LBB0_99

; #define GAS __attribute__((address_space(1)))
; __device__ __forceinline__ void unpack8(const v4u w, float* f) { f[0] = bflo(w.x); f[1] = bfhi(w.x); f[2] = bflo(w.y); f[3] = bfhi(w.y); f[4] = bflo(w.z); f[5] = bfhi(w.z); f[6] = bflo(w.w); f[7] = bfhi(w.w); }
; __device__ __forceinline__ void norm_load(NormRow& R, int m, int lane, const bf16* O, const bf16* GF, const bf16* OD, const float* LD) {
;     R.oa = __builtin_nontemporal_load((const GAS v4u*)(O + (size_t)m * DM + 8 * lane));
;     if (lane < 16) { R.oc = __builtin_nontemporal_load((const GAS v4u*)(O + (size_t)m * DM + 512 + 8 * lane)); R.gc = __builtin_nontemporal_load((const GAS v4u*)(GF + (size_t)m * 384 + 256 + 8 * lane)); }
;     else { const int dc = 8 * lane - 128, hd = dc >> 6;
;         R.d0 = __builtin_nontemporal_load((const GAS v4u*)(OD + (size_t)m * 384 + dc)); R.d1 = __builtin_nontemporal_load((const GAS v4u*)(OD + OD_BRANCH + (size_t)m * 384 + dc)); R.d2 = __builtin_nontemporal_load((const GAS v4u*)(OD + 2 * OD_BRANCH + (size_t)m * 384 + dc));
;         R.l0 = LD[(size_t)m * 8 + hd]; R.l1 = LD[LD_BRANCH + (size_t)m * 8 + hd]; R.l2 = LD[2 * LD_BRANCH + (size_t)m * 8 + hd]; }
;     if (lane >= 32) R.ga = __builtin_nontemporal_load((const GAS v4u*)(GF + (size_t)m * 384 + 8 * lane - 256));
; __device__ __forceinline__ void norm_compute(const NormRow& R, int lane, v4u& ya, v4u& yc) {
;     float fa[8], fc[8];
;     unpack8(R.oa, fa);
;     if (lane < 16) unpack8(R.oc, fc);
;     else { float f0[8], f1[8], f2[8]; unpack8(R.d0, f0); unpack8(R.d1, f1); unpack8(R.d2, f2);
;         const float inv = 1.0f / (R.l0 + R.l1 + R.l2);
; #pragma unroll
;         for (int e = 0; e < 8; ++e) fc[e] = (f0[e] + f1[e] + f2[e]) * inv; }
;     float sa = 0.f, sc = 0.f;
; #pragma unroll
;     for (int e = 0; e < 8; ++e) { sa += fa[e] * fa[e]; sc += fc[e] * fc[e]; }
;     const float s_moba = wave_sum(lane < 32 ? sa : 0.f), s_fox = wave_sum((lane >= 32 ? sa : 0.f) + (lane < 16 ? sc : 0.f)), s_dil = wave_sum(lane >= 16 ? sc : 0.f);
;     const float r_moba = 1.0f / sqrtf(s_moba * (1.0f / 256.0f) + EPS), r_fox = 1.0f / sqrtf(s_fox * (1.0f / 384.0f) + EPS), r_dil = 1.0f / sqrtf(s_dil * (1.0f / 384.0f) + EPS);
;     float ga[8], gc[8];
; #pragma unroll
;     for (int e = 0; e < 8; ++e) { ga[e] = 1.f; gc[e] = 1.f; }
;     if (lane >= 32) unpack8(R.ga, ga);
;     if (lane < 16) unpack8(R.gc, gc);
.LBB0_99:
	s_or_b64 exec, exec, s[12:13]
	v_and_b32_e32 v115, 64, v214
	v_add_u32_e32 v115, 64, v115
	v_xor_b32_e32 v118, 1, v214
	v_cmp_lt_i32_e32 vcc, v118, v115
	s_waitcnt vmcnt(0)
	v_lshlrev_b32_e32 v141, 16, v103
	v_lshlrev_b32_e32 v140, 16, v102
	v_cndmask_b32_e32 v118, v214, v118, vcc
	v_lshlrev_b32_e32 v164, 2, v118
	v_xor_b32_e32 v118, 2, v214
	v_cmp_lt_i32_e32 vcc, v118, v115
	v_and_b32_e32 v135, 0xffff0000, v103
	v_and_b32_e32 v134, 0xffff0000, v102
	v_cndmask_b32_e32 v118, v214, v118, vcc
	v_lshlrev_b32_e32 v162, 2, v118
	v_xor_b32_e32 v118, 4, v214
	v_cmp_lt_i32_e32 vcc, v118, v115
	v_lshlrev_b32_e32 v139, 16, v105
	v_lshlrev_b32_e32 v138, 16, v104
	v_cndmask_b32_e32 v118, v214, v118, vcc
	v_lshlrev_b32_e32 v161, 2, v118
	v_xor_b32_e32 v118, 8, v214
	v_cmp_lt_i32_e32 vcc, v118, v115
	v_and_b32_e32 v137, 0xffff0000, v105
	v_and_b32_e32 v136, 0xffff0000, v104
	v_cndmask_b32_e32 v118, v214, v118, vcc
	v_lshlrev_b32_e32 v160, 2, v118
	v_xor_b32_e32 v118, 16, v214
	v_cmp_lt_i32_e32 vcc, v118, v115
	v_mul_f32_e32 v102, v140, v140
	v_mul_f32_e32 v103, v141, v141
	v_mul_f32_e32 v104, v134, v134
	v_mul_f32_e32 v105, v135, v135
	v_cndmask_b32_e32 v118, v214, v118, vcc
	v_lshlrev_b32_e32 v159, 2, v118
	v_xor_b32_e32 v118, 32, v214
	v_add_f32_e32 v102, v102, v104
	v_cmp_lt_i32_e32 vcc, v118, v115
	v_add_f32_e32 v102, v103, v102
	v_add_f32_e32 v102, v105, v102
	v_cndmask_b32_e32 v115, v214, v118, vcc
	v_mul_f32_e32 v118, v138, v138
	v_mul_f32_e32 v119, v139, v139
	v_mul_f32_e32 v120, v136, v136
	v_mul_f32_e32 v121, v137, v137
	v_add_f32_e32 v102, v118, v102
	v_add_f32_e32 v102, v120, v102
	v_add_f32_e32 v102, v119, v102
	v_cmp_gt_u32_e64 s[40:41], 32, v194
	v_add_f32_e32 v102, v121, v102
	v_lshlrev_b32_e32 v158, 2, v115
	v_cndmask_b32_e64 v103, 0, v102, s[40:41]
	ds_bpermute_b32 v104, v164, v103
	v_mul_f32_e32 v115, v116, v116
	v_fmac_f32_e32 v115, v132, v132
	v_fmac_f32_e32 v115, v133, v133
	v_fmac_f32_e32 v115, v117, v117
	s_waitcnt lgkmcnt(0)
	v_add_f32_e32 v103, v103, v104
	ds_bpermute_b32 v104, v162, v103
	v_fmac_f32_e32 v115, v130, v130
	v_fmac_f32_e32 v115, v128, v128
	v_fmac_f32_e32 v115, v131, v131
	v_fmac_f32_e32 v115, v129, v129
	s_waitcnt lgkmcnt(0)
	v_add_f32_e32 v103, v103, v104
	ds_bpermute_b32 v104, v161, v103
	v_cndmask_b32_e64 v102, 0, v102, s[36:37]
	v_cmp_lt_u32_e64 s[42:43], 15, v194
	v_mov_b32_e32 v142, 1.0
	v_mov_b32_e32 v156, 1.0
	s_waitcnt lgkmcnt(0)
	v_add_f32_e32 v103, v103, v104
	ds_bpermute_b32 v104, v160, v103
	v_mov_b32_e32 v152, 1.0
	v_mov_b32_e32 v157, 1.0
	v_mov_b32_e32 v153, 1.0
	v_mov_b32_e32 v154, 1.0
	s_waitcnt lgkmcnt(0)
	v_add_f32_e32 v103, v103, v104
	ds_bpermute_b32 v104, v159, v103
	v_mov_b32_e32 v150, 1.0
	v_mov_b32_e32 v155, 1.0
	v_mov_b32_e32 v151, 1.0
	s_waitcnt lgkmcnt(0)
	v_add_f32_e32 v176, v103, v104
	v_cndmask_b32_e64 v103, 0, v115, s[34:35]
	v_add_f32_e32 v102, v102, v103
	ds_bpermute_b32 v103, v164, v102
	ds_bpermute_b32 v178, v158, v176
	s_waitcnt lgkmcnt(1)
	v_add_f32_e32 v102, v102, v103
	ds_bpermute_b32 v103, v162, v102
	s_waitcnt lgkmcnt(0)
	v_add_f32_e32 v102, v102, v103
	ds_bpermute_b32 v103, v161, v102
	s_waitcnt lgkmcnt(0)
	v_add_f32_e32 v102, v102, v103
	ds_bpermute_b32 v103, v160, v102
	s_waitcnt lgkmcnt(0)
	v_add_f32_e32 v102, v102, v103
	ds_bpermute_b32 v103, v159, v102
	s_waitcnt lgkmcnt(0)
	v_add_f32_e32 v177, v102, v103
	v_cndmask_b32_e64 v102, 0, v115, s[42:43]
	ds_bpermute_b32 v103, v164, v102
	ds_bpermute_b32 v179, v158, v177
	s_waitcnt lgkmcnt(1)
	v_add_f32_e32 v102, v102, v103
	ds_bpermute_b32 v103, v162, v102
	s_waitcnt lgkmcnt(0)
	v_add_f32_e32 v102, v102, v103
	ds_bpermute_b32 v103, v161, v102
	s_waitcnt lgkmcnt(0)
	v_add_f32_e32 v102, v102, v103
	ds_bpermute_b32 v103, v160, v102
	s_waitcnt lgkmcnt(0)
	v_add_f32_e32 v102, v102, v103
	ds_bpermute_b32 v103, v159, v102
	s_waitcnt lgkmcnt(0)
	v_add_f32_e32 v180, v102, v103
	ds_bpermute_b32 v181, v158, v180
	s_and_saveexec_b64 s[12:13], s[36:37]
	v_lshlrev_b32_e32 v156, 16, v78
	v_and_b32_e32 v152, 0xffff0000, v78
	v_lshlrev_b32_e32 v157, 16, v79
	v_and_b32_e32 v153, 0xffff0000, v79
	v_lshlrev_b32_e32 v154, 16, v80
	v_and_b32_e32 v150, 0xffff0000, v80
	v_lshlrev_b32_e32 v155, 16, v81
	v_and_b32_e32 v151, 0xffff0000, v81
	s_or_b64 exec, exec, s[12:13]
	v_mov_b32_e32 v148, 1.0
	v_mov_b32_e32 v143, 1.0
	v_mov_b32_e32 v149, 1.0
	v_mov_b32_e32 v146, 1.0
	v_mov_b32_e32 v144, 1.0
	v_mov_b32_e32 v147, 1.0
	v_mov_b32_e32 v145, 1.0
	s_and_saveexec_b64 s[12:13], s[34:35]
	v_lshlrev_b32_e32 v142, 16, v74
	v_and_b32_e32 v148, 0xffff0000, v74
	v_lshlrev_b32_e32 v143, 16, v75
	v_and_b32_e32 v149, 0xffff0000, v75
	v_lshlrev_b32_e32 v146, 16, v76
	v_and_b32_e32 v144, 0xffff0000, v76
	v_lshlrev_b32_e32 v147, 16, v77
	v_and_b32_e32 v145, 0xffff0000, v77
	s_or_b64 exec, exec, s[12:13]
	v_ashrrev_i32_e32 v115, 31, v114
	v_lshlrev_b64 v[102:103], 1, v[114:115]
	v_lshl_add_u64 v[124:125], s[0:1], 0, v[102:103]
	v_lshl_add_u64 v[102:103], s[74:75], 0, v[102:103]
	s_mov_b64 s[0:1], 0x1b000000
	v_lshl_add_u64 v[122:123], v[102:103], 0, s[0:1]
	s_mov_b64 s[0:1], 0x1c800000
	v_lshl_add_u64 v[120:121], v[102:103], 0, s[0:1]
	s_or_b32 s0, s8, 4
	s_ashr_i32 s1, s0, 31
	s_lshl_b64 s[12:13], s[0:1], 11
	s_add_u32 s20, s29, s12
	s_addc_u32 s21, s30, s13
	global_load_dwordx4 v[102:105], v0, s[20:21] nt
	v_ashrrev_i32_e32 v118, 6, v114
	v_ashrrev_i32_e32 v119, 31, v118
	s_and_saveexec_b64 s[22:23], s[38:39]
	s_xor_b64 s[22:23], exec, s[22:23]
	s_cbranch_execz .LBB0_759
	v_mad_i64_i32 v[82:83], s[44:45], s0, v252, v[124:125]
	v_mad_i64_i32 v[86:87], s[44:45], s0, v252, v[122:123]
	v_mad_i64_i32 v[90:91], s[44:45], s0, v252, v[120:121]
	s_lshl_b64 s[44:45], s[0:1], 5
	s_add_u32 s44, s26, s44
	s_addc_u32 s45, s27, s45
	v_lshl_add_u64 v[114:115], v[118:119], 2, s[44:45]
	v_add_co_u32_e32 v126, vcc, 0x100000, v114
	flat_load_dword v173, v[114:115]
	s_nop 0
	v_addc_co_u32_e32 v127, vcc, 0, v115, vcc
	flat_load_dword v174, v[126:127]
	v_add_co_u32_e32 v114, vcc, 0x200000, v114
	global_load_dwordx4 v[82:85], v[82:83], off nt
	s_nop 0
	v_addc_co_u32_e32 v115, vcc, 0, v115, vcc
	global_load_dwordx4 v[86:89], v[86:87], off nt
	s_nop 0
	global_load_dwordx4 v[90:93], v[90:91], off nt
	s_nop 0
	flat_load_dword v175, v[114:115]
	s_andn2_saveexec_b64 s[22:23], s[22:23]
	s_cbranch_execnz .LBB0_760

; __device__ __forceinline__ unsigned pk2(float lo, float hi) { return f2bf(lo) | (f2bf(hi) << 16); }
; __device__ __forceinline__ void unpack8(const v4u w, float* f) { f[0] = bflo(w.x); f[1] = bfhi(w.x); f[2] = bflo(w.y); f[3] = bfhi(w.y); f[4] = bflo(w.z); f[5] = bfhi(w.z); f[6] = bflo(w.w); f[7] = bfhi(w.w); }
; __device__ __forceinline__ void norm_compute(const NormRow& R, int lane, v4u& ya, v4u& yc) {
;     ...
;     const float s_moba = wave_sum(lane < 32 ? sa : 0.f), s_fox = wave_sum((lane >= 32 ? sa : 0.f) + (lane < 16 ? sc : 0.f)), s_dil = wave_sum(lane >= 16 ? sc : 0.f);
;     const float r_moba = 1.0f / sqrtf(s_moba * (1.0f / 256.0f) + EPS), r_fox = 1.0f / sqrtf(s_fox * (1.0f / 384.0f) + EPS), r_dil = 1.0f / sqrtf(s_dil * (1.0f / 384.0f) + EPS);
;     float ga[8], gc[8];
; #pragma unroll
;     for (int e = 0; e < 8; ++e) { ga[e] = 1.f; gc[e] = 1.f; }
;     if (lane >= 32) unpack8(R.ga, ga);
;     if (lane < 16) unpack8(R.gc, gc);
;     const float ra = lane < 32 ? r_moba : r_fox, rc = lane < 16 ? r_fox : r_dil;
;     ya.x = pk2(fa[0] * ra * ga[0], fa[1] * ra * ga[1]); ya.y = pk2(fa[2] * ra * ga[2], fa[3] * ra * ga[3]); ya.z = pk2(fa[4] * ra * ga[4], fa[5] * ra * ga[5]); ya.w = pk2(fa[6] * ra * ga[6], fa[7] * ra * ga[7]);
;     yc.x = pk2(fc[0] * rc * gc[0], fc[1] * rc * gc[1]); yc.y = pk2(fc[2] * rc * gc[2], fc[3] * rc * gc[3]); yc.z = pk2(fc[4] * rc * gc[4], fc[5] * rc * gc[5]); yc.w = pk2(fc[6] * rc * gc[6], fc[7] * rc * gc[7]);
; }
.LBB0_107:
	s_or_b64 exec, exec, s[20:21]
	s_waitcnt lgkmcnt(0)
	v_add_f32_e32 v114, v180, v181
	v_fmamk_f32 v114, v114, 0x3b2aaaab, v215
	s_mov_b32 s3, 0xf800000
	v_mul_f32_e32 v115, 0x4f800000, v114
	v_cmp_gt_f32_e32 vcc, s3, v114
	v_add_f32_e32 v177, v177, v179
	v_fmamk_f32 v177, v177, 0x3b2aaaab, v215
	v_cndmask_b32_e32 v114, v114, v115, vcc
	v_sqrt_f32_e32 v115, v114
	v_mul_f32_e32 v179, 0x4f800000, v177
	v_add_f32_e32 v176, v176, v178
	v_fmamk_f32 v176, v176, 0x3b800000, v215
	v_add_u32_e32 v180, -1, v115
	v_fma_f32 v182, -v180, v115, v114
	v_add_u32_e32 v181, 1, v115
	v_cmp_ge_f32_e64 s[0:1], 0, v182
	v_mul_f32_e32 v178, 0x4f800000, v176
	s_nop 0
	v_cndmask_b32_e64 v180, v115, v180, s[0:1]
	v_fma_f32 v115, -v181, v115, v114
	v_cmp_lt_f32_e64 s[0:1], 0, v115
	s_nop 1
	v_cndmask_b32_e64 v115, v180, v181, s[0:1]
	v_cmp_gt_f32_e64 s[0:1], s3, v177
	v_mul_f32_e32 v180, 0x37800000, v115
	v_cndmask_b32_e32 v115, v115, v180, vcc
	v_cndmask_b32_e64 v177, v177, v179, s[0:1]
	v_sqrt_f32_e32 v179, v177
	v_cmp_class_f32_e32 vcc, v114, v216
	s_nop 1
	v_cndmask_b32_e32 v114, v115, v114, vcc
	v_add_u32_e32 v115, -1, v179
	v_fma_f32 v180, -v115, v179, v177
	v_cmp_ge_f32_e32 vcc, 0, v180
	v_add_u32_e32 v180, 1, v179
	s_nop 0
	v_cndmask_b32_e32 v115, v179, v115, vcc
	v_fma_f32 v179, -v180, v179, v177
	v_cmp_lt_f32_e32 vcc, 0, v179
	s_nop 1
	v_cndmask_b32_e32 v115, v115, v180, vcc
	v_cmp_gt_f32_e32 vcc, s3, v176
	v_mul_f32_e32 v179, 0x37800000, v115
	v_cndmask_b32_e64 v115, v115, v179, s[0:1]
	v_cndmask_b32_e32 v176, v176, v178, vcc
	v_sqrt_f32_e32 v178, v176
	v_cmp_class_f32_e64 s[0:1], v177, v216
	s_nop 1
	v_cndmask_b32_e64 v115, v115, v177, s[0:1]
	v_add_u32_e32 v177, -1, v178
	v_fma_f32 v179, -v177, v178, v176
	v_cmp_ge_f32_e64 s[0:1], 0, v179
	v_add_u32_e32 v179, 1, v178
	s_nop 0
	v_cndmask_b32_e64 v177, v178, v177, s[0:1]
	v_fma_f32 v178, -v179, v178, v176
	v_cmp_lt_f32_e64 s[0:1], 0, v178
	s_nop 1
	v_cndmask_b32_e64 v177, v177, v179, s[0:1]
	v_div_scale_f32 v179, s[0:1], v114, v114, 1.0
	v_rcp_f32_e32 v180, v179
	v_mul_f32_e32 v178, 0x37800000, v177
	v_cndmask_b32_e32 v177, v177, v178, vcc
	v_cmp_class_f32_e32 vcc, v176, v216
	s_nop 1
	v_cndmask_b32_e32 v176, v177, v176, vcc
	v_fma_f32 v177, -v179, v180, 1.0
	v_fmac_f32_e32 v180, v177, v180
	v_div_scale_f32 v177, vcc, 1.0, v114, 1.0
	v_mul_f32_e32 v178, v177, v180
	v_fma_f32 v181, -v179, v178, v177
	v_fmac_f32_e32 v178, v181, v180
	v_fma_f32 v177, -v179, v178, v177
	v_div_scale_f32 v179, s[0:1], v115, v115, 1.0
	v_rcp_f32_e32 v181, v179
	v_div_fmas_f32 v177, v177, v180, v178
	v_div_fixup_f32 v177, v177, v114, 1.0
	v_fma_f32 v114, -v179, v181, 1.0
	v_fmac_f32_e32 v181, v114, v181
	v_div_scale_f32 v114, vcc, 1.0, v115, 1.0
	v_mul_f32_e32 v178, v114, v181
	v_fma_f32 v180, -v179, v178, v114
	v_fmac_f32_e32 v178, v180, v181
	v_fma_f32 v114, -v179, v178, v114
	v_div_scale_f32 v179, s[0:1], v176, v176, 1.0
	v_rcp_f32_e32 v180, v179
	v_div_fmas_f32 v114, v114, v181, v178
	v_div_fixup_f32 v115, v114, v115, 1.0
	s_movk_i32 s1, 0x7fff
	v_fma_f32 v114, -v179, v180, 1.0
	v_fmac_f32_e32 v180, v114, v180
	v_div_scale_f32 v114, vcc, 1.0, v176, 1.0
	v_mul_f32_e32 v178, v114, v180
	v_fma_f32 v181, -v179, v178, v114
	v_fmac_f32_e32 v178, v181, v180
	v_fma_f32 v114, -v179, v178, v114
	v_div_fmas_f32 v114, v114, v180, v178
	v_div_fixup_f32 v114, v114, v176, 1.0
	v_cndmask_b32_e64 v114, v115, v114, s[40:41]
	v_cndmask_b32_e64 v176, v177, v115, s[34:35]
	v_mul_f32_e32 v140, v114, v140
	v_mul_f32_e32 v141, v114, v141
	v_mul_f32_e32 v134, v114, v134
	v_mul_f32_e32 v135, v114, v135
	v_mul_f32_e32 v138, v114, v138
	v_mul_f32_e32 v139, v114, v139
	v_mul_f32_e32 v115, v114, v137
	v_mul_f32_e32 v114, v114, v136
	v_mul_f32_e32 v134, v134, v152
	v_mul_f32_e32 v135, v135, v153
	v_mul_f32_e32 v114, v114, v150
	v_mul_f32_e32 v115, v115, v151
	v_mul_f32_e32 v140, v140, v156
	v_mul_f32_e32 v141, v141, v157
	v_mul_f32_e32 v138, v138, v154
	v_mul_f32_e32 v139, v139, v155
	v_bfe_u32 v136, v115, 16, 1
	v_bfe_u32 v137, v114, 16, 1
	v_bfe_u32 v150, v135, 16, 1
	v_bfe_u32 v151, v134, 16, 1
	v_add3_u32 v134, v134, v151, s1
	v_add3_u32 v135, v135, v150, s1
	v_add3_u32 v114, v114, v137, s1
	v_add3_u32 v115, v115, v136, s1
	v_bfe_u32 v136, v140, 16, 1
	v_bfe_u32 v137, v141, 16, 1
	v_bfe_u32 v150, v138, 16, 1
	v_bfe_u32 v151, v139, 16, 1
	v_add3_u32 v139, v139, v151, s1
	v_add3_u32 v138, v138, v150, s1
	v_add3_u32 v137, v141, v137, s1
	v_add3_u32 v136, v140, v136, s1
	v_lshrrev_b32_e32 v140, 16, v136
	v_lshrrev_b32_e32 v141, 16, v137
	v_lshrrev_b32_e32 v136, 16, v138
	v_lshrrev_b32_e32 v137, 16, v139
	s_mov_b32 s0, 0xffff0000
	v_mul_f32_e32 v116, v116, v176
	v_mul_f32_e32 v117, v117, v176
	v_mul_f32_e32 v128, v128, v176
	v_mul_f32_e32 v129, v129, v176
	v_and_or_b32 v137, v115, s0, v137
	v_and_or_b32 v136, v114, s0, v136
	v_mul_f32_e32 v114, v132, v176
	v_mul_f32_e32 v115, v133, v176
	v_mul_f32_e32 v116, v116, v148
	v_mul_f32_e32 v117, v117, v149
	v_mul_f32_e32 v130, v130, v176
	v_mul_f32_e32 v131, v131, v176
	v_mul_f32_e32 v128, v128, v144
	v_mul_f32_e32 v129, v129, v145
	v_mul_f32_e32 v114, v114, v142
	v_mul_f32_e32 v115, v115, v143
	v_mul_f32_e32 v130, v130, v146
	v_mul_f32_e32 v131, v131, v147
	v_bfe_u32 v132, v129, 16, 1
	v_bfe_u32 v133, v128, 16, 1
	v_bfe_u32 v138, v117, 16, 1
	v_bfe_u32 v139, v116, 16, 1
	v_add3_u32 v139, v116, v139, s1
	v_add3_u32 v138, v117, v138, s1
	v_add3_u32 v116, v128, v133, s1
	v_add3_u32 v117, v129, v132, s1
	v_bfe_u32 v128, v114, 16, 1
	v_bfe_u32 v129, v115, 16, 1
	v_bfe_u32 v132, v130, 16, 1
	v_bfe_u32 v133, v131, 16, 1
	v_add3_u32 v131, v131, v133, s1
	v_add3_u32 v130, v130, v132, s1
	v_add3_u32 v115, v115, v129, s1
	v_add3_u32 v114, v114, v128, s1
	v_lshrrev_b32_e32 v114, 16, v114
	v_lshrrev_b32_e32 v115, 16, v115
	v_lshrrev_b32_e32 v128, 16, v130
	v_lshrrev_b32_e32 v129, 16, v131
	v_and_or_b32 v135, v135, s0, v141
	v_and_or_b32 v134, v134, s0, v140
	v_and_or_b32 v117, v117, s0, v129
	v_and_or_b32 v116, v116, s0, v128
	v_and_or_b32 v115, v138, s0, v115
	v_and_or_b32 v114, v139, s0, v114
	s_add_u32 s0, s24, s14
	s_addc_u32 s1, s25, s15
	global_store_dwordx4 v0, v[134:137], s[0:1]
	global_store_dwordx4 v0, v[114:117], s[0:1] offset:1024
	s_and_saveexec_b64 s[0:1], s[38:39]
	s_xor_b64 s[0:1], exec, s[0:1]
	s_cbranch_execz .LBB0_109
; __device__ __forceinline__ void unpack8(const v4u w, float* f) { f[0] = bflo(w.x); f[1] = bfhi(w.x); f[2] = bflo(w.y); f[3] = bfhi(w.y); f[4] = bflo(w.z); f[5] = bfhi(w.z); f[6] = bflo(w.w); f[7] = bfhi(w.w); }
; __device__ __forceinline__ void norm_compute(const NormRow& R, int lane, v4u& ya, v4u& yc) {
;     ...
;     else { float f0[8], f1[8], f2[8]; unpack8(R.d0, f0); unpack8(R.d1, f1); unpack8(R.d2, f2);
;         const float inv = 1.0f / (R.l0 + R.l1 + R.l2);
; #pragma unroll
;         for (int e = 0; e < 8; ++e) fc[e] = (f0[e] + f1[e] + f2[e]) * inv; }
	v_add_f32_e32 v114, v171, v170
	v_add_f32_e32 v114, v172, v114
	v_div_scale_f32 v115, s[14:15], v114, v114, 1.0
	v_rcp_f32_e32 v130, v115
	v_lshlrev_b32_e32 v134, 16, v66
	v_and_b32_e32 v135, 0xffff0000, v66
	v_lshlrev_b32_e32 v136, 16, v67
	v_fma_f32 v131, -v115, v130, 1.0
	v_fmac_f32_e32 v130, v131, v130
	v_div_scale_f32 v131, vcc, 1.0, v114, 1.0
	v_mul_f32_e32 v132, v131, v130
	v_fma_f32 v133, -v115, v132, v131
	v_fmac_f32_e32 v132, v133, v130
	v_fma_f32 v115, -v115, v132, v131
	v_div_fmas_f32 v115, v115, v130, v132
	v_div_fixup_f32 v130, v115, v114, 1.0
	v_lshlrev_b32_e32 v114, 16, v58
	v_and_b32_e32 v115, 0xffff0000, v58
	v_lshlrev_b32_e32 v132, 16, v62
	v_and_b32_e32 v133, 0xffff0000, v62
	v_add_f32_e32 v114, v132, v114
	v_add_f32_e32 v115, v133, v115
	v_and_b32_e32 v137, 0xffff0000, v67
	v_add_f32_e32 v114, v114, v134
	v_add_f32_e32 v115, v115, v135
	v_lshlrev_b32_e32 v134, 16, v63
	v_mul_f32_e32 v132, v130, v114
	v_mul_f32_e32 v133, v130, v115
	v_lshlrev_b32_e32 v114, 16, v59
	v_and_b32_e32 v115, 0xffff0000, v59
	v_and_b32_e32 v135, 0xffff0000, v63
	v_add_f32_e32 v114, v134, v114
	v_add_f32_e32 v115, v135, v115
	v_lshlrev_b32_e32 v116, 16, v61
	v_lshlrev_b32_e32 v128, 16, v65
	v_and_b32_e32 v117, 0xffff0000, v61
	v_and_b32_e32 v129, 0xffff0000, v65
	v_add_f32_e32 v114, v114, v136
	v_add_f32_e32 v115, v115, v137
	v_lshlrev_b32_e32 v134, 16, v60
	v_and_b32_e32 v135, 0xffff0000, v60
	v_lshlrev_b32_e32 v136, 16, v64
	v_and_b32_e32 v137, 0xffff0000, v64
	v_lshlrev_b32_e32 v138, 16, v68
	v_and_b32_e32 v139, 0xffff0000, v68
	v_add_f32_e32 v134, v136, v134
	v_add_f32_e32 v135, v137, v135
	v_lshlrev_b32_e32 v136, 16, v69
	v_and_b32_e32 v137, 0xffff0000, v69
	v_add_f32_e32 v116, v128, v116
	v_add_f32_e32 v117, v129, v117
	v_add_f32_e32 v134, v134, v138
	v_add_f32_e32 v135, v135, v139
	v_add_f32_e32 v116, v116, v136
	v_add_f32_e32 v117, v117, v137
	v_mul_f32_e32 v114, v130, v114
	v_mul_f32_e32 v115, v130, v115
	v_mul_f32_e32 v134, v130, v134
	v_mul_f32_e32 v135, v130, v135
	v_mul_f32_e32 v116, v130, v116
	v_mul_f32_e32 v117, v130, v117
	v_mov_b32_e32 v129, v116
	v_mov_b32_e32 v116, v135
	v_mov_b32_e32 v128, v134
	v_mov_b32_e32 v131, v114
	v_mov_b32_e32 v114, v133
	v_mov_b32_e32 v130, v132
; #define GAS __attribute__((address_space(1)))
; __device__ __forceinline__ void unpack8(const v4u w, float* f) { f[0] = bflo(w.x); f[1] = bfhi(w.x); f[2] = bflo(w.y); f[3] = bfhi(w.y); f[4] = bflo(w.z); f[5] = bfhi(w.z); f[6] = bflo(w.w); f[7] = bfhi(w.w); }
; __device__ __forceinline__ void norm_load(NormRow& R, int m, int lane, const bf16* O, const bf16* GF, const bf16* OD, const float* LD) {
;     R.oa = __builtin_nontemporal_load((const GAS v4u*)(O + (size_t)m * DM + 8 * lane));
;     if (lane < 16) { R.oc = __builtin_nontemporal_load((const GAS v4u*)(O + (size_t)m * DM + 512 + 8 * lane)); R.gc = __builtin_nontemporal_load((const GAS v4u*)(GF + (size_t)m * 384 + 256 + 8 * lane)); }
;     else { const int dc = 8 * lane - 128, hd = dc >> 6;
;         R.d0 = __builtin_nontemporal_load((const GAS v4u*)(OD + (size_t)m * 384 + dc)); R.d1 = __builtin_nontemporal_load((const GAS v4u*)(OD + OD_BRANCH + (size_t)m * 384 + dc)); R.d2 = __builtin_nontemporal_load((const GAS v4u*)(OD + 2 * OD_BRANCH + (size_t)m * 384 + dc));
;         R.l0 = LD[(size_t)m * 8 + hd]; R.l1 = LD[LD_BRANCH + (size_t)m * 8 + hd]; R.l2 = LD[2 * LD_BRANCH + (size_t)m * 8 + hd]; }
;     if (lane >= 32) R.ga = __builtin_nontemporal_load((const GAS v4u*)(GF + (size_t)m * 384 + 8 * lane - 256));
; __device__ __forceinline__ void norm_compute(const NormRow& R, int lane, v4u& ya, v4u& yc) {
;     float fa[8], fc[8];
;     unpack8(R.oa, fa);
;     if (lane < 16) unpack8(R.oc, fc);
;     else { float f0[8], f1[8], f2[8]; unpack8(R.d0, f0); unpack8(R.d1, f1); unpack8(R.d2, f2);
;         const float inv = 1.0f / (R.l0 + R.l1 + R.l2);
; #pragma unroll
;         for (int e = 0; e < 8; ++e) fc[e] = (f0[e] + f1[e] + f2[e]) * inv; }
;     float sa = 0.f, sc = 0.f;
; #pragma unroll
;     for (int e = 0; e < 8; ++e) { sa += fa[e] * fa[e]; sc += fc[e] * fc[e]; }
;     const float s_moba = wave_sum(lane < 32 ? sa : 0.f), s_fox = wave_sum((lane >= 32 ? sa : 0.f) + (lane < 16 ? sc : 0.f)), s_dil = wave_sum(lane >= 16 ? sc : 0.f);
;     const float r_moba = 1.0f / sqrtf(s_moba * (1.0f / 256.0f) + EPS), r_fox = 1.0f / sqrtf(s_fox * (1.0f / 384.0f) + EPS), r_dil = 1.0f / sqrtf(s_dil * (1.0f / 384.0f) + EPS);
;     float ga[8], gc[8];
; #pragma unroll
;     for (int e = 0; e < 8; ++e) { ga[e] = 1.f; gc[e] = 1.f; }
;     if (lane >= 32) unpack8(R.ga, ga);
;     if (lane < 16) unpack8(R.gc, gc);
.LBB0_109:
	s_andn2_saveexec_b64 s[0:1], s[0:1]
	v_lshlrev_b32_e32 v130, 16, v70
	v_and_b32_e32 v114, 0xffff0000, v70
	v_lshlrev_b32_e32 v131, 16, v71
	v_and_b32_e32 v115, 0xffff0000, v71
	v_lshlrev_b32_e32 v128, 16, v72
	v_and_b32_e32 v116, 0xffff0000, v72
	v_lshlrev_b32_e32 v129, 16, v73
	v_and_b32_e32 v117, 0xffff0000, v73
	s_or_b64 exec, exec, s[0:1]
	v_lshlrev_b32_e32 v139, 16, v107
	v_lshlrev_b32_e32 v138, 16, v106
	v_and_b32_e32 v133, 0xffff0000, v107
	v_and_b32_e32 v132, 0xffff0000, v106
	v_lshlrev_b32_e32 v137, 16, v109
	v_lshlrev_b32_e32 v136, 16, v108
	v_and_b32_e32 v135, 0xffff0000, v109
	v_and_b32_e32 v134, 0xffff0000, v108
	v_mul_f32_e32 v106, v138, v138
	v_mul_f32_e32 v107, v139, v139
	v_mul_f32_e32 v108, v132, v132
	v_mul_f32_e32 v109, v133, v133
	v_mul_f32_e32 v144, v114, v114
	v_fmac_f32_e32 v144, v130, v130
	v_add_f32_e32 v106, v106, v108
	v_fmac_f32_e32 v144, v131, v131
	v_add_f32_e32 v106, v107, v106
	v_fmac_f32_e32 v144, v115, v115
	v_mul_f32_e32 v140, v136, v136
	v_mul_f32_e32 v141, v137, v137
	v_add_f32_e32 v106, v109, v106
	v_fmac_f32_e32 v144, v128, v128
	v_mul_f32_e32 v142, v134, v134
	v_mul_f32_e32 v143, v135, v135
	v_add_f32_e32 v106, v140, v106
	v_fmac_f32_e32 v144, v116, v116
	v_add_f32_e32 v106, v142, v106
	v_fmac_f32_e32 v144, v129, v129
	v_add_f32_e32 v106, v141, v106
	v_add_f32_e32 v106, v143, v106
	v_fmac_f32_e32 v144, v117, v117
	v_cndmask_b32_e64 v107, 0, v106, s[40:41]
	v_cndmask_b32_e64 v106, 0, v106, s[36:37]
	v_cndmask_b32_e64 v109, 0, v144, s[34:35]
	v_add_f32_e32 v106, v106, v109
	v_cndmask_b32_e64 v140, 0, v144, s[42:43]
	ds_bpermute_b32 v108, v164, v107
	ds_bpermute_b32 v109, v164, v106
	ds_bpermute_b32 v141, v164, v140
	v_mov_b32_e32 v154, 1.0
	v_mov_b32_e32 v150, 1.0
	s_waitcnt lgkmcnt(0)
	v_add_f32_e32 v107, v107, v108
	v_add_f32_e32 v106, v106, v109
	v_add_f32_e32 v140, v140, v141
	ds_bpermute_b32 v108, v162, v107
	ds_bpermute_b32 v109, v162, v106
	ds_bpermute_b32 v141, v162, v140
	v_mov_b32_e32 v155, 1.0
	v_mov_b32_e32 v151, 1.0
	s_waitcnt lgkmcnt(0)
	v_add_f32_e32 v107, v107, v108
	v_add_f32_e32 v106, v106, v109
	v_add_f32_e32 v140, v140, v141
	ds_bpermute_b32 v108, v161, v107
	ds_bpermute_b32 v109, v161, v106
	ds_bpermute_b32 v141, v161, v140
	v_mov_b32_e32 v152, 1.0
	v_mov_b32_e32 v148, 1.0
	s_waitcnt lgkmcnt(0)
	v_add_f32_e32 v107, v107, v108
	v_add_f32_e32 v106, v106, v109
	v_add_f32_e32 v140, v140, v141
	ds_bpermute_b32 v108, v160, v107
	ds_bpermute_b32 v109, v160, v106
	ds_bpermute_b32 v141, v160, v140
	v_mov_b32_e32 v153, 1.0
	v_mov_b32_e32 v149, 1.0
	s_waitcnt lgkmcnt(0)
	v_add_f32_e32 v107, v107, v108
	v_add_f32_e32 v106, v106, v109
	v_add_f32_e32 v140, v140, v141
	ds_bpermute_b32 v108, v159, v107
	ds_bpermute_b32 v109, v159, v106
	ds_bpermute_b32 v141, v159, v140
	s_waitcnt lgkmcnt(0)
	v_add_f32_e32 v156, v107, v108
	v_add_f32_e32 v176, v106, v109
	v_add_f32_e32 v178, v140, v141
	ds_bpermute_b32 v157, v158, v156
	ds_bpermute_b32 v177, v158, v176
	ds_bpermute_b32 v179, v158, v178
	v_mov_b32_e32 v140, 1.0
	s_and_saveexec_b64 s[0:1], s[36:37]
	v_lshlrev_b32_e32 v154, 16, v54
	v_and_b32_e32 v150, 0xffff0000, v54
	v_lshlrev_b32_e32 v155, 16, v55
	v_and_b32_e32 v151, 0xffff0000, v55
	v_lshlrev_b32_e32 v152, 16, v56
	v_and_b32_e32 v148, 0xffff0000, v56
	v_lshlrev_b32_e32 v153, 16, v57
	v_and_b32_e32 v149, 0xffff0000, v57
	s_or_b64 exec, exec, s[0:1]
	v_mov_b32_e32 v146, 1.0
	v_mov_b32_e32 v141, 1.0
	v_mov_b32_e32 v147, 1.0
	v_mov_b32_e32 v144, 1.0
	v_mov_b32_e32 v142, 1.0
	v_mov_b32_e32 v145, 1.0
	v_mov_b32_e32 v143, 1.0
	s_and_saveexec_b64 s[0:1], s[34:35]
	v_lshlrev_b32_e32 v140, 16, v50
	v_and_b32_e32 v146, 0xffff0000, v50
	v_lshlrev_b32_e32 v141, 16, v51
	v_and_b32_e32 v147, 0xffff0000, v51
	v_lshlrev_b32_e32 v144, 16, v52
	v_and_b32_e32 v142, 0xffff0000, v52
	v_lshlrev_b32_e32 v145, 16, v53
	v_and_b32_e32 v143, 0xffff0000, v53
	s_or_b64 exec, exec, s[0:1]
	s_or_b32 s0, s8, 5
	s_ashr_i32 s1, s0, 31
	s_lshl_b64 s[14:15], s[0:1], 11
	s_add_u32 s20, s29, s14
	s_addc_u32 s21, s30, s15
	global_load_dwordx4 v[106:109], v0, s[20:21] nt
	s_and_saveexec_b64 s[22:23], s[38:39]
	s_xor_b64 s[22:23], exec, s[22:23]
	s_cbranch_execz .LBB0_761
	v_mad_i64_i32 v[58:59], s[44:45], s0, v252, v[124:125]
	v_mad_i64_i32 v[62:63], s[44:45], s0, v252, v[122:123]
	v_mad_i64_i32 v[66:67], s[44:45], s0, v252, v[120:121]
	s_lshl_b64 s[44:45], s[0:1], 5
	s_add_u32 s44, s26, s44
	s_addc_u32 s45, s27, s45
	v_lshl_add_u64 v[180:181], v[118:119], 2, s[44:45]
	v_add_co_u32_e32 v182, vcc, 0x100000, v180
	flat_load_dword v170, v[180:181]
	s_nop 0
	v_addc_co_u32_e32 v183, vcc, 0, v181, vcc
	flat_load_dword v171, v[182:183]
	v_add_co_u32_e32 v180, vcc, 0x200000, v180
	global_load_dwordx4 v[58:61], v[58:59], off nt
	s_nop 0
	v_addc_co_u32_e32 v181, vcc, 0, v181, vcc
	global_load_dwordx4 v[62:65], v[62:63], off nt
	s_nop 0
	global_load_dwordx4 v[66:69], v[66:67], off nt
	s_nop 0
	flat_load_dword v172, v[180:181]
	s_andn2_saveexec_b64 s[22:23], s[22:23]
	s_cbranch_execnz .LBB0_762

; __device__ __forceinline__ unsigned pk2(float lo, float hi) { return f2bf(lo) | (f2bf(hi) << 16); }
; __device__ __forceinline__ void unpack8(const v4u w, float* f) { f[0] = bflo(w.x); f[1] = bfhi(w.x); f[2] = bflo(w.y); f[3] = bfhi(w.y); f[4] = bflo(w.z); f[5] = bfhi(w.z); f[6] = bflo(w.w); f[7] = bfhi(w.w); }
; __device__ __forceinline__ void norm_compute(const NormRow& R, int lane, v4u& ya, v4u& yc) {
;     ...
;     const float s_moba = wave_sum(lane < 32 ? sa : 0.f), s_fox = wave_sum((lane >= 32 ? sa : 0.f) + (lane < 16 ? sc : 0.f)), s_dil = wave_sum(lane >= 16 ? sc : 0.f);
;     const float r_moba = 1.0f / sqrtf(s_moba * (1.0f / 256.0f) + EPS), r_fox = 1.0f / sqrtf(s_fox * (1.0f / 384.0f) + EPS), r_dil = 1.0f / sqrtf(s_dil * (1.0f / 384.0f) + EPS);
;     float ga[8], gc[8];
; #pragma unroll
;     for (int e = 0; e < 8; ++e) { ga[e] = 1.f; gc[e] = 1.f; }
;     if (lane >= 32) unpack8(R.ga, ga);
;     if (lane < 16) unpack8(R.gc, gc);
;     const float ra = lane < 32 ? r_moba : r_fox, rc = lane < 16 ? r_fox : r_dil;
;     ya.x = pk2(fa[0] * ra * ga[0], fa[1] * ra * ga[1]); ya.y = pk2(fa[2] * ra * ga[2], fa[3] * ra * ga[3]); ya.z = pk2(fa[4] * ra * ga[4], fa[5] * ra * ga[5]); ya.w = pk2(fa[6] * ra * ga[6], fa[7] * ra * ga[7]);
;     yc.x = pk2(fc[0] * rc * gc[0], fc[1] * rc * gc[1]); yc.y = pk2(fc[2] * rc * gc[2], fc[3] * rc * gc[3]); yc.z = pk2(fc[4] * rc * gc[4], fc[5] * rc * gc[5]); yc.w = pk2(fc[6] * rc * gc[6], fc[7] * rc * gc[7]);
; }
.LBB0_119:
	s_or_b64 exec, exec, s[20:21]
	s_waitcnt lgkmcnt(0)
	v_add_f32_e32 v178, v178, v179
	v_fmamk_f32 v178, v178, 0x3b2aaaab, v215
	v_mul_f32_e32 v179, 0x4f800000, v178
	v_cmp_gt_f32_e32 vcc, s3, v178
	v_add_f32_e32 v176, v176, v177
	v_fmamk_f32 v176, v176, 0x3b2aaaab, v215
	v_cndmask_b32_e32 v178, v178, v179, vcc
	v_sqrt_f32_e32 v179, v178
	v_mul_f32_e32 v177, 0x4f800000, v176
	v_add_f32_e32 v156, v156, v157
	v_fmamk_f32 v156, v156, 0x3b800000, v215
	v_add_u32_e32 v180, -1, v179
	v_fma_f32 v182, -v180, v179, v178
	v_add_u32_e32 v181, 1, v179
	v_cmp_ge_f32_e64 s[0:1], 0, v182
	v_mul_f32_e32 v157, 0x4f800000, v156
	s_nop 0
	v_cndmask_b32_e64 v180, v179, v180, s[0:1]
	v_fma_f32 v179, -v181, v179, v178
	v_cmp_lt_f32_e64 s[0:1], 0, v179
	s_nop 1
	v_cndmask_b32_e64 v179, v180, v181, s[0:1]
	v_cmp_gt_f32_e64 s[0:1], s3, v176
	v_mul_f32_e32 v180, 0x37800000, v179
	v_cndmask_b32_e32 v179, v179, v180, vcc
	v_cndmask_b32_e64 v176, v176, v177, s[0:1]
	v_sqrt_f32_e32 v177, v176
	v_cmp_class_f32_e32 vcc, v178, v216
	s_nop 1
	v_cndmask_b32_e32 v178, v179, v178, vcc
	v_add_u32_e32 v179, -1, v177
	v_fma_f32 v180, -v179, v177, v176
	v_cmp_ge_f32_e32 vcc, 0, v180
	v_add_u32_e32 v180, 1, v177
	s_nop 0
	v_cndmask_b32_e32 v179, v177, v179, vcc
	v_fma_f32 v177, -v180, v177, v176
	v_cmp_lt_f32_e32 vcc, 0, v177
	s_nop 1
	v_cndmask_b32_e32 v177, v179, v180, vcc
	v_cmp_gt_f32_e32 vcc, s3, v156
	v_mul_f32_e32 v179, 0x37800000, v177
	v_cndmask_b32_e64 v177, v177, v179, s[0:1]
	v_cndmask_b32_e32 v156, v156, v157, vcc
	v_sqrt_f32_e32 v157, v156
	v_cmp_class_f32_e64 s[0:1], v176, v216
	s_nop 1
	v_cndmask_b32_e64 v176, v177, v176, s[0:1]
	v_add_u32_e32 v177, -1, v157
	v_fma_f32 v179, -v177, v157, v156
	v_cmp_ge_f32_e64 s[0:1], 0, v179
	v_add_u32_e32 v179, 1, v157
	s_nop 0
	v_cndmask_b32_e64 v177, v157, v177, s[0:1]
	v_fma_f32 v157, -v179, v157, v156
	v_cmp_lt_f32_e64 s[0:1], 0, v157
	s_nop 1
	v_cndmask_b32_e64 v157, v177, v179, s[0:1]
	v_div_scale_f32 v179, s[0:1], v178, v178, 1.0
	v_rcp_f32_e32 v180, v179
	v_mul_f32_e32 v177, 0x37800000, v157
	v_cndmask_b32_e32 v157, v157, v177, vcc
	v_cmp_class_f32_e32 vcc, v156, v216
	s_nop 1
	v_cndmask_b32_e32 v156, v157, v156, vcc
	v_fma_f32 v157, -v179, v180, 1.0
	v_fmac_f32_e32 v180, v157, v180
	v_div_scale_f32 v157, vcc, 1.0, v178, 1.0
	v_mul_f32_e32 v177, v157, v180
	v_fma_f32 v181, -v179, v177, v157
	v_fmac_f32_e32 v177, v181, v180
	v_fma_f32 v157, -v179, v177, v157
	v_div_scale_f32 v179, s[0:1], v176, v176, 1.0
	v_rcp_f32_e32 v181, v179
	v_div_fmas_f32 v157, v157, v180, v177
	v_div_fixup_f32 v157, v157, v178, 1.0
	v_fma_f32 v177, -v179, v181, 1.0
	v_fmac_f32_e32 v181, v177, v181
	v_div_scale_f32 v177, vcc, 1.0, v176, 1.0
	v_mul_f32_e32 v178, v177, v181
	v_fma_f32 v180, -v179, v178, v177
	v_fmac_f32_e32 v178, v180, v181
	v_fma_f32 v177, -v179, v178, v177
	v_div_scale_f32 v179, s[0:1], v156, v156, 1.0
	v_rcp_f32_e32 v180, v179
	v_div_fmas_f32 v177, v177, v181, v178
	v_div_fixup_f32 v176, v177, v176, 1.0
	s_movk_i32 s1, 0x7fff
	v_fma_f32 v177, -v179, v180, 1.0
	v_fmac_f32_e32 v180, v177, v180
	v_div_scale_f32 v177, vcc, 1.0, v156, 1.0
	v_mul_f32_e32 v178, v177, v180
	v_fma_f32 v181, -v179, v178, v177
	v_fmac_f32_e32 v178, v181, v180
	v_fma_f32 v177, -v179, v178, v177
	v_div_fmas_f32 v177, v177, v180, v178
	v_div_fixup_f32 v156, v177, v156, 1.0
	v_cndmask_b32_e64 v156, v176, v156, s[40:41]
	v_mul_f32_e32 v132, v156, v132
	v_mul_f32_e32 v133, v156, v133
	v_mul_f32_e32 v134, v156, v134
	v_mul_f32_e32 v135, v156, v135
	v_mul_f32_e32 v138, v156, v138
	v_mul_f32_e32 v139, v156, v139
	v_mul_f32_e32 v132, v132, v150
	v_mul_f32_e32 v133, v133, v151
	v_mul_f32_e32 v136, v156, v136
	v_mul_f32_e32 v137, v156, v137
	v_mul_f32_e32 v134, v134, v148
	v_mul_f32_e32 v135, v135, v149
	v_mul_f32_e32 v138, v138, v154
	v_mul_f32_e32 v139, v139, v155
	v_mul_f32_e32 v136, v136, v152
	v_mul_f32_e32 v137, v137, v153
	v_bfe_u32 v148, v135, 16, 1
	v_bfe_u32 v149, v134, 16, 1
	v_bfe_u32 v150, v133, 16, 1
	v_bfe_u32 v151, v132, 16, 1
	v_cndmask_b32_e64 v176, v157, v176, s[34:35]
	v_add3_u32 v132, v132, v151, s1
	v_add3_u32 v133, v133, v150, s1
	v_add3_u32 v134, v134, v149, s1
	v_add3_u32 v135, v135, v148, s1
	v_bfe_u32 v148, v138, 16, 1
	v_bfe_u32 v149, v139, 16, 1
	v_bfe_u32 v150, v136, 16, 1
	v_bfe_u32 v151, v137, 16, 1
	v_add3_u32 v137, v137, v151, s1
	v_add3_u32 v136, v136, v150, s1
	v_add3_u32 v139, v139, v149, s1
	v_add3_u32 v138, v138, v148, s1
	v_mul_f32_e32 v114, v114, v176
	v_mul_f32_e32 v115, v115, v176
	v_mul_f32_e32 v116, v116, v176
	v_mul_f32_e32 v117, v117, v176
	v_lshrrev_b32_e32 v138, 16, v138
	v_lshrrev_b32_e32 v139, 16, v139
	v_lshrrev_b32_e32 v136, 16, v136
	v_lshrrev_b32_e32 v137, 16, v137
	s_mov_b32 s0, 0xffff0000
	v_mul_f32_e32 v130, v130, v176
	v_mul_f32_e32 v131, v131, v176
	v_mul_f32_e32 v114, v114, v146
	v_mul_f32_e32 v115, v115, v147
	v_mul_f32_e32 v128, v128, v176
	v_mul_f32_e32 v129, v129, v176
	v_mul_f32_e32 v116, v116, v142
	v_mul_f32_e32 v117, v117, v143
	v_and_or_b32 v135, v135, s0, v137
	v_and_or_b32 v134, v134, s0, v136
	v_and_or_b32 v133, v133, s0, v139
	v_and_or_b32 v132, v132, s0, v138
	v_mul_f32_e32 v130, v130, v140
	v_mul_f32_e32 v131, v131, v141
	v_mul_f32_e32 v128, v128, v144
	v_mul_f32_e32 v129, v129, v145
	v_bfe_u32 v136, v117, 16, 1
	v_bfe_u32 v137, v116, 16, 1
	v_bfe_u32 v138, v115, 16, 1
	v_bfe_u32 v139, v114, 16, 1
	v_add3_u32 v114, v114, v139, s1
	v_add3_u32 v115, v115, v138, s1
	v_add3_u32 v116, v116, v137, s1
	v_add3_u32 v117, v117, v136, s1
	v_bfe_u32 v136, v130, 16, 1
	v_bfe_u32 v137, v131, 16, 1
	v_bfe_u32 v138, v128, 16, 1
	v_bfe_u32 v139, v129, 16, 1
	v_add3_u32 v129, v129, v139, s1
	v_add3_u32 v128, v128, v138, s1
	v_add3_u32 v131, v131, v137, s1
	v_add3_u32 v130, v130, v136, s1
	v_lshrrev_b32_e32 v130, 16, v130
	v_lshrrev_b32_e32 v131, 16, v131
	v_lshrrev_b32_e32 v128, 16, v128
	v_lshrrev_b32_e32 v129, 16, v129
	v_and_or_b32 v117, v117, s0, v129
	v_and_or_b32 v116, v116, s0, v128
	v_and_or_b32 v115, v115, s0, v131
	v_and_or_b32 v114, v114, s0, v130
	s_add_u32 s0, s24, s16
	s_addc_u32 s1, s25, s17
	global_store_dwordx4 v0, v[132:135], s[0:1]
	global_store_dwordx4 v0, v[114:117], s[0:1] offset:1024
	s_and_saveexec_b64 s[0:1], s[38:39]
	s_xor_b64 s[0:1], exec, s[0:1]
	s_cbranch_execz .LBB0_121
; __device__ __forceinline__ void unpack8(const v4u w, float* f) { f[0] = bflo(w.x); f[1] = bfhi(w.x); f[2] = bflo(w.y); f[3] = bfhi(w.y); f[4] = bflo(w.z); f[5] = bfhi(w.z); f[6] = bflo(w.w); f[7] = bfhi(w.w); }
; __device__ __forceinline__ void norm_compute(const NormRow& R, int lane, v4u& ya, v4u& yc) {
;     ...
;     else { float f0[8], f1[8], f2[8]; unpack8(R.d0, f0); unpack8(R.d1, f1); unpack8(R.d2, f2);
;         const float inv = 1.0f / (R.l0 + R.l1 + R.l2);
; #pragma unroll
;         for (int e = 0; e < 8; ++e) fc[e] = (f0[e] + f1[e] + f2[e]) * inv; }
	v_add_f32_e32 v114, v168, v167
	v_add_f32_e32 v114, v169, v114
	v_div_scale_f32 v115, s[16:17], v114, v114, 1.0
	v_rcp_f32_e32 v130, v115
	v_lshlrev_b32_e32 v134, 16, v42
	v_and_b32_e32 v135, 0xffff0000, v42
	v_lshlrev_b32_e32 v136, 16, v43
	v_fma_f32 v131, -v115, v130, 1.0
	v_fmac_f32_e32 v130, v131, v130
	v_div_scale_f32 v131, vcc, 1.0, v114, 1.0
	v_mul_f32_e32 v132, v131, v130
	v_fma_f32 v133, -v115, v132, v131
	v_fmac_f32_e32 v132, v133, v130
	v_fma_f32 v115, -v115, v132, v131
	v_div_fmas_f32 v115, v115, v130, v132
	v_div_fixup_f32 v130, v115, v114, 1.0
	v_lshlrev_b32_e32 v114, 16, v34
	v_and_b32_e32 v115, 0xffff0000, v34
	v_lshlrev_b32_e32 v132, 16, v38
	v_and_b32_e32 v133, 0xffff0000, v38
	v_add_f32_e32 v114, v132, v114
	v_add_f32_e32 v115, v133, v115
	v_and_b32_e32 v137, 0xffff0000, v43
	v_add_f32_e32 v114, v114, v134
	v_add_f32_e32 v115, v115, v135
	v_lshlrev_b32_e32 v134, 16, v39
	v_mul_f32_e32 v132, v130, v114
	v_mul_f32_e32 v133, v130, v115
	v_lshlrev_b32_e32 v114, 16, v35
	v_and_b32_e32 v115, 0xffff0000, v35
	v_and_b32_e32 v135, 0xffff0000, v39
	v_add_f32_e32 v114, v134, v114
	v_add_f32_e32 v115, v135, v115
	v_lshlrev_b32_e32 v116, 16, v37
	v_lshlrev_b32_e32 v128, 16, v41
	v_and_b32_e32 v117, 0xffff0000, v37
	v_and_b32_e32 v129, 0xffff0000, v41
	v_add_f32_e32 v114, v114, v136
	v_add_f32_e32 v115, v115, v137
	v_lshlrev_b32_e32 v134, 16, v36
	v_and_b32_e32 v135, 0xffff0000, v36
	v_lshlrev_b32_e32 v136, 16, v40
	v_and_b32_e32 v137, 0xffff0000, v40
	v_lshlrev_b32_e32 v138, 16, v44
	v_and_b32_e32 v139, 0xffff0000, v44
	v_add_f32_e32 v134, v136, v134
	v_add_f32_e32 v135, v137, v135
	v_lshlrev_b32_e32 v136, 16, v45
	v_and_b32_e32 v137, 0xffff0000, v45
	v_add_f32_e32 v116, v128, v116
	v_add_f32_e32 v117, v129, v117
	v_add_f32_e32 v134, v134, v138
	v_add_f32_e32 v135, v135, v139
	v_add_f32_e32 v116, v116, v136
	v_add_f32_e32 v117, v117, v137
	v_mul_f32_e32 v114, v130, v114
	v_mul_f32_e32 v115, v130, v115
	v_mul_f32_e32 v134, v130, v134
	v_mul_f32_e32 v135, v130, v135
	v_mul_f32_e32 v116, v130, v116
	v_mul_f32_e32 v117, v130, v117
	v_mov_b32_e32 v129, v116
	v_mov_b32_e32 v116, v135
	v_mov_b32_e32 v128, v134
	v_mov_b32_e32 v131, v114
	v_mov_b32_e32 v114, v133
	v_mov_b32_e32 v130, v132
; #define GAS __attribute__((address_space(1)))
; __device__ __forceinline__ void unpack8(const v4u w, float* f) { f[0] = bflo(w.x); f[1] = bfhi(w.x); f[2] = bflo(w.y); f[3] = bfhi(w.y); f[4] = bflo(w.z); f[5] = bfhi(w.z); f[6] = bflo(w.w); f[7] = bfhi(w.w); }
; __device__ __forceinline__ void norm_load(NormRow& R, int m, int lane, const bf16* O, const bf16* GF, const bf16* OD, const float* LD) {
;     R.oa = __builtin_nontemporal_load((const GAS v4u*)(O + (size_t)m * DM + 8 * lane));
;     if (lane < 16) { R.oc = __builtin_nontemporal_load((const GAS v4u*)(O + (size_t)m * DM + 512 + 8 * lane)); R.gc = __builtin_nontemporal_load((const GAS v4u*)(GF + (size_t)m * 384 + 256 + 8 * lane)); }
;     else { const int dc = 8 * lane - 128, hd = dc >> 6;
;         R.d0 = __builtin_nontemporal_load((const GAS v4u*)(OD + (size_t)m * 384 + dc)); R.d1 = __builtin_nontemporal_load((const GAS v4u*)(OD + OD_BRANCH + (size_t)m * 384 + dc)); R.d2 = __builtin_nontemporal_load((const GAS v4u*)(OD + 2 * OD_BRANCH + (size_t)m * 384 + dc));
;         R.l0 = LD[(size_t)m * 8 + hd]; R.l1 = LD[LD_BRANCH + (size_t)m * 8 + hd]; R.l2 = LD[2 * LD_BRANCH + (size_t)m * 8 + hd]; }
;     if (lane >= 32) R.ga = __builtin_nontemporal_load((const GAS v4u*)(GF + (size_t)m * 384 + 8 * lane - 256));
; __device__ __forceinline__ void norm_compute(const NormRow& R, int lane, v4u& ya, v4u& yc) {
;     float fa[8], fc[8];
;     unpack8(R.oa, fa);
;     if (lane < 16) unpack8(R.oc, fc);
;     else { float f0[8], f1[8], f2[8]; unpack8(R.d0, f0); unpack8(R.d1, f1); unpack8(R.d2, f2);
;         const float inv = 1.0f / (R.l0 + R.l1 + R.l2);
; #pragma unroll
;         for (int e = 0; e < 8; ++e) fc[e] = (f0[e] + f1[e] + f2[e]) * inv; }
;     float sa = 0.f, sc = 0.f;
; #pragma unroll
;     for (int e = 0; e < 8; ++e) { sa += fa[e] * fa[e]; sc += fc[e] * fc[e]; }
;     const float s_moba = wave_sum(lane < 32 ? sa : 0.f), s_fox = wave_sum((lane >= 32 ? sa : 0.f) + (lane < 16 ? sc : 0.f)), s_dil = wave_sum(lane >= 16 ? sc : 0.f);
;     const float r_moba = 1.0f / sqrtf(s_moba * (1.0f / 256.0f) + EPS), r_fox = 1.0f / sqrtf(s_fox * (1.0f / 384.0f) + EPS), r_dil = 1.0f / sqrtf(s_dil * (1.0f / 384.0f) + EPS);
;     float ga[8], gc[8];
; #pragma unroll
;     for (int e = 0; e < 8; ++e) { ga[e] = 1.f; gc[e] = 1.f; }
;     if (lane >= 32) unpack8(R.ga, ga);
;     if (lane < 16) unpack8(R.gc, gc);
.LBB0_121:
	s_andn2_saveexec_b64 s[0:1], s[0:1]
	v_lshlrev_b32_e32 v130, 16, v46
	v_and_b32_e32 v114, 0xffff0000, v46
	v_lshlrev_b32_e32 v131, 16, v47
	v_and_b32_e32 v115, 0xffff0000, v47
	v_lshlrev_b32_e32 v128, 16, v48
	v_and_b32_e32 v116, 0xffff0000, v48
	v_lshlrev_b32_e32 v129, 16, v49
	v_and_b32_e32 v117, 0xffff0000, v49
	s_or_b64 exec, exec, s[0:1]
	v_lshlrev_b32_e32 v139, 16, v111
	v_lshlrev_b32_e32 v138, 16, v110
	v_and_b32_e32 v133, 0xffff0000, v111
	v_and_b32_e32 v132, 0xffff0000, v110
	v_lshlrev_b32_e32 v137, 16, v113
	v_lshlrev_b32_e32 v136, 16, v112
	v_and_b32_e32 v135, 0xffff0000, v113
	v_and_b32_e32 v134, 0xffff0000, v112
	v_mul_f32_e32 v110, v138, v138
	v_mul_f32_e32 v111, v139, v139
	v_mul_f32_e32 v112, v132, v132
	v_mul_f32_e32 v113, v133, v133
	v_mul_f32_e32 v144, v114, v114
	v_fmac_f32_e32 v144, v130, v130
	v_add_f32_e32 v110, v110, v112
	v_fmac_f32_e32 v144, v131, v131
	v_add_f32_e32 v110, v111, v110
	v_fmac_f32_e32 v144, v115, v115
	v_mul_f32_e32 v140, v136, v136
	v_mul_f32_e32 v141, v137, v137
	v_add_f32_e32 v110, v113, v110
	v_fmac_f32_e32 v144, v128, v128
	v_mul_f32_e32 v142, v134, v134
	v_mul_f32_e32 v143, v135, v135
	v_add_f32_e32 v110, v140, v110
	v_fmac_f32_e32 v144, v116, v116
	v_add_f32_e32 v110, v142, v110
	v_fmac_f32_e32 v144, v129, v129
	v_add_f32_e32 v110, v141, v110
	v_add_f32_e32 v110, v143, v110
	v_fmac_f32_e32 v144, v117, v117
	v_cndmask_b32_e64 v111, 0, v110, s[40:41]
	v_cndmask_b32_e64 v110, 0, v110, s[36:37]
	v_cndmask_b32_e64 v113, 0, v144, s[34:35]
	v_add_f32_e32 v110, v110, v113
	v_cndmask_b32_e64 v140, 0, v144, s[42:43]
	ds_bpermute_b32 v112, v164, v111
	ds_bpermute_b32 v113, v164, v110
	ds_bpermute_b32 v141, v164, v140
	v_mov_b32_e32 v154, 1.0
	v_mov_b32_e32 v150, 1.0
	s_waitcnt lgkmcnt(0)
	v_add_f32_e32 v111, v111, v112
	v_add_f32_e32 v110, v110, v113
	v_add_f32_e32 v140, v140, v141
	ds_bpermute_b32 v112, v162, v111
	ds_bpermute_b32 v113, v162, v110
	ds_bpermute_b32 v141, v162, v140
	v_mov_b32_e32 v155, 1.0
	v_mov_b32_e32 v151, 1.0
	s_waitcnt lgkmcnt(0)
	v_add_f32_e32 v111, v111, v112
	v_add_f32_e32 v110, v110, v113
	v_add_f32_e32 v140, v140, v141
	ds_bpermute_b32 v112, v161, v111
	ds_bpermute_b32 v113, v161, v110
	ds_bpermute_b32 v141, v161, v140
	v_mov_b32_e32 v152, 1.0
	v_mov_b32_e32 v148, 1.0
	s_waitcnt lgkmcnt(0)
	v_add_f32_e32 v111, v111, v112
	v_add_f32_e32 v110, v110, v113
	v_add_f32_e32 v140, v140, v141
	ds_bpermute_b32 v112, v160, v111
	ds_bpermute_b32 v113, v160, v110
	ds_bpermute_b32 v141, v160, v140
	v_mov_b32_e32 v153, 1.0
	v_mov_b32_e32 v149, 1.0
	s_waitcnt lgkmcnt(0)
	v_add_f32_e32 v111, v111, v112
	v_add_f32_e32 v110, v110, v113
	v_add_f32_e32 v140, v140, v141
	ds_bpermute_b32 v112, v159, v111
	ds_bpermute_b32 v113, v159, v110
	ds_bpermute_b32 v141, v159, v140
	s_waitcnt lgkmcnt(0)
	v_add_f32_e32 v156, v111, v112
	v_add_f32_e32 v176, v110, v113
	v_add_f32_e32 v178, v140, v141
	ds_bpermute_b32 v157, v158, v156
	ds_bpermute_b32 v177, v158, v176
	ds_bpermute_b32 v179, v158, v178
	v_mov_b32_e32 v140, 1.0
	s_and_saveexec_b64 s[0:1], s[36:37]
	v_lshlrev_b32_e32 v154, 16, v30
	v_and_b32_e32 v150, 0xffff0000, v30
	v_lshlrev_b32_e32 v155, 16, v31
	v_and_b32_e32 v151, 0xffff0000, v31
	v_lshlrev_b32_e32 v152, 16, v32
	v_and_b32_e32 v148, 0xffff0000, v32
	v_lshlrev_b32_e32 v153, 16, v33
	v_and_b32_e32 v149, 0xffff0000, v33
	s_or_b64 exec, exec, s[0:1]
	v_mov_b32_e32 v146, 1.0
	v_mov_b32_e32 v141, 1.0
	v_mov_b32_e32 v147, 1.0
	v_mov_b32_e32 v144, 1.0
	v_mov_b32_e32 v142, 1.0
	v_mov_b32_e32 v145, 1.0
	v_mov_b32_e32 v143, 1.0
	s_and_saveexec_b64 s[0:1], s[34:35]
	v_lshlrev_b32_e32 v140, 16, v26
	v_and_b32_e32 v146, 0xffff0000, v26
	v_lshlrev_b32_e32 v141, 16, v27
	v_and_b32_e32 v147, 0xffff0000, v27
	v_lshlrev_b32_e32 v144, 16, v28
	v_and_b32_e32 v142, 0xffff0000, v28
	v_lshlrev_b32_e32 v145, 16, v29
	v_and_b32_e32 v143, 0xffff0000, v29
	s_or_b64 exec, exec, s[0:1]
	s_or_b32 s0, s8, 6
	s_ashr_i32 s1, s0, 31
	s_lshl_b64 s[16:17], s[0:1], 11
	s_add_u32 s20, s29, s16
	s_addc_u32 s21, s30, s17
	global_load_dwordx4 v[110:113], v0, s[20:21] nt
	s_and_saveexec_b64 s[22:23], s[38:39]
	s_xor_b64 s[22:23], exec, s[22:23]
	s_cbranch_execz .LBB0_763
	v_mad_i64_i32 v[34:35], s[44:45], s0, v252, v[124:125]
	v_mad_i64_i32 v[38:39], s[44:45], s0, v252, v[122:123]
	v_mad_i64_i32 v[42:43], s[44:45], s0, v252, v[120:121]
	s_lshl_b64 s[44:45], s[0:1], 5
	s_add_u32 s44, s26, s44
	s_addc_u32 s45, s27, s45
	v_lshl_add_u64 v[180:181], v[118:119], 2, s[44:45]
	v_add_co_u32_e32 v168, vcc, 0x100000, v180
	flat_load_dword v167, v[180:181]
	s_nop 0
	v_addc_co_u32_e32 v169, vcc, 0, v181, vcc
	flat_load_dword v168, v[168:169]
	v_add_co_u32_e32 v180, vcc, 0x200000, v180
	global_load_dwordx4 v[34:37], v[34:35], off nt
	s_nop 0
	v_addc_co_u32_e32 v181, vcc, 0, v181, vcc
	global_load_dwordx4 v[38:41], v[38:39], off nt
	s_nop 0
	global_load_dwordx4 v[42:45], v[42:43], off nt
	s_nop 0
	flat_load_dword v169, v[180:181]
	s_andn2_saveexec_b64 s[22:23], s[22:23]
	s_cbranch_execnz .LBB0_764

; __device__ __forceinline__ unsigned pk2(float lo, float hi) { return f2bf(lo) | (f2bf(hi) << 16); }
; __device__ __forceinline__ void unpack8(const v4u w, float* f) { f[0] = bflo(w.x); f[1] = bfhi(w.x); f[2] = bflo(w.y); f[3] = bfhi(w.y); f[4] = bflo(w.z); f[5] = bfhi(w.z); f[6] = bflo(w.w); f[7] = bfhi(w.w); }
; __device__ __forceinline__ void norm_compute(const NormRow& R, int lane, v4u& ya, v4u& yc) {
;     ...
;     const float s_moba = wave_sum(lane < 32 ? sa : 0.f), s_fox = wave_sum((lane >= 32 ? sa : 0.f) + (lane < 16 ? sc : 0.f)), s_dil = wave_sum(lane >= 16 ? sc : 0.f);
;     const float r_moba = 1.0f / sqrtf(s_moba * (1.0f / 256.0f) + EPS), r_fox = 1.0f / sqrtf(s_fox * (1.0f / 384.0f) + EPS), r_dil = 1.0f / sqrtf(s_dil * (1.0f / 384.0f) + EPS);
;     float ga[8], gc[8];
; #pragma unroll
;     for (int e = 0; e < 8; ++e) { ga[e] = 1.f; gc[e] = 1.f; }
;     if (lane >= 32) unpack8(R.ga, ga);
;     if (lane < 16) unpack8(R.gc, gc);
;     const float ra = lane < 32 ? r_moba : r_fox, rc = lane < 16 ? r_fox : r_dil;
;     ya.x = pk2(fa[0] * ra * ga[0], fa[1] * ra * ga[1]); ya.y = pk2(fa[2] * ra * ga[2], fa[3] * ra * ga[3]); ya.z = pk2(fa[4] * ra * ga[4], fa[5] * ra * ga[5]); ya.w = pk2(fa[6] * ra * ga[6], fa[7] * ra * ga[7]);
;     yc.x = pk2(fc[0] * rc * gc[0], fc[1] * rc * gc[1]); yc.y = pk2(fc[2] * rc * gc[2], fc[3] * rc * gc[3]); yc.z = pk2(fc[4] * rc * gc[4], fc[5] * rc * gc[5]); yc.w = pk2(fc[6] * rc * gc[6], fc[7] * rc * gc[7]);
; }
.LBB0_131:
	s_or_b64 exec, exec, s[20:21]
	s_waitcnt lgkmcnt(0)
	v_add_f32_e32 v178, v178, v179
	v_fmamk_f32 v178, v178, 0x3b2aaaab, v215
	v_mul_f32_e32 v179, 0x4f800000, v178
	v_cmp_gt_f32_e32 vcc, s3, v178
	v_add_f32_e32 v176, v176, v177
	v_fmamk_f32 v176, v176, 0x3b2aaaab, v215
	v_cndmask_b32_e32 v178, v178, v179, vcc
	v_sqrt_f32_e32 v179, v178
	v_mul_f32_e32 v177, 0x4f800000, v176
	v_add_f32_e32 v156, v156, v157
	v_fmamk_f32 v156, v156, 0x3b800000, v215
	v_add_u32_e32 v180, -1, v179
	v_fma_f32 v182, -v180, v179, v178
	v_add_u32_e32 v181, 1, v179
	v_cmp_ge_f32_e64 s[0:1], 0, v182
	v_mul_f32_e32 v157, 0x4f800000, v156
	s_nop 0
	v_cndmask_b32_e64 v180, v179, v180, s[0:1]
	v_fma_f32 v179, -v181, v179, v178
	v_cmp_lt_f32_e64 s[0:1], 0, v179
	s_nop 1
	v_cndmask_b32_e64 v179, v180, v181, s[0:1]
	v_cmp_gt_f32_e64 s[0:1], s3, v176
	v_mul_f32_e32 v180, 0x37800000, v179
	v_cndmask_b32_e32 v179, v179, v180, vcc
	v_cndmask_b32_e64 v176, v176, v177, s[0:1]
	v_sqrt_f32_e32 v177, v176
	v_cmp_class_f32_e32 vcc, v178, v216
	s_nop 1
	v_cndmask_b32_e32 v178, v179, v178, vcc
	v_add_u32_e32 v179, -1, v177
	v_fma_f32 v180, -v179, v177, v176
	v_cmp_ge_f32_e32 vcc, 0, v180
	v_add_u32_e32 v180, 1, v177
	s_nop 0
	v_cndmask_b32_e32 v179, v177, v179, vcc
	v_fma_f32 v177, -v180, v177, v176
	v_cmp_lt_f32_e32 vcc, 0, v177
	s_nop 1
	v_cndmask_b32_e32 v177, v179, v180, vcc
	v_cmp_gt_f32_e32 vcc, s3, v156
	v_mul_f32_e32 v179, 0x37800000, v177
	v_cndmask_b32_e64 v177, v177, v179, s[0:1]
	v_cndmask_b32_e32 v156, v156, v157, vcc
	v_sqrt_f32_e32 v157, v156
	v_cmp_class_f32_e64 s[0:1], v176, v216
	s_nop 1
	v_cndmask_b32_e64 v176, v177, v176, s[0:1]
	v_add_u32_e32 v177, -1, v157
	v_fma_f32 v179, -v177, v157, v156
	v_cmp_ge_f32_e64 s[0:1], 0, v179
	v_add_u32_e32 v179, 1, v157
	s_nop 0
	v_cndmask_b32_e64 v177, v157, v177, s[0:1]
	v_fma_f32 v157, -v179, v157, v156
	v_cmp_lt_f32_e64 s[0:1], 0, v157
	s_nop 1
	v_cndmask_b32_e64 v157, v177, v179, s[0:1]
	v_div_scale_f32 v179, s[0:1], v178, v178, 1.0
	v_rcp_f32_e32 v180, v179
	v_mul_f32_e32 v177, 0x37800000, v157
	v_cndmask_b32_e32 v157, v157, v177, vcc
	v_cmp_class_f32_e32 vcc, v156, v216
	s_nop 1
	v_cndmask_b32_e32 v156, v157, v156, vcc
	v_fma_f32 v157, -v179, v180, 1.0
	v_fmac_f32_e32 v180, v157, v180
	v_div_scale_f32 v157, vcc, 1.0, v178, 1.0
	v_mul_f32_e32 v177, v157, v180
	v_fma_f32 v181, -v179, v177, v157
	v_fmac_f32_e32 v177, v181, v180
	v_fma_f32 v157, -v179, v177, v157
	v_div_scale_f32 v179, s[0:1], v176, v176, 1.0
	v_rcp_f32_e32 v181, v179
	v_div_fmas_f32 v157, v157, v180, v177
	v_div_fixup_f32 v157, v157, v178, 1.0
	v_fma_f32 v177, -v179, v181, 1.0
	v_fmac_f32_e32 v181, v177, v181
	v_div_scale_f32 v177, vcc, 1.0, v176, 1.0
	v_mul_f32_e32 v178, v177, v181
	v_fma_f32 v180, -v179, v178, v177
	v_fmac_f32_e32 v178, v180, v181
	v_fma_f32 v177, -v179, v178, v177
	v_div_scale_f32 v179, s[0:1], v156, v156, 1.0
	v_rcp_f32_e32 v180, v179
	v_div_fmas_f32 v177, v177, v181, v178
	v_div_fixup_f32 v176, v177, v176, 1.0
	s_movk_i32 s1, 0x7fff
	v_fma_f32 v177, -v179, v180, 1.0
	v_fmac_f32_e32 v180, v177, v180
	v_div_scale_f32 v177, vcc, 1.0, v156, 1.0
	v_mul_f32_e32 v178, v177, v180
	v_fma_f32 v181, -v179, v178, v177
	v_fmac_f32_e32 v178, v181, v180
	v_fma_f32 v177, -v179, v178, v177
	v_div_fmas_f32 v177, v177, v180, v178
	v_div_fixup_f32 v156, v177, v156, 1.0
	v_cndmask_b32_e64 v156, v176, v156, s[40:41]
	v_mul_f32_e32 v132, v156, v132
	v_mul_f32_e32 v133, v156, v133
	v_mul_f32_e32 v134, v156, v134
	v_mul_f32_e32 v135, v156, v135
	v_mul_f32_e32 v138, v156, v138
	v_mul_f32_e32 v139, v156, v139
	v_mul_f32_e32 v132, v132, v150
	v_mul_f32_e32 v133, v133, v151
	v_mul_f32_e32 v136, v156, v136
	v_mul_f32_e32 v137, v156, v137
	v_mul_f32_e32 v134, v134, v148
	v_mul_f32_e32 v135, v135, v149
	v_mul_f32_e32 v138, v138, v154
	v_mul_f32_e32 v139, v139, v155
	v_mul_f32_e32 v136, v136, v152
	v_mul_f32_e32 v137, v137, v153
	v_bfe_u32 v148, v135, 16, 1
	v_bfe_u32 v149, v134, 16, 1
	v_bfe_u32 v150, v133, 16, 1
	v_bfe_u32 v151, v132, 16, 1
	v_cndmask_b32_e64 v176, v157, v176, s[34:35]
	v_add3_u32 v132, v132, v151, s1
	v_add3_u32 v133, v133, v150, s1
	v_add3_u32 v134, v134, v149, s1
	v_add3_u32 v135, v135, v148, s1
	v_bfe_u32 v148, v138, 16, 1
	v_bfe_u32 v149, v139, 16, 1
	v_bfe_u32 v150, v136, 16, 1
	v_bfe_u32 v151, v137, 16, 1
	v_add3_u32 v137, v137, v151, s1
	v_add3_u32 v136, v136, v150, s1
	v_add3_u32 v139, v139, v149, s1
	v_add3_u32 v138, v138, v148, s1
	v_mul_f32_e32 v114, v114, v176
	v_mul_f32_e32 v115, v115, v176
	v_mul_f32_e32 v116, v116, v176
	v_mul_f32_e32 v117, v117, v176
	v_lshrrev_b32_e32 v138, 16, v138
	v_lshrrev_b32_e32 v139, 16, v139
	v_lshrrev_b32_e32 v136, 16, v136
	v_lshrrev_b32_e32 v137, 16, v137
	s_mov_b32 s0, 0xffff0000
	v_mul_f32_e32 v130, v130, v176
	v_mul_f32_e32 v131, v131, v176
	v_mul_f32_e32 v114, v114, v146
	v_mul_f32_e32 v115, v115, v147
	v_mul_f32_e32 v128, v128, v176
	v_mul_f32_e32 v129, v129, v176
	v_mul_f32_e32 v116, v116, v142
	v_mul_f32_e32 v117, v117, v143
	v_and_or_b32 v135, v135, s0, v137
	v_and_or_b32 v134, v134, s0, v136
	v_and_or_b32 v133, v133, s0, v139
	v_and_or_b32 v132, v132, s0, v138
	v_mul_f32_e32 v130, v130, v140
	v_mul_f32_e32 v131, v131, v141
	v_mul_f32_e32 v128, v128, v144
	v_mul_f32_e32 v129, v129, v145
	v_bfe_u32 v136, v117, 16, 1
	v_bfe_u32 v137, v116, 16, 1
	v_bfe_u32 v138, v115, 16, 1
	v_bfe_u32 v139, v114, 16, 1
	v_add3_u32 v114, v114, v139, s1
	v_add3_u32 v115, v115, v138, s1
	v_add3_u32 v116, v116, v137, s1
	v_add3_u32 v117, v117, v136, s1
	v_bfe_u32 v136, v130, 16, 1
	v_bfe_u32 v137, v131, 16, 1
	v_bfe_u32 v138, v128, 16, 1
	v_bfe_u32 v139, v129, 16, 1
	v_add3_u32 v129, v129, v139, s1
	v_add3_u32 v128, v128, v138, s1
	v_add3_u32 v131, v131, v137, s1
	v_add3_u32 v130, v130, v136, s1
	v_lshrrev_b32_e32 v130, 16, v130
	v_lshrrev_b32_e32 v131, 16, v131
	v_lshrrev_b32_e32 v128, 16, v128
	v_lshrrev_b32_e32 v129, 16, v129
	v_and_or_b32 v117, v117, s0, v129
	v_and_or_b32 v116, v116, s0, v128
	v_and_or_b32 v115, v115, s0, v131
	v_and_or_b32 v114, v114, s0, v130
	s_add_u32 s0, s24, s18
	s_addc_u32 s1, s25, s19
	global_store_dwordx4 v0, v[132:135], s[0:1]
	global_store_dwordx4 v0, v[114:117], s[0:1] offset:1024
	s_and_saveexec_b64 s[0:1], s[38:39]
	s_xor_b64 s[0:1], exec, s[0:1]
	s_cbranch_execz .LBB0_133
; __device__ __forceinline__ void unpack8(const v4u w, float* f) { f[0] = bflo(w.x); f[1] = bfhi(w.x); f[2] = bflo(w.y); f[3] = bfhi(w.y); f[4] = bflo(w.z); f[5] = bfhi(w.z); f[6] = bflo(w.w); f[7] = bfhi(w.w); }
; __device__ __forceinline__ void norm_compute(const NormRow& R, int lane, v4u& ya, v4u& yc) {
;     ...
;     else { float f0[8], f1[8], f2[8]; unpack8(R.d0, f0); unpack8(R.d1, f1); unpack8(R.d2, f2);
;         const float inv = 1.0f / (R.l0 + R.l1 + R.l2);
; #pragma unroll
;         for (int e = 0; e < 8; ++e) fc[e] = (f0[e] + f1[e] + f2[e]) * inv; }
	v_add_f32_e32 v114, v165, v163
	v_add_f32_e32 v114, v166, v114
	v_div_scale_f32 v115, s[18:19], v114, v114, 1.0
	v_rcp_f32_e32 v130, v115
	v_lshlrev_b32_e32 v134, 16, v18
	v_and_b32_e32 v135, 0xffff0000, v18
	v_lshlrev_b32_e32 v136, 16, v19
	v_fma_f32 v131, -v115, v130, 1.0
	v_fmac_f32_e32 v130, v131, v130
	v_div_scale_f32 v131, vcc, 1.0, v114, 1.0
	v_mul_f32_e32 v132, v131, v130
	v_fma_f32 v133, -v115, v132, v131
	v_fmac_f32_e32 v132, v133, v130
	v_fma_f32 v115, -v115, v132, v131
	v_div_fmas_f32 v115, v115, v130, v132
	v_div_fixup_f32 v130, v115, v114, 1.0
	v_lshlrev_b32_e32 v114, 16, v10
	v_and_b32_e32 v115, 0xffff0000, v10
	v_lshlrev_b32_e32 v132, 16, v14
	v_and_b32_e32 v133, 0xffff0000, v14
	v_add_f32_e32 v114, v132, v114
	v_add_f32_e32 v115, v133, v115
	v_and_b32_e32 v137, 0xffff0000, v19
	v_add_f32_e32 v114, v114, v134
	v_add_f32_e32 v115, v115, v135
	v_lshlrev_b32_e32 v134, 16, v15
	v_mul_f32_e32 v132, v130, v114
	v_mul_f32_e32 v133, v130, v115
	v_lshlrev_b32_e32 v114, 16, v11
	v_and_b32_e32 v115, 0xffff0000, v11
	v_and_b32_e32 v135, 0xffff0000, v15
	v_add_f32_e32 v114, v134, v114
	v_add_f32_e32 v115, v135, v115
	v_lshlrev_b32_e32 v116, 16, v13
	v_lshlrev_b32_e32 v128, 16, v17
	v_and_b32_e32 v117, 0xffff0000, v13
	v_and_b32_e32 v129, 0xffff0000, v17
	v_add_f32_e32 v114, v114, v136
	v_add_f32_e32 v115, v115, v137
	v_lshlrev_b32_e32 v134, 16, v12
	v_and_b32_e32 v135, 0xffff0000, v12
	v_lshlrev_b32_e32 v136, 16, v16
	v_and_b32_e32 v137, 0xffff0000, v16
	v_lshlrev_b32_e32 v138, 16, v20
	v_and_b32_e32 v139, 0xffff0000, v20
	v_add_f32_e32 v134, v136, v134
	v_add_f32_e32 v135, v137, v135
	v_lshlrev_b32_e32 v136, 16, v21
	v_and_b32_e32 v137, 0xffff0000, v21
	v_add_f32_e32 v116, v128, v116
	v_add_f32_e32 v117, v129, v117
	v_add_f32_e32 v134, v134, v138
	v_add_f32_e32 v135, v135, v139
	v_add_f32_e32 v116, v116, v136
	v_add_f32_e32 v117, v117, v137
	v_mul_f32_e32 v114, v130, v114
	v_mul_f32_e32 v115, v130, v115
	v_mul_f32_e32 v134, v130, v134
	v_mul_f32_e32 v135, v130, v135
	v_mul_f32_e32 v116, v130, v116
	v_mul_f32_e32 v117, v130, v117
	v_mov_b32_e32 v129, v116
	v_mov_b32_e32 v116, v135
	v_mov_b32_e32 v128, v134
	v_mov_b32_e32 v131, v114
	v_mov_b32_e32 v114, v133
	v_mov_b32_e32 v130, v132
; #define GAS __attribute__((address_space(1)))
; __device__ __forceinline__ void unpack8(const v4u w, float* f) { f[0] = bflo(w.x); f[1] = bfhi(w.x); f[2] = bflo(w.y); f[3] = bfhi(w.y); f[4] = bflo(w.z); f[5] = bfhi(w.z); f[6] = bflo(w.w); f[7] = bfhi(w.w); }
; __device__ __forceinline__ void norm_load(NormRow& R, int m, int lane, const bf16* O, const bf16* GF, const bf16* OD, const float* LD) {
;     R.oa = __builtin_nontemporal_load((const GAS v4u*)(O + (size_t)m * DM + 8 * lane));
;     if (lane < 16) { R.oc = __builtin_nontemporal_load((const GAS v4u*)(O + (size_t)m * DM + 512 + 8 * lane)); R.gc = __builtin_nontemporal_load((const GAS v4u*)(GF + (size_t)m * 384 + 256 + 8 * lane)); }
;     else { const int dc = 8 * lane - 128, hd = dc >> 6;
;         R.d0 = __builtin_nontemporal_load((const GAS v4u*)(OD + (size_t)m * 384 + dc)); R.d1 = __builtin_nontemporal_load((const GAS v4u*)(OD + OD_BRANCH + (size_t)m * 384 + dc)); R.d2 = __builtin_nontemporal_load((const GAS v4u*)(OD + 2 * OD_BRANCH + (size_t)m * 384 + dc));
;         R.l0 = LD[(size_t)m * 8 + hd]; R.l1 = LD[LD_BRANCH + (size_t)m * 8 + hd]; R.l2 = LD[2 * LD_BRANCH + (size_t)m * 8 + hd]; }
;     if (lane >= 32) R.ga = __builtin_nontemporal_load((const GAS v4u*)(GF + (size_t)m * 384 + 8 * lane - 256));
; __device__ __forceinline__ void norm_compute(const NormRow& R, int lane, v4u& ya, v4u& yc) {
;     float fa[8], fc[8];
;     unpack8(R.oa, fa);
;     if (lane < 16) unpack8(R.oc, fc);
;     else { float f0[8], f1[8], f2[8]; unpack8(R.d0, f0); unpack8(R.d1, f1); unpack8(R.d2, f2);
;         const float inv = 1.0f / (R.l0 + R.l1 + R.l2);
; #pragma unroll
;         for (int e = 0; e < 8; ++e) fc[e] = (f0[e] + f1[e] + f2[e]) * inv; }
;     float sa = 0.f, sc = 0.f;
; #pragma unroll
;     for (int e = 0; e < 8; ++e) { sa += fa[e] * fa[e]; sc += fc[e] * fc[e]; }
;     const float s_moba = wave_sum(lane < 32 ? sa : 0.f), s_fox = wave_sum((lane >= 32 ? sa : 0.f) + (lane < 16 ? sc : 0.f)), s_dil = wave_sum(lane >= 16 ? sc : 0.f);
;     const float r_moba = 1.0f / sqrtf(s_moba * (1.0f / 256.0f) + EPS), r_fox = 1.0f / sqrtf(s_fox * (1.0f / 384.0f) + EPS), r_dil = 1.0f / sqrtf(s_dil * (1.0f / 384.0f) + EPS);
;     float ga[8], gc[8];
; #pragma unroll
;     for (int e = 0; e < 8; ++e) { ga[e] = 1.f; gc[e] = 1.f; }
;     if (lane >= 32) unpack8(R.ga, ga);
;     if (lane < 16) unpack8(R.gc, gc);
.LBB0_133:
	s_andn2_saveexec_b64 s[0:1], s[0:1]
	v_lshlrev_b32_e32 v130, 16, v22
	v_and_b32_e32 v114, 0xffff0000, v22
	v_lshlrev_b32_e32 v131, 16, v23
	v_and_b32_e32 v115, 0xffff0000, v23
	v_lshlrev_b32_e32 v128, 16, v24
	v_and_b32_e32 v116, 0xffff0000, v24
	v_lshlrev_b32_e32 v129, 16, v25
	v_and_b32_e32 v117, 0xffff0000, v25
	s_or_b64 exec, exec, s[0:1]
	v_lshlrev_b32_e32 v139, 16, v99
	v_lshlrev_b32_e32 v138, 16, v98
	v_and_b32_e32 v133, 0xffff0000, v99
	v_and_b32_e32 v132, 0xffff0000, v98
	v_lshlrev_b32_e32 v137, 16, v101
	v_lshlrev_b32_e32 v136, 16, v100
	v_and_b32_e32 v135, 0xffff0000, v101
	v_and_b32_e32 v134, 0xffff0000, v100
	v_mul_f32_e32 v98, v138, v138
	v_mul_f32_e32 v99, v139, v139
	v_mul_f32_e32 v100, v132, v132
	v_mul_f32_e32 v101, v133, v133
	v_mul_f32_e32 v144, v114, v114
	v_fmac_f32_e32 v144, v130, v130
	v_add_f32_e32 v98, v98, v100
	v_fmac_f32_e32 v144, v131, v131
	v_add_f32_e32 v98, v99, v98
	v_fmac_f32_e32 v144, v115, v115
	v_mul_f32_e32 v140, v136, v136
	v_mul_f32_e32 v141, v137, v137
	v_add_f32_e32 v98, v101, v98
	v_fmac_f32_e32 v144, v128, v128
	v_mul_f32_e32 v142, v134, v134
	v_mul_f32_e32 v143, v135, v135
	v_add_f32_e32 v98, v140, v98
	v_fmac_f32_e32 v144, v116, v116
	v_add_f32_e32 v98, v142, v98
	v_fmac_f32_e32 v144, v129, v129
	v_add_f32_e32 v98, v141, v98
	v_add_f32_e32 v98, v143, v98
	v_fmac_f32_e32 v144, v117, v117
	v_cndmask_b32_e64 v99, 0, v98, s[40:41]
	v_cndmask_b32_e64 v98, 0, v98, s[36:37]
	v_cndmask_b32_e64 v101, 0, v144, s[34:35]
	v_add_f32_e32 v98, v98, v101
	v_cndmask_b32_e64 v140, 0, v144, s[42:43]
	ds_bpermute_b32 v100, v164, v99
	ds_bpermute_b32 v101, v164, v98
	ds_bpermute_b32 v141, v164, v140
	v_mov_b32_e32 v154, 1.0
	v_mov_b32_e32 v150, 1.0
	s_waitcnt lgkmcnt(0)
	v_add_f32_e32 v99, v99, v100
	v_add_f32_e32 v98, v98, v101
	v_add_f32_e32 v140, v140, v141
	ds_bpermute_b32 v100, v162, v99
	ds_bpermute_b32 v101, v162, v98
	ds_bpermute_b32 v141, v162, v140
	v_mov_b32_e32 v155, 1.0
	v_mov_b32_e32 v151, 1.0
	s_waitcnt lgkmcnt(0)
	v_add_f32_e32 v99, v99, v100
	v_add_f32_e32 v98, v98, v101
	v_add_f32_e32 v140, v140, v141
	ds_bpermute_b32 v100, v161, v99
	ds_bpermute_b32 v101, v161, v98
	ds_bpermute_b32 v141, v161, v140
	v_mov_b32_e32 v152, 1.0
	v_mov_b32_e32 v148, 1.0
	s_waitcnt lgkmcnt(0)
	v_add_f32_e32 v99, v99, v100
	v_add_f32_e32 v98, v98, v101
	v_add_f32_e32 v140, v140, v141
	ds_bpermute_b32 v100, v160, v99
	ds_bpermute_b32 v101, v160, v98
	ds_bpermute_b32 v141, v160, v140
	v_mov_b32_e32 v153, 1.0
	v_mov_b32_e32 v149, 1.0
	s_waitcnt lgkmcnt(0)
	v_add_f32_e32 v99, v99, v100
	v_add_f32_e32 v98, v98, v101
	v_add_f32_e32 v140, v140, v141
	ds_bpermute_b32 v100, v159, v99
	ds_bpermute_b32 v101, v159, v98
	ds_bpermute_b32 v141, v159, v140
	s_waitcnt lgkmcnt(0)
	v_add_f32_e32 v156, v99, v100
	v_add_f32_e32 v176, v98, v101
	v_add_f32_e32 v178, v140, v141
	ds_bpermute_b32 v157, v158, v156
	ds_bpermute_b32 v177, v158, v176
	ds_bpermute_b32 v179, v158, v178
	v_mov_b32_e32 v140, 1.0
	s_and_saveexec_b64 s[0:1], s[36:37]
	v_lshlrev_b32_e32 v154, 16, v6
	v_and_b32_e32 v150, 0xffff0000, v6
	v_lshlrev_b32_e32 v155, 16, v7
	v_and_b32_e32 v151, 0xffff0000, v7
	v_lshlrev_b32_e32 v152, 16, v8
	v_and_b32_e32 v148, 0xffff0000, v8
	v_lshlrev_b32_e32 v153, 16, v9
	v_and_b32_e32 v149, 0xffff0000, v9
	s_or_b64 exec, exec, s[0:1]
	v_mov_b32_e32 v146, 1.0
	v_mov_b32_e32 v141, 1.0
	v_mov_b32_e32 v147, 1.0
	v_mov_b32_e32 v144, 1.0
	v_mov_b32_e32 v142, 1.0
	v_mov_b32_e32 v145, 1.0
	v_mov_b32_e32 v143, 1.0
	s_and_saveexec_b64 s[0:1], s[34:35]
	v_lshlrev_b32_e32 v140, 16, v2
	v_and_b32_e32 v146, 0xffff0000, v2
	v_lshlrev_b32_e32 v141, 16, v3
	v_and_b32_e32 v147, 0xffff0000, v3
	v_lshlrev_b32_e32 v144, 16, v4
	v_and_b32_e32 v142, 0xffff0000, v4
	v_lshlrev_b32_e32 v145, 16, v5
	v_and_b32_e32 v143, 0xffff0000, v5
	s_or_b64 exec, exec, s[0:1]
	s_or_b32 s0, s8, 7
	s_ashr_i32 s1, s0, 31
	s_lshl_b64 s[18:19], s[0:1], 11
	s_add_u32 s20, s29, s18
	s_addc_u32 s21, s30, s19
	global_load_dwordx4 v[98:101], v0, s[20:21] nt
	s_and_saveexec_b64 s[22:23], s[38:39]
	s_xor_b64 s[22:23], exec, s[22:23]
	s_cbranch_execz .LBB0_765
	v_mad_i64_i32 v[10:11], s[44:45], s0, v252, v[124:125]
	v_mad_i64_i32 v[14:15], s[44:45], s0, v252, v[122:123]
	v_mad_i64_i32 v[18:19], s[44:45], s0, v252, v[120:121]
	s_lshl_b64 s[44:45], s[0:1], 5
	s_add_u32 s44, s26, s44
	s_addc_u32 s45, s27, s45
	v_lshl_add_u64 v[180:181], v[118:119], 2, s[44:45]
	v_add_co_u32_e32 v182, vcc, 0x100000, v180
	flat_load_dword v163, v[180:181]
	s_nop 0
	v_addc_co_u32_e32 v183, vcc, 0, v181, vcc
	flat_load_dword v165, v[182:183]
	v_add_co_u32_e32 v180, vcc, 0x200000, v180
	global_load_dwordx4 v[10:13], v[10:11], off nt
	s_nop 0
	v_addc_co_u32_e32 v181, vcc, 0, v181, vcc
	global_load_dwordx4 v[14:17], v[14:15], off nt
	s_nop 0
	global_load_dwordx4 v[18:21], v[18:19], off nt
	s_nop 0
	flat_load_dword v166, v[180:181]
	s_andn2_saveexec_b64 s[22:23], s[22:23]
	s_cbranch_execnz .LBB0_766

; __device__ __forceinline__ unsigned pk2(float lo, float hi) { return f2bf(lo) | (f2bf(hi) << 16); }
; __device__ __forceinline__ void unpack8(const v4u w, float* f) { f[0] = bflo(w.x); f[1] = bfhi(w.x); f[2] = bflo(w.y); f[3] = bfhi(w.y); f[4] = bflo(w.z); f[5] = bfhi(w.z); f[6] = bflo(w.w); f[7] = bfhi(w.w); }
; __device__ __forceinline__ void norm_compute(const NormRow& R, int lane, v4u& ya, v4u& yc) {
;     ...
;     const float s_moba = wave_sum(lane < 32 ? sa : 0.f), s_fox = wave_sum((lane >= 32 ? sa : 0.f) + (lane < 16 ? sc : 0.f)), s_dil = wave_sum(lane >= 16 ? sc : 0.f);
;     const float r_moba = 1.0f / sqrtf(s_moba * (1.0f / 256.0f) + EPS), r_fox = 1.0f / sqrtf(s_fox * (1.0f / 384.0f) + EPS), r_dil = 1.0f / sqrtf(s_dil * (1.0f / 384.0f) + EPS);
;     float ga[8], gc[8];
; #pragma unroll
;     for (int e = 0; e < 8; ++e) { ga[e] = 1.f; gc[e] = 1.f; }
;     if (lane >= 32) unpack8(R.ga, ga);
;     if (lane < 16) unpack8(R.gc, gc);
;     const float ra = lane < 32 ? r_moba : r_fox, rc = lane < 16 ? r_fox : r_dil;
;     ya.x = pk2(fa[0] * ra * ga[0], fa[1] * ra * ga[1]); ya.y = pk2(fa[2] * ra * ga[2], fa[3] * ra * ga[3]); ya.z = pk2(fa[4] * ra * ga[4], fa[5] * ra * ga[5]); ya.w = pk2(fa[6] * ra * ga[6], fa[7] * ra * ga[7]);
;     yc.x = pk2(fc[0] * rc * gc[0], fc[1] * rc * gc[1]); yc.y = pk2(fc[2] * rc * gc[2], fc[3] * rc * gc[3]); yc.z = pk2(fc[4] * rc * gc[4], fc[5] * rc * gc[5]); yc.w = pk2(fc[6] * rc * gc[6], fc[7] * rc * gc[7]);
; }
.LBB0_143:
	s_or_b64 exec, exec, s[20:21]
	s_waitcnt lgkmcnt(0)
	v_add_f32_e32 v178, v178, v179
	v_fmamk_f32 v178, v178, 0x3b2aaaab, v215
	v_mul_f32_e32 v179, 0x4f800000, v178
	v_cmp_gt_f32_e32 vcc, s3, v178
	v_add_f32_e32 v176, v176, v177
	v_fmamk_f32 v176, v176, 0x3b2aaaab, v215
	v_cndmask_b32_e32 v178, v178, v179, vcc
	v_sqrt_f32_e32 v179, v178
	v_mul_f32_e32 v177, 0x4f800000, v176
	v_add_f32_e32 v156, v156, v157
	v_fmamk_f32 v156, v156, 0x3b800000, v215
	v_add_u32_e32 v180, -1, v179
	v_fma_f32 v182, -v180, v179, v178
	v_add_u32_e32 v181, 1, v179
	v_cmp_ge_f32_e64 s[0:1], 0, v182
	v_mul_f32_e32 v157, 0x4f800000, v156
	s_nop 0
	v_cndmask_b32_e64 v180, v179, v180, s[0:1]
	v_fma_f32 v179, -v181, v179, v178
	v_cmp_lt_f32_e64 s[0:1], 0, v179
	s_nop 1
	v_cndmask_b32_e64 v179, v180, v181, s[0:1]
	v_cmp_gt_f32_e64 s[0:1], s3, v176
	v_mul_f32_e32 v180, 0x37800000, v179
	v_cndmask_b32_e32 v179, v179, v180, vcc
	v_cndmask_b32_e64 v176, v176, v177, s[0:1]
	v_sqrt_f32_e32 v177, v176
	v_cmp_class_f32_e32 vcc, v178, v216
	s_nop 1
	v_cndmask_b32_e32 v178, v179, v178, vcc
	v_add_u32_e32 v179, -1, v177
	v_fma_f32 v180, -v179, v177, v176
	v_cmp_ge_f32_e32 vcc, 0, v180
	v_add_u32_e32 v180, 1, v177
	s_nop 0
	v_cndmask_b32_e32 v179, v177, v179, vcc
	v_fma_f32 v177, -v180, v177, v176
	v_cmp_lt_f32_e32 vcc, 0, v177
	s_nop 1
	v_cndmask_b32_e32 v177, v179, v180, vcc
	v_cmp_gt_f32_e32 vcc, s3, v156
	v_mul_f32_e32 v179, 0x37800000, v177
	v_cndmask_b32_e64 v177, v177, v179, s[0:1]
	v_cndmask_b32_e32 v156, v156, v157, vcc
	v_sqrt_f32_e32 v157, v156
	v_cmp_class_f32_e64 s[0:1], v176, v216
	s_nop 1
	v_cndmask_b32_e64 v176, v177, v176, s[0:1]
	v_add_u32_e32 v177, -1, v157
	v_fma_f32 v179, -v177, v157, v156
	v_cmp_ge_f32_e64 s[0:1], 0, v179
	v_add_u32_e32 v179, 1, v157
	s_nop 0
	v_cndmask_b32_e64 v177, v157, v177, s[0:1]
	v_fma_f32 v157, -v179, v157, v156
	v_cmp_lt_f32_e64 s[0:1], 0, v157
	s_nop 1
	v_cndmask_b32_e64 v157, v177, v179, s[0:1]
	v_div_scale_f32 v179, s[0:1], v178, v178, 1.0
	v_rcp_f32_e32 v180, v179
	v_mul_f32_e32 v177, 0x37800000, v157
	v_cndmask_b32_e32 v157, v157, v177, vcc
	v_cmp_class_f32_e32 vcc, v156, v216
	s_nop 1
	v_cndmask_b32_e32 v156, v157, v156, vcc
	v_fma_f32 v157, -v179, v180, 1.0
	v_fmac_f32_e32 v180, v157, v180
	v_div_scale_f32 v157, vcc, 1.0, v178, 1.0
	v_mul_f32_e32 v177, v157, v180
	v_fma_f32 v181, -v179, v177, v157
	v_fmac_f32_e32 v177, v181, v180
	v_fma_f32 v157, -v179, v177, v157
	v_div_scale_f32 v179, s[0:1], v176, v176, 1.0
	v_rcp_f32_e32 v181, v179
	v_div_fmas_f32 v157, v157, v180, v177
	v_div_fixup_f32 v157, v157, v178, 1.0
	v_fma_f32 v177, -v179, v181, 1.0
	v_fmac_f32_e32 v181, v177, v181
	v_div_scale_f32 v177, vcc, 1.0, v176, 1.0
	v_mul_f32_e32 v178, v177, v181
	v_fma_f32 v180, -v179, v178, v177
	v_fmac_f32_e32 v178, v180, v181
	v_fma_f32 v177, -v179, v178, v177
	v_div_scale_f32 v179, s[0:1], v156, v156, 1.0
	v_rcp_f32_e32 v180, v179
	v_div_fmas_f32 v177, v177, v181, v178
	v_div_fixup_f32 v176, v177, v176, 1.0
	s_movk_i32 s1, 0x7fff
	v_fma_f32 v177, -v179, v180, 1.0
	v_fmac_f32_e32 v180, v177, v180
	v_div_scale_f32 v177, vcc, 1.0, v156, 1.0
	v_mul_f32_e32 v178, v177, v180
	v_fma_f32 v181, -v179, v178, v177
	v_fmac_f32_e32 v178, v181, v180
	v_fma_f32 v177, -v179, v178, v177
	v_div_fmas_f32 v177, v177, v180, v178
	v_div_fixup_f32 v156, v177, v156, 1.0
	v_cndmask_b32_e64 v156, v176, v156, s[40:41]
	v_mul_f32_e32 v132, v156, v132
	v_mul_f32_e32 v133, v156, v133
	v_mul_f32_e32 v134, v156, v134
	v_mul_f32_e32 v135, v156, v135
	v_mul_f32_e32 v138, v156, v138
	v_mul_f32_e32 v139, v156, v139
	v_mul_f32_e32 v132, v132, v150
	v_mul_f32_e32 v133, v133, v151
	v_mul_f32_e32 v136, v156, v136
	v_mul_f32_e32 v137, v156, v137
	v_mul_f32_e32 v134, v134, v148
	v_mul_f32_e32 v135, v135, v149
	v_mul_f32_e32 v138, v138, v154
	v_mul_f32_e32 v139, v139, v155
	v_mul_f32_e32 v136, v136, v152
	v_mul_f32_e32 v137, v137, v153
	v_bfe_u32 v148, v135, 16, 1
	v_bfe_u32 v149, v134, 16, 1
	v_bfe_u32 v150, v133, 16, 1
	v_bfe_u32 v151, v132, 16, 1
	v_cndmask_b32_e64 v176, v157, v176, s[34:35]
	v_add3_u32 v132, v132, v151, s1
	v_add3_u32 v133, v133, v150, s1
	v_add3_u32 v134, v134, v149, s1
	v_add3_u32 v135, v135, v148, s1
	v_bfe_u32 v148, v138, 16, 1
	v_bfe_u32 v149, v139, 16, 1
	v_bfe_u32 v150, v136, 16, 1
	v_bfe_u32 v151, v137, 16, 1
	v_add3_u32 v137, v137, v151, s1
	v_add3_u32 v136, v136, v150, s1
	v_add3_u32 v139, v139, v149, s1
	v_add3_u32 v138, v138, v148, s1
	v_mul_f32_e32 v114, v114, v176
	v_mul_f32_e32 v115, v115, v176
	v_mul_f32_e32 v116, v116, v176
	v_mul_f32_e32 v117, v117, v176
	v_lshrrev_b32_e32 v138, 16, v138
	v_lshrrev_b32_e32 v139, 16, v139
	v_lshrrev_b32_e32 v136, 16, v136
	v_lshrrev_b32_e32 v137, 16, v137
	s_mov_b32 s0, 0xffff0000
	v_mul_f32_e32 v130, v130, v176
	v_mul_f32_e32 v131, v131, v176
	v_mul_f32_e32 v114, v114, v146
	v_mul_f32_e32 v115, v115, v147
	v_mul_f32_e32 v128, v128, v176
	v_mul_f32_e32 v129, v129, v176
	v_mul_f32_e32 v116, v116, v142
	v_mul_f32_e32 v117, v117, v143
	v_and_or_b32 v135, v135, s0, v137
	v_and_or_b32 v134, v134, s0, v136
	v_and_or_b32 v133, v133, s0, v139
	v_and_or_b32 v132, v132, s0, v138
	v_mul_f32_e32 v130, v130, v140
	v_mul_f32_e32 v131, v131, v141
	v_mul_f32_e32 v128, v128, v144
	v_mul_f32_e32 v129, v129, v145
	v_bfe_u32 v136, v117, 16, 1
	v_bfe_u32 v137, v116, 16, 1
	v_bfe_u32 v138, v115, 16, 1
	v_bfe_u32 v139, v114, 16, 1
	v_add3_u32 v114, v114, v139, s1
	v_add3_u32 v115, v115, v138, s1
	v_add3_u32 v116, v116, v137, s1
	v_add3_u32 v117, v117, v136, s1
	v_bfe_u32 v136, v130, 16, 1
	v_bfe_u32 v137, v131, 16, 1
	v_bfe_u32 v138, v128, 16, 1
	v_bfe_u32 v139, v129, 16, 1
	v_add3_u32 v129, v129, v139, s1
	v_add3_u32 v128, v128, v138, s1
	v_add3_u32 v131, v131, v137, s1
	v_add3_u32 v130, v130, v136, s1
	v_lshrrev_b32_e32 v130, 16, v130
	v_lshrrev_b32_e32 v131, 16, v131
	v_lshrrev_b32_e32 v128, 16, v128
	v_lshrrev_b32_e32 v129, 16, v129
	v_and_or_b32 v117, v117, s0, v129
	v_and_or_b32 v116, v116, s0, v128
	v_and_or_b32 v115, v115, s0, v131
	v_and_or_b32 v114, v114, s0, v130
	s_add_u32 s0, s24, s10
	s_addc_u32 s1, s25, s11
	global_store_dwordx4 v0, v[132:135], s[0:1]
	global_store_dwordx4 v0, v[114:117], s[0:1] offset:1024
	s_and_saveexec_b64 s[0:1], s[38:39]
	s_xor_b64 s[0:1], exec, s[0:1]
	s_cbranch_execz .LBB0_145
; __device__ __forceinline__ void unpack8(const v4u w, float* f) { f[0] = bflo(w.x); f[1] = bfhi(w.x); f[2] = bflo(w.y); f[3] = bfhi(w.y); f[4] = bflo(w.z); f[5] = bfhi(w.z); f[6] = bflo(w.w); f[7] = bfhi(w.w); }
; __device__ __forceinline__ void norm_compute(const NormRow& R, int lane, v4u& ya, v4u& yc) {
;     ...
;     else { float f0[8], f1[8], f2[8]; unpack8(R.d0, f0); unpack8(R.d1, f1); unpack8(R.d2, f2);
;         const float inv = 1.0f / (R.l0 + R.l1 + R.l2);
; #pragma unroll
;         for (int e = 0; e < 8; ++e) fc[e] = (f0[e] + f1[e] + f2[e]) * inv; }
	s_waitcnt vmcnt(0)
	v_add_f32_e32 v114, v173, v174
	v_add_f32_e32 v114, v114, v175
	v_div_scale_f32 v115, s[10:11], v114, v114, 1.0
	v_rcp_f32_e32 v130, v115
	v_lshlrev_b32_e32 v134, 16, v90
	v_and_b32_e32 v135, 0xffff0000, v90
	v_lshlrev_b32_e32 v136, 16, v91
	v_fma_f32 v131, -v115, v130, 1.0
	v_fmac_f32_e32 v130, v131, v130
	v_div_scale_f32 v131, vcc, 1.0, v114, 1.0
	v_mul_f32_e32 v132, v131, v130
	v_fma_f32 v133, -v115, v132, v131
	v_fmac_f32_e32 v132, v133, v130
	v_fma_f32 v115, -v115, v132, v131
	v_div_fmas_f32 v115, v115, v130, v132
	v_div_fixup_f32 v130, v115, v114, 1.0
	v_lshlrev_b32_e32 v114, 16, v82
	v_and_b32_e32 v115, 0xffff0000, v82
	v_lshlrev_b32_e32 v132, 16, v86
	v_and_b32_e32 v133, 0xffff0000, v86
	v_add_f32_e32 v114, v132, v114
	v_add_f32_e32 v115, v133, v115
	v_and_b32_e32 v137, 0xffff0000, v91
	v_add_f32_e32 v114, v114, v134
	v_add_f32_e32 v115, v115, v135
	v_lshlrev_b32_e32 v134, 16, v87
	v_mul_f32_e32 v132, v114, v130
	v_mul_f32_e32 v133, v115, v130
	v_lshlrev_b32_e32 v114, 16, v83
	v_and_b32_e32 v115, 0xffff0000, v83
	v_and_b32_e32 v135, 0xffff0000, v87
	v_add_f32_e32 v114, v134, v114
	v_add_f32_e32 v115, v135, v115
	v_lshlrev_b32_e32 v116, 16, v85
	v_lshlrev_b32_e32 v128, 16, v89
	v_and_b32_e32 v117, 0xffff0000, v85
	v_and_b32_e32 v129, 0xffff0000, v89
	v_add_f32_e32 v114, v114, v136
	v_add_f32_e32 v115, v115, v137
	v_lshlrev_b32_e32 v134, 16, v84
	v_and_b32_e32 v135, 0xffff0000, v84
	v_lshlrev_b32_e32 v136, 16, v88
	v_and_b32_e32 v137, 0xffff0000, v88
	v_lshlrev_b32_e32 v138, 16, v92
	v_and_b32_e32 v139, 0xffff0000, v92
	v_add_f32_e32 v134, v136, v134
	v_add_f32_e32 v135, v137, v135
	v_lshlrev_b32_e32 v136, 16, v93
	v_and_b32_e32 v137, 0xffff0000, v93
	v_add_f32_e32 v116, v128, v116
	v_add_f32_e32 v117, v129, v117
	v_add_f32_e32 v134, v134, v138
	v_add_f32_e32 v135, v135, v139
	v_add_f32_e32 v116, v116, v136
	v_add_f32_e32 v117, v117, v137
	v_mul_f32_e32 v114, v114, v130
	v_mul_f32_e32 v115, v115, v130
	v_mul_f32_e32 v134, v134, v130
	v_mul_f32_e32 v135, v135, v130
	v_mul_f32_e32 v116, v116, v130
	v_mul_f32_e32 v117, v117, v130
	v_mov_b32_e32 v128, v134
	v_mov_b32_e32 v129, v116
	v_mov_b32_e32 v116, v135
	v_mov_b32_e32 v131, v114
	v_mov_b32_e32 v114, v133
	v_mov_b32_e32 v130, v132

; #define GAS __attribute__((address_space(1)))
; __device__ __forceinline__ void unpack8(const v4u w, float* f) { f[0] = bflo(w.x); f[1] = bfhi(w.x); f[2] = bflo(w.y); f[3] = bfhi(w.y); f[4] = bflo(w.z); f[5] = bfhi(w.z); f[6] = bflo(w.w); f[7] = bfhi(w.w); }
; __device__ __forceinline__ void norm_load(NormRow& R, int m, int lane, const bf16* O, const bf16* GF, const bf16* OD, const float* LD) {
;     R.oa = __builtin_nontemporal_load((const GAS v4u*)(O + (size_t)m * DM + 8 * lane));
;     if (lane < 16) { R.oc = __builtin_nontemporal_load((const GAS v4u*)(O + (size_t)m * DM + 512 + 8 * lane)); R.gc = __builtin_nontemporal_load((const GAS v4u*)(GF + (size_t)m * 384 + 256 + 8 * lane)); }
;     else { const int dc = 8 * lane - 128, hd = dc >> 6;
;         R.d0 = __builtin_nontemporal_load((const GAS v4u*)(OD + (size_t)m * 384 + dc)); R.d1 = __builtin_nontemporal_load((const GAS v4u*)(OD + OD_BRANCH + (size_t)m * 384 + dc)); R.d2 = __builtin_nontemporal_load((const GAS v4u*)(OD + 2 * OD_BRANCH + (size_t)m * 384 + dc));
;         R.l0 = LD[(size_t)m * 8 + hd]; R.l1 = LD[LD_BRANCH + (size_t)m * 8 + hd]; R.l2 = LD[2 * LD_BRANCH + (size_t)m * 8 + hd]; }
;     if (lane >= 32) R.ga = __builtin_nontemporal_load((const GAS v4u*)(GF + (size_t)m * 384 + 8 * lane - 256));
; __device__ __forceinline__ void norm_compute(const NormRow& R, int lane, v4u& ya, v4u& yc) {
;     float fa[8], fc[8];
;     unpack8(R.oa, fa);
;     if (lane < 16) unpack8(R.oc, fc);
;     else { float f0[8], f1[8], f2[8]; unpack8(R.d0, f0); unpack8(R.d1, f1); unpack8(R.d2, f2);
;         const float inv = 1.0f / (R.l0 + R.l1 + R.l2);
; #pragma unroll
;         for (int e = 0; e < 8; ++e) fc[e] = (f0[e] + f1[e] + f2[e]) * inv; }
;     float sa = 0.f, sc = 0.f;
; #pragma unroll
;     for (int e = 0; e < 8; ++e) { sa += fa[e] * fa[e]; sc += fc[e] * fc[e]; }
;     const float s_moba = wave_sum(lane < 32 ? sa : 0.f), s_fox = wave_sum((lane >= 32 ? sa : 0.f) + (lane < 16 ? sc : 0.f)), s_dil = wave_sum(lane >= 16 ? sc : 0.f);
;     const float r_moba = 1.0f / sqrtf(s_moba * (1.0f / 256.0f) + EPS), r_fox = 1.0f / sqrtf(s_fox * (1.0f / 384.0f) + EPS), r_dil = 1.0f / sqrtf(s_dil * (1.0f / 384.0f) + EPS);
;     float ga[8], gc[8];
; #pragma unroll
;     for (int e = 0; e < 8; ++e) { ga[e] = 1.f; gc[e] = 1.f; }
;     if (lane >= 32) unpack8(R.ga, ga);
;     if (lane < 16) unpack8(R.gc, gc);
.LBB0_147:
	s_or_b64 exec, exec, s[0:1]
	s_waitcnt vmcnt(0)
	v_lshlrev_b32_e32 v139, 16, v103
	v_lshlrev_b32_e32 v138, 16, v102
	v_and_b32_e32 v133, 0xffff0000, v103
	v_and_b32_e32 v132, 0xffff0000, v102
	v_lshlrev_b32_e32 v137, 16, v105
	v_lshlrev_b32_e32 v136, 16, v104
	v_and_b32_e32 v135, 0xffff0000, v105
	v_and_b32_e32 v134, 0xffff0000, v104
	v_mul_f32_e32 v102, v138, v138
	v_mul_f32_e32 v103, v139, v139
	v_mul_f32_e32 v104, v132, v132
	v_mul_f32_e32 v105, v133, v133
	v_mul_f32_e32 v144, v114, v114
	v_fmac_f32_e32 v144, v130, v130
	v_add_f32_e32 v102, v102, v104
	v_fmac_f32_e32 v144, v131, v131
	v_add_f32_e32 v102, v103, v102
	v_fmac_f32_e32 v144, v115, v115
	v_mul_f32_e32 v140, v136, v136
	v_mul_f32_e32 v141, v137, v137
	v_add_f32_e32 v102, v105, v102
	v_fmac_f32_e32 v144, v128, v128
	v_mul_f32_e32 v142, v134, v134
	v_mul_f32_e32 v143, v135, v135
	v_add_f32_e32 v102, v140, v102
	v_fmac_f32_e32 v144, v116, v116
	v_add_f32_e32 v102, v142, v102
	v_fmac_f32_e32 v144, v129, v129
	v_add_f32_e32 v102, v141, v102
	v_add_f32_e32 v102, v143, v102
	v_fmac_f32_e32 v144, v117, v117
	v_cndmask_b32_e64 v103, 0, v102, s[40:41]
	v_cndmask_b32_e64 v102, 0, v102, s[36:37]
	v_cndmask_b32_e64 v105, 0, v144, s[34:35]
	v_add_f32_e32 v102, v102, v105
	v_cndmask_b32_e64 v140, 0, v144, s[42:43]
	ds_bpermute_b32 v104, v164, v103
	ds_bpermute_b32 v105, v164, v102
	ds_bpermute_b32 v141, v164, v140
	v_mov_b32_e32 v154, 1.0
	v_mov_b32_e32 v150, 1.0
	s_waitcnt lgkmcnt(2)
	v_add_f32_e32 v103, v103, v104
	s_waitcnt lgkmcnt(1)
	v_add_f32_e32 v102, v102, v105
	s_waitcnt lgkmcnt(0)
	v_add_f32_e32 v140, v140, v141
	ds_bpermute_b32 v104, v162, v103
	ds_bpermute_b32 v105, v162, v102
	ds_bpermute_b32 v141, v162, v140
	v_mov_b32_e32 v155, 1.0
	v_mov_b32_e32 v151, 1.0
	s_waitcnt lgkmcnt(2)
	v_add_f32_e32 v103, v103, v104
	s_waitcnt lgkmcnt(1)
	v_add_f32_e32 v102, v102, v105
	s_waitcnt lgkmcnt(0)
	v_add_f32_e32 v140, v140, v141
	ds_bpermute_b32 v104, v161, v103
	ds_bpermute_b32 v105, v161, v102
	ds_bpermute_b32 v141, v161, v140
	v_mov_b32_e32 v152, 1.0
	v_mov_b32_e32 v148, 1.0
	s_waitcnt lgkmcnt(2)
	v_add_f32_e32 v103, v103, v104
	s_waitcnt lgkmcnt(1)
	v_add_f32_e32 v102, v102, v105
	s_waitcnt lgkmcnt(0)
	v_add_f32_e32 v140, v140, v141
	ds_bpermute_b32 v104, v160, v103
	ds_bpermute_b32 v105, v160, v102
	ds_bpermute_b32 v141, v160, v140
	v_mov_b32_e32 v153, 1.0
	v_mov_b32_e32 v149, 1.0
	s_waitcnt lgkmcnt(2)
	v_add_f32_e32 v103, v103, v104
	s_waitcnt lgkmcnt(1)
	v_add_f32_e32 v102, v102, v105
	s_waitcnt lgkmcnt(0)
	v_add_f32_e32 v140, v140, v141
	ds_bpermute_b32 v104, v159, v103
	ds_bpermute_b32 v105, v159, v102
	ds_bpermute_b32 v141, v159, v140
	s_waitcnt lgkmcnt(2)
	v_add_f32_e32 v156, v103, v104
	s_waitcnt lgkmcnt(1)
	v_add_f32_e32 v176, v102, v105
	s_waitcnt lgkmcnt(0)
	v_add_f32_e32 v178, v140, v141
	ds_bpermute_b32 v157, v158, v156
	ds_bpermute_b32 v177, v158, v176
	ds_bpermute_b32 v179, v158, v178
	v_mov_b32_e32 v140, 1.0
	s_and_saveexec_b64 s[0:1], s[36:37]
	v_lshlrev_b32_e32 v154, 16, v78
	v_and_b32_e32 v150, 0xffff0000, v78
	v_lshlrev_b32_e32 v155, 16, v79
	v_and_b32_e32 v151, 0xffff0000, v79
	v_lshlrev_b32_e32 v152, 16, v80
	v_and_b32_e32 v148, 0xffff0000, v80
	v_lshlrev_b32_e32 v153, 16, v81
	v_and_b32_e32 v149, 0xffff0000, v81
	s_or_b64 exec, exec, s[0:1]
	v_mov_b32_e32 v146, 1.0
	v_mov_b32_e32 v141, 1.0
	v_mov_b32_e32 v147, 1.0
	v_mov_b32_e32 v144, 1.0
	v_mov_b32_e32 v142, 1.0
	v_mov_b32_e32 v145, 1.0
	v_mov_b32_e32 v143, 1.0
	s_and_saveexec_b64 s[0:1], s[34:35]
	v_lshlrev_b32_e32 v140, 16, v74
	v_and_b32_e32 v146, 0xffff0000, v74
	v_lshlrev_b32_e32 v141, 16, v75
	v_and_b32_e32 v147, 0xffff0000, v75
	v_lshlrev_b32_e32 v144, 16, v76
	v_and_b32_e32 v142, 0xffff0000, v76
	v_lshlrev_b32_e32 v145, 16, v77
	v_and_b32_e32 v143, 0xffff0000, v77
	s_or_b64 exec, exec, s[0:1]
	s_or_b32 s0, s8, 8
	s_ashr_i32 s1, s0, 31
	s_lshl_b64 s[10:11], s[0:1], 11
	s_add_u32 s20, s29, s10
	s_addc_u32 s21, s30, s11
	global_load_dwordx4 v[102:105], v0, s[20:21] nt
	s_and_saveexec_b64 s[22:23], s[38:39]
	s_xor_b64 s[22:23], exec, s[22:23]
	s_cbranch_execz .LBB0_767
	v_mad_i64_i32 v[82:83], s[44:45], s0, v252, v[124:125]
	v_mad_i64_i32 v[86:87], s[44:45], s0, v252, v[122:123]
	v_mad_i64_i32 v[90:91], s[44:45], s0, v252, v[120:121]
	s_lshl_b64 s[44:45], s[0:1], 5
	s_add_u32 s44, s26, s44
	s_addc_u32 s45, s27, s45
	v_lshl_add_u64 v[180:181], v[118:119], 2, s[44:45]
	v_add_co_u32_e32 v174, vcc, 0x100000, v180
	flat_load_dword v173, v[180:181]
	s_nop 0
	v_addc_co_u32_e32 v175, vcc, 0, v181, vcc
	flat_load_dword v174, v[174:175]
	v_add_co_u32_e32 v180, vcc, 0x200000, v180
	global_load_dwordx4 v[82:85], v[82:83], off nt
	s_nop 0
	v_addc_co_u32_e32 v181, vcc, 0, v181, vcc
	global_load_dwordx4 v[86:89], v[86:87], off nt
	s_nop 0
	global_load_dwordx4 v[90:93], v[90:91], off nt
	s_nop 0
	flat_load_dword v175, v[180:181]
	s_andn2_saveexec_b64 s[22:23], s[22:23]
	s_cbranch_execnz .LBB0_768

; __device__ __forceinline__ unsigned pk2(float lo, float hi) { return f2bf(lo) | (f2bf(hi) << 16); }
; __device__ __forceinline__ void unpack8(const v4u w, float* f) { f[0] = bflo(w.x); f[1] = bfhi(w.x); f[2] = bflo(w.y); f[3] = bfhi(w.y); f[4] = bflo(w.z); f[5] = bfhi(w.z); f[6] = bflo(w.w); f[7] = bfhi(w.w); }
; __device__ __forceinline__ void norm_compute(const NormRow& R, int lane, v4u& ya, v4u& yc) {
;     ...
;     const float s_moba = wave_sum(lane < 32 ? sa : 0.f), s_fox = wave_sum((lane >= 32 ? sa : 0.f) + (lane < 16 ? sc : 0.f)), s_dil = wave_sum(lane >= 16 ? sc : 0.f);
;     const float r_moba = 1.0f / sqrtf(s_moba * (1.0f / 256.0f) + EPS), r_fox = 1.0f / sqrtf(s_fox * (1.0f / 384.0f) + EPS), r_dil = 1.0f / sqrtf(s_dil * (1.0f / 384.0f) + EPS);
;     float ga[8], gc[8];
; #pragma unroll
;     for (int e = 0; e < 8; ++e) { ga[e] = 1.f; gc[e] = 1.f; }
;     if (lane >= 32) unpack8(R.ga, ga);
;     if (lane < 16) unpack8(R.gc, gc);
;     const float ra = lane < 32 ? r_moba : r_fox, rc = lane < 16 ? r_fox : r_dil;
;     ya.x = pk2(fa[0] * ra * ga[0], fa[1] * ra * ga[1]); ya.y = pk2(fa[2] * ra * ga[2], fa[3] * ra * ga[3]); ya.z = pk2(fa[4] * ra * ga[4], fa[5] * ra * ga[5]); ya.w = pk2(fa[6] * ra * ga[6], fa[7] * ra * ga[7]);
;     yc.x = pk2(fc[0] * rc * gc[0], fc[1] * rc * gc[1]); yc.y = pk2(fc[2] * rc * gc[2], fc[3] * rc * gc[3]); yc.z = pk2(fc[4] * rc * gc[4], fc[5] * rc * gc[5]); yc.w = pk2(fc[6] * rc * gc[6], fc[7] * rc * gc[7]);
; }
.LBB0_155:
	s_or_b64 exec, exec, s[20:21]
	s_waitcnt lgkmcnt(0)
	v_add_f32_e32 v178, v178, v179
	v_fmamk_f32 v178, v178, 0x3b2aaaab, v215
	v_mul_f32_e32 v179, 0x4f800000, v178
	v_cmp_gt_f32_e32 vcc, s3, v178
	v_add_f32_e32 v176, v176, v177
	v_fmamk_f32 v176, v176, 0x3b2aaaab, v215
	v_cndmask_b32_e32 v178, v178, v179, vcc
	v_sqrt_f32_e32 v179, v178
	v_mul_f32_e32 v177, 0x4f800000, v176
	v_add_f32_e32 v156, v156, v157
	v_fmamk_f32 v156, v156, 0x3b800000, v215
	v_add_u32_e32 v180, -1, v179
	v_fma_f32 v182, -v180, v179, v178
	v_add_u32_e32 v181, 1, v179
	v_cmp_ge_f32_e64 s[0:1], 0, v182
	v_mul_f32_e32 v157, 0x4f800000, v156
	s_nop 0
	v_cndmask_b32_e64 v180, v179, v180, s[0:1]
	v_fma_f32 v179, -v181, v179, v178
	v_cmp_lt_f32_e64 s[0:1], 0, v179
	s_nop 1
	v_cndmask_b32_e64 v179, v180, v181, s[0:1]
	v_cmp_gt_f32_e64 s[0:1], s3, v176
	v_mul_f32_e32 v180, 0x37800000, v179
	v_cndmask_b32_e32 v179, v179, v180, vcc
	v_cndmask_b32_e64 v176, v176, v177, s[0:1]
	v_sqrt_f32_e32 v177, v176
	v_cmp_class_f32_e32 vcc, v178, v216
	s_nop 1
	v_cndmask_b32_e32 v178, v179, v178, vcc
	v_add_u32_e32 v179, -1, v177
	v_fma_f32 v180, -v179, v177, v176
	v_cmp_ge_f32_e32 vcc, 0, v180
	v_add_u32_e32 v180, 1, v177
	s_nop 0
	v_cndmask_b32_e32 v179, v177, v179, vcc
	v_fma_f32 v177, -v180, v177, v176
	v_cmp_lt_f32_e32 vcc, 0, v177
	s_nop 1
	v_cndmask_b32_e32 v177, v179, v180, vcc
	v_cmp_gt_f32_e32 vcc, s3, v156
	v_mul_f32_e32 v179, 0x37800000, v177
	v_cndmask_b32_e64 v177, v177, v179, s[0:1]
	v_cndmask_b32_e32 v156, v156, v157, vcc
	v_sqrt_f32_e32 v157, v156
	v_cmp_class_f32_e64 s[0:1], v176, v216
	s_nop 1
	v_cndmask_b32_e64 v176, v177, v176, s[0:1]
	v_add_u32_e32 v177, -1, v157
	v_fma_f32 v179, -v177, v157, v156
	v_cmp_ge_f32_e64 s[0:1], 0, v179
	v_add_u32_e32 v179, 1, v157
	s_nop 0
	v_cndmask_b32_e64 v177, v157, v177, s[0:1]
	v_fma_f32 v157, -v179, v157, v156
	v_cmp_lt_f32_e64 s[0:1], 0, v157
	s_nop 1
	v_cndmask_b32_e64 v157, v177, v179, s[0:1]
	v_div_scale_f32 v179, s[0:1], v178, v178, 1.0
	v_rcp_f32_e32 v180, v179
	v_mul_f32_e32 v177, 0x37800000, v157
	v_cndmask_b32_e32 v157, v157, v177, vcc
	v_cmp_class_f32_e32 vcc, v156, v216
	s_nop 1
	v_cndmask_b32_e32 v156, v157, v156, vcc
	v_fma_f32 v157, -v179, v180, 1.0
	v_fmac_f32_e32 v180, v157, v180
	v_div_scale_f32 v157, vcc, 1.0, v178, 1.0
	v_mul_f32_e32 v177, v157, v180
	v_fma_f32 v181, -v179, v177, v157
	v_fmac_f32_e32 v177, v181, v180
	v_fma_f32 v157, -v179, v177, v157
	v_div_scale_f32 v179, s[0:1], v176, v176, 1.0
	v_rcp_f32_e32 v181, v179
	v_div_fmas_f32 v157, v157, v180, v177
	v_div_fixup_f32 v157, v157, v178, 1.0
	v_fma_f32 v177, -v179, v181, 1.0
	v_fmac_f32_e32 v181, v177, v181
	v_div_scale_f32 v177, vcc, 1.0, v176, 1.0
	v_mul_f32_e32 v178, v177, v181
	v_fma_f32 v180, -v179, v178, v177
	v_fmac_f32_e32 v178, v180, v181
	v_fma_f32 v177, -v179, v178, v177
	v_div_scale_f32 v179, s[0:1], v156, v156, 1.0
	v_rcp_f32_e32 v180, v179
	v_div_fmas_f32 v177, v177, v181, v178
	v_div_fixup_f32 v176, v177, v176, 1.0
	s_movk_i32 s1, 0x7fff
	v_fma_f32 v177, -v179, v180, 1.0
	v_fmac_f32_e32 v180, v177, v180
	v_div_scale_f32 v177, vcc, 1.0, v156, 1.0
	v_mul_f32_e32 v178, v177, v180
	v_fma_f32 v181, -v179, v178, v177
	v_fmac_f32_e32 v178, v181, v180
	v_fma_f32 v177, -v179, v178, v177
	v_div_fmas_f32 v177, v177, v180, v178
	v_div_fixup_f32 v156, v177, v156, 1.0
	v_cndmask_b32_e64 v156, v176, v156, s[40:41]
	v_mul_f32_e32 v132, v156, v132
	v_mul_f32_e32 v133, v156, v133
	v_mul_f32_e32 v134, v156, v134
	v_mul_f32_e32 v135, v156, v135
	v_mul_f32_e32 v138, v156, v138
	v_mul_f32_e32 v139, v156, v139
	v_mul_f32_e32 v132, v132, v150
	v_mul_f32_e32 v133, v133, v151
	v_mul_f32_e32 v136, v156, v136
	v_mul_f32_e32 v137, v156, v137
	v_mul_f32_e32 v134, v134, v148
	v_mul_f32_e32 v135, v135, v149
	v_mul_f32_e32 v138, v138, v154
	v_mul_f32_e32 v139, v139, v155
	v_mul_f32_e32 v136, v136, v152
	v_mul_f32_e32 v137, v137, v153
	v_bfe_u32 v148, v135, 16, 1
	v_bfe_u32 v149, v134, 16, 1
	v_bfe_u32 v150, v133, 16, 1
	v_bfe_u32 v151, v132, 16, 1
	v_cndmask_b32_e64 v176, v157, v176, s[34:35]
	v_add3_u32 v132, v132, v151, s1
	v_add3_u32 v133, v133, v150, s1
	v_add3_u32 v134, v134, v149, s1
	v_add3_u32 v135, v135, v148, s1
	v_bfe_u32 v148, v138, 16, 1
	v_bfe_u32 v149, v139, 16, 1
	v_bfe_u32 v150, v136, 16, 1
	v_bfe_u32 v151, v137, 16, 1
	v_add3_u32 v137, v137, v151, s1
	v_add3_u32 v136, v136, v150, s1
	v_add3_u32 v139, v139, v149, s1
	v_add3_u32 v138, v138, v148, s1
	v_mul_f32_e32 v114, v114, v176
	v_mul_f32_e32 v115, v115, v176
	v_mul_f32_e32 v116, v116, v176
	v_mul_f32_e32 v117, v117, v176
	v_lshrrev_b32_e32 v138, 16, v138
	v_lshrrev_b32_e32 v139, 16, v139
	v_lshrrev_b32_e32 v136, 16, v136
	v_lshrrev_b32_e32 v137, 16, v137
	s_mov_b32 s0, 0xffff0000
	v_mul_f32_e32 v130, v130, v176
	v_mul_f32_e32 v131, v131, v176
	v_mul_f32_e32 v114, v114, v146
	v_mul_f32_e32 v115, v115, v147
	v_mul_f32_e32 v128, v128, v176
	v_mul_f32_e32 v129, v129, v176
	v_mul_f32_e32 v116, v116, v142
	v_mul_f32_e32 v117, v117, v143
	v_and_or_b32 v135, v135, s0, v137
	v_and_or_b32 v134, v134, s0, v136
	v_and_or_b32 v133, v133, s0, v139
	v_and_or_b32 v132, v132, s0, v138
	v_mul_f32_e32 v130, v130, v140
	v_mul_f32_e32 v131, v131, v141
	v_mul_f32_e32 v128, v128, v144
	v_mul_f32_e32 v129, v129, v145
	v_bfe_u32 v136, v117, 16, 1
	v_bfe_u32 v137, v116, 16, 1
	v_bfe_u32 v138, v115, 16, 1
	v_bfe_u32 v139, v114, 16, 1
	v_add3_u32 v114, v114, v139, s1
	v_add3_u32 v115, v115, v138, s1
	v_add3_u32 v116, v116, v137, s1
	v_add3_u32 v117, v117, v136, s1
	v_bfe_u32 v136, v130, 16, 1
	v_bfe_u32 v137, v131, 16, 1
	v_bfe_u32 v138, v128, 16, 1
	v_bfe_u32 v139, v129, 16, 1
	v_add3_u32 v129, v129, v139, s1
	v_add3_u32 v128, v128, v138, s1
	v_add3_u32 v131, v131, v137, s1
	v_add3_u32 v130, v130, v136, s1
	v_lshrrev_b32_e32 v130, 16, v130
	v_lshrrev_b32_e32 v131, 16, v131
	v_lshrrev_b32_e32 v128, 16, v128
	v_lshrrev_b32_e32 v129, 16, v129
	v_and_or_b32 v117, v117, s0, v129
	v_and_or_b32 v116, v116, s0, v128
	v_and_or_b32 v115, v115, s0, v131
	v_and_or_b32 v114, v114, s0, v130
	s_add_u32 s0, s24, s12
	s_addc_u32 s1, s25, s13
	global_store_dwordx4 v0, v[132:135], s[0:1]
	global_store_dwordx4 v0, v[114:117], s[0:1] offset:1024
	s_and_saveexec_b64 s[0:1], s[38:39]
	s_xor_b64 s[0:1], exec, s[0:1]
	s_cbranch_execz .LBB0_157
; __device__ __forceinline__ void unpack8(const v4u w, float* f) { f[0] = bflo(w.x); f[1] = bfhi(w.x); f[2] = bflo(w.y); f[3] = bfhi(w.y); f[4] = bflo(w.z); f[5] = bfhi(w.z); f[6] = bflo(w.w); f[7] = bfhi(w.w); }
; __device__ __forceinline__ void norm_compute(const NormRow& R, int lane, v4u& ya, v4u& yc) {
;     ...
;     else { float f0[8], f1[8], f2[8]; unpack8(R.d0, f0); unpack8(R.d1, f1); unpack8(R.d2, f2);
;         const float inv = 1.0f / (R.l0 + R.l1 + R.l2);
; #pragma unroll
;         for (int e = 0; e < 8; ++e) fc[e] = (f0[e] + f1[e] + f2[e]) * inv; }
	v_add_f32_e32 v114, v171, v170
	v_add_f32_e32 v114, v172, v114
	v_div_scale_f32 v115, s[12:13], v114, v114, 1.0
	v_rcp_f32_e32 v130, v115
	v_lshlrev_b32_e32 v134, 16, v66
	v_and_b32_e32 v135, 0xffff0000, v66
	v_lshlrev_b32_e32 v136, 16, v67
	v_fma_f32 v131, -v115, v130, 1.0
	v_fmac_f32_e32 v130, v131, v130
	v_div_scale_f32 v131, vcc, 1.0, v114, 1.0
	v_mul_f32_e32 v132, v131, v130
	v_fma_f32 v133, -v115, v132, v131
	v_fmac_f32_e32 v132, v133, v130
	v_fma_f32 v115, -v115, v132, v131
	v_div_fmas_f32 v115, v115, v130, v132
	v_div_fixup_f32 v130, v115, v114, 1.0
	v_lshlrev_b32_e32 v114, 16, v58
	v_and_b32_e32 v115, 0xffff0000, v58
	v_lshlrev_b32_e32 v132, 16, v62
	v_and_b32_e32 v133, 0xffff0000, v62
	v_add_f32_e32 v114, v132, v114
	v_add_f32_e32 v115, v133, v115
	v_and_b32_e32 v137, 0xffff0000, v67
	v_add_f32_e32 v114, v114, v134
	v_add_f32_e32 v115, v115, v135
	v_lshlrev_b32_e32 v134, 16, v63
	v_mul_f32_e32 v132, v130, v114
	v_mul_f32_e32 v133, v130, v115
	v_lshlrev_b32_e32 v114, 16, v59
	v_and_b32_e32 v115, 0xffff0000, v59
	v_and_b32_e32 v135, 0xffff0000, v63
	v_add_f32_e32 v114, v134, v114
	v_add_f32_e32 v115, v135, v115
	v_lshlrev_b32_e32 v116, 16, v61
	v_lshlrev_b32_e32 v128, 16, v65
	v_and_b32_e32 v117, 0xffff0000, v61
	v_and_b32_e32 v129, 0xffff0000, v65
	v_add_f32_e32 v114, v114, v136
	v_add_f32_e32 v115, v115, v137
	v_lshlrev_b32_e32 v134, 16, v60
	v_and_b32_e32 v135, 0xffff0000, v60
	v_lshlrev_b32_e32 v136, 16, v64
	v_and_b32_e32 v137, 0xffff0000, v64
	v_lshlrev_b32_e32 v138, 16, v68
	v_and_b32_e32 v139, 0xffff0000, v68
	v_add_f32_e32 v134, v136, v134
	v_add_f32_e32 v135, v137, v135
	v_lshlrev_b32_e32 v136, 16, v69
	v_and_b32_e32 v137, 0xffff0000, v69
	v_add_f32_e32 v116, v128, v116
	v_add_f32_e32 v117, v129, v117
	v_add_f32_e32 v134, v134, v138
	v_add_f32_e32 v135, v135, v139
	v_add_f32_e32 v116, v116, v136
	v_add_f32_e32 v117, v117, v137
	v_mul_f32_e32 v114, v130, v114
	v_mul_f32_e32 v115, v130, v115
	v_mul_f32_e32 v134, v130, v134
	v_mul_f32_e32 v135, v130, v135
	v_mul_f32_e32 v116, v130, v116
	v_mul_f32_e32 v117, v130, v117
	v_mov_b32_e32 v129, v116
	v_mov_b32_e32 v116, v135
	v_mov_b32_e32 v128, v134
	v_mov_b32_e32 v131, v114
	v_mov_b32_e32 v114, v133
	v_mov_b32_e32 v130, v132
; #define GAS __attribute__((address_space(1)))
; __device__ __forceinline__ void unpack8(const v4u w, float* f) { f[0] = bflo(w.x); f[1] = bfhi(w.x); f[2] = bflo(w.y); f[3] = bfhi(w.y); f[4] = bflo(w.z); f[5] = bfhi(w.z); f[6] = bflo(w.w); f[7] = bfhi(w.w); }
; __device__ __forceinline__ void norm_load(NormRow& R, int m, int lane, const bf16* O, const bf16* GF, const bf16* OD, const float* LD) {
;     R.oa = __builtin_nontemporal_load((const GAS v4u*)(O + (size_t)m * DM + 8 * lane));
;     if (lane < 16) { R.oc = __builtin_nontemporal_load((const GAS v4u*)(O + (size_t)m * DM + 512 + 8 * lane)); R.gc = __builtin_nontemporal_load((const GAS v4u*)(GF + (size_t)m * 384 + 256 + 8 * lane)); }
;     else { const int dc = 8 * lane - 128, hd = dc >> 6;
;         R.d0 = __builtin_nontemporal_load((const GAS v4u*)(OD + (size_t)m * 384 + dc)); R.d1 = __builtin_nontemporal_load((const GAS v4u*)(OD + OD_BRANCH + (size_t)m * 384 + dc)); R.d2 = __builtin_nontemporal_load((const GAS v4u*)(OD + 2 * OD_BRANCH + (size_t)m * 384 + dc));
;         R.l0 = LD[(size_t)m * 8 + hd]; R.l1 = LD[LD_BRANCH + (size_t)m * 8 + hd]; R.l2 = LD[2 * LD_BRANCH + (size_t)m * 8 + hd]; }
;     if (lane >= 32) R.ga = __builtin_nontemporal_load((const GAS v4u*)(GF + (size_t)m * 384 + 8 * lane - 256));
; __device__ __forceinline__ void norm_compute(const NormRow& R, int lane, v4u& ya, v4u& yc) {
;     float fa[8], fc[8];
;     unpack8(R.oa, fa);
;     if (lane < 16) unpack8(R.oc, fc);
;     else { float f0[8], f1[8], f2[8]; unpack8(R.d0, f0); unpack8(R.d1, f1); unpack8(R.d2, f2);
;         const float inv = 1.0f / (R.l0 + R.l1 + R.l2);
; #pragma unroll
;         for (int e = 0; e < 8; ++e) fc[e] = (f0[e] + f1[e] + f2[e]) * inv; }
;     float sa = 0.f, sc = 0.f;
; #pragma unroll
;     for (int e = 0; e < 8; ++e) { sa += fa[e] * fa[e]; sc += fc[e] * fc[e]; }
;     const float s_moba = wave_sum(lane < 32 ? sa : 0.f), s_fox = wave_sum((lane >= 32 ? sa : 0.f) + (lane < 16 ? sc : 0.f)), s_dil = wave_sum(lane >= 16 ? sc : 0.f);
;     const float r_moba = 1.0f / sqrtf(s_moba * (1.0f / 256.0f) + EPS), r_fox = 1.0f / sqrtf(s_fox * (1.0f / 384.0f) + EPS), r_dil = 1.0f / sqrtf(s_dil * (1.0f / 384.0f) + EPS);
;     float ga[8], gc[8];
; #pragma unroll
;     for (int e = 0; e < 8; ++e) { ga[e] = 1.f; gc[e] = 1.f; }
;     if (lane >= 32) unpack8(R.ga, ga);
;     if (lane < 16) unpack8(R.gc, gc);
.LBB0_157:
	s_andn2_saveexec_b64 s[0:1], s[0:1]
	v_lshlrev_b32_e32 v130, 16, v70
	v_and_b32_e32 v114, 0xffff0000, v70
	v_lshlrev_b32_e32 v131, 16, v71
	v_and_b32_e32 v115, 0xffff0000, v71
	v_lshlrev_b32_e32 v128, 16, v72
	v_and_b32_e32 v116, 0xffff0000, v72
	v_lshlrev_b32_e32 v129, 16, v73
	v_and_b32_e32 v117, 0xffff0000, v73
	s_or_b64 exec, exec, s[0:1]
	v_lshlrev_b32_e32 v139, 16, v107
	v_lshlrev_b32_e32 v138, 16, v106
	v_and_b32_e32 v133, 0xffff0000, v107
	v_and_b32_e32 v132, 0xffff0000, v106
	v_lshlrev_b32_e32 v137, 16, v109
	v_lshlrev_b32_e32 v136, 16, v108
	v_and_b32_e32 v135, 0xffff0000, v109
	v_and_b32_e32 v134, 0xffff0000, v108
	v_mul_f32_e32 v106, v138, v138
	v_mul_f32_e32 v107, v139, v139
	v_mul_f32_e32 v108, v132, v132
	v_mul_f32_e32 v109, v133, v133
	v_mul_f32_e32 v144, v114, v114
	v_fmac_f32_e32 v144, v130, v130
	v_add_f32_e32 v106, v106, v108
	v_fmac_f32_e32 v144, v131, v131
	v_add_f32_e32 v106, v107, v106
	v_fmac_f32_e32 v144, v115, v115
	v_mul_f32_e32 v140, v136, v136
	v_mul_f32_e32 v141, v137, v137
	v_add_f32_e32 v106, v109, v106
	v_fmac_f32_e32 v144, v128, v128
	v_mul_f32_e32 v142, v134, v134
	v_mul_f32_e32 v143, v135, v135
	v_add_f32_e32 v106, v140, v106
	v_fmac_f32_e32 v144, v116, v116
	v_add_f32_e32 v106, v142, v106
	v_fmac_f32_e32 v144, v129, v129
	v_add_f32_e32 v106, v141, v106
	v_add_f32_e32 v106, v143, v106
	v_fmac_f32_e32 v144, v117, v117
	v_cndmask_b32_e64 v107, 0, v106, s[40:41]
	v_cndmask_b32_e64 v106, 0, v106, s[36:37]
	v_cndmask_b32_e64 v109, 0, v144, s[34:35]
	v_add_f32_e32 v106, v106, v109
	v_cndmask_b32_e64 v140, 0, v144, s[42:43]
	ds_bpermute_b32 v108, v164, v107
	ds_bpermute_b32 v109, v164, v106
	ds_bpermute_b32 v141, v164, v140
	v_mov_b32_e32 v154, 1.0
	v_mov_b32_e32 v150, 1.0
	s_waitcnt lgkmcnt(0)
	v_add_f32_e32 v107, v107, v108
	v_add_f32_e32 v106, v106, v109
	v_add_f32_e32 v140, v140, v141
	ds_bpermute_b32 v108, v162, v107
	ds_bpermute_b32 v109, v162, v106
	ds_bpermute_b32 v141, v162, v140
	v_mov_b32_e32 v155, 1.0
	v_mov_b32_e32 v151, 1.0
	s_waitcnt lgkmcnt(0)
	v_add_f32_e32 v107, v107, v108
	v_add_f32_e32 v106, v106, v109
	v_add_f32_e32 v140, v140, v141
	ds_bpermute_b32 v108, v161, v107
	ds_bpermute_b32 v109, v161, v106
	ds_bpermute_b32 v141, v161, v140
	v_mov_b32_e32 v152, 1.0
	v_mov_b32_e32 v148, 1.0
	s_waitcnt lgkmcnt(0)
	v_add_f32_e32 v107, v107, v108
	v_add_f32_e32 v106, v106, v109
	v_add_f32_e32 v140, v140, v141
	ds_bpermute_b32 v108, v160, v107
	ds_bpermute_b32 v109, v160, v106
	ds_bpermute_b32 v141, v160, v140
	v_mov_b32_e32 v153, 1.0
	v_mov_b32_e32 v149, 1.0
	s_waitcnt lgkmcnt(0)
	v_add_f32_e32 v107, v107, v108
	v_add_f32_e32 v106, v106, v109
	v_add_f32_e32 v140, v140, v141
	ds_bpermute_b32 v108, v159, v107
	ds_bpermute_b32 v109, v159, v106
	ds_bpermute_b32 v141, v159, v140
	s_waitcnt lgkmcnt(0)
	v_add_f32_e32 v156, v107, v108
	v_add_f32_e32 v176, v106, v109
	v_add_f32_e32 v178, v140, v141
	ds_bpermute_b32 v157, v158, v156
	ds_bpermute_b32 v177, v158, v176
	ds_bpermute_b32 v179, v158, v178
	v_mov_b32_e32 v140, 1.0
	s_and_saveexec_b64 s[0:1], s[36:37]
	v_lshlrev_b32_e32 v154, 16, v54
	v_and_b32_e32 v150, 0xffff0000, v54
	v_lshlrev_b32_e32 v155, 16, v55
	v_and_b32_e32 v151, 0xffff0000, v55
	v_lshlrev_b32_e32 v152, 16, v56
	v_and_b32_e32 v148, 0xffff0000, v56
	v_lshlrev_b32_e32 v153, 16, v57
	v_and_b32_e32 v149, 0xffff0000, v57
	s_or_b64 exec, exec, s[0:1]
	v_mov_b32_e32 v146, 1.0
	v_mov_b32_e32 v141, 1.0
	v_mov_b32_e32 v147, 1.0
	v_mov_b32_e32 v144, 1.0
	v_mov_b32_e32 v142, 1.0
	v_mov_b32_e32 v145, 1.0
	v_mov_b32_e32 v143, 1.0
	s_and_saveexec_b64 s[0:1], s[34:35]
	v_lshlrev_b32_e32 v140, 16, v50
	v_and_b32_e32 v146, 0xffff0000, v50
	v_lshlrev_b32_e32 v141, 16, v51
	v_and_b32_e32 v147, 0xffff0000, v51
	v_lshlrev_b32_e32 v144, 16, v52
	v_and_b32_e32 v142, 0xffff0000, v52
	v_lshlrev_b32_e32 v145, 16, v53
	v_and_b32_e32 v143, 0xffff0000, v53
	s_or_b64 exec, exec, s[0:1]
	s_or_b32 s0, s8, 9
	s_ashr_i32 s1, s0, 31
	s_lshl_b64 s[12:13], s[0:1], 11
	s_add_u32 s20, s29, s12
	s_addc_u32 s21, s30, s13
	global_load_dwordx4 v[106:109], v0, s[20:21] nt
	s_and_saveexec_b64 s[22:23], s[38:39]
	s_xor_b64 s[22:23], exec, s[22:23]
	s_cbranch_execz .LBB0_769
	v_mad_i64_i32 v[58:59], s[44:45], s0, v252, v[124:125]
	v_mad_i64_i32 v[62:63], s[44:45], s0, v252, v[122:123]
	v_mad_i64_i32 v[66:67], s[44:45], s0, v252, v[120:121]
	s_lshl_b64 s[44:45], s[0:1], 5
	s_add_u32 s44, s26, s44
	s_addc_u32 s45, s27, s45
	v_lshl_add_u64 v[180:181], v[118:119], 2, s[44:45]
	v_add_co_u32_e32 v182, vcc, 0x100000, v180
	flat_load_dword v170, v[180:181]
	s_nop 0
	v_addc_co_u32_e32 v183, vcc, 0, v181, vcc
	flat_load_dword v171, v[182:183]
	v_add_co_u32_e32 v180, vcc, 0x200000, v180
	global_load_dwordx4 v[58:61], v[58:59], off nt
	s_nop 0
	v_addc_co_u32_e32 v181, vcc, 0, v181, vcc
	global_load_dwordx4 v[62:65], v[62:63], off nt
	s_nop 0
	global_load_dwordx4 v[66:69], v[66:67], off nt
	s_nop 0
	flat_load_dword v172, v[180:181]
	s_andn2_saveexec_b64 s[22:23], s[22:23]
	s_cbranch_execnz .LBB0_770

; __device__ __forceinline__ unsigned pk2(float lo, float hi) { return f2bf(lo) | (f2bf(hi) << 16); }
; __device__ __forceinline__ void unpack8(const v4u w, float* f) { f[0] = bflo(w.x); f[1] = bfhi(w.x); f[2] = bflo(w.y); f[3] = bfhi(w.y); f[4] = bflo(w.z); f[5] = bfhi(w.z); f[6] = bflo(w.w); f[7] = bfhi(w.w); }
; __device__ __forceinline__ void norm_compute(const NormRow& R, int lane, v4u& ya, v4u& yc) {
;     ...
;     const float r_moba = 1.0f / sqrtf(s_moba * (1.0f / 256.0f) + EPS), r_fox = 1.0f / sqrtf(s_fox * (1.0f / 384.0f) + EPS), r_dil = 1.0f / sqrtf(s_dil * (1.0f / 384.0f) + EPS);
;     float ga[8], gc[8];
; #pragma unroll
;     for (int e = 0; e < 8; ++e) { ga[e] = 1.f; gc[e] = 1.f; }
;     if (lane >= 32) unpack8(R.ga, ga);
;     if (lane < 16) unpack8(R.gc, gc);
;     const float ra = lane < 32 ? r_moba : r_fox, rc = lane < 16 ? r_fox : r_dil;
;     ya.x = pk2(fa[0] * ra * ga[0], fa[1] * ra * ga[1]); ya.y = pk2(fa[2] * ra * ga[2], fa[3] * ra * ga[3]); ya.z = pk2(fa[4] * ra * ga[4], fa[5] * ra * ga[5]); ya.w = pk2(fa[6] * ra * ga[6], fa[7] * ra * ga[7]);
;     yc.x = pk2(fc[0] * rc * gc[0], fc[1] * rc * gc[1]); yc.y = pk2(fc[2] * rc * gc[2], fc[3] * rc * gc[3]); yc.z = pk2(fc[4] * rc * gc[4], fc[5] * rc * gc[5]); yc.w = pk2(fc[6] * rc * gc[6], fc[7] * rc * gc[7]);
; }
.LBB0_167:
	s_or_b64 exec, exec, s[20:21]
	s_waitcnt lgkmcnt(0)
	v_add_f32_e32 v178, v178, v179
	v_fmamk_f32 v178, v178, 0x3b2aaaab, v215
	v_mul_f32_e32 v179, 0x4f800000, v178
	v_cmp_gt_f32_e32 vcc, s3, v178
	v_add_f32_e32 v176, v176, v177
	v_fmamk_f32 v176, v176, 0x3b2aaaab, v215
	v_cndmask_b32_e32 v178, v178, v179, vcc
	v_sqrt_f32_e32 v179, v178
	v_mul_f32_e32 v177, 0x4f800000, v176
	v_add_f32_e32 v156, v156, v157
	v_fmamk_f32 v156, v156, 0x3b800000, v215
	v_add_u32_e32 v180, -1, v179
	v_fma_f32 v182, -v180, v179, v178
	v_add_u32_e32 v181, 1, v179
	v_cmp_ge_f32_e64 s[0:1], 0, v182
	v_mul_f32_e32 v157, 0x4f800000, v156
	s_nop 0
	v_cndmask_b32_e64 v180, v179, v180, s[0:1]
	v_fma_f32 v179, -v181, v179, v178
	v_cmp_lt_f32_e64 s[0:1], 0, v179
	s_nop 1
	v_cndmask_b32_e64 v179, v180, v181, s[0:1]
	v_cmp_gt_f32_e64 s[0:1], s3, v176
	v_mul_f32_e32 v180, 0x37800000, v179
	v_cndmask_b32_e32 v179, v179, v180, vcc
	v_cndmask_b32_e64 v176, v176, v177, s[0:1]
	v_sqrt_f32_e32 v177, v176
	v_cmp_class_f32_e32 vcc, v178, v216
	s_nop 1
	v_cndmask_b32_e32 v178, v179, v178, vcc
	v_add_u32_e32 v179, -1, v177
	v_fma_f32 v180, -v179, v177, v176
	v_cmp_ge_f32_e32 vcc, 0, v180
	v_add_u32_e32 v180, 1, v177
	s_nop 0
	v_cndmask_b32_e32 v179, v177, v179, vcc
	v_fma_f32 v177, -v180, v177, v176
	v_cmp_lt_f32_e32 vcc, 0, v177
	s_nop 1
	v_cndmask_b32_e32 v177, v179, v180, vcc
	v_cmp_gt_f32_e32 vcc, s3, v156
	v_mul_f32_e32 v179, 0x37800000, v177
	v_cndmask_b32_e64 v177, v177, v179, s[0:1]
	v_cndmask_b32_e32 v156, v156, v157, vcc
	v_sqrt_f32_e32 v157, v156
	v_cmp_class_f32_e64 s[0:1], v176, v216
	s_nop 1
	v_cndmask_b32_e64 v176, v177, v176, s[0:1]
	v_add_u32_e32 v177, -1, v157
	v_fma_f32 v179, -v177, v157, v156
	v_cmp_ge_f32_e64 s[0:1], 0, v179
	v_add_u32_e32 v179, 1, v157
	s_nop 0
	v_cndmask_b32_e64 v177, v157, v177, s[0:1]
	v_fma_f32 v157, -v179, v157, v156
	v_cmp_lt_f32_e64 s[0:1], 0, v157
	s_nop 1
	v_cndmask_b32_e64 v157, v177, v179, s[0:1]
	v_div_scale_f32 v179, s[0:1], v178, v178, 1.0
	v_rcp_f32_e32 v180, v179
	v_mul_f32_e32 v177, 0x37800000, v157
	v_cndmask_b32_e32 v157, v157, v177, vcc
	v_cmp_class_f32_e32 vcc, v156, v216
	s_nop 1
	v_cndmask_b32_e32 v156, v157, v156, vcc
	v_fma_f32 v157, -v179, v180, 1.0
	v_fmac_f32_e32 v180, v157, v180
	v_div_scale_f32 v157, vcc, 1.0, v178, 1.0
	v_mul_f32_e32 v177, v157, v180
	v_fma_f32 v181, -v179, v177, v157
	v_fmac_f32_e32 v177, v181, v180
	v_fma_f32 v157, -v179, v177, v157
	v_div_scale_f32 v179, s[0:1], v176, v176, 1.0
	v_rcp_f32_e32 v181, v179
	v_div_fmas_f32 v157, v157, v180, v177
	v_div_fixup_f32 v157, v157, v178, 1.0
	v_fma_f32 v177, -v179, v181, 1.0
	v_fmac_f32_e32 v181, v177, v181
	v_div_scale_f32 v177, vcc, 1.0, v176, 1.0
	v_mul_f32_e32 v178, v177, v181
	v_fma_f32 v180, -v179, v178, v177
	v_fmac_f32_e32 v178, v180, v181
	v_fma_f32 v177, -v179, v178, v177
	v_div_scale_f32 v179, s[0:1], v156, v156, 1.0
	v_rcp_f32_e32 v180, v179
	v_div_fmas_f32 v177, v177, v181, v178
	v_div_fixup_f32 v176, v177, v176, 1.0
	s_movk_i32 s1, 0x7fff
	v_fma_f32 v177, -v179, v180, 1.0
	v_fmac_f32_e32 v180, v177, v180
	v_div_scale_f32 v177, vcc, 1.0, v156, 1.0
	v_mul_f32_e32 v178, v177, v180
	v_fma_f32 v181, -v179, v178, v177
	v_fmac_f32_e32 v178, v181, v180
	v_fma_f32 v177, -v179, v178, v177
	v_div_fmas_f32 v177, v177, v180, v178
	v_div_fixup_f32 v156, v177, v156, 1.0
	v_cndmask_b32_e64 v156, v176, v156, s[40:41]
	v_mul_f32_e32 v132, v156, v132
	v_mul_f32_e32 v133, v156, v133
	v_mul_f32_e32 v134, v156, v134
	v_mul_f32_e32 v135, v156, v135
	v_mul_f32_e32 v138, v156, v138
	v_mul_f32_e32 v139, v156, v139
	v_mul_f32_e32 v132, v132, v150
	v_mul_f32_e32 v133, v133, v151
	v_mul_f32_e32 v136, v156, v136
	v_mul_f32_e32 v137, v156, v137
	v_mul_f32_e32 v134, v134, v148
	v_mul_f32_e32 v135, v135, v149
	v_mul_f32_e32 v138, v138, v154
	v_mul_f32_e32 v139, v139, v155
	v_mul_f32_e32 v136, v136, v152
	v_mul_f32_e32 v137, v137, v153
	v_bfe_u32 v148, v135, 16, 1
	v_bfe_u32 v149, v134, 16, 1
	v_bfe_u32 v150, v133, 16, 1
	v_bfe_u32 v151, v132, 16, 1
	v_cndmask_b32_e64 v176, v157, v176, s[34:35]
	v_add3_u32 v132, v132, v151, s1
	v_add3_u32 v133, v133, v150, s1
	v_add3_u32 v134, v134, v149, s1
	v_add3_u32 v135, v135, v148, s1
	v_bfe_u32 v148, v138, 16, 1
	v_bfe_u32 v149, v139, 16, 1
	v_bfe_u32 v150, v136, 16, 1
	v_bfe_u32 v151, v137, 16, 1
	v_add3_u32 v137, v137, v151, s1
	v_add3_u32 v136, v136, v150, s1
	v_add3_u32 v139, v139, v149, s1
	v_add3_u32 v138, v138, v148, s1
	v_mul_f32_e32 v114, v114, v176
	v_mul_f32_e32 v115, v115, v176
	v_mul_f32_e32 v116, v116, v176
	v_mul_f32_e32 v117, v117, v176
	v_lshrrev_b32_e32 v138, 16, v138
	v_lshrrev_b32_e32 v139, 16, v139
	v_lshrrev_b32_e32 v136, 16, v136
	v_lshrrev_b32_e32 v137, 16, v137
	s_mov_b32 s0, 0xffff0000
	v_mul_f32_e32 v130, v130, v176
	v_mul_f32_e32 v131, v131, v176
	v_mul_f32_e32 v114, v114, v146
	v_mul_f32_e32 v115, v115, v147
	v_mul_f32_e32 v128, v128, v176
	v_mul_f32_e32 v129, v129, v176
	v_mul_f32_e32 v116, v116, v142
	v_mul_f32_e32 v117, v117, v143
	v_and_or_b32 v135, v135, s0, v137
	v_and_or_b32 v134, v134, s0, v136
	v_and_or_b32 v133, v133, s0, v139
	v_and_or_b32 v132, v132, s0, v138
	v_mul_f32_e32 v130, v130, v140
	v_mul_f32_e32 v131, v131, v141
	v_mul_f32_e32 v128, v128, v144
	v_mul_f32_e32 v129, v129, v145
	v_bfe_u32 v136, v117, 16, 1
	v_bfe_u32 v137, v116, 16, 1
	v_bfe_u32 v138, v115, 16, 1
	v_bfe_u32 v139, v114, 16, 1
	v_add3_u32 v114, v114, v139, s1
	v_add3_u32 v115, v115, v138, s1
	v_add3_u32 v116, v116, v137, s1
	v_add3_u32 v117, v117, v136, s1
	v_bfe_u32 v136, v130, 16, 1
	v_bfe_u32 v137, v131, 16, 1
	v_bfe_u32 v138, v128, 16, 1
	v_bfe_u32 v139, v129, 16, 1
	v_add3_u32 v129, v129, v139, s1
	v_add3_u32 v128, v128, v138, s1
	v_add3_u32 v131, v131, v137, s1
	v_add3_u32 v130, v130, v136, s1
	v_lshrrev_b32_e32 v130, 16, v130
	v_lshrrev_b32_e32 v131, 16, v131
	v_lshrrev_b32_e32 v128, 16, v128
	v_lshrrev_b32_e32 v129, 16, v129
	v_and_or_b32 v117, v117, s0, v129
	v_and_or_b32 v116, v116, s0, v128
	v_and_or_b32 v115, v115, s0, v131
	v_and_or_b32 v114, v114, s0, v130
	s_add_u32 s0, s24, s14
	s_addc_u32 s1, s25, s15
	global_store_dwordx4 v0, v[132:135], s[0:1]
	global_store_dwordx4 v0, v[114:117], s[0:1] offset:1024
	s_and_saveexec_b64 s[0:1], s[38:39]
	s_xor_b64 s[0:1], exec, s[0:1]
	s_cbranch_execz .LBB0_169
; __device__ __forceinline__ void unpack8(const v4u w, float* f) { f[0] = bflo(w.x); f[1] = bfhi(w.x); f[2] = bflo(w.y); f[3] = bfhi(w.y); f[4] = bflo(w.z); f[5] = bfhi(w.z); f[6] = bflo(w.w); f[7] = bfhi(w.w); }
; __device__ __forceinline__ void norm_compute(const NormRow& R, int lane, v4u& ya, v4u& yc) {
;     ...
;     else { float f0[8], f1[8], f2[8]; unpack8(R.d0, f0); unpack8(R.d1, f1); unpack8(R.d2, f2);
;         const float inv = 1.0f / (R.l0 + R.l1 + R.l2);
; #pragma unroll
;         for (int e = 0; e < 8; ++e) fc[e] = (f0[e] + f1[e] + f2[e]) * inv; }
	v_add_f32_e32 v114, v168, v167
	v_add_f32_e32 v114, v169, v114
	v_div_scale_f32 v115, s[14:15], v114, v114, 1.0
	v_rcp_f32_e32 v130, v115
	v_lshlrev_b32_e32 v134, 16, v42
	v_and_b32_e32 v135, 0xffff0000, v42
	v_lshlrev_b32_e32 v136, 16, v43
	v_fma_f32 v131, -v115, v130, 1.0
	v_fmac_f32_e32 v130, v131, v130
	v_div_scale_f32 v131, vcc, 1.0, v114, 1.0
	v_mul_f32_e32 v132, v131, v130
	v_fma_f32 v133, -v115, v132, v131
	v_fmac_f32_e32 v132, v133, v130
	v_fma_f32 v115, -v115, v132, v131
	v_div_fmas_f32 v115, v115, v130, v132
	v_div_fixup_f32 v130, v115, v114, 1.0
	v_lshlrev_b32_e32 v114, 16, v34
	v_and_b32_e32 v115, 0xffff0000, v34
	v_lshlrev_b32_e32 v132, 16, v38
	v_and_b32_e32 v133, 0xffff0000, v38
	v_add_f32_e32 v114, v132, v114
	v_add_f32_e32 v115, v133, v115
	v_and_b32_e32 v137, 0xffff0000, v43
	v_add_f32_e32 v114, v114, v134
	v_add_f32_e32 v115, v115, v135
	v_lshlrev_b32_e32 v134, 16, v39
	v_mul_f32_e32 v132, v130, v114
	v_mul_f32_e32 v133, v130, v115
	v_lshlrev_b32_e32 v114, 16, v35
	v_and_b32_e32 v115, 0xffff0000, v35
	v_and_b32_e32 v135, 0xffff0000, v39
	v_add_f32_e32 v114, v134, v114
	v_add_f32_e32 v115, v135, v115
	v_lshlrev_b32_e32 v116, 16, v37
	v_lshlrev_b32_e32 v128, 16, v41
	v_and_b32_e32 v117, 0xffff0000, v37
	v_and_b32_e32 v129, 0xffff0000, v41
	v_add_f32_e32 v114, v114, v136
	v_add_f32_e32 v115, v115, v137
	v_lshlrev_b32_e32 v134, 16, v36
	v_and_b32_e32 v135, 0xffff0000, v36
	v_lshlrev_b32_e32 v136, 16, v40
	v_and_b32_e32 v137, 0xffff0000, v40
	v_lshlrev_b32_e32 v138, 16, v44
	v_and_b32_e32 v139, 0xffff0000, v44
	v_add_f32_e32 v134, v136, v134
	v_add_f32_e32 v135, v137, v135
	v_lshlrev_b32_e32 v136, 16, v45
	v_and_b32_e32 v137, 0xffff0000, v45
	v_add_f32_e32 v116, v128, v116
	v_add_f32_e32 v117, v129, v117
	v_add_f32_e32 v134, v134, v138
	v_add_f32_e32 v135, v135, v139
	v_add_f32_e32 v116, v116, v136
	v_add_f32_e32 v117, v117, v137
	v_mul_f32_e32 v114, v130, v114
	v_mul_f32_e32 v115, v130, v115
	v_mul_f32_e32 v134, v130, v134
	v_mul_f32_e32 v135, v130, v135
	v_mul_f32_e32 v116, v130, v116
	v_mul_f32_e32 v117, v130, v117
	v_mov_b32_e32 v129, v116
	v_mov_b32_e32 v116, v135
	v_mov_b32_e32 v128, v134
	v_mov_b32_e32 v131, v114
	v_mov_b32_e32 v114, v133
	v_mov_b32_e32 v130, v132
; #define GAS __attribute__((address_space(1)))
; __device__ __forceinline__ void unpack8(const v4u w, float* f) { f[0] = bflo(w.x); f[1] = bfhi(w.x); f[2] = bflo(w.y); f[3] = bfhi(w.y); f[4] = bflo(w.z); f[5] = bfhi(w.z); f[6] = bflo(w.w); f[7] = bfhi(w.w); }
; __device__ __forceinline__ void norm_load(NormRow& R, int m, int lane, const bf16* O, const bf16* GF, const bf16* OD, const float* LD) {
;     R.oa = __builtin_nontemporal_load((const GAS v4u*)(O + (size_t)m * DM + 8 * lane));
;     if (lane < 16) { R.oc = __builtin_nontemporal_load((const GAS v4u*)(O + (size_t)m * DM + 512 + 8 * lane)); R.gc = __builtin_nontemporal_load((const GAS v4u*)(GF + (size_t)m * 384 + 256 + 8 * lane)); }
;     else { const int dc = 8 * lane - 128, hd = dc >> 6;
;         R.d0 = __builtin_nontemporal_load((const GAS v4u*)(OD + (size_t)m * 384 + dc)); R.d1 = __builtin_nontemporal_load((const GAS v4u*)(OD + OD_BRANCH + (size_t)m * 384 + dc)); R.d2 = __builtin_nontemporal_load((const GAS v4u*)(OD + 2 * OD_BRANCH + (size_t)m * 384 + dc));
;         R.l0 = LD[(size_t)m * 8 + hd]; R.l1 = LD[LD_BRANCH + (size_t)m * 8 + hd]; R.l2 = LD[2 * LD_BRANCH + (size_t)m * 8 + hd]; }
;     if (lane >= 32) R.ga = __builtin_nontemporal_load((const GAS v4u*)(GF + (size_t)m * 384 + 8 * lane - 256));
; __device__ __forceinline__ void norm_compute(const NormRow& R, int lane, v4u& ya, v4u& yc) {
;     ...
;     float sa = 0.f, sc = 0.f;
; #pragma unroll
;     for (int e = 0; e < 8; ++e) { sa += fa[e] * fa[e]; sc += fc[e] * fc[e]; }
;     const float s_moba = wave_sum(lane < 32 ? sa : 0.f), s_fox = wave_sum((lane >= 32 ? sa : 0.f) + (lane < 16 ? sc : 0.f)), s_dil = wave_sum(lane >= 16 ? sc : 0.f);
;     const float r_moba = 1.0f / sqrtf(s_moba * (1.0f / 256.0f) + EPS), r_fox = 1.0f / sqrtf(s_fox * (1.0f / 384.0f) + EPS), r_dil = 1.0f / sqrtf(s_dil * (1.0f / 384.0f) + EPS);
;     float ga[8], gc[8];
; #pragma unroll
;     for (int e = 0; e < 8; ++e) { ga[e] = 1.f; gc[e] = 1.f; }
;     if (lane >= 32) unpack8(R.ga, ga);
;     if (lane < 16) unpack8(R.gc, gc);
.LBB0_169:
	s_andn2_saveexec_b64 s[0:1], s[0:1]
	v_lshlrev_b32_e32 v130, 16, v46
	v_and_b32_e32 v114, 0xffff0000, v46
	v_lshlrev_b32_e32 v131, 16, v47
	v_and_b32_e32 v115, 0xffff0000, v47
	v_lshlrev_b32_e32 v128, 16, v48
	v_and_b32_e32 v116, 0xffff0000, v48
	v_lshlrev_b32_e32 v129, 16, v49
	v_and_b32_e32 v117, 0xffff0000, v49
	s_or_b64 exec, exec, s[0:1]
	v_lshlrev_b32_e32 v139, 16, v111
	v_lshlrev_b32_e32 v138, 16, v110
	v_and_b32_e32 v133, 0xffff0000, v111
	v_and_b32_e32 v132, 0xffff0000, v110
	v_lshlrev_b32_e32 v137, 16, v113
	v_lshlrev_b32_e32 v136, 16, v112
	v_and_b32_e32 v135, 0xffff0000, v113
	v_and_b32_e32 v134, 0xffff0000, v112
	v_mul_f32_e32 v110, v138, v138
	v_mul_f32_e32 v111, v139, v139
	v_mul_f32_e32 v112, v132, v132
	v_mul_f32_e32 v113, v133, v133
	v_mul_f32_e32 v144, v114, v114
	v_fmac_f32_e32 v144, v130, v130
	v_add_f32_e32 v110, v110, v112
	v_fmac_f32_e32 v144, v131, v131
	v_add_f32_e32 v110, v111, v110
	v_fmac_f32_e32 v144, v115, v115
	v_mul_f32_e32 v140, v136, v136
	v_mul_f32_e32 v141, v137, v137
	v_add_f32_e32 v110, v113, v110
	v_fmac_f32_e32 v144, v128, v128
	v_mul_f32_e32 v142, v134, v134
	v_mul_f32_e32 v143, v135, v135
	v_add_f32_e32 v110, v140, v110
	v_fmac_f32_e32 v144, v116, v116
	v_add_f32_e32 v110, v142, v110
	v_fmac_f32_e32 v144, v129, v129
	v_add_f32_e32 v110, v141, v110
	v_add_f32_e32 v110, v143, v110
	v_fmac_f32_e32 v144, v117, v117
	v_cndmask_b32_e64 v111, 0, v110, s[40:41]
	v_cndmask_b32_e64 v110, 0, v110, s[36:37]
	v_cndmask_b32_e64 v113, 0, v144, s[34:35]
	v_add_f32_e32 v110, v110, v113
	v_cndmask_b32_e64 v140, 0, v144, s[42:43]
	ds_bpermute_b32 v112, v164, v111
	ds_bpermute_b32 v113, v164, v110
	ds_bpermute_b32 v141, v164, v140
	v_mov_b32_e32 v154, 1.0
	v_mov_b32_e32 v150, 1.0
	s_waitcnt lgkmcnt(0)
	v_add_f32_e32 v111, v111, v112
	v_add_f32_e32 v110, v110, v113
	v_add_f32_e32 v140, v140, v141
	ds_bpermute_b32 v112, v162, v111
	ds_bpermute_b32 v113, v162, v110
	ds_bpermute_b32 v141, v162, v140
	v_mov_b32_e32 v155, 1.0
	v_mov_b32_e32 v151, 1.0
	s_waitcnt lgkmcnt(0)
	v_add_f32_e32 v111, v111, v112
	v_add_f32_e32 v110, v110, v113
	v_add_f32_e32 v140, v140, v141
	ds_bpermute_b32 v112, v161, v111
	ds_bpermute_b32 v113, v161, v110
	ds_bpermute_b32 v141, v161, v140
	v_mov_b32_e32 v152, 1.0
	v_mov_b32_e32 v148, 1.0
	s_waitcnt lgkmcnt(0)
	v_add_f32_e32 v111, v111, v112
	v_add_f32_e32 v110, v110, v113
	v_add_f32_e32 v140, v140, v141
	ds_bpermute_b32 v112, v160, v111
	ds_bpermute_b32 v113, v160, v110
	ds_bpermute_b32 v141, v160, v140
	v_mov_b32_e32 v153, 1.0
	v_mov_b32_e32 v149, 1.0
	s_waitcnt lgkmcnt(0)
	v_add_f32_e32 v111, v111, v112
	v_add_f32_e32 v110, v110, v113
	v_add_f32_e32 v140, v140, v141
	ds_bpermute_b32 v112, v159, v111
	ds_bpermute_b32 v113, v159, v110
	ds_bpermute_b32 v141, v159, v140
	s_waitcnt lgkmcnt(0)
	v_add_f32_e32 v156, v111, v112
	v_add_f32_e32 v176, v110, v113
	v_add_f32_e32 v178, v140, v141
	ds_bpermute_b32 v157, v158, v156
	ds_bpermute_b32 v177, v158, v176
	ds_bpermute_b32 v179, v158, v178
	v_mov_b32_e32 v140, 1.0
	s_and_saveexec_b64 s[0:1], s[36:37]
	v_lshlrev_b32_e32 v154, 16, v30
	v_and_b32_e32 v150, 0xffff0000, v30
	v_lshlrev_b32_e32 v155, 16, v31
	v_and_b32_e32 v151, 0xffff0000, v31
	v_lshlrev_b32_e32 v152, 16, v32
	v_and_b32_e32 v148, 0xffff0000, v32
	v_lshlrev_b32_e32 v153, 16, v33
	v_and_b32_e32 v149, 0xffff0000, v33
	s_or_b64 exec, exec, s[0:1]
	v_mov_b32_e32 v146, 1.0
	v_mov_b32_e32 v141, 1.0
	v_mov_b32_e32 v147, 1.0
	v_mov_b32_e32 v144, 1.0
	v_mov_b32_e32 v142, 1.0
	v_mov_b32_e32 v145, 1.0
	v_mov_b32_e32 v143, 1.0
	s_and_saveexec_b64 s[0:1], s[34:35]
	v_lshlrev_b32_e32 v140, 16, v26
	v_and_b32_e32 v146, 0xffff0000, v26
	v_lshlrev_b32_e32 v141, 16, v27
	v_and_b32_e32 v147, 0xffff0000, v27
	v_lshlrev_b32_e32 v144, 16, v28
	v_and_b32_e32 v142, 0xffff0000, v28
	v_lshlrev_b32_e32 v145, 16, v29
	v_and_b32_e32 v143, 0xffff0000, v29
	s_or_b64 exec, exec, s[0:1]
	s_or_b32 s0, s8, 10
	s_ashr_i32 s1, s0, 31
	s_lshl_b64 s[14:15], s[0:1], 11
	s_add_u32 s20, s29, s14
	s_addc_u32 s21, s30, s15
	global_load_dwordx4 v[110:113], v0, s[20:21] nt
	s_and_saveexec_b64 s[22:23], s[38:39]
	s_xor_b64 s[22:23], exec, s[22:23]
	s_cbranch_execz .LBB0_771
	v_mad_i64_i32 v[34:35], s[44:45], s0, v252, v[124:125]
	v_mad_i64_i32 v[38:39], s[44:45], s0, v252, v[122:123]
	v_mad_i64_i32 v[42:43], s[44:45], s0, v252, v[120:121]
	s_lshl_b64 s[44:45], s[0:1], 5
	s_add_u32 s44, s26, s44
	s_addc_u32 s45, s27, s45
	v_lshl_add_u64 v[180:181], v[118:119], 2, s[44:45]
	v_add_co_u32_e32 v168, vcc, 0x100000, v180
	flat_load_dword v167, v[180:181]
	s_nop 0
	v_addc_co_u32_e32 v169, vcc, 0, v181, vcc
	flat_load_dword v168, v[168:169]
	v_add_co_u32_e32 v180, vcc, 0x200000, v180
	global_load_dwordx4 v[34:37], v[34:35], off nt
	s_nop 0
	v_addc_co_u32_e32 v181, vcc, 0, v181, vcc
	global_load_dwordx4 v[38:41], v[38:39], off nt
	s_nop 0
	global_load_dwordx4 v[42:45], v[42:43], off nt
	s_nop 0
	flat_load_dword v169, v[180:181]
	s_andn2_saveexec_b64 s[22:23], s[22:23]
	s_cbranch_execnz .LBB0_772

; __device__ __forceinline__ unsigned pk2(float lo, float hi) { return f2bf(lo) | (f2bf(hi) << 16); }
; __device__ __forceinline__ void unpack8(const v4u w, float* f) { f[0] = bflo(w.x); f[1] = bfhi(w.x); f[2] = bflo(w.y); f[3] = bfhi(w.y); f[4] = bflo(w.z); f[5] = bfhi(w.z); f[6] = bflo(w.w); f[7] = bfhi(w.w); }
; __device__ __forceinline__ void norm_compute(const NormRow& R, int lane, v4u& ya, v4u& yc) {
;     ...
;     const float r_moba = 1.0f / sqrtf(s_moba * (1.0f / 256.0f) + EPS), r_fox = 1.0f / sqrtf(s_fox * (1.0f / 384.0f) + EPS), r_dil = 1.0f / sqrtf(s_dil * (1.0f / 384.0f) + EPS);
;     float ga[8], gc[8];
; #pragma unroll
;     for (int e = 0; e < 8; ++e) { ga[e] = 1.f; gc[e] = 1.f; }
;     if (lane >= 32) unpack8(R.ga, ga);
;     if (lane < 16) unpack8(R.gc, gc);
;     const float ra = lane < 32 ? r_moba : r_fox, rc = lane < 16 ? r_fox : r_dil;
;     ya.x = pk2(fa[0] * ra * ga[0], fa[1] * ra * ga[1]); ya.y = pk2(fa[2] * ra * ga[2], fa[3] * ra * ga[3]); ya.z = pk2(fa[4] * ra * ga[4], fa[5] * ra * ga[5]); ya.w = pk2(fa[6] * ra * ga[6], fa[7] * ra * ga[7]);
;     yc.x = pk2(fc[0] * rc * gc[0], fc[1] * rc * gc[1]); yc.y = pk2(fc[2] * rc * gc[2], fc[3] * rc * gc[3]); yc.z = pk2(fc[4] * rc * gc[4], fc[5] * rc * gc[5]); yc.w = pk2(fc[6] * rc * gc[6], fc[7] * rc * gc[7]);
; }
.LBB0_179:
	s_or_b64 exec, exec, s[20:21]
	s_waitcnt lgkmcnt(0)
	v_add_f32_e32 v178, v178, v179
	v_fmamk_f32 v178, v178, 0x3b2aaaab, v215
	v_mul_f32_e32 v179, 0x4f800000, v178
	v_cmp_gt_f32_e32 vcc, s3, v178
	v_add_f32_e32 v176, v176, v177
	v_fmamk_f32 v176, v176, 0x3b2aaaab, v215
	v_cndmask_b32_e32 v178, v178, v179, vcc
	v_sqrt_f32_e32 v179, v178
	v_mul_f32_e32 v177, 0x4f800000, v176
	v_add_f32_e32 v156, v156, v157
	v_fmamk_f32 v156, v156, 0x3b800000, v215
	v_add_u32_e32 v180, -1, v179
	v_fma_f32 v182, -v180, v179, v178
	v_add_u32_e32 v181, 1, v179
	v_cmp_ge_f32_e64 s[0:1], 0, v182
	v_mul_f32_e32 v157, 0x4f800000, v156
	s_nop 0
	v_cndmask_b32_e64 v180, v179, v180, s[0:1]
	v_fma_f32 v179, -v181, v179, v178
	v_cmp_lt_f32_e64 s[0:1], 0, v179
	s_nop 1
	v_cndmask_b32_e64 v179, v180, v181, s[0:1]
	v_cmp_gt_f32_e64 s[0:1], s3, v176
	v_mul_f32_e32 v180, 0x37800000, v179
	v_cndmask_b32_e32 v179, v179, v180, vcc
	v_cndmask_b32_e64 v176, v176, v177, s[0:1]
	v_sqrt_f32_e32 v177, v176
	v_cmp_class_f32_e32 vcc, v178, v216
	s_nop 1
	v_cndmask_b32_e32 v178, v179, v178, vcc
	v_add_u32_e32 v179, -1, v177
	v_fma_f32 v180, -v179, v177, v176
	v_cmp_ge_f32_e32 vcc, 0, v180
	v_add_u32_e32 v180, 1, v177
	s_nop 0
	v_cndmask_b32_e32 v179, v177, v179, vcc
	v_fma_f32 v177, -v180, v177, v176
	v_cmp_lt_f32_e32 vcc, 0, v177
	s_nop 1
	v_cndmask_b32_e32 v177, v179, v180, vcc
	v_cmp_gt_f32_e32 vcc, s3, v156
	v_mul_f32_e32 v179, 0x37800000, v177
	v_cndmask_b32_e64 v177, v177, v179, s[0:1]
	v_cndmask_b32_e32 v156, v156, v157, vcc
	v_sqrt_f32_e32 v157, v156
	v_cmp_class_f32_e64 s[0:1], v176, v216
	s_nop 1
	v_cndmask_b32_e64 v176, v177, v176, s[0:1]
	v_add_u32_e32 v177, -1, v157
	v_fma_f32 v179, -v177, v157, v156
	v_cmp_ge_f32_e64 s[0:1], 0, v179
	v_add_u32_e32 v179, 1, v157
	s_nop 0
	v_cndmask_b32_e64 v177, v157, v177, s[0:1]
	v_fma_f32 v157, -v179, v157, v156
	v_cmp_lt_f32_e64 s[0:1], 0, v157
	s_nop 1
	v_cndmask_b32_e64 v157, v177, v179, s[0:1]
	v_div_scale_f32 v179, s[0:1], v178, v178, 1.0
	v_rcp_f32_e32 v180, v179
	v_mul_f32_e32 v177, 0x37800000, v157
	v_cndmask_b32_e32 v157, v157, v177, vcc
	v_cmp_class_f32_e32 vcc, v156, v216
	s_nop 1
	v_cndmask_b32_e32 v156, v157, v156, vcc
	v_fma_f32 v157, -v179, v180, 1.0
	v_fmac_f32_e32 v180, v157, v180
	v_div_scale_f32 v157, vcc, 1.0, v178, 1.0
	v_mul_f32_e32 v177, v157, v180
	v_fma_f32 v181, -v179, v177, v157
	v_fmac_f32_e32 v177, v181, v180
	v_fma_f32 v157, -v179, v177, v157
	v_div_scale_f32 v179, s[0:1], v176, v176, 1.0
	v_rcp_f32_e32 v181, v179
	v_div_fmas_f32 v157, v157, v180, v177
	v_div_fixup_f32 v157, v157, v178, 1.0
	v_fma_f32 v177, -v179, v181, 1.0
	v_fmac_f32_e32 v181, v177, v181
	v_div_scale_f32 v177, vcc, 1.0, v176, 1.0
	v_mul_f32_e32 v178, v177, v181
	v_fma_f32 v180, -v179, v178, v177
	v_fmac_f32_e32 v178, v180, v181
	v_fma_f32 v177, -v179, v178, v177
	v_div_scale_f32 v179, s[0:1], v156, v156, 1.0
	v_rcp_f32_e32 v180, v179
	v_div_fmas_f32 v177, v177, v181, v178
	v_div_fixup_f32 v176, v177, v176, 1.0
	s_movk_i32 s1, 0x7fff
	v_fma_f32 v177, -v179, v180, 1.0
	v_fmac_f32_e32 v180, v177, v180
	v_div_scale_f32 v177, vcc, 1.0, v156, 1.0
	v_mul_f32_e32 v178, v177, v180
	v_fma_f32 v181, -v179, v178, v177
	v_fmac_f32_e32 v178, v181, v180
	v_fma_f32 v177, -v179, v178, v177
	v_div_fmas_f32 v177, v177, v180, v178
	v_div_fixup_f32 v156, v177, v156, 1.0
	v_cndmask_b32_e64 v156, v176, v156, s[40:41]
	v_mul_f32_e32 v132, v156, v132
	v_mul_f32_e32 v133, v156, v133
	v_mul_f32_e32 v134, v156, v134
	v_mul_f32_e32 v135, v156, v135
	v_mul_f32_e32 v138, v156, v138
	v_mul_f32_e32 v139, v156, v139
	v_mul_f32_e32 v132, v132, v150
	v_mul_f32_e32 v133, v133, v151
	v_mul_f32_e32 v136, v156, v136
	v_mul_f32_e32 v137, v156, v137
	v_mul_f32_e32 v134, v134, v148
	v_mul_f32_e32 v135, v135, v149
	v_mul_f32_e32 v138, v138, v154
	v_mul_f32_e32 v139, v139, v155
	v_mul_f32_e32 v136, v136, v152
	v_mul_f32_e32 v137, v137, v153
	v_bfe_u32 v148, v135, 16, 1
	v_bfe_u32 v149, v134, 16, 1
	v_bfe_u32 v150, v133, 16, 1
	v_bfe_u32 v151, v132, 16, 1
	v_cndmask_b32_e64 v176, v157, v176, s[34:35]
	v_add3_u32 v132, v132, v151, s1
	v_add3_u32 v133, v133, v150, s1
	v_add3_u32 v134, v134, v149, s1
	v_add3_u32 v135, v135, v148, s1
	v_bfe_u32 v148, v138, 16, 1
	v_bfe_u32 v149, v139, 16, 1
	v_bfe_u32 v150, v136, 16, 1
	v_bfe_u32 v151, v137, 16, 1
	v_add3_u32 v137, v137, v151, s1
	v_add3_u32 v136, v136, v150, s1
	v_add3_u32 v139, v139, v149, s1
	v_add3_u32 v138, v138, v148, s1
	v_mul_f32_e32 v114, v114, v176
	v_mul_f32_e32 v115, v115, v176
	v_mul_f32_e32 v116, v116, v176
	v_mul_f32_e32 v117, v117, v176
	v_lshrrev_b32_e32 v138, 16, v138
	v_lshrrev_b32_e32 v139, 16, v139
	v_lshrrev_b32_e32 v136, 16, v136
	v_lshrrev_b32_e32 v137, 16, v137
	s_mov_b32 s0, 0xffff0000
	v_mul_f32_e32 v130, v130, v176
	v_mul_f32_e32 v131, v131, v176
	v_mul_f32_e32 v114, v114, v146
	v_mul_f32_e32 v115, v115, v147
	v_mul_f32_e32 v128, v128, v176
	v_mul_f32_e32 v129, v129, v176
	v_mul_f32_e32 v116, v116, v142
	v_mul_f32_e32 v117, v117, v143
	v_and_or_b32 v135, v135, s0, v137
	v_and_or_b32 v134, v134, s0, v136
	v_and_or_b32 v133, v133, s0, v139
	v_and_or_b32 v132, v132, s0, v138
	v_mul_f32_e32 v130, v130, v140
	v_mul_f32_e32 v131, v131, v141
	v_mul_f32_e32 v128, v128, v144
	v_mul_f32_e32 v129, v129, v145
	v_bfe_u32 v136, v117, 16, 1
	v_bfe_u32 v137, v116, 16, 1
	v_bfe_u32 v138, v115, 16, 1
	v_bfe_u32 v139, v114, 16, 1
	v_add3_u32 v114, v114, v139, s1
	v_add3_u32 v115, v115, v138, s1
	v_add3_u32 v116, v116, v137, s1
	v_add3_u32 v117, v117, v136, s1
	v_bfe_u32 v136, v130, 16, 1
	v_bfe_u32 v137, v131, 16, 1
	v_bfe_u32 v138, v128, 16, 1
	v_bfe_u32 v139, v129, 16, 1
	v_add3_u32 v129, v129, v139, s1
	v_add3_u32 v128, v128, v138, s1
	v_add3_u32 v131, v131, v137, s1
	v_add3_u32 v130, v130, v136, s1
	v_lshrrev_b32_e32 v130, 16, v130
	v_lshrrev_b32_e32 v131, 16, v131
	v_lshrrev_b32_e32 v128, 16, v128
	v_lshrrev_b32_e32 v129, 16, v129
	v_and_or_b32 v117, v117, s0, v129
	v_and_or_b32 v116, v116, s0, v128
	v_and_or_b32 v115, v115, s0, v131
	v_and_or_b32 v114, v114, s0, v130
	s_add_u32 s0, s24, s16
	s_addc_u32 s1, s25, s17
	global_store_dwordx4 v0, v[132:135], s[0:1]
	global_store_dwordx4 v0, v[114:117], s[0:1] offset:1024
	s_and_saveexec_b64 s[0:1], s[38:39]
	s_xor_b64 s[0:1], exec, s[0:1]
	s_cbranch_execz .LBB0_181
; __device__ __forceinline__ void unpack8(const v4u w, float* f) { f[0] = bflo(w.x); f[1] = bfhi(w.x); f[2] = bflo(w.y); f[3] = bfhi(w.y); f[4] = bflo(w.z); f[5] = bfhi(w.z); f[6] = bflo(w.w); f[7] = bfhi(w.w); }
; __device__ __forceinline__ void norm_compute(const NormRow& R, int lane, v4u& ya, v4u& yc) {
;     ...
;     else { float f0[8], f1[8], f2[8]; unpack8(R.d0, f0); unpack8(R.d1, f1); unpack8(R.d2, f2);
;         const float inv = 1.0f / (R.l0 + R.l1 + R.l2);
; #pragma unroll
;         for (int e = 0; e < 8; ++e) fc[e] = (f0[e] + f1[e] + f2[e]) * inv; }
	v_add_f32_e32 v115, v165, v163
	v_add_f32_e32 v128, v166, v115
	v_div_scale_f32 v129, s[16:17], v128, v128, 1.0
	v_rcp_f32_e32 v130, v129
	v_lshlrev_b32_e32 v134, 16, v18
	v_and_b32_e32 v135, 0xffff0000, v18
	v_lshlrev_b32_e32 v138, 16, v20
	v_fma_f32 v131, -v129, v130, 1.0
	v_fmac_f32_e32 v130, v131, v130
	v_div_scale_f32 v131, vcc, 1.0, v128, 1.0
	v_mul_f32_e32 v132, v131, v130
	v_fma_f32 v133, -v129, v132, v131
	v_fmac_f32_e32 v132, v133, v130
	v_fma_f32 v129, -v129, v132, v131
	v_div_fmas_f32 v129, v129, v130, v132
	v_div_fixup_f32 v130, v129, v128, 1.0
	v_lshlrev_b32_e32 v128, 16, v10
	v_and_b32_e32 v129, 0xffff0000, v10
	v_lshlrev_b32_e32 v132, 16, v14
	v_and_b32_e32 v133, 0xffff0000, v14
	v_add_f32_e32 v128, v132, v128
	v_add_f32_e32 v129, v133, v129
	v_lshlrev_b32_e32 v132, 16, v15
	v_add_f32_e32 v128, v128, v134
	v_add_f32_e32 v129, v129, v135
	v_and_b32_e32 v133, 0xffff0000, v15
	v_mul_f32_e32 v136, v130, v128
	v_mul_f32_e32 v137, v130, v129
	v_lshlrev_b32_e32 v128, 16, v11
	v_and_b32_e32 v129, 0xffff0000, v11
	v_lshlrev_b32_e32 v134, 16, v19
	v_and_b32_e32 v135, 0xffff0000, v19
	v_add_f32_e32 v128, v132, v128
	v_add_f32_e32 v129, v133, v129
	v_lshlrev_b32_e32 v132, 16, v12
	v_add_f32_e32 v128, v128, v134
	v_add_f32_e32 v129, v129, v135
	v_and_b32_e32 v133, 0xffff0000, v12
	v_lshlrev_b32_e32 v134, 16, v16
	v_and_b32_e32 v135, 0xffff0000, v16
	v_and_b32_e32 v139, 0xffff0000, v20
	v_add_f32_e32 v132, v134, v132
	v_add_f32_e32 v133, v135, v133
	v_lshlrev_b32_e32 v114, 16, v13
	v_lshlrev_b32_e32 v116, 16, v17
	v_and_b32_e32 v115, 0xffff0000, v13
	v_and_b32_e32 v117, 0xffff0000, v17
	v_add_f32_e32 v132, v132, v138
	v_add_f32_e32 v133, v133, v139
	v_add_f32_e32 v114, v116, v114
	v_add_f32_e32 v115, v117, v115
	v_mul_f32_e32 v134, v130, v132
	v_mul_f32_e32 v135, v130, v133
	v_lshlrev_b32_e32 v132, 16, v21
	v_and_b32_e32 v133, 0xffff0000, v21
	v_add_f32_e32 v114, v114, v132
	v_add_f32_e32 v115, v115, v133
	v_mul_f32_e32 v128, v130, v128
	v_mul_f32_e32 v129, v130, v129
	v_mul_f32_e32 v131, v130, v115
	v_mul_f32_e32 v130, v130, v114
	v_mov_b32_e32 v133, v130
	v_mov_b32_e32 v130, v135
	v_mov_b32_e32 v132, v134
	v_mov_b32_e32 v135, v128
	v_mov_b32_e32 v128, v137
	v_mov_b32_e32 v134, v136
; #define GAS __attribute__((address_space(1)))
; __device__ __forceinline__ void unpack8(const v4u w, float* f) { f[0] = bflo(w.x); f[1] = bfhi(w.x); f[2] = bflo(w.y); f[3] = bfhi(w.y); f[4] = bflo(w.z); f[5] = bfhi(w.z); f[6] = bflo(w.w); f[7] = bfhi(w.w); }
; __device__ __forceinline__ void norm_load(NormRow& R, int m, int lane, const bf16* O, const bf16* GF, const bf16* OD, const float* LD) {
;     R.oa = __builtin_nontemporal_load((const GAS v4u*)(O + (size_t)m * DM + 8 * lane));
;     if (lane < 16) { R.oc = __builtin_nontemporal_load((const GAS v4u*)(O + (size_t)m * DM + 512 + 8 * lane)); R.gc = __builtin_nontemporal_load((const GAS v4u*)(GF + (size_t)m * 384 + 256 + 8 * lane)); }
;     else { const int dc = 8 * lane - 128, hd = dc >> 6;
;         R.d0 = __builtin_nontemporal_load((const GAS v4u*)(OD + (size_t)m * 384 + dc)); R.d1 = __builtin_nontemporal_load((const GAS v4u*)(OD + OD_BRANCH + (size_t)m * 384 + dc)); R.d2 = __builtin_nontemporal_load((const GAS v4u*)(OD + 2 * OD_BRANCH + (size_t)m * 384 + dc));
;         R.l0 = LD[(size_t)m * 8 + hd]; R.l1 = LD[LD_BRANCH + (size_t)m * 8 + hd]; R.l2 = LD[2 * LD_BRANCH + (size_t)m * 8 + hd]; }
;     if (lane >= 32) R.ga = __builtin_nontemporal_load((const GAS v4u*)(GF + (size_t)m * 384 + 8 * lane - 256));
; __device__ __forceinline__ void norm_compute(const NormRow& R, int lane, v4u& ya, v4u& yc) {
;     ...
;     float sa = 0.f, sc = 0.f;
; #pragma unroll
;     for (int e = 0; e < 8; ++e) { sa += fa[e] * fa[e]; sc += fc[e] * fc[e]; }
;     const float s_moba = wave_sum(lane < 32 ? sa : 0.f), s_fox = wave_sum((lane >= 32 ? sa : 0.f) + (lane < 16 ? sc : 0.f)), s_dil = wave_sum(lane >= 16 ? sc : 0.f);
;     const float r_moba = 1.0f / sqrtf(s_moba * (1.0f / 256.0f) + EPS), r_fox = 1.0f / sqrtf(s_fox * (1.0f / 384.0f) + EPS), r_dil = 1.0f / sqrtf(s_dil * (1.0f / 384.0f) + EPS);
;     float ga[8], gc[8];
; #pragma unroll
;     for (int e = 0; e < 8; ++e) { ga[e] = 1.f; gc[e] = 1.f; }
;     if (lane >= 32) unpack8(R.ga, ga);
;     if (lane < 16) unpack8(R.gc, gc);
.LBB0_181:
	s_andn2_saveexec_b64 s[0:1], s[0:1]
	v_lshlrev_b32_e32 v134, 16, v22
	v_and_b32_e32 v128, 0xffff0000, v22
	v_lshlrev_b32_e32 v135, 16, v23
	v_and_b32_e32 v129, 0xffff0000, v23
	v_lshlrev_b32_e32 v132, 16, v24
	v_and_b32_e32 v130, 0xffff0000, v24
	v_lshlrev_b32_e32 v133, 16, v25
	v_and_b32_e32 v131, 0xffff0000, v25
	s_or_b64 exec, exec, s[0:1]
	v_lshlrev_b32_e32 v139, 16, v99
	v_lshlrev_b32_e32 v138, 16, v98
	v_and_b32_e32 v99, 0xffff0000, v99
	v_and_b32_e32 v98, 0xffff0000, v98
	v_mul_f32_e32 v114, v138, v138
	v_mul_f32_e32 v115, v139, v139
	v_mul_f32_e32 v116, v98, v98
	v_mul_f32_e32 v117, v99, v99
	v_mul_f32_e32 v144, v128, v128
	v_fmac_f32_e32 v144, v134, v134
	v_add_f32_e32 v114, v114, v116
	v_lshlrev_b32_e32 v137, 16, v101
	v_lshlrev_b32_e32 v136, 16, v100
	v_fmac_f32_e32 v144, v135, v135
	v_add_f32_e32 v114, v115, v114
	v_and_b32_e32 v101, 0xffff0000, v101
	v_and_b32_e32 v100, 0xffff0000, v100
	v_fmac_f32_e32 v144, v129, v129
	v_mul_f32_e32 v140, v136, v136
	v_mul_f32_e32 v141, v137, v137
	v_add_f32_e32 v114, v117, v114
	v_fmac_f32_e32 v144, v132, v132
	v_mul_f32_e32 v142, v100, v100
	v_mul_f32_e32 v143, v101, v101
	v_add_f32_e32 v114, v140, v114
	v_fmac_f32_e32 v144, v130, v130
	v_add_f32_e32 v114, v142, v114
	v_fmac_f32_e32 v144, v133, v133
	v_add_f32_e32 v114, v141, v114
	v_add_f32_e32 v114, v143, v114
	v_fmac_f32_e32 v144, v131, v131
	v_cndmask_b32_e64 v115, 0, v114, s[40:41]
	v_cndmask_b32_e64 v114, 0, v114, s[36:37]
	v_cndmask_b32_e64 v117, 0, v144, s[34:35]
	v_add_f32_e32 v114, v114, v117
	v_cndmask_b32_e64 v140, 0, v144, s[42:43]
	ds_bpermute_b32 v116, v164, v115
	ds_bpermute_b32 v117, v164, v114
	ds_bpermute_b32 v141, v164, v140
	v_mov_b32_e32 v154, 1.0
	v_mov_b32_e32 v150, 1.0
	s_waitcnt lgkmcnt(0)
	v_add_f32_e32 v115, v115, v116
	v_add_f32_e32 v114, v114, v117
	v_add_f32_e32 v140, v140, v141
	ds_bpermute_b32 v116, v162, v115
	ds_bpermute_b32 v117, v162, v114
	ds_bpermute_b32 v141, v162, v140
	v_mov_b32_e32 v155, 1.0
	v_mov_b32_e32 v151, 1.0
	s_waitcnt lgkmcnt(0)
	v_add_f32_e32 v115, v115, v116
	v_add_f32_e32 v114, v114, v117
	v_add_f32_e32 v140, v140, v141
	ds_bpermute_b32 v116, v161, v115
	ds_bpermute_b32 v117, v161, v114
	ds_bpermute_b32 v141, v161, v140
	v_mov_b32_e32 v152, 1.0
	v_mov_b32_e32 v148, 1.0
	s_waitcnt lgkmcnt(0)
	v_add_f32_e32 v115, v115, v116
	v_add_f32_e32 v114, v114, v117
	v_add_f32_e32 v140, v140, v141
	ds_bpermute_b32 v116, v160, v115
	ds_bpermute_b32 v117, v160, v114
	ds_bpermute_b32 v141, v160, v140
	v_mov_b32_e32 v153, 1.0
	v_mov_b32_e32 v149, 1.0
	s_waitcnt lgkmcnt(0)
	v_add_f32_e32 v115, v115, v116
	v_add_f32_e32 v114, v114, v117
	v_add_f32_e32 v140, v140, v141
	ds_bpermute_b32 v116, v159, v115
	ds_bpermute_b32 v117, v159, v114
	ds_bpermute_b32 v141, v159, v140
	s_waitcnt lgkmcnt(0)
	v_add_f32_e32 v156, v115, v116
	v_add_f32_e32 v176, v114, v117
	v_add_f32_e32 v178, v140, v141
	ds_bpermute_b32 v157, v158, v156
	ds_bpermute_b32 v177, v158, v176
	ds_bpermute_b32 v179, v158, v178
	v_mov_b32_e32 v140, 1.0
	s_and_saveexec_b64 s[0:1], s[36:37]
	v_lshlrev_b32_e32 v154, 16, v6
	v_and_b32_e32 v150, 0xffff0000, v6
	v_lshlrev_b32_e32 v155, 16, v7
	v_and_b32_e32 v151, 0xffff0000, v7
	v_lshlrev_b32_e32 v152, 16, v8
	v_and_b32_e32 v148, 0xffff0000, v8
	v_lshlrev_b32_e32 v153, 16, v9
	v_and_b32_e32 v149, 0xffff0000, v9
	s_or_b64 exec, exec, s[0:1]
	v_mov_b32_e32 v146, 1.0
	v_mov_b32_e32 v141, 1.0
	v_mov_b32_e32 v147, 1.0
	v_mov_b32_e32 v144, 1.0
	v_mov_b32_e32 v142, 1.0
	v_mov_b32_e32 v145, 1.0
	v_mov_b32_e32 v143, 1.0
	s_and_saveexec_b64 s[0:1], s[34:35]
	v_lshlrev_b32_e32 v140, 16, v2
	v_and_b32_e32 v146, 0xffff0000, v2
	v_lshlrev_b32_e32 v141, 16, v3
	v_and_b32_e32 v147, 0xffff0000, v3
	v_lshlrev_b32_e32 v144, 16, v4
	v_and_b32_e32 v142, 0xffff0000, v4
	v_lshlrev_b32_e32 v145, 16, v5
	v_and_b32_e32 v143, 0xffff0000, v5
	s_or_b64 exec, exec, s[0:1]
	s_or_b32 s0, s8, 11
	s_ashr_i32 s1, s0, 31
	s_lshl_b64 s[16:17], s[0:1], 11
	s_add_u32 s20, s29, s16
	s_addc_u32 s21, s30, s17
	global_load_dwordx4 v[114:117], v0, s[20:21] nt
	s_and_saveexec_b64 s[22:23], s[38:39]
	s_xor_b64 s[22:23], exec, s[22:23]
	s_cbranch_execz .LBB0_773
	v_mad_i64_i32 v[10:11], s[44:45], s0, v252, v[124:125]
	v_mad_i64_i32 v[14:15], s[44:45], s0, v252, v[122:123]
	v_mad_i64_i32 v[18:19], s[44:45], s0, v252, v[120:121]
	s_lshl_b64 s[44:45], s[0:1], 5
	s_add_u32 s44, s26, s44
	s_addc_u32 s45, s27, s45
	v_lshl_add_u64 v[180:181], v[118:119], 2, s[44:45]
	v_add_co_u32_e32 v182, vcc, 0x100000, v180
	flat_load_dword v163, v[180:181]
	s_nop 0
	v_addc_co_u32_e32 v183, vcc, 0, v181, vcc
	flat_load_dword v165, v[182:183]
	v_add_co_u32_e32 v180, vcc, 0x200000, v180
	global_load_dwordx4 v[10:13], v[10:11], off nt
	s_nop 0
	v_addc_co_u32_e32 v181, vcc, 0, v181, vcc
	global_load_dwordx4 v[14:17], v[14:15], off nt
	s_nop 0
	global_load_dwordx4 v[18:21], v[18:19], off nt
	s_nop 0
	flat_load_dword v166, v[180:181]
	s_andn2_saveexec_b64 s[22:23], s[22:23]
	s_cbranch_execnz .LBB0_774

; __device__ __forceinline__ unsigned pk2(float lo, float hi) { return f2bf(lo) | (f2bf(hi) << 16); }
; __device__ __forceinline__ void unpack8(const v4u w, float* f) { f[0] = bflo(w.x); f[1] = bfhi(w.x); f[2] = bflo(w.y); f[3] = bfhi(w.y); f[4] = bflo(w.z); f[5] = bfhi(w.z); f[6] = bflo(w.w); f[7] = bfhi(w.w); }
; __device__ __forceinline__ void norm_compute(const NormRow& R, int lane, v4u& ya, v4u& yc) {
;     ...
;     const float r_moba = 1.0f / sqrtf(s_moba * (1.0f / 256.0f) + EPS), r_fox = 1.0f / sqrtf(s_fox * (1.0f / 384.0f) + EPS), r_dil = 1.0f / sqrtf(s_dil * (1.0f / 384.0f) + EPS);
;     float ga[8], gc[8];
; #pragma unroll
;     for (int e = 0; e < 8; ++e) { ga[e] = 1.f; gc[e] = 1.f; }
;     if (lane >= 32) unpack8(R.ga, ga);
;     if (lane < 16) unpack8(R.gc, gc);
;     const float ra = lane < 32 ? r_moba : r_fox, rc = lane < 16 ? r_fox : r_dil;
;     ya.x = pk2(fa[0] * ra * ga[0], fa[1] * ra * ga[1]); ya.y = pk2(fa[2] * ra * ga[2], fa[3] * ra * ga[3]); ya.z = pk2(fa[4] * ra * ga[4], fa[5] * ra * ga[5]); ya.w = pk2(fa[6] * ra * ga[6], fa[7] * ra * ga[7]);
;     yc.x = pk2(fc[0] * rc * gc[0], fc[1] * rc * gc[1]); yc.y = pk2(fc[2] * rc * gc[2], fc[3] * rc * gc[3]); yc.z = pk2(fc[4] * rc * gc[4], fc[5] * rc * gc[5]); yc.w = pk2(fc[6] * rc * gc[6], fc[7] * rc * gc[7]);
; }
.LBB0_191:
	s_or_b64 exec, exec, s[20:21]
	s_waitcnt lgkmcnt(0)
	v_add_f32_e32 v178, v178, v179
	v_fmamk_f32 v178, v178, 0x3b2aaaab, v215
	v_mul_f32_e32 v179, 0x4f800000, v178
	v_cmp_gt_f32_e32 vcc, s3, v178
	v_add_f32_e32 v176, v176, v177
	v_fmamk_f32 v176, v176, 0x3b2aaaab, v215
	v_cndmask_b32_e32 v178, v178, v179, vcc
	v_sqrt_f32_e32 v179, v178
	v_mul_f32_e32 v177, 0x4f800000, v176
	v_add_f32_e32 v156, v156, v157
	v_fmamk_f32 v156, v156, 0x3b800000, v215
	v_add_u32_e32 v180, -1, v179
	v_fma_f32 v182, -v180, v179, v178
	v_add_u32_e32 v181, 1, v179
	v_cmp_ge_f32_e64 s[0:1], 0, v182
	v_mul_f32_e32 v157, 0x4f800000, v156
	s_nop 0
	v_cndmask_b32_e64 v180, v179, v180, s[0:1]
	v_fma_f32 v179, -v181, v179, v178
	v_cmp_lt_f32_e64 s[0:1], 0, v179
	s_nop 1
	v_cndmask_b32_e64 v179, v180, v181, s[0:1]
	v_cmp_gt_f32_e64 s[0:1], s3, v176
	v_mul_f32_e32 v180, 0x37800000, v179
	v_cndmask_b32_e32 v179, v179, v180, vcc
	v_cndmask_b32_e64 v176, v176, v177, s[0:1]
	v_sqrt_f32_e32 v177, v176
	v_cmp_class_f32_e32 vcc, v178, v216
	s_nop 1
	v_cndmask_b32_e32 v178, v179, v178, vcc
	v_add_u32_e32 v179, -1, v177
	v_fma_f32 v180, -v179, v177, v176
	v_cmp_ge_f32_e32 vcc, 0, v180
	v_add_u32_e32 v180, 1, v177
	s_nop 0
	v_cndmask_b32_e32 v179, v177, v179, vcc
	v_fma_f32 v177, -v180, v177, v176
	v_cmp_lt_f32_e32 vcc, 0, v177
	s_nop 1
	v_cndmask_b32_e32 v177, v179, v180, vcc
	v_cmp_gt_f32_e32 vcc, s3, v156
	v_mul_f32_e32 v179, 0x37800000, v177
	v_cndmask_b32_e64 v177, v177, v179, s[0:1]
	v_cndmask_b32_e32 v156, v156, v157, vcc
	v_sqrt_f32_e32 v157, v156
	v_cmp_class_f32_e64 s[0:1], v176, v216
	s_nop 1
	v_cndmask_b32_e64 v176, v177, v176, s[0:1]
	v_add_u32_e32 v177, -1, v157
	v_fma_f32 v179, -v177, v157, v156
	v_cmp_ge_f32_e64 s[0:1], 0, v179
	v_add_u32_e32 v179, 1, v157
	s_nop 0
	v_cndmask_b32_e64 v177, v157, v177, s[0:1]
	v_fma_f32 v157, -v179, v157, v156
	v_cmp_lt_f32_e64 s[0:1], 0, v157
	s_nop 1
	v_cndmask_b32_e64 v157, v177, v179, s[0:1]
	v_div_scale_f32 v179, s[0:1], v178, v178, 1.0
	v_rcp_f32_e32 v180, v179
	v_mul_f32_e32 v177, 0x37800000, v157
	v_cndmask_b32_e32 v157, v157, v177, vcc
	v_cmp_class_f32_e32 vcc, v156, v216
	s_nop 1
	v_cndmask_b32_e32 v156, v157, v156, vcc
	v_fma_f32 v157, -v179, v180, 1.0
	v_fmac_f32_e32 v180, v157, v180
	v_div_scale_f32 v157, vcc, 1.0, v178, 1.0
	v_mul_f32_e32 v177, v157, v180
	v_fma_f32 v181, -v179, v177, v157
	v_fmac_f32_e32 v177, v181, v180
	v_fma_f32 v157, -v179, v177, v157
	v_div_scale_f32 v179, s[0:1], v176, v176, 1.0
	v_rcp_f32_e32 v181, v179
	v_div_fmas_f32 v157, v157, v180, v177
	v_div_fixup_f32 v157, v157, v178, 1.0
	v_fma_f32 v177, -v179, v181, 1.0
	v_fmac_f32_e32 v181, v177, v181
	v_div_scale_f32 v177, vcc, 1.0, v176, 1.0
	v_mul_f32_e32 v178, v177, v181
	v_fma_f32 v180, -v179, v178, v177
	v_fmac_f32_e32 v178, v180, v181
	v_fma_f32 v177, -v179, v178, v177
	v_div_scale_f32 v179, s[0:1], v156, v156, 1.0
	v_rcp_f32_e32 v180, v179
	v_div_fmas_f32 v177, v177, v181, v178
	v_div_fixup_f32 v176, v177, v176, 1.0
	s_movk_i32 s1, 0x7fff
	v_fma_f32 v177, -v179, v180, 1.0
	v_fmac_f32_e32 v180, v177, v180
	v_div_scale_f32 v177, vcc, 1.0, v156, 1.0
	v_mul_f32_e32 v178, v177, v180
	v_fma_f32 v181, -v179, v178, v177
	v_fmac_f32_e32 v178, v181, v180
	v_fma_f32 v177, -v179, v178, v177
	v_div_fmas_f32 v177, v177, v180, v178
	v_div_fixup_f32 v156, v177, v156, 1.0
	v_cndmask_b32_e64 v156, v176, v156, s[40:41]
	v_mul_f32_e32 v98, v156, v98
	v_mul_f32_e32 v99, v156, v99
	v_mul_f32_e32 v100, v156, v100
	v_mul_f32_e32 v101, v156, v101
	v_mul_f32_e32 v138, v156, v138
	v_mul_f32_e32 v139, v156, v139
	v_mul_f32_e32 v98, v98, v150
	v_mul_f32_e32 v99, v99, v151
	v_mul_f32_e32 v136, v156, v136
	v_mul_f32_e32 v137, v156, v137
	v_mul_f32_e32 v100, v100, v148
	v_mul_f32_e32 v101, v101, v149
	v_mul_f32_e32 v138, v138, v154
	v_mul_f32_e32 v139, v139, v155
	v_mul_f32_e32 v136, v136, v152
	v_mul_f32_e32 v137, v137, v153
	v_bfe_u32 v148, v101, 16, 1
	v_bfe_u32 v149, v100, 16, 1
	v_bfe_u32 v150, v99, 16, 1
	v_bfe_u32 v151, v98, 16, 1
	v_cndmask_b32_e64 v176, v157, v176, s[34:35]
	v_add3_u32 v98, v98, v151, s1
	v_add3_u32 v99, v99, v150, s1
	v_add3_u32 v100, v100, v149, s1
	v_add3_u32 v101, v101, v148, s1
	v_bfe_u32 v148, v138, 16, 1
	v_bfe_u32 v149, v139, 16, 1
	v_bfe_u32 v150, v136, 16, 1
	v_bfe_u32 v151, v137, 16, 1
	v_add3_u32 v137, v137, v151, s1
	v_add3_u32 v136, v136, v150, s1
	v_add3_u32 v139, v139, v149, s1
	v_add3_u32 v138, v138, v148, s1
	v_mul_f32_e32 v128, v128, v176
	v_mul_f32_e32 v129, v129, v176
	v_mul_f32_e32 v130, v130, v176
	v_mul_f32_e32 v131, v131, v176
	v_lshrrev_b32_e32 v138, 16, v138
	v_lshrrev_b32_e32 v139, 16, v139
	v_lshrrev_b32_e32 v136, 16, v136
	v_lshrrev_b32_e32 v137, 16, v137
	s_mov_b32 s0, 0xffff0000
	v_mul_f32_e32 v134, v134, v176
	v_mul_f32_e32 v135, v135, v176
	v_mul_f32_e32 v128, v128, v146
	v_mul_f32_e32 v129, v129, v147
	v_mul_f32_e32 v132, v132, v176
	v_mul_f32_e32 v133, v133, v176
	v_mul_f32_e32 v130, v130, v142
	v_mul_f32_e32 v131, v131, v143
	v_and_or_b32 v101, v101, s0, v137
	v_and_or_b32 v100, v100, s0, v136
	v_and_or_b32 v99, v99, s0, v139
	v_and_or_b32 v98, v98, s0, v138
	v_mul_f32_e32 v134, v134, v140
	v_mul_f32_e32 v135, v135, v141
	v_mul_f32_e32 v132, v132, v144
	v_mul_f32_e32 v133, v133, v145
	v_bfe_u32 v136, v131, 16, 1
	v_bfe_u32 v137, v130, 16, 1
	v_bfe_u32 v138, v129, 16, 1
	v_bfe_u32 v139, v128, 16, 1
	v_add3_u32 v128, v128, v139, s1
	v_add3_u32 v129, v129, v138, s1
	v_add3_u32 v130, v130, v137, s1
	v_add3_u32 v131, v131, v136, s1
	v_bfe_u32 v136, v134, 16, 1
	v_bfe_u32 v137, v135, 16, 1
	v_bfe_u32 v138, v132, 16, 1
	v_bfe_u32 v139, v133, 16, 1
	v_add3_u32 v133, v133, v139, s1
	v_add3_u32 v132, v132, v138, s1
	v_add3_u32 v135, v135, v137, s1
	v_add3_u32 v134, v134, v136, s1
	v_lshrrev_b32_e32 v134, 16, v134
	v_lshrrev_b32_e32 v135, 16, v135
	v_lshrrev_b32_e32 v132, 16, v132
	v_lshrrev_b32_e32 v133, 16, v133
	v_and_or_b32 v131, v131, s0, v133
	v_and_or_b32 v130, v130, s0, v132
	v_and_or_b32 v129, v129, s0, v135
	v_and_or_b32 v128, v128, s0, v134
	s_add_u32 s0, s24, s18
	s_addc_u32 s1, s25, s19
	global_store_dwordx4 v0, v[98:101], s[0:1]
	global_store_dwordx4 v0, v[128:131], s[0:1] offset:1024
	s_and_saveexec_b64 s[0:1], s[38:39]
	s_xor_b64 s[0:1], exec, s[0:1]
	s_cbranch_execz .LBB0_193
; __device__ __forceinline__ void unpack8(const v4u w, float* f) { f[0] = bflo(w.x); f[1] = bfhi(w.x); f[2] = bflo(w.y); f[3] = bfhi(w.y); f[4] = bflo(w.z); f[5] = bfhi(w.z); f[6] = bflo(w.w); f[7] = bfhi(w.w); }
; __device__ __forceinline__ void norm_compute(const NormRow& R, int lane, v4u& ya, v4u& yc) {
;     ...
;     else { float f0[8], f1[8], f2[8]; unpack8(R.d0, f0); unpack8(R.d1, f1); unpack8(R.d2, f2);
;         const float inv = 1.0f / (R.l0 + R.l1 + R.l2);
; #pragma unroll
;         for (int e = 0; e < 8; ++e) fc[e] = (f0[e] + f1[e] + f2[e]) * inv; }
	s_waitcnt vmcnt(0)
	v_add_f32_e32 v99, v173, v174
	v_add_f32_e32 v128, v99, v175
	v_div_scale_f32 v129, s[18:19], v128, v128, 1.0
	v_rcp_f32_e32 v130, v129
	v_lshlrev_b32_e32 v134, 16, v90
	v_and_b32_e32 v135, 0xffff0000, v90
	v_lshlrev_b32_e32 v138, 16, v92
	v_fma_f32 v131, -v129, v130, 1.0
	v_fmac_f32_e32 v130, v131, v130
	v_div_scale_f32 v131, vcc, 1.0, v128, 1.0
	v_mul_f32_e32 v132, v131, v130
	v_fma_f32 v133, -v129, v132, v131
	v_fmac_f32_e32 v132, v133, v130
	v_fma_f32 v129, -v129, v132, v131
	v_div_fmas_f32 v129, v129, v130, v132
	v_div_fixup_f32 v130, v129, v128, 1.0
	v_lshlrev_b32_e32 v128, 16, v82
	v_and_b32_e32 v129, 0xffff0000, v82
	v_lshlrev_b32_e32 v132, 16, v86
	v_and_b32_e32 v133, 0xffff0000, v86
	v_add_f32_e32 v128, v132, v128
	v_add_f32_e32 v129, v133, v129
	v_lshlrev_b32_e32 v132, 16, v87
	v_add_f32_e32 v128, v128, v134
	v_add_f32_e32 v129, v129, v135
	v_and_b32_e32 v133, 0xffff0000, v87
	v_mul_f32_e32 v136, v128, v130
	v_mul_f32_e32 v137, v129, v130
	v_lshlrev_b32_e32 v128, 16, v83
	v_and_b32_e32 v129, 0xffff0000, v83
	v_lshlrev_b32_e32 v134, 16, v91
	v_and_b32_e32 v135, 0xffff0000, v91
	v_add_f32_e32 v128, v132, v128
	v_add_f32_e32 v129, v133, v129
	v_lshlrev_b32_e32 v132, 16, v84
	v_add_f32_e32 v128, v128, v134
	v_add_f32_e32 v129, v129, v135
	v_and_b32_e32 v133, 0xffff0000, v84
	v_lshlrev_b32_e32 v134, 16, v88
	v_and_b32_e32 v135, 0xffff0000, v88
	v_and_b32_e32 v139, 0xffff0000, v92
	v_add_f32_e32 v132, v134, v132
	v_add_f32_e32 v133, v135, v133
	v_lshlrev_b32_e32 v98, 16, v85
	v_lshlrev_b32_e32 v100, 16, v89
	v_and_b32_e32 v99, 0xffff0000, v85
	v_and_b32_e32 v101, 0xffff0000, v89
	v_add_f32_e32 v132, v132, v138
	v_add_f32_e32 v133, v133, v139
	v_add_f32_e32 v98, v100, v98
	v_add_f32_e32 v99, v101, v99
	v_mul_f32_e32 v134, v132, v130
	v_mul_f32_e32 v135, v133, v130
	v_lshlrev_b32_e32 v132, 16, v93
	v_and_b32_e32 v133, 0xffff0000, v93
	v_add_f32_e32 v98, v98, v132
	v_add_f32_e32 v99, v99, v133
	v_mul_f32_e32 v128, v128, v130
	v_mul_f32_e32 v129, v129, v130
	v_mul_f32_e32 v131, v99, v130
	v_mul_f32_e32 v130, v98, v130
	v_mov_b32_e32 v132, v134
	v_mov_b32_e32 v133, v130
	v_mov_b32_e32 v130, v135
	v_mov_b32_e32 v135, v128
	v_mov_b32_e32 v128, v137
	v_mov_b32_e32 v134, v136

; #define GAS __attribute__((address_space(1)))
; __device__ __forceinline__ void unpack8(const v4u w, float* f) { f[0] = bflo(w.x); f[1] = bfhi(w.x); f[2] = bflo(w.y); f[3] = bfhi(w.y); f[4] = bflo(w.z); f[5] = bfhi(w.z); f[6] = bflo(w.w); f[7] = bfhi(w.w); }
; __device__ __forceinline__ void norm_load(NormRow& R, int m, int lane, const bf16* O, const bf16* GF, const bf16* OD, const float* LD) {
;     R.oa = __builtin_nontemporal_load((const GAS v4u*)(O + (size_t)m * DM + 8 * lane));
;     if (lane < 16) { R.oc = __builtin_nontemporal_load((const GAS v4u*)(O + (size_t)m * DM + 512 + 8 * lane)); R.gc = __builtin_nontemporal_load((const GAS v4u*)(GF + (size_t)m * 384 + 256 + 8 * lane)); }
;     else { const int dc = 8 * lane - 128, hd = dc >> 6;
;         R.d0 = __builtin_nontemporal_load((const GAS v4u*)(OD + (size_t)m * 384 + dc)); R.d1 = __builtin_nontemporal_load((const GAS v4u*)(OD + OD_BRANCH + (size_t)m * 384 + dc)); R.d2 = __builtin_nontemporal_load((const GAS v4u*)(OD + 2 * OD_BRANCH + (size_t)m * 384 + dc));
;         R.l0 = LD[(size_t)m * 8 + hd]; R.l1 = LD[LD_BRANCH + (size_t)m * 8 + hd]; R.l2 = LD[2 * LD_BRANCH + (size_t)m * 8 + hd]; }
;     if (lane >= 32) R.ga = __builtin_nontemporal_load((const GAS v4u*)(GF + (size_t)m * 384 + 8 * lane - 256));
; __device__ __forceinline__ void norm_compute(const NormRow& R, int lane, v4u& ya, v4u& yc) {
;     ...
;     float sa = 0.f, sc = 0.f;
; #pragma unroll
;     for (int e = 0; e < 8; ++e) { sa += fa[e] * fa[e]; sc += fc[e] * fc[e]; }
;     const float s_moba = wave_sum(lane < 32 ? sa : 0.f), s_fox = wave_sum((lane >= 32 ? sa : 0.f) + (lane < 16 ? sc : 0.f)), s_dil = wave_sum(lane >= 16 ? sc : 0.f);
;     const float r_moba = 1.0f / sqrtf(s_moba * (1.0f / 256.0f) + EPS), r_fox = 1.0f / sqrtf(s_fox * (1.0f / 384.0f) + EPS), r_dil = 1.0f / sqrtf(s_dil * (1.0f / 384.0f) + EPS);
;     float ga[8], gc[8];
; #pragma unroll
;     for (int e = 0; e < 8; ++e) { ga[e] = 1.f; gc[e] = 1.f; }
;     if (lane >= 32) unpack8(R.ga, ga);
;     if (lane < 16) unpack8(R.gc, gc);
.LBB0_195:
	s_or_b64 exec, exec, s[0:1]
	s_waitcnt vmcnt(0)
	v_lshlrev_b32_e32 v139, 16, v103
	v_lshlrev_b32_e32 v138, 16, v102
	v_and_b32_e32 v103, 0xffff0000, v103
	v_and_b32_e32 v102, 0xffff0000, v102
	v_mul_f32_e32 v98, v138, v138
	v_mul_f32_e32 v99, v139, v139
	v_mul_f32_e32 v100, v102, v102
	v_mul_f32_e32 v101, v103, v103
	v_mul_f32_e32 v144, v128, v128
	v_fmac_f32_e32 v144, v134, v134
	v_add_f32_e32 v98, v98, v100
	v_lshlrev_b32_e32 v137, 16, v105
	v_lshlrev_b32_e32 v136, 16, v104
	v_fmac_f32_e32 v144, v135, v135
	v_add_f32_e32 v98, v99, v98
	v_and_b32_e32 v105, 0xffff0000, v105
	v_and_b32_e32 v104, 0xffff0000, v104
	v_fmac_f32_e32 v144, v129, v129
	v_mul_f32_e32 v140, v136, v136
	v_mul_f32_e32 v141, v137, v137
	v_add_f32_e32 v98, v101, v98
	v_fmac_f32_e32 v144, v132, v132
	v_mul_f32_e32 v142, v104, v104
	v_mul_f32_e32 v143, v105, v105
	v_add_f32_e32 v98, v140, v98
	v_fmac_f32_e32 v144, v130, v130
	v_add_f32_e32 v98, v142, v98
	v_fmac_f32_e32 v144, v133, v133
	v_add_f32_e32 v98, v141, v98
	v_add_f32_e32 v98, v143, v98
	v_fmac_f32_e32 v144, v131, v131
	v_cndmask_b32_e64 v99, 0, v98, s[40:41]
	v_cndmask_b32_e64 v98, 0, v98, s[36:37]
	v_cndmask_b32_e64 v101, 0, v144, s[34:35]
	v_add_f32_e32 v98, v98, v101
	v_cndmask_b32_e64 v140, 0, v144, s[42:43]
	ds_bpermute_b32 v100, v164, v99
	ds_bpermute_b32 v101, v164, v98
	ds_bpermute_b32 v141, v164, v140
	v_mov_b32_e32 v154, 1.0
	v_mov_b32_e32 v150, 1.0
	s_waitcnt lgkmcnt(2)
	v_add_f32_e32 v99, v99, v100
	s_waitcnt lgkmcnt(1)
	v_add_f32_e32 v98, v98, v101
	s_waitcnt lgkmcnt(0)
	v_add_f32_e32 v140, v140, v141
	ds_bpermute_b32 v100, v162, v99
	ds_bpermute_b32 v101, v162, v98
	ds_bpermute_b32 v141, v162, v140
	v_mov_b32_e32 v155, 1.0
	v_mov_b32_e32 v151, 1.0
	s_waitcnt lgkmcnt(2)
	v_add_f32_e32 v99, v99, v100
	s_waitcnt lgkmcnt(1)
	v_add_f32_e32 v98, v98, v101
	s_waitcnt lgkmcnt(0)
	v_add_f32_e32 v140, v140, v141
	ds_bpermute_b32 v100, v161, v99
	ds_bpermute_b32 v101, v161, v98
	ds_bpermute_b32 v141, v161, v140
	v_mov_b32_e32 v152, 1.0
	v_mov_b32_e32 v148, 1.0
	s_waitcnt lgkmcnt(2)
	v_add_f32_e32 v99, v99, v100
	s_waitcnt lgkmcnt(1)
	v_add_f32_e32 v98, v98, v101
	s_waitcnt lgkmcnt(0)
	v_add_f32_e32 v140, v140, v141
	ds_bpermute_b32 v100, v160, v99
	ds_bpermute_b32 v101, v160, v98
	ds_bpermute_b32 v141, v160, v140
	v_mov_b32_e32 v153, 1.0
	v_mov_b32_e32 v149, 1.0
	s_waitcnt lgkmcnt(2)
	v_add_f32_e32 v99, v99, v100
	s_waitcnt lgkmcnt(1)
	v_add_f32_e32 v98, v98, v101
	s_waitcnt lgkmcnt(0)
	v_add_f32_e32 v140, v140, v141
	ds_bpermute_b32 v100, v159, v99
	ds_bpermute_b32 v101, v159, v98
	ds_bpermute_b32 v141, v159, v140
	s_waitcnt lgkmcnt(2)
	v_add_f32_e32 v156, v99, v100
	s_waitcnt lgkmcnt(1)
	v_add_f32_e32 v176, v98, v101
	s_waitcnt lgkmcnt(0)
	v_add_f32_e32 v178, v140, v141
	ds_bpermute_b32 v157, v158, v156
	ds_bpermute_b32 v177, v158, v176
	ds_bpermute_b32 v179, v158, v178
	v_mov_b32_e32 v140, 1.0
	s_and_saveexec_b64 s[0:1], s[36:37]
	v_lshlrev_b32_e32 v154, 16, v78
	v_and_b32_e32 v150, 0xffff0000, v78
	v_lshlrev_b32_e32 v155, 16, v79
	v_and_b32_e32 v151, 0xffff0000, v79
	v_lshlrev_b32_e32 v152, 16, v80
	v_and_b32_e32 v148, 0xffff0000, v80
	v_lshlrev_b32_e32 v153, 16, v81
	v_and_b32_e32 v149, 0xffff0000, v81
	s_or_b64 exec, exec, s[0:1]
	v_mov_b32_e32 v146, 1.0
	v_mov_b32_e32 v141, 1.0
	v_mov_b32_e32 v147, 1.0
	v_mov_b32_e32 v144, 1.0
	v_mov_b32_e32 v142, 1.0
	v_mov_b32_e32 v145, 1.0
	v_mov_b32_e32 v143, 1.0
	s_and_saveexec_b64 s[0:1], s[34:35]
	v_lshlrev_b32_e32 v140, 16, v74
	v_and_b32_e32 v146, 0xffff0000, v74
	v_lshlrev_b32_e32 v141, 16, v75
	v_and_b32_e32 v147, 0xffff0000, v75
	v_lshlrev_b32_e32 v144, 16, v76
	v_and_b32_e32 v142, 0xffff0000, v76
	v_lshlrev_b32_e32 v145, 16, v77
	v_and_b32_e32 v143, 0xffff0000, v77
	s_or_b64 exec, exec, s[0:1]
	s_or_b32 s0, s8, 12
	s_ashr_i32 s1, s0, 31
	s_lshl_b64 s[18:19], s[0:1], 11
	s_add_u32 s20, s29, s18
	s_addc_u32 s21, s30, s19
	global_load_dwordx4 v[98:101], v0, s[20:21] nt
	s_and_saveexec_b64 s[22:23], s[38:39]
	s_xor_b64 s[22:23], exec, s[22:23]
	s_cbranch_execz .LBB0_775
	v_mad_i64_i32 v[82:83], s[44:45], s0, v252, v[124:125]
	v_mad_i64_i32 v[86:87], s[44:45], s0, v252, v[122:123]
	v_mad_i64_i32 v[90:91], s[44:45], s0, v252, v[120:121]
	s_lshl_b64 s[44:45], s[0:1], 5
	s_add_u32 s44, s26, s44
	s_addc_u32 s45, s27, s45
	v_lshl_add_u64 v[180:181], v[118:119], 2, s[44:45]
	v_add_co_u32_e32 v174, vcc, 0x100000, v180
	flat_load_dword v173, v[180:181]
	s_nop 0
	v_addc_co_u32_e32 v175, vcc, 0, v181, vcc
	flat_load_dword v174, v[174:175]
	v_add_co_u32_e32 v180, vcc, 0x200000, v180
	global_load_dwordx4 v[82:85], v[82:83], off nt
	s_nop 0
	v_addc_co_u32_e32 v181, vcc, 0, v181, vcc
	global_load_dwordx4 v[86:89], v[86:87], off nt
	s_nop 0
	global_load_dwordx4 v[90:93], v[90:91], off nt
	s_nop 0
	flat_load_dword v175, v[180:181]
	s_andn2_saveexec_b64 s[22:23], s[22:23]
	s_cbranch_execnz .LBB0_776

; __device__ __forceinline__ unsigned pk2(float lo, float hi) { return f2bf(lo) | (f2bf(hi) << 16); }
; __device__ __forceinline__ void unpack8(const v4u w, float* f) { f[0] = bflo(w.x); f[1] = bfhi(w.x); f[2] = bflo(w.y); f[3] = bfhi(w.y); f[4] = bflo(w.z); f[5] = bfhi(w.z); f[6] = bflo(w.w); f[7] = bfhi(w.w); }
; __device__ __forceinline__ void norm_compute(const NormRow& R, int lane, v4u& ya, v4u& yc) {
;     ...
;     const float r_moba = 1.0f / sqrtf(s_moba * (1.0f / 256.0f) + EPS), r_fox = 1.0f / sqrtf(s_fox * (1.0f / 384.0f) + EPS), r_dil = 1.0f / sqrtf(s_dil * (1.0f / 384.0f) + EPS);
;     float ga[8], gc[8];
; #pragma unroll
;     for (int e = 0; e < 8; ++e) { ga[e] = 1.f; gc[e] = 1.f; }
;     if (lane >= 32) unpack8(R.ga, ga);
;     if (lane < 16) unpack8(R.gc, gc);
;     const float ra = lane < 32 ? r_moba : r_fox, rc = lane < 16 ? r_fox : r_dil;
;     ya.x = pk2(fa[0] * ra * ga[0], fa[1] * ra * ga[1]); ya.y = pk2(fa[2] * ra * ga[2], fa[3] * ra * ga[3]); ya.z = pk2(fa[4] * ra * ga[4], fa[5] * ra * ga[5]); ya.w = pk2(fa[6] * ra * ga[6], fa[7] * ra * ga[7]);
;     yc.x = pk2(fc[0] * rc * gc[0], fc[1] * rc * gc[1]); yc.y = pk2(fc[2] * rc * gc[2], fc[3] * rc * gc[3]); yc.z = pk2(fc[4] * rc * gc[4], fc[5] * rc * gc[5]); yc.w = pk2(fc[6] * rc * gc[6], fc[7] * rc * gc[7]);
; }
.LBB0_203:
	s_or_b64 exec, exec, s[20:21]
	s_waitcnt lgkmcnt(0)
	v_add_f32_e32 v178, v178, v179
	v_fmamk_f32 v178, v178, 0x3b2aaaab, v215
	v_mul_f32_e32 v179, 0x4f800000, v178
	v_cmp_gt_f32_e32 vcc, s3, v178
	v_add_f32_e32 v176, v176, v177
	v_fmamk_f32 v176, v176, 0x3b2aaaab, v215
	v_cndmask_b32_e32 v178, v178, v179, vcc
	v_sqrt_f32_e32 v179, v178
	v_mul_f32_e32 v177, 0x4f800000, v176
	v_add_f32_e32 v156, v156, v157
	v_fmamk_f32 v156, v156, 0x3b800000, v215
	v_add_u32_e32 v180, -1, v179
	v_fma_f32 v182, -v180, v179, v178
	v_add_u32_e32 v181, 1, v179
	v_cmp_ge_f32_e64 s[0:1], 0, v182
	v_mul_f32_e32 v157, 0x4f800000, v156
	s_nop 0
	v_cndmask_b32_e64 v180, v179, v180, s[0:1]
	v_fma_f32 v179, -v181, v179, v178
	v_cmp_lt_f32_e64 s[0:1], 0, v179
	s_nop 1
	v_cndmask_b32_e64 v179, v180, v181, s[0:1]
	v_cmp_gt_f32_e64 s[0:1], s3, v176
	v_mul_f32_e32 v180, 0x37800000, v179
	v_cndmask_b32_e32 v179, v179, v180, vcc
	v_cndmask_b32_e64 v176, v176, v177, s[0:1]
	v_sqrt_f32_e32 v177, v176
	v_cmp_class_f32_e32 vcc, v178, v216
	s_nop 1
	v_cndmask_b32_e32 v178, v179, v178, vcc
	v_add_u32_e32 v179, -1, v177
	v_fma_f32 v180, -v179, v177, v176
	v_cmp_ge_f32_e32 vcc, 0, v180
	v_add_u32_e32 v180, 1, v177
	s_nop 0
	v_cndmask_b32_e32 v179, v177, v179, vcc
	v_fma_f32 v177, -v180, v177, v176
	v_cmp_lt_f32_e32 vcc, 0, v177
	s_nop 1
	v_cndmask_b32_e32 v177, v179, v180, vcc
	v_cmp_gt_f32_e32 vcc, s3, v156
	v_mul_f32_e32 v179, 0x37800000, v177
	v_cndmask_b32_e64 v177, v177, v179, s[0:1]
	v_cndmask_b32_e32 v156, v156, v157, vcc
	v_sqrt_f32_e32 v157, v156
	v_cmp_class_f32_e64 s[0:1], v176, v216
	s_nop 1
	v_cndmask_b32_e64 v176, v177, v176, s[0:1]
	v_add_u32_e32 v177, -1, v157
	v_fma_f32 v179, -v177, v157, v156
	v_cmp_ge_f32_e64 s[0:1], 0, v179
	v_add_u32_e32 v179, 1, v157
	s_nop 0
	v_cndmask_b32_e64 v177, v157, v177, s[0:1]
	v_fma_f32 v157, -v179, v157, v156
	v_cmp_lt_f32_e64 s[0:1], 0, v157
	s_nop 1
	v_cndmask_b32_e64 v157, v177, v179, s[0:1]
	v_div_scale_f32 v179, s[0:1], v178, v178, 1.0
	v_rcp_f32_e32 v180, v179
	v_mul_f32_e32 v177, 0x37800000, v157
	v_cndmask_b32_e32 v157, v157, v177, vcc
	v_cmp_class_f32_e32 vcc, v156, v216
	s_nop 1
	v_cndmask_b32_e32 v156, v157, v156, vcc
	v_fma_f32 v157, -v179, v180, 1.0
	v_fmac_f32_e32 v180, v157, v180
	v_div_scale_f32 v157, vcc, 1.0, v178, 1.0
	v_mul_f32_e32 v177, v157, v180
	v_fma_f32 v181, -v179, v177, v157
	v_fmac_f32_e32 v177, v181, v180
	v_fma_f32 v157, -v179, v177, v157
	v_div_scale_f32 v179, s[0:1], v176, v176, 1.0
	v_rcp_f32_e32 v181, v179
	v_div_fmas_f32 v157, v157, v180, v177
	v_div_fixup_f32 v157, v157, v178, 1.0
	v_fma_f32 v177, -v179, v181, 1.0
	v_fmac_f32_e32 v181, v177, v181
	v_div_scale_f32 v177, vcc, 1.0, v176, 1.0
	v_mul_f32_e32 v178, v177, v181
	v_fma_f32 v180, -v179, v178, v177
	v_fmac_f32_e32 v178, v180, v181
	v_fma_f32 v177, -v179, v178, v177
	v_div_scale_f32 v179, s[0:1], v156, v156, 1.0
	v_rcp_f32_e32 v180, v179
	v_div_fmas_f32 v177, v177, v181, v178
	v_div_fixup_f32 v176, v177, v176, 1.0
	s_movk_i32 s1, 0x7fff
	v_fma_f32 v177, -v179, v180, 1.0
	v_fmac_f32_e32 v180, v177, v180
	v_div_scale_f32 v177, vcc, 1.0, v156, 1.0
	v_mul_f32_e32 v178, v177, v180
	v_fma_f32 v181, -v179, v178, v177
	v_fmac_f32_e32 v178, v181, v180
	v_fma_f32 v177, -v179, v178, v177
	v_div_fmas_f32 v177, v177, v180, v178
	v_div_fixup_f32 v156, v177, v156, 1.0
	v_cndmask_b32_e64 v156, v176, v156, s[40:41]
	v_mul_f32_e32 v102, v156, v102
	v_mul_f32_e32 v103, v156, v103
	v_mul_f32_e32 v104, v156, v104
	v_mul_f32_e32 v105, v156, v105
	v_mul_f32_e32 v138, v156, v138
	v_mul_f32_e32 v139, v156, v139
	v_mul_f32_e32 v102, v102, v150
	v_mul_f32_e32 v103, v103, v151
	v_mul_f32_e32 v136, v156, v136
	v_mul_f32_e32 v137, v156, v137
	v_mul_f32_e32 v104, v104, v148
	v_mul_f32_e32 v105, v105, v149
	v_mul_f32_e32 v138, v138, v154
	v_mul_f32_e32 v139, v139, v155
	v_mul_f32_e32 v136, v136, v152
	v_mul_f32_e32 v137, v137, v153
	v_bfe_u32 v148, v105, 16, 1
	v_bfe_u32 v149, v104, 16, 1
	v_bfe_u32 v150, v103, 16, 1
	v_bfe_u32 v151, v102, 16, 1
	v_cndmask_b32_e64 v176, v157, v176, s[34:35]
	v_add3_u32 v102, v102, v151, s1
	v_add3_u32 v103, v103, v150, s1
	v_add3_u32 v104, v104, v149, s1
	v_add3_u32 v105, v105, v148, s1
	v_bfe_u32 v148, v138, 16, 1
	v_bfe_u32 v149, v139, 16, 1
	v_bfe_u32 v150, v136, 16, 1
	v_bfe_u32 v151, v137, 16, 1
	v_add3_u32 v137, v137, v151, s1
	v_add3_u32 v136, v136, v150, s1
	v_add3_u32 v139, v139, v149, s1
	v_add3_u32 v138, v138, v148, s1
	v_mul_f32_e32 v128, v128, v176
	v_mul_f32_e32 v129, v129, v176
	v_mul_f32_e32 v130, v130, v176
	v_mul_f32_e32 v131, v131, v176
	v_lshrrev_b32_e32 v138, 16, v138
	v_lshrrev_b32_e32 v139, 16, v139
	v_lshrrev_b32_e32 v136, 16, v136
	v_lshrrev_b32_e32 v137, 16, v137
	s_mov_b32 s0, 0xffff0000
	v_mul_f32_e32 v134, v134, v176
	v_mul_f32_e32 v135, v135, v176
	v_mul_f32_e32 v128, v128, v146
	v_mul_f32_e32 v129, v129, v147
	v_mul_f32_e32 v132, v132, v176
	v_mul_f32_e32 v133, v133, v176
	v_mul_f32_e32 v130, v130, v142
	v_mul_f32_e32 v131, v131, v143
	v_and_or_b32 v105, v105, s0, v137
	v_and_or_b32 v104, v104, s0, v136
	v_and_or_b32 v103, v103, s0, v139
	v_and_or_b32 v102, v102, s0, v138
	v_mul_f32_e32 v134, v134, v140
	v_mul_f32_e32 v135, v135, v141
	v_mul_f32_e32 v132, v132, v144
	v_mul_f32_e32 v133, v133, v145
	v_bfe_u32 v136, v131, 16, 1
	v_bfe_u32 v137, v130, 16, 1
	v_bfe_u32 v138, v129, 16, 1
	v_bfe_u32 v139, v128, 16, 1
	v_add3_u32 v128, v128, v139, s1
	v_add3_u32 v129, v129, v138, s1
	v_add3_u32 v130, v130, v137, s1
	v_add3_u32 v131, v131, v136, s1
	v_bfe_u32 v136, v134, 16, 1
	v_bfe_u32 v137, v135, 16, 1
	v_bfe_u32 v138, v132, 16, 1
	v_bfe_u32 v139, v133, 16, 1
	v_add3_u32 v133, v133, v139, s1
	v_add3_u32 v132, v132, v138, s1
	v_add3_u32 v135, v135, v137, s1
	v_add3_u32 v134, v134, v136, s1
	v_lshrrev_b32_e32 v134, 16, v134
	v_lshrrev_b32_e32 v135, 16, v135
	v_lshrrev_b32_e32 v132, 16, v132
	v_lshrrev_b32_e32 v133, 16, v133
	v_and_or_b32 v131, v131, s0, v133
	v_and_or_b32 v130, v130, s0, v132
	v_and_or_b32 v129, v129, s0, v135
	v_and_or_b32 v128, v128, s0, v134
	s_add_u32 s0, s24, s10
	s_addc_u32 s1, s25, s11
	global_store_dwordx4 v0, v[102:105], s[0:1]
	global_store_dwordx4 v0, v[128:131], s[0:1] offset:1024
	s_and_saveexec_b64 s[0:1], s[38:39]
	s_xor_b64 s[0:1], exec, s[0:1]
	s_cbranch_execz .LBB0_205
; __device__ __forceinline__ void unpack8(const v4u w, float* f) { f[0] = bflo(w.x); f[1] = bfhi(w.x); f[2] = bflo(w.y); f[3] = bfhi(w.y); f[4] = bflo(w.z); f[5] = bfhi(w.z); f[6] = bflo(w.w); f[7] = bfhi(w.w); }
; __device__ __forceinline__ void norm_compute(const NormRow& R, int lane, v4u& ya, v4u& yc) {
;     ...
;     else { float f0[8], f1[8], f2[8]; unpack8(R.d0, f0); unpack8(R.d1, f1); unpack8(R.d2, f2);
;         const float inv = 1.0f / (R.l0 + R.l1 + R.l2);
; #pragma unroll
;         for (int e = 0; e < 8; ++e) fc[e] = (f0[e] + f1[e] + f2[e]) * inv; }
	v_add_f32_e32 v103, v171, v170
	v_add_f32_e32 v128, v172, v103
	v_div_scale_f32 v129, s[10:11], v128, v128, 1.0
	v_rcp_f32_e32 v130, v129
	v_lshlrev_b32_e32 v134, 16, v66
	v_and_b32_e32 v135, 0xffff0000, v66
	v_lshlrev_b32_e32 v138, 16, v68
	v_fma_f32 v131, -v129, v130, 1.0
	v_fmac_f32_e32 v130, v131, v130
	v_div_scale_f32 v131, vcc, 1.0, v128, 1.0
	v_mul_f32_e32 v132, v131, v130
	v_fma_f32 v133, -v129, v132, v131
	v_fmac_f32_e32 v132, v133, v130
	v_fma_f32 v129, -v129, v132, v131
	v_div_fmas_f32 v129, v129, v130, v132
	v_div_fixup_f32 v130, v129, v128, 1.0
	v_lshlrev_b32_e32 v128, 16, v58
	v_and_b32_e32 v129, 0xffff0000, v58
	v_lshlrev_b32_e32 v132, 16, v62
	v_and_b32_e32 v133, 0xffff0000, v62
	v_add_f32_e32 v128, v132, v128
	v_add_f32_e32 v129, v133, v129
	v_lshlrev_b32_e32 v132, 16, v63
	v_add_f32_e32 v128, v128, v134
	v_add_f32_e32 v129, v129, v135
	v_and_b32_e32 v133, 0xffff0000, v63
	v_mul_f32_e32 v136, v130, v128
	v_mul_f32_e32 v137, v130, v129
	v_lshlrev_b32_e32 v128, 16, v59
	v_and_b32_e32 v129, 0xffff0000, v59
	v_lshlrev_b32_e32 v134, 16, v67
	v_and_b32_e32 v135, 0xffff0000, v67
	v_add_f32_e32 v128, v132, v128
	v_add_f32_e32 v129, v133, v129
	v_lshlrev_b32_e32 v132, 16, v60
	v_add_f32_e32 v128, v128, v134
	v_add_f32_e32 v129, v129, v135
	v_and_b32_e32 v133, 0xffff0000, v60
	v_lshlrev_b32_e32 v134, 16, v64
	v_and_b32_e32 v135, 0xffff0000, v64
	v_and_b32_e32 v139, 0xffff0000, v68
	v_add_f32_e32 v132, v134, v132
	v_add_f32_e32 v133, v135, v133
	v_lshlrev_b32_e32 v102, 16, v61
	v_lshlrev_b32_e32 v104, 16, v65
	v_and_b32_e32 v103, 0xffff0000, v61
	v_and_b32_e32 v105, 0xffff0000, v65
	v_add_f32_e32 v132, v132, v138
	v_add_f32_e32 v133, v133, v139
	v_add_f32_e32 v102, v104, v102
	v_add_f32_e32 v103, v105, v103
	v_mul_f32_e32 v134, v130, v132
	v_mul_f32_e32 v135, v130, v133
	v_lshlrev_b32_e32 v132, 16, v69
	v_and_b32_e32 v133, 0xffff0000, v69
	v_add_f32_e32 v102, v102, v132
	v_add_f32_e32 v103, v103, v133
	v_mul_f32_e32 v128, v130, v128
	v_mul_f32_e32 v129, v130, v129
	v_mul_f32_e32 v131, v130, v103
	v_mul_f32_e32 v130, v130, v102
	v_mov_b32_e32 v133, v130
	v_mov_b32_e32 v130, v135
	v_mov_b32_e32 v132, v134
	v_mov_b32_e32 v135, v128
	v_mov_b32_e32 v128, v137
	v_mov_b32_e32 v134, v136
; #define GAS __attribute__((address_space(1)))
; __device__ __forceinline__ void unpack8(const v4u w, float* f) { f[0] = bflo(w.x); f[1] = bfhi(w.x); f[2] = bflo(w.y); f[3] = bfhi(w.y); f[4] = bflo(w.z); f[5] = bfhi(w.z); f[6] = bflo(w.w); f[7] = bfhi(w.w); }
; __device__ __forceinline__ void norm_load(NormRow& R, int m, int lane, const bf16* O, const bf16* GF, const bf16* OD, const float* LD) {
;     R.oa = __builtin_nontemporal_load((const GAS v4u*)(O + (size_t)m * DM + 8 * lane));
;     if (lane < 16) { R.oc = __builtin_nontemporal_load((const GAS v4u*)(O + (size_t)m * DM + 512 + 8 * lane)); R.gc = __builtin_nontemporal_load((const GAS v4u*)(GF + (size_t)m * 384 + 256 + 8 * lane)); }
;     else { const int dc = 8 * lane - 128, hd = dc >> 6;
;         R.d0 = __builtin_nontemporal_load((const GAS v4u*)(OD + (size_t)m * 384 + dc)); R.d1 = __builtin_nontemporal_load((const GAS v4u*)(OD + OD_BRANCH + (size_t)m * 384 + dc)); R.d2 = __builtin_nontemporal_load((const GAS v4u*)(OD + 2 * OD_BRANCH + (size_t)m * 384 + dc));
;         R.l0 = LD[(size_t)m * 8 + hd]; R.l1 = LD[LD_BRANCH + (size_t)m * 8 + hd]; R.l2 = LD[2 * LD_BRANCH + (size_t)m * 8 + hd]; }
;     if (lane >= 32) R.ga = __builtin_nontemporal_load((const GAS v4u*)(GF + (size_t)m * 384 + 8 * lane - 256));
; __device__ __forceinline__ void norm_compute(const NormRow& R, int lane, v4u& ya, v4u& yc) {
;     ...
;     float sa = 0.f, sc = 0.f;
; #pragma unroll
;     for (int e = 0; e < 8; ++e) { sa += fa[e] * fa[e]; sc += fc[e] * fc[e]; }
;     const float s_moba = wave_sum(lane < 32 ? sa : 0.f), s_fox = wave_sum((lane >= 32 ? sa : 0.f) + (lane < 16 ? sc : 0.f)), s_dil = wave_sum(lane >= 16 ? sc : 0.f);
;     const float r_moba = 1.0f / sqrtf(s_moba * (1.0f / 256.0f) + EPS), r_fox = 1.0f / sqrtf(s_fox * (1.0f / 384.0f) + EPS), r_dil = 1.0f / sqrtf(s_dil * (1.0f / 384.0f) + EPS);
;     float ga[8], gc[8];
; #pragma unroll
;     for (int e = 0; e < 8; ++e) { ga[e] = 1.f; gc[e] = 1.f; }
;     if (lane >= 32) unpack8(R.ga, ga);
;     if (lane < 16) unpack8(R.gc, gc);
.LBB0_205:
	s_andn2_saveexec_b64 s[0:1], s[0:1]
	v_lshlrev_b32_e32 v134, 16, v70
	v_and_b32_e32 v128, 0xffff0000, v70
	v_lshlrev_b32_e32 v135, 16, v71
	v_and_b32_e32 v129, 0xffff0000, v71
	v_lshlrev_b32_e32 v132, 16, v72
	v_and_b32_e32 v130, 0xffff0000, v72
	v_lshlrev_b32_e32 v133, 16, v73
	v_and_b32_e32 v131, 0xffff0000, v73
	s_or_b64 exec, exec, s[0:1]
	v_lshlrev_b32_e32 v139, 16, v107
	v_lshlrev_b32_e32 v138, 16, v106
	v_and_b32_e32 v107, 0xffff0000, v107
	v_and_b32_e32 v106, 0xffff0000, v106
	v_mul_f32_e32 v102, v138, v138
	v_mul_f32_e32 v103, v139, v139
	v_mul_f32_e32 v104, v106, v106
	v_mul_f32_e32 v105, v107, v107
	v_mul_f32_e32 v144, v128, v128
	v_fmac_f32_e32 v144, v134, v134
	v_add_f32_e32 v102, v102, v104
	v_lshlrev_b32_e32 v137, 16, v109
	v_lshlrev_b32_e32 v136, 16, v108
	v_fmac_f32_e32 v144, v135, v135
	v_add_f32_e32 v102, v103, v102
	v_and_b32_e32 v109, 0xffff0000, v109
	v_and_b32_e32 v108, 0xffff0000, v108
	v_fmac_f32_e32 v144, v129, v129
	v_mul_f32_e32 v140, v136, v136
	v_mul_f32_e32 v141, v137, v137
	v_add_f32_e32 v102, v105, v102
	v_fmac_f32_e32 v144, v132, v132
	v_mul_f32_e32 v142, v108, v108
	v_mul_f32_e32 v143, v109, v109
	v_add_f32_e32 v102, v140, v102
	v_fmac_f32_e32 v144, v130, v130
	v_add_f32_e32 v102, v142, v102
	v_fmac_f32_e32 v144, v133, v133
	v_add_f32_e32 v102, v141, v102
	v_add_f32_e32 v102, v143, v102
	v_fmac_f32_e32 v144, v131, v131
	v_cndmask_b32_e64 v103, 0, v102, s[40:41]
	v_cndmask_b32_e64 v102, 0, v102, s[36:37]
	v_cndmask_b32_e64 v105, 0, v144, s[34:35]
	v_add_f32_e32 v102, v102, v105
	v_cndmask_b32_e64 v140, 0, v144, s[42:43]
	ds_bpermute_b32 v104, v164, v103
	ds_bpermute_b32 v105, v164, v102
	ds_bpermute_b32 v141, v164, v140
	v_mov_b32_e32 v154, 1.0
	v_mov_b32_e32 v150, 1.0
	s_waitcnt lgkmcnt(0)
	v_add_f32_e32 v103, v103, v104
	v_add_f32_e32 v102, v102, v105
	v_add_f32_e32 v140, v140, v141
	ds_bpermute_b32 v104, v162, v103
	ds_bpermute_b32 v105, v162, v102
	ds_bpermute_b32 v141, v162, v140
	v_mov_b32_e32 v155, 1.0
	v_mov_b32_e32 v151, 1.0
	s_waitcnt lgkmcnt(0)
	v_add_f32_e32 v103, v103, v104
	v_add_f32_e32 v102, v102, v105
	v_add_f32_e32 v140, v140, v141
	ds_bpermute_b32 v104, v161, v103
	ds_bpermute_b32 v105, v161, v102
	ds_bpermute_b32 v141, v161, v140
	v_mov_b32_e32 v152, 1.0
	v_mov_b32_e32 v148, 1.0
	s_waitcnt lgkmcnt(0)
	v_add_f32_e32 v103, v103, v104
	v_add_f32_e32 v102, v102, v105
	v_add_f32_e32 v140, v140, v141
	ds_bpermute_b32 v104, v160, v103
	ds_bpermute_b32 v105, v160, v102
	ds_bpermute_b32 v141, v160, v140
	v_mov_b32_e32 v153, 1.0
	v_mov_b32_e32 v149, 1.0
	s_waitcnt lgkmcnt(0)
	v_add_f32_e32 v103, v103, v104
	v_add_f32_e32 v102, v102, v105
	v_add_f32_e32 v140, v140, v141
	ds_bpermute_b32 v104, v159, v103
	ds_bpermute_b32 v105, v159, v102
	ds_bpermute_b32 v141, v159, v140
	s_waitcnt lgkmcnt(0)
	v_add_f32_e32 v156, v103, v104
	v_add_f32_e32 v176, v102, v105
	v_add_f32_e32 v178, v140, v141
	ds_bpermute_b32 v157, v158, v156
	ds_bpermute_b32 v177, v158, v176
	ds_bpermute_b32 v179, v158, v178
	v_mov_b32_e32 v140, 1.0
	s_and_saveexec_b64 s[0:1], s[36:37]
	v_lshlrev_b32_e32 v154, 16, v54
	v_and_b32_e32 v150, 0xffff0000, v54
	v_lshlrev_b32_e32 v155, 16, v55
	v_and_b32_e32 v151, 0xffff0000, v55
	v_lshlrev_b32_e32 v152, 16, v56
	v_and_b32_e32 v148, 0xffff0000, v56
	v_lshlrev_b32_e32 v153, 16, v57
	v_and_b32_e32 v149, 0xffff0000, v57
	s_or_b64 exec, exec, s[0:1]
	v_mov_b32_e32 v146, 1.0
	v_mov_b32_e32 v141, 1.0
	v_mov_b32_e32 v147, 1.0
	v_mov_b32_e32 v144, 1.0
	v_mov_b32_e32 v142, 1.0
	v_mov_b32_e32 v145, 1.0
	v_mov_b32_e32 v143, 1.0
	s_and_saveexec_b64 s[0:1], s[34:35]
	v_lshlrev_b32_e32 v140, 16, v50
	v_and_b32_e32 v146, 0xffff0000, v50
	v_lshlrev_b32_e32 v141, 16, v51
	v_and_b32_e32 v147, 0xffff0000, v51
	v_lshlrev_b32_e32 v144, 16, v52
	v_and_b32_e32 v142, 0xffff0000, v52
	v_lshlrev_b32_e32 v145, 16, v53
	v_and_b32_e32 v143, 0xffff0000, v53
	s_or_b64 exec, exec, s[0:1]
	s_or_b32 s0, s8, 13
	s_ashr_i32 s1, s0, 31
	s_lshl_b64 s[10:11], s[0:1], 11
	s_add_u32 s20, s29, s10
	s_addc_u32 s21, s30, s11
	global_load_dwordx4 v[102:105], v0, s[20:21] nt
	s_and_saveexec_b64 s[22:23], s[38:39]
	s_xor_b64 s[22:23], exec, s[22:23]
	s_cbranch_execz .LBB0_777
	v_mad_i64_i32 v[58:59], s[44:45], s0, v252, v[124:125]
	v_mad_i64_i32 v[62:63], s[44:45], s0, v252, v[122:123]
	v_mad_i64_i32 v[66:67], s[44:45], s0, v252, v[120:121]
	s_lshl_b64 s[44:45], s[0:1], 5
	s_add_u32 s44, s26, s44
	s_addc_u32 s45, s27, s45
	v_lshl_add_u64 v[180:181], v[118:119], 2, s[44:45]
	v_add_co_u32_e32 v182, vcc, 0x100000, v180
	flat_load_dword v170, v[180:181]
	s_nop 0
	v_addc_co_u32_e32 v183, vcc, 0, v181, vcc
	flat_load_dword v171, v[182:183]
	v_add_co_u32_e32 v180, vcc, 0x200000, v180
	global_load_dwordx4 v[58:61], v[58:59], off nt
	s_nop 0
	v_addc_co_u32_e32 v181, vcc, 0, v181, vcc
	global_load_dwordx4 v[62:65], v[62:63], off nt
	s_nop 0
	global_load_dwordx4 v[66:69], v[66:67], off nt
	s_nop 0
	flat_load_dword v172, v[180:181]
	s_andn2_saveexec_b64 s[22:23], s[22:23]
	s_cbranch_execnz .LBB0_778

; __device__ __forceinline__ unsigned pk2(float lo, float hi) { return f2bf(lo) | (f2bf(hi) << 16); }
; __device__ __forceinline__ void unpack8(const v4u w, float* f) { f[0] = bflo(w.x); f[1] = bfhi(w.x); f[2] = bflo(w.y); f[3] = bfhi(w.y); f[4] = bflo(w.z); f[5] = bfhi(w.z); f[6] = bflo(w.w); f[7] = bfhi(w.w); }
; __device__ __forceinline__ void norm_compute(const NormRow& R, int lane, v4u& ya, v4u& yc) {
;     ...
;     const float r_moba = 1.0f / sqrtf(s_moba * (1.0f / 256.0f) + EPS), r_fox = 1.0f / sqrtf(s_fox * (1.0f / 384.0f) + EPS), r_dil = 1.0f / sqrtf(s_dil * (1.0f / 384.0f) + EPS);
;     float ga[8], gc[8];
; #pragma unroll
;     for (int e = 0; e < 8; ++e) { ga[e] = 1.f; gc[e] = 1.f; }
;     if (lane >= 32) unpack8(R.ga, ga);
;     if (lane < 16) unpack8(R.gc, gc);
;     const float ra = lane < 32 ? r_moba : r_fox, rc = lane < 16 ? r_fox : r_dil;
;     ya.x = pk2(fa[0] * ra * ga[0], fa[1] * ra * ga[1]); ya.y = pk2(fa[2] * ra * ga[2], fa[3] * ra * ga[3]); ya.z = pk2(fa[4] * ra * ga[4], fa[5] * ra * ga[5]); ya.w = pk2(fa[6] * ra * ga[6], fa[7] * ra * ga[7]);
;     yc.x = pk2(fc[0] * rc * gc[0], fc[1] * rc * gc[1]); yc.y = pk2(fc[2] * rc * gc[2], fc[3] * rc * gc[3]); yc.z = pk2(fc[4] * rc * gc[4], fc[5] * rc * gc[5]); yc.w = pk2(fc[6] * rc * gc[6], fc[7] * rc * gc[7]);
; }
.LBB0_215:
	s_or_b64 exec, exec, s[20:21]
	s_waitcnt lgkmcnt(0)
	v_add_f32_e32 v178, v178, v179
	v_fmamk_f32 v178, v178, 0x3b2aaaab, v215
	v_mul_f32_e32 v179, 0x4f800000, v178
	v_cmp_gt_f32_e32 vcc, s3, v178
	v_add_f32_e32 v176, v176, v177
	v_fmamk_f32 v176, v176, 0x3b2aaaab, v215
	v_cndmask_b32_e32 v178, v178, v179, vcc
	v_sqrt_f32_e32 v179, v178
	v_mul_f32_e32 v177, 0x4f800000, v176
	v_add_f32_e32 v156, v156, v157
	v_fmamk_f32 v156, v156, 0x3b800000, v215
	v_add_u32_e32 v180, -1, v179
	v_fma_f32 v182, -v180, v179, v178
	v_add_u32_e32 v181, 1, v179
	v_cmp_ge_f32_e64 s[0:1], 0, v182
	v_mul_f32_e32 v157, 0x4f800000, v156
	s_nop 0
	v_cndmask_b32_e64 v180, v179, v180, s[0:1]
	v_fma_f32 v179, -v181, v179, v178
	v_cmp_lt_f32_e64 s[0:1], 0, v179
	s_nop 1
	v_cndmask_b32_e64 v179, v180, v181, s[0:1]
	v_cmp_gt_f32_e64 s[0:1], s3, v176
	v_mul_f32_e32 v180, 0x37800000, v179
	v_cndmask_b32_e32 v179, v179, v180, vcc
	v_cndmask_b32_e64 v176, v176, v177, s[0:1]
	v_sqrt_f32_e32 v177, v176
	v_cmp_class_f32_e32 vcc, v178, v216
	s_nop 1
	v_cndmask_b32_e32 v178, v179, v178, vcc
	v_add_u32_e32 v179, -1, v177
	v_fma_f32 v180, -v179, v177, v176
	v_cmp_ge_f32_e32 vcc, 0, v180
	v_add_u32_e32 v180, 1, v177
	s_nop 0
	v_cndmask_b32_e32 v179, v177, v179, vcc
	v_fma_f32 v177, -v180, v177, v176
	v_cmp_lt_f32_e32 vcc, 0, v177
	s_nop 1
	v_cndmask_b32_e32 v177, v179, v180, vcc
	v_cmp_gt_f32_e32 vcc, s3, v156
	v_mul_f32_e32 v179, 0x37800000, v177
	v_cndmask_b32_e64 v177, v177, v179, s[0:1]
	v_cndmask_b32_e32 v156, v156, v157, vcc
	v_sqrt_f32_e32 v157, v156
	v_cmp_class_f32_e64 s[0:1], v176, v216
	s_nop 1
	v_cndmask_b32_e64 v176, v177, v176, s[0:1]
	v_add_u32_e32 v177, -1, v157
	v_fma_f32 v179, -v177, v157, v156
	v_cmp_ge_f32_e64 s[0:1], 0, v179
	v_add_u32_e32 v179, 1, v157
	s_nop 0
	v_cndmask_b32_e64 v177, v157, v177, s[0:1]
	v_fma_f32 v157, -v179, v157, v156
	v_cmp_lt_f32_e64 s[0:1], 0, v157
	s_nop 1
	v_cndmask_b32_e64 v157, v177, v179, s[0:1]
	v_div_scale_f32 v179, s[0:1], v178, v178, 1.0
	v_rcp_f32_e32 v180, v179
	v_mul_f32_e32 v177, 0x37800000, v157
	v_cndmask_b32_e32 v157, v157, v177, vcc
	v_cmp_class_f32_e32 vcc, v156, v216
	s_nop 1
	v_cndmask_b32_e32 v156, v157, v156, vcc
	v_fma_f32 v157, -v179, v180, 1.0
	v_fmac_f32_e32 v180, v157, v180
	v_div_scale_f32 v157, vcc, 1.0, v178, 1.0
	v_mul_f32_e32 v177, v157, v180
	v_fma_f32 v181, -v179, v177, v157
	v_fmac_f32_e32 v177, v181, v180
	v_fma_f32 v157, -v179, v177, v157
	v_div_scale_f32 v179, s[0:1], v176, v176, 1.0
	v_rcp_f32_e32 v181, v179
	v_div_fmas_f32 v157, v157, v180, v177
	v_div_fixup_f32 v157, v157, v178, 1.0
	v_fma_f32 v177, -v179, v181, 1.0
	v_fmac_f32_e32 v181, v177, v181
	v_div_scale_f32 v177, vcc, 1.0, v176, 1.0
	v_mul_f32_e32 v178, v177, v181
	v_fma_f32 v180, -v179, v178, v177
	v_fmac_f32_e32 v178, v180, v181
	v_fma_f32 v177, -v179, v178, v177
	v_div_scale_f32 v179, s[0:1], v156, v156, 1.0
	v_rcp_f32_e32 v180, v179
	v_div_fmas_f32 v177, v177, v181, v178
	v_div_fixup_f32 v176, v177, v176, 1.0
	s_movk_i32 s1, 0x7fff
	v_fma_f32 v177, -v179, v180, 1.0
	v_fmac_f32_e32 v180, v177, v180
	v_div_scale_f32 v177, vcc, 1.0, v156, 1.0
	v_mul_f32_e32 v178, v177, v180
	v_fma_f32 v181, -v179, v178, v177
	v_fmac_f32_e32 v178, v181, v180
	v_fma_f32 v177, -v179, v178, v177
	v_div_fmas_f32 v177, v177, v180, v178
	v_div_fixup_f32 v156, v177, v156, 1.0
	v_cndmask_b32_e64 v156, v176, v156, s[40:41]
	v_mul_f32_e32 v106, v156, v106
	v_mul_f32_e32 v107, v156, v107
	v_mul_f32_e32 v108, v156, v108
	v_mul_f32_e32 v109, v156, v109
	v_mul_f32_e32 v138, v156, v138
	v_mul_f32_e32 v139, v156, v139
	v_mul_f32_e32 v106, v106, v150
	v_mul_f32_e32 v107, v107, v151
	v_mul_f32_e32 v136, v156, v136
	v_mul_f32_e32 v137, v156, v137
	v_mul_f32_e32 v108, v108, v148
	v_mul_f32_e32 v109, v109, v149
	v_mul_f32_e32 v138, v138, v154
	v_mul_f32_e32 v139, v139, v155
	v_mul_f32_e32 v136, v136, v152
	v_mul_f32_e32 v137, v137, v153
	v_bfe_u32 v148, v109, 16, 1
	v_bfe_u32 v149, v108, 16, 1
	v_bfe_u32 v150, v107, 16, 1
	v_bfe_u32 v151, v106, 16, 1
	v_cndmask_b32_e64 v176, v157, v176, s[34:35]
	v_add3_u32 v106, v106, v151, s1
	v_add3_u32 v107, v107, v150, s1
	v_add3_u32 v108, v108, v149, s1
	v_add3_u32 v109, v109, v148, s1
	v_bfe_u32 v148, v138, 16, 1
	v_bfe_u32 v149, v139, 16, 1
	v_bfe_u32 v150, v136, 16, 1
	v_bfe_u32 v151, v137, 16, 1
	v_add3_u32 v137, v137, v151, s1
	v_add3_u32 v136, v136, v150, s1
	v_add3_u32 v139, v139, v149, s1
	v_add3_u32 v138, v138, v148, s1
	v_mul_f32_e32 v128, v128, v176
	v_mul_f32_e32 v129, v129, v176
	v_mul_f32_e32 v130, v130, v176
	v_mul_f32_e32 v131, v131, v176
	v_lshrrev_b32_e32 v138, 16, v138
	v_lshrrev_b32_e32 v139, 16, v139
	v_lshrrev_b32_e32 v136, 16, v136
	v_lshrrev_b32_e32 v137, 16, v137
	s_mov_b32 s0, 0xffff0000
	v_mul_f32_e32 v134, v134, v176
	v_mul_f32_e32 v135, v135, v176
	v_mul_f32_e32 v128, v128, v146
	v_mul_f32_e32 v129, v129, v147
	v_mul_f32_e32 v132, v132, v176
	v_mul_f32_e32 v133, v133, v176
	v_mul_f32_e32 v130, v130, v142
	v_mul_f32_e32 v131, v131, v143
	v_and_or_b32 v109, v109, s0, v137
	v_and_or_b32 v108, v108, s0, v136
	v_and_or_b32 v107, v107, s0, v139
	v_and_or_b32 v106, v106, s0, v138
	v_mul_f32_e32 v134, v134, v140
	v_mul_f32_e32 v135, v135, v141
	v_mul_f32_e32 v132, v132, v144
	v_mul_f32_e32 v133, v133, v145
	v_bfe_u32 v136, v131, 16, 1
	v_bfe_u32 v137, v130, 16, 1
	v_bfe_u32 v138, v129, 16, 1
	v_bfe_u32 v139, v128, 16, 1
	v_add3_u32 v128, v128, v139, s1
	v_add3_u32 v129, v129, v138, s1
	v_add3_u32 v130, v130, v137, s1
	v_add3_u32 v131, v131, v136, s1
	v_bfe_u32 v136, v134, 16, 1
	v_bfe_u32 v137, v135, 16, 1
	v_bfe_u32 v138, v132, 16, 1
	v_bfe_u32 v139, v133, 16, 1
	v_add3_u32 v133, v133, v139, s1
	v_add3_u32 v132, v132, v138, s1
	v_add3_u32 v135, v135, v137, s1
	v_add3_u32 v134, v134, v136, s1
	v_lshrrev_b32_e32 v134, 16, v134
	v_lshrrev_b32_e32 v135, 16, v135
	v_lshrrev_b32_e32 v132, 16, v132
	v_lshrrev_b32_e32 v133, 16, v133
	v_and_or_b32 v131, v131, s0, v133
	v_and_or_b32 v130, v130, s0, v132
	v_and_or_b32 v129, v129, s0, v135
	v_and_or_b32 v128, v128, s0, v134
	s_add_u32 s0, s24, s12
	s_addc_u32 s1, s25, s13
	global_store_dwordx4 v0, v[106:109], s[0:1]
	global_store_dwordx4 v0, v[128:131], s[0:1] offset:1024
	s_and_saveexec_b64 s[0:1], s[38:39]
	s_xor_b64 s[0:1], exec, s[0:1]
	s_cbranch_execz .LBB0_217
; __device__ __forceinline__ void unpack8(const v4u w, float* f) { f[0] = bflo(w.x); f[1] = bfhi(w.x); f[2] = bflo(w.y); f[3] = bfhi(w.y); f[4] = bflo(w.z); f[5] = bfhi(w.z); f[6] = bflo(w.w); f[7] = bfhi(w.w); }
; __device__ __forceinline__ void norm_compute(const NormRow& R, int lane, v4u& ya, v4u& yc) {
;     ...
;     else { float f0[8], f1[8], f2[8]; unpack8(R.d0, f0); unpack8(R.d1, f1); unpack8(R.d2, f2);
;         const float inv = 1.0f / (R.l0 + R.l1 + R.l2);
; #pragma unroll
;         for (int e = 0; e < 8; ++e) fc[e] = (f0[e] + f1[e] + f2[e]) * inv; }
	v_add_f32_e32 v107, v168, v167
	v_add_f32_e32 v128, v169, v107
	v_div_scale_f32 v129, s[12:13], v128, v128, 1.0
	v_rcp_f32_e32 v130, v129
	v_lshlrev_b32_e32 v134, 16, v42
	v_and_b32_e32 v135, 0xffff0000, v42
	v_lshlrev_b32_e32 v138, 16, v44
	v_fma_f32 v131, -v129, v130, 1.0
	v_fmac_f32_e32 v130, v131, v130
	v_div_scale_f32 v131, vcc, 1.0, v128, 1.0
	v_mul_f32_e32 v132, v131, v130
	v_fma_f32 v133, -v129, v132, v131
	v_fmac_f32_e32 v132, v133, v130
	v_fma_f32 v129, -v129, v132, v131
	v_div_fmas_f32 v129, v129, v130, v132
	v_div_fixup_f32 v130, v129, v128, 1.0
	v_lshlrev_b32_e32 v128, 16, v34
	v_and_b32_e32 v129, 0xffff0000, v34
	v_lshlrev_b32_e32 v132, 16, v38
	v_and_b32_e32 v133, 0xffff0000, v38
	v_add_f32_e32 v128, v132, v128
	v_add_f32_e32 v129, v133, v129
	v_lshlrev_b32_e32 v132, 16, v39
	v_add_f32_e32 v128, v128, v134
	v_add_f32_e32 v129, v129, v135
	v_and_b32_e32 v133, 0xffff0000, v39
	v_mul_f32_e32 v136, v130, v128
	v_mul_f32_e32 v137, v130, v129
	v_lshlrev_b32_e32 v128, 16, v35
	v_and_b32_e32 v129, 0xffff0000, v35
	v_lshlrev_b32_e32 v134, 16, v43
	v_and_b32_e32 v135, 0xffff0000, v43
	v_add_f32_e32 v128, v132, v128
	v_add_f32_e32 v129, v133, v129
	v_lshlrev_b32_e32 v132, 16, v36
	v_add_f32_e32 v128, v128, v134
	v_add_f32_e32 v129, v129, v135
	v_and_b32_e32 v133, 0xffff0000, v36
	v_lshlrev_b32_e32 v134, 16, v40
	v_and_b32_e32 v135, 0xffff0000, v40
	v_and_b32_e32 v139, 0xffff0000, v44
	v_add_f32_e32 v132, v134, v132
	v_add_f32_e32 v133, v135, v133
	v_lshlrev_b32_e32 v106, 16, v37
	v_lshlrev_b32_e32 v108, 16, v41
	v_and_b32_e32 v107, 0xffff0000, v37
	v_and_b32_e32 v109, 0xffff0000, v41
	v_add_f32_e32 v132, v132, v138
	v_add_f32_e32 v133, v133, v139
	v_add_f32_e32 v106, v108, v106
	v_add_f32_e32 v107, v109, v107
	v_mul_f32_e32 v134, v130, v132
	v_mul_f32_e32 v135, v130, v133
	v_lshlrev_b32_e32 v132, 16, v45
	v_and_b32_e32 v133, 0xffff0000, v45
	v_add_f32_e32 v106, v106, v132
	v_add_f32_e32 v107, v107, v133
	v_mul_f32_e32 v128, v130, v128
	v_mul_f32_e32 v129, v130, v129
	v_mul_f32_e32 v131, v130, v107
	v_mul_f32_e32 v130, v130, v106
	v_mov_b32_e32 v133, v130
	v_mov_b32_e32 v130, v135
	v_mov_b32_e32 v132, v134
	v_mov_b32_e32 v135, v128
	v_mov_b32_e32 v128, v137
	v_mov_b32_e32 v134, v136
; #define GAS __attribute__((address_space(1)))
; __device__ __forceinline__ void unpack8(const v4u w, float* f) { f[0] = bflo(w.x); f[1] = bfhi(w.x); f[2] = bflo(w.y); f[3] = bfhi(w.y); f[4] = bflo(w.z); f[5] = bfhi(w.z); f[6] = bflo(w.w); f[7] = bfhi(w.w); }
; __device__ __forceinline__ void norm_load(NormRow& R, int m, int lane, const bf16* O, const bf16* GF, const bf16* OD, const float* LD) {
;     R.oa = __builtin_nontemporal_load((const GAS v4u*)(O + (size_t)m * DM + 8 * lane));
;     if (lane < 16) { R.oc = __builtin_nontemporal_load((const GAS v4u*)(O + (size_t)m * DM + 512 + 8 * lane)); R.gc = __builtin_nontemporal_load((const GAS v4u*)(GF + (size_t)m * 384 + 256 + 8 * lane)); }
;     else { const int dc = 8 * lane - 128, hd = dc >> 6;
;         R.d0 = __builtin_nontemporal_load((const GAS v4u*)(OD + (size_t)m * 384 + dc)); R.d1 = __builtin_nontemporal_load((const GAS v4u*)(OD + OD_BRANCH + (size_t)m * 384 + dc)); R.d2 = __builtin_nontemporal_load((const GAS v4u*)(OD + 2 * OD_BRANCH + (size_t)m * 384 + dc));
;         R.l0 = LD[(size_t)m * 8 + hd]; R.l1 = LD[LD_BRANCH + (size_t)m * 8 + hd]; R.l2 = LD[2 * LD_BRANCH + (size_t)m * 8 + hd]; }
;     if (lane >= 32) R.ga = __builtin_nontemporal_load((const GAS v4u*)(GF + (size_t)m * 384 + 8 * lane - 256));
; __device__ __forceinline__ void norm_compute(const NormRow& R, int lane, v4u& ya, v4u& yc) {
;     ...
;     float sa = 0.f, sc = 0.f;
; #pragma unroll
;     for (int e = 0; e < 8; ++e) { sa += fa[e] * fa[e]; sc += fc[e] * fc[e]; }
;     const float s_moba = wave_sum(lane < 32 ? sa : 0.f), s_fox = wave_sum((lane >= 32 ? sa : 0.f) + (lane < 16 ? sc : 0.f)), s_dil = wave_sum(lane >= 16 ? sc : 0.f);
;     const float r_moba = 1.0f / sqrtf(s_moba * (1.0f / 256.0f) + EPS), r_fox = 1.0f / sqrtf(s_fox * (1.0f / 384.0f) + EPS), r_dil = 1.0f / sqrtf(s_dil * (1.0f / 384.0f) + EPS);
;     float ga[8], gc[8];
; #pragma unroll
;     for (int e = 0; e < 8; ++e) { ga[e] = 1.f; gc[e] = 1.f; }
;     if (lane >= 32) unpack8(R.ga, ga);
;     if (lane < 16) unpack8(R.gc, gc);
.LBB0_217:
	s_andn2_saveexec_b64 s[0:1], s[0:1]
	v_lshlrev_b32_e32 v134, 16, v46
	v_and_b32_e32 v128, 0xffff0000, v46
	v_lshlrev_b32_e32 v135, 16, v47
	v_and_b32_e32 v129, 0xffff0000, v47
	v_lshlrev_b32_e32 v132, 16, v48
	v_and_b32_e32 v130, 0xffff0000, v48
	v_lshlrev_b32_e32 v133, 16, v49
	v_and_b32_e32 v131, 0xffff0000, v49
	s_or_b64 exec, exec, s[0:1]
	v_lshlrev_b32_e32 v139, 16, v111
	v_lshlrev_b32_e32 v138, 16, v110
	v_and_b32_e32 v111, 0xffff0000, v111
	v_and_b32_e32 v110, 0xffff0000, v110
	v_mul_f32_e32 v106, v138, v138
	v_mul_f32_e32 v107, v139, v139
	v_mul_f32_e32 v108, v110, v110
	v_mul_f32_e32 v109, v111, v111
	v_mul_f32_e32 v144, v128, v128
	v_fmac_f32_e32 v144, v134, v134
	v_add_f32_e32 v106, v106, v108
	v_lshlrev_b32_e32 v137, 16, v113
	v_lshlrev_b32_e32 v136, 16, v112
	v_fmac_f32_e32 v144, v135, v135
	v_add_f32_e32 v106, v107, v106
	v_and_b32_e32 v113, 0xffff0000, v113
	v_and_b32_e32 v112, 0xffff0000, v112
	v_fmac_f32_e32 v144, v129, v129
	v_mul_f32_e32 v140, v136, v136
	v_mul_f32_e32 v141, v137, v137
	v_add_f32_e32 v106, v109, v106
	v_fmac_f32_e32 v144, v132, v132
	v_mul_f32_e32 v142, v112, v112
	v_mul_f32_e32 v143, v113, v113
	v_add_f32_e32 v106, v140, v106
	v_fmac_f32_e32 v144, v130, v130
	v_add_f32_e32 v106, v142, v106
	v_fmac_f32_e32 v144, v133, v133
	v_add_f32_e32 v106, v141, v106
	v_add_f32_e32 v106, v143, v106
	v_fmac_f32_e32 v144, v131, v131
	v_cndmask_b32_e64 v107, 0, v106, s[40:41]
	v_cndmask_b32_e64 v106, 0, v106, s[36:37]
	v_cndmask_b32_e64 v109, 0, v144, s[34:35]
	v_add_f32_e32 v106, v106, v109
	v_cndmask_b32_e64 v140, 0, v144, s[42:43]
	ds_bpermute_b32 v108, v164, v107
	ds_bpermute_b32 v109, v164, v106
	ds_bpermute_b32 v141, v164, v140
	v_mov_b32_e32 v154, 1.0
	v_mov_b32_e32 v150, 1.0
	s_waitcnt lgkmcnt(0)
	v_add_f32_e32 v107, v107, v108
	v_add_f32_e32 v106, v106, v109
	v_add_f32_e32 v140, v140, v141
	ds_bpermute_b32 v108, v162, v107
	ds_bpermute_b32 v109, v162, v106
	ds_bpermute_b32 v141, v162, v140
	v_mov_b32_e32 v155, 1.0
	v_mov_b32_e32 v151, 1.0
	s_waitcnt lgkmcnt(0)
	v_add_f32_e32 v107, v107, v108
	v_add_f32_e32 v106, v106, v109
	v_add_f32_e32 v140, v140, v141
	ds_bpermute_b32 v108, v161, v107
	ds_bpermute_b32 v109, v161, v106
	ds_bpermute_b32 v141, v161, v140
	v_mov_b32_e32 v152, 1.0
	v_mov_b32_e32 v148, 1.0
	s_waitcnt lgkmcnt(0)
	v_add_f32_e32 v107, v107, v108
	v_add_f32_e32 v106, v106, v109
	v_add_f32_e32 v140, v140, v141
	ds_bpermute_b32 v108, v160, v107
	ds_bpermute_b32 v109, v160, v106
	ds_bpermute_b32 v141, v160, v140
	v_mov_b32_e32 v153, 1.0
	v_mov_b32_e32 v149, 1.0
	s_waitcnt lgkmcnt(0)
	v_add_f32_e32 v107, v107, v108
	v_add_f32_e32 v106, v106, v109
	v_add_f32_e32 v140, v140, v141
	ds_bpermute_b32 v108, v159, v107
	ds_bpermute_b32 v109, v159, v106
	ds_bpermute_b32 v141, v159, v140
	s_waitcnt lgkmcnt(0)
	v_add_f32_e32 v156, v107, v108
	v_add_f32_e32 v176, v106, v109
	v_add_f32_e32 v178, v140, v141
	ds_bpermute_b32 v157, v158, v156
	ds_bpermute_b32 v177, v158, v176
	ds_bpermute_b32 v179, v158, v178
	v_mov_b32_e32 v140, 1.0
	s_and_saveexec_b64 s[0:1], s[36:37]
	v_lshlrev_b32_e32 v154, 16, v30
	v_and_b32_e32 v150, 0xffff0000, v30
	v_lshlrev_b32_e32 v155, 16, v31
	v_and_b32_e32 v151, 0xffff0000, v31
	v_lshlrev_b32_e32 v152, 16, v32
	v_and_b32_e32 v148, 0xffff0000, v32
	v_lshlrev_b32_e32 v153, 16, v33
	v_and_b32_e32 v149, 0xffff0000, v33
	s_or_b64 exec, exec, s[0:1]
	v_mov_b32_e32 v146, 1.0
	v_mov_b32_e32 v141, 1.0
	v_mov_b32_e32 v147, 1.0
	v_mov_b32_e32 v144, 1.0
	v_mov_b32_e32 v142, 1.0
	v_mov_b32_e32 v145, 1.0
	v_mov_b32_e32 v143, 1.0
	s_and_saveexec_b64 s[0:1], s[34:35]
	v_lshlrev_b32_e32 v140, 16, v26
	v_and_b32_e32 v146, 0xffff0000, v26
	v_lshlrev_b32_e32 v141, 16, v27
	v_and_b32_e32 v147, 0xffff0000, v27
	v_lshlrev_b32_e32 v144, 16, v28
	v_and_b32_e32 v142, 0xffff0000, v28
	v_lshlrev_b32_e32 v145, 16, v29
	v_and_b32_e32 v143, 0xffff0000, v29
	s_or_b64 exec, exec, s[0:1]
	s_or_b32 s0, s8, 14
	s_ashr_i32 s1, s0, 31
	s_lshl_b64 s[12:13], s[0:1], 11
	s_add_u32 s20, s29, s12
	s_addc_u32 s21, s30, s13
	global_load_dwordx4 v[106:109], v0, s[20:21] nt
	s_and_saveexec_b64 s[22:23], s[38:39]
	s_xor_b64 s[22:23], exec, s[22:23]
	s_cbranch_execz .LBB0_779
	v_mad_i64_i32 v[34:35], s[44:45], s0, v252, v[124:125]
	v_mad_i64_i32 v[38:39], s[44:45], s0, v252, v[122:123]
	v_mad_i64_i32 v[42:43], s[44:45], s0, v252, v[120:121]
	s_lshl_b64 s[44:45], s[0:1], 5
	s_add_u32 s44, s26, s44
	s_addc_u32 s45, s27, s45
	v_lshl_add_u64 v[180:181], v[118:119], 2, s[44:45]
	v_add_co_u32_e32 v168, vcc, 0x100000, v180
	flat_load_dword v167, v[180:181]
	s_nop 0
	v_addc_co_u32_e32 v169, vcc, 0, v181, vcc
	flat_load_dword v168, v[168:169]
	v_add_co_u32_e32 v180, vcc, 0x200000, v180
	global_load_dwordx4 v[34:37], v[34:35], off nt
	s_nop 0
	v_addc_co_u32_e32 v181, vcc, 0, v181, vcc
	global_load_dwordx4 v[38:41], v[38:39], off nt
	s_nop 0
	global_load_dwordx4 v[42:45], v[42:43], off nt
	s_nop 0
	flat_load_dword v169, v[180:181]
	s_andn2_saveexec_b64 s[22:23], s[22:23]
	s_cbranch_execnz .LBB0_780

; __device__ __forceinline__ unsigned pk2(float lo, float hi) { return f2bf(lo) | (f2bf(hi) << 16); }
; __device__ __forceinline__ void unpack8(const v4u w, float* f) { f[0] = bflo(w.x); f[1] = bfhi(w.x); f[2] = bflo(w.y); f[3] = bfhi(w.y); f[4] = bflo(w.z); f[5] = bfhi(w.z); f[6] = bflo(w.w); f[7] = bfhi(w.w); }
; __device__ __forceinline__ void norm_compute(const NormRow& R, int lane, v4u& ya, v4u& yc) {
;     ...
;     const float r_moba = 1.0f / sqrtf(s_moba * (1.0f / 256.0f) + EPS), r_fox = 1.0f / sqrtf(s_fox * (1.0f / 384.0f) + EPS), r_dil = 1.0f / sqrtf(s_dil * (1.0f / 384.0f) + EPS);
;     float ga[8], gc[8];
; #pragma unroll
;     for (int e = 0; e < 8; ++e) { ga[e] = 1.f; gc[e] = 1.f; }
;     if (lane >= 32) unpack8(R.ga, ga);
;     if (lane < 16) unpack8(R.gc, gc);
;     const float ra = lane < 32 ? r_moba : r_fox, rc = lane < 16 ? r_fox : r_dil;
;     ya.x = pk2(fa[0] * ra * ga[0], fa[1] * ra * ga[1]); ya.y = pk2(fa[2] * ra * ga[2], fa[3] * ra * ga[3]); ya.z = pk2(fa[4] * ra * ga[4], fa[5] * ra * ga[5]); ya.w = pk2(fa[6] * ra * ga[6], fa[7] * ra * ga[7]);
;     yc.x = pk2(fc[0] * rc * gc[0], fc[1] * rc * gc[1]); yc.y = pk2(fc[2] * rc * gc[2], fc[3] * rc * gc[3]); yc.z = pk2(fc[4] * rc * gc[4], fc[5] * rc * gc[5]); yc.w = pk2(fc[6] * rc * gc[6], fc[7] * rc * gc[7]);
; }
.LBB0_227:
	s_or_b64 exec, exec, s[20:21]
	s_waitcnt lgkmcnt(0)
	v_add_f32_e32 v178, v178, v179
	v_fmamk_f32 v178, v178, 0x3b2aaaab, v215
	v_mul_f32_e32 v179, 0x4f800000, v178
	v_cmp_gt_f32_e32 vcc, s3, v178
	v_add_f32_e32 v176, v176, v177
	v_fmamk_f32 v176, v176, 0x3b2aaaab, v215
	v_cndmask_b32_e32 v178, v178, v179, vcc
	v_sqrt_f32_e32 v179, v178
	v_mul_f32_e32 v177, 0x4f800000, v176
	v_add_f32_e32 v156, v156, v157
	v_fmamk_f32 v156, v156, 0x3b800000, v215
	v_add_u32_e32 v180, -1, v179
	v_fma_f32 v182, -v180, v179, v178
	v_add_u32_e32 v181, 1, v179
	v_cmp_ge_f32_e64 s[0:1], 0, v182
	v_mul_f32_e32 v157, 0x4f800000, v156
	s_nop 0
	v_cndmask_b32_e64 v180, v179, v180, s[0:1]
	v_fma_f32 v179, -v181, v179, v178
	v_cmp_lt_f32_e64 s[0:1], 0, v179
	s_nop 1
	v_cndmask_b32_e64 v179, v180, v181, s[0:1]
	v_cmp_gt_f32_e64 s[0:1], s3, v176
	v_mul_f32_e32 v180, 0x37800000, v179
	v_cndmask_b32_e32 v179, v179, v180, vcc
	v_cndmask_b32_e64 v176, v176, v177, s[0:1]
	v_sqrt_f32_e32 v177, v176
	v_cmp_class_f32_e32 vcc, v178, v216
	s_nop 1
	v_cndmask_b32_e32 v178, v179, v178, vcc
	v_add_u32_e32 v179, -1, v177
	v_fma_f32 v180, -v179, v177, v176
	v_cmp_ge_f32_e32 vcc, 0, v180
	v_add_u32_e32 v180, 1, v177
	s_nop 0
	v_cndmask_b32_e32 v179, v177, v179, vcc
	v_fma_f32 v177, -v180, v177, v176
	v_cmp_lt_f32_e32 vcc, 0, v177
	s_nop 1
	v_cndmask_b32_e32 v177, v179, v180, vcc
	v_cmp_gt_f32_e32 vcc, s3, v156
	v_mul_f32_e32 v179, 0x37800000, v177
	v_cndmask_b32_e64 v177, v177, v179, s[0:1]
	v_cndmask_b32_e32 v156, v156, v157, vcc
	v_sqrt_f32_e32 v157, v156
	v_cmp_class_f32_e64 s[0:1], v176, v216
	s_nop 1
	v_cndmask_b32_e64 v176, v177, v176, s[0:1]
	v_add_u32_e32 v177, -1, v157
	v_fma_f32 v179, -v177, v157, v156
	v_cmp_ge_f32_e64 s[0:1], 0, v179
	v_add_u32_e32 v179, 1, v157
	s_nop 0
	v_cndmask_b32_e64 v177, v157, v177, s[0:1]
	v_fma_f32 v157, -v179, v157, v156
	v_cmp_lt_f32_e64 s[0:1], 0, v157
	s_nop 1
	v_cndmask_b32_e64 v157, v177, v179, s[0:1]
	v_div_scale_f32 v179, s[0:1], v178, v178, 1.0
	v_rcp_f32_e32 v180, v179
	v_mul_f32_e32 v177, 0x37800000, v157
	v_cndmask_b32_e32 v157, v157, v177, vcc
	v_cmp_class_f32_e32 vcc, v156, v216
	s_nop 1
	v_cndmask_b32_e32 v156, v157, v156, vcc
	v_fma_f32 v157, -v179, v180, 1.0
	v_fmac_f32_e32 v180, v157, v180
	v_div_scale_f32 v157, vcc, 1.0, v178, 1.0
	v_mul_f32_e32 v177, v157, v180
	v_fma_f32 v181, -v179, v177, v157
	v_fmac_f32_e32 v177, v181, v180
	v_fma_f32 v157, -v179, v177, v157
	v_div_scale_f32 v179, s[0:1], v176, v176, 1.0
	v_rcp_f32_e32 v181, v179
	v_div_fmas_f32 v157, v157, v180, v177
	v_div_fixup_f32 v157, v157, v178, 1.0
	v_fma_f32 v177, -v179, v181, 1.0
	v_fmac_f32_e32 v181, v177, v181
	v_div_scale_f32 v177, vcc, 1.0, v176, 1.0
	v_mul_f32_e32 v178, v177, v181
	v_fma_f32 v180, -v179, v178, v177
	v_fmac_f32_e32 v178, v180, v181
	v_fma_f32 v177, -v179, v178, v177
	v_div_scale_f32 v179, s[0:1], v156, v156, 1.0
	v_rcp_f32_e32 v180, v179
	v_div_fmas_f32 v177, v177, v181, v178
	v_div_fixup_f32 v176, v177, v176, 1.0
	s_movk_i32 s1, 0x7fff
	v_fma_f32 v177, -v179, v180, 1.0
	v_fmac_f32_e32 v180, v177, v180
	v_div_scale_f32 v177, vcc, 1.0, v156, 1.0
	v_mul_f32_e32 v178, v177, v180
	v_fma_f32 v181, -v179, v178, v177
	v_fmac_f32_e32 v178, v181, v180
	v_fma_f32 v177, -v179, v178, v177
	v_div_fmas_f32 v177, v177, v180, v178
	v_div_fixup_f32 v156, v177, v156, 1.0
	v_cndmask_b32_e64 v156, v176, v156, s[40:41]
	v_mul_f32_e32 v110, v156, v110
	v_mul_f32_e32 v111, v156, v111
	v_mul_f32_e32 v112, v156, v112
	v_mul_f32_e32 v113, v156, v113
	v_mul_f32_e32 v138, v156, v138
	v_mul_f32_e32 v139, v156, v139
	v_mul_f32_e32 v110, v110, v150
	v_mul_f32_e32 v111, v111, v151
	v_mul_f32_e32 v136, v156, v136
	v_mul_f32_e32 v137, v156, v137
	v_mul_f32_e32 v112, v112, v148
	v_mul_f32_e32 v113, v113, v149
	v_mul_f32_e32 v138, v138, v154
	v_mul_f32_e32 v139, v139, v155
	v_mul_f32_e32 v136, v136, v152
	v_mul_f32_e32 v137, v137, v153
	v_bfe_u32 v148, v113, 16, 1
	v_bfe_u32 v149, v112, 16, 1
	v_bfe_u32 v150, v111, 16, 1
	v_bfe_u32 v151, v110, 16, 1
	v_cndmask_b32_e64 v176, v157, v176, s[34:35]
	v_add3_u32 v110, v110, v151, s1
	v_add3_u32 v111, v111, v150, s1
	v_add3_u32 v112, v112, v149, s1
	v_add3_u32 v113, v113, v148, s1
	v_bfe_u32 v148, v138, 16, 1
	v_bfe_u32 v149, v139, 16, 1
	v_bfe_u32 v150, v136, 16, 1
	v_bfe_u32 v151, v137, 16, 1
	v_add3_u32 v137, v137, v151, s1
	v_add3_u32 v136, v136, v150, s1
	v_add3_u32 v139, v139, v149, s1
	v_add3_u32 v138, v138, v148, s1
	v_mul_f32_e32 v128, v128, v176
	v_mul_f32_e32 v129, v129, v176
	v_mul_f32_e32 v130, v130, v176
	v_mul_f32_e32 v131, v131, v176
	v_lshrrev_b32_e32 v138, 16, v138
	v_lshrrev_b32_e32 v139, 16, v139
	v_lshrrev_b32_e32 v136, 16, v136
	v_lshrrev_b32_e32 v137, 16, v137
	s_mov_b32 s0, 0xffff0000
	v_mul_f32_e32 v134, v134, v176
	v_mul_f32_e32 v135, v135, v176
	v_mul_f32_e32 v128, v128, v146
	v_mul_f32_e32 v129, v129, v147
	v_mul_f32_e32 v132, v132, v176
	v_mul_f32_e32 v133, v133, v176
	v_mul_f32_e32 v130, v130, v142
	v_mul_f32_e32 v131, v131, v143
	v_and_or_b32 v113, v113, s0, v137
	v_and_or_b32 v112, v112, s0, v136
	v_and_or_b32 v111, v111, s0, v139
	v_and_or_b32 v110, v110, s0, v138
	v_mul_f32_e32 v134, v134, v140
	v_mul_f32_e32 v135, v135, v141
	v_mul_f32_e32 v132, v132, v144
	v_mul_f32_e32 v133, v133, v145
	v_bfe_u32 v136, v131, 16, 1
	v_bfe_u32 v137, v130, 16, 1
	v_bfe_u32 v138, v129, 16, 1
	v_bfe_u32 v139, v128, 16, 1
	v_add3_u32 v128, v128, v139, s1
	v_add3_u32 v129, v129, v138, s1
	v_add3_u32 v130, v130, v137, s1
	v_add3_u32 v131, v131, v136, s1
	v_bfe_u32 v136, v134, 16, 1
	v_bfe_u32 v137, v135, 16, 1
	v_bfe_u32 v138, v132, 16, 1
	v_bfe_u32 v139, v133, 16, 1
	v_add3_u32 v133, v133, v139, s1
	v_add3_u32 v132, v132, v138, s1
	v_add3_u32 v135, v135, v137, s1
	v_add3_u32 v134, v134, v136, s1
	v_lshrrev_b32_e32 v134, 16, v134
	v_lshrrev_b32_e32 v135, 16, v135
	v_lshrrev_b32_e32 v132, 16, v132
	v_lshrrev_b32_e32 v133, 16, v133
	v_and_or_b32 v131, v131, s0, v133
	v_and_or_b32 v130, v130, s0, v132
	v_and_or_b32 v129, v129, s0, v135
	v_and_or_b32 v128, v128, s0, v134
	s_add_u32 s0, s24, s14
	s_addc_u32 s1, s25, s15
	global_store_dwordx4 v0, v[110:113], s[0:1]
	global_store_dwordx4 v0, v[128:131], s[0:1] offset:1024
	s_and_saveexec_b64 s[0:1], s[38:39]
	s_xor_b64 s[0:1], exec, s[0:1]
	s_cbranch_execz .LBB0_229
; __device__ __forceinline__ void unpack8(const v4u w, float* f) { f[0] = bflo(w.x); f[1] = bfhi(w.x); f[2] = bflo(w.y); f[3] = bfhi(w.y); f[4] = bflo(w.z); f[5] = bfhi(w.z); f[6] = bflo(w.w); f[7] = bfhi(w.w); }
; __device__ __forceinline__ void norm_compute(const NormRow& R, int lane, v4u& ya, v4u& yc) {
;     ...
;     else { float f0[8], f1[8], f2[8]; unpack8(R.d0, f0); unpack8(R.d1, f1); unpack8(R.d2, f2);
;         const float inv = 1.0f / (R.l0 + R.l1 + R.l2);
; #pragma unroll
;         for (int e = 0; e < 8; ++e) fc[e] = (f0[e] + f1[e] + f2[e]) * inv; }
	v_add_f32_e32 v111, v165, v163
	v_add_f32_e32 v128, v166, v111
	v_div_scale_f32 v129, s[14:15], v128, v128, 1.0
	v_rcp_f32_e32 v130, v129
	v_lshlrev_b32_e32 v134, 16, v18
	v_and_b32_e32 v135, 0xffff0000, v18
	v_lshlrev_b32_e32 v138, 16, v20
	v_fma_f32 v131, -v129, v130, 1.0
	v_fmac_f32_e32 v130, v131, v130
	v_div_scale_f32 v131, vcc, 1.0, v128, 1.0
	v_mul_f32_e32 v132, v131, v130
	v_fma_f32 v133, -v129, v132, v131
	v_fmac_f32_e32 v132, v133, v130
	v_fma_f32 v129, -v129, v132, v131
	v_div_fmas_f32 v129, v129, v130, v132
	v_div_fixup_f32 v130, v129, v128, 1.0
	v_lshlrev_b32_e32 v128, 16, v10
	v_and_b32_e32 v129, 0xffff0000, v10
	v_lshlrev_b32_e32 v132, 16, v14
	v_and_b32_e32 v133, 0xffff0000, v14
	v_add_f32_e32 v128, v132, v128
	v_add_f32_e32 v129, v133, v129
	v_lshlrev_b32_e32 v132, 16, v15
	v_add_f32_e32 v128, v128, v134
	v_add_f32_e32 v129, v129, v135
	v_and_b32_e32 v133, 0xffff0000, v15
	v_mul_f32_e32 v136, v130, v128
	v_mul_f32_e32 v137, v130, v129
	v_lshlrev_b32_e32 v128, 16, v11
	v_and_b32_e32 v129, 0xffff0000, v11
	v_lshlrev_b32_e32 v134, 16, v19
	v_and_b32_e32 v135, 0xffff0000, v19
	v_add_f32_e32 v128, v132, v128
	v_add_f32_e32 v129, v133, v129
	v_lshlrev_b32_e32 v132, 16, v12
	v_add_f32_e32 v128, v128, v134
	v_add_f32_e32 v129, v129, v135
	v_and_b32_e32 v133, 0xffff0000, v12
	v_lshlrev_b32_e32 v134, 16, v16
	v_and_b32_e32 v135, 0xffff0000, v16
	v_and_b32_e32 v139, 0xffff0000, v20
	v_add_f32_e32 v132, v134, v132
	v_add_f32_e32 v133, v135, v133
	v_lshlrev_b32_e32 v110, 16, v13
	v_lshlrev_b32_e32 v112, 16, v17
	v_and_b32_e32 v111, 0xffff0000, v13
	v_and_b32_e32 v113, 0xffff0000, v17
	v_add_f32_e32 v132, v132, v138
	v_add_f32_e32 v133, v133, v139
	v_add_f32_e32 v110, v112, v110
	v_add_f32_e32 v111, v113, v111
	v_mul_f32_e32 v134, v130, v132
	v_mul_f32_e32 v135, v130, v133
	v_lshlrev_b32_e32 v132, 16, v21
	v_and_b32_e32 v133, 0xffff0000, v21
	v_add_f32_e32 v110, v110, v132
	v_add_f32_e32 v111, v111, v133
	v_mul_f32_e32 v128, v130, v128
	v_mul_f32_e32 v129, v130, v129
	v_mul_f32_e32 v131, v130, v111
	v_mul_f32_e32 v130, v130, v110
	v_mov_b32_e32 v133, v130
	v_mov_b32_e32 v130, v135
	v_mov_b32_e32 v132, v134
	v_mov_b32_e32 v135, v128
	v_mov_b32_e32 v128, v137
	v_mov_b32_e32 v134, v136
; #define GAS __attribute__((address_space(1)))
; __device__ __forceinline__ void unpack8(const v4u w, float* f) { f[0] = bflo(w.x); f[1] = bfhi(w.x); f[2] = bflo(w.y); f[3] = bfhi(w.y); f[4] = bflo(w.z); f[5] = bfhi(w.z); f[6] = bflo(w.w); f[7] = bfhi(w.w); }
; __device__ __forceinline__ void norm_load(NormRow& R, int m, int lane, const bf16* O, const bf16* GF, const bf16* OD, const float* LD) {
;     R.oa = __builtin_nontemporal_load((const GAS v4u*)(O + (size_t)m * DM + 8 * lane));
;     if (lane < 16) { R.oc = __builtin_nontemporal_load((const GAS v4u*)(O + (size_t)m * DM + 512 + 8 * lane)); R.gc = __builtin_nontemporal_load((const GAS v4u*)(GF + (size_t)m * 384 + 256 + 8 * lane)); }
;     else { const int dc = 8 * lane - 128, hd = dc >> 6;
;         R.d0 = __builtin_nontemporal_load((const GAS v4u*)(OD + (size_t)m * 384 + dc)); R.d1 = __builtin_nontemporal_load((const GAS v4u*)(OD + OD_BRANCH + (size_t)m * 384 + dc)); R.d2 = __builtin_nontemporal_load((const GAS v4u*)(OD + 2 * OD_BRANCH + (size_t)m * 384 + dc));
;         R.l0 = LD[(size_t)m * 8 + hd]; R.l1 = LD[LD_BRANCH + (size_t)m * 8 + hd]; R.l2 = LD[2 * LD_BRANCH + (size_t)m * 8 + hd]; }
;     if (lane >= 32) R.ga = __builtin_nontemporal_load((const GAS v4u*)(GF + (size_t)m * 384 + 8 * lane - 256));
; __device__ __forceinline__ void norm_compute(const NormRow& R, int lane, v4u& ya, v4u& yc) {
;     ...
;     float sa = 0.f, sc = 0.f;
; #pragma unroll
;     for (int e = 0; e < 8; ++e) { sa += fa[e] * fa[e]; sc += fc[e] * fc[e]; }
;     const float s_moba = wave_sum(lane < 32 ? sa : 0.f), s_fox = wave_sum((lane >= 32 ? sa : 0.f) + (lane < 16 ? sc : 0.f)), s_dil = wave_sum(lane >= 16 ? sc : 0.f);
;     const float r_moba = 1.0f / sqrtf(s_moba * (1.0f / 256.0f) + EPS), r_fox = 1.0f / sqrtf(s_fox * (1.0f / 384.0f) + EPS), r_dil = 1.0f / sqrtf(s_dil * (1.0f / 384.0f) + EPS);
;     float ga[8], gc[8];
; #pragma unroll
;     for (int e = 0; e < 8; ++e) { ga[e] = 1.f; gc[e] = 1.f; }
;     if (lane >= 32) unpack8(R.ga, ga);
;     if (lane < 16) unpack8(R.gc, gc);
.LBB0_229:
	s_andn2_saveexec_b64 s[0:1], s[0:1]
	v_lshlrev_b32_e32 v134, 16, v22
	v_and_b32_e32 v128, 0xffff0000, v22
	v_lshlrev_b32_e32 v135, 16, v23
	v_and_b32_e32 v129, 0xffff0000, v23
	v_lshlrev_b32_e32 v132, 16, v24
	v_and_b32_e32 v130, 0xffff0000, v24
	v_lshlrev_b32_e32 v133, 16, v25
	v_and_b32_e32 v131, 0xffff0000, v25
	s_or_b64 exec, exec, s[0:1]
	v_lshlrev_b32_e32 v139, 16, v115
	v_lshlrev_b32_e32 v138, 16, v114
	v_and_b32_e32 v115, 0xffff0000, v115
	v_and_b32_e32 v114, 0xffff0000, v114
	v_mul_f32_e32 v110, v138, v138
	v_mul_f32_e32 v111, v139, v139
	v_mul_f32_e32 v112, v114, v114
	v_mul_f32_e32 v113, v115, v115
	v_mul_f32_e32 v144, v128, v128
	v_fmac_f32_e32 v144, v134, v134
	v_add_f32_e32 v110, v110, v112
	v_lshlrev_b32_e32 v137, 16, v117
	v_lshlrev_b32_e32 v136, 16, v116
	v_fmac_f32_e32 v144, v135, v135
	v_add_f32_e32 v110, v111, v110
	v_and_b32_e32 v117, 0xffff0000, v117
	v_and_b32_e32 v116, 0xffff0000, v116
	v_fmac_f32_e32 v144, v129, v129
	v_mul_f32_e32 v140, v136, v136
	v_mul_f32_e32 v141, v137, v137
	v_add_f32_e32 v110, v113, v110
	v_fmac_f32_e32 v144, v132, v132
	v_mul_f32_e32 v142, v116, v116
	v_mul_f32_e32 v143, v117, v117
	v_add_f32_e32 v110, v140, v110
	v_fmac_f32_e32 v144, v130, v130
	v_add_f32_e32 v110, v142, v110
	v_fmac_f32_e32 v144, v133, v133
	v_add_f32_e32 v110, v141, v110
	v_add_f32_e32 v110, v143, v110
	v_fmac_f32_e32 v144, v131, v131
	v_cndmask_b32_e64 v111, 0, v110, s[40:41]
	v_cndmask_b32_e64 v110, 0, v110, s[36:37]
	v_cndmask_b32_e64 v113, 0, v144, s[34:35]
	v_add_f32_e32 v110, v110, v113
	v_cndmask_b32_e64 v140, 0, v144, s[42:43]
	ds_bpermute_b32 v112, v164, v111
	ds_bpermute_b32 v113, v164, v110
	ds_bpermute_b32 v141, v164, v140
	v_mov_b32_e32 v154, 1.0
	v_mov_b32_e32 v150, 1.0
	s_waitcnt lgkmcnt(0)
	v_add_f32_e32 v111, v111, v112
	v_add_f32_e32 v110, v110, v113
	v_add_f32_e32 v140, v140, v141
	ds_bpermute_b32 v112, v162, v111
	ds_bpermute_b32 v113, v162, v110
	ds_bpermute_b32 v141, v162, v140
	v_mov_b32_e32 v155, 1.0
	v_mov_b32_e32 v151, 1.0
	s_waitcnt lgkmcnt(0)
	v_add_f32_e32 v111, v111, v112
	v_add_f32_e32 v110, v110, v113
	v_add_f32_e32 v140, v140, v141
	ds_bpermute_b32 v112, v161, v111
	ds_bpermute_b32 v113, v161, v110
	ds_bpermute_b32 v141, v161, v140
	v_mov_b32_e32 v152, 1.0
	v_mov_b32_e32 v148, 1.0
	s_waitcnt lgkmcnt(0)
	v_add_f32_e32 v111, v111, v112
	v_add_f32_e32 v110, v110, v113
	v_add_f32_e32 v140, v140, v141
	ds_bpermute_b32 v112, v160, v111
	ds_bpermute_b32 v113, v160, v110
	ds_bpermute_b32 v141, v160, v140
	v_mov_b32_e32 v153, 1.0
	v_mov_b32_e32 v149, 1.0
	s_waitcnt lgkmcnt(0)
	v_add_f32_e32 v111, v111, v112
	v_add_f32_e32 v110, v110, v113
	v_add_f32_e32 v140, v140, v141
	ds_bpermute_b32 v112, v159, v111
	ds_bpermute_b32 v113, v159, v110
	ds_bpermute_b32 v141, v159, v140
	s_waitcnt lgkmcnt(0)
	v_add_f32_e32 v156, v111, v112
	v_add_f32_e32 v176, v110, v113
	v_add_f32_e32 v178, v140, v141
	ds_bpermute_b32 v157, v158, v156
	ds_bpermute_b32 v177, v158, v176
	ds_bpermute_b32 v179, v158, v178
	v_mov_b32_e32 v140, 1.0
	s_and_saveexec_b64 s[0:1], s[36:37]
	v_lshlrev_b32_e32 v154, 16, v6
	v_and_b32_e32 v150, 0xffff0000, v6
	v_lshlrev_b32_e32 v155, 16, v7
	v_and_b32_e32 v151, 0xffff0000, v7
	v_lshlrev_b32_e32 v152, 16, v8
	v_and_b32_e32 v148, 0xffff0000, v8
	v_lshlrev_b32_e32 v153, 16, v9
	v_and_b32_e32 v149, 0xffff0000, v9
	s_or_b64 exec, exec, s[0:1]
	v_mov_b32_e32 v146, 1.0
	v_mov_b32_e32 v141, 1.0
	v_mov_b32_e32 v147, 1.0
	v_mov_b32_e32 v144, 1.0
	v_mov_b32_e32 v142, 1.0
	v_mov_b32_e32 v145, 1.0
	v_mov_b32_e32 v143, 1.0
	s_and_saveexec_b64 s[0:1], s[34:35]
	v_lshlrev_b32_e32 v140, 16, v2
	v_and_b32_e32 v146, 0xffff0000, v2
	v_lshlrev_b32_e32 v141, 16, v3
	v_and_b32_e32 v147, 0xffff0000, v3
	v_lshlrev_b32_e32 v144, 16, v4
	v_and_b32_e32 v142, 0xffff0000, v4
	v_lshlrev_b32_e32 v145, 16, v5
	v_and_b32_e32 v143, 0xffff0000, v5
	s_or_b64 exec, exec, s[0:1]
	s_or_b32 s0, s8, 15
	s_ashr_i32 s1, s0, 31
	s_lshl_b64 s[8:9], s[0:1], 11
	s_add_u32 s14, s29, s8
	s_addc_u32 s15, s30, s9
	global_load_dwordx4 v[110:113], v0, s[14:15] nt
	s_and_saveexec_b64 s[20:21], s[38:39]
	s_xor_b64 s[20:21], exec, s[20:21]
	s_cbranch_execz .LBB0_781
	v_mad_i64_i32 v[10:11], s[22:23], s0, v252, v[124:125]
	v_mad_i64_i32 v[14:15], s[22:23], s0, v252, v[122:123]
	v_mad_i64_i32 v[18:19], s[22:23], s0, v252, v[120:121]
	s_lshl_b64 s[22:23], s[0:1], 5
	s_add_u32 s22, s26, s22
	s_addc_u32 s23, s27, s23
	v_lshl_add_u64 v[118:119], v[118:119], 2, s[22:23]
	v_add_co_u32_e32 v120, vcc, 0x100000, v118
	flat_load_dword v163, v[118:119]
	s_nop 0
	v_addc_co_u32_e32 v121, vcc, 0, v119, vcc
	flat_load_dword v165, v[120:121]
	v_add_co_u32_e32 v118, vcc, 0x200000, v118
	global_load_dwordx4 v[10:13], v[10:11], off nt
	s_nop 0
	v_addc_co_u32_e32 v119, vcc, 0, v119, vcc
	global_load_dwordx4 v[14:17], v[14:15], off nt
	s_nop 0
	global_load_dwordx4 v[18:21], v[18:19], off nt
	s_nop 0
	flat_load_dword v166, v[118:119]
	s_andn2_saveexec_b64 s[20:21], s[20:21]
	s_cbranch_execnz .LBB0_782

; __device__ __forceinline__ unsigned pk2(float lo, float hi) { return f2bf(lo) | (f2bf(hi) << 16); }
; __device__ __forceinline__ void unpack8(const v4u w, float* f) { f[0] = bflo(w.x); f[1] = bfhi(w.x); f[2] = bflo(w.y); f[3] = bfhi(w.y); f[4] = bflo(w.z); f[5] = bfhi(w.z); f[6] = bflo(w.w); f[7] = bfhi(w.w); }
; __device__ __forceinline__ void norm_compute(const NormRow& R, int lane, v4u& ya, v4u& yc) {
;     ...
;     const float r_moba = 1.0f / sqrtf(s_moba * (1.0f / 256.0f) + EPS), r_fox = 1.0f / sqrtf(s_fox * (1.0f / 384.0f) + EPS), r_dil = 1.0f / sqrtf(s_dil * (1.0f / 384.0f) + EPS);
;     float ga[8], gc[8];
; #pragma unroll
;     for (int e = 0; e < 8; ++e) { ga[e] = 1.f; gc[e] = 1.f; }
;     if (lane >= 32) unpack8(R.ga, ga);
;     if (lane < 16) unpack8(R.gc, gc);
;     const float ra = lane < 32 ? r_moba : r_fox, rc = lane < 16 ? r_fox : r_dil;
;     ya.x = pk2(fa[0] * ra * ga[0], fa[1] * ra * ga[1]); ya.y = pk2(fa[2] * ra * ga[2], fa[3] * ra * ga[3]); ya.z = pk2(fa[4] * ra * ga[4], fa[5] * ra * ga[5]); ya.w = pk2(fa[6] * ra * ga[6], fa[7] * ra * ga[7]);
;     yc.x = pk2(fc[0] * rc * gc[0], fc[1] * rc * gc[1]); yc.y = pk2(fc[2] * rc * gc[2], fc[3] * rc * gc[3]); yc.z = pk2(fc[4] * rc * gc[4], fc[5] * rc * gc[5]); yc.w = pk2(fc[6] * rc * gc[6], fc[7] * rc * gc[7]);
; }
.LBB0_239:
	s_or_b64 exec, exec, s[6:7]
	s_waitcnt lgkmcnt(0)
	v_add_f32_e32 v118, v178, v179
	v_fmamk_f32 v118, v118, 0x3b2aaaab, v215
	v_mul_f32_e32 v119, 0x4f800000, v118
	v_cmp_gt_f32_e32 vcc, s3, v118
	s_nop 1
	v_cndmask_b32_e32 v118, v118, v119, vcc
	v_sqrt_f32_e32 v119, v118
	s_nop 0
	v_add_u32_e32 v120, -1, v119
	v_fma_f32 v122, -v120, v119, v118
	v_add_u32_e32 v121, 1, v119
	v_cmp_ge_f32_e64 s[0:1], 0, v122
	s_nop 1
	v_cndmask_b32_e64 v120, v119, v120, s[0:1]
	v_fma_f32 v119, -v121, v119, v118
	v_cmp_lt_f32_e64 s[0:1], 0, v119
	s_nop 1
	v_cndmask_b32_e64 v119, v120, v121, s[0:1]
	v_add_f32_e32 v121, v176, v177
	v_fmamk_f32 v121, v121, 0x3b2aaaab, v215
	v_mul_f32_e32 v122, 0x4f800000, v121
	v_cmp_gt_f32_e64 s[0:1], s3, v121
	v_mul_f32_e32 v120, 0x37800000, v119
	v_cndmask_b32_e32 v119, v119, v120, vcc
	v_cndmask_b32_e64 v121, v121, v122, s[0:1]
	v_sqrt_f32_e32 v122, v121
	v_cmp_class_f32_e32 vcc, v118, v216
	s_nop 1
	v_cndmask_b32_e32 v118, v119, v118, vcc
	v_add_u32_e32 v119, -1, v122
	v_fma_f32 v120, -v119, v122, v121
	v_cmp_ge_f32_e32 vcc, 0, v120
	v_add_u32_e32 v120, 1, v122
	s_nop 0
	v_cndmask_b32_e32 v119, v122, v119, vcc
	v_fma_f32 v122, -v120, v122, v121
	v_cmp_lt_f32_e32 vcc, 0, v122
	v_add_f32_e32 v122, v156, v157
	v_fmamk_f32 v122, v122, 0x3b800000, v215
	v_cndmask_b32_e32 v119, v119, v120, vcc
	v_mul_f32_e32 v123, 0x4f800000, v122
	v_cmp_gt_f32_e32 vcc, s3, v122
	v_mul_f32_e32 v120, 0x37800000, v119
	v_cndmask_b32_e64 v119, v119, v120, s[0:1]
	v_cndmask_b32_e32 v122, v122, v123, vcc
	v_sqrt_f32_e32 v123, v122
	v_cmp_class_f32_e64 s[0:1], v121, v216
	v_add_u32_e32 v120, -1, v123
	s_nop 0
	v_cndmask_b32_e64 v119, v119, v121, s[0:1]
	v_fma_f32 v121, -v120, v123, v122
	v_cmp_ge_f32_e64 s[0:1], 0, v121
	v_add_u32_e32 v121, 1, v123
	s_nop 0
	v_cndmask_b32_e64 v120, v123, v120, s[0:1]
	v_fma_f32 v123, -v121, v123, v122
	v_cmp_lt_f32_e64 s[0:1], 0, v123
	s_nop 1
	v_cndmask_b32_e64 v120, v120, v121, s[0:1]
	v_div_scale_f32 v123, s[0:1], v118, v118, 1.0
	v_rcp_f32_e32 v124, v123
	v_mul_f32_e32 v121, 0x37800000, v120
	v_cndmask_b32_e32 v120, v120, v121, vcc
	v_cmp_class_f32_e32 vcc, v122, v216
	v_fma_f32 v121, -v123, v124, 1.0
	v_fmac_f32_e32 v124, v121, v124
	v_cndmask_b32_e32 v120, v120, v122, vcc
	v_div_scale_f32 v121, vcc, 1.0, v118, 1.0
	v_mul_f32_e32 v122, v121, v124
	v_fma_f32 v125, -v123, v122, v121
	v_fmac_f32_e32 v122, v125, v124
	v_fma_f32 v121, -v123, v122, v121
	v_div_scale_f32 v123, s[0:1], v119, v119, 1.0
	v_rcp_f32_e32 v125, v123
	v_div_fmas_f32 v121, v121, v124, v122
	v_div_fixup_f32 v121, v121, v118, 1.0
	v_fma_f32 v118, -v123, v125, 1.0
	v_fmac_f32_e32 v125, v118, v125
	v_div_scale_f32 v118, vcc, 1.0, v119, 1.0
	v_mul_f32_e32 v122, v118, v125
	v_fma_f32 v124, -v123, v122, v118
	v_fmac_f32_e32 v122, v124, v125
	v_fma_f32 v118, -v123, v122, v118
	v_div_scale_f32 v123, s[0:1], v120, v120, 1.0
	v_rcp_f32_e32 v124, v123
	v_div_fmas_f32 v118, v118, v125, v122
	v_div_fixup_f32 v119, v118, v119, 1.0
	s_movk_i32 s1, 0x7fff
	v_fma_f32 v118, -v123, v124, 1.0
	v_fmac_f32_e32 v124, v118, v124
	v_div_scale_f32 v118, vcc, 1.0, v120, 1.0
	v_mul_f32_e32 v122, v118, v124
	v_fma_f32 v125, -v123, v122, v118
	v_fmac_f32_e32 v122, v125, v124
	v_fma_f32 v118, -v123, v122, v118
	v_div_fmas_f32 v118, v118, v124, v122
	v_div_fixup_f32 v118, v118, v120, 1.0
	v_cndmask_b32_e64 v118, v119, v118, s[40:41]
	v_mul_f32_e32 v114, v118, v114
	v_mul_f32_e32 v115, v118, v115
	v_mul_f32_e32 v116, v118, v116
	v_mul_f32_e32 v117, v118, v117
	v_mul_f32_e32 v122, v118, v138
	v_mul_f32_e32 v123, v118, v139
	v_mul_f32_e32 v114, v114, v150
	v_mul_f32_e32 v115, v115, v151
	v_mul_f32_e32 v124, v118, v136
	v_mul_f32_e32 v125, v118, v137
	v_mul_f32_e32 v116, v116, v148
	v_mul_f32_e32 v117, v117, v149
	v_cndmask_b32_e64 v120, v121, v119, s[34:35]
	v_mul_f32_e32 v122, v122, v154
	v_mul_f32_e32 v123, v123, v155
	v_mul_f32_e32 v124, v124, v152
	v_mul_f32_e32 v125, v125, v153
	v_bfe_u32 v118, v117, 16, 1
	v_bfe_u32 v119, v116, 16, 1
	v_bfe_u32 v121, v115, 16, 1
	v_bfe_u32 v126, v114, 16, 1
	v_add3_u32 v114, v114, v126, s1
	v_add3_u32 v115, v115, v121, s1
	v_add3_u32 v116, v116, v119, s1
	v_add3_u32 v117, v117, v118, s1
	v_bfe_u32 v118, v122, 16, 1
	v_bfe_u32 v119, v123, 16, 1
	v_bfe_u32 v121, v124, 16, 1
	v_bfe_u32 v126, v125, 16, 1
	v_add3_u32 v125, v125, v126, s1
	v_add3_u32 v121, v124, v121, s1
	v_add3_u32 v119, v123, v119, s1
	v_add3_u32 v118, v122, v118, s1
	v_lshrrev_b32_e32 v118, 16, v118
	v_lshrrev_b32_e32 v119, 16, v119
	v_lshrrev_b32_e32 v121, 16, v121
	v_lshrrev_b32_e32 v122, 16, v125
	s_mov_b32 s0, 0xffff0000
	v_and_or_b32 v117, v117, s0, v122
	v_and_or_b32 v116, v116, s0, v121
	v_and_or_b32 v115, v115, s0, v119
	v_and_or_b32 v114, v114, s0, v118
	v_mul_f32_e32 v118, v134, v120
	v_mul_f32_e32 v119, v135, v120
	v_mul_f32_e32 v122, v128, v120
	v_mul_f32_e32 v123, v129, v120
	v_mul_f32_e32 v124, v132, v120
	v_mul_f32_e32 v125, v133, v120
	v_mul_f32_e32 v121, v131, v120
	v_mul_f32_e32 v120, v130, v120
	v_mul_f32_e32 v122, v122, v146
	v_mul_f32_e32 v123, v123, v147
	v_mul_f32_e32 v120, v120, v142
	v_mul_f32_e32 v121, v121, v143
	v_mul_f32_e32 v118, v118, v140
	v_mul_f32_e32 v119, v119, v141
	v_mul_f32_e32 v124, v124, v144
	v_mul_f32_e32 v125, v125, v145
	v_bfe_u32 v126, v121, 16, 1
	v_bfe_u32 v127, v120, 16, 1
	v_bfe_u32 v128, v123, 16, 1
	v_bfe_u32 v129, v122, 16, 1
	v_add3_u32 v122, v122, v129, s1
	v_add3_u32 v123, v123, v128, s1
	v_add3_u32 v120, v120, v127, s1
	v_add3_u32 v121, v121, v126, s1
	v_bfe_u32 v126, v118, 16, 1
	v_bfe_u32 v127, v119, 16, 1
	v_bfe_u32 v128, v124, 16, 1
	v_bfe_u32 v129, v125, 16, 1
	v_add3_u32 v125, v125, v129, s1
	v_add3_u32 v124, v124, v128, s1
	v_add3_u32 v119, v119, v127, s1
	v_add3_u32 v118, v118, v126, s1
	v_lshrrev_b32_e32 v118, 16, v118
	v_lshrrev_b32_e32 v119, 16, v119
	v_lshrrev_b32_e32 v124, 16, v124
	v_lshrrev_b32_e32 v125, 16, v125
	v_and_or_b32 v121, v121, s0, v125
	v_and_or_b32 v120, v120, s0, v124
	v_and_or_b32 v119, v123, s0, v119
	v_and_or_b32 v118, v122, s0, v118
	s_add_u32 s0, s24, s16
	s_addc_u32 s1, s25, s17
	global_store_dwordx4 v0, v[114:117], s[0:1]
	global_store_dwordx4 v0, v[118:121], s[0:1] offset:1024
	s_and_saveexec_b64 s[0:1], s[38:39]
	s_xor_b64 s[0:1], exec, s[0:1]
	s_cbranch_execz .LBB0_241
; __device__ __forceinline__ void unpack8(const v4u w, float* f) { f[0] = bflo(w.x); f[1] = bfhi(w.x); f[2] = bflo(w.y); f[3] = bfhi(w.y); f[4] = bflo(w.z); f[5] = bfhi(w.z); f[6] = bflo(w.w); f[7] = bfhi(w.w); }
; __device__ __forceinline__ void norm_compute(const NormRow& R, int lane, v4u& ya, v4u& yc) {
;     ...
;     else { float f0[8], f1[8], f2[8]; unpack8(R.d0, f0); unpack8(R.d1, f1); unpack8(R.d2, f2);
;         const float inv = 1.0f / (R.l0 + R.l1 + R.l2);
; #pragma unroll
;         for (int e = 0; e < 8; ++e) fc[e] = (f0[e] + f1[e] + f2[e]) * inv; }
	s_waitcnt vmcnt(0)
	v_add_f32_e32 v95, v173, v174
	v_add_f32_e32 v114, v95, v175
	v_div_scale_f32 v115, s[6:7], v114, v114, 1.0
	v_rcp_f32_e32 v116, v115
	v_lshlrev_b32_e32 v94, 16, v85
	v_and_b32_e32 v95, 0xffff0000, v85
	v_lshlrev_b32_e32 v96, 16, v89
	v_fma_f32 v85, -v115, v116, 1.0
	v_fmac_f32_e32 v116, v85, v116
	v_div_scale_f32 v85, vcc, 1.0, v114, 1.0
	v_and_b32_e32 v97, 0xffff0000, v89
	v_mul_f32_e32 v89, v85, v116
	v_fma_f32 v117, -v115, v89, v85
	v_fmac_f32_e32 v89, v117, v116
	v_fma_f32 v85, -v115, v89, v85
	v_div_fmas_f32 v85, v85, v116, v89
	v_div_fixup_f32 v116, v85, v114, 1.0
	v_lshlrev_b32_e32 v114, 16, v82
	v_and_b32_e32 v115, 0xffff0000, v82
	v_lshlrev_b32_e32 v118, 16, v86
	v_and_b32_e32 v119, 0xffff0000, v86
	v_lshlrev_b32_e32 v82, 16, v83
	v_and_b32_e32 v83, 0xffff0000, v83
	v_lshlrev_b32_e32 v86, 16, v87
	v_and_b32_e32 v87, 0xffff0000, v87
	v_lshlrev_b32_e32 v120, 16, v90
	v_and_b32_e32 v121, 0xffff0000, v90
	v_add_f32_e32 v114, v118, v114
	v_add_f32_e32 v115, v119, v115
	v_lshlrev_b32_e32 v90, 16, v91
	v_and_b32_e32 v91, 0xffff0000, v91
	v_add_f32_e32 v82, v86, v82
	v_add_f32_e32 v83, v87, v83
	v_add_f32_e32 v114, v114, v120
	v_add_f32_e32 v115, v115, v121
	v_add_f32_e32 v82, v82, v90
	v_add_f32_e32 v83, v83, v91
	v_mul_f32_e32 v122, v114, v116
	v_mul_f32_e32 v123, v115, v116
	v_mul_f32_e32 v114, v82, v116
	v_mul_f32_e32 v115, v83, v116
	v_lshlrev_b32_e32 v82, 16, v84
	v_and_b32_e32 v83, 0xffff0000, v84
	v_lshlrev_b32_e32 v84, 16, v88
	v_and_b32_e32 v85, 0xffff0000, v88
	v_lshlrev_b32_e32 v86, 16, v92
	v_and_b32_e32 v87, 0xffff0000, v92
	v_add_f32_e32 v82, v84, v82
	v_add_f32_e32 v83, v85, v83
	v_lshlrev_b32_e32 v84, 16, v93
	v_add_f32_e32 v82, v82, v86
	v_add_f32_e32 v83, v83, v87
	v_and_b32_e32 v85, 0xffff0000, v93
	v_add_f32_e32 v86, v96, v94
	v_add_f32_e32 v87, v97, v95
	v_mul_f32_e32 v82, v82, v116
	v_mul_f32_e32 v83, v83, v116
	v_add_f32_e32 v84, v86, v84
	v_add_f32_e32 v85, v87, v85
	v_mov_b32_e32 v118, v82
	v_mul_f32_e32 v117, v85, v116
	v_mul_f32_e32 v116, v84, v116
	v_mov_b32_e32 v121, v114
	v_mov_b32_e32 v119, v116
	v_mov_b32_e32 v116, v83
	v_mov_b32_e32 v114, v123
	v_mov_b32_e32 v120, v122

; __device__ __forceinline__ void unpack8(const v4u w, float* f) { f[0] = bflo(w.x); f[1] = bfhi(w.x); f[2] = bflo(w.y); f[3] = bfhi(w.y); f[4] = bflo(w.z); f[5] = bfhi(w.z); f[6] = bflo(w.w); f[7] = bfhi(w.w); }
; __device__ __forceinline__ void norm_compute(const NormRow& R, int lane, v4u& ya, v4u& yc) {
;     ...
;     float sa = 0.f, sc = 0.f;
; #pragma unroll
;     for (int e = 0; e < 8; ++e) { sa += fa[e] * fa[e]; sc += fc[e] * fc[e]; }
;     const float s_moba = wave_sum(lane < 32 ? sa : 0.f), s_fox = wave_sum((lane >= 32 ? sa : 0.f) + (lane < 16 ? sc : 0.f)), s_dil = wave_sum(lane >= 16 ? sc : 0.f);
;     const float r_moba = 1.0f / sqrtf(s_moba * (1.0f / 256.0f) + EPS), r_fox = 1.0f / sqrtf(s_fox * (1.0f / 384.0f) + EPS), r_dil = 1.0f / sqrtf(s_dil * (1.0f / 384.0f) + EPS);
;     float ga[8], gc[8];
; #pragma unroll
;     for (int e = 0; e < 8; ++e) { ga[e] = 1.f; gc[e] = 1.f; }
;     if (lane >= 32) unpack8(R.ga, ga);
;     if (lane < 16) unpack8(R.gc, gc);
;     const float ra = lane < 32 ? r_moba : r_fox, rc = lane < 16 ? r_fox : r_dil;
.LBB0_243:
	s_or_b64 exec, exec, s[0:1]
	s_waitcnt vmcnt(0)
	v_lshlrev_b32_e32 v85, 16, v99
	v_lshlrev_b32_e32 v84, 16, v98
	v_and_b32_e32 v87, 0xffff0000, v99
	v_and_b32_e32 v86, 0xffff0000, v98
	v_mul_f32_e32 v90, v84, v84
	v_mul_f32_e32 v91, v85, v85
	v_mul_f32_e32 v92, v86, v86
	v_mul_f32_e32 v93, v87, v87
	v_mul_f32_e32 v98, v114, v114
	v_fmac_f32_e32 v98, v120, v120
	v_add_f32_e32 v90, v90, v92
	v_lshlrev_b32_e32 v83, 16, v101
	v_lshlrev_b32_e32 v82, 16, v100
	v_fmac_f32_e32 v98, v121, v121
	v_add_f32_e32 v90, v91, v90
	v_and_b32_e32 v89, 0xffff0000, v101
	v_and_b32_e32 v88, 0xffff0000, v100
	v_fmac_f32_e32 v98, v115, v115
	v_mul_f32_e32 v94, v82, v82
	v_mul_f32_e32 v95, v83, v83
	v_add_f32_e32 v90, v93, v90
	v_fmac_f32_e32 v98, v118, v118
	v_mul_f32_e32 v96, v88, v88
	v_mul_f32_e32 v97, v89, v89
	v_add_f32_e32 v90, v94, v90
	v_fmac_f32_e32 v98, v116, v116
	v_add_f32_e32 v90, v96, v90
	v_fmac_f32_e32 v98, v119, v119
	v_add_f32_e32 v90, v95, v90
	v_add_f32_e32 v90, v97, v90
	v_fmac_f32_e32 v98, v117, v117
	v_cndmask_b32_e64 v91, 0, v90, s[40:41]
	v_cndmask_b32_e64 v90, 0, v90, s[36:37]
	v_cndmask_b32_e64 v93, 0, v98, s[34:35]
	v_add_f32_e32 v90, v90, v93
	v_cndmask_b32_e64 v94, 0, v98, s[42:43]
	ds_bpermute_b32 v92, v164, v91
	ds_bpermute_b32 v93, v164, v90
	ds_bpermute_b32 v95, v164, v94
	v_mov_b32_e32 v98, 1.0
	v_mov_b32_e32 v96, 1.0
	s_waitcnt lgkmcnt(2)
	v_add_f32_e32 v91, v91, v92
	s_waitcnt lgkmcnt(1)
	v_add_f32_e32 v90, v90, v93
	s_waitcnt lgkmcnt(0)
	v_add_f32_e32 v94, v94, v95
	ds_bpermute_b32 v92, v162, v91
	ds_bpermute_b32 v93, v162, v90
	ds_bpermute_b32 v95, v162, v94
	v_mov_b32_e32 v97, 1.0
	s_waitcnt lgkmcnt(2)
	v_add_f32_e32 v91, v91, v92
	s_waitcnt lgkmcnt(1)
	v_add_f32_e32 v90, v90, v93
	s_waitcnt lgkmcnt(0)
	v_add_f32_e32 v94, v94, v95
	ds_bpermute_b32 v92, v161, v91
	ds_bpermute_b32 v93, v161, v90
	ds_bpermute_b32 v95, v161, v94
	s_waitcnt lgkmcnt(2)
	v_add_f32_e32 v91, v91, v92
	s_waitcnt lgkmcnt(1)
	v_add_f32_e32 v90, v90, v93
	s_waitcnt lgkmcnt(0)
	v_add_f32_e32 v94, v94, v95
	ds_bpermute_b32 v92, v160, v91
	ds_bpermute_b32 v93, v160, v90
	ds_bpermute_b32 v95, v160, v94
	s_waitcnt lgkmcnt(2)
	v_add_f32_e32 v91, v91, v92
	s_waitcnt lgkmcnt(1)
	v_add_f32_e32 v90, v90, v93
	s_waitcnt lgkmcnt(0)
	v_add_f32_e32 v94, v94, v95
	ds_bpermute_b32 v92, v159, v91
	ds_bpermute_b32 v93, v159, v90
	ds_bpermute_b32 v95, v159, v94
	s_waitcnt lgkmcnt(2)
	v_add_f32_e32 v122, v91, v92
	s_waitcnt lgkmcnt(1)
	v_add_f32_e32 v126, v90, v93
	s_waitcnt lgkmcnt(0)
	v_add_f32_e32 v124, v94, v95
	ds_bpermute_b32 v123, v158, v122
	ds_bpermute_b32 v127, v158, v126
	ds_bpermute_b32 v125, v158, v124
	v_mov_b32_e32 v92, 1.0
	v_mov_b32_e32 v93, 1.0
	v_mov_b32_e32 v90, 1.0
	v_mov_b32_e32 v94, 1.0
	v_mov_b32_e32 v91, 1.0
	v_mov_b32_e32 v95, 1.0
	s_and_saveexec_b64 s[0:1], s[36:37]
	v_lshlrev_b32_e32 v92, 16, v78
	v_and_b32_e32 v96, 0xffff0000, v78
	v_lshlrev_b32_e32 v93, 16, v79
	v_and_b32_e32 v97, 0xffff0000, v79
	v_lshlrev_b32_e32 v90, 16, v80
	v_and_b32_e32 v94, 0xffff0000, v80
	v_lshlrev_b32_e32 v91, 16, v81
	v_and_b32_e32 v95, 0xffff0000, v81
	s_or_b64 exec, exec, s[0:1]
	v_mov_b32_e32 v100, 1.0
	v_mov_b32_e32 v99, 1.0
	v_mov_b32_e32 v101, 1.0
	v_mov_b32_e32 v78, 1.0
	v_mov_b32_e32 v80, 1.0
	v_mov_b32_e32 v79, 1.0
	v_mov_b32_e32 v81, 1.0
	s_and_saveexec_b64 s[0:1], s[34:35]
	v_lshlrev_b32_e32 v98, 16, v74
	v_and_b32_e32 v100, 0xffff0000, v74
	v_lshlrev_b32_e32 v99, 16, v75
	v_and_b32_e32 v101, 0xffff0000, v75
	v_lshlrev_b32_e32 v78, 16, v76
	v_and_b32_e32 v80, 0xffff0000, v76
	v_lshlrev_b32_e32 v79, 16, v77
	v_and_b32_e32 v81, 0xffff0000, v77
	s_or_b64 exec, exec, s[0:1]
	s_waitcnt lgkmcnt(1)
	v_add_f32_e32 v74, v126, v127
	v_fmamk_f32 v74, v74, 0x3b2aaaab, v215
	v_cmp_gt_f32_e32 vcc, s3, v74
	v_mul_f32_e32 v75, 0x4f800000, v74
	s_movk_i32 s7, 0x7fff
	v_cndmask_b32_e32 v74, v74, v75, vcc
	v_sqrt_f32_e32 v75, v74
	s_mov_b32 s6, 0xffff0000
	v_add_u32_e32 v76, -1, v75
	v_fma_f32 v77, -v76, v75, v74
	v_cmp_ge_f32_e64 s[0:1], 0, v77
	v_add_u32_e32 v77, 1, v75
	s_nop 0
	v_cndmask_b32_e64 v76, v75, v76, s[0:1]
	v_fma_f32 v75, -v77, v75, v74
	v_cmp_lt_f32_e64 s[0:1], 0, v75
	s_nop 1
	v_cndmask_b32_e64 v75, v76, v77, s[0:1]
	v_mul_f32_e32 v76, 0x37800000, v75
	v_cndmask_b32_e32 v75, v75, v76, vcc
	v_cmp_class_f32_e32 vcc, v74, v216
	s_nop 1
	v_cndmask_b32_e32 v74, v75, v74, vcc
	v_div_scale_f32 v75, s[0:1], v74, v74, 1.0
	v_rcp_f32_e32 v76, v75
	s_nop 0
	v_fma_f32 v77, -v75, v76, 1.0
	v_fmac_f32_e32 v76, v77, v76
	v_div_scale_f32 v77, vcc, 1.0, v74, 1.0
	v_mul_f32_e32 v126, v77, v76
	v_fma_f32 v127, -v75, v126, v77
	v_fmac_f32_e32 v126, v127, v76
	v_fma_f32 v75, -v75, v126, v77
	v_div_fmas_f32 v75, v75, v76, v126
	v_div_fixup_f32 v126, v75, v74, 1.0
	s_waitcnt lgkmcnt(0)
; __device__ __forceinline__ unsigned pk2(float lo, float hi) { return f2bf(lo) | (f2bf(hi) << 16); }
; __device__ __forceinline__ void unpack8(const v4u w, float* f) { f[0] = bflo(w.x); f[1] = bfhi(w.x); f[2] = bflo(w.y); f[3] = bfhi(w.y); f[4] = bflo(w.z); f[5] = bfhi(w.z); f[6] = bflo(w.w); f[7] = bfhi(w.w); }
; __device__ __forceinline__ void norm_compute(const NormRow& R, int lane, v4u& ya, v4u& yc) {
;     ...
;     else { float f0[8], f1[8], f2[8]; unpack8(R.d0, f0); unpack8(R.d1, f1); unpack8(R.d2, f2);
;         const float inv = 1.0f / (R.l0 + R.l1 + R.l2);
; #pragma unroll
;         for (int e = 0; e < 8; ++e) fc[e] = (f0[e] + f1[e] + f2[e]) * inv; }
;     ...
;     const float r_moba = 1.0f / sqrtf(s_moba * (1.0f / 256.0f) + EPS), r_fox = 1.0f / sqrtf(s_fox * (1.0f / 384.0f) + EPS), r_dil = 1.0f / sqrtf(s_dil * (1.0f / 384.0f) + EPS);
;     float ga[8], gc[8];
; #pragma unroll
;     for (int e = 0; e < 8; ++e) { ga[e] = 1.f; gc[e] = 1.f; }
;     if (lane >= 32) unpack8(R.ga, ga);
;     if (lane < 16) unpack8(R.gc, gc);
;     const float ra = lane < 32 ? r_moba : r_fox, rc = lane < 16 ? r_fox : r_dil;
;     ya.x = pk2(fa[0] * ra * ga[0], fa[1] * ra * ga[1]); ya.y = pk2(fa[2] * ra * ga[2], fa[3] * ra * ga[3]); ya.z = pk2(fa[4] * ra * ga[4], fa[5] * ra * ga[5]); ya.w = pk2(fa[6] * ra * ga[6], fa[7] * ra * ga[7]);
;     yc.x = pk2(fc[0] * rc * gc[0], fc[1] * rc * gc[1]); yc.y = pk2(fc[2] * rc * gc[2], fc[3] * rc * gc[3]); yc.z = pk2(fc[4] * rc * gc[4], fc[5] * rc * gc[5]); yc.w = pk2(fc[6] * rc * gc[6], fc[7] * rc * gc[7]);
; }
	v_add_f32_e32 v74, v124, v125
	v_fmamk_f32 v74, v74, 0x3b2aaaab, v215
	v_cmp_gt_f32_e32 vcc, s3, v74
	v_mul_f32_e32 v75, 0x4f800000, v74
	s_nop 0
	v_cndmask_b32_e32 v74, v74, v75, vcc
	v_sqrt_f32_e32 v75, v74
	s_nop 0
	v_add_u32_e32 v76, -1, v75
	v_fma_f32 v77, -v76, v75, v74
	v_cmp_ge_f32_e64 s[0:1], 0, v77
	v_add_u32_e32 v77, 1, v75
	s_nop 0
	v_cndmask_b32_e64 v76, v75, v76, s[0:1]
	v_fma_f32 v75, -v77, v75, v74
	v_cmp_lt_f32_e64 s[0:1], 0, v75
	s_nop 1
	v_cndmask_b32_e64 v75, v76, v77, s[0:1]
	v_mul_f32_e32 v76, 0x37800000, v75
	v_cndmask_b32_e32 v75, v75, v76, vcc
	v_cmp_class_f32_e32 vcc, v74, v216
	s_nop 1
	v_cndmask_b32_e32 v74, v75, v74, vcc
	v_div_scale_f32 v75, s[0:1], v74, v74, 1.0
	v_rcp_f32_e32 v76, v75
	s_nop 0
	v_fma_f32 v77, -v75, v76, 1.0
	v_fmac_f32_e32 v76, v77, v76
	v_div_scale_f32 v77, vcc, 1.0, v74, 1.0
	v_mul_f32_e32 v124, v77, v76
	v_fma_f32 v125, -v75, v124, v77
	v_fmac_f32_e32 v124, v125, v76
	v_fma_f32 v75, -v75, v124, v77
	v_div_fmas_f32 v75, v75, v76, v124
	v_div_fixup_f32 v74, v75, v74, 1.0
	v_cndmask_b32_e64 v74, v74, v126, s[34:35]
	v_mul_f32_e32 v76, v114, v74
	v_mul_f32_e32 v77, v115, v74
	s_nop 0
	v_mul_f32_e32 v76, v76, v100
	v_mul_f32_e32 v77, v77, v101
	v_mul_f32_e32 v100, v120, v74
	v_mul_f32_e32 v101, v121, v74
	s_nop 0
	v_mul_f32_e32 v98, v100, v98
	v_mul_f32_e32 v99, v101, v99
	v_mul_f32_e32 v100, v116, v74
	v_mul_f32_e32 v101, v117, v74
	v_mul_f32_e32 v75, v119, v74
	v_mul_f32_e32 v74, v118, v74
	v_mul_f32_e32 v80, v100, v80
	v_mul_f32_e32 v81, v101, v81
	v_mul_f32_e32 v74, v74, v78
	v_mul_f32_e32 v75, v75, v79
	v_bfe_u32 v78, v81, 16, 1
	v_bfe_u32 v79, v80, 16, 1
	v_bfe_u32 v100, v77, 16, 1
	v_bfe_u32 v101, v76, 16, 1
	v_add3_u32 v101, v76, v101, s7
	v_add3_u32 v100, v77, v100, s7
	v_add3_u32 v76, v80, v79, s7
	v_add3_u32 v77, v81, v78, s7
	v_bfe_u32 v78, v98, 16, 1
	v_bfe_u32 v80, v74, 16, 1
	v_add3_u32 v74, v74, v80, s7
	v_add3_u32 v78, v98, v78, s7
	v_bfe_u32 v79, v99, 16, 1
	v_bfe_u32 v81, v75, 16, 1
	v_lshrrev_b32_e32 v78, 16, v78
	v_lshrrev_b32_e32 v74, 16, v74
	v_add3_u32 v75, v75, v81, s7
	v_add3_u32 v79, v99, v79, s7
	v_and_or_b32 v76, v76, s6, v74
	v_and_or_b32 v74, v101, s6, v78
	v_add_f32_e32 v78, v122, v123
	v_lshrrev_b32_e32 v79, 16, v79
	v_lshrrev_b32_e32 v75, 16, v75
	v_fmamk_f32 v78, v78, 0x3b800000, v215
	v_and_or_b32 v77, v77, s6, v75
	v_and_or_b32 v75, v100, s6, v79
	v_cmp_gt_f32_e32 vcc, s3, v78
	v_mul_f32_e32 v79, 0x4f800000, v78
	s_nop 0
	v_cndmask_b32_e32 v78, v78, v79, vcc
	v_sqrt_f32_e32 v79, v78
	s_nop 0
	v_add_u32_e32 v80, -1, v79
	v_fma_f32 v81, -v80, v79, v78
	v_cmp_ge_f32_e64 s[0:1], 0, v81
	v_add_u32_e32 v81, 1, v79
	s_nop 0
	v_cndmask_b32_e64 v80, v79, v80, s[0:1]
	v_fma_f32 v79, -v81, v79, v78
	v_cmp_lt_f32_e64 s[0:1], 0, v79
	s_nop 1
	v_cndmask_b32_e64 v79, v80, v81, s[0:1]
	v_mul_f32_e32 v80, 0x37800000, v79
	v_cndmask_b32_e32 v79, v79, v80, vcc
	v_cmp_class_f32_e32 vcc, v78, v216
	s_nop 1
	v_cndmask_b32_e32 v78, v79, v78, vcc
	v_div_scale_f32 v79, s[0:1], v78, v78, 1.0
	v_rcp_f32_e32 v80, v79
	s_add_u32 s0, s24, s18
	s_addc_u32 s1, s25, s19
	v_fma_f32 v81, -v79, v80, 1.0
	v_fmac_f32_e32 v80, v81, v80
	v_div_scale_f32 v81, vcc, 1.0, v78, 1.0
	v_mul_f32_e32 v98, v81, v80
	v_fma_f32 v99, -v79, v98, v81
	v_fmac_f32_e32 v98, v99, v80
	v_fma_f32 v79, -v79, v98, v81
	v_div_fmas_f32 v79, v79, v80, v98
	v_div_fixup_f32 v78, v79, v78, 1.0
	v_cndmask_b32_e64 v78, v126, v78, s[40:41]
	v_mul_f32_e32 v80, v78, v86
	v_mul_f32_e32 v81, v78, v87
	v_mul_f32_e32 v86, v78, v88
	v_mul_f32_e32 v87, v78, v89
	v_mul_f32_e32 v80, v80, v96
	v_mul_f32_e32 v81, v81, v97
	v_mul_f32_e32 v84, v78, v84
	v_mul_f32_e32 v85, v78, v85
	v_mul_f32_e32 v86, v86, v94
	v_mul_f32_e32 v87, v87, v95
	v_mul_f32_e32 v79, v78, v83
	v_mul_f32_e32 v78, v78, v82
	v_mul_f32_e32 v84, v84, v92
	v_mul_f32_e32 v85, v85, v93
	v_mul_f32_e32 v78, v78, v90
	v_mul_f32_e32 v79, v79, v91
	v_bfe_u32 v82, v87, 16, 1
	v_bfe_u32 v83, v86, 16, 1
	v_bfe_u32 v88, v81, 16, 1
	v_bfe_u32 v89, v80, 16, 1
	v_add3_u32 v89, v80, v89, s7
	v_add3_u32 v88, v81, v88, s7
	v_add3_u32 v80, v86, v83, s7
	v_add3_u32 v81, v87, v82, s7
	v_bfe_u32 v82, v84, 16, 1
	v_bfe_u32 v83, v85, 16, 1
	v_bfe_u32 v86, v78, 16, 1
	v_bfe_u32 v87, v79, 16, 1
	v_add3_u32 v79, v79, v87, s7
	v_add3_u32 v78, v78, v86, s7
	v_add3_u32 v83, v85, v83, s7
	v_add3_u32 v82, v84, v82, s7
	v_lshrrev_b32_e32 v82, 16, v82
	v_lshrrev_b32_e32 v83, 16, v83
	v_lshrrev_b32_e32 v78, 16, v78
	v_lshrrev_b32_e32 v79, 16, v79
	v_and_or_b32 v81, v81, s6, v79
	v_and_or_b32 v80, v80, s6, v78
	v_and_or_b32 v79, v88, s6, v83
	v_and_or_b32 v78, v89, s6, v82
	global_store_dwordx4 v0, v[78:81], s[0:1]
	global_store_dwordx4 v0, v[74:77], s[0:1] offset:1024
	s_and_saveexec_b64 s[0:1], s[38:39]
	s_xor_b64 s[0:1], exec, s[0:1]
	s_cbranch_execz .LBB0_249
	v_add_f32_e32 v71, v171, v170
	v_add_f32_e32 v74, v172, v71
	v_div_scale_f32 v75, s[6:7], v74, v74, 1.0
	v_rcp_f32_e32 v76, v75
	v_lshlrev_b32_e32 v70, 16, v61
	v_and_b32_e32 v71, 0xffff0000, v61
	v_lshlrev_b32_e32 v72, 16, v65
	v_fma_f32 v61, -v75, v76, 1.0
	v_fmac_f32_e32 v76, v61, v76
	v_div_scale_f32 v61, vcc, 1.0, v74, 1.0
	v_and_b32_e32 v73, 0xffff0000, v65
	v_mul_f32_e32 v65, v61, v76
	v_fma_f32 v77, -v75, v65, v61
	v_fmac_f32_e32 v65, v77, v76
	v_fma_f32 v61, -v75, v65, v61
	v_div_fmas_f32 v61, v61, v76, v65
	v_div_fixup_f32 v76, v61, v74, 1.0
	v_lshlrev_b32_e32 v74, 16, v58
	v_and_b32_e32 v75, 0xffff0000, v58
	v_lshlrev_b32_e32 v78, 16, v62
	v_and_b32_e32 v79, 0xffff0000, v62
	v_lshlrev_b32_e32 v58, 16, v59
	v_and_b32_e32 v59, 0xffff0000, v59
	v_lshlrev_b32_e32 v62, 16, v63
	v_and_b32_e32 v63, 0xffff0000, v63
	v_lshlrev_b32_e32 v80, 16, v66
	v_and_b32_e32 v81, 0xffff0000, v66
	v_add_f32_e32 v74, v78, v74
	v_add_f32_e32 v75, v79, v75
	v_lshlrev_b32_e32 v66, 16, v67
	v_and_b32_e32 v67, 0xffff0000, v67
	v_add_f32_e32 v58, v62, v58
	v_add_f32_e32 v59, v63, v59
	v_add_f32_e32 v74, v74, v80
	v_add_f32_e32 v75, v75, v81
	v_add_f32_e32 v58, v58, v66
	v_add_f32_e32 v59, v59, v67
	v_mul_f32_e32 v82, v76, v74
	v_mul_f32_e32 v83, v76, v75
	v_mul_f32_e32 v74, v76, v58
	v_mul_f32_e32 v75, v76, v59
	v_lshlrev_b32_e32 v58, 16, v60
	v_and_b32_e32 v59, 0xffff0000, v60
	v_lshlrev_b32_e32 v60, 16, v64
	v_and_b32_e32 v61, 0xffff0000, v64
	v_lshlrev_b32_e32 v62, 16, v68
	v_and_b32_e32 v63, 0xffff0000, v68
	v_add_f32_e32 v58, v60, v58
	v_add_f32_e32 v59, v61, v59
	v_lshlrev_b32_e32 v60, 16, v69
	v_add_f32_e32 v58, v58, v62
	v_add_f32_e32 v59, v59, v63
	v_and_b32_e32 v61, 0xffff0000, v69
	v_add_f32_e32 v62, v72, v70
	v_add_f32_e32 v63, v73, v71
	v_mul_f32_e32 v58, v76, v58
	v_mul_f32_e32 v59, v76, v59
	v_add_f32_e32 v60, v62, v60
	v_add_f32_e32 v61, v63, v61
	v_mov_b32_e32 v78, v58
	v_mul_f32_e32 v77, v76, v61
	v_mul_f32_e32 v76, v76, v60
	v_mov_b32_e32 v79, v76
	v_mov_b32_e32 v76, v59
	v_mov_b32_e32 v81, v74
	v_mov_b32_e32 v74, v83
	v_mov_b32_e32 v80, v82
; __device__ __forceinline__ void unpack8(const v4u w, float* f) { f[0] = bflo(w.x); f[1] = bfhi(w.x); f[2] = bflo(w.y); f[3] = bfhi(w.y); f[4] = bflo(w.z); f[5] = bfhi(w.z); f[6] = bflo(w.w); f[7] = bfhi(w.w); }
; __device__ __forceinline__ void norm_compute(const NormRow& R, int lane, v4u& ya, v4u& yc) {
;     ...
;     float sa = 0.f, sc = 0.f;
; #pragma unroll
;     for (int e = 0; e < 8; ++e) { sa += fa[e] * fa[e]; sc += fc[e] * fc[e]; }
;     const float s_moba = wave_sum(lane < 32 ? sa : 0.f), s_fox = wave_sum((lane >= 32 ? sa : 0.f) + (lane < 16 ? sc : 0.f)), s_dil = wave_sum(lane >= 16 ? sc : 0.f);
;     const float r_moba = 1.0f / sqrtf(s_moba * (1.0f / 256.0f) + EPS), r_fox = 1.0f / sqrtf(s_fox * (1.0f / 384.0f) + EPS), r_dil = 1.0f / sqrtf(s_dil * (1.0f / 384.0f) + EPS);
;     float ga[8], gc[8];
; #pragma unroll
;     for (int e = 0; e < 8; ++e) { ga[e] = 1.f; gc[e] = 1.f; }
;     if (lane >= 32) unpack8(R.ga, ga);
;     if (lane < 16) unpack8(R.gc, gc);
;     const float ra = lane < 32 ? r_moba : r_fox, rc = lane < 16 ? r_fox : r_dil;
.LBB0_249:
	s_andn2_saveexec_b64 s[0:1], s[0:1]
	v_lshlrev_b32_e32 v80, 16, v70
	v_and_b32_e32 v74, 0xffff0000, v70
	v_lshlrev_b32_e32 v81, 16, v71
	v_and_b32_e32 v75, 0xffff0000, v71
	v_lshlrev_b32_e32 v78, 16, v72
	v_and_b32_e32 v76, 0xffff0000, v72
	v_lshlrev_b32_e32 v79, 16, v73
	v_and_b32_e32 v77, 0xffff0000, v73
	s_or_b64 exec, exec, s[0:1]
	v_lshlrev_b32_e32 v61, 16, v103
	v_lshlrev_b32_e32 v60, 16, v102
	v_and_b32_e32 v63, 0xffff0000, v103
	v_and_b32_e32 v62, 0xffff0000, v102
	v_mul_f32_e32 v66, v60, v60
	v_mul_f32_e32 v67, v61, v61
	v_mul_f32_e32 v68, v62, v62
	v_mul_f32_e32 v69, v63, v63
	v_mul_f32_e32 v82, v74, v74
	v_fmac_f32_e32 v82, v80, v80
	v_add_f32_e32 v66, v66, v68
	v_lshlrev_b32_e32 v59, 16, v105
	v_lshlrev_b32_e32 v58, 16, v104
	v_fmac_f32_e32 v82, v81, v81
	v_add_f32_e32 v66, v67, v66
	v_and_b32_e32 v65, 0xffff0000, v105
	v_and_b32_e32 v64, 0xffff0000, v104
	v_fmac_f32_e32 v82, v75, v75
	v_mul_f32_e32 v70, v58, v58
	v_mul_f32_e32 v71, v59, v59
	v_add_f32_e32 v66, v69, v66
	v_fmac_f32_e32 v82, v78, v78
	v_mul_f32_e32 v72, v64, v64
	v_mul_f32_e32 v73, v65, v65
	v_add_f32_e32 v66, v70, v66
	v_fmac_f32_e32 v82, v76, v76
	v_add_f32_e32 v66, v72, v66
	v_fmac_f32_e32 v82, v79, v79
	v_add_f32_e32 v66, v71, v66
	v_add_f32_e32 v66, v73, v66
	v_fmac_f32_e32 v82, v77, v77
	v_cndmask_b32_e64 v67, 0, v66, s[40:41]
	v_cndmask_b32_e64 v66, 0, v66, s[36:37]
	v_cndmask_b32_e64 v69, 0, v82, s[34:35]
	v_add_f32_e32 v66, v66, v69
	v_cndmask_b32_e64 v70, 0, v82, s[42:43]
	ds_bpermute_b32 v68, v164, v67
	ds_bpermute_b32 v69, v164, v66
	ds_bpermute_b32 v71, v164, v70
	v_mov_b32_e32 v82, 1.0
	v_mov_b32_e32 v72, 1.0
	s_waitcnt lgkmcnt(2)
	v_add_f32_e32 v67, v67, v68
	s_waitcnt lgkmcnt(1)
	v_add_f32_e32 v66, v66, v69
	s_waitcnt lgkmcnt(0)
	v_add_f32_e32 v70, v70, v71
	ds_bpermute_b32 v68, v162, v67
	ds_bpermute_b32 v69, v162, v66
	ds_bpermute_b32 v71, v162, v70
	v_mov_b32_e32 v73, 1.0
	s_waitcnt lgkmcnt(2)
	v_add_f32_e32 v67, v67, v68
	s_waitcnt lgkmcnt(1)
	v_add_f32_e32 v66, v66, v69
	s_waitcnt lgkmcnt(0)
	v_add_f32_e32 v70, v70, v71
	ds_bpermute_b32 v68, v161, v67
	ds_bpermute_b32 v69, v161, v66
	ds_bpermute_b32 v71, v161, v70
	s_waitcnt lgkmcnt(2)
	v_add_f32_e32 v67, v67, v68
	s_waitcnt lgkmcnt(1)
	v_add_f32_e32 v66, v66, v69
	s_waitcnt lgkmcnt(0)
	v_add_f32_e32 v70, v70, v71
	ds_bpermute_b32 v68, v160, v67
	ds_bpermute_b32 v69, v160, v66
	ds_bpermute_b32 v71, v160, v70
	s_waitcnt lgkmcnt(2)
	v_add_f32_e32 v67, v67, v68
	s_waitcnt lgkmcnt(1)
	v_add_f32_e32 v66, v66, v69
	s_waitcnt lgkmcnt(0)
	v_add_f32_e32 v70, v70, v71
	ds_bpermute_b32 v68, v159, v67
	ds_bpermute_b32 v69, v159, v66
	ds_bpermute_b32 v71, v159, v70
	s_waitcnt lgkmcnt(2)
	v_add_f32_e32 v86, v67, v68
	s_waitcnt lgkmcnt(1)
	v_add_f32_e32 v90, v66, v69
	s_waitcnt lgkmcnt(0)
	v_add_f32_e32 v88, v70, v71
	ds_bpermute_b32 v87, v158, v86
	ds_bpermute_b32 v91, v158, v90
	ds_bpermute_b32 v89, v158, v88
	v_mov_b32_e32 v68, 1.0
	v_mov_b32_e32 v69, 1.0
	v_mov_b32_e32 v66, 1.0
	v_mov_b32_e32 v70, 1.0
	v_mov_b32_e32 v67, 1.0
	v_mov_b32_e32 v71, 1.0
	s_and_saveexec_b64 s[0:1], s[36:37]
	v_lshlrev_b32_e32 v68, 16, v54
	v_and_b32_e32 v72, 0xffff0000, v54
	v_lshlrev_b32_e32 v69, 16, v55
	v_and_b32_e32 v73, 0xffff0000, v55
	v_lshlrev_b32_e32 v66, 16, v56
	v_and_b32_e32 v70, 0xffff0000, v56
	v_lshlrev_b32_e32 v67, 16, v57
	v_and_b32_e32 v71, 0xffff0000, v57
	s_or_b64 exec, exec, s[0:1]
	v_mov_b32_e32 v84, 1.0
	v_mov_b32_e32 v83, 1.0
	v_mov_b32_e32 v85, 1.0
	v_mov_b32_e32 v54, 1.0
	v_mov_b32_e32 v56, 1.0
	v_mov_b32_e32 v55, 1.0
	v_mov_b32_e32 v57, 1.0
	s_and_saveexec_b64 s[0:1], s[34:35]
	v_lshlrev_b32_e32 v82, 16, v50
	v_and_b32_e32 v84, 0xffff0000, v50
	v_lshlrev_b32_e32 v83, 16, v51
	v_and_b32_e32 v85, 0xffff0000, v51
	v_lshlrev_b32_e32 v54, 16, v52
	v_and_b32_e32 v56, 0xffff0000, v52
	v_lshlrev_b32_e32 v55, 16, v53
	v_and_b32_e32 v57, 0xffff0000, v53
	s_or_b64 exec, exec, s[0:1]
	s_waitcnt lgkmcnt(1)
	v_add_f32_e32 v50, v90, v91
	v_fmamk_f32 v50, v50, 0x3b2aaaab, v215
	v_cmp_gt_f32_e32 vcc, s3, v50
	v_mul_f32_e32 v51, 0x4f800000, v50
	s_movk_i32 s7, 0x7fff
	v_cndmask_b32_e32 v50, v50, v51, vcc
	v_sqrt_f32_e32 v51, v50
	s_mov_b32 s6, 0xffff0000
	v_add_u32_e32 v52, -1, v51
	v_fma_f32 v53, -v52, v51, v50
	v_cmp_ge_f32_e64 s[0:1], 0, v53
	v_add_u32_e32 v53, 1, v51
	s_nop 0
	v_cndmask_b32_e64 v52, v51, v52, s[0:1]
	v_fma_f32 v51, -v53, v51, v50
	v_cmp_lt_f32_e64 s[0:1], 0, v51
	s_nop 1
	v_cndmask_b32_e64 v51, v52, v53, s[0:1]
	v_mul_f32_e32 v52, 0x37800000, v51
	v_cndmask_b32_e32 v51, v51, v52, vcc
	v_cmp_class_f32_e32 vcc, v50, v216
	s_nop 1
	v_cndmask_b32_e32 v50, v51, v50, vcc
	v_div_scale_f32 v51, s[0:1], v50, v50, 1.0
	v_rcp_f32_e32 v52, v51
	s_nop 0
	v_fma_f32 v53, -v51, v52, 1.0
	v_fmac_f32_e32 v52, v53, v52
	v_div_scale_f32 v53, vcc, 1.0, v50, 1.0
	v_mul_f32_e32 v90, v53, v52
	v_fma_f32 v91, -v51, v90, v53
	v_fmac_f32_e32 v90, v91, v52
	v_fma_f32 v51, -v51, v90, v53
	v_div_fmas_f32 v51, v51, v52, v90
	v_div_fixup_f32 v90, v51, v50, 1.0
	s_waitcnt lgkmcnt(0)
; __device__ __forceinline__ unsigned pk2(float lo, float hi) { return f2bf(lo) | (f2bf(hi) << 16); }
; __device__ __forceinline__ void unpack8(const v4u w, float* f) { f[0] = bflo(w.x); f[1] = bfhi(w.x); f[2] = bflo(w.y); f[3] = bfhi(w.y); f[4] = bflo(w.z); f[5] = bfhi(w.z); f[6] = bflo(w.w); f[7] = bfhi(w.w); }
; __device__ __forceinline__ void norm_compute(const NormRow& R, int lane, v4u& ya, v4u& yc) {
;     float fa[8], fc[8];
;     unpack8(R.oa, fa);
;     if (lane < 16) unpack8(R.oc, fc);
;     else { float f0[8], f1[8], f2[8]; unpack8(R.d0, f0); unpack8(R.d1, f1); unpack8(R.d2, f2);
;         const float inv = 1.0f / (R.l0 + R.l1 + R.l2);
; #pragma unroll
;         for (int e = 0; e < 8; ++e) fc[e] = (f0[e] + f1[e] + f2[e]) * inv; }
;     float sa = 0.f, sc = 0.f;
; #pragma unroll
;     for (int e = 0; e < 8; ++e) { sa += fa[e] * fa[e]; sc += fc[e] * fc[e]; }
;     const float s_moba = wave_sum(lane < 32 ? sa : 0.f), s_fox = wave_sum((lane >= 32 ? sa : 0.f) + (lane < 16 ? sc : 0.f)), s_dil = wave_sum(lane >= 16 ? sc : 0.f);
;     const float r_moba = 1.0f / sqrtf(s_moba * (1.0f / 256.0f) + EPS), r_fox = 1.0f / sqrtf(s_fox * (1.0f / 384.0f) + EPS), r_dil = 1.0f / sqrtf(s_dil * (1.0f / 384.0f) + EPS);
;     float ga[8], gc[8];
; #pragma unroll
;     for (int e = 0; e < 8; ++e) { ga[e] = 1.f; gc[e] = 1.f; }
;     if (lane >= 32) unpack8(R.ga, ga);
;     if (lane < 16) unpack8(R.gc, gc);
;     const float ra = lane < 32 ? r_moba : r_fox, rc = lane < 16 ? r_fox : r_dil;
;     ya.x = pk2(fa[0] * ra * ga[0], fa[1] * ra * ga[1]); ya.y = pk2(fa[2] * ra * ga[2], fa[3] * ra * ga[3]); ya.z = pk2(fa[4] * ra * ga[4], fa[5] * ra * ga[5]); ya.w = pk2(fa[6] * ra * ga[6], fa[7] * ra * ga[7]);
;     yc.x = pk2(fc[0] * rc * gc[0], fc[1] * rc * gc[1]); yc.y = pk2(fc[2] * rc * gc[2], fc[3] * rc * gc[3]); yc.z = pk2(fc[4] * rc * gc[4], fc[5] * rc * gc[5]); yc.w = pk2(fc[6] * rc * gc[6], fc[7] * rc * gc[7]);
; }
	v_add_f32_e32 v50, v88, v89
	v_fmamk_f32 v50, v50, 0x3b2aaaab, v215
	v_cmp_gt_f32_e32 vcc, s3, v50
	v_mul_f32_e32 v51, 0x4f800000, v50
	s_nop 0
	v_cndmask_b32_e32 v50, v50, v51, vcc
	v_sqrt_f32_e32 v51, v50
	s_nop 0
	v_add_u32_e32 v52, -1, v51
	v_fma_f32 v53, -v52, v51, v50
	v_cmp_ge_f32_e64 s[0:1], 0, v53
	v_add_u32_e32 v53, 1, v51
	s_nop 0
	v_cndmask_b32_e64 v52, v51, v52, s[0:1]
	v_fma_f32 v51, -v53, v51, v50
	v_cmp_lt_f32_e64 s[0:1], 0, v51
	s_nop 1
	v_cndmask_b32_e64 v51, v52, v53, s[0:1]
	v_mul_f32_e32 v52, 0x37800000, v51
	v_cndmask_b32_e32 v51, v51, v52, vcc
	v_cmp_class_f32_e32 vcc, v50, v216
	s_nop 1
	v_cndmask_b32_e32 v50, v51, v50, vcc
	v_div_scale_f32 v51, s[0:1], v50, v50, 1.0
	v_rcp_f32_e32 v52, v51
	s_nop 0
	v_fma_f32 v53, -v51, v52, 1.0
	v_fmac_f32_e32 v52, v53, v52
	v_div_scale_f32 v53, vcc, 1.0, v50, 1.0
	v_mul_f32_e32 v88, v53, v52
	v_fma_f32 v89, -v51, v88, v53
	v_fmac_f32_e32 v88, v89, v52
	v_fma_f32 v51, -v51, v88, v53
	v_div_fmas_f32 v51, v51, v52, v88
	v_div_fixup_f32 v50, v51, v50, 1.0
	v_cndmask_b32_e64 v50, v50, v90, s[34:35]
	v_mul_f32_e32 v52, v74, v50
	v_mul_f32_e32 v53, v75, v50
	v_mul_f32_e32 v76, v76, v50
	v_mul_f32_e32 v77, v77, v50
	v_mul_f32_e32 v52, v52, v84
	v_mul_f32_e32 v53, v53, v85
	v_mul_f32_e32 v74, v80, v50
	v_mul_f32_e32 v75, v81, v50
	v_mul_f32_e32 v56, v76, v56
	v_mul_f32_e32 v57, v77, v57
	v_mul_f32_e32 v51, v79, v50
	v_mul_f32_e32 v50, v78, v50
	v_mul_f32_e32 v74, v74, v82
	v_mul_f32_e32 v75, v75, v83
	v_mul_f32_e32 v50, v50, v54
	v_mul_f32_e32 v51, v51, v55
	v_bfe_u32 v54, v57, 16, 1
	v_bfe_u32 v55, v56, 16, 1
	v_bfe_u32 v76, v53, 16, 1
	v_bfe_u32 v77, v52, 16, 1
	v_add3_u32 v77, v52, v77, s7
	v_add3_u32 v76, v53, v76, s7
	v_add3_u32 v52, v56, v55, s7
	v_add3_u32 v53, v57, v54, s7
	v_bfe_u32 v54, v74, 16, 1
	v_bfe_u32 v56, v50, 16, 1
	v_add3_u32 v50, v50, v56, s7
	v_add3_u32 v54, v74, v54, s7
	v_bfe_u32 v55, v75, 16, 1
	v_bfe_u32 v57, v51, 16, 1
	v_lshrrev_b32_e32 v54, 16, v54
	v_lshrrev_b32_e32 v50, 16, v50
	v_add3_u32 v51, v51, v57, s7
	v_add3_u32 v55, v75, v55, s7
	v_and_or_b32 v52, v52, s6, v50
	v_and_or_b32 v50, v77, s6, v54
	v_add_f32_e32 v54, v86, v87
	v_lshrrev_b32_e32 v55, 16, v55
	v_lshrrev_b32_e32 v51, 16, v51
	v_fmamk_f32 v54, v54, 0x3b800000, v215
	v_and_or_b32 v53, v53, s6, v51
	v_and_or_b32 v51, v76, s6, v55
	v_cmp_gt_f32_e32 vcc, s3, v54
	v_mul_f32_e32 v55, 0x4f800000, v54
	s_nop 0
	v_cndmask_b32_e32 v54, v54, v55, vcc
	v_sqrt_f32_e32 v55, v54
	s_nop 0
	v_add_u32_e32 v56, -1, v55
	v_fma_f32 v57, -v56, v55, v54
	v_cmp_ge_f32_e64 s[0:1], 0, v57
	v_add_u32_e32 v57, 1, v55
	s_nop 0
	v_cndmask_b32_e64 v56, v55, v56, s[0:1]
	v_fma_f32 v55, -v57, v55, v54
	v_cmp_lt_f32_e64 s[0:1], 0, v55
	s_nop 1
	v_cndmask_b32_e64 v55, v56, v57, s[0:1]
	v_mul_f32_e32 v56, 0x37800000, v55
	v_cndmask_b32_e32 v55, v55, v56, vcc
	v_cmp_class_f32_e32 vcc, v54, v216
	s_nop 1
	v_cndmask_b32_e32 v54, v55, v54, vcc
	v_div_scale_f32 v55, s[0:1], v54, v54, 1.0
	v_rcp_f32_e32 v56, v55
	s_add_u32 s0, s24, s10
	s_addc_u32 s1, s25, s11
	v_fma_f32 v57, -v55, v56, 1.0
	v_fmac_f32_e32 v56, v57, v56
	v_div_scale_f32 v57, vcc, 1.0, v54, 1.0
	v_mul_f32_e32 v74, v57, v56
	v_fma_f32 v75, -v55, v74, v57
	v_fmac_f32_e32 v74, v75, v56
	v_fma_f32 v55, -v55, v74, v57
	v_div_fmas_f32 v55, v55, v56, v74
	v_div_fixup_f32 v54, v55, v54, 1.0
	v_cndmask_b32_e64 v54, v90, v54, s[40:41]
	v_mul_f32_e32 v56, v54, v62
	v_mul_f32_e32 v57, v54, v63
	v_mul_f32_e32 v62, v54, v64
	v_mul_f32_e32 v63, v54, v65
	v_mul_f32_e32 v56, v56, v72
	v_mul_f32_e32 v57, v57, v73
	v_mul_f32_e32 v60, v54, v60
	v_mul_f32_e32 v61, v54, v61
	v_mul_f32_e32 v62, v62, v70
	v_mul_f32_e32 v63, v63, v71
	v_mul_f32_e32 v55, v54, v59
	v_mul_f32_e32 v54, v54, v58
	v_mul_f32_e32 v60, v60, v68
	v_mul_f32_e32 v61, v61, v69
	v_mul_f32_e32 v54, v54, v66
	v_mul_f32_e32 v55, v55, v67
	v_bfe_u32 v58, v63, 16, 1
	v_bfe_u32 v59, v62, 16, 1
	v_bfe_u32 v64, v57, 16, 1
	v_bfe_u32 v65, v56, 16, 1
	v_add3_u32 v65, v56, v65, s7
	v_add3_u32 v64, v57, v64, s7
	v_add3_u32 v56, v62, v59, s7
	v_add3_u32 v57, v63, v58, s7
	v_bfe_u32 v58, v60, 16, 1
	v_bfe_u32 v59, v61, 16, 1
	v_bfe_u32 v62, v54, 16, 1
	v_bfe_u32 v63, v55, 16, 1
	v_add3_u32 v55, v55, v63, s7
	v_add3_u32 v54, v54, v62, s7
	v_add3_u32 v59, v61, v59, s7
	v_add3_u32 v58, v60, v58, s7
	v_lshrrev_b32_e32 v58, 16, v58
	v_lshrrev_b32_e32 v59, 16, v59
	v_lshrrev_b32_e32 v54, 16, v54
	v_lshrrev_b32_e32 v55, 16, v55
	v_and_or_b32 v57, v57, s6, v55
	v_and_or_b32 v56, v56, s6, v54
	v_and_or_b32 v55, v64, s6, v59
	v_and_or_b32 v54, v65, s6, v58
	global_store_dwordx4 v0, v[54:57], s[0:1]
	global_store_dwordx4 v0, v[50:53], s[0:1] offset:1024
	s_and_saveexec_b64 s[0:1], s[38:39]
	s_xor_b64 s[0:1], exec, s[0:1]
	s_cbranch_execz .LBB0_257
	v_add_f32_e32 v47, v168, v167
	v_add_f32_e32 v50, v169, v47
	v_div_scale_f32 v51, s[6:7], v50, v50, 1.0
	v_rcp_f32_e32 v52, v51
	v_lshlrev_b32_e32 v46, 16, v37
	v_and_b32_e32 v47, 0xffff0000, v37
	v_lshlrev_b32_e32 v48, 16, v41
	v_fma_f32 v37, -v51, v52, 1.0
	v_fmac_f32_e32 v52, v37, v52
	v_div_scale_f32 v37, vcc, 1.0, v50, 1.0
	v_and_b32_e32 v49, 0xffff0000, v41
	v_mul_f32_e32 v41, v37, v52
	v_fma_f32 v53, -v51, v41, v37
	v_fmac_f32_e32 v41, v53, v52
	v_fma_f32 v37, -v51, v41, v37
	v_div_fmas_f32 v37, v37, v52, v41
	v_div_fixup_f32 v52, v37, v50, 1.0
	v_lshlrev_b32_e32 v50, 16, v34
	v_and_b32_e32 v51, 0xffff0000, v34
	v_lshlrev_b32_e32 v54, 16, v38
	v_and_b32_e32 v55, 0xffff0000, v38
	v_lshlrev_b32_e32 v34, 16, v35
	v_and_b32_e32 v35, 0xffff0000, v35
	v_lshlrev_b32_e32 v38, 16, v39
	v_and_b32_e32 v39, 0xffff0000, v39
	v_lshlrev_b32_e32 v56, 16, v42
	v_and_b32_e32 v57, 0xffff0000, v42
	v_add_f32_e32 v50, v54, v50
	v_add_f32_e32 v51, v55, v51
	v_lshlrev_b32_e32 v42, 16, v43
	v_and_b32_e32 v43, 0xffff0000, v43
	v_add_f32_e32 v34, v38, v34
	v_add_f32_e32 v35, v39, v35
	v_add_f32_e32 v50, v50, v56
	v_add_f32_e32 v51, v51, v57
	v_add_f32_e32 v34, v34, v42
	v_add_f32_e32 v35, v35, v43
	v_mul_f32_e32 v58, v52, v50
	v_mul_f32_e32 v59, v52, v51
	v_mul_f32_e32 v50, v52, v34
	v_mul_f32_e32 v51, v52, v35
	v_lshlrev_b32_e32 v34, 16, v36
	v_and_b32_e32 v35, 0xffff0000, v36
	v_lshlrev_b32_e32 v36, 16, v40
	v_and_b32_e32 v37, 0xffff0000, v40
	v_lshlrev_b32_e32 v38, 16, v44
	v_and_b32_e32 v39, 0xffff0000, v44
	v_add_f32_e32 v34, v36, v34
	v_add_f32_e32 v35, v37, v35
	v_lshlrev_b32_e32 v36, 16, v45
	v_add_f32_e32 v34, v34, v38
	v_add_f32_e32 v35, v35, v39
	v_and_b32_e32 v37, 0xffff0000, v45
	v_add_f32_e32 v38, v48, v46
	v_add_f32_e32 v39, v49, v47
	v_mul_f32_e32 v34, v52, v34
	v_mul_f32_e32 v35, v52, v35
	v_add_f32_e32 v36, v38, v36
	v_add_f32_e32 v37, v39, v37
	v_mov_b32_e32 v54, v34
	v_mul_f32_e32 v53, v52, v37
	v_mul_f32_e32 v52, v52, v36
	v_mov_b32_e32 v55, v52
	v_mov_b32_e32 v52, v35
	v_mov_b32_e32 v57, v50
	v_mov_b32_e32 v50, v59
	v_mov_b32_e32 v56, v58
; __device__ __forceinline__ void unpack8(const v4u w, float* f) { f[0] = bflo(w.x); f[1] = bfhi(w.x); f[2] = bflo(w.y); f[3] = bfhi(w.y); f[4] = bflo(w.z); f[5] = bfhi(w.z); f[6] = bflo(w.w); f[7] = bfhi(w.w); }
; __device__ __forceinline__ void norm_compute(const NormRow& R, int lane, v4u& ya, v4u& yc) {
;     float fa[8], fc[8];
;     unpack8(R.oa, fa);
;     if (lane < 16) unpack8(R.oc, fc);
;     else { float f0[8], f1[8], f2[8]; unpack8(R.d0, f0); unpack8(R.d1, f1); unpack8(R.d2, f2);
;         const float inv = 1.0f / (R.l0 + R.l1 + R.l2);
; #pragma unroll
;         for (int e = 0; e < 8; ++e) fc[e] = (f0[e] + f1[e] + f2[e]) * inv; }
;     float sa = 0.f, sc = 0.f;
; #pragma unroll
;     for (int e = 0; e < 8; ++e) { sa += fa[e] * fa[e]; sc += fc[e] * fc[e]; }
;     const float s_moba = wave_sum(lane < 32 ? sa : 0.f), s_fox = wave_sum((lane >= 32 ? sa : 0.f) + (lane < 16 ? sc : 0.f)), s_dil = wave_sum(lane >= 16 ? sc : 0.f);
;     const float r_moba = 1.0f / sqrtf(s_moba * (1.0f / 256.0f) + EPS), r_fox = 1.0f / sqrtf(s_fox * (1.0f / 384.0f) + EPS), r_dil = 1.0f / sqrtf(s_dil * (1.0f / 384.0f) + EPS);
;     float ga[8], gc[8];
; #pragma unroll
;     for (int e = 0; e < 8; ++e) { ga[e] = 1.f; gc[e] = 1.f; }
;     if (lane >= 32) unpack8(R.ga, ga);
;     if (lane < 16) unpack8(R.gc, gc);
.LBB0_257:
	s_andn2_saveexec_b64 s[0:1], s[0:1]
	v_lshlrev_b32_e32 v56, 16, v46
	v_and_b32_e32 v50, 0xffff0000, v46
	v_lshlrev_b32_e32 v57, 16, v47
	v_and_b32_e32 v51, 0xffff0000, v47
	v_lshlrev_b32_e32 v54, 16, v48
	v_and_b32_e32 v52, 0xffff0000, v48
	v_lshlrev_b32_e32 v55, 16, v49
	v_and_b32_e32 v53, 0xffff0000, v49
	s_or_b64 exec, exec, s[0:1]
	v_lshlrev_b32_e32 v37, 16, v107
	v_lshlrev_b32_e32 v36, 16, v106
	v_and_b32_e32 v39, 0xffff0000, v107
	v_and_b32_e32 v38, 0xffff0000, v106
	v_mul_f32_e32 v42, v36, v36
	v_mul_f32_e32 v43, v37, v37
	v_mul_f32_e32 v44, v38, v38
	v_mul_f32_e32 v45, v39, v39
	v_mul_f32_e32 v58, v50, v50
	v_fmac_f32_e32 v58, v56, v56
	v_add_f32_e32 v42, v42, v44
	v_lshlrev_b32_e32 v35, 16, v109
	v_lshlrev_b32_e32 v34, 16, v108
	v_fmac_f32_e32 v58, v57, v57
	v_add_f32_e32 v42, v43, v42
	v_and_b32_e32 v41, 0xffff0000, v109
	v_and_b32_e32 v40, 0xffff0000, v108
	v_fmac_f32_e32 v58, v51, v51
	v_mul_f32_e32 v46, v34, v34
	v_mul_f32_e32 v47, v35, v35
	v_add_f32_e32 v42, v45, v42
	v_fmac_f32_e32 v58, v54, v54
	v_mul_f32_e32 v48, v40, v40
	v_mul_f32_e32 v49, v41, v41
	v_add_f32_e32 v42, v46, v42
	v_fmac_f32_e32 v58, v52, v52
	v_add_f32_e32 v42, v48, v42
	v_fmac_f32_e32 v58, v55, v55
	v_add_f32_e32 v42, v47, v42
	v_add_f32_e32 v42, v49, v42
	v_fmac_f32_e32 v58, v53, v53
	v_cndmask_b32_e64 v43, 0, v42, s[40:41]
	v_cndmask_b32_e64 v42, 0, v42, s[36:37]
	v_cndmask_b32_e64 v45, 0, v58, s[34:35]
	v_add_f32_e32 v42, v42, v45
	v_cndmask_b32_e64 v46, 0, v58, s[42:43]
	ds_bpermute_b32 v44, v164, v43
	ds_bpermute_b32 v45, v164, v42
	ds_bpermute_b32 v47, v164, v46
	v_mov_b32_e32 v58, 1.0
	v_mov_b32_e32 v48, 1.0
	s_waitcnt lgkmcnt(2)
	v_add_f32_e32 v43, v43, v44
	s_waitcnt lgkmcnt(1)
	v_add_f32_e32 v42, v42, v45
	s_waitcnt lgkmcnt(0)
	v_add_f32_e32 v46, v46, v47
	ds_bpermute_b32 v44, v162, v43
	ds_bpermute_b32 v45, v162, v42
	ds_bpermute_b32 v47, v162, v46
	v_mov_b32_e32 v49, 1.0
	s_waitcnt lgkmcnt(2)
	v_add_f32_e32 v43, v43, v44
	s_waitcnt lgkmcnt(1)
	v_add_f32_e32 v42, v42, v45
	s_waitcnt lgkmcnt(0)
	v_add_f32_e32 v46, v46, v47
	ds_bpermute_b32 v44, v161, v43
	ds_bpermute_b32 v45, v161, v42
	ds_bpermute_b32 v47, v161, v46
	s_waitcnt lgkmcnt(2)
	v_add_f32_e32 v43, v43, v44
	s_waitcnt lgkmcnt(1)
	v_add_f32_e32 v42, v42, v45
	s_waitcnt lgkmcnt(0)
	v_add_f32_e32 v46, v46, v47
	ds_bpermute_b32 v44, v160, v43
	ds_bpermute_b32 v45, v160, v42
	ds_bpermute_b32 v47, v160, v46
	s_waitcnt lgkmcnt(2)
	v_add_f32_e32 v43, v43, v44
	s_waitcnt lgkmcnt(1)
	v_add_f32_e32 v42, v42, v45
	s_waitcnt lgkmcnt(0)
	v_add_f32_e32 v46, v46, v47
	ds_bpermute_b32 v44, v159, v43
	ds_bpermute_b32 v45, v159, v42
	ds_bpermute_b32 v47, v159, v46
	s_waitcnt lgkmcnt(2)
	v_add_f32_e32 v62, v43, v44
	s_waitcnt lgkmcnt(1)
	v_add_f32_e32 v66, v42, v45
	s_waitcnt lgkmcnt(0)
	v_add_f32_e32 v64, v46, v47
	ds_bpermute_b32 v63, v158, v62
	ds_bpermute_b32 v67, v158, v66
	ds_bpermute_b32 v65, v158, v64
	v_mov_b32_e32 v44, 1.0
	v_mov_b32_e32 v45, 1.0
	v_mov_b32_e32 v42, 1.0
	v_mov_b32_e32 v46, 1.0
	v_mov_b32_e32 v43, 1.0
	v_mov_b32_e32 v47, 1.0
	s_and_saveexec_b64 s[0:1], s[36:37]
	v_lshlrev_b32_e32 v44, 16, v30
	v_and_b32_e32 v48, 0xffff0000, v30
	v_lshlrev_b32_e32 v45, 16, v31
	v_and_b32_e32 v49, 0xffff0000, v31
	v_lshlrev_b32_e32 v42, 16, v32
	v_and_b32_e32 v46, 0xffff0000, v32
	v_lshlrev_b32_e32 v43, 16, v33
	v_and_b32_e32 v47, 0xffff0000, v33
	s_or_b64 exec, exec, s[0:1]
	v_mov_b32_e32 v60, 1.0
	v_mov_b32_e32 v59, 1.0
	v_mov_b32_e32 v61, 1.0
	v_mov_b32_e32 v30, 1.0
	v_mov_b32_e32 v32, 1.0
	v_mov_b32_e32 v31, 1.0
	v_mov_b32_e32 v33, 1.0
	s_and_saveexec_b64 s[0:1], s[34:35]
	v_lshlrev_b32_e32 v58, 16, v26
	v_and_b32_e32 v60, 0xffff0000, v26
	v_lshlrev_b32_e32 v59, 16, v27
	v_and_b32_e32 v61, 0xffff0000, v27
	v_lshlrev_b32_e32 v30, 16, v28
	v_and_b32_e32 v32, 0xffff0000, v28
	v_lshlrev_b32_e32 v31, 16, v29
	v_and_b32_e32 v33, 0xffff0000, v29
	s_or_b64 exec, exec, s[0:1]
	s_waitcnt lgkmcnt(1)
	v_add_f32_e32 v26, v66, v67
	v_fmamk_f32 v26, v26, 0x3b2aaaab, v215
	v_cmp_gt_f32_e32 vcc, s3, v26
	v_mul_f32_e32 v27, 0x4f800000, v26
	s_movk_i32 s7, 0x7fff
	v_cndmask_b32_e32 v26, v26, v27, vcc
	v_sqrt_f32_e32 v27, v26
	s_mov_b32 s6, 0xffff0000
	v_add_u32_e32 v28, -1, v27
	v_fma_f32 v29, -v28, v27, v26
	v_cmp_ge_f32_e64 s[0:1], 0, v29
	v_add_u32_e32 v29, 1, v27
	s_nop 0
	v_cndmask_b32_e64 v28, v27, v28, s[0:1]
	v_fma_f32 v27, -v29, v27, v26
	v_cmp_lt_f32_e64 s[0:1], 0, v27
	s_nop 1
	v_cndmask_b32_e64 v27, v28, v29, s[0:1]
	v_mul_f32_e32 v28, 0x37800000, v27
	v_cndmask_b32_e32 v27, v27, v28, vcc
	v_cmp_class_f32_e32 vcc, v26, v216
	s_nop 1
	v_cndmask_b32_e32 v26, v27, v26, vcc
	v_div_scale_f32 v27, s[0:1], v26, v26, 1.0
	v_rcp_f32_e32 v28, v27
	s_nop 0
	v_fma_f32 v29, -v27, v28, 1.0
	v_fmac_f32_e32 v28, v29, v28
	v_div_scale_f32 v29, vcc, 1.0, v26, 1.0
	v_mul_f32_e32 v66, v29, v28
	v_fma_f32 v67, -v27, v66, v29
	v_fmac_f32_e32 v66, v67, v28
	v_fma_f32 v27, -v27, v66, v29
	v_div_fmas_f32 v27, v27, v28, v66
	v_div_fixup_f32 v66, v27, v26, 1.0
	s_waitcnt lgkmcnt(0)
; __device__ __forceinline__ unsigned pk2(float lo, float hi) { return f2bf(lo) | (f2bf(hi) << 16); }
; __device__ __forceinline__ void unpack8(const v4u w, float* f) { f[0] = bflo(w.x); f[1] = bfhi(w.x); f[2] = bflo(w.y); f[3] = bfhi(w.y); f[4] = bflo(w.z); f[5] = bfhi(w.z); f[6] = bflo(w.w); f[7] = bfhi(w.w); }
; __device__ __forceinline__ void norm_compute(const NormRow& R, int lane, v4u& ya, v4u& yc) {
;     float fa[8], fc[8];
;     unpack8(R.oa, fa);
;     if (lane < 16) unpack8(R.oc, fc);
;     else { float f0[8], f1[8], f2[8]; unpack8(R.d0, f0); unpack8(R.d1, f1); unpack8(R.d2, f2);
;         const float inv = 1.0f / (R.l0 + R.l1 + R.l2);
; #pragma unroll
;         for (int e = 0; e < 8; ++e) fc[e] = (f0[e] + f1[e] + f2[e]) * inv; }
;     float sa = 0.f, sc = 0.f;
; #pragma unroll
;     for (int e = 0; e < 8; ++e) { sa += fa[e] * fa[e]; sc += fc[e] * fc[e]; }
;     const float s_moba = wave_sum(lane < 32 ? sa : 0.f), s_fox = wave_sum((lane >= 32 ? sa : 0.f) + (lane < 16 ? sc : 0.f)), s_dil = wave_sum(lane >= 16 ? sc : 0.f);
;     const float r_moba = 1.0f / sqrtf(s_moba * (1.0f / 256.0f) + EPS), r_fox = 1.0f / sqrtf(s_fox * (1.0f / 384.0f) + EPS), r_dil = 1.0f / sqrtf(s_dil * (1.0f / 384.0f) + EPS);
;     float ga[8], gc[8];
; #pragma unroll
;     for (int e = 0; e < 8; ++e) { ga[e] = 1.f; gc[e] = 1.f; }
;     if (lane >= 32) unpack8(R.ga, ga);
;     if (lane < 16) unpack8(R.gc, gc);
;     const float ra = lane < 32 ? r_moba : r_fox, rc = lane < 16 ? r_fox : r_dil;
;     ya.x = pk2(fa[0] * ra * ga[0], fa[1] * ra * ga[1]); ya.y = pk2(fa[2] * ra * ga[2], fa[3] * ra * ga[3]); ya.z = pk2(fa[4] * ra * ga[4], fa[5] * ra * ga[5]); ya.w = pk2(fa[6] * ra * ga[6], fa[7] * ra * ga[7]);
;     yc.x = pk2(fc[0] * rc * gc[0], fc[1] * rc * gc[1]); yc.y = pk2(fc[2] * rc * gc[2], fc[3] * rc * gc[3]); yc.z = pk2(fc[4] * rc * gc[4], fc[5] * rc * gc[5]); yc.w = pk2(fc[6] * rc * gc[6], fc[7] * rc * gc[7]);
; }
	v_add_f32_e32 v26, v64, v65
	v_fmamk_f32 v26, v26, 0x3b2aaaab, v215
	v_cmp_gt_f32_e32 vcc, s3, v26
	v_mul_f32_e32 v27, 0x4f800000, v26
	s_nop 0
	v_cndmask_b32_e32 v26, v26, v27, vcc
	v_sqrt_f32_e32 v27, v26
	s_nop 0
	v_add_u32_e32 v28, -1, v27
	v_fma_f32 v29, -v28, v27, v26
	v_cmp_ge_f32_e64 s[0:1], 0, v29
	v_add_u32_e32 v29, 1, v27
	s_nop 0
	v_cndmask_b32_e64 v28, v27, v28, s[0:1]
	v_fma_f32 v27, -v29, v27, v26
	v_cmp_lt_f32_e64 s[0:1], 0, v27
	s_nop 1
	v_cndmask_b32_e64 v27, v28, v29, s[0:1]
	v_mul_f32_e32 v28, 0x37800000, v27
	v_cndmask_b32_e32 v27, v27, v28, vcc
	v_cmp_class_f32_e32 vcc, v26, v216
	s_nop 1
	v_cndmask_b32_e32 v26, v27, v26, vcc
	v_div_scale_f32 v27, s[0:1], v26, v26, 1.0
	v_rcp_f32_e32 v28, v27
	s_nop 0
	v_fma_f32 v29, -v27, v28, 1.0
	v_fmac_f32_e32 v28, v29, v28
	v_div_scale_f32 v29, vcc, 1.0, v26, 1.0
	v_mul_f32_e32 v64, v29, v28
	v_fma_f32 v65, -v27, v64, v29
	v_fmac_f32_e32 v64, v65, v28
	v_fma_f32 v27, -v27, v64, v29
	v_div_fmas_f32 v27, v27, v28, v64
	v_div_fixup_f32 v26, v27, v26, 1.0
	v_cndmask_b32_e64 v26, v26, v66, s[34:35]
	v_mul_f32_e32 v28, v50, v26
	v_mul_f32_e32 v29, v51, v26
	v_mul_f32_e32 v52, v52, v26
	v_mul_f32_e32 v53, v53, v26
	v_mul_f32_e32 v28, v28, v60
	v_mul_f32_e32 v29, v29, v61
	v_mul_f32_e32 v50, v56, v26
	v_mul_f32_e32 v51, v57, v26
	v_mul_f32_e32 v32, v52, v32
	v_mul_f32_e32 v33, v53, v33
	v_mul_f32_e32 v27, v55, v26
	v_mul_f32_e32 v26, v54, v26
	v_mul_f32_e32 v50, v50, v58
	v_mul_f32_e32 v51, v51, v59
	v_mul_f32_e32 v26, v26, v30
	v_mul_f32_e32 v27, v27, v31
	v_bfe_u32 v30, v33, 16, 1
	v_bfe_u32 v31, v32, 16, 1
	v_bfe_u32 v52, v29, 16, 1
	v_bfe_u32 v53, v28, 16, 1
	v_add3_u32 v53, v28, v53, s7
	v_add3_u32 v52, v29, v52, s7
	v_add3_u32 v28, v32, v31, s7
	v_add3_u32 v29, v33, v30, s7
	v_bfe_u32 v30, v50, 16, 1
	v_bfe_u32 v32, v26, 16, 1
	v_add3_u32 v26, v26, v32, s7
	v_add3_u32 v30, v50, v30, s7
	v_bfe_u32 v31, v51, 16, 1
	v_bfe_u32 v33, v27, 16, 1
	v_lshrrev_b32_e32 v30, 16, v30
	v_lshrrev_b32_e32 v26, 16, v26
	v_add3_u32 v27, v27, v33, s7
	v_add3_u32 v31, v51, v31, s7
	v_and_or_b32 v28, v28, s6, v26
	v_and_or_b32 v26, v53, s6, v30
	v_add_f32_e32 v30, v62, v63
	v_lshrrev_b32_e32 v31, 16, v31
	v_lshrrev_b32_e32 v27, 16, v27
	v_fmamk_f32 v30, v30, 0x3b800000, v215
	v_and_or_b32 v29, v29, s6, v27
	v_and_or_b32 v27, v52, s6, v31
	v_cmp_gt_f32_e32 vcc, s3, v30
	v_mul_f32_e32 v31, 0x4f800000, v30
	s_nop 0
	v_cndmask_b32_e32 v30, v30, v31, vcc
	v_sqrt_f32_e32 v31, v30
	s_nop 0
	v_add_u32_e32 v32, -1, v31
	v_fma_f32 v33, -v32, v31, v30
	v_cmp_ge_f32_e64 s[0:1], 0, v33
	v_add_u32_e32 v33, 1, v31
	s_nop 0
	v_cndmask_b32_e64 v32, v31, v32, s[0:1]
	v_fma_f32 v31, -v33, v31, v30
	v_cmp_lt_f32_e64 s[0:1], 0, v31
	s_nop 1
	v_cndmask_b32_e64 v31, v32, v33, s[0:1]
	v_mul_f32_e32 v32, 0x37800000, v31
	v_cndmask_b32_e32 v31, v31, v32, vcc
	v_cmp_class_f32_e32 vcc, v30, v216
	s_nop 1
	v_cndmask_b32_e32 v30, v31, v30, vcc
	v_div_scale_f32 v31, s[0:1], v30, v30, 1.0
	v_rcp_f32_e32 v32, v31
	s_add_u32 s0, s24, s12
	s_addc_u32 s1, s25, s13
	v_fma_f32 v33, -v31, v32, 1.0
	v_fmac_f32_e32 v32, v33, v32
	v_div_scale_f32 v33, vcc, 1.0, v30, 1.0
	v_mul_f32_e32 v50, v33, v32
	v_fma_f32 v51, -v31, v50, v33
	v_fmac_f32_e32 v50, v51, v32
	v_fma_f32 v31, -v31, v50, v33
	v_div_fmas_f32 v31, v31, v32, v50
	v_div_fixup_f32 v30, v31, v30, 1.0
	v_cndmask_b32_e64 v30, v66, v30, s[40:41]
	v_mul_f32_e32 v32, v30, v38
	v_mul_f32_e32 v33, v30, v39
	v_mul_f32_e32 v38, v30, v40
	v_mul_f32_e32 v39, v30, v41
	v_mul_f32_e32 v32, v32, v48
	v_mul_f32_e32 v33, v33, v49
	v_mul_f32_e32 v36, v30, v36
	v_mul_f32_e32 v37, v30, v37
	v_mul_f32_e32 v38, v38, v46
	v_mul_f32_e32 v39, v39, v47
	v_mul_f32_e32 v31, v30, v35
	v_mul_f32_e32 v30, v30, v34
	v_mul_f32_e32 v36, v36, v44
	v_mul_f32_e32 v37, v37, v45
	v_mul_f32_e32 v30, v30, v42
	v_mul_f32_e32 v31, v31, v43
	v_bfe_u32 v34, v39, 16, 1
	v_bfe_u32 v35, v38, 16, 1
	v_bfe_u32 v40, v33, 16, 1
	v_bfe_u32 v41, v32, 16, 1
	v_add3_u32 v41, v32, v41, s7
	v_add3_u32 v40, v33, v40, s7
	v_add3_u32 v32, v38, v35, s7
	v_add3_u32 v33, v39, v34, s7
	v_bfe_u32 v34, v36, 16, 1
	v_bfe_u32 v35, v37, 16, 1
	v_bfe_u32 v38, v30, 16, 1
	v_bfe_u32 v39, v31, 16, 1
	v_add3_u32 v31, v31, v39, s7
	v_add3_u32 v30, v30, v38, s7
	v_add3_u32 v35, v37, v35, s7
	v_add3_u32 v34, v36, v34, s7
	v_lshrrev_b32_e32 v34, 16, v34
	v_lshrrev_b32_e32 v35, 16, v35
	v_lshrrev_b32_e32 v30, 16, v30
	v_lshrrev_b32_e32 v31, 16, v31
	v_and_or_b32 v33, v33, s6, v31
	v_and_or_b32 v32, v32, s6, v30
	v_and_or_b32 v31, v40, s6, v35
	v_and_or_b32 v30, v41, s6, v34
	global_store_dwordx4 v0, v[30:33], s[0:1]
	global_store_dwordx4 v0, v[26:29], s[0:1] offset:1024
	s_and_saveexec_b64 s[0:1], s[38:39]
	s_xor_b64 s[0:1], exec, s[0:1]
	s_cbranch_execz .LBB0_265
	v_add_f32_e32 v23, v165, v163
	v_add_f32_e32 v26, v166, v23
	v_div_scale_f32 v27, s[6:7], v26, v26, 1.0
	v_rcp_f32_e32 v28, v27
	v_lshlrev_b32_e32 v22, 16, v13
	v_and_b32_e32 v23, 0xffff0000, v13
	v_lshlrev_b32_e32 v24, 16, v17
	v_fma_f32 v13, -v27, v28, 1.0
	v_fmac_f32_e32 v28, v13, v28
	v_div_scale_f32 v13, vcc, 1.0, v26, 1.0
	v_and_b32_e32 v25, 0xffff0000, v17
	v_mul_f32_e32 v17, v13, v28
	v_fma_f32 v29, -v27, v17, v13
	v_fmac_f32_e32 v17, v29, v28
	v_fma_f32 v13, -v27, v17, v13
	v_div_fmas_f32 v13, v13, v28, v17
	v_div_fixup_f32 v28, v13, v26, 1.0
	v_lshlrev_b32_e32 v26, 16, v10
	v_and_b32_e32 v27, 0xffff0000, v10
	v_lshlrev_b32_e32 v30, 16, v14
	v_and_b32_e32 v31, 0xffff0000, v14
	v_lshlrev_b32_e32 v10, 16, v11
	v_and_b32_e32 v11, 0xffff0000, v11
	v_lshlrev_b32_e32 v14, 16, v15
	v_and_b32_e32 v15, 0xffff0000, v15
	v_lshlrev_b32_e32 v32, 16, v18
	v_and_b32_e32 v33, 0xffff0000, v18
	v_add_f32_e32 v26, v30, v26
	v_add_f32_e32 v27, v31, v27
	v_lshlrev_b32_e32 v18, 16, v19
	v_and_b32_e32 v19, 0xffff0000, v19
	v_add_f32_e32 v10, v14, v10
	v_add_f32_e32 v11, v15, v11
	v_add_f32_e32 v26, v26, v32
	v_add_f32_e32 v27, v27, v33
	v_add_f32_e32 v10, v10, v18
	v_add_f32_e32 v11, v11, v19
	v_mul_f32_e32 v34, v28, v26
	v_mul_f32_e32 v35, v28, v27
	v_mul_f32_e32 v26, v28, v10
	v_mul_f32_e32 v27, v28, v11
	v_lshlrev_b32_e32 v10, 16, v12
	v_and_b32_e32 v11, 0xffff0000, v12
	v_lshlrev_b32_e32 v12, 16, v16
	v_and_b32_e32 v13, 0xffff0000, v16
	v_lshlrev_b32_e32 v14, 16, v20
	v_and_b32_e32 v15, 0xffff0000, v20
	v_add_f32_e32 v10, v12, v10
	v_add_f32_e32 v11, v13, v11
	v_lshlrev_b32_e32 v12, 16, v21
	v_add_f32_e32 v10, v10, v14
	v_add_f32_e32 v11, v11, v15
	v_and_b32_e32 v13, 0xffff0000, v21
	v_add_f32_e32 v14, v24, v22
	v_add_f32_e32 v15, v25, v23
	v_mul_f32_e32 v10, v28, v10
	v_mul_f32_e32 v11, v28, v11
	v_add_f32_e32 v12, v14, v12
	v_add_f32_e32 v13, v15, v13
	v_mov_b32_e32 v30, v10
	v_mul_f32_e32 v29, v28, v13
	v_mul_f32_e32 v28, v28, v12
	v_mov_b32_e32 v31, v28
	v_mov_b32_e32 v28, v11
	v_mov_b32_e32 v33, v26
	v_mov_b32_e32 v26, v35
	v_mov_b32_e32 v32, v34
; __device__ __forceinline__ void unpack8(const v4u w, float* f) { f[0] = bflo(w.x); f[1] = bfhi(w.x); f[2] = bflo(w.y); f[3] = bfhi(w.y); f[4] = bflo(w.z); f[5] = bfhi(w.z); f[6] = bflo(w.w); f[7] = bfhi(w.w); }
; __device__ __forceinline__ void norm_compute(const NormRow& R, int lane, v4u& ya, v4u& yc) {
;     float fa[8], fc[8];
;     unpack8(R.oa, fa);
;     if (lane < 16) unpack8(R.oc, fc);
;     else { float f0[8], f1[8], f2[8]; unpack8(R.d0, f0); unpack8(R.d1, f1); unpack8(R.d2, f2);
;         const float inv = 1.0f / (R.l0 + R.l1 + R.l2);
; #pragma unroll
;         for (int e = 0; e < 8; ++e) fc[e] = (f0[e] + f1[e] + f2[e]) * inv; }
;     float sa = 0.f, sc = 0.f;
; #pragma unroll
;     for (int e = 0; e < 8; ++e) { sa += fa[e] * fa[e]; sc += fc[e] * fc[e]; }
;     const float s_moba = wave_sum(lane < 32 ? sa : 0.f), s_fox = wave_sum((lane >= 32 ? sa : 0.f) + (lane < 16 ? sc : 0.f)), s_dil = wave_sum(lane >= 16 ? sc : 0.f);
;     const float r_moba = 1.0f / sqrtf(s_moba * (1.0f / 256.0f) + EPS), r_fox = 1.0f / sqrtf(s_fox * (1.0f / 384.0f) + EPS), r_dil = 1.0f / sqrtf(s_dil * (1.0f / 384.0f) + EPS);
;     float ga[8], gc[8];
; #pragma unroll
;     for (int e = 0; e < 8; ++e) { ga[e] = 1.f; gc[e] = 1.f; }
;     if (lane >= 32) unpack8(R.ga, ga);
;     if (lane < 16) unpack8(R.gc, gc);
.LBB0_265:
	s_andn2_saveexec_b64 s[0:1], s[0:1]
	v_lshlrev_b32_e32 v32, 16, v22
	v_and_b32_e32 v26, 0xffff0000, v22
	v_lshlrev_b32_e32 v33, 16, v23
	v_and_b32_e32 v27, 0xffff0000, v23
	v_lshlrev_b32_e32 v30, 16, v24
	v_and_b32_e32 v28, 0xffff0000, v24
	v_lshlrev_b32_e32 v31, 16, v25
	v_and_b32_e32 v29, 0xffff0000, v25
	s_or_b64 exec, exec, s[0:1]
	v_lshlrev_b32_e32 v13, 16, v111
	v_lshlrev_b32_e32 v12, 16, v110
	v_and_b32_e32 v15, 0xffff0000, v111
	v_and_b32_e32 v14, 0xffff0000, v110
	v_mul_f32_e32 v18, v12, v12
	v_mul_f32_e32 v19, v13, v13
	v_mul_f32_e32 v20, v14, v14
	v_mul_f32_e32 v21, v15, v15
	v_mul_f32_e32 v34, v26, v26
	v_fmac_f32_e32 v34, v32, v32
	v_add_f32_e32 v18, v18, v20
	v_lshlrev_b32_e32 v11, 16, v113
	v_lshlrev_b32_e32 v10, 16, v112
	v_fmac_f32_e32 v34, v33, v33
	v_add_f32_e32 v18, v19, v18
	v_and_b32_e32 v17, 0xffff0000, v113
	v_and_b32_e32 v16, 0xffff0000, v112
	v_fmac_f32_e32 v34, v27, v27
	v_mul_f32_e32 v22, v10, v10
	v_mul_f32_e32 v23, v11, v11
	v_add_f32_e32 v18, v21, v18
	v_fmac_f32_e32 v34, v30, v30
	v_mul_f32_e32 v24, v16, v16
	v_mul_f32_e32 v25, v17, v17
	v_add_f32_e32 v18, v22, v18
	v_fmac_f32_e32 v34, v28, v28
	v_add_f32_e32 v18, v24, v18
	v_fmac_f32_e32 v34, v31, v31
	v_add_f32_e32 v18, v23, v18
	v_add_f32_e32 v18, v25, v18
	v_fmac_f32_e32 v34, v29, v29
	v_cndmask_b32_e64 v19, 0, v18, s[40:41]
	v_cndmask_b32_e64 v18, 0, v18, s[36:37]
	v_cndmask_b32_e64 v21, 0, v34, s[34:35]
	v_add_f32_e32 v18, v18, v21
	v_cndmask_b32_e64 v22, 0, v34, s[42:43]
	ds_bpermute_b32 v20, v164, v19
	ds_bpermute_b32 v21, v164, v18
	ds_bpermute_b32 v23, v164, v22
	v_mov_b32_e32 v34, 1.0
	v_mov_b32_e32 v24, 1.0
	s_waitcnt lgkmcnt(2)
	v_add_f32_e32 v19, v19, v20
	s_waitcnt lgkmcnt(1)
	v_add_f32_e32 v18, v18, v21
	s_waitcnt lgkmcnt(0)
	v_add_f32_e32 v22, v22, v23
	ds_bpermute_b32 v20, v162, v19
	ds_bpermute_b32 v21, v162, v18
	ds_bpermute_b32 v23, v162, v22
	v_mov_b32_e32 v25, 1.0
	s_waitcnt lgkmcnt(2)
	v_add_f32_e32 v19, v19, v20
	s_waitcnt lgkmcnt(1)
	v_add_f32_e32 v18, v18, v21
	s_waitcnt lgkmcnt(0)
	v_add_f32_e32 v22, v22, v23
	ds_bpermute_b32 v20, v161, v19
	ds_bpermute_b32 v21, v161, v18
	ds_bpermute_b32 v23, v161, v22
	s_waitcnt lgkmcnt(2)
	v_add_f32_e32 v19, v19, v20
	s_waitcnt lgkmcnt(1)
	v_add_f32_e32 v18, v18, v21
	s_waitcnt lgkmcnt(0)
	v_add_f32_e32 v22, v22, v23
	ds_bpermute_b32 v20, v160, v19
	ds_bpermute_b32 v21, v160, v18
	ds_bpermute_b32 v23, v160, v22
	s_waitcnt lgkmcnt(2)
	v_add_f32_e32 v19, v19, v20
	s_waitcnt lgkmcnt(1)
	v_add_f32_e32 v18, v18, v21
	s_waitcnt lgkmcnt(0)
	v_add_f32_e32 v22, v22, v23
	ds_bpermute_b32 v20, v159, v19
	ds_bpermute_b32 v21, v159, v18
	ds_bpermute_b32 v23, v159, v22
	s_waitcnt lgkmcnt(2)
	v_add_f32_e32 v38, v19, v20
	s_waitcnt lgkmcnt(1)
	v_add_f32_e32 v42, v18, v21
	s_waitcnt lgkmcnt(0)
	v_add_f32_e32 v40, v22, v23
	ds_bpermute_b32 v39, v158, v38
	ds_bpermute_b32 v43, v158, v42
	ds_bpermute_b32 v41, v158, v40
	v_mov_b32_e32 v20, 1.0
	v_mov_b32_e32 v21, 1.0
	v_mov_b32_e32 v18, 1.0
	v_mov_b32_e32 v22, 1.0
	v_mov_b32_e32 v19, 1.0
	v_mov_b32_e32 v23, 1.0
	s_and_saveexec_b64 s[0:1], s[36:37]
	v_lshlrev_b32_e32 v20, 16, v6
	v_and_b32_e32 v24, 0xffff0000, v6
	v_lshlrev_b32_e32 v21, 16, v7
	v_and_b32_e32 v25, 0xffff0000, v7
	v_lshlrev_b32_e32 v18, 16, v8
	v_and_b32_e32 v22, 0xffff0000, v8
	v_lshlrev_b32_e32 v19, 16, v9
	v_and_b32_e32 v23, 0xffff0000, v9
	s_or_b64 exec, exec, s[0:1]
	v_mov_b32_e32 v36, 1.0
	v_mov_b32_e32 v35, 1.0
	v_mov_b32_e32 v37, 1.0
	v_mov_b32_e32 v6, 1.0
	v_mov_b32_e32 v8, 1.0
	v_mov_b32_e32 v7, 1.0
	v_mov_b32_e32 v9, 1.0
	s_and_saveexec_b64 s[0:1], s[34:35]
	v_lshlrev_b32_e32 v34, 16, v2
	v_and_b32_e32 v36, 0xffff0000, v2
	v_lshlrev_b32_e32 v35, 16, v3
	v_and_b32_e32 v37, 0xffff0000, v3
	v_lshlrev_b32_e32 v6, 16, v4
	v_and_b32_e32 v8, 0xffff0000, v4
	v_lshlrev_b32_e32 v7, 16, v5
	v_and_b32_e32 v9, 0xffff0000, v5
	s_or_b64 exec, exec, s[0:1]
	s_waitcnt lgkmcnt(1)
	v_add_f32_e32 v2, v42, v43
	v_fmamk_f32 v2, v2, 0x3b2aaaab, v215
	v_cmp_gt_f32_e32 vcc, s3, v2
	v_mul_f32_e32 v3, 0x4f800000, v2
	s_movk_i32 s7, 0x7fff
	v_cndmask_b32_e32 v2, v2, v3, vcc
	v_sqrt_f32_e32 v3, v2
	s_mov_b32 s6, 0xffff0000
	v_add_u32_e32 v4, -1, v3
	v_fma_f32 v5, -v4, v3, v2
	v_cmp_ge_f32_e64 s[0:1], 0, v5
	v_add_u32_e32 v5, 1, v3
	s_nop 0
	v_cndmask_b32_e64 v4, v3, v4, s[0:1]
	v_fma_f32 v3, -v5, v3, v2
	v_cmp_lt_f32_e64 s[0:1], 0, v3
	s_nop 1
	v_cndmask_b32_e64 v3, v4, v5, s[0:1]
	v_mul_f32_e32 v4, 0x37800000, v3
	v_cndmask_b32_e32 v3, v3, v4, vcc
	v_cmp_class_f32_e32 vcc, v2, v216
	s_nop 1
	v_cndmask_b32_e32 v2, v3, v2, vcc
	v_div_scale_f32 v3, s[0:1], v2, v2, 1.0
	v_rcp_f32_e32 v4, v3
	s_nop 0
	v_fma_f32 v5, -v3, v4, 1.0
	v_fmac_f32_e32 v4, v5, v4
	v_div_scale_f32 v5, vcc, 1.0, v2, 1.0
	v_mul_f32_e32 v42, v5, v4
	v_fma_f32 v43, -v3, v42, v5
	v_fmac_f32_e32 v42, v43, v4
	v_fma_f32 v3, -v3, v42, v5
	v_div_fmas_f32 v3, v3, v4, v42
	v_div_fixup_f32 v42, v3, v2, 1.0
	s_waitcnt lgkmcnt(0)
; __device__ __forceinline__ unsigned pk2(float lo, float hi) { return f2bf(lo) | (f2bf(hi) << 16); }
; __device__ __forceinline__ void unpack8(const v4u w, float* f) { f[0] = bflo(w.x); f[1] = bfhi(w.x); f[2] = bflo(w.y); f[3] = bfhi(w.y); f[4] = bflo(w.z); f[5] = bfhi(w.z); f[6] = bflo(w.w); f[7] = bfhi(w.w); }
; __device__ __forceinline__ void norm_compute(const NormRow& R, int lane, v4u& ya, v4u& yc) {
;     ...
;     const float r_moba = 1.0f / sqrtf(s_moba * (1.0f / 256.0f) + EPS), r_fox = 1.0f / sqrtf(s_fox * (1.0f / 384.0f) + EPS), r_dil = 1.0f / sqrtf(s_dil * (1.0f / 384.0f) + EPS);
;     float ga[8], gc[8];
; #pragma unroll
;     for (int e = 0; e < 8; ++e) { ga[e] = 1.f; gc[e] = 1.f; }
;     if (lane >= 32) unpack8(R.ga, ga);
;     if (lane < 16) unpack8(R.gc, gc);
;     const float ra = lane < 32 ? r_moba : r_fox, rc = lane < 16 ? r_fox : r_dil;
;     ya.x = pk2(fa[0] * ra * ga[0], fa[1] * ra * ga[1]); ya.y = pk2(fa[2] * ra * ga[2], fa[3] * ra * ga[3]); ya.z = pk2(fa[4] * ra * ga[4], fa[5] * ra * ga[5]); ya.w = pk2(fa[6] * ra * ga[6], fa[7] * ra * ga[7]);
;     yc.x = pk2(fc[0] * rc * gc[0], fc[1] * rc * gc[1]); yc.y = pk2(fc[2] * rc * gc[2], fc[3] * rc * gc[3]); yc.z = pk2(fc[4] * rc * gc[4], fc[5] * rc * gc[5]); yc.w = pk2(fc[6] * rc * gc[6], fc[7] * rc * gc[7]);
; }
	v_add_f32_e32 v2, v40, v41
	v_fmamk_f32 v2, v2, 0x3b2aaaab, v215
	v_cmp_gt_f32_e32 vcc, s3, v2
	v_mul_f32_e32 v3, 0x4f800000, v2
	s_nop 0
	v_cndmask_b32_e32 v2, v2, v3, vcc
	v_sqrt_f32_e32 v3, v2
	s_nop 0
	v_add_u32_e32 v4, -1, v3
	v_fma_f32 v5, -v4, v3, v2
	v_cmp_ge_f32_e64 s[0:1], 0, v5
	v_add_u32_e32 v5, 1, v3
	s_nop 0
	v_cndmask_b32_e64 v4, v3, v4, s[0:1]
	v_fma_f32 v3, -v5, v3, v2
	v_cmp_lt_f32_e64 s[0:1], 0, v3
	s_nop 1
	v_cndmask_b32_e64 v3, v4, v5, s[0:1]
	v_mul_f32_e32 v4, 0x37800000, v3
	v_cndmask_b32_e32 v3, v3, v4, vcc
	v_cmp_class_f32_e32 vcc, v2, v216
	s_nop 1
	v_cndmask_b32_e32 v2, v3, v2, vcc
	v_div_scale_f32 v3, s[0:1], v2, v2, 1.0
	v_rcp_f32_e32 v4, v3
	s_nop 0
	v_fma_f32 v5, -v3, v4, 1.0
	v_fmac_f32_e32 v4, v5, v4
	v_div_scale_f32 v5, vcc, 1.0, v2, 1.0
	v_mul_f32_e32 v40, v5, v4
	v_fma_f32 v41, -v3, v40, v5
	v_fmac_f32_e32 v40, v41, v4
	v_fma_f32 v3, -v3, v40, v5
	v_div_fmas_f32 v3, v3, v4, v40
	v_div_fixup_f32 v2, v3, v2, 1.0
	v_cndmask_b32_e64 v2, v2, v42, s[34:35]
	v_mul_f32_e32 v4, v26, v2
	v_mul_f32_e32 v5, v27, v2
	v_mul_f32_e32 v28, v28, v2
	v_mul_f32_e32 v29, v29, v2
	v_mul_f32_e32 v4, v4, v36
	v_mul_f32_e32 v5, v5, v37
	v_mul_f32_e32 v26, v32, v2
	v_mul_f32_e32 v27, v33, v2
	v_mul_f32_e32 v8, v28, v8
	v_mul_f32_e32 v9, v29, v9
	v_mul_f32_e32 v3, v31, v2
	v_mul_f32_e32 v2, v30, v2
	v_mul_f32_e32 v26, v26, v34
	v_mul_f32_e32 v27, v27, v35
	v_mul_f32_e32 v2, v2, v6
	v_mul_f32_e32 v3, v3, v7
	v_bfe_u32 v6, v9, 16, 1
	v_bfe_u32 v7, v8, 16, 1
	v_bfe_u32 v28, v5, 16, 1
	v_bfe_u32 v29, v4, 16, 1
	v_add3_u32 v29, v4, v29, s7
	v_add3_u32 v28, v5, v28, s7
	v_add3_u32 v4, v8, v7, s7
	v_add3_u32 v5, v9, v6, s7
	v_bfe_u32 v6, v26, 16, 1
	v_bfe_u32 v8, v2, 16, 1
	v_add3_u32 v2, v2, v8, s7
	v_add3_u32 v6, v26, v6, s7
	v_bfe_u32 v7, v27, 16, 1
	v_bfe_u32 v9, v3, 16, 1
	v_lshrrev_b32_e32 v6, 16, v6
	v_lshrrev_b32_e32 v2, 16, v2
	v_add3_u32 v3, v3, v9, s7
	v_add3_u32 v7, v27, v7, s7
	v_and_or_b32 v4, v4, s6, v2
	v_and_or_b32 v2, v29, s6, v6
	v_add_f32_e32 v6, v38, v39
	v_lshrrev_b32_e32 v7, 16, v7
	v_lshrrev_b32_e32 v3, 16, v3
	v_fmamk_f32 v6, v6, 0x3b800000, v215
	v_and_or_b32 v5, v5, s6, v3
	v_and_or_b32 v3, v28, s6, v7
	v_cmp_gt_f32_e32 vcc, s3, v6
	v_mul_f32_e32 v7, 0x4f800000, v6
	s_nop 0
	v_cndmask_b32_e32 v6, v6, v7, vcc
	v_sqrt_f32_e32 v7, v6
	s_nop 0
	v_add_u32_e32 v8, -1, v7
	v_fma_f32 v9, -v8, v7, v6
	v_cmp_ge_f32_e64 s[0:1], 0, v9
	v_add_u32_e32 v9, 1, v7
	s_nop 0
	v_cndmask_b32_e64 v8, v7, v8, s[0:1]
	v_fma_f32 v7, -v9, v7, v6
	v_cmp_lt_f32_e64 s[0:1], 0, v7
	s_nop 1
	v_cndmask_b32_e64 v7, v8, v9, s[0:1]
	v_mul_f32_e32 v8, 0x37800000, v7
	v_cndmask_b32_e32 v7, v7, v8, vcc
	v_cmp_class_f32_e32 vcc, v6, v216
	s_nop 1
	v_cndmask_b32_e32 v6, v7, v6, vcc
	v_div_scale_f32 v7, s[0:1], v6, v6, 1.0
	v_rcp_f32_e32 v8, v7
	s_add_u32 s0, s24, s8
	s_addc_u32 s1, s25, s9
	v_fma_f32 v9, -v7, v8, 1.0
	v_fmac_f32_e32 v8, v9, v8
	v_div_scale_f32 v9, vcc, 1.0, v6, 1.0
	v_mul_f32_e32 v26, v9, v8
	v_fma_f32 v27, -v7, v26, v9
	v_fmac_f32_e32 v26, v27, v8
	v_fma_f32 v7, -v7, v26, v9
	v_div_fmas_f32 v7, v7, v8, v26
	v_div_fixup_f32 v6, v7, v6, 1.0
	v_cndmask_b32_e64 v6, v42, v6, s[40:41]
	v_mul_f32_e32 v8, v6, v14
	v_mul_f32_e32 v9, v6, v15
	v_mul_f32_e32 v14, v6, v16
	v_mul_f32_e32 v15, v6, v17
	v_mul_f32_e32 v8, v8, v24
	v_mul_f32_e32 v9, v9, v25
	v_mul_f32_e32 v12, v6, v12
	v_mul_f32_e32 v13, v6, v13
	v_mul_f32_e32 v14, v14, v22
	v_mul_f32_e32 v15, v15, v23
	v_mul_f32_e32 v7, v6, v11
	v_mul_f32_e32 v6, v6, v10
	v_mul_f32_e32 v12, v12, v20
	v_mul_f32_e32 v13, v13, v21
	v_mul_f32_e32 v6, v6, v18
	v_mul_f32_e32 v7, v7, v19
	v_bfe_u32 v10, v15, 16, 1
	v_bfe_u32 v11, v14, 16, 1
	v_bfe_u32 v16, v9, 16, 1
	v_bfe_u32 v17, v8, 16, 1
	v_add3_u32 v17, v8, v17, s7
	v_add3_u32 v16, v9, v16, s7
	v_add3_u32 v8, v14, v11, s7
	v_add3_u32 v9, v15, v10, s7
	v_bfe_u32 v10, v12, 16, 1
	v_bfe_u32 v11, v13, 16, 1
	v_bfe_u32 v14, v6, 16, 1
	v_bfe_u32 v15, v7, 16, 1
	v_add3_u32 v7, v7, v15, s7
	v_add3_u32 v6, v6, v14, s7
	v_add3_u32 v11, v13, v11, s7
	v_add3_u32 v10, v12, v10, s7
	v_lshrrev_b32_e32 v10, 16, v10
	v_lshrrev_b32_e32 v11, 16, v11
	v_lshrrev_b32_e32 v6, 16, v6
	v_lshrrev_b32_e32 v7, 16, v7
	v_and_or_b32 v9, v9, s6, v7
	v_and_or_b32 v8, v8, s6, v6
	v_and_or_b32 v7, v16, s6, v11
	v_and_or_b32 v6, v17, s6, v10
	global_store_dwordx4 v0, v[6:9], s[0:1]
	global_store_dwordx4 v0, v[2:5], s[0:1] offset:1024
	s_mov_b64 s[0:1], 0

;     __device__ __forceinline__ void init(f32x16& c0, f32x16& c1, int t) const {
;         float base = slope2 * ((float)(64 * t + 4 * hi) - tqf);
;         if (t < nb0) { if (!((selmask >> (t >> 2)) & 1u)) base = ATT_NEG; }
;         const float d32 = 32.0f * slope2;
; #pragma unroll
;         for (int i = 0; i < 8; ++i) { const int r = 2 * i; const f32x2_t kc = (f32x2_t){slope2 * (float)((r & 3) + 8 * (r >> 2)), slope2 * (float)(((r + 1) & 3) + 8 * ((r + 1) >> 2))};
;             const f32x2_t p = kc + base, q = p + d32; c0[r] = p[0]; c0[r + 1] = p[1]; c1[r] = q[0]; c1[r + 1] = q[1]; }
; __device__ __forceinline__ void moba_unit(Frame& F, const AttnBufs& A, int b, int h, int qb) {
;     ...
;     att::BiasMoba B; B.slope2 = exp2f(-8.0f * (float)(7 + h) / 10.0f) * LOG2E; B.qrel = w * 32 + r32; B.tqf = (float)(qb * 256 + B.qrel); B.hi = hi; B.w = w; B.nb0 = 4 * qb; B.selmask = selmask; B.u = 32 * (w & 1) + r32 - 4 * hi;
;     att::UnitIO io; io.Q = Qw; io.qstride = DM; io.K0 = A.K + bo + (size_t)b * SEQ * DM + h * 64; io.V0 = A.V + bo + (size_t)b * SEQ * DM + h * 64; io.kstride = DM;
;     io.O = A.O + bo + row0 * DM + h * 64; io.ostride = DM; io.L = nullptr; io.lstride = 0; io.norm = true;
.LBB0_274:
	s_and_b64 vcc, exec, s[0:1]
	s_cbranch_vccz .LBB0_316
	v_readlane_b32 s0, v254, 27
	s_cmp_gt_i32 s0, 0
	s_mov_b64 s[0:1], -1
	s_cbranch_scc0 .LBB0_394
	v_readlane_b32 s100, v253, 15
	v_and_b32_e32 v248, 31, v214
	v_lshlrev_b32_e32 v248, 7, v248
	v_lshrrev_b32_e32 v249, 5, v214
	v_bfe_u32 v250, v214, 1, 3
	v_xor_b32_e32 v251, v249, v250
	v_lshl_add_u32 v240, v251, 4, v248
	v_add_u32_e32 v251, 2, v249
	v_xor_b32_e32 v251, v251, v250
	v_lshl_add_u32 v241, v251, 4, v248
	v_add_u32_e32 v251, 4, v249
	v_xor_b32_e32 v251, v251, v250
	v_lshl_add_u32 v242, v251, 4, v248
	v_add_u32_e32 v251, 6, v249
	v_xor_b32_e32 v251, v251, v250
	v_lshl_add_u32 v243, v251, 4, v248
	v_lshrrev_b32_e32 v248, 3, v214
	s_lshl_b32 s101, s100, 3
	v_add_u32_e32 v248, s101, v248
	v_sub_u32_e32 v246, v248, v214
	v_bfe_u32 v249, v248, 1, 3
	v_and_b32_e32 v250, 7, v214
	v_xor_b32_e32 v249, v250, v249
	v_subrev_u32_e32 v249, s100, v249
	v_lshlrev_b32_e32 v247, 4, v249
	v_lshl_add_u32 v244, v246, 11, v247
	v_ashrrev_i32_e32 v245, 31, v244
	v_readlane_b32 s0, v254, 13
	s_mov_b32 s6, s0
	s_ashr_i32 s34, s0, 5
	s_and_b32 s0, s0, 24
	s_sub_i32 s0, 0xffffffc8, s0
	v_cvt_f32_i32_e32 v0, s0
	v_readlane_b32 s1, v254, 14
	s_and_b32 s0, s6, 31
	s_mov_b32 s2, 0x41200000
	v_writelane_b32 v254, s0, 30
	s_mov_b32 s3, 0x41300000
	s_waitcnt vmcnt(0)
	v_div_scale_f32 v2, s[0:1], s2, s2, v0
	v_rcp_f32_e32 v3, v2
	s_and_b32 s0, s6, 7
	v_writelane_b32 v254, s0, 31
	s_xor_b32 s0, s0, 15
	v_fma_f32 v4, -v2, v3, 1.0
	v_fmac_f32_e32 v3, v4, v3
	v_div_scale_f32 v4, vcc, v0, s2, v0
	v_mul_f32_e32 v5, v4, v3
	v_fma_f32 v6, -v2, v5, v4
	v_fmac_f32_e32 v5, v6, v3
	v_fma_f32 v2, -v2, v5, v4
	v_div_fmas_f32 v2, v2, v3, v5
	v_writelane_b32 v254, s0, 33
	v_div_fixup_f32 v0, v2, s2, v0
	s_mov_b32 s0, 0xc2fc0000
	v_cmp_gt_f32_e32 vcc, s0, v0
	s_ashr_i32 s35, s34, 31
	s_bfe_u32 s4, s6, 0x20003
	v_cndmask_b32_e32 v2, 0, v224, vcc
	v_add_f32_e32 v0, v0, v2
	v_exp_f32_e32 v0, v0
	s_lshl_b64 s[6:7], s[34:35], 12
	s_and_b64 s[0:1], vcc, exec
	s_cselect_b32 s0, 0xffffffc0, 0
	v_ldexp_f32 v0, v0, s0
	s_lshl_b32 s0, s34, 6
	v_mul_f32_e32 v115, 0x3fb8aa3b, v0
	s_or_b32 s21, s0, s4
	s_mov_b32 s0, 2.0
	v_mov_b32_e32 v0, v115
	s_mov_b32 s1, 0x40400000
	v_mul_f32_e32 v118, s0, v0
	v_mul_f32_e32 v119, s1, v0
	s_mov_b32 s0, 0x41000000
	s_mov_b32 s1, 0x41100000
	v_mul_f32_e32 v120, s0, v0
	v_mul_f32_e32 v121, s1, v0
	s_mov_b32 s0, 0x41800000
	s_mov_b32 s1, 0x41880000
	v_mul_f32_e32 v124, s0, v0
	v_mul_f32_e32 v125, s1, v0
	s_mov_b32 s0, 0x41900000
	s_mov_b32 s1, 0x41980000
	v_mul_f32_e32 v126, s0, v0
	v_mul_f32_e32 v127, s1, v0
	s_mov_b32 s0, 0x41c00000
	s_mov_b32 s1, 0x41c80000
	v_mul_f32_e32 v128, s0, v0
	v_mul_f32_e32 v129, s1, v0
	s_mov_b32 s0, 0x41d00000
	v_mul_f32_e32 v122, s2, v0
	v_mul_f32_e32 v123, s3, v0
	s_mov_b32 s1, 0x41d80000
	s_lshl_b32 s2, s72, 5
	v_mul_f32_e32 v140, s0, v0
	v_mul_f32_e32 v141, s1, v0
	s_ashr_i32 s0, s2, 31
	v_writelane_b32 v254, s72, 35
	s_add_u32 s1, s6, s2
	v_writelane_b32 v254, s1, 36
	v_writelane_b32 v254, s6, 38
	s_addc_u32 s0, s7, s0
	s_mul_i32 s1, s34, 0x1800000
	v_writelane_b32 v254, s7, 39
	v_writelane_b32 v254, s0, 40
	s_mul_hi_i32 s0, s34, 0x1800000
	s_add_u32 s20, s74, s1
	s_addc_u32 s22, s75, s0
	s_add_u32 s0, s20, 0x8000000
	s_addc_u32 s1, s22, 0
	s_lshl_b32 s33, s4, 7
	v_writelane_b32 v254, s0, 42
	s_add_u32 s0, s0, s33
	v_writelane_b32 v254, s0, 43
	v_writelane_b32 v254, s1, 45
	s_addc_u32 s0, s1, 0
	v_and_b32_e32 v146, 31, v232
	v_writelane_b32 v254, s0, 46
	v_or_b32_e32 v143, s2, v146
	v_writelane_b32 v254, s2, 48
	v_and_or_b32 v147, s2, 32, v146
	s_add_u32 s2, s20, 0x8800000
	s_addc_u32 s3, s22, 0
	s_lshl_b64 s[0:1], s[34:35], 23
	v_writelane_b32 v254, s2, 49
	s_add_u32 s2, s2, s0
	v_writelane_b32 v254, s3, 50
	s_addc_u32 s3, s3, s1
	s_add_u32 s4, s2, s33
	v_writelane_b32 v254, s2, 51
	s_addc_u32 s5, s3, 0
	v_lshlrev_b32_e32 v130, 3, v232
	v_writelane_b32 v254, s3, 52
	s_add_u32 s2, s20, 0x9000000
	s_addc_u32 s3, s22, 0
	s_add_u32 s0, s2, s0
	s_addc_u32 s1, s3, s1
	v_writelane_b32 v254, s2, 53
	s_add_u32 s30, s0, s33
	v_writelane_b32 v254, s3, 54
	s_addc_u32 s31, s1, 0
	s_ashr_i32 s73, s28, 7
	v_writelane_b32 v254, s0, 55
	s_add_u32 s2, s20, 0x9800000
	v_writelane_b32 v254, s1, 57
	s_addc_u32 s3, s22, 0
	v_writelane_b32 v254, s2, 59
	s_add_u32 s2, s2, s33
	v_lshrrev_b32_e32 v131, 5, v194
	v_and_b32_e32 v144, 24, v130
	v_lshlrev_b32_e32 v0, 1, v232
	v_lshlrev_b32_e32 v7, 4, v232
	s_addc_u32 s25, s3, 0
	s_lshl_b64 s[22:23], s[34:35], 25
	v_lshlrev_b32_e32 v6, 4, v146
;     __device__ __forceinline__ void init(f32x16& c0, f32x16& c1, int t) const {
;     ...
;         if (t - nb0 == (w >> 1)) {
; #pragma unroll
;             for (int r = 0; r < 16; ++r) { const int ko = (r & 3) + 8 * (r >> 2); if (ko > u) c0[r] = ATT_NEG; if (ko > u - 32) c1[r] = ATT_NEG; }
; template <class BIAS>
; __device__ __forceinline__ void attn_tiles(char* shm, const UnitIO& io, int t_begin, int t_end, const BIAS& B, int tid) {
;     const int lane = tid & 63, r32 = lane & 31, hi = lane >> 5; const int wid = __builtin_amdgcn_readfirstlane(tid >> 6);
;     const unsigned lds0 = (unsigned)(uintptr_t)shm;
;     const bf16* ksrc = io.K0 + (long)lane * io.kstride + wid * 8;
;     const bf16* vsrc = io.V0 + (long)(16 * (wid & 3) + (lane >> 2)) * io.kstride + (wid >> 2) * 32 + (lane & 3) * 8;
;     const unsigned kdst = lds0 + LDS_K + wid * 1024, vdst = lds0 + LDS_V + wid * 1024;
;     const long tstep = 64 * io.kstride;
;     ...
;     const lds_cptr shm3 = (lds_cptr)shm;
;     const lds_cptr kp0 = shm3 + LDS_K + hi * 1024 + r32 * 16;
;     const lds_cptr vp0 = shm3 + LDS_V + ((lane >> 4) & 1) * 32 + (lane & 3) * 8 + (4 * hi + ((lane & 15) >> 2)) * 64;
;     float* wsf = (float*)(shm + LDS_WS) + wid * 64;
	v_and_or_b32 v0, v0, 32, v144
	v_lshlrev_b32_e32 v179, 8, v131
	v_and_b32_e32 v7, 0xc0, v7
	s_or_b32 s20, s22, s33
	v_or3_b32 v180, v0, v179, v7
	v_lshl_or_b32 v181, v131, 10, v6
	v_lshlrev_b32_e32 v6, 2, v194
	v_mov_b32_e32 v7, v1
	s_add_u32 s36, s74, s20
	v_bfe_u32 v3, v232, 5, 1
	v_lshl_add_u64 v[6:7], s[74:75], 0, v[6:7]
	s_mov_b64 s[0:1], 0x3700000
	s_addc_u32 s37, s75, s23
	v_lshlrev_b32_e32 v145, 2, v3
	v_lshl_add_u64 v[158:159], v[6:7], 0, s[0:1]
	s_add_u32 s20, s74, s33
	v_and_b32_e32 v6, 3, v232
	v_sub_u32_e32 v5, v147, v145
	v_writelane_b32 v255, s74, 1
	s_addc_u32 s33, s75, 0
	v_lshlrev_b32_e32 v6, 4, v6
	v_mov_b32_e32 v7, v1
	s_add_u32 s22, s20, s22
	v_cmp_gt_i32_e64 s[34:35], 57, v5
	v_lshl_add_u64 v[6:7], s[36:37], 0, v[6:7]
	v_cmp_gt_i32_e64 s[36:37], 58, v5
	v_cmp_gt_i32_e64 s[28:29], 56, v5
	s_addc_u32 s23, s33, s23
	s_and_b64 s[40:41], s[36:37], s[34:35]
	v_cmp_gt_i32_e64 s[26:27], 51, v5
	s_and_b64 s[42:43], s[40:41], s[28:29]
	v_cmp_gt_i32_e64 s[46:47], 50, v5
	s_and_b64 s[44:45], s[42:43], s[26:27]
	v_cmp_gt_i32_e64 s[48:49], 49, v5
	s_and_b64 s[46:47], s[44:45], s[46:47]
	v_cmp_gt_i32_e64 s[50:51], 48, v5
	s_and_b64 s[48:49], s[46:47], s[48:49]
	v_cmp_gt_i32_e64 s[16:17], 43, v5
	s_and_b64 s[50:51], s[48:49], s[50:51]
	v_cmp_gt_i32_e64 s[12:13], 42, v5
	s_and_b64 s[52:53], s[50:51], s[16:17]
	v_cmp_gt_i32_e64 s[10:11], 41, v5
	s_and_b64 s[54:55], s[52:53], s[12:13]
	v_lshlrev_b32_e32 v0, 11, v194
	v_cmp_gt_i32_e64 s[6:7], 40, v5
	s_and_b64 s[56:57], s[54:55], s[10:11]
	v_lshl_add_u64 v[156:157], s[4:5], 0, v[0:1]
	v_cmp_gt_i32_e64 s[4:5], 35, v5
	v_cmp_gt_i32_e64 s[68:69], 26, v5
	v_cmp_gt_i32_e64 s[38:39], 27, v5
	s_and_b64 s[58:59], s[56:57], s[6:7]
	v_cmp_gt_i32_e64 s[62:63], 34, v5
	v_cmp_gt_i32_e64 s[18:19], 25, v5
	s_and_b64 s[60:61], s[58:59], s[4:5]
	s_and_b64 s[68:69], s[38:39], s[68:69]
	v_cmp_gt_i32_e64 s[0:1], 33, v5
	v_cmp_gt_i32_e64 s[14:15], 24, v5
	s_and_b64 s[62:63], s[60:61], s[62:63]
	s_and_b64 s[70:71], s[68:69], s[18:19]
	v_cmp_gt_i32_e32 vcc, 32, v5
	v_cmp_gt_i32_e64 s[8:9], 19, v5
	s_and_b64 s[64:65], s[62:63], s[0:1]
	s_and_b64 s[18:19], s[70:71], s[14:15]
	v_writelane_b32 v255, s75, 2
	s_and_b64 s[66:67], s[64:65], vcc
	s_and_b64 s[74:75], s[18:19], s[8:9]
	v_cmp_gt_i32_e32 vcc, 18, v5
	s_and_b64 s[76:77], s[74:75], vcc
	v_cmp_gt_i32_e32 vcc, 17, v5
	s_and_b64 s[78:79], s[76:77], vcc
	v_cmp_gt_i32_e32 vcc, 16, v5
	s_and_b64 s[80:81], s[78:79], vcc
	v_cmp_gt_i32_e32 vcc, 11, v5
	s_and_b64 s[82:83], s[80:81], vcc
	v_cmp_gt_i32_e32 vcc, 10, v5
	v_writelane_b32 v254, s2, 61
	s_and_b64 s[84:85], s[82:83], vcc
	v_cmp_gt_i32_e32 vcc, 9, v5
	v_writelane_b32 v254, s3, 63
	s_and_b64 s[2:3], s[84:85], vcc
	v_cmp_gt_i32_e32 vcc, 8, v5
	s_and_b64 s[88:89], s[2:3], vcc
	v_cmp_gt_i32_e32 vcc, 3, v5
	v_lshrrev_b32_e32 v182, 3, v194
	s_and_b64 s[90:91], s[88:89], vcc
	v_cmp_gt_i32_e32 vcc, 2, v5
	v_lshl_add_u64 v[8:9], s[22:23], 0, v[0:1]
	v_or_b32_e32 v184, 8, v182
	v_or_b32_e32 v186, 16, v182
	v_or_b32_e32 v188, 24, v182
	s_mov_b64 s[22:23], 0x9060000
	s_and_b64 s[92:93], s[90:91], vcc
	v_cmp_gt_i32_e32 vcc, 1, v5
	v_cmp_gt_u32_e64 s[4:5], 32, v194
	v_mul_f32_e32 v116, 0x42000000, v115
	v_lshlrev_b32_e32 v2, 10, v146
	v_lshlrev_b32_e32 v4, 3, v3
	v_lshrrev_b32_e32 v178, 2, v194
	v_lshlrev_b32_e32 v0, 10, v182
	v_lshlrev_b32_e32 v10, 10, v184
	v_lshlrev_b32_e32 v12, 10, v186
	v_lshlrev_b32_e32 v14, 10, v188
	v_lshl_add_u64 v[164:165], v[6:7], 0, s[22:23]
	s_mov_b64 s[22:23], 0x8860000
	s_and_b64 s[94:95], s[92:93], vcc
	v_cmp_gt_i32_e32 vcc, 0, v5
	s_movk_i32 s0, 0x400
	v_writelane_b32 v255, s4, 3
	v_mul_f32_e32 v114, 0, v115
	v_lshlrev_b32_e32 v142, 10, v194
	v_lshlrev_b32_e32 v132, 11, v146
	v_mov_b32_e32 v133, v1
	v_lshlrev_b32_e32 v154, 3, v131
	v_mov_b32_e32 v195, v1
	v_lshlrev_b32_e32 v155, 4, v131
	v_and_b32_e32 v160, 56, v130
	v_lshlrev_b32_e32 v183, 7, v182
	v_lshlrev_b32_e32 v185, 7, v184
	v_lshlrev_b32_e32 v187, 7, v186
	v_lshlrev_b32_e32 v189, 7, v188
	v_mov_b32_e32 v162, v116
	v_mov_b32_e32 v163, v116
	v_lshl_add_u32 v161, v232, 2, v239
	v_lshlrev_b32_e32 v174, 5, v3
	v_lshlrev_b32_e32 v175, 10, v178
	v_lshl_add_u64 v[166:167], v[8:9], 0, s[22:23]
	v_lshlrev_b32_e32 v168, 1, v2
	v_lshlrev_b32_e32 v170, 1, v4
	v_lshlrev_b32_e32 v0, 1, v0
	v_lshlrev_b32_e32 v134, 1, v10
	v_lshlrev_b32_e32 v136, 1, v12
	v_lshlrev_b32_e32 v138, 1, v14
	s_and_b64 s[96:97], s[94:95], vcc
	s_sub_i32 s72, 0, s73
	v_cmp_gt_i32_e64 s[0:1], s0, v232
	v_cmp_gt_i32_e64 s[6:7], 59, v5
	v_writelane_b32 v255, s5, 4
	s_mov_b64 s[4:5], -1
	s_branch .LBB0_278

; #define LAS __attribute__((address_space(3)))
; __device__ __forceinline__ void moba_unit(Frame& F, const AttnBufs& A, int b, int h, int qb) {
;     ...
;     for (int j = 0; j < qb; ++j) {
;         float dot = 0.f;
; #pragma unroll
;         for (int d0 = 0; d0 < 4; ++d0) { const f32x4 ka = *(const LAS f32x4*)(KM + j * 64 + d0 * 16 + hi * 8), kb = *(const LAS f32x4*)(KM + j * 64 + d0 * 16 + hi * 8 + 4);
; #pragma unroll
;             for (int e = 0; e < 4; ++e) { dot += qf[8 * d0 + e] * ka[e]; dot += qf[8 * d0 + 4 + e] * kb[e]; } }
;         { auto rr = __builtin_amdgcn_permlane32_swap(__float_as_uint(dot), __float_as_uint(dot), false, false); dot = __uint_as_float(rr[0]) + __uint_as_float(rr[1]); }
;         if (dot > g0) { g2 = g1; i2 = i1; g1 = g0; i1 = i0; g0 = dot; i0 = j; } else if (dot > g1) { g2 = g1; i2 = i1; g1 = dot; i1 = j; } else if (dot > g2) { g2 = dot; i2 = j; }
;     }
.LBB0_285:
	v_add_u32_e32 v48, s23, v174
	v_add_u32_e32 v49, 0x18800, v48
	ds_read_b128 v[98:101], v49
	ds_read_b128 v[102:105], v49 offset:16
	ds_read_b128 v[82:85], v49 offset:64
	ds_read_b128 v[86:89], v49 offset:80
	ds_read_b128 v[90:93], v49 offset:128
	ds_read_b128 v[94:97], v49 offset:144
	ds_read_b128 v[40:43], v49 offset:192
	ds_read_b128 v[44:47], v49 offset:208
	s_waitcnt lgkmcnt(7)
	v_fma_f32 v50, v98, v18, 0
	s_waitcnt lgkmcnt(6)
	v_fmac_f32_e32 v50, v102, v20
	v_fmac_f32_e32 v50, v99, v14
	v_fmac_f32_e32 v50, v103, v16
	v_fmac_f32_e32 v50, v100, v19
	v_fmac_f32_e32 v50, v104, v21
	v_fmac_f32_e32 v50, v101, v15
	v_fmac_f32_e32 v50, v105, v17
	s_waitcnt lgkmcnt(5)
	v_fmac_f32_e32 v50, v82, v22
	s_waitcnt lgkmcnt(4)
	v_fmac_f32_e32 v50, v86, v26
	v_fmac_f32_e32 v50, v83, v23
	v_fmac_f32_e32 v50, v87, v12
	v_fmac_f32_e32 v50, v84, v24
	v_fmac_f32_e32 v50, v88, v27
	v_fmac_f32_e32 v50, v85, v25
	v_fmac_f32_e32 v50, v89, v13
	s_waitcnt lgkmcnt(3)
	v_fmac_f32_e32 v50, v90, v28
	s_waitcnt lgkmcnt(2)
	v_fmac_f32_e32 v50, v94, v32
	v_fmac_f32_e32 v50, v91, v29
	v_fmac_f32_e32 v50, v95, v33
	v_fmac_f32_e32 v50, v92, v30
	v_fmac_f32_e32 v50, v96, v34
	v_fmac_f32_e32 v50, v93, v31
	v_fmac_f32_e32 v50, v97, v35
	s_waitcnt lgkmcnt(1)
	v_mov_b32_e32 v49, v40
	s_waitcnt lgkmcnt(0)
	v_mov_b32_e32 v48, v44
	v_mul_f32_e32 v48, v48, v6
	v_mul_f32_e32 v49, v49, v7
	s_nop 0
	v_add_f32_e32 v40, v49, v50
	v_add_f32_e32 v44, v48, v40
	v_mov_b32_e32 v40, v45
	v_mul_f32_e32 v40, v40, v8
	v_mul_f32_e32 v41, v41, v9
	s_nop 0
	v_add_f32_e32 v41, v41, v44
	v_add_f32_e32 v44, v40, v41
	v_mov_b32_e32 v40, v46
	v_mov_b32_e32 v41, v42
	v_mul_f32_e32 v40, v40, v10
	v_mul_f32_e32 v41, v41, v11
	v_mov_b32_e32 v42, v47
	v_add_f32_e32 v41, v41, v44
	v_add_f32_e32 v44, v40, v41
	v_mul_f32_e32 v40, v42, v2
	v_mul_f32_e32 v41, v43, v3
	s_nop 0
	v_add_f32_e32 v41, v41, v44
	v_add_f32_e32 v40, v40, v41
	v_mov_b32_e32 v41, v40
	s_nop 1
	v_permlane32_swap_b32_e32 v40, v41
	v_add_f32_e32 v40, v40, v41
	v_cmp_ngt_f32_e32 vcc, v40, v37
	v_mov_b32_e32 v41, s26
	s_and_saveexec_b64 s[12:13], vcc
	s_cbranch_execz .LBB0_291
	v_cmp_ngt_f32_e32 vcc, v40, v36
	v_mov_b32_e32 v42, s26
	s_and_saveexec_b64 s[14:15], vcc
	s_cbranch_execz .LBB0_290
	v_cmp_gt_f32_e32 vcc, v40, v39
	s_and_saveexec_b64 s[16:17], vcc
	v_mov_b32_e32 v38, s26
	v_mov_b32_e32 v39, v40
	s_or_b64 exec, exec, s[16:17]
	v_mov_b32_e32 v42, v4
	v_mov_b32_e32 v40, v36
	v_mov_b32_e32 v36, v39
	v_mov_b32_e32 v4, v38

; #define LAS __attribute__((address_space(3)))
; __device__ __forceinline__ void fox_unit(Frame& F, const AttnBufs& A, int b, int h, int qb) {
;     ...
;     float woff = 0.f;
; #pragma unroll
;     for (int k = 0; k < 8; ++k) { const float tk = WT[k]; if (k < w) woff += tk; }
;     const float excl = woff + inc - run;
;     if (8 * tid < n) {
;         *(LAS f32x4*)(CS + 8 * tid) = (f32x4){v[0] + excl, v[1] + excl, v[2] + excl, v[3] + excl}; *(LAS f32x4*)(CS + 8 * tid + 4) = (f32x4){v[4] + excl, v[5] + excl, v[6] + excl, v[7] + excl}; }
.LBB0_323:
	s_or_b64 exec, exec, s[34:35]
	s_waitcnt lgkmcnt(0)
	s_barrier
	s_and_saveexec_b64 s[34:35], vcc
	s_cbranch_execz .LBB0_325
	v_readlane_b32 s22, v255, 19
	v_readlane_b32 s23, v255, 20
	s_nop 1
	v_cndmask_b32_e64 v14, v11, v10, s[22:23]
	v_mov_b32_e32 v10, 0x1c800
	ds_read_b128 v[10:13], v10
	v_readlane_b32 s22, v255, 17
	v_readlane_b32 s23, v255, 18
	s_waitcnt lgkmcnt(0)
	v_add_f32_e32 v10, 0, v10
	v_cndmask_b32_e64 v10, 0, v10, s[22:23]
	v_readlane_b32 s22, v255, 15
	v_add_f32_e32 v11, v11, v10
	v_readlane_b32 s23, v255, 16
	s_nop 1
	v_cndmask_b32_e64 v10, v10, v11, s[22:23]
	v_readlane_b32 s22, v255, 13
	v_add_f32_e32 v11, v12, v10
	v_readlane_b32 s23, v255, 14
	s_nop 1
	v_cndmask_b32_e64 v10, v10, v11, s[22:23]
	v_readlane_b32 s22, v255, 11
	v_add_f32_e32 v11, v13, v10
	v_readlane_b32 s23, v255, 12
	s_nop 1
	v_cndmask_b32_e64 v15, v10, v11, s[22:23]
	v_mov_b32_e32 v10, 0x1c810
	ds_read_b128 v[10:13], v10
	v_readlane_b32 s22, v255, 9
	v_readlane_b32 s23, v255, 10
	s_waitcnt lgkmcnt(0)
	v_add_f32_e32 v10, v10, v15
	v_cndmask_b32_e64 v10, v15, v10, s[22:23]
	v_readlane_b32 s22, v255, 7
	v_add_f32_e32 v11, v11, v10
	v_readlane_b32 s23, v255, 8
	s_nop 1
	v_cndmask_b32_e64 v10, v10, v11, s[22:23]
	v_readlane_b32 s22, v255, 5
	v_add_f32_e32 v11, v12, v10
	v_readlane_b32 s23, v255, 6
	s_nop 1
	v_cndmask_b32_e64 v10, v10, v11, s[22:23]
	v_readlane_b32 s22, v254, 51
	v_add_f32_e32 v11, v13, v10
	v_readlane_b32 s23, v254, 52
	s_nop 1
	v_cndmask_b32_e64 v10, v10, v11, s[22:23]
	v_add_f32_e32 v10, v14, v10
	v_sub_f32_e32 v10, v10, v3
	v_add_f32_e32 v6, v6, v10
	v_add_f32_e32 v7, v7, v10
	v_add_f32_e32 v8, v8, v10
	v_add_f32_e32 v9, v9, v10
	ds_write_b128 v131, v[6:9]
	v_add_f32_e32 v4, v4, v10
	v_add_f32_e32 v5, v5, v10
	v_add_f32_e32 v6, v2, v10
	v_add_f32_e32 v7, v3, v10
	ds_write_b128 v131, v[4:7] offset:16

; #pragma unroll
;         for (int i = 0; i < 8; ++i) { const int r = 2 * i; kc[i] = (f32x2_t){sd * (float)((r & 3) + 8 * (r >> 2)), sd * (float)(((r + 1) & 3) + 8 * ((r + 1) >> 2))}; } }
; __device__ __forceinline__ void dil_unit(Frame& F, const AttnBufs& A, int b, int h, int g, int r, int c) {
;     char* shm = (char*)F.lds; const int tid = F.tid, lane = tid & 63, r32 = lane & 31, hi = lane >> 5, w = F.wave;
;     const int dil = (g == 0) ? 1 : (g == 1 ? 4 : 16);
;     const int i0 = 256 * c;
;     att::BiasDil B; B.sd = exp2f(-8.0f * (float)(h - 10 + 1) / 10.0f) * LOG2E * (float)dil; B.qrel = 128 + w * 32 + r32; B.hi = hi; B.w = w; B.setup(r32);
;     const long tok_q0 = (long)b * SEQ + r + (long)dil * (i0 + w * 32);
;     const long tok_k0 = (long)b * SEQ + r + (long)dil * (i0 - 128);
;     const long bo = (long)b * (long)BADJ;
;     att::UnitIO io; io.Q = A.Q + bo + tok_q0 * DM + h * 64; io.qstride = (long)DM * dil; io.K0 = A.K + bo + tok_k0 * DM + h * 64; io.V0 = A.V + bo + tok_k0 * DM + h * 64; io.kstride = (long)DM * dil;
.LBB0_363:
	v_mov_b32_e32 v59, v1
	s_lshl_b32 s56, s74, 5
	v_readlane_b32 s2, v254, 30
	s_or_b32 s56, s56, s2
	s_mul_hi_u32 s57, s56, 0xaaaaaaab
	s_lshr_b32 s75, s57, 5
	s_mul_i32 s57, s75, 48
	s_sub_i32 s66, s56, s57
	s_lshr_b32 s2, s66, 4
	s_and_b32 s67, s66, 15
	s_cmp_lt_u32 s66, 16
	s_cselect_b64 s[62:63], -1, 0
	s_cmp_eq_u32 s2, 1
	s_cselect_b64 s[64:65], -1, 0
	s_bfe_u32 s68, s66, 0x20002
	s_and_b64 s[56:57], s[64:65], exec
	s_cselect_b32 s68, s68, s67
	s_and_b64 s[56:57], s[62:63], exec
	s_cselect_b32 s68, 0, s68
	s_and_b32 s66, s66, 3
	s_and_b64 s[56:57], s[64:65], exec
	s_cselect_b32 s66, s66, 0
	s_and_b64 s[56:57], s[62:63], exec
	s_cselect_b32 s76, s67, s66
	s_and_b64 s[56:57], s[64:65], exec
	s_cselect_b32 s66, 4, 16
	s_and_b64 s[56:57], s[62:63], exec
	s_cselect_b32 s80, 1, s66
	s_not_b32 s56, s75
	s_lshl_b32 s56, s56, 3
	v_cvt_f32_i32_e32 v58, s56
	s_mov_b32 s84, 0x41200000
	s_mov_b32 s85, 0x41300000
	s_lshl_b32 s69, s76, 8
	v_div_scale_f32 v60, s[56:57], s84, s84, v58
	v_rcp_f32_e32 v61, v60
	s_mov_b32 s56, 0xc2fc0000
	v_readlane_b32 s70, v254, 38
	v_readlane_b32 s71, v254, 39
	v_fma_f32 v62, -v60, v61, 1.0
	v_fmac_f32_e32 v61, v62, v61
	v_div_scale_f32 v62, vcc, v58, s84, v58
	v_mul_f32_e32 v63, v62, v61
	v_fma_f32 v64, -v60, v63, v62
	v_fmac_f32_e32 v63, v64, v61
	v_fma_f32 v60, -v60, v63, v62
	v_div_fmas_f32 v60, v60, v61, v63
	v_div_fixup_f32 v58, v60, s84, v58
	v_cmp_gt_f32_e32 vcc, s56, v58
	s_and_b64 s[56:57], vcc, exec
	v_readlane_b32 s56, v254, 48
	s_cselect_b32 s81, 0xffffffc0, 0
	s_add_i32 s56, s69, s56
	s_or_b32 s68, s70, s68
	s_ashr_i32 s57, s56, 31
	s_and_b64 s[66:67], s[64:65], exec
	s_cselect_b32 s70, 2, 4
	s_and_b64 s[66:67], s[62:63], exec
	s_cselect_b32 s70, 0, s70
	s_lshl_b64 s[56:57], s[56:57], s70
	s_add_u32 s66, s56, s68
	s_addc_u32 s67, s57, s71
	s_add_i32 s56, s69, 0xffffff80
	s_ashr_i32 s57, s56, 31
	s_lshl_b64 s[56:57], s[56:57], s70
	s_add_u32 s56, s56, s68
	s_addc_u32 s57, s57, s71
	s_lshl_b64 s[68:69], s[66:67], 11
	v_readlane_b32 s70, v254, 42
	s_add_u32 s68, s70, s68
	v_readlane_b32 s70, v254, 45
	s_addc_u32 s69, s70, s69
	s_lshl_b32 s70, s75, 6
	s_lshl_b32 s77, s75, 7
	v_writelane_b32 v255, s70, 49
	v_writelane_b32 v191, s70, 9
	s_add_u32 s70, s68, s77
	s_addc_u32 s71, s69, 0
	s_lshl_b64 s[68:69], s[56:57], 11
	v_readlane_b32 s56, v254, 49
	s_add_u32 s56, s56, s68
	v_readlane_b32 s57, v254, 50
	s_addc_u32 s57, s57, s69
	s_add_u32 s56, s56, s77
	s_addc_u32 s57, s57, 0
	v_readlane_b32 s78, v254, 53
	s_add_u32 s68, s78, s68
	v_readlane_b32 s78, v254, 54
	s_addc_u32 s69, s78, s69
	s_add_u32 s68, s68, s77
	s_addc_u32 s69, s69, 0
	s_cmp_eq_u32 s76, 0
	v_readfirstlane_b32 s77, v232
	s_cselect_b32 s88, 2, 0
	s_ashr_i32 s76, s77, 6
	s_and_b64 s[78:79], s[64:65], exec
	s_cselect_b32 s82, 12, 14
	s_and_b64 s[78:79], s[62:63], exec
	s_cselect_b32 s83, 10, s82
	v_lshlrev_b64 v[60:61], s83, v[146:147]
	v_lshl_add_u64 v[60:61], v[60:61], 1, s[70:71]
	v_mov_b32_e32 v149, v1
	v_lshl_add_u64 v[60:61], v[60:61], 0, v[148:149]
	flat_load_dwordx4 v[98:101], v[60:61] offset:1280
	flat_load_dwordx4 v[102:105], v[60:61] offset:1312
	flat_load_dwordx4 v[106:109], v[60:61] offset:1344
	flat_load_dwordx4 v[110:113], v[60:61] offset:1376
	v_cndmask_b32_e32 v62, 0, v224, vcc
	v_add_f32_e32 v58, v58, v62
	v_exp_f32_e32 v58, v58
	v_cvt_f32_ubyte0_e32 v61, s80
	s_mov_b32 s78, 2.0
	s_mov_b32 s79, 0x40400000
	v_ldexp_f32 v58, v58, s81
	v_mul_f32_e32 v58, 0x3fb8aa3b, v58
	v_mul_f32_e32 v155, v58, v61
	v_mov_b32_e32 v58, v155
	v_mul_f32_e32 v158, s78, v58
	v_mul_f32_e32 v159, s79, v58
	s_mov_b32 s78, 0x41000000
	s_mov_b32 s79, 0x41100000
	v_mul_f32_e32 v160, s78, v58
	v_mul_f32_e32 v161, s79, v58
	s_mov_b32 s78, 0x41800000
	s_mov_b32 s79, 0x41880000
	v_mul_f32_e32 v164, s78, v58
	v_mul_f32_e32 v165, s79, v58
	s_mov_b32 s78, 0x41900000
	s_mov_b32 s79, 0x41980000
	v_mul_f32_e32 v166, s78, v58
	v_mul_f32_e32 v167, s79, v58
	s_mov_b32 s78, 0x41c00000
	s_mov_b32 s79, 0x41c80000
	v_mul_f32_e32 v168, s78, v58
	v_mul_f32_e32 v169, s79, v58
	s_mov_b32 s78, 0x41d00000
	s_mov_b32 s79, 0x41d80000
	v_mul_f32_e32 v170, s78, v58
	v_mul_f32_e32 v171, s79, v58
	s_lshl_b32 s70, s76, 4
	s_ashr_i32 s79, s77, 3
	v_mul_f32_e32 v162, s84, v58
	v_mul_f32_e32 v163, s85, v58
	s_lshl_b32 s80, s76, 3
	s_lshl_b32 s78, s76, 10
	v_and_or_b32 v58, s70, 48, v178
	s_and_b32 s82, s79, 0xffffffe0
	v_lshlrev_b64 v[62:63], s83, v[194:195]
	s_ashr_i32 s81, s80, 31
	s_add_i32 s79, s78, 0x8000
	v_lshlrev_b64 v[64:65], s83, v[58:59]
	s_ashr_i32 s83, s82, 31
	v_lshl_add_u64 v[62:63], v[62:63], 1, s[56:57]
	s_and_b64 s[56:57], s[64:65], exec
	v_lshl_add_u64 v[172:173], s[80:81], 1, v[62:63]
	v_lshlrev_b32_e32 v248, 11, v246
	v_mov_b32_e32 v249, s2
	v_lshlrev_b32_e32 v249, 1, v249
	v_lshlrev_b32_e32 v248, v249, v248
	v_add_u32_e32 v248, v248, v247
	v_ashrrev_i32_e32 v249, 31, v248
	v_lshl_add_u64 v[172:173], v[172:173], 0, v[248:249]
	v_lshl_add_u64 v[62:63], v[64:65], 1, s[68:69]
	s_cselect_b32 s68, 18, 20
	s_and_b64 s[56:57], s[62:63], exec
	s_mov_b32 s89, s3
	s_cselect_b32 s80, 16, s68
	v_mov_b32_e32 v66, v150
	v_mov_b32_e32 v67, v1
	v_lshl_add_u64 v[62:63], s[82:83], 1, v[62:63]
	v_lshl_add_u64 v[174:175], v[62:63], 0, v[66:67]
	v_writelane_b32 v254, s2, 9
	v_writelane_b32 v191, s2, 7
	v_writelane_b32 v191, s3, 8
	s_mov_b32 s81, s88
	s_mov_b32 s100, s88
	v_writelane_b32 v191, s62, 0
	v_writelane_b32 v191, s63, 1
	v_writelane_b32 v191, s64, 2
	v_writelane_b32 v191, s65, 3
	v_writelane_b32 v191, s66, 4
	v_writelane_b32 v191, s67, 5
	v_writelane_b32 v191, s75, 6
	s_barrier

; #define PG8_GAS __attribute__((address_space(1)))
; #define PG8_PACK8(y0, y1) (u32x4){cvt_pk_bf16((y0)[0], (y0)[1]), cvt_pk_bf16((y0)[2], (y0)[3]), cvt_pk_bf16((y1)[0], (y1)[1]), cvt_pk_bf16((y1)[2], (y1)[3])}
;     __device__ __forceinline__ void operator()(const f32x4 (&acc)[2][2][4][2], const Unit& u, int ui, int wr, int wc, int fr, int fq) const {
;     ...
;                 for (int bj = 0; bj < 2; ++bj) { const unsigned off = (row0 + ai * HALF + m * 16) * 1024u + col0 + bj * HALF;
;                     xw[ai][m][bj] = *(const PG8_GAS u32x4*)((PG8_GAS unsigned char*)ws + E_XB + (size_t)(off * 2u)); }
;         float ssv[2][4];
; #pragma unroll
;         for (int ai = 0; ai < 2; ++ai) {
; #pragma unroll
;             for (int m = 0; m < 4; ++m) {
;                 const unsigned row = row0 + ai * HALF + m * 16; float ss = 0.f;
; #pragma unroll
;                 for (int bj = 0; bj < 2; ++bj) {
;                     const unsigned off = row * 1024u + col0 + bj * HALF;
;                     const u32x4 x4 = xw[ai][m][bj];
;                     f32x4 o0, o1;
;                     o0[0] = __builtin_bit_cast(float, x4[0] << 16) + acc[ai][bj][m][0][0]; o0[1] = __builtin_bit_cast(float, x4[0] & 0xffff0000u) + acc[ai][bj][m][0][1];
;                     o0[2] = __builtin_bit_cast(float, x4[1] << 16) + acc[ai][bj][m][0][2]; o0[3] = __builtin_bit_cast(float, x4[1] & 0xffff0000u) + acc[ai][bj][m][0][3];
;                     o1[0] = __builtin_bit_cast(float, x4[2] << 16) + acc[ai][bj][m][1][0]; o1[1] = __builtin_bit_cast(float, x4[2] & 0xffff0000u) + acc[ai][bj][m][1][1];
;                     o1[2] = __builtin_bit_cast(float, x4[3] << 16) + acc[ai][bj][m][1][2]; o1[3] = __builtin_bit_cast(float, x4[3] & 0xffff0000u) + acc[ai][bj][m][1][3];
;                     if (last) { __builtin_nontemporal_store(o0, (PG8_GAS f32x4*)((PG8_GAS float*)out + (size_t)off)); __builtin_nontemporal_store(o1, (PG8_GAS f32x4*)((PG8_GAS float*)out + (size_t)off + 4)); }
;                     else {
;                         const f32x4 q4 = o0 * o0 + o1 * o1; ss += (q4[0] + q4[1]) + (q4[2] + q4[3]);
;                         *(PG8_GAS u32x4*)((PG8_GAS unsigned char*)ws + E_XB + (size_t)(off * 2u)) = PG8_PACK8(o0, o1);
;                     }
.LBB0_421:
	v_lshl_or_b32 v0, s4, 8, v210
	v_lshl_add_u32 v213, s0, 8, v195
	v_lshlrev_b32_e32 v74, 1, v0
	v_lshl_add_u32 v74, v213, 11, v74
	v_or_b32_e32 v75, 0x100, v74
	global_load_dwordx4 v[218:221], v74, s[12:13]
	global_load_dwordx4 v[186:189], v75, s[12:13]
	v_add_u32_e32 v75, 0x8000, v74
	global_load_dwordx4 v[182:185], v75, s[12:13]
	v_add_u32_e32 v75, 0x8100, v74
	global_load_dwordx4 v[178:181], v75, s[12:13]
	v_add_u32_e32 v75, 0x10000, v74
	global_load_dwordx4 v[174:177], v75, s[12:13]
	v_add_u32_e32 v75, 0x10100, v74
	global_load_dwordx4 v[170:173], v75, s[12:13]
	v_add_u32_e32 v75, 0x18000, v74
	global_load_dwordx4 v[166:169], v75, s[12:13]
	v_add_u32_e32 v75, 0x18100, v74
	global_load_dwordx4 v[154:157], v75, s[12:13]
	v_add_u32_e32 v75, 0x40000, v74
	global_load_dwordx4 v[150:153], v75, s[12:13]
	v_add_u32_e32 v75, 0x40100, v74
	global_load_dwordx4 v[142:145], v75, s[12:13]
	v_add_u32_e32 v75, 0x48000, v74
	global_load_dwordx4 v[126:129], v75, s[12:13]
	v_add_u32_e32 v75, 0x48100, v74
	global_load_dwordx4 v[122:125], v75, s[12:13]
	v_add_u32_e32 v75, 0x50000, v74
	global_load_dwordx4 v[106:109], v75, s[12:13]
	v_add_u32_e32 v75, 0x50100, v74
	global_load_dwordx4 v[98:101], v75, s[12:13]
	v_add_u32_e32 v75, 0x58000, v74
	v_add_u32_e32 v74, 0x58100, v74
	global_load_dwordx4 v[86:89], v75, s[12:13]
	v_lshl_add_u32 v0, v213, 10, v0
	global_load_dwordx4 v[74:77], v74, s[12:13]
	s_mov_b64 s[0:1], -1
	s_and_b64 vcc, exec, s[8:9]
	s_waitcnt vmcnt(15)
	v_lshlrev_b32_e32 v190, 16, v218
	v_and_b32_e32 v191, 0xffff0000, v218
	v_add_f32_e32 v162, v162, v190
	v_add_f32_e32 v163, v163, v191
	v_lshlrev_b32_e32 v190, 16, v219
	v_and_b32_e32 v191, 0xffff0000, v219
	v_add_f32_e32 v164, v164, v190
	v_add_f32_e32 v165, v165, v191
	v_lshlrev_b32_e32 v190, 16, v220
	v_and_b32_e32 v191, 0xffff0000, v220
	v_add_f32_e32 v158, v158, v190
	v_add_f32_e32 v159, v159, v191
	v_lshlrev_b32_e32 v190, 16, v221
	v_and_b32_e32 v191, 0xffff0000, v221
	v_add_f32_e32 v160, v160, v190
	v_add_f32_e32 v161, v161, v191
	s_cbranch_vccz .LBB0_423
	v_mul_f32_e32 v190, v160, v160
	v_mul_f32_e32 v191, v161, v161
	v_mul_f32_e32 v218, v158, v158
	v_mul_f32_e32 v219, v159, v159
	v_fma_f32 v190, v164, v164, v190
	v_fma_f32 v191, v165, v165, v191
	v_fma_f32 v218, v162, v162, v218
	v_fma_f32 v219, v163, v163, v219
	s_mov_b64 s[0:1], 0
	v_pk_mov_b32 v[220:221], v[218:219], v[190:191] op_sel:[1,0]
	v_mov_b32_e32 v219, v191
	v_add_f32_e32 v190, v220, v218
	v_add_f32_e32 v191, v221, v219
	v_cvt_pk_bf16_f32 v218, v162, v163
	v_cvt_pk_bf16_f32 v219, v164, v165
	v_cvt_pk_bf16_f32 v220, v158, v159
	v_cvt_pk_bf16_f32 v221, v160, v161
	s_nop 0
	v_add_f32_e32 v233, v190, v191
	v_lshlrev_b32_e32 v190, 1, v0
	global_store_dwordx4 v190, v[218:221], s[12:13]

; #define PG8_GAS __attribute__((address_space(1)))
; #define PG8_PACK8(y0, y1) (u32x4){cvt_pk_bf16((y0)[0], (y0)[1]), cvt_pk_bf16((y0)[2], (y0)[3]), cvt_pk_bf16((y1)[0], (y1)[1]), cvt_pk_bf16((y1)[2], (y1)[3])}
;     __device__ __forceinline__ void operator()(const f32x4 (&acc)[2][2][4][2], const Unit& u, int ui, int wr, int wc, int fr, int fq) const {
;     ...
;                 for (int bj = 0; bj < 2; ++bj) { const unsigned off = (row0 + ai * HALF + m * 16) * 1024u + col0 + bj * HALF;
;                     xw[ai][m][bj] = *(const PG8_GAS u32x4*)((PG8_GAS unsigned char*)ws + E_XB + (size_t)(off * 2u)); }
;         float ssv[2][4];
; #pragma unroll
;         for (int ai = 0; ai < 2; ++ai) {
; #pragma unroll
;             for (int m = 0; m < 4; ++m) {
;                 const unsigned row = row0 + ai * HALF + m * 16; float ss = 0.f;
; #pragma unroll
;                 for (int bj = 0; bj < 2; ++bj) {
;                     const unsigned off = row * 1024u + col0 + bj * HALF;
;                     const u32x4 x4 = xw[ai][m][bj];
;                     f32x4 o0, o1;
;                     o0[0] = __builtin_bit_cast(float, x4[0] << 16) + acc[ai][bj][m][0][0]; o0[1] = __builtin_bit_cast(float, x4[0] & 0xffff0000u) + acc[ai][bj][m][0][1];
;                     o0[2] = __builtin_bit_cast(float, x4[1] << 16) + acc[ai][bj][m][0][2]; o0[3] = __builtin_bit_cast(float, x4[1] & 0xffff0000u) + acc[ai][bj][m][0][3];
;                     o1[0] = __builtin_bit_cast(float, x4[2] << 16) + acc[ai][bj][m][1][0]; o1[1] = __builtin_bit_cast(float, x4[2] & 0xffff0000u) + acc[ai][bj][m][1][1];
;                     o1[2] = __builtin_bit_cast(float, x4[3] << 16) + acc[ai][bj][m][1][2]; o1[3] = __builtin_bit_cast(float, x4[3] & 0xffff0000u) + acc[ai][bj][m][1][3];
;                     if (last) { __builtin_nontemporal_store(o0, (PG8_GAS f32x4*)((PG8_GAS float*)out + (size_t)off)); __builtin_nontemporal_store(o1, (PG8_GAS f32x4*)((PG8_GAS float*)out + (size_t)off + 4)); }
;                     else {
;                         const f32x4 q4 = o0 * o0 + o1 * o1; ss += (q4[0] + q4[1]) + (q4[2] + q4[3]);
;                         *(PG8_GAS u32x4*)((PG8_GAS unsigned char*)ws + E_XB + (size_t)(off * 2u)) = PG8_PACK8(o0, o1);
;                     }
.LBB0_425:
	s_nop 1
	s_waitcnt vmcnt(15)
	v_lshlrev_b32_e32 v158, 16, v186
	v_and_b32_e32 v159, 0xffff0000, v186
	v_add_f32_e32 v146, v146, v158
	v_add_f32_e32 v147, v147, v159
	v_lshlrev_b32_e32 v158, 16, v187
	v_and_b32_e32 v159, 0xffff0000, v187
	v_add_f32_e32 v148, v148, v158
	v_add_f32_e32 v149, v149, v159
	v_lshlrev_b32_e32 v158, 16, v188
	v_and_b32_e32 v159, 0xffff0000, v188
	v_add_f32_e32 v138, v138, v158
	v_add_f32_e32 v139, v139, v159
	v_lshlrev_b32_e32 v158, 16, v189
	v_and_b32_e32 v159, 0xffff0000, v189
	v_add_f32_e32 v140, v140, v158
	v_add_f32_e32 v141, v141, v159
	v_cndmask_b32_e64 v158, 0, 1, s[8:9]
	v_cmp_ne_u32_e64 s[0:1], 1, v158
	s_andn2_b64 vcc, exec, s[8:9]
	s_mov_b64 s[24:25], -1
	s_cbranch_vccnz .LBB0_427
	v_mul_f32_e32 v158, v140, v140
	v_mul_f32_e32 v159, v141, v141
	v_mul_f32_e32 v160, v138, v138
	v_mul_f32_e32 v161, v139, v139
	v_fma_f32 v158, v148, v148, v158
	v_fma_f32 v159, v149, v149, v159
	v_fma_f32 v160, v146, v146, v160
	v_fma_f32 v161, v147, v147, v161
	s_mov_b64 s[24:25], 0
	v_pk_mov_b32 v[162:163], v[160:161], v[158:159] op_sel:[1,0]
	v_mov_b32_e32 v161, v159
	v_add_f32_e32 v158, v162, v160
	v_add_f32_e32 v159, v163, v161
	v_cvt_pk_bf16_f32 v160, v146, v147
	v_cvt_pk_bf16_f32 v161, v148, v149
	v_cvt_pk_bf16_f32 v162, v138, v139
	v_cvt_pk_bf16_f32 v163, v140, v141
	s_nop 0
	v_add_f32_e32 v158, v158, v159
	v_mov_b32_e32 v159, 0x100
	v_add_f32_e32 v158, v158, v233
	v_lshl_or_b32 v159, v0, 1, v159
	global_store_dwordx4 v159, v[160:163], s[12:13]

; #define PG8_GAS __attribute__((address_space(1)))
; #define PG8_PACK8(y0, y1) (u32x4){cvt_pk_bf16((y0)[0], (y0)[1]), cvt_pk_bf16((y0)[2], (y0)[3]), cvt_pk_bf16((y1)[0], (y1)[1]), cvt_pk_bf16((y1)[2], (y1)[3])}
;     __device__ __forceinline__ void operator()(const f32x4 (&acc)[2][2][4][2], const Unit& u, int ui, int wr, int wc, int fr, int fq) const {
;     ...
;                 for (int bj = 0; bj < 2; ++bj) { const unsigned off = (row0 + ai * HALF + m * 16) * 1024u + col0 + bj * HALF;
;                     xw[ai][m][bj] = *(const PG8_GAS u32x4*)((PG8_GAS unsigned char*)ws + E_XB + (size_t)(off * 2u)); }
;         float ssv[2][4];
; #pragma unroll
;         for (int ai = 0; ai < 2; ++ai) {
; #pragma unroll
;             for (int m = 0; m < 4; ++m) {
;                 const unsigned row = row0 + ai * HALF + m * 16; float ss = 0.f;
; #pragma unroll
;                 for (int bj = 0; bj < 2; ++bj) {
;                     const unsigned off = row * 1024u + col0 + bj * HALF;
;                     const u32x4 x4 = xw[ai][m][bj];
;                     f32x4 o0, o1;
;                     o0[0] = __builtin_bit_cast(float, x4[0] << 16) + acc[ai][bj][m][0][0]; o0[1] = __builtin_bit_cast(float, x4[0] & 0xffff0000u) + acc[ai][bj][m][0][1];
;                     o0[2] = __builtin_bit_cast(float, x4[1] << 16) + acc[ai][bj][m][0][2]; o0[3] = __builtin_bit_cast(float, x4[1] & 0xffff0000u) + acc[ai][bj][m][0][3];
;                     o1[0] = __builtin_bit_cast(float, x4[2] << 16) + acc[ai][bj][m][1][0]; o1[1] = __builtin_bit_cast(float, x4[2] & 0xffff0000u) + acc[ai][bj][m][1][1];
;                     o1[2] = __builtin_bit_cast(float, x4[3] << 16) + acc[ai][bj][m][1][2]; o1[3] = __builtin_bit_cast(float, x4[3] & 0xffff0000u) + acc[ai][bj][m][1][3];
;                     if (last) { __builtin_nontemporal_store(o0, (PG8_GAS f32x4*)((PG8_GAS float*)out + (size_t)off)); __builtin_nontemporal_store(o1, (PG8_GAS f32x4*)((PG8_GAS float*)out + (size_t)off + 4)); }
;                     else {
;                         const f32x4 q4 = o0 * o0 + o1 * o1; ss += (q4[0] + q4[1]) + (q4[2] + q4[3]);
;                         *(PG8_GAS u32x4*)((PG8_GAS unsigned char*)ws + E_XB + (size_t)(off * 2u)) = PG8_PACK8(o0, o1);
;                     }
.LBB0_429:
	s_waitcnt vmcnt(15)
	v_lshlrev_b32_e32 v140, 16, v182
	v_and_b32_e32 v141, 0xffff0000, v182
	v_add_f32_e32 v134, v134, v140
	v_add_f32_e32 v135, v135, v141
	v_lshlrev_b32_e32 v140, 16, v183
	v_and_b32_e32 v141, 0xffff0000, v183
	v_add_f32_e32 v136, v136, v140
	v_add_f32_e32 v137, v137, v141
	v_lshlrev_b32_e32 v140, 16, v184
	v_and_b32_e32 v141, 0xffff0000, v184
	v_add_f32_e32 v130, v130, v140
	v_add_f32_e32 v131, v131, v141
	v_lshlrev_b32_e32 v140, 16, v185
	v_and_b32_e32 v141, 0xffff0000, v185
	v_add_u32_e32 v138, 0x4000, v0
	v_add_f32_e32 v132, v132, v140
	v_add_f32_e32 v133, v133, v141
	s_and_b64 vcc, exec, s[0:1]
	s_mov_b64 s[24:25], -1
	s_cbranch_vccnz .LBB0_431
	v_mul_f32_e32 v140, v132, v132
	v_mul_f32_e32 v141, v133, v133
	v_mul_f32_e32 v146, v130, v130
	v_mul_f32_e32 v147, v131, v131
	v_fma_f32 v140, v136, v136, v140
	v_fma_f32 v141, v137, v137, v141
	v_fma_f32 v146, v134, v134, v146
	v_fma_f32 v147, v135, v135, v147
	s_mov_b64 s[24:25], 0
	v_pk_mov_b32 v[148:149], v[146:147], v[140:141] op_sel:[1,0]
	v_mov_b32_e32 v147, v141
	v_add_f32_e32 v140, v148, v146
	v_add_f32_e32 v141, v149, v147
	v_cvt_pk_bf16_f32 v146, v134, v135
	v_cvt_pk_bf16_f32 v147, v136, v137
	v_cvt_pk_bf16_f32 v148, v130, v131
	v_cvt_pk_bf16_f32 v149, v132, v133
	s_nop 0
	v_add_f32_e32 v139, v140, v141
	v_lshlrev_b32_e32 v140, 1, v138
	global_store_dwordx4 v140, v[146:149], s[12:13]

; #define PG8_GAS __attribute__((address_space(1)))
; #define PG8_PACK8(y0, y1) (u32x4){cvt_pk_bf16((y0)[0], (y0)[1]), cvt_pk_bf16((y0)[2], (y0)[3]), cvt_pk_bf16((y1)[0], (y1)[1]), cvt_pk_bf16((y1)[2], (y1)[3])}
;     __device__ __forceinline__ void operator()(const f32x4 (&acc)[2][2][4][2], const Unit& u, int ui, int wr, int wc, int fr, int fq) const {
;     ...
;                 for (int bj = 0; bj < 2; ++bj) { const unsigned off = (row0 + ai * HALF + m * 16) * 1024u + col0 + bj * HALF;
;                     xw[ai][m][bj] = *(const PG8_GAS u32x4*)((PG8_GAS unsigned char*)ws + E_XB + (size_t)(off * 2u)); }
;         float ssv[2][4];
; #pragma unroll
;         for (int ai = 0; ai < 2; ++ai) {
; #pragma unroll
;             for (int m = 0; m < 4; ++m) {
;                 const unsigned row = row0 + ai * HALF + m * 16; float ss = 0.f;
; #pragma unroll
;                 for (int bj = 0; bj < 2; ++bj) {
;                     const unsigned off = row * 1024u + col0 + bj * HALF;
;                     const u32x4 x4 = xw[ai][m][bj];
;                     f32x4 o0, o1;
;                     o0[0] = __builtin_bit_cast(float, x4[0] << 16) + acc[ai][bj][m][0][0]; o0[1] = __builtin_bit_cast(float, x4[0] & 0xffff0000u) + acc[ai][bj][m][0][1];
;                     o0[2] = __builtin_bit_cast(float, x4[1] << 16) + acc[ai][bj][m][0][2]; o0[3] = __builtin_bit_cast(float, x4[1] & 0xffff0000u) + acc[ai][bj][m][0][3];
;                     o1[0] = __builtin_bit_cast(float, x4[2] << 16) + acc[ai][bj][m][1][0]; o1[1] = __builtin_bit_cast(float, x4[2] & 0xffff0000u) + acc[ai][bj][m][1][1];
;                     o1[2] = __builtin_bit_cast(float, x4[3] << 16) + acc[ai][bj][m][1][2]; o1[3] = __builtin_bit_cast(float, x4[3] & 0xffff0000u) + acc[ai][bj][m][1][3];
;                     if (last) { __builtin_nontemporal_store(o0, (PG8_GAS f32x4*)((PG8_GAS float*)out + (size_t)off)); __builtin_nontemporal_store(o1, (PG8_GAS f32x4*)((PG8_GAS float*)out + (size_t)off + 4)); }
;                     else {
;                         const f32x4 q4 = o0 * o0 + o1 * o1; ss += (q4[0] + q4[1]) + (q4[2] + q4[3]);
;                         *(PG8_GAS u32x4*)((PG8_GAS unsigned char*)ws + E_XB + (size_t)(off * 2u)) = PG8_PACK8(o0, o1);
;                     }
.LBB0_433:
	s_waitcnt vmcnt(15)
	v_lshlrev_b32_e32 v132, 16, v178
	v_and_b32_e32 v133, 0xffff0000, v178
	v_add_f32_e32 v118, v118, v132
	v_add_f32_e32 v119, v119, v133
	v_lshlrev_b32_e32 v132, 16, v179
	v_and_b32_e32 v133, 0xffff0000, v179
	v_add_f32_e32 v120, v120, v132
	v_add_f32_e32 v121, v121, v133
	v_lshlrev_b32_e32 v132, 16, v180
	v_and_b32_e32 v133, 0xffff0000, v180
	v_add_f32_e32 v114, v114, v132
	v_add_f32_e32 v115, v115, v133
	v_lshlrev_b32_e32 v132, 16, v181
	v_and_b32_e32 v133, 0xffff0000, v181
	v_add_u32_e32 v130, 0x4080, v0
	v_add_f32_e32 v116, v116, v132
	v_add_f32_e32 v117, v117, v133
	s_and_b64 vcc, exec, s[0:1]
	s_mov_b64 s[24:25], -1
	s_cbranch_vccnz .LBB0_435
	v_mul_f32_e32 v132, v116, v116
	v_mul_f32_e32 v133, v117, v117
	v_mul_f32_e32 v134, v114, v114
	v_mul_f32_e32 v135, v115, v115
	v_fma_f32 v132, v120, v120, v132
	v_fma_f32 v133, v121, v121, v133
	v_fma_f32 v134, v118, v118, v134
	v_fma_f32 v135, v119, v119, v135
	s_mov_b64 s[24:25], 0
	v_pk_mov_b32 v[136:137], v[134:135], v[132:133] op_sel:[1,0]
	v_mov_b32_e32 v135, v133
	v_add_f32_e32 v132, v136, v134
	v_add_f32_e32 v133, v137, v135
	v_lshlrev_b32_e32 v136, 1, v130
	v_add_f32_e32 v131, v132, v133
	v_add_f32_e32 v131, v131, v139
	v_cvt_pk_bf16_f32 v132, v118, v119
	v_cvt_pk_bf16_f32 v133, v120, v121
	v_cvt_pk_bf16_f32 v134, v114, v115
	v_cvt_pk_bf16_f32 v135, v116, v117
	global_store_dwordx4 v136, v[132:135], s[12:13]

; #define PG8_GAS __attribute__((address_space(1)))
; #define PG8_PACK8(y0, y1) (u32x4){cvt_pk_bf16((y0)[0], (y0)[1]), cvt_pk_bf16((y0)[2], (y0)[3]), cvt_pk_bf16((y1)[0], (y1)[1]), cvt_pk_bf16((y1)[2], (y1)[3])}
;     __device__ __forceinline__ void operator()(const f32x4 (&acc)[2][2][4][2], const Unit& u, int ui, int wr, int wc, int fr, int fq) const {
;     ...
;                 for (int bj = 0; bj < 2; ++bj) { const unsigned off = (row0 + ai * HALF + m * 16) * 1024u + col0 + bj * HALF;
;                     xw[ai][m][bj] = *(const PG8_GAS u32x4*)((PG8_GAS unsigned char*)ws + E_XB + (size_t)(off * 2u)); }
;         float ssv[2][4];
; #pragma unroll
;         for (int ai = 0; ai < 2; ++ai) {
; #pragma unroll
;             for (int m = 0; m < 4; ++m) {
;                 const unsigned row = row0 + ai * HALF + m * 16; float ss = 0.f;
; #pragma unroll
;                 for (int bj = 0; bj < 2; ++bj) {
;                     const unsigned off = row * 1024u + col0 + bj * HALF;
;                     const u32x4 x4 = xw[ai][m][bj];
;                     f32x4 o0, o1;
;                     o0[0] = __builtin_bit_cast(float, x4[0] << 16) + acc[ai][bj][m][0][0]; o0[1] = __builtin_bit_cast(float, x4[0] & 0xffff0000u) + acc[ai][bj][m][0][1];
;                     o0[2] = __builtin_bit_cast(float, x4[1] << 16) + acc[ai][bj][m][0][2]; o0[3] = __builtin_bit_cast(float, x4[1] & 0xffff0000u) + acc[ai][bj][m][0][3];
;                     o1[0] = __builtin_bit_cast(float, x4[2] << 16) + acc[ai][bj][m][1][0]; o1[1] = __builtin_bit_cast(float, x4[2] & 0xffff0000u) + acc[ai][bj][m][1][1];
;                     o1[2] = __builtin_bit_cast(float, x4[3] << 16) + acc[ai][bj][m][1][2]; o1[3] = __builtin_bit_cast(float, x4[3] & 0xffff0000u) + acc[ai][bj][m][1][3];
;                     if (last) { __builtin_nontemporal_store(o0, (PG8_GAS f32x4*)((PG8_GAS float*)out + (size_t)off)); __builtin_nontemporal_store(o1, (PG8_GAS f32x4*)((PG8_GAS float*)out + (size_t)off + 4)); }
;                     else {
;                         const f32x4 q4 = o0 * o0 + o1 * o1; ss += (q4[0] + q4[1]) + (q4[2] + q4[3]);
;                         *(PG8_GAS u32x4*)((PG8_GAS unsigned char*)ws + E_XB + (size_t)(off * 2u)) = PG8_PACK8(o0, o1);
;                     }
.LBB0_437:
	s_waitcnt vmcnt(15)
	v_lshlrev_b32_e32 v116, 16, v174
	v_and_b32_e32 v117, 0xffff0000, v174
	v_add_f32_e32 v110, v110, v116
	v_add_f32_e32 v111, v111, v117
	v_lshlrev_b32_e32 v116, 16, v175
	v_and_b32_e32 v117, 0xffff0000, v175
	v_add_f32_e32 v112, v112, v116
	v_add_f32_e32 v113, v113, v117
	v_lshlrev_b32_e32 v116, 16, v176
	v_and_b32_e32 v117, 0xffff0000, v176
	v_add_f32_e32 v102, v102, v116
	v_add_f32_e32 v103, v103, v117
	v_lshlrev_b32_e32 v116, 16, v177
	v_and_b32_e32 v117, 0xffff0000, v177
	v_add_u32_e32 v114, 0x8000, v0
	v_add_f32_e32 v104, v104, v116
	v_add_f32_e32 v105, v105, v117
	s_and_b64 vcc, exec, s[0:1]
	s_mov_b64 s[24:25], -1
	s_cbranch_vccnz .LBB0_439
	v_mul_f32_e32 v116, v104, v104
	v_mul_f32_e32 v117, v105, v105
	v_mul_f32_e32 v118, v102, v102
	v_mul_f32_e32 v119, v103, v103
	v_fma_f32 v116, v112, v112, v116
	v_fma_f32 v117, v113, v113, v117
	v_fma_f32 v118, v110, v110, v118
	v_fma_f32 v119, v111, v111, v119
	s_mov_b64 s[24:25], 0
	v_pk_mov_b32 v[120:121], v[118:119], v[116:117] op_sel:[1,0]
	v_mov_b32_e32 v119, v117
	v_add_f32_e32 v116, v120, v118
	v_add_f32_e32 v117, v121, v119
	v_lshlrev_b32_e32 v120, 1, v114
	v_add_f32_e32 v115, v116, v117
	v_cvt_pk_bf16_f32 v116, v110, v111
	v_cvt_pk_bf16_f32 v117, v112, v113
	v_cvt_pk_bf16_f32 v118, v102, v103
	v_cvt_pk_bf16_f32 v119, v104, v105
	global_store_dwordx4 v120, v[116:119], s[12:13]

; #define PG8_GAS __attribute__((address_space(1)))
; #define PG8_PACK8(y0, y1) (u32x4){cvt_pk_bf16((y0)[0], (y0)[1]), cvt_pk_bf16((y0)[2], (y0)[3]), cvt_pk_bf16((y1)[0], (y1)[1]), cvt_pk_bf16((y1)[2], (y1)[3])}
;     __device__ __forceinline__ void operator()(const f32x4 (&acc)[2][2][4][2], const Unit& u, int ui, int wr, int wc, int fr, int fq) const {
;     ...
;                 for (int bj = 0; bj < 2; ++bj) { const unsigned off = (row0 + ai * HALF + m * 16) * 1024u + col0 + bj * HALF;
;                     xw[ai][m][bj] = *(const PG8_GAS u32x4*)((PG8_GAS unsigned char*)ws + E_XB + (size_t)(off * 2u)); }
;         float ssv[2][4];
; #pragma unroll
;         for (int ai = 0; ai < 2; ++ai) {
; #pragma unroll
;             for (int m = 0; m < 4; ++m) {
;                 const unsigned row = row0 + ai * HALF + m * 16; float ss = 0.f;
; #pragma unroll
;                 for (int bj = 0; bj < 2; ++bj) {
;                     const unsigned off = row * 1024u + col0 + bj * HALF;
;                     const u32x4 x4 = xw[ai][m][bj];
;                     f32x4 o0, o1;
;                     o0[0] = __builtin_bit_cast(float, x4[0] << 16) + acc[ai][bj][m][0][0]; o0[1] = __builtin_bit_cast(float, x4[0] & 0xffff0000u) + acc[ai][bj][m][0][1];
;                     o0[2] = __builtin_bit_cast(float, x4[1] << 16) + acc[ai][bj][m][0][2]; o0[3] = __builtin_bit_cast(float, x4[1] & 0xffff0000u) + acc[ai][bj][m][0][3];
;                     o1[0] = __builtin_bit_cast(float, x4[2] << 16) + acc[ai][bj][m][1][0]; o1[1] = __builtin_bit_cast(float, x4[2] & 0xffff0000u) + acc[ai][bj][m][1][1];
;                     o1[2] = __builtin_bit_cast(float, x4[3] << 16) + acc[ai][bj][m][1][2]; o1[3] = __builtin_bit_cast(float, x4[3] & 0xffff0000u) + acc[ai][bj][m][1][3];
;                     if (last) { __builtin_nontemporal_store(o0, (PG8_GAS f32x4*)((PG8_GAS float*)out + (size_t)off)); __builtin_nontemporal_store(o1, (PG8_GAS f32x4*)((PG8_GAS float*)out + (size_t)off + 4)); }
;                     else {
;                         const f32x4 q4 = o0 * o0 + o1 * o1; ss += (q4[0] + q4[1]) + (q4[2] + q4[3]);
;                         *(PG8_GAS u32x4*)((PG8_GAS unsigned char*)ws + E_XB + (size_t)(off * 2u)) = PG8_PACK8(o0, o1);
;                     }
.LBB0_441:
	s_waitcnt vmcnt(15)
	v_lshlrev_b32_e32 v104, 16, v170
	v_and_b32_e32 v105, 0xffff0000, v170
	v_add_f32_e32 v94, v94, v104
	v_add_f32_e32 v95, v95, v105
	v_lshlrev_b32_e32 v104, 16, v171
	v_and_b32_e32 v105, 0xffff0000, v171
	v_add_f32_e32 v96, v96, v104
	v_add_f32_e32 v97, v97, v105
	v_lshlrev_b32_e32 v104, 16, v172
	v_and_b32_e32 v105, 0xffff0000, v172
	v_add_f32_e32 v90, v90, v104
	v_add_f32_e32 v91, v91, v105
	v_lshlrev_b32_e32 v104, 16, v173
	v_and_b32_e32 v105, 0xffff0000, v173
	v_add_u32_e32 v102, 0x8080, v0
	v_add_f32_e32 v92, v92, v104
	v_add_f32_e32 v93, v93, v105
	s_and_b64 vcc, exec, s[0:1]
	s_mov_b64 s[24:25], -1
	s_cbranch_vccnz .LBB0_443
	v_mul_f32_e32 v104, v92, v92
	v_mul_f32_e32 v105, v93, v93
	v_mul_f32_e32 v110, v90, v90
	v_mul_f32_e32 v111, v91, v91
	v_fma_f32 v104, v96, v96, v104
	v_fma_f32 v105, v97, v97, v105
	v_fma_f32 v110, v94, v94, v110
	v_fma_f32 v111, v95, v95, v111
	s_mov_b64 s[24:25], 0
	v_pk_mov_b32 v[112:113], v[110:111], v[104:105] op_sel:[1,0]
	v_mov_b32_e32 v111, v105
	v_add_f32_e32 v104, v112, v110
	v_add_f32_e32 v105, v113, v111
	v_cvt_pk_bf16_f32 v110, v94, v95
	v_cvt_pk_bf16_f32 v111, v96, v97
	v_cvt_pk_bf16_f32 v112, v90, v91
	v_cvt_pk_bf16_f32 v113, v92, v93
	s_nop 0
	v_add_f32_e32 v103, v104, v105
	v_add_f32_e32 v103, v103, v115
	v_lshlrev_b32_e32 v104, 1, v102
	global_store_dwordx4 v104, v[110:113], s[12:13]

; #define PG8_GAS __attribute__((address_space(1)))
; #define PG8_PACK8(y0, y1) (u32x4){cvt_pk_bf16((y0)[0], (y0)[1]), cvt_pk_bf16((y0)[2], (y0)[3]), cvt_pk_bf16((y1)[0], (y1)[1]), cvt_pk_bf16((y1)[2], (y1)[3])}
;     __device__ __forceinline__ void operator()(const f32x4 (&acc)[2][2][4][2], const Unit& u, int ui, int wr, int wc, int fr, int fq) const {
;     ...
;                 for (int bj = 0; bj < 2; ++bj) { const unsigned off = (row0 + ai * HALF + m * 16) * 1024u + col0 + bj * HALF;
;                     xw[ai][m][bj] = *(const PG8_GAS u32x4*)((PG8_GAS unsigned char*)ws + E_XB + (size_t)(off * 2u)); }
;         float ssv[2][4];
; #pragma unroll
;         for (int ai = 0; ai < 2; ++ai) {
; #pragma unroll
;             for (int m = 0; m < 4; ++m) {
;                 const unsigned row = row0 + ai * HALF + m * 16; float ss = 0.f;
; #pragma unroll
;                 for (int bj = 0; bj < 2; ++bj) {
;                     const unsigned off = row * 1024u + col0 + bj * HALF;
;                     const u32x4 x4 = xw[ai][m][bj];
;                     f32x4 o0, o1;
;                     o0[0] = __builtin_bit_cast(float, x4[0] << 16) + acc[ai][bj][m][0][0]; o0[1] = __builtin_bit_cast(float, x4[0] & 0xffff0000u) + acc[ai][bj][m][0][1];
;                     o0[2] = __builtin_bit_cast(float, x4[1] << 16) + acc[ai][bj][m][0][2]; o0[3] = __builtin_bit_cast(float, x4[1] & 0xffff0000u) + acc[ai][bj][m][0][3];
;                     o1[0] = __builtin_bit_cast(float, x4[2] << 16) + acc[ai][bj][m][1][0]; o1[1] = __builtin_bit_cast(float, x4[2] & 0xffff0000u) + acc[ai][bj][m][1][1];
;                     o1[2] = __builtin_bit_cast(float, x4[3] << 16) + acc[ai][bj][m][1][2]; o1[3] = __builtin_bit_cast(float, x4[3] & 0xffff0000u) + acc[ai][bj][m][1][3];
;                     if (last) { __builtin_nontemporal_store(o0, (PG8_GAS f32x4*)((PG8_GAS float*)out + (size_t)off)); __builtin_nontemporal_store(o1, (PG8_GAS f32x4*)((PG8_GAS float*)out + (size_t)off + 4)); }
;                     else {
;                         const f32x4 q4 = o0 * o0 + o1 * o1; ss += (q4[0] + q4[1]) + (q4[2] + q4[3]);
;                         *(PG8_GAS u32x4*)((PG8_GAS unsigned char*)ws + E_XB + (size_t)(off * 2u)) = PG8_PACK8(o0, o1);
;                     }
.LBB0_445:
	s_waitcnt vmcnt(15)
	v_lshlrev_b32_e32 v92, 16, v166
	v_and_b32_e32 v93, 0xffff0000, v166
	v_add_f32_e32 v82, v82, v92
	v_add_f32_e32 v83, v83, v93
	v_lshlrev_b32_e32 v92, 16, v167
	v_and_b32_e32 v93, 0xffff0000, v167
	v_add_f32_e32 v84, v84, v92
	v_add_f32_e32 v85, v85, v93
	v_lshlrev_b32_e32 v92, 16, v168
	v_and_b32_e32 v93, 0xffff0000, v168
	v_add_f32_e32 v78, v78, v92
	v_add_f32_e32 v79, v79, v93
	v_lshlrev_b32_e32 v92, 16, v169
	v_and_b32_e32 v93, 0xffff0000, v169
	v_add_u32_e32 v90, 0xc000, v0
	v_add_f32_e32 v80, v80, v92
	v_add_f32_e32 v81, v81, v93
	s_and_b64 vcc, exec, s[0:1]
	s_mov_b64 s[24:25], -1
	s_cbranch_vccnz .LBB0_447
	v_mul_f32_e32 v92, v80, v80
	v_mul_f32_e32 v93, v81, v81
	v_mul_f32_e32 v94, v78, v78
	v_mul_f32_e32 v95, v79, v79
	v_fma_f32 v92, v84, v84, v92
	v_fma_f32 v93, v85, v85, v93
	v_fma_f32 v94, v82, v82, v94
	v_fma_f32 v95, v83, v83, v95
	s_mov_b64 s[24:25], 0
	v_pk_mov_b32 v[96:97], v[94:95], v[92:93] op_sel:[1,0]
	v_mov_b32_e32 v95, v93
	v_add_f32_e32 v92, v96, v94
	v_add_f32_e32 v93, v97, v95
	v_lshlrev_b32_e32 v96, 1, v90
	v_add_f32_e32 v91, v92, v93
	v_cvt_pk_bf16_f32 v92, v82, v83
	v_cvt_pk_bf16_f32 v93, v84, v85
	v_cvt_pk_bf16_f32 v94, v78, v79
	v_cvt_pk_bf16_f32 v95, v80, v81
	global_store_dwordx4 v96, v[92:95], s[12:13]

; #define PG8_GAS __attribute__((address_space(1)))
; #define PG8_PACK8(y0, y1) (u32x4){cvt_pk_bf16((y0)[0], (y0)[1]), cvt_pk_bf16((y0)[2], (y0)[3]), cvt_pk_bf16((y1)[0], (y1)[1]), cvt_pk_bf16((y1)[2], (y1)[3])}
;     __device__ __forceinline__ void operator()(const f32x4 (&acc)[2][2][4][2], const Unit& u, int ui, int wr, int wc, int fr, int fq) const {
;     ...
;                 for (int bj = 0; bj < 2; ++bj) { const unsigned off = (row0 + ai * HALF + m * 16) * 1024u + col0 + bj * HALF;
;                     xw[ai][m][bj] = *(const PG8_GAS u32x4*)((PG8_GAS unsigned char*)ws + E_XB + (size_t)(off * 2u)); }
;         float ssv[2][4];
; #pragma unroll
;         for (int ai = 0; ai < 2; ++ai) {
; #pragma unroll
;             for (int m = 0; m < 4; ++m) {
;                 const unsigned row = row0 + ai * HALF + m * 16; float ss = 0.f;
; #pragma unroll
;                 for (int bj = 0; bj < 2; ++bj) {
;                     const unsigned off = row * 1024u + col0 + bj * HALF;
;                     const u32x4 x4 = xw[ai][m][bj];
;                     f32x4 o0, o1;
;                     o0[0] = __builtin_bit_cast(float, x4[0] << 16) + acc[ai][bj][m][0][0]; o0[1] = __builtin_bit_cast(float, x4[0] & 0xffff0000u) + acc[ai][bj][m][0][1];
;                     o0[2] = __builtin_bit_cast(float, x4[1] << 16) + acc[ai][bj][m][0][2]; o0[3] = __builtin_bit_cast(float, x4[1] & 0xffff0000u) + acc[ai][bj][m][0][3];
;                     o1[0] = __builtin_bit_cast(float, x4[2] << 16) + acc[ai][bj][m][1][0]; o1[1] = __builtin_bit_cast(float, x4[2] & 0xffff0000u) + acc[ai][bj][m][1][1];
;                     o1[2] = __builtin_bit_cast(float, x4[3] << 16) + acc[ai][bj][m][1][2]; o1[3] = __builtin_bit_cast(float, x4[3] & 0xffff0000u) + acc[ai][bj][m][1][3];
;                     if (last) { __builtin_nontemporal_store(o0, (PG8_GAS f32x4*)((PG8_GAS float*)out + (size_t)off)); __builtin_nontemporal_store(o1, (PG8_GAS f32x4*)((PG8_GAS float*)out + (size_t)off + 4)); }
;                     else {
;                         const f32x4 q4 = o0 * o0 + o1 * o1; ss += (q4[0] + q4[1]) + (q4[2] + q4[3]);
;                         *(PG8_GAS u32x4*)((PG8_GAS unsigned char*)ws + E_XB + (size_t)(off * 2u)) = PG8_PACK8(o0, o1);
;                     }
.LBB0_449:
	s_waitcnt vmcnt(15)
	v_lshlrev_b32_e32 v80, 16, v154
	v_and_b32_e32 v81, 0xffff0000, v154
	v_add_f32_e32 v70, v70, v80
	v_add_f32_e32 v71, v71, v81
	v_lshlrev_b32_e32 v80, 16, v155
	v_and_b32_e32 v81, 0xffff0000, v155
	v_add_f32_e32 v72, v72, v80
	v_add_f32_e32 v73, v73, v81
	v_lshlrev_b32_e32 v80, 16, v156
	v_and_b32_e32 v81, 0xffff0000, v156
	v_add_f32_e32 v66, v66, v80
	v_add_f32_e32 v67, v67, v81
	v_lshlrev_b32_e32 v80, 16, v157
	v_and_b32_e32 v81, 0xffff0000, v157
	v_add_u32_e32 v78, 0xc080, v0
	v_add_f32_e32 v68, v68, v80
	v_add_f32_e32 v69, v69, v81
	s_and_b64 vcc, exec, s[0:1]
	s_mov_b64 s[24:25], -1
	s_cbranch_vccnz .LBB0_451
	v_mul_f32_e32 v80, v68, v68
	v_mul_f32_e32 v81, v69, v69
	v_mul_f32_e32 v82, v66, v66
	v_mul_f32_e32 v83, v67, v67
	v_fma_f32 v80, v72, v72, v80
	v_fma_f32 v81, v73, v73, v81
	v_fma_f32 v82, v70, v70, v82
	v_fma_f32 v83, v71, v71, v83
	s_mov_b64 s[24:25], 0
	v_pk_mov_b32 v[84:85], v[82:83], v[80:81] op_sel:[1,0]
	v_mov_b32_e32 v83, v81
	v_add_f32_e32 v80, v84, v82
	v_add_f32_e32 v81, v85, v83
	v_lshlrev_b32_e32 v84, 1, v78
	v_add_f32_e32 v79, v80, v81
	v_add_f32_e32 v79, v79, v91
	v_cvt_pk_bf16_f32 v80, v70, v71
	v_cvt_pk_bf16_f32 v81, v72, v73
	v_cvt_pk_bf16_f32 v82, v66, v67
	v_cvt_pk_bf16_f32 v83, v68, v69
	global_store_dwordx4 v84, v[80:83], s[12:13]

; #define PG8_GAS __attribute__((address_space(1)))
; #define PG8_PACK8(y0, y1) (u32x4){cvt_pk_bf16((y0)[0], (y0)[1]), cvt_pk_bf16((y0)[2], (y0)[3]), cvt_pk_bf16((y1)[0], (y1)[1]), cvt_pk_bf16((y1)[2], (y1)[3])}
;     __device__ __forceinline__ void operator()(const f32x4 (&acc)[2][2][4][2], const Unit& u, int ui, int wr, int wc, int fr, int fq) const {
;     ...
;                 for (int bj = 0; bj < 2; ++bj) { const unsigned off = (row0 + ai * HALF + m * 16) * 1024u + col0 + bj * HALF;
;                     xw[ai][m][bj] = *(const PG8_GAS u32x4*)((PG8_GAS unsigned char*)ws + E_XB + (size_t)(off * 2u)); }
;         float ssv[2][4];
; #pragma unroll
;         for (int ai = 0; ai < 2; ++ai) {
; #pragma unroll
;             for (int m = 0; m < 4; ++m) {
;                 const unsigned row = row0 + ai * HALF + m * 16; float ss = 0.f;
; #pragma unroll
;                 for (int bj = 0; bj < 2; ++bj) {
;                     const unsigned off = row * 1024u + col0 + bj * HALF;
;                     const u32x4 x4 = xw[ai][m][bj];
;                     f32x4 o0, o1;
;                     o0[0] = __builtin_bit_cast(float, x4[0] << 16) + acc[ai][bj][m][0][0]; o0[1] = __builtin_bit_cast(float, x4[0] & 0xffff0000u) + acc[ai][bj][m][0][1];
;                     o0[2] = __builtin_bit_cast(float, x4[1] << 16) + acc[ai][bj][m][0][2]; o0[3] = __builtin_bit_cast(float, x4[1] & 0xffff0000u) + acc[ai][bj][m][0][3];
;                     o1[0] = __builtin_bit_cast(float, x4[2] << 16) + acc[ai][bj][m][1][0]; o1[1] = __builtin_bit_cast(float, x4[2] & 0xffff0000u) + acc[ai][bj][m][1][1];
;                     o1[2] = __builtin_bit_cast(float, x4[3] << 16) + acc[ai][bj][m][1][2]; o1[3] = __builtin_bit_cast(float, x4[3] & 0xffff0000u) + acc[ai][bj][m][1][3];
;                     if (last) { __builtin_nontemporal_store(o0, (PG8_GAS f32x4*)((PG8_GAS float*)out + (size_t)off)); __builtin_nontemporal_store(o1, (PG8_GAS f32x4*)((PG8_GAS float*)out + (size_t)off + 4)); }
;                     else {
;                         const f32x4 q4 = o0 * o0 + o1 * o1; ss += (q4[0] + q4[1]) + (q4[2] + q4[3]);
;                         *(PG8_GAS u32x4*)((PG8_GAS unsigned char*)ws + E_XB + (size_t)(off * 2u)) = PG8_PACK8(o0, o1);
;                     }
.LBB0_453:
	s_waitcnt vmcnt(15)
	v_lshlrev_b32_e32 v68, 16, v150
	v_and_b32_e32 v69, 0xffff0000, v150
	v_add_f32_e32 v62, v62, v68
	v_add_f32_e32 v63, v63, v69
	v_lshlrev_b32_e32 v68, 16, v151
	v_and_b32_e32 v69, 0xffff0000, v151
	v_add_f32_e32 v64, v64, v68
	v_add_f32_e32 v65, v65, v69
	v_lshlrev_b32_e32 v68, 16, v152
	v_and_b32_e32 v69, 0xffff0000, v152
	v_add_f32_e32 v58, v58, v68
	v_add_f32_e32 v59, v59, v69
	v_lshlrev_b32_e32 v68, 16, v153
	v_and_b32_e32 v69, 0xffff0000, v153
	v_add_u32_e32 v66, 0x20000, v0
	v_add_f32_e32 v60, v60, v68
	v_add_f32_e32 v61, v61, v69
	s_and_b64 vcc, exec, s[0:1]
	s_mov_b64 s[24:25], -1
	s_cbranch_vccnz .LBB0_455
	v_mul_f32_e32 v68, v60, v60
	v_mul_f32_e32 v69, v61, v61
	v_mul_f32_e32 v70, v58, v58
	v_mul_f32_e32 v71, v59, v59
	v_fma_f32 v68, v64, v64, v68
	v_fma_f32 v69, v65, v65, v69
	v_fma_f32 v70, v62, v62, v70
	v_fma_f32 v71, v63, v63, v71
	s_mov_b64 s[24:25], 0
	v_pk_mov_b32 v[72:73], v[70:71], v[68:69] op_sel:[1,0]
	v_mov_b32_e32 v71, v69
	v_add_f32_e32 v68, v72, v70
	v_add_f32_e32 v69, v73, v71
	v_lshlrev_b32_e32 v72, 1, v66
	v_add_f32_e32 v67, v68, v69
	v_cvt_pk_bf16_f32 v68, v62, v63
	v_cvt_pk_bf16_f32 v69, v64, v65
	v_cvt_pk_bf16_f32 v70, v58, v59
	v_cvt_pk_bf16_f32 v71, v60, v61
	global_store_dwordx4 v72, v[68:71], s[12:13]

; #define PG8_GAS __attribute__((address_space(1)))
; #define PG8_PACK8(y0, y1) (u32x4){cvt_pk_bf16((y0)[0], (y0)[1]), cvt_pk_bf16((y0)[2], (y0)[3]), cvt_pk_bf16((y1)[0], (y1)[1]), cvt_pk_bf16((y1)[2], (y1)[3])}
;     __device__ __forceinline__ void operator()(const f32x4 (&acc)[2][2][4][2], const Unit& u, int ui, int wr, int wc, int fr, int fq) const {
;     ...
;                 for (int bj = 0; bj < 2; ++bj) { const unsigned off = (row0 + ai * HALF + m * 16) * 1024u + col0 + bj * HALF;
;                     xw[ai][m][bj] = *(const PG8_GAS u32x4*)((PG8_GAS unsigned char*)ws + E_XB + (size_t)(off * 2u)); }
;         float ssv[2][4];
; #pragma unroll
;         for (int ai = 0; ai < 2; ++ai) {
; #pragma unroll
;             for (int m = 0; m < 4; ++m) {
;                 const unsigned row = row0 + ai * HALF + m * 16; float ss = 0.f;
; #pragma unroll
;                 for (int bj = 0; bj < 2; ++bj) {
;                     const unsigned off = row * 1024u + col0 + bj * HALF;
;                     const u32x4 x4 = xw[ai][m][bj];
;                     f32x4 o0, o1;
;                     o0[0] = __builtin_bit_cast(float, x4[0] << 16) + acc[ai][bj][m][0][0]; o0[1] = __builtin_bit_cast(float, x4[0] & 0xffff0000u) + acc[ai][bj][m][0][1];
;                     o0[2] = __builtin_bit_cast(float, x4[1] << 16) + acc[ai][bj][m][0][2]; o0[3] = __builtin_bit_cast(float, x4[1] & 0xffff0000u) + acc[ai][bj][m][0][3];
;                     o1[0] = __builtin_bit_cast(float, x4[2] << 16) + acc[ai][bj][m][1][0]; o1[1] = __builtin_bit_cast(float, x4[2] & 0xffff0000u) + acc[ai][bj][m][1][1];
;                     o1[2] = __builtin_bit_cast(float, x4[3] << 16) + acc[ai][bj][m][1][2]; o1[3] = __builtin_bit_cast(float, x4[3] & 0xffff0000u) + acc[ai][bj][m][1][3];
;                     if (last) { __builtin_nontemporal_store(o0, (PG8_GAS f32x4*)((PG8_GAS float*)out + (size_t)off)); __builtin_nontemporal_store(o1, (PG8_GAS f32x4*)((PG8_GAS float*)out + (size_t)off + 4)); }
;                     else {
;                         const f32x4 q4 = o0 * o0 + o1 * o1; ss += (q4[0] + q4[1]) + (q4[2] + q4[3]);
;                         *(PG8_GAS u32x4*)((PG8_GAS unsigned char*)ws + E_XB + (size_t)(off * 2u)) = PG8_PACK8(o0, o1);
;                     }
.LBB0_457:
	s_waitcnt vmcnt(15)
	v_lshlrev_b32_e32 v60, 16, v142
	v_and_b32_e32 v61, 0xffff0000, v142
	v_add_f32_e32 v54, v54, v60
	v_add_f32_e32 v55, v55, v61
	v_lshlrev_b32_e32 v60, 16, v143
	v_and_b32_e32 v61, 0xffff0000, v143
	v_add_f32_e32 v56, v56, v60
	v_add_f32_e32 v57, v57, v61
	v_lshlrev_b32_e32 v60, 16, v144
	v_and_b32_e32 v61, 0xffff0000, v144
	v_add_f32_e32 v50, v50, v60
	v_add_f32_e32 v51, v51, v61
	v_lshlrev_b32_e32 v60, 16, v145
	v_and_b32_e32 v61, 0xffff0000, v145
	v_add_u32_e32 v58, 0x20080, v0
	v_add_f32_e32 v52, v52, v60
	v_add_f32_e32 v53, v53, v61
	s_and_b64 vcc, exec, s[0:1]
	s_mov_b64 s[24:25], -1
	s_cbranch_vccnz .LBB0_459
	v_mul_f32_e32 v60, v52, v52
	v_mul_f32_e32 v61, v53, v53
	v_mul_f32_e32 v62, v50, v50
	v_mul_f32_e32 v63, v51, v51
	v_fma_f32 v60, v56, v56, v60
	v_fma_f32 v61, v57, v57, v61
	v_fma_f32 v62, v54, v54, v62
	v_fma_f32 v63, v55, v55, v63
	s_mov_b64 s[24:25], 0
	v_pk_mov_b32 v[64:65], v[62:63], v[60:61] op_sel:[1,0]
	v_mov_b32_e32 v63, v61
	v_add_f32_e32 v60, v64, v62
	v_add_f32_e32 v61, v65, v63
	v_lshlrev_b32_e32 v64, 1, v58
	v_add_f32_e32 v59, v60, v61
	v_add_f32_e32 v59, v59, v67
	v_cvt_pk_bf16_f32 v60, v54, v55
	v_cvt_pk_bf16_f32 v61, v56, v57
	v_cvt_pk_bf16_f32 v62, v50, v51
	v_cvt_pk_bf16_f32 v63, v52, v53
	global_store_dwordx4 v64, v[60:63], s[12:13]

; #define PG8_GAS __attribute__((address_space(1)))
; #define PG8_PACK8(y0, y1) (u32x4){cvt_pk_bf16((y0)[0], (y0)[1]), cvt_pk_bf16((y0)[2], (y0)[3]), cvt_pk_bf16((y1)[0], (y1)[1]), cvt_pk_bf16((y1)[2], (y1)[3])}
;     __device__ __forceinline__ void operator()(const f32x4 (&acc)[2][2][4][2], const Unit& u, int ui, int wr, int wc, int fr, int fq) const {
;     ...
;                 for (int bj = 0; bj < 2; ++bj) { const unsigned off = (row0 + ai * HALF + m * 16) * 1024u + col0 + bj * HALF;
;                     xw[ai][m][bj] = *(const PG8_GAS u32x4*)((PG8_GAS unsigned char*)ws + E_XB + (size_t)(off * 2u)); }
;         float ssv[2][4];
; #pragma unroll
;         for (int ai = 0; ai < 2; ++ai) {
; #pragma unroll
;             for (int m = 0; m < 4; ++m) {
;                 const unsigned row = row0 + ai * HALF + m * 16; float ss = 0.f;
; #pragma unroll
;                 for (int bj = 0; bj < 2; ++bj) {
;                     const unsigned off = row * 1024u + col0 + bj * HALF;
;                     const u32x4 x4 = xw[ai][m][bj];
;                     f32x4 o0, o1;
;                     o0[0] = __builtin_bit_cast(float, x4[0] << 16) + acc[ai][bj][m][0][0]; o0[1] = __builtin_bit_cast(float, x4[0] & 0xffff0000u) + acc[ai][bj][m][0][1];
;                     o0[2] = __builtin_bit_cast(float, x4[1] << 16) + acc[ai][bj][m][0][2]; o0[3] = __builtin_bit_cast(float, x4[1] & 0xffff0000u) + acc[ai][bj][m][0][3];
;                     o1[0] = __builtin_bit_cast(float, x4[2] << 16) + acc[ai][bj][m][1][0]; o1[1] = __builtin_bit_cast(float, x4[2] & 0xffff0000u) + acc[ai][bj][m][1][1];
;                     o1[2] = __builtin_bit_cast(float, x4[3] << 16) + acc[ai][bj][m][1][2]; o1[3] = __builtin_bit_cast(float, x4[3] & 0xffff0000u) + acc[ai][bj][m][1][3];
;                     if (last) { __builtin_nontemporal_store(o0, (PG8_GAS f32x4*)((PG8_GAS float*)out + (size_t)off)); __builtin_nontemporal_store(o1, (PG8_GAS f32x4*)((PG8_GAS float*)out + (size_t)off + 4)); }
;                     else {
;                         const f32x4 q4 = o0 * o0 + o1 * o1; ss += (q4[0] + q4[1]) + (q4[2] + q4[3]);
;                         *(PG8_GAS u32x4*)((PG8_GAS unsigned char*)ws + E_XB + (size_t)(off * 2u)) = PG8_PACK8(o0, o1);
;                     }
.LBB0_461:
	s_waitcnt vmcnt(15)
	v_lshlrev_b32_e32 v52, 16, v126
	v_and_b32_e32 v53, 0xffff0000, v126
	v_add_f32_e32 v46, v46, v52
	v_add_f32_e32 v47, v47, v53
	v_lshlrev_b32_e32 v52, 16, v127
	v_and_b32_e32 v53, 0xffff0000, v127
	v_add_f32_e32 v48, v48, v52
	v_add_f32_e32 v49, v49, v53
	v_lshlrev_b32_e32 v52, 16, v128
	v_and_b32_e32 v53, 0xffff0000, v128
	v_add_f32_e32 v42, v42, v52
	v_add_f32_e32 v43, v43, v53
	v_lshlrev_b32_e32 v52, 16, v129
	v_and_b32_e32 v53, 0xffff0000, v129
	v_add_u32_e32 v50, 0x24000, v0
	v_add_f32_e32 v44, v44, v52
	v_add_f32_e32 v45, v45, v53
	s_and_b64 vcc, exec, s[0:1]
	s_mov_b64 s[24:25], -1
	s_cbranch_vccnz .LBB0_463
	v_mul_f32_e32 v52, v44, v44
	v_mul_f32_e32 v53, v45, v45
	v_mul_f32_e32 v54, v42, v42
	v_mul_f32_e32 v55, v43, v43
	v_fma_f32 v52, v48, v48, v52
	v_fma_f32 v53, v49, v49, v53
	v_fma_f32 v54, v46, v46, v54
	v_fma_f32 v55, v47, v47, v55
	s_mov_b64 s[24:25], 0
	v_pk_mov_b32 v[56:57], v[54:55], v[52:53] op_sel:[1,0]
	v_mov_b32_e32 v55, v53
	v_add_f32_e32 v52, v56, v54
	v_add_f32_e32 v53, v57, v55
	v_lshlrev_b32_e32 v56, 1, v50
	v_add_f32_e32 v51, v52, v53
	v_cvt_pk_bf16_f32 v52, v46, v47
	v_cvt_pk_bf16_f32 v53, v48, v49
	v_cvt_pk_bf16_f32 v54, v42, v43
	v_cvt_pk_bf16_f32 v55, v44, v45
	global_store_dwordx4 v56, v[52:55], s[12:13]

; #define PG8_GAS __attribute__((address_space(1)))
; #define PG8_PACK8(y0, y1) (u32x4){cvt_pk_bf16((y0)[0], (y0)[1]), cvt_pk_bf16((y0)[2], (y0)[3]), cvt_pk_bf16((y1)[0], (y1)[1]), cvt_pk_bf16((y1)[2], (y1)[3])}
;     __device__ __forceinline__ void operator()(const f32x4 (&acc)[2][2][4][2], const Unit& u, int ui, int wr, int wc, int fr, int fq) const {
;     ...
;                 for (int bj = 0; bj < 2; ++bj) { const unsigned off = (row0 + ai * HALF + m * 16) * 1024u + col0 + bj * HALF;
;                     xw[ai][m][bj] = *(const PG8_GAS u32x4*)((PG8_GAS unsigned char*)ws + E_XB + (size_t)(off * 2u)); }
;         float ssv[2][4];
; #pragma unroll
;         for (int ai = 0; ai < 2; ++ai) {
; #pragma unroll
;             for (int m = 0; m < 4; ++m) {
;                 const unsigned row = row0 + ai * HALF + m * 16; float ss = 0.f;
; #pragma unroll
;                 for (int bj = 0; bj < 2; ++bj) {
;                     const unsigned off = row * 1024u + col0 + bj * HALF;
;                     const u32x4 x4 = xw[ai][m][bj];
;                     f32x4 o0, o1;
;                     o0[0] = __builtin_bit_cast(float, x4[0] << 16) + acc[ai][bj][m][0][0]; o0[1] = __builtin_bit_cast(float, x4[0] & 0xffff0000u) + acc[ai][bj][m][0][1];
;                     o0[2] = __builtin_bit_cast(float, x4[1] << 16) + acc[ai][bj][m][0][2]; o0[3] = __builtin_bit_cast(float, x4[1] & 0xffff0000u) + acc[ai][bj][m][0][3];
;                     o1[0] = __builtin_bit_cast(float, x4[2] << 16) + acc[ai][bj][m][1][0]; o1[1] = __builtin_bit_cast(float, x4[2] & 0xffff0000u) + acc[ai][bj][m][1][1];
;                     o1[2] = __builtin_bit_cast(float, x4[3] << 16) + acc[ai][bj][m][1][2]; o1[3] = __builtin_bit_cast(float, x4[3] & 0xffff0000u) + acc[ai][bj][m][1][3];
;                     if (last) { __builtin_nontemporal_store(o0, (PG8_GAS f32x4*)((PG8_GAS float*)out + (size_t)off)); __builtin_nontemporal_store(o1, (PG8_GAS f32x4*)((PG8_GAS float*)out + (size_t)off + 4)); }
;                     else {
;                         const f32x4 q4 = o0 * o0 + o1 * o1; ss += (q4[0] + q4[1]) + (q4[2] + q4[3]);
;                         *(PG8_GAS u32x4*)((PG8_GAS unsigned char*)ws + E_XB + (size_t)(off * 2u)) = PG8_PACK8(o0, o1);
;                     }
.LBB0_465:
	s_waitcnt vmcnt(15)
	v_lshlrev_b32_e32 v44, 16, v122
	v_and_b32_e32 v45, 0xffff0000, v122
	v_add_f32_e32 v38, v38, v44
	v_add_f32_e32 v39, v39, v45
	v_lshlrev_b32_e32 v44, 16, v123
	v_and_b32_e32 v45, 0xffff0000, v123
	v_add_f32_e32 v40, v40, v44
	v_add_f32_e32 v41, v41, v45
	v_lshlrev_b32_e32 v44, 16, v124
	v_and_b32_e32 v45, 0xffff0000, v124
	v_add_f32_e32 v34, v34, v44
	v_add_f32_e32 v35, v35, v45
	v_lshlrev_b32_e32 v44, 16, v125
	v_and_b32_e32 v45, 0xffff0000, v125
	v_add_u32_e32 v42, 0x24080, v0
	v_add_f32_e32 v36, v36, v44
	v_add_f32_e32 v37, v37, v45
	s_and_b64 vcc, exec, s[0:1]
	s_mov_b64 s[24:25], -1
	s_cbranch_vccnz .LBB0_467
	v_mul_f32_e32 v44, v36, v36
	v_mul_f32_e32 v45, v37, v37
	v_mul_f32_e32 v46, v34, v34
	v_mul_f32_e32 v47, v35, v35
	v_fma_f32 v44, v40, v40, v44
	v_fma_f32 v45, v41, v41, v45
	v_fma_f32 v46, v38, v38, v46
	v_fma_f32 v47, v39, v39, v47
	s_mov_b64 s[24:25], 0
	v_pk_mov_b32 v[48:49], v[46:47], v[44:45] op_sel:[1,0]
	v_mov_b32_e32 v47, v45
	v_add_f32_e32 v44, v48, v46
	v_add_f32_e32 v45, v49, v47
	v_lshlrev_b32_e32 v48, 1, v42
	v_add_f32_e32 v43, v44, v45
	v_add_f32_e32 v43, v43, v51
	v_cvt_pk_bf16_f32 v44, v38, v39
	v_cvt_pk_bf16_f32 v45, v40, v41
	v_cvt_pk_bf16_f32 v46, v34, v35
	v_cvt_pk_bf16_f32 v47, v36, v37
	global_store_dwordx4 v48, v[44:47], s[12:13]

; #define PG8_GAS __attribute__((address_space(1)))
; #define PG8_PACK8(y0, y1) (u32x4){cvt_pk_bf16((y0)[0], (y0)[1]), cvt_pk_bf16((y0)[2], (y0)[3]), cvt_pk_bf16((y1)[0], (y1)[1]), cvt_pk_bf16((y1)[2], (y1)[3])}
;     __device__ __forceinline__ void operator()(const f32x4 (&acc)[2][2][4][2], const Unit& u, int ui, int wr, int wc, int fr, int fq) const {
;     ...
;                 for (int bj = 0; bj < 2; ++bj) { const unsigned off = (row0 + ai * HALF + m * 16) * 1024u + col0 + bj * HALF;
;                     xw[ai][m][bj] = *(const PG8_GAS u32x4*)((PG8_GAS unsigned char*)ws + E_XB + (size_t)(off * 2u)); }
;         float ssv[2][4];
; #pragma unroll
;         for (int ai = 0; ai < 2; ++ai) {
; #pragma unroll
;             for (int m = 0; m < 4; ++m) {
;                 const unsigned row = row0 + ai * HALF + m * 16; float ss = 0.f;
; #pragma unroll
;                 for (int bj = 0; bj < 2; ++bj) {
;                     const unsigned off = row * 1024u + col0 + bj * HALF;
;                     const u32x4 x4 = xw[ai][m][bj];
;                     f32x4 o0, o1;
;                     o0[0] = __builtin_bit_cast(float, x4[0] << 16) + acc[ai][bj][m][0][0]; o0[1] = __builtin_bit_cast(float, x4[0] & 0xffff0000u) + acc[ai][bj][m][0][1];
;                     o0[2] = __builtin_bit_cast(float, x4[1] << 16) + acc[ai][bj][m][0][2]; o0[3] = __builtin_bit_cast(float, x4[1] & 0xffff0000u) + acc[ai][bj][m][0][3];
;                     o1[0] = __builtin_bit_cast(float, x4[2] << 16) + acc[ai][bj][m][1][0]; o1[1] = __builtin_bit_cast(float, x4[2] & 0xffff0000u) + acc[ai][bj][m][1][1];
;                     o1[2] = __builtin_bit_cast(float, x4[3] << 16) + acc[ai][bj][m][1][2]; o1[3] = __builtin_bit_cast(float, x4[3] & 0xffff0000u) + acc[ai][bj][m][1][3];
;                     if (last) { __builtin_nontemporal_store(o0, (PG8_GAS f32x4*)((PG8_GAS float*)out + (size_t)off)); __builtin_nontemporal_store(o1, (PG8_GAS f32x4*)((PG8_GAS float*)out + (size_t)off + 4)); }
;                     else {
;                         const f32x4 q4 = o0 * o0 + o1 * o1; ss += (q4[0] + q4[1]) + (q4[2] + q4[3]);
;                         *(PG8_GAS u32x4*)((PG8_GAS unsigned char*)ws + E_XB + (size_t)(off * 2u)) = PG8_PACK8(o0, o1);
;                     }
.LBB0_469:
	s_waitcnt vmcnt(15)
	v_lshlrev_b32_e32 v36, 16, v106
	v_and_b32_e32 v37, 0xffff0000, v106
	v_add_f32_e32 v30, v30, v36
	v_add_f32_e32 v31, v31, v37
	v_lshlrev_b32_e32 v36, 16, v107
	v_and_b32_e32 v37, 0xffff0000, v107
	v_add_f32_e32 v32, v32, v36
	v_add_f32_e32 v33, v33, v37
	v_lshlrev_b32_e32 v36, 16, v108
	v_and_b32_e32 v37, 0xffff0000, v108
	v_add_f32_e32 v26, v26, v36
	v_add_f32_e32 v27, v27, v37
	v_lshlrev_b32_e32 v36, 16, v109
	v_and_b32_e32 v37, 0xffff0000, v109
	v_add_u32_e32 v34, 0x28000, v0
	v_add_f32_e32 v28, v28, v36
	v_add_f32_e32 v29, v29, v37
	s_and_b64 vcc, exec, s[0:1]
	s_mov_b64 s[24:25], -1
	s_cbranch_vccnz .LBB0_471
	v_mul_f32_e32 v36, v28, v28
	v_mul_f32_e32 v37, v29, v29
	v_mul_f32_e32 v38, v26, v26
	v_mul_f32_e32 v39, v27, v27
	v_fma_f32 v36, v32, v32, v36
	v_fma_f32 v37, v33, v33, v37
	v_fma_f32 v38, v30, v30, v38
	v_fma_f32 v39, v31, v31, v39
	s_mov_b64 s[24:25], 0
	v_pk_mov_b32 v[40:41], v[38:39], v[36:37] op_sel:[1,0]
	v_mov_b32_e32 v39, v37
	v_add_f32_e32 v36, v40, v38
	v_add_f32_e32 v37, v41, v39
	v_lshlrev_b32_e32 v40, 1, v34
	v_add_f32_e32 v35, v36, v37
	v_cvt_pk_bf16_f32 v36, v30, v31
	v_cvt_pk_bf16_f32 v37, v32, v33
	v_cvt_pk_bf16_f32 v38, v26, v27
	v_cvt_pk_bf16_f32 v39, v28, v29
	global_store_dwordx4 v40, v[36:39], s[12:13]

; #define PG8_GAS __attribute__((address_space(1)))
; #define PG8_PACK8(y0, y1) (u32x4){cvt_pk_bf16((y0)[0], (y0)[1]), cvt_pk_bf16((y0)[2], (y0)[3]), cvt_pk_bf16((y1)[0], (y1)[1]), cvt_pk_bf16((y1)[2], (y1)[3])}
;     __device__ __forceinline__ void operator()(const f32x4 (&acc)[2][2][4][2], const Unit& u, int ui, int wr, int wc, int fr, int fq) const {
;     ...
;                 for (int bj = 0; bj < 2; ++bj) { const unsigned off = (row0 + ai * HALF + m * 16) * 1024u + col0 + bj * HALF;
;                     xw[ai][m][bj] = *(const PG8_GAS u32x4*)((PG8_GAS unsigned char*)ws + E_XB + (size_t)(off * 2u)); }
;         float ssv[2][4];
; #pragma unroll
;         for (int ai = 0; ai < 2; ++ai) {
; #pragma unroll
;             for (int m = 0; m < 4; ++m) {
;                 const unsigned row = row0 + ai * HALF + m * 16; float ss = 0.f;
; #pragma unroll
;                 for (int bj = 0; bj < 2; ++bj) {
;                     const unsigned off = row * 1024u + col0 + bj * HALF;
;                     const u32x4 x4 = xw[ai][m][bj];
;                     f32x4 o0, o1;
;                     o0[0] = __builtin_bit_cast(float, x4[0] << 16) + acc[ai][bj][m][0][0]; o0[1] = __builtin_bit_cast(float, x4[0] & 0xffff0000u) + acc[ai][bj][m][0][1];
;                     o0[2] = __builtin_bit_cast(float, x4[1] << 16) + acc[ai][bj][m][0][2]; o0[3] = __builtin_bit_cast(float, x4[1] & 0xffff0000u) + acc[ai][bj][m][0][3];
;                     o1[0] = __builtin_bit_cast(float, x4[2] << 16) + acc[ai][bj][m][1][0]; o1[1] = __builtin_bit_cast(float, x4[2] & 0xffff0000u) + acc[ai][bj][m][1][1];
;                     o1[2] = __builtin_bit_cast(float, x4[3] << 16) + acc[ai][bj][m][1][2]; o1[3] = __builtin_bit_cast(float, x4[3] & 0xffff0000u) + acc[ai][bj][m][1][3];
;                     if (last) { __builtin_nontemporal_store(o0, (PG8_GAS f32x4*)((PG8_GAS float*)out + (size_t)off)); __builtin_nontemporal_store(o1, (PG8_GAS f32x4*)((PG8_GAS float*)out + (size_t)off + 4)); }
;                     else {
;                         const f32x4 q4 = o0 * o0 + o1 * o1; ss += (q4[0] + q4[1]) + (q4[2] + q4[3]);
;                         *(PG8_GAS u32x4*)((PG8_GAS unsigned char*)ws + E_XB + (size_t)(off * 2u)) = PG8_PACK8(o0, o1);
;                     }
.LBB0_473:
	s_waitcnt vmcnt(15)
	v_lshlrev_b32_e32 v28, 16, v98
	v_and_b32_e32 v29, 0xffff0000, v98
	v_add_f32_e32 v22, v22, v28
	v_add_f32_e32 v23, v23, v29
	v_lshlrev_b32_e32 v28, 16, v99
	v_and_b32_e32 v29, 0xffff0000, v99
	v_add_f32_e32 v24, v24, v28
	v_add_f32_e32 v25, v25, v29
	v_lshlrev_b32_e32 v28, 16, v100
	v_and_b32_e32 v29, 0xffff0000, v100
	v_add_f32_e32 v18, v18, v28
	v_add_f32_e32 v19, v19, v29
	v_lshlrev_b32_e32 v28, 16, v101
	v_and_b32_e32 v29, 0xffff0000, v101
	v_add_u32_e32 v26, 0x28080, v0
	v_add_f32_e32 v20, v20, v28
	v_add_f32_e32 v21, v21, v29
	s_and_b64 vcc, exec, s[0:1]
	s_mov_b64 s[24:25], -1
	s_cbranch_vccnz .LBB0_475
	v_mul_f32_e32 v28, v20, v20
	v_mul_f32_e32 v29, v21, v21
	v_mul_f32_e32 v30, v18, v18
	v_mul_f32_e32 v31, v19, v19
	v_fma_f32 v28, v24, v24, v28
	v_fma_f32 v29, v25, v25, v29
	v_fma_f32 v30, v22, v22, v30
	v_fma_f32 v31, v23, v23, v31
	s_mov_b64 s[24:25], 0
	v_pk_mov_b32 v[32:33], v[30:31], v[28:29] op_sel:[1,0]
	v_mov_b32_e32 v31, v29
	v_add_f32_e32 v28, v32, v30
	v_add_f32_e32 v29, v33, v31
	v_lshlrev_b32_e32 v32, 1, v26
	v_add_f32_e32 v27, v28, v29
	v_add_f32_e32 v27, v27, v35
	v_cvt_pk_bf16_f32 v28, v22, v23
	v_cvt_pk_bf16_f32 v29, v24, v25
	v_cvt_pk_bf16_f32 v30, v18, v19
	v_cvt_pk_bf16_f32 v31, v20, v21
	global_store_dwordx4 v32, v[28:31], s[12:13]

; #define PG8_GAS __attribute__((address_space(1)))
; #define PG8_PACK8(y0, y1) (u32x4){cvt_pk_bf16((y0)[0], (y0)[1]), cvt_pk_bf16((y0)[2], (y0)[3]), cvt_pk_bf16((y1)[0], (y1)[1]), cvt_pk_bf16((y1)[2], (y1)[3])}
;     __device__ __forceinline__ void operator()(const f32x4 (&acc)[2][2][4][2], const Unit& u, int ui, int wr, int wc, int fr, int fq) const {
;     ...
;                 for (int bj = 0; bj < 2; ++bj) { const unsigned off = (row0 + ai * HALF + m * 16) * 1024u + col0 + bj * HALF;
;                     xw[ai][m][bj] = *(const PG8_GAS u32x4*)((PG8_GAS unsigned char*)ws + E_XB + (size_t)(off * 2u)); }
;         float ssv[2][4];
; #pragma unroll
;         for (int ai = 0; ai < 2; ++ai) {
; #pragma unroll
;             for (int m = 0; m < 4; ++m) {
;                 const unsigned row = row0 + ai * HALF + m * 16; float ss = 0.f;
; #pragma unroll
;                 for (int bj = 0; bj < 2; ++bj) {
;                     const unsigned off = row * 1024u + col0 + bj * HALF;
;                     const u32x4 x4 = xw[ai][m][bj];
;                     f32x4 o0, o1;
;                     o0[0] = __builtin_bit_cast(float, x4[0] << 16) + acc[ai][bj][m][0][0]; o0[1] = __builtin_bit_cast(float, x4[0] & 0xffff0000u) + acc[ai][bj][m][0][1];
;                     o0[2] = __builtin_bit_cast(float, x4[1] << 16) + acc[ai][bj][m][0][2]; o0[3] = __builtin_bit_cast(float, x4[1] & 0xffff0000u) + acc[ai][bj][m][0][3];
;                     o1[0] = __builtin_bit_cast(float, x4[2] << 16) + acc[ai][bj][m][1][0]; o1[1] = __builtin_bit_cast(float, x4[2] & 0xffff0000u) + acc[ai][bj][m][1][1];
;                     o1[2] = __builtin_bit_cast(float, x4[3] << 16) + acc[ai][bj][m][1][2]; o1[3] = __builtin_bit_cast(float, x4[3] & 0xffff0000u) + acc[ai][bj][m][1][3];
;                     if (last) { __builtin_nontemporal_store(o0, (PG8_GAS f32x4*)((PG8_GAS float*)out + (size_t)off)); __builtin_nontemporal_store(o1, (PG8_GAS f32x4*)((PG8_GAS float*)out + (size_t)off + 4)); }
;                     else {
;                         const f32x4 q4 = o0 * o0 + o1 * o1; ss += (q4[0] + q4[1]) + (q4[2] + q4[3]);
;                         *(PG8_GAS u32x4*)((PG8_GAS unsigned char*)ws + E_XB + (size_t)(off * 2u)) = PG8_PACK8(o0, o1);
;                     }
.LBB0_477:
	s_waitcnt vmcnt(15)
	v_lshlrev_b32_e32 v20, 16, v86
	v_and_b32_e32 v21, 0xffff0000, v86
	v_add_f32_e32 v14, v14, v20
	v_add_f32_e32 v15, v15, v21
	v_lshlrev_b32_e32 v20, 16, v87
	v_and_b32_e32 v21, 0xffff0000, v87
	v_add_f32_e32 v16, v16, v20
	v_add_f32_e32 v17, v17, v21
	v_lshlrev_b32_e32 v20, 16, v88
	v_and_b32_e32 v21, 0xffff0000, v88
	v_add_f32_e32 v10, v10, v20
	v_add_f32_e32 v11, v11, v21
	v_lshlrev_b32_e32 v20, 16, v89
	v_and_b32_e32 v21, 0xffff0000, v89
	v_add_u32_e32 v18, 0x2c000, v0
	v_add_f32_e32 v12, v12, v20
	v_add_f32_e32 v13, v13, v21
	s_and_b64 vcc, exec, s[0:1]
	s_mov_b64 s[24:25], -1
	s_cbranch_vccnz .LBB0_479
	v_mul_f32_e32 v20, v12, v12
	v_mul_f32_e32 v21, v13, v13
	v_mul_f32_e32 v22, v10, v10
	v_mul_f32_e32 v23, v11, v11
	v_fma_f32 v20, v16, v16, v20
	v_fma_f32 v21, v17, v17, v21
	v_fma_f32 v22, v14, v14, v22
	v_fma_f32 v23, v15, v15, v23
	s_mov_b64 s[24:25], 0
	v_pk_mov_b32 v[24:25], v[22:23], v[20:21] op_sel:[1,0]
	v_mov_b32_e32 v23, v21
	v_add_f32_e32 v20, v24, v22
	v_add_f32_e32 v21, v25, v23
	v_lshlrev_b32_e32 v24, 1, v18
	v_add_f32_e32 v19, v20, v21
	v_cvt_pk_bf16_f32 v20, v14, v15
	v_cvt_pk_bf16_f32 v21, v16, v17
	v_cvt_pk_bf16_f32 v22, v10, v11
	v_cvt_pk_bf16_f32 v23, v12, v13
	global_store_dwordx4 v24, v[20:23], s[12:13]

; #define PG8_GAS __attribute__((address_space(1)))
; #define PG8_PACK8(y0, y1) (u32x4){cvt_pk_bf16((y0)[0], (y0)[1]), cvt_pk_bf16((y0)[2], (y0)[3]), cvt_pk_bf16((y1)[0], (y1)[1]), cvt_pk_bf16((y1)[2], (y1)[3])}
;     __device__ __forceinline__ void operator()(const f32x4 (&acc)[2][2][4][2], const Unit& u, int ui, int wr, int wc, int fr, int fq) const {
;     ...
;                 for (int bj = 0; bj < 2; ++bj) { const unsigned off = (row0 + ai * HALF + m * 16) * 1024u + col0 + bj * HALF;
;                     xw[ai][m][bj] = *(const PG8_GAS u32x4*)((PG8_GAS unsigned char*)ws + E_XB + (size_t)(off * 2u)); }
;         float ssv[2][4];
; #pragma unroll
;         for (int ai = 0; ai < 2; ++ai) {
; #pragma unroll
;             for (int m = 0; m < 4; ++m) {
;                 const unsigned row = row0 + ai * HALF + m * 16; float ss = 0.f;
; #pragma unroll
;                 for (int bj = 0; bj < 2; ++bj) {
;                     const unsigned off = row * 1024u + col0 + bj * HALF;
;                     const u32x4 x4 = xw[ai][m][bj];
;                     f32x4 o0, o1;
;                     o0[0] = __builtin_bit_cast(float, x4[0] << 16) + acc[ai][bj][m][0][0]; o0[1] = __builtin_bit_cast(float, x4[0] & 0xffff0000u) + acc[ai][bj][m][0][1];
;                     o0[2] = __builtin_bit_cast(float, x4[1] << 16) + acc[ai][bj][m][0][2]; o0[3] = __builtin_bit_cast(float, x4[1] & 0xffff0000u) + acc[ai][bj][m][0][3];
;                     o1[0] = __builtin_bit_cast(float, x4[2] << 16) + acc[ai][bj][m][1][0]; o1[1] = __builtin_bit_cast(float, x4[2] & 0xffff0000u) + acc[ai][bj][m][1][1];
;                     o1[2] = __builtin_bit_cast(float, x4[3] << 16) + acc[ai][bj][m][1][2]; o1[3] = __builtin_bit_cast(float, x4[3] & 0xffff0000u) + acc[ai][bj][m][1][3];
;                     if (last) { __builtin_nontemporal_store(o0, (PG8_GAS f32x4*)((PG8_GAS float*)out + (size_t)off)); __builtin_nontemporal_store(o1, (PG8_GAS f32x4*)((PG8_GAS float*)out + (size_t)off + 4)); }
;                     else {
;                         const f32x4 q4 = o0 * o0 + o1 * o1; ss += (q4[0] + q4[1]) + (q4[2] + q4[3]);
;                         *(PG8_GAS u32x4*)((PG8_GAS unsigned char*)ws + E_XB + (size_t)(off * 2u)) = PG8_PACK8(o0, o1);
;                     }
.LBB0_481:
	s_waitcnt vmcnt(15)
	v_lshlrev_b32_e32 v10, 16, v74
	v_and_b32_e32 v11, 0xffff0000, v74
	v_add_f32_e32 v6, v6, v10
	v_add_f32_e32 v7, v7, v11
	v_lshlrev_b32_e32 v10, 16, v75
	v_and_b32_e32 v11, 0xffff0000, v75
	v_add_f32_e32 v8, v8, v10
	v_add_f32_e32 v9, v9, v11
	v_lshlrev_b32_e32 v10, 16, v76
	v_and_b32_e32 v11, 0xffff0000, v76
	v_add_f32_e32 v2, v2, v10
	v_add_f32_e32 v3, v3, v11
	v_lshlrev_b32_e32 v10, 16, v77
	v_and_b32_e32 v11, 0xffff0000, v77
	v_add_u32_e32 v0, 0x2c080, v0
	v_add_f32_e32 v4, v4, v10
	v_add_f32_e32 v5, v5, v11
	s_and_b64 vcc, exec, s[0:1]
	s_mov_b64 s[24:25], -1
	s_cbranch_vccnz .LBB0_487
	v_mul_f32_e32 v10, v4, v4
	v_mul_f32_e32 v11, v5, v5
	v_mul_f32_e32 v12, v2, v2
	v_mul_f32_e32 v13, v3, v3
	v_fma_f32 v10, v8, v8, v10
	v_fma_f32 v11, v9, v9, v11
	v_fma_f32 v12, v6, v6, v12
	v_fma_f32 v13, v7, v7, v13
	s_nop 0
	v_pk_mov_b32 v[14:15], v[12:13], v[10:11] op_sel:[1,0]
	v_mov_b32_e32 v13, v11
	v_add_f32_e32 v10, v14, v12
	v_add_f32_e32 v11, v15, v13
	v_cvt_pk_bf16_f32 v12, v6, v7
	v_cvt_pk_bf16_f32 v13, v8, v9
	v_cvt_pk_bf16_f32 v14, v2, v3
	v_cvt_pk_bf16_f32 v15, v4, v5
	s_nop 0
	v_add_f32_e32 v10, v10, v11
	v_add_f32_e32 v10, v10, v19
	v_lshlrev_b32_e32 v11, 1, v0
	global_store_dwordx4 v11, v[12:15], s[12:13]
	s_cbranch_execz .LBB0_488

; __device__ __forceinline__ float row_rstd(const float* ssq, unsigned row) {
;     const float* p = ssq + (size_t)(row * 16u);
;     const f32x4 a = *(const f32x4*)(p), b = *(const f32x4*)(p + 4), c = *(const f32x4*)(p + 8), d = *(const f32x4*)(p + 12);
;     const float s = ((a[0] + a[1]) + (a[2] + a[3])) + ((b[0] + b[1]) + (b[2] + b[3])) + ((c[0] + c[1]) + (c[2] + c[3])) + ((d[0] + d[1]) + (d[2] + d[3]));
;     return 1.0f / sqrtf(s * (1.0f / 1024.0f) + RMS_EPS);
; }
.LBB0_501:
	s_movk_i32 s0, 0x100
	v_mov_b32_e32 v0, s8
	s_waitcnt vmcnt(0)
	v_mov_b32_e32 v2, s42
	v_cmp_gt_u32_e32 vcc, s0, v232
	s_waitcnt lgkmcnt(0)
	v_lshlrev_b32_e32 v8, 4, v232
	v_cndmask_b32_e32 v0, v0, v2, vcc
	v_cmp_lt_i32_e32 vcc, -1, v0
	s_and_saveexec_b64 s[6:7], vcc
	s_cbranch_execz .LBB0_503
	v_and_b32_e32 v2, 0xff0, v8
	v_lshl_or_b32 v0, v0, 12, v2
	v_lshl_add_u64 v[2:3], v[0:1], 2, s[74:75]
	s_mov_b64 s[0:1], 0x3400000
	v_lshl_add_u64 v[6:7], v[2:3], 0, s[0:1]
	v_add_co_u32_e32 v2, vcc, 0x3400000, v2
	s_mov_b32 s0, 0xf800000
	s_nop 0
	v_addc_co_u32_e32 v3, vcc, 0, v3, vcc
	flat_load_dwordx4 v[2:5], v[2:3]
	s_nop 0
	flat_load_dwordx4 v[10:13], v[6:7] offset:16
	flat_load_dwordx4 v[14:17], v[6:7] offset:32
	flat_load_dwordx4 v[18:21], v[6:7] offset:48
	s_waitcnt vmcnt(0) lgkmcnt(0)
	v_mov_b32_e32 v6, v3
	v_mov_b32_e32 v7, v4
	v_mov_b32_e32 v3, v5
	v_mov_b32_e32 v4, v11
	v_mov_b32_e32 v5, v12
	v_mov_b32_e32 v11, v13
	v_add_f32_e32 v2, v6, v2
	v_add_f32_e32 v3, v7, v3
	v_add_f32_e32 v4, v4, v10
	v_add_f32_e32 v5, v5, v11
	v_pk_add_f32 v[2:3], v[2:3], v[2:3] op_sel:[0,1] op_sel_hi:[1,0]
	v_pk_add_f32 v[4:5], v[4:5], v[4:5] op_sel:[0,1] op_sel_hi:[1,0]
	v_add_f32_e32 v6, v14, v15
	v_add_f32_e32 v10, v16, v17
	v_mov_b32_e32 v3, v18
	v_mov_b32_e32 v5, v19
	v_mov_b32_e32 v7, v20
	v_mov_b32_e32 v11, v21
	v_add_f32_e32 v2, v2, v4
	v_add_f32_e32 v3, v3, v5
	v_add_f32_e32 v4, v6, v10
	v_add_f32_e32 v5, v7, v11
	s_nop 0
	v_add_f32_e32 v2, v2, v4
	v_add_f32_e32 v3, v3, v5
	s_nop 0
	v_add_f32_e32 v0, v2, v3
	v_fmamk_f32 v0, v0, 0x3a800000, v215
	v_cmp_gt_f32_e32 vcc, s0, v0
	v_mul_f32_e32 v2, 0x4f800000, v0
	s_nop 0
	v_cndmask_b32_e32 v0, v0, v2, vcc
	v_sqrt_f32_e32 v2, v0
	s_nop 0
	v_add_u32_e32 v3, -1, v2
	v_fma_f32 v4, -v3, v2, v0
	v_cmp_ge_f32_e64 s[0:1], 0, v4
	v_add_u32_e32 v4, 1, v2
	s_nop 0
	v_cndmask_b32_e64 v3, v2, v3, s[0:1]
	v_fma_f32 v2, -v4, v2, v0
	v_cmp_lt_f32_e64 s[0:1], 0, v2
	s_nop 1
	v_cndmask_b32_e64 v2, v3, v4, s[0:1]
	v_mul_f32_e32 v3, 0x37800000, v2
	v_cndmask_b32_e32 v2, v2, v3, vcc
	v_cmp_class_f32_e32 vcc, v0, v216
	s_nop 1
	v_cndmask_b32_e32 v0, v2, v0, vcc
	v_div_scale_f32 v2, s[0:1], v0, v0, 1.0
	v_rcp_f32_e32 v3, v2
	s_nop 0
	v_fma_f32 v4, -v2, v3, 1.0
	v_fmac_f32_e32 v3, v4, v3
	v_div_scale_f32 v4, vcc, 1.0, v0, 1.0
	v_mul_f32_e32 v5, v4, v3
	v_fma_f32 v6, -v2, v5, v4
	v_fmac_f32_e32 v5, v6, v3
	v_fma_f32 v2, -v2, v5, v4
	v_div_fmas_f32 v2, v2, v3, v5
	v_div_fixup_f32 v0, v2, v0, 1.0
	v_lshl_add_u32 v2, v232, 2, v238
	ds_write_b32 v2, v0

; #define PG8_PACK8(y0, y1) (u32x4){cvt_pk_bf16((y0)[0], (y0)[1]), cvt_pk_bf16((y0)[2], (y0)[3]), cvt_pk_bf16((y1)[0], (y1)[1]), cvt_pk_bf16((y1)[2], (y1)[3])}
;     __device__ __forceinline__ void operator()(const f32x4 (&acc)[2][2][4][2], const Unit& u, int ui, int wr, int wc, int fr, int fq) const {
;     ...
;         } else {
; #pragma unroll
;             for (int ai = 0; ai < 2; ++ai)
; #pragma unroll
;                 for (int m = 0; m < 4; ++m) {
;                     const unsigned row = row0 + ai * HALF + m * 16; const float rs = rsp[ai * HALF + m * 16];
; #pragma unroll
;                     for (int bj = 0; bj < 2; ++bj) {
;                         const f32x4 y0 = acc[ai][bj][m][0] * rs, y1 = acc[ai][bj][m][1] * rs;
;                         if (pn == 12 || bj == 0) {
;                             const unsigned gcol = (unsigned)((pn == 12 ? 0 : 256) + 128 * bj + 32 * wc + 8 * fq);
;                             f32x4 s0, s1;
; #pragma unroll
;                             for (int e = 0; e < 4; ++e) { s0[e] = __builtin_amdgcn_rcpf(1.0f + __builtin_amdgcn_exp2f(y0[e] * -1.4426950408889634f)); s1[e] = __builtin_amdgcn_rcpf(1.0f + __builtin_amdgcn_exp2f(y1[e] * -1.4426950408889634f)); }
;                             *(u32x4*)(ws + E_GF + (size_t)((row * 384u + gcol) * 2u)) = PG8_PACK8(s0, s1);
.LBB0_559:
	s_cmp_eq_u32 s4, s42
	s_cselect_b32 s19, 0, 0x400
	v_lshl_add_u32 v158, s4, 8, v163
	v_add_u32_e32 v160, s19, v181
	s_cmp_gt_i32 s26, 7
	s_mov_b64 s[28:29], -1
	s_cbranch_scc0 .LBB0_613
	s_cmp_lt_u32 s26, 12
	s_cbranch_scc1 .LBB0_610
	ds_read_b32 v140, v160
	s_cmp_lg_u32 s26, 12
	s_cselect_b64 s[28:29], -1, 0
	s_cmp_eq_u32 s26, 12
	s_cselect_b32 s19, 0, 0x100
	s_waitcnt lgkmcnt(0)
	v_mul_f32_e32 v130, v124, v140
	v_mul_f32_e32 v131, v125, v140
	v_mul_f32_e32 v134, v126, v140
	v_mul_f32_e32 v135, v127, v140
	v_mul_f32_e32 v136, v128, v140
	v_mul_f32_e32 v137, v129, v140
	v_mul_f32_e32 v130, 0xbfb8aa3b, v130
	v_mul_f32_e32 v0, 0xbfb8aa3b, v134
	v_mul_f32_e32 v134, 0xbfb8aa3b, v135
	v_mul_f32_e32 v135, 0xbfb8aa3b, v136
	v_exp_f32_e32 v130, v130
	v_mul_f32_e32 v136, 0xbfb8aa3b, v137
	v_mul_f32_e32 v132, v122, v140
	v_mul_f32_e32 v133, v123, v140
	v_exp_f32_e32 v0, v0
	v_exp_f32_e32 v136, v136
	v_mul_f32_e32 v131, 0xbfb8aa3b, v131
	v_mul_f32_e32 v132, 0xbfb8aa3b, v132
	v_exp_f32_e32 v134, v134
	v_mul_f32_e32 v133, 0xbfb8aa3b, v133
	v_exp_f32_e32 v135, v135
	v_exp_f32_e32 v131, v131
	v_exp_f32_e32 v132, v132
	v_exp_f32_e32 v133, v133
	v_add_f32_e32 v130, 1.0, v130
	v_or_b32_e32 v161, s19, v237
	s_movk_i32 s19, 0x180
	v_add_f32_e32 v0, 1.0, v0
	v_rcp_f32_e32 v137, v130
	v_add_f32_e32 v130, 1.0, v136
	v_mul_lo_u32 v144, v158, s19
	v_rcp_f32_e32 v0, v0
	v_add_f32_e32 v134, 1.0, v134
	v_add_f32_e32 v135, 1.0, v135
	v_rcp_f32_e32 v136, v130
	v_add_f32_e32 v130, 1.0, v131
	v_add_f32_e32 v132, 1.0, v132
	v_rcp_f32_e32 v134, v134
	v_add_f32_e32 v133, 1.0, v133
	v_rcp_f32_e32 v135, v135
	v_rcp_f32_e32 v138, v130
	v_cvt_pk_bf16_f32 v130, v0, v134
	v_add_lshl_u32 v0, v144, v161, 1
	v_rcp_f32_e32 v132, v132
	v_rcp_f32_e32 v133, v133
	v_cvt_pk_bf16_f32 v131, v135, v136
	v_lshl_add_u64 v[134:135], s[10:11], 0, v[0:1]
	v_cvt_pk_bf16_f32 v132, v132, v133
	v_cvt_pk_bf16_f32 v133, v137, v138
	flat_store_dwordx4 v[134:135], v[130:133]
	v_mul_f32_e32 v134, v120, v140
	v_mul_f32_e32 v135, v121, v140
	v_mul_f32_e32 v138, v118, v140
	v_mul_f32_e32 v139, v119, v140
	v_mul_f32_e32 v136, v116, v140
	v_mul_f32_e32 v137, v117, v140
	v_mul_f32_e32 v141, v115, v140
	v_mul_f32_e32 v140, v114, v140
	s_mov_b64 s[30:31], -1
	s_and_b64 vcc, exec, s[28:29]
	s_cbranch_vccz .LBB0_565
	s_and_saveexec_b64 s[30:31], s[34:35]
	s_cbranch_execz .LBB0_564

; #define PG8_PACK8(y0, y1) (u32x4){cvt_pk_bf16((y0)[0], (y0)[1]), cvt_pk_bf16((y0)[2], (y0)[3]), cvt_pk_bf16((y1)[0], (y1)[1]), cvt_pk_bf16((y1)[2], (y1)[3])}
;     __device__ __forceinline__ void operator()(const f32x4 (&acc)[2][2][4][2], const Unit& u, int ui, int wr, int wc, int fr, int fq) const {
;     ...
;         } else {
; #pragma unroll
;             for (int ai = 0; ai < 2; ++ai)
; #pragma unroll
;                 for (int m = 0; m < 4; ++m) {
;                     const unsigned row = row0 + ai * HALF + m * 16; const float rs = rsp[ai * HALF + m * 16];
; #pragma unroll
;                     for (int bj = 0; bj < 2; ++bj) {
;                         const f32x4 y0 = acc[ai][bj][m][0] * rs, y1 = acc[ai][bj][m][1] * rs;
;                         if (pn == 12 || bj == 0) {
;                             const unsigned gcol = (unsigned)((pn == 12 ? 0 : 256) + 128 * bj + 32 * wc + 8 * fq);
;                             f32x4 s0, s1;
; #pragma unroll
;                             for (int e = 0; e < 4; ++e) { s0[e] = __builtin_amdgcn_rcpf(1.0f + __builtin_amdgcn_exp2f(y0[e] * -1.4426950408889634f)); s1[e] = __builtin_amdgcn_rcpf(1.0f + __builtin_amdgcn_exp2f(y1[e] * -1.4426950408889634f)); }
;                             *(u32x4*)(ws + E_GF + (size_t)((row * 384u + gcol) * 2u)) = PG8_PACK8(s0, s1);
.LBB0_567:
	ds_read_b32 v140, v160 offset:64
	v_add_u32_e32 v159, 0x1800, v144
	s_andn2_b64 vcc, exec, s[28:29]
	s_waitcnt lgkmcnt(0)
	v_mul_f32_e32 v130, v106, v140
	v_mul_f32_e32 v131, v107, v140
	v_mul_f32_e32 v132, v110, v140
	v_mul_f32_e32 v133, v111, v140
	v_mul_f32_e32 v130, 0xbfb8aa3b, v130
	v_mul_f32_e32 v0, 0xbfb8aa3b, v132
	v_exp_f32_e32 v130, v130
	v_mul_f32_e32 v132, 0xbfb8aa3b, v133
	v_exp_f32_e32 v132, v132
	v_mul_f32_e32 v134, v108, v140
	v_mul_f32_e32 v135, v109, v140
	v_mul_f32_e32 v136, v112, v140
	v_mul_f32_e32 v137, v113, v140
	v_add_f32_e32 v130, 1.0, v130
	v_mul_f32_e32 v131, 0xbfb8aa3b, v131
	v_exp_f32_e32 v131, v131
	v_rcp_f32_e32 v133, v130
	v_add_f32_e32 v130, 1.0, v132
	v_mul_f32_e32 v132, 0xbfb8aa3b, v136
	v_mul_f32_e32 v134, 0xbfb8aa3b, v134
	v_exp_f32_e32 v132, v132
	v_exp_f32_e32 v134, v134
	v_add_f32_e32 v131, 1.0, v131
	v_exp_f32_e32 v0, v0
	v_rcp_f32_e32 v136, v131
	v_add_f32_e32 v131, 1.0, v132
	v_add_f32_e32 v132, 1.0, v134
	v_mul_f32_e32 v134, 0xbfb8aa3b, v137
	v_mul_f32_e32 v135, 0xbfb8aa3b, v135
	v_exp_f32_e32 v134, v134
	v_exp_f32_e32 v135, v135
	v_add_f32_e32 v0, 1.0, v0
	v_rcp_f32_e32 v0, v0
	v_rcp_f32_e32 v130, v130
	v_rcp_f32_e32 v137, v132
	v_add_f32_e32 v132, 1.0, v134
	v_add_f32_e32 v134, 1.0, v135
	v_rcp_f32_e32 v131, v131
	v_rcp_f32_e32 v132, v132
	v_rcp_f32_e32 v134, v134
	v_cvt_pk_bf16_f32 v130, v0, v130
	v_add_lshl_u32 v0, v159, v161, 1
	v_cvt_pk_bf16_f32 v131, v131, v132
	v_cvt_pk_bf16_f32 v132, v133, v136
	v_cvt_pk_bf16_f32 v133, v137, v134
	v_lshl_add_u64 v[134:135], s[10:11], 0, v[0:1]
	flat_store_dwordx4 v[134:135], v[130:133]
	v_mul_f32_e32 v134, v104, v140
	v_mul_f32_e32 v135, v105, v140
	v_mul_f32_e32 v138, v102, v140
	v_mul_f32_e32 v139, v103, v140
	v_cndmask_b32_e64 v130, 0, 1, s[28:29]
	v_mul_f32_e32 v136, v100, v140
	v_mul_f32_e32 v137, v101, v140
	v_mul_f32_e32 v141, v99, v140
	v_mul_f32_e32 v140, v98, v140
	v_cmp_ne_u32_e64 s[40:41], 1, v130
	s_mov_b64 s[28:29], -1
	s_cbranch_vccnz .LBB0_571
	s_and_saveexec_b64 s[28:29], s[34:35]
	s_cbranch_execz .LBB0_570

; #define PG8_PACK8(y0, y1) (u32x4){cvt_pk_bf16((y0)[0], (y0)[1]), cvt_pk_bf16((y0)[2], (y0)[3]), cvt_pk_bf16((y1)[0], (y1)[1]), cvt_pk_bf16((y1)[2], (y1)[3])}
;     __device__ __forceinline__ void operator()(const f32x4 (&acc)[2][2][4][2], const Unit& u, int ui, int wr, int wc, int fr, int fq) const {
;     ...
;         } else {
; #pragma unroll
;             for (int ai = 0; ai < 2; ++ai)
; #pragma unroll
;                 for (int m = 0; m < 4; ++m) {
;                     const unsigned row = row0 + ai * HALF + m * 16; const float rs = rsp[ai * HALF + m * 16];
; #pragma unroll
;                     for (int bj = 0; bj < 2; ++bj) {
;                         const f32x4 y0 = acc[ai][bj][m][0] * rs, y1 = acc[ai][bj][m][1] * rs;
;                         if (pn == 12 || bj == 0) {
;                             const unsigned gcol = (unsigned)((pn == 12 ? 0 : 256) + 128 * bj + 32 * wc + 8 * fq);
;                             f32x4 s0, s1;
; #pragma unroll
;                             for (int e = 0; e < 4; ++e) { s0[e] = __builtin_amdgcn_rcpf(1.0f + __builtin_amdgcn_exp2f(y0[e] * -1.4426950408889634f)); s1[e] = __builtin_amdgcn_rcpf(1.0f + __builtin_amdgcn_exp2f(y1[e] * -1.4426950408889634f)); }
;                             *(u32x4*)(ws + E_GF + (size_t)((row * 384u + gcol) * 2u)) = PG8_PACK8(s0, s1);
.LBB0_573:
	ds_read_b32 v140, v160 offset:128
	v_add_u32_e32 v159, 0x1800, v159
	s_and_b64 vcc, exec, s[40:41]
	s_mov_b64 s[28:29], -1
	s_waitcnt lgkmcnt(0)
	v_mul_f32_e32 v130, v90, v140
	v_mul_f32_e32 v131, v91, v140
	v_mul_f32_e32 v132, v94, v140
	v_mul_f32_e32 v133, v95, v140
	v_mul_f32_e32 v130, 0xbfb8aa3b, v130
	v_mul_f32_e32 v0, 0xbfb8aa3b, v132
	v_exp_f32_e32 v130, v130
	v_mul_f32_e32 v132, 0xbfb8aa3b, v133
	v_exp_f32_e32 v132, v132
	v_mul_f32_e32 v134, v92, v140
	v_mul_f32_e32 v135, v93, v140
	v_mul_f32_e32 v136, v96, v140
	v_mul_f32_e32 v137, v97, v140
	v_add_f32_e32 v130, 1.0, v130
	v_mul_f32_e32 v131, 0xbfb8aa3b, v131
	v_exp_f32_e32 v131, v131
	v_rcp_f32_e32 v133, v130
	v_add_f32_e32 v130, 1.0, v132
	v_mul_f32_e32 v132, 0xbfb8aa3b, v136
	v_mul_f32_e32 v134, 0xbfb8aa3b, v134
	v_exp_f32_e32 v132, v132
	v_exp_f32_e32 v134, v134
	v_add_f32_e32 v131, 1.0, v131
	v_exp_f32_e32 v0, v0
	v_rcp_f32_e32 v136, v131
	v_add_f32_e32 v131, 1.0, v132
	v_add_f32_e32 v132, 1.0, v134
	v_mul_f32_e32 v134, 0xbfb8aa3b, v137
	v_mul_f32_e32 v135, 0xbfb8aa3b, v135
	v_exp_f32_e32 v134, v134
	v_exp_f32_e32 v135, v135
	v_add_f32_e32 v0, 1.0, v0
	v_rcp_f32_e32 v0, v0
	v_rcp_f32_e32 v130, v130
	v_rcp_f32_e32 v137, v132
	v_add_f32_e32 v132, 1.0, v134
	v_add_f32_e32 v134, 1.0, v135
	v_rcp_f32_e32 v131, v131
	v_rcp_f32_e32 v132, v132
	v_rcp_f32_e32 v134, v134
	v_cvt_pk_bf16_f32 v130, v0, v130
	v_add_lshl_u32 v0, v159, v161, 1
	v_cvt_pk_bf16_f32 v131, v131, v132
	v_cvt_pk_bf16_f32 v132, v133, v136
	v_cvt_pk_bf16_f32 v133, v137, v134
	v_lshl_add_u64 v[134:135], s[10:11], 0, v[0:1]
	flat_store_dwordx4 v[134:135], v[130:133]
	v_mul_f32_e32 v134, v88, v140
	v_mul_f32_e32 v135, v89, v140
	v_mul_f32_e32 v138, v86, v140
	v_mul_f32_e32 v139, v87, v140
	v_mul_f32_e32 v136, v84, v140
	v_mul_f32_e32 v137, v85, v140
	v_mul_f32_e32 v141, v83, v140
	v_mul_f32_e32 v140, v82, v140
	s_cbranch_vccnz .LBB0_577
	s_and_saveexec_b64 s[28:29], s[34:35]
	s_cbranch_execz .LBB0_576

; #define PG8_PACK8(y0, y1) (u32x4){cvt_pk_bf16((y0)[0], (y0)[1]), cvt_pk_bf16((y0)[2], (y0)[3]), cvt_pk_bf16((y1)[0], (y1)[1]), cvt_pk_bf16((y1)[2], (y1)[3])}
;     __device__ __forceinline__ void operator()(const f32x4 (&acc)[2][2][4][2], const Unit& u, int ui, int wr, int wc, int fr, int fq) const {
;     ...
;         } else {
; #pragma unroll
;             for (int ai = 0; ai < 2; ++ai)
; #pragma unroll
;                 for (int m = 0; m < 4; ++m) {
;                     const unsigned row = row0 + ai * HALF + m * 16; const float rs = rsp[ai * HALF + m * 16];
; #pragma unroll
;                     for (int bj = 0; bj < 2; ++bj) {
;                         const f32x4 y0 = acc[ai][bj][m][0] * rs, y1 = acc[ai][bj][m][1] * rs;
;                         if (pn == 12 || bj == 0) {
;                             const unsigned gcol = (unsigned)((pn == 12 ? 0 : 256) + 128 * bj + 32 * wc + 8 * fq);
;                             f32x4 s0, s1;
; #pragma unroll
;                             for (int e = 0; e < 4; ++e) { s0[e] = __builtin_amdgcn_rcpf(1.0f + __builtin_amdgcn_exp2f(y0[e] * -1.4426950408889634f)); s1[e] = __builtin_amdgcn_rcpf(1.0f + __builtin_amdgcn_exp2f(y1[e] * -1.4426950408889634f)); }
;                             *(u32x4*)(ws + E_GF + (size_t)((row * 384u + gcol) * 2u)) = PG8_PACK8(s0, s1);
.LBB0_579:
	ds_read_b32 v140, v160 offset:192
	v_add_u32_e32 v159, 0x1800, v159
	s_and_b64 vcc, exec, s[40:41]
	s_mov_b64 s[28:29], -1
	s_waitcnt lgkmcnt(0)
	v_mul_f32_e32 v130, v74, v140
	v_mul_f32_e32 v131, v75, v140
	v_mul_f32_e32 v132, v78, v140
	v_mul_f32_e32 v133, v79, v140
	v_mul_f32_e32 v130, 0xbfb8aa3b, v130
	v_mul_f32_e32 v0, 0xbfb8aa3b, v132
	v_exp_f32_e32 v130, v130
	v_mul_f32_e32 v132, 0xbfb8aa3b, v133
	v_exp_f32_e32 v132, v132
	v_mul_f32_e32 v134, v76, v140
	v_mul_f32_e32 v135, v77, v140
	v_mul_f32_e32 v136, v80, v140
	v_mul_f32_e32 v137, v81, v140
	v_add_f32_e32 v130, 1.0, v130
	v_mul_f32_e32 v131, 0xbfb8aa3b, v131
	v_exp_f32_e32 v131, v131
	v_rcp_f32_e32 v133, v130
	v_add_f32_e32 v130, 1.0, v132
	v_mul_f32_e32 v132, 0xbfb8aa3b, v136
	v_mul_f32_e32 v134, 0xbfb8aa3b, v134
	v_exp_f32_e32 v132, v132
	v_exp_f32_e32 v134, v134
	v_add_f32_e32 v131, 1.0, v131
	v_exp_f32_e32 v0, v0
	v_rcp_f32_e32 v136, v131
	v_add_f32_e32 v131, 1.0, v132
	v_add_f32_e32 v132, 1.0, v134
	v_mul_f32_e32 v134, 0xbfb8aa3b, v137
	v_mul_f32_e32 v135, 0xbfb8aa3b, v135
	v_exp_f32_e32 v134, v134
	v_exp_f32_e32 v135, v135
	v_add_f32_e32 v0, 1.0, v0
	v_rcp_f32_e32 v0, v0
	v_rcp_f32_e32 v130, v130
	v_rcp_f32_e32 v137, v132
	v_add_f32_e32 v132, 1.0, v134
	v_add_f32_e32 v134, 1.0, v135
	v_rcp_f32_e32 v131, v131
	v_rcp_f32_e32 v132, v132
	v_rcp_f32_e32 v134, v134
	v_cvt_pk_bf16_f32 v130, v0, v130
	v_add_lshl_u32 v0, v159, v161, 1
	v_cvt_pk_bf16_f32 v131, v131, v132
	v_cvt_pk_bf16_f32 v132, v133, v136
	v_cvt_pk_bf16_f32 v133, v137, v134
	v_lshl_add_u64 v[134:135], s[10:11], 0, v[0:1]
	flat_store_dwordx4 v[134:135], v[130:133]
	v_mul_f32_e32 v134, v72, v140
	v_mul_f32_e32 v135, v73, v140
	v_mul_f32_e32 v138, v70, v140
	v_mul_f32_e32 v139, v71, v140
	v_mul_f32_e32 v136, v68, v140
	v_mul_f32_e32 v137, v69, v140
	v_mul_f32_e32 v141, v67, v140
	v_mul_f32_e32 v140, v66, v140
	s_cbranch_vccnz .LBB0_583
	s_and_saveexec_b64 s[28:29], s[34:35]
	s_cbranch_execz .LBB0_582

; #define PG8_PACK8(y0, y1) (u32x4){cvt_pk_bf16((y0)[0], (y0)[1]), cvt_pk_bf16((y0)[2], (y0)[3]), cvt_pk_bf16((y1)[0], (y1)[1]), cvt_pk_bf16((y1)[2], (y1)[3])}
;     __device__ __forceinline__ void operator()(const f32x4 (&acc)[2][2][4][2], const Unit& u, int ui, int wr, int wc, int fr, int fq) const {
;     ...
;         } else {
; #pragma unroll
;             for (int ai = 0; ai < 2; ++ai)
; #pragma unroll
;                 for (int m = 0; m < 4; ++m) {
;                     const unsigned row = row0 + ai * HALF + m * 16; const float rs = rsp[ai * HALF + m * 16];
; #pragma unroll
;                     for (int bj = 0; bj < 2; ++bj) {
;                         const f32x4 y0 = acc[ai][bj][m][0] * rs, y1 = acc[ai][bj][m][1] * rs;
;                         if (pn == 12 || bj == 0) {
;                             const unsigned gcol = (unsigned)((pn == 12 ? 0 : 256) + 128 * bj + 32 * wc + 8 * fq);
;                             f32x4 s0, s1;
; #pragma unroll
;                             for (int e = 0; e < 4; ++e) { s0[e] = __builtin_amdgcn_rcpf(1.0f + __builtin_amdgcn_exp2f(y0[e] * -1.4426950408889634f)); s1[e] = __builtin_amdgcn_rcpf(1.0f + __builtin_amdgcn_exp2f(y1[e] * -1.4426950408889634f)); }
;                             *(u32x4*)(ws + E_GF + (size_t)((row * 384u + gcol) * 2u)) = PG8_PACK8(s0, s1);
.LBB0_585:
	ds_read_b32 v140, v160 offset:512
	v_add_u32_e32 v159, 0x7800, v159
	s_and_b64 vcc, exec, s[40:41]
	s_mov_b64 s[28:29], -1
	s_waitcnt lgkmcnt(0)
	v_mul_f32_e32 v130, v58, v140
	v_mul_f32_e32 v131, v59, v140
	v_mul_f32_e32 v132, v62, v140
	v_mul_f32_e32 v133, v63, v140
	v_mul_f32_e32 v130, 0xbfb8aa3b, v130
	v_mul_f32_e32 v0, 0xbfb8aa3b, v132
	v_exp_f32_e32 v130, v130
	v_mul_f32_e32 v132, 0xbfb8aa3b, v133
	v_exp_f32_e32 v132, v132
	v_mul_f32_e32 v134, v60, v140
	v_mul_f32_e32 v135, v61, v140
	v_mul_f32_e32 v136, v64, v140
	v_mul_f32_e32 v137, v65, v140
	v_add_f32_e32 v130, 1.0, v130
	v_mul_f32_e32 v131, 0xbfb8aa3b, v131
	v_exp_f32_e32 v131, v131
	v_rcp_f32_e32 v133, v130
	v_add_f32_e32 v130, 1.0, v132
	v_mul_f32_e32 v132, 0xbfb8aa3b, v136
	v_mul_f32_e32 v134, 0xbfb8aa3b, v134
	v_exp_f32_e32 v132, v132
	v_exp_f32_e32 v134, v134
	v_add_f32_e32 v131, 1.0, v131
	v_exp_f32_e32 v0, v0
	v_rcp_f32_e32 v136, v131
	v_add_f32_e32 v131, 1.0, v132
	v_add_f32_e32 v132, 1.0, v134
	v_mul_f32_e32 v134, 0xbfb8aa3b, v137
	v_mul_f32_e32 v135, 0xbfb8aa3b, v135
	v_exp_f32_e32 v134, v134
	v_exp_f32_e32 v135, v135
	v_add_f32_e32 v0, 1.0, v0
	v_rcp_f32_e32 v0, v0
	v_rcp_f32_e32 v130, v130
	v_rcp_f32_e32 v137, v132
	v_add_f32_e32 v132, 1.0, v134
	v_add_f32_e32 v134, 1.0, v135
	v_rcp_f32_e32 v131, v131
	v_rcp_f32_e32 v132, v132
	v_rcp_f32_e32 v134, v134
	v_cvt_pk_bf16_f32 v130, v0, v130
	v_add_lshl_u32 v0, v159, v161, 1
	v_cvt_pk_bf16_f32 v131, v131, v132
	v_cvt_pk_bf16_f32 v132, v133, v136
	v_cvt_pk_bf16_f32 v133, v137, v134
	v_lshl_add_u64 v[134:135], s[10:11], 0, v[0:1]
	flat_store_dwordx4 v[134:135], v[130:133]
	v_mul_f32_e32 v134, v56, v140
	v_mul_f32_e32 v135, v57, v140
	v_mul_f32_e32 v138, v54, v140
	v_mul_f32_e32 v139, v55, v140
	v_mul_f32_e32 v136, v52, v140
	v_mul_f32_e32 v137, v53, v140
	v_mul_f32_e32 v141, v51, v140
	v_mul_f32_e32 v140, v50, v140
	s_cbranch_vccnz .LBB0_589
	s_and_saveexec_b64 s[28:29], s[34:35]
	s_cbranch_execz .LBB0_588

; #define PG8_PACK8(y0, y1) (u32x4){cvt_pk_bf16((y0)[0], (y0)[1]), cvt_pk_bf16((y0)[2], (y0)[3]), cvt_pk_bf16((y1)[0], (y1)[1]), cvt_pk_bf16((y1)[2], (y1)[3])}
;     __device__ __forceinline__ void operator()(const f32x4 (&acc)[2][2][4][2], const Unit& u, int ui, int wr, int wc, int fr, int fq) const {
;     ...
;         } else {
; #pragma unroll
;             for (int ai = 0; ai < 2; ++ai)
; #pragma unroll
;                 for (int m = 0; m < 4; ++m) {
;                     const unsigned row = row0 + ai * HALF + m * 16; const float rs = rsp[ai * HALF + m * 16];
; #pragma unroll
;                     for (int bj = 0; bj < 2; ++bj) {
;                         const f32x4 y0 = acc[ai][bj][m][0] * rs, y1 = acc[ai][bj][m][1] * rs;
;                         if (pn == 12 || bj == 0) {
;                             const unsigned gcol = (unsigned)((pn == 12 ? 0 : 256) + 128 * bj + 32 * wc + 8 * fq);
;                             f32x4 s0, s1;
; #pragma unroll
;                             for (int e = 0; e < 4; ++e) { s0[e] = __builtin_amdgcn_rcpf(1.0f + __builtin_amdgcn_exp2f(y0[e] * -1.4426950408889634f)); s1[e] = __builtin_amdgcn_rcpf(1.0f + __builtin_amdgcn_exp2f(y1[e] * -1.4426950408889634f)); }
;                             *(u32x4*)(ws + E_GF + (size_t)((row * 384u + gcol) * 2u)) = PG8_PACK8(s0, s1);
.LBB0_591:
	ds_read_b32 v140, v160 offset:576
	v_add_u32_e32 v159, 0x1800, v159
	s_and_b64 vcc, exec, s[40:41]
	s_mov_b64 s[28:29], -1
	s_waitcnt lgkmcnt(0)
	v_mul_f32_e32 v130, v42, v140
	v_mul_f32_e32 v131, v43, v140
	v_mul_f32_e32 v132, v46, v140
	v_mul_f32_e32 v133, v47, v140
	v_mul_f32_e32 v130, 0xbfb8aa3b, v130
	v_mul_f32_e32 v0, 0xbfb8aa3b, v132
	v_exp_f32_e32 v130, v130
	v_mul_f32_e32 v132, 0xbfb8aa3b, v133
	v_exp_f32_e32 v132, v132
	v_mul_f32_e32 v134, v44, v140
	v_mul_f32_e32 v135, v45, v140
	v_mul_f32_e32 v136, v48, v140
	v_mul_f32_e32 v137, v49, v140
	v_add_f32_e32 v130, 1.0, v130
	v_mul_f32_e32 v131, 0xbfb8aa3b, v131
	v_exp_f32_e32 v131, v131
	v_rcp_f32_e32 v133, v130
	v_add_f32_e32 v130, 1.0, v132
	v_mul_f32_e32 v132, 0xbfb8aa3b, v136
	v_mul_f32_e32 v134, 0xbfb8aa3b, v134
	v_exp_f32_e32 v132, v132
	v_exp_f32_e32 v134, v134
	v_add_f32_e32 v131, 1.0, v131
	v_exp_f32_e32 v0, v0
	v_rcp_f32_e32 v136, v131
	v_add_f32_e32 v131, 1.0, v132
	v_add_f32_e32 v132, 1.0, v134
	v_mul_f32_e32 v134, 0xbfb8aa3b, v137
	v_mul_f32_e32 v135, 0xbfb8aa3b, v135
	v_exp_f32_e32 v134, v134
	v_exp_f32_e32 v135, v135
	v_add_f32_e32 v0, 1.0, v0
	v_rcp_f32_e32 v0, v0
	v_rcp_f32_e32 v130, v130
	v_rcp_f32_e32 v137, v132
	v_add_f32_e32 v132, 1.0, v134
	v_add_f32_e32 v134, 1.0, v135
	v_rcp_f32_e32 v131, v131
	v_rcp_f32_e32 v132, v132
	v_rcp_f32_e32 v134, v134
	v_cvt_pk_bf16_f32 v130, v0, v130
	v_add_lshl_u32 v0, v159, v161, 1
	v_cvt_pk_bf16_f32 v131, v131, v132
	v_cvt_pk_bf16_f32 v132, v133, v136
	v_cvt_pk_bf16_f32 v133, v137, v134
	v_lshl_add_u64 v[134:135], s[10:11], 0, v[0:1]
	flat_store_dwordx4 v[134:135], v[130:133]
	v_mul_f32_e32 v134, v40, v140
	v_mul_f32_e32 v135, v41, v140
	v_mul_f32_e32 v138, v38, v140
	v_mul_f32_e32 v139, v39, v140
	v_mul_f32_e32 v136, v36, v140
	v_mul_f32_e32 v137, v37, v140
	v_mul_f32_e32 v141, v35, v140
	v_mul_f32_e32 v140, v34, v140
	s_cbranch_vccnz .LBB0_595
	s_and_saveexec_b64 s[28:29], s[34:35]
	s_cbranch_execz .LBB0_594

; #define PG8_PACK8(y0, y1) (u32x4){cvt_pk_bf16((y0)[0], (y0)[1]), cvt_pk_bf16((y0)[2], (y0)[3]), cvt_pk_bf16((y1)[0], (y1)[1]), cvt_pk_bf16((y1)[2], (y1)[3])}
;     __device__ __forceinline__ void operator()(const f32x4 (&acc)[2][2][4][2], const Unit& u, int ui, int wr, int wc, int fr, int fq) const {
;     ...
;         } else {
; #pragma unroll
;             for (int ai = 0; ai < 2; ++ai)
; #pragma unroll
;                 for (int m = 0; m < 4; ++m) {
;                     const unsigned row = row0 + ai * HALF + m * 16; const float rs = rsp[ai * HALF + m * 16];
; #pragma unroll
;                     for (int bj = 0; bj < 2; ++bj) {
;                         const f32x4 y0 = acc[ai][bj][m][0] * rs, y1 = acc[ai][bj][m][1] * rs;
;                         if (pn == 12 || bj == 0) {
;                             const unsigned gcol = (unsigned)((pn == 12 ? 0 : 256) + 128 * bj + 32 * wc + 8 * fq);
;                             f32x4 s0, s1;
; #pragma unroll
;                             for (int e = 0; e < 4; ++e) { s0[e] = __builtin_amdgcn_rcpf(1.0f + __builtin_amdgcn_exp2f(y0[e] * -1.4426950408889634f)); s1[e] = __builtin_amdgcn_rcpf(1.0f + __builtin_amdgcn_exp2f(y1[e] * -1.4426950408889634f)); }
;                             *(u32x4*)(ws + E_GF + (size_t)((row * 384u + gcol) * 2u)) = PG8_PACK8(s0, s1);
.LBB0_597:
	ds_read_b32 v140, v160 offset:640
	v_add_u32_e32 v159, 0x1800, v159
	s_and_b64 vcc, exec, s[40:41]
	s_mov_b64 s[28:29], -1
	s_waitcnt lgkmcnt(0)
	v_mul_f32_e32 v130, v26, v140
	v_mul_f32_e32 v131, v27, v140
	v_mul_f32_e32 v132, v30, v140
	v_mul_f32_e32 v133, v31, v140
	v_mul_f32_e32 v130, 0xbfb8aa3b, v130
	v_mul_f32_e32 v0, 0xbfb8aa3b, v132
	v_exp_f32_e32 v130, v130
	v_mul_f32_e32 v132, 0xbfb8aa3b, v133
	v_exp_f32_e32 v132, v132
	v_mul_f32_e32 v134, v28, v140
	v_mul_f32_e32 v135, v29, v140
	v_mul_f32_e32 v136, v32, v140
	v_mul_f32_e32 v137, v33, v140
	v_add_f32_e32 v130, 1.0, v130
	v_mul_f32_e32 v131, 0xbfb8aa3b, v131
	v_exp_f32_e32 v131, v131
	v_rcp_f32_e32 v133, v130
	v_add_f32_e32 v130, 1.0, v132
	v_mul_f32_e32 v132, 0xbfb8aa3b, v136
	v_mul_f32_e32 v134, 0xbfb8aa3b, v134
	v_exp_f32_e32 v132, v132
	v_exp_f32_e32 v134, v134
	v_add_f32_e32 v131, 1.0, v131
	v_exp_f32_e32 v0, v0
	v_rcp_f32_e32 v136, v131
	v_add_f32_e32 v131, 1.0, v132
	v_add_f32_e32 v132, 1.0, v134
	v_mul_f32_e32 v134, 0xbfb8aa3b, v137
	v_mul_f32_e32 v135, 0xbfb8aa3b, v135
	v_exp_f32_e32 v134, v134
	v_exp_f32_e32 v135, v135
	v_add_f32_e32 v0, 1.0, v0
	v_rcp_f32_e32 v0, v0
	v_rcp_f32_e32 v130, v130
	v_rcp_f32_e32 v137, v132
	v_add_f32_e32 v132, 1.0, v134
	v_add_f32_e32 v134, 1.0, v135
	v_rcp_f32_e32 v131, v131
	v_rcp_f32_e32 v132, v132
	v_rcp_f32_e32 v134, v134
	v_cvt_pk_bf16_f32 v130, v0, v130
	v_add_lshl_u32 v0, v159, v161, 1
	v_cvt_pk_bf16_f32 v131, v131, v132
	v_cvt_pk_bf16_f32 v132, v133, v136
	v_cvt_pk_bf16_f32 v133, v137, v134
	v_lshl_add_u64 v[134:135], s[10:11], 0, v[0:1]
	flat_store_dwordx4 v[134:135], v[130:133]
	v_mul_f32_e32 v134, v24, v140
	v_mul_f32_e32 v135, v25, v140
	v_mul_f32_e32 v138, v22, v140
	v_mul_f32_e32 v139, v23, v140
	v_mul_f32_e32 v136, v20, v140
	v_mul_f32_e32 v137, v21, v140
	v_mul_f32_e32 v141, v19, v140
	v_mul_f32_e32 v140, v18, v140
	s_cbranch_vccnz .LBB0_601
	s_and_saveexec_b64 s[28:29], s[34:35]
	s_cbranch_execz .LBB0_600

; #define PG8_PACK8(y0, y1) (u32x4){cvt_pk_bf16((y0)[0], (y0)[1]), cvt_pk_bf16((y0)[2], (y0)[3]), cvt_pk_bf16((y1)[0], (y1)[1]), cvt_pk_bf16((y1)[2], (y1)[3])}
;     __device__ __forceinline__ void operator()(const f32x4 (&acc)[2][2][4][2], const Unit& u, int ui, int wr, int wc, int fr, int fq) const {
;     ...
;                     const unsigned row = row0 + ai * HALF + m * 16; const float rs = rsp[ai * HALF + m * 16];
; #pragma unroll
;                     for (int bj = 0; bj < 2; ++bj) {
;                         const f32x4 y0 = acc[ai][bj][m][0] * rs, y1 = acc[ai][bj][m][1] * rs;
;                         if (pn == 12 || bj == 0) {
;                             const unsigned gcol = (unsigned)((pn == 12 ? 0 : 256) + 128 * bj + 32 * wc + 8 * fq);
;                             f32x4 s0, s1;
; #pragma unroll
;                             for (int e = 0; e < 4; ++e) { s0[e] = __builtin_amdgcn_rcpf(1.0f + __builtin_amdgcn_exp2f(y0[e] * -1.4426950408889634f)); s1[e] = __builtin_amdgcn_rcpf(1.0f + __builtin_amdgcn_exp2f(y1[e] * -1.4426950408889634f)); }
;                             *(u32x4*)(ws + E_GF + (size_t)((row * 384u + gcol) * 2u)) = PG8_PACK8(s0, s1);
;                         } else if (wc == 0 && fq == 0) {
;                             float z[6] = {y0[0], y0[1], y0[2], y0[3], y1[0], y1[1]};
; #pragma unroll
;                             for (int e = 0; e < 6; ++e) { const float zz = z[e] + bfg[e]; z[e] = fminf(zz, 0.f) - log1pf(__expf(-fabsf(zz))); }
;                             float* lp = (float*)(ws + E_LS) + (size_t)row;
; #pragma unroll
;                             for (int e = 0; e < 6; ++e) lp[(size_t)(e * 32768u)] = z[e];
.LBB0_603:
	ds_read_b32 v140, v160 offset:704
	v_add_u32_e32 v0, v159, v161
	s_and_b64 vcc, exec, s[40:41]
	s_mov_b64 s[28:29], -1
	s_waitcnt lgkmcnt(0)
	v_mul_f32_e32 v130, v10, v140
	v_mul_f32_e32 v131, v11, v140
	v_mul_f32_e32 v132, v14, v140
	v_mul_f32_e32 v133, v15, v140
	v_mul_f32_e32 v130, 0xbfb8aa3b, v130
	v_exp_f32_e32 v130, v130
	v_mul_f32_e32 v133, 0xbfb8aa3b, v133
	v_exp_f32_e32 v133, v133
	v_mul_f32_e32 v134, v12, v140
	v_mul_f32_e32 v135, v13, v140
	v_mul_f32_e32 v136, v16, v140
	v_mul_f32_e32 v137, v17, v140
	v_add_f32_e32 v130, 1.0, v130
	v_mul_f32_e32 v131, 0xbfb8aa3b, v131
	v_exp_f32_e32 v131, v131
	v_rcp_f32_e32 v138, v130
	v_add_f32_e32 v130, 1.0, v133
	v_mul_f32_e32 v133, 0xbfb8aa3b, v136
	v_mul_f32_e32 v134, 0xbfb8aa3b, v134
	v_exp_f32_e32 v133, v133
	v_exp_f32_e32 v134, v134
	v_add_f32_e32 v131, 1.0, v131
	v_rcp_f32_e32 v136, v131
	v_add_f32_e32 v131, 1.0, v133
	v_add_f32_e32 v133, 1.0, v134
	v_mul_f32_e32 v134, 0xbfb8aa3b, v137
	v_mul_f32_e32 v132, 0xbfb8aa3b, v132
	v_exp_f32_e32 v134, v134
	v_exp_f32_e32 v132, v132
	v_mul_f32_e32 v135, 0xbfb8aa3b, v135
	v_exp_f32_e32 v135, v135
	v_add_f32_e32 v134, 1.0, v134
	v_add_f32_e32 v132, 1.0, v132
	v_rcp_f32_e32 v130, v130
	v_rcp_f32_e32 v131, v131
	v_rcp_f32_e32 v134, v134
	v_rcp_f32_e32 v132, v132
	v_add_f32_e32 v135, 1.0, v135
	v_cvt_pk_bf16_f32 v130, v132, v130
	v_cvt_pk_bf16_f32 v131, v131, v134
	v_mov_b32_e32 v134, 0x3000
	v_rcp_f32_e32 v133, v133
	v_rcp_f32_e32 v135, v135
	v_lshl_add_u32 v0, v0, 1, v134
	v_cvt_pk_bf16_f32 v132, v138, v136
	v_cvt_pk_bf16_f32 v133, v133, v135
	v_lshl_add_u64 v[134:135], s[10:11], 0, v[0:1]
	flat_store_dwordx4 v[134:135], v[130:133]
	v_mul_f32_e32 v134, v8, v140
	v_mul_f32_e32 v135, v9, v140
	v_mul_f32_e32 v138, v6, v140
	v_mul_f32_e32 v139, v7, v140
	v_mul_f32_e32 v136, v4, v140
	v_mul_f32_e32 v137, v5, v140
	v_mul_f32_e32 v141, v3, v140
	v_mul_f32_e32 v140, v2, v140
	s_cbranch_vccnz .LBB0_607
	s_cmp_eq_u64 s[34:35], 0
	s_cbranch_scc1 .Lflg_done
	global_load_dwordx4 v[10:13], v1, s[6:7]
	global_load_dwordx2 v[14:15], v1, s[6:7] offset:16
	v_mbcnt_lo_u32_b32 v16, -1, 0
	v_mbcnt_hi_u32_b32 v16, -1, v16
	v_lshrrev_b32_e32 v17, 5, v16
	v_bfe_u32 v16, v16, 4, 1
	v_lshlrev_b32_e32 v17, 9, v17
	v_lshl_add_u32 v17, v16, 7, v17
	v_add_u32_e32 v16, v160, v17
	ds_read_b32 v26, v16
	ds_read_b32 v27, v16 offset:64
	v_lshl_add_u32 v28, v158, 2, v17
	s_mov_b32 s3, 0xbfb8aa3b
	s_mov_b32 s19, 0x3f2aaaab
	s_mov_b32 s21, 0x3f317218
	s_mov_b32 s27, 0x7f800000
	s_mov_b32 s33, 0x33800000
	v_permlane32_swap_b32_e32 v118, v54
	v_permlane32_swap_b32_e32 v119, v55
	v_permlane32_swap_b32_e32 v120, v56
	v_permlane32_swap_b32_e32 v121, v57
	v_permlane32_swap_b32_e32 v114, v50
	v_permlane32_swap_b32_e32 v115, v51
	v_permlane32_swap_b32_e32 v102, v38
	v_permlane32_swap_b32_e32 v103, v39
	v_permlane32_swap_b32_e32 v104, v40
	v_permlane32_swap_b32_e32 v105, v41
	v_permlane32_swap_b32_e32 v98, v34
	v_permlane32_swap_b32_e32 v99, v35
	v_permlane32_swap_b32_e32 v86, v22
	v_permlane32_swap_b32_e32 v87, v23
	v_permlane32_swap_b32_e32 v88, v24
	v_permlane32_swap_b32_e32 v89, v25
	v_permlane32_swap_b32_e32 v82, v18
	v_permlane32_swap_b32_e32 v83, v19
	v_permlane32_swap_b32_e32 v70, v6
	v_permlane32_swap_b32_e32 v71, v7
	v_permlane32_swap_b32_e32 v72, v8
	v_permlane32_swap_b32_e32 v73, v9
	v_permlane32_swap_b32_e32 v66, v2
	v_permlane32_swap_b32_e32 v67, v3
	s_nop 1
	v_permlane16_swap_b32_e32 v118, v86
	v_permlane16_swap_b32_e32 v119, v87
	v_permlane16_swap_b32_e32 v120, v88
	v_permlane16_swap_b32_e32 v121, v89
	v_permlane16_swap_b32_e32 v114, v82
	v_permlane16_swap_b32_e32 v115, v83
	v_permlane16_swap_b32_e32 v102, v70
	v_permlane16_swap_b32_e32 v103, v71
	v_permlane16_swap_b32_e32 v104, v72
	v_permlane16_swap_b32_e32 v105, v73
	v_permlane16_swap_b32_e32 v98, v66
	v_permlane16_swap_b32_e32 v99, v67
	s_waitcnt vmcnt(0) lgkmcnt(0)
	s_nop 1
	v_mul_f32_e32 v118, v118, v26
	v_add_f32_e32 v30, v118, v10
	v_min_f32_e32 v29, 0, v30
	v_mul_f32_e64 v30, |v30|, s3
	v_exp_f32_e32 v30, v30
	s_nop 0
	v_add_f32_e32 v32, 1.0, v30
	v_add_f32_e32 v31, -1.0, v32
	v_sub_f32_e32 v33, v31, v32
	v_add_f32_e32 v33, 1.0, v33
	v_sub_f32_e32 v31, v30, v31
	v_add_f32_e32 v33, v31, v33
	v_frexp_mant_f32_e32 v31, v32
	v_cvt_f64_f32_e32 v[42:43], v32
	v_cmp_gt_f32_e32 vcc, s19, v31
	v_frexp_exp_i32_f64_e32 v31, v[42:43]
	s_nop 0
	v_subbrev_co_u32_e32 v31, vcc, 0, v31, vcc
	v_sub_u32_e32 v42, 0, v31
	v_ldexp_f32 v32, v32, v42
	v_ldexp_f32 v33, v33, v42
	v_add_f32_e32 v42, -1.0, v32
	v_add_f32_e32 v43, 1.0, v42
	v_sub_f32_e32 v43, v32, v43
	v_add_f32_e32 v43, v33, v43
	v_add_f32_e32 v44, v42, v43
	v_sub_f32_e32 v42, v44, v42
	v_sub_f32_e32 v42, v43, v42
	v_add_f32_e32 v43, 1.0, v32
	v_add_f32_e32 v45, -1.0, v43
	v_sub_f32_e32 v32, v32, v45
	v_add_f32_e32 v32, v33, v32
	v_add_f32_e32 v33, v43, v32
	v_sub_f32_e32 v43, v33, v43
	v_sub_f32_e32 v32, v32, v43
	v_rcp_f32_e32 v43, v33
	v_cvt_f32_i32_e32 v31, v31
	v_cmp_neq_f32_e32 vcc, s27, v30
	v_mul_f32_e32 v45, v44, v43
	v_mul_f32_e32 v46, v33, v45
	v_fma_f32 v47, v45, v33, -v46
	v_fmac_f32_e32 v47, v45, v32
	v_add_f32_e32 v48, v46, v47
	v_sub_f32_e32 v49, v44, v48
	v_sub_f32_e32 v44, v44, v49
	v_sub_f32_e32 v46, v48, v46
	v_sub_f32_e32 v44, v44, v48
	v_add_f32_e32 v42, v42, v44
	v_sub_f32_e32 v44, v46, v47
	v_add_f32_e32 v42, v44, v42
	v_add_f32_e32 v44, v49, v42
	v_mul_f32_e32 v46, v43, v44
	v_mul_f32_e32 v47, v33, v46
	v_fma_f32 v33, v46, v33, -v47
	v_fmac_f32_e32 v33, v46, v32
	v_sub_f32_e32 v32, v49, v44
	v_add_f32_e32 v32, v42, v32
	v_add_f32_e32 v42, v47, v33
	v_sub_f32_e32 v48, v44, v42
	v_sub_f32_e32 v44, v44, v48
	v_sub_f32_e32 v47, v42, v47
;     __device__ __forceinline__ void operator()(const f32x4 (&acc)[2][2][4][2], const Unit& u, int ui, int wr, int wc, int fr, int fq) const {
;     ...
;                         } else if (wc == 0 && fq == 0) {
;                             float z[6] = {y0[0], y0[1], y0[2], y0[3], y1[0], y1[1]};
; #pragma unroll
;                             for (int e = 0; e < 6; ++e) { const float zz = z[e] + bfg[e]; z[e] = fminf(zz, 0.f) - log1pf(__expf(-fabsf(zz))); }
;                             float* lp = (float*)(ws + E_LS) + (size_t)row;
; #pragma unroll
;                             for (int e = 0; e < 6; ++e) lp[(size_t)(e * 32768u)] = z[e];
	v_sub_f32_e32 v42, v44, v42
	v_add_f32_e32 v32, v32, v42
	v_sub_f32_e32 v33, v47, v33
	v_add_f32_e32 v32, v33, v32
	v_add_f32_e32 v33, v45, v46
	v_add_f32_e32 v32, v48, v32
	v_sub_f32_e32 v42, v33, v45
	v_mul_f32_e32 v32, v43, v32
	v_sub_f32_e32 v42, v46, v42
	v_add_f32_e32 v32, v42, v32
	v_mul_f32_e32 v45, 0x3f317218, v31
	v_add_f32_e32 v42, v33, v32
	v_fma_f32 v46, v31, s21, -v45
	v_mul_f32_e32 v43, v42, v42
	v_fmac_f32_e32 v46, 0xb102e308, v31
	v_sub_f32_e32 v31, v42, v33
	v_fmamk_f32 v44, v43, 0x3e9b6dac, v217
	v_sub_f32_e32 v31, v32, v31
	v_add_f32_e32 v32, v45, v46
	v_fmaak_f32 v44, v43, v44, 0x3f2aaada
	v_sub_f32_e32 v33, v32, v45
	v_ldexp_f32 v45, v42, 1
	v_mul_f32_e32 v42, v42, v43
	v_mul_f32_e32 v42, v42, v44
	v_add_f32_e32 v43, v45, v42
	v_sub_f32_e32 v44, v43, v45
	v_ldexp_f32 v31, v31, 1
	v_sub_f32_e32 v42, v42, v44
	v_add_f32_e32 v31, v31, v42
	v_add_f32_e32 v42, v43, v31
	v_sub_f32_e32 v43, v42, v43
	v_sub_f32_e32 v31, v31, v43
	v_add_f32_e32 v43, v32, v42
	v_sub_f32_e32 v44, v43, v32
	v_sub_f32_e32 v45, v43, v44
	v_sub_f32_e32 v33, v46, v33
	v_sub_f32_e32 v32, v32, v45
	v_sub_f32_e32 v42, v42, v44
	v_add_f32_e32 v32, v42, v32
	v_add_f32_e32 v42, v33, v31
	v_sub_f32_e32 v44, v42, v33
	v_sub_f32_e32 v45, v42, v44
	v_sub_f32_e32 v33, v33, v45
	v_sub_f32_e32 v31, v31, v44
	v_add_f32_e32 v32, v42, v32
	v_add_f32_e32 v31, v31, v33
	v_add_f32_e32 v33, v43, v32
	v_sub_f32_e32 v42, v33, v43
	v_sub_f32_e32 v32, v32, v42
	v_add_f32_e32 v31, v31, v32
	v_add_f32_e32 v31, v33, v31
	v_cndmask_b32_e32 v31, v230, v31, vcc
	v_cmp_ngt_f32_e32 vcc, -1.0, v30
	s_nop 1
	v_cndmask_b32_e32 v31, v231, v31, vcc
	v_cmp_neq_f32_e32 vcc, -1.0, v30
	s_nop 1
	v_cndmask_b32_e32 v31, v226, v31, vcc
	v_cmp_lt_f32_e64 vcc, |v30|, s33
	s_nop 1
	v_cndmask_b32_e32 v30, v31, v30, vcc
	v_sub_f32_e32 v118, v29, v30
	v_mul_f32_e32 v119, v119, v26
	v_add_f32_e32 v30, v119, v11
	v_min_f32_e32 v29, 0, v30
	v_mul_f32_e64 v30, |v30|, s3
	v_exp_f32_e32 v30, v30
	s_nop 0
	v_add_f32_e32 v32, 1.0, v30
	v_add_f32_e32 v31, -1.0, v32
	v_sub_f32_e32 v33, v31, v32
	v_add_f32_e32 v33, 1.0, v33
	v_sub_f32_e32 v31, v30, v31
	v_add_f32_e32 v33, v31, v33
	v_frexp_mant_f32_e32 v31, v32
	v_cvt_f64_f32_e32 v[42:43], v32
	v_cmp_gt_f32_e32 vcc, s19, v31
	v_frexp_exp_i32_f64_e32 v31, v[42:43]
	s_nop 0
	v_subbrev_co_u32_e32 v31, vcc, 0, v31, vcc
	v_sub_u32_e32 v42, 0, v31
	v_ldexp_f32 v32, v32, v42
	v_ldexp_f32 v33, v33, v42
	v_add_f32_e32 v42, -1.0, v32
	v_add_f32_e32 v43, 1.0, v42
	v_sub_f32_e32 v43, v32, v43
	v_add_f32_e32 v43, v33, v43
	v_add_f32_e32 v44, v42, v43
	v_sub_f32_e32 v42, v44, v42
	v_sub_f32_e32 v42, v43, v42
	v_add_f32_e32 v43, 1.0, v32
	v_add_f32_e32 v45, -1.0, v43
	v_sub_f32_e32 v32, v32, v45
	v_add_f32_e32 v32, v33, v32
	v_add_f32_e32 v33, v43, v32
	v_sub_f32_e32 v43, v33, v43
	v_sub_f32_e32 v32, v32, v43
	v_rcp_f32_e32 v43, v33
	v_cvt_f32_i32_e32 v31, v31
	v_cmp_neq_f32_e32 vcc, s27, v30
	v_mul_f32_e32 v45, v44, v43
	v_mul_f32_e32 v46, v33, v45
	v_fma_f32 v47, v45, v33, -v46
	v_fmac_f32_e32 v47, v45, v32
	v_add_f32_e32 v48, v46, v47
	v_sub_f32_e32 v49, v44, v48
	v_sub_f32_e32 v44, v44, v49
	v_sub_f32_e32 v46, v48, v46
	v_sub_f32_e32 v44, v44, v48
	v_add_f32_e32 v42, v42, v44
	v_sub_f32_e32 v44, v46, v47
	v_add_f32_e32 v42, v44, v42
	v_add_f32_e32 v44, v49, v42
	v_mul_f32_e32 v46, v43, v44
	v_mul_f32_e32 v47, v33, v46
	v_fma_f32 v33, v46, v33, -v47
	v_fmac_f32_e32 v33, v46, v32
	v_sub_f32_e32 v32, v49, v44
	v_add_f32_e32 v32, v42, v32
	v_add_f32_e32 v42, v47, v33
	v_sub_f32_e32 v48, v44, v42
	v_sub_f32_e32 v44, v44, v48
	v_sub_f32_e32 v47, v42, v47
	v_sub_f32_e32 v42, v44, v42
	v_add_f32_e32 v32, v32, v42
	v_sub_f32_e32 v33, v47, v33
	v_add_f32_e32 v32, v33, v32
	v_add_f32_e32 v33, v45, v46
	v_add_f32_e32 v32, v48, v32
	v_sub_f32_e32 v42, v33, v45
	v_mul_f32_e32 v32, v43, v32
	v_sub_f32_e32 v42, v46, v42
	v_add_f32_e32 v32, v42, v32
	v_mul_f32_e32 v45, 0x3f317218, v31
	v_add_f32_e32 v42, v33, v32
	v_fma_f32 v46, v31, s21, -v45
	v_mul_f32_e32 v43, v42, v42
	v_fmac_f32_e32 v46, 0xb102e308, v31
	v_sub_f32_e32 v31, v42, v33
	v_fmamk_f32 v44, v43, 0x3e9b6dac, v217
	v_sub_f32_e32 v31, v32, v31
	v_add_f32_e32 v32, v45, v46
	v_fmaak_f32 v44, v43, v44, 0x3f2aaada
	v_sub_f32_e32 v33, v32, v45
	v_ldexp_f32 v45, v42, 1
	v_mul_f32_e32 v42, v42, v43
	v_mul_f32_e32 v42, v42, v44
	v_add_f32_e32 v43, v45, v42
	v_sub_f32_e32 v44, v43, v45
	v_ldexp_f32 v31, v31, 1
	v_sub_f32_e32 v42, v42, v44
	v_add_f32_e32 v31, v31, v42
	v_add_f32_e32 v42, v43, v31
	v_sub_f32_e32 v43, v42, v43
	v_sub_f32_e32 v31, v31, v43
	v_add_f32_e32 v43, v32, v42
	v_sub_f32_e32 v44, v43, v32
	v_sub_f32_e32 v45, v43, v44
	v_sub_f32_e32 v33, v46, v33
	v_sub_f32_e32 v32, v32, v45
	v_sub_f32_e32 v42, v42, v44
	v_add_f32_e32 v32, v42, v32
	v_add_f32_e32 v42, v33, v31
	v_sub_f32_e32 v44, v42, v33
	v_sub_f32_e32 v45, v42, v44
	v_sub_f32_e32 v33, v33, v45
	v_sub_f32_e32 v31, v31, v44
	v_add_f32_e32 v32, v42, v32
	v_add_f32_e32 v31, v31, v33
	v_add_f32_e32 v33, v43, v32
	v_sub_f32_e32 v42, v33, v43
	v_sub_f32_e32 v32, v32, v42
	v_add_f32_e32 v31, v31, v32
	v_add_f32_e32 v31, v33, v31
	v_cndmask_b32_e32 v31, v230, v31, vcc
	v_cmp_ngt_f32_e32 vcc, -1.0, v30
	s_nop 1
	v_cndmask_b32_e32 v31, v231, v31, vcc
	v_cmp_neq_f32_e32 vcc, -1.0, v30
	s_nop 1
	v_cndmask_b32_e32 v31, v226, v31, vcc
	v_cmp_lt_f32_e64 vcc, |v30|, s33
	s_nop 1
	v_cndmask_b32_e32 v30, v31, v30, vcc
	v_sub_f32_e32 v119, v29, v30
	v_mul_f32_e32 v120, v120, v26
	v_add_f32_e32 v30, v120, v12
	v_min_f32_e32 v29, 0, v30
	v_mul_f32_e64 v30, |v30|, s3
	v_exp_f32_e32 v30, v30
	s_nop 0
	v_add_f32_e32 v32, 1.0, v30
	v_add_f32_e32 v31, -1.0, v32
	v_sub_f32_e32 v33, v31, v32
;     __device__ __forceinline__ void operator()(const f32x4 (&acc)[2][2][4][2], const Unit& u, int ui, int wr, int wc, int fr, int fq) const {
;     ...
;                         } else if (wc == 0 && fq == 0) {
;                             float z[6] = {y0[0], y0[1], y0[2], y0[3], y1[0], y1[1]};
; #pragma unroll
;                             for (int e = 0; e < 6; ++e) { const float zz = z[e] + bfg[e]; z[e] = fminf(zz, 0.f) - log1pf(__expf(-fabsf(zz))); }
;                             float* lp = (float*)(ws + E_LS) + (size_t)row;
; #pragma unroll
;                             for (int e = 0; e < 6; ++e) lp[(size_t)(e * 32768u)] = z[e];
	v_add_f32_e32 v33, 1.0, v33
	v_sub_f32_e32 v31, v30, v31
	v_add_f32_e32 v33, v31, v33
	v_frexp_mant_f32_e32 v31, v32
	v_cvt_f64_f32_e32 v[42:43], v32
	v_cmp_gt_f32_e32 vcc, s19, v31
	v_frexp_exp_i32_f64_e32 v31, v[42:43]
	s_nop 0
	v_subbrev_co_u32_e32 v31, vcc, 0, v31, vcc
	v_sub_u32_e32 v42, 0, v31
	v_ldexp_f32 v32, v32, v42
	v_ldexp_f32 v33, v33, v42
	v_add_f32_e32 v42, -1.0, v32
	v_add_f32_e32 v43, 1.0, v42
	v_sub_f32_e32 v43, v32, v43
	v_add_f32_e32 v43, v33, v43
	v_add_f32_e32 v44, v42, v43
	v_sub_f32_e32 v42, v44, v42
	v_sub_f32_e32 v42, v43, v42
	v_add_f32_e32 v43, 1.0, v32
	v_add_f32_e32 v45, -1.0, v43
	v_sub_f32_e32 v32, v32, v45
	v_add_f32_e32 v32, v33, v32
	v_add_f32_e32 v33, v43, v32
	v_sub_f32_e32 v43, v33, v43
	v_sub_f32_e32 v32, v32, v43
	v_rcp_f32_e32 v43, v33
	v_cvt_f32_i32_e32 v31, v31
	v_cmp_neq_f32_e32 vcc, s27, v30
	v_mul_f32_e32 v45, v44, v43
	v_mul_f32_e32 v46, v33, v45
	v_fma_f32 v47, v45, v33, -v46
	v_fmac_f32_e32 v47, v45, v32
	v_add_f32_e32 v48, v46, v47
	v_sub_f32_e32 v49, v44, v48
	v_sub_f32_e32 v44, v44, v49
	v_sub_f32_e32 v46, v48, v46
	v_sub_f32_e32 v44, v44, v48
	v_add_f32_e32 v42, v42, v44
	v_sub_f32_e32 v44, v46, v47
	v_add_f32_e32 v42, v44, v42
	v_add_f32_e32 v44, v49, v42
	v_mul_f32_e32 v46, v43, v44
	v_mul_f32_e32 v47, v33, v46
	v_fma_f32 v33, v46, v33, -v47
	v_fmac_f32_e32 v33, v46, v32
	v_sub_f32_e32 v32, v49, v44
	v_add_f32_e32 v32, v42, v32
	v_add_f32_e32 v42, v47, v33
	v_sub_f32_e32 v48, v44, v42
	v_sub_f32_e32 v44, v44, v48
	v_sub_f32_e32 v47, v42, v47
	v_sub_f32_e32 v42, v44, v42
	v_add_f32_e32 v32, v32, v42
	v_sub_f32_e32 v33, v47, v33
	v_add_f32_e32 v32, v33, v32
	v_add_f32_e32 v33, v45, v46
	v_add_f32_e32 v32, v48, v32
	v_sub_f32_e32 v42, v33, v45
	v_mul_f32_e32 v32, v43, v32
	v_sub_f32_e32 v42, v46, v42
	v_add_f32_e32 v32, v42, v32
	v_mul_f32_e32 v45, 0x3f317218, v31
	v_add_f32_e32 v42, v33, v32
	v_fma_f32 v46, v31, s21, -v45
	v_mul_f32_e32 v43, v42, v42
	v_fmac_f32_e32 v46, 0xb102e308, v31
	v_sub_f32_e32 v31, v42, v33
	v_fmamk_f32 v44, v43, 0x3e9b6dac, v217
	v_sub_f32_e32 v31, v32, v31
	v_add_f32_e32 v32, v45, v46
	v_fmaak_f32 v44, v43, v44, 0x3f2aaada
	v_sub_f32_e32 v33, v32, v45
	v_ldexp_f32 v45, v42, 1
	v_mul_f32_e32 v42, v42, v43
	v_mul_f32_e32 v42, v42, v44
	v_add_f32_e32 v43, v45, v42
	v_sub_f32_e32 v44, v43, v45
	v_ldexp_f32 v31, v31, 1
	v_sub_f32_e32 v42, v42, v44
	v_add_f32_e32 v31, v31, v42
	v_add_f32_e32 v42, v43, v31
	v_sub_f32_e32 v43, v42, v43
	v_sub_f32_e32 v31, v31, v43
	v_add_f32_e32 v43, v32, v42
	v_sub_f32_e32 v44, v43, v32
	v_sub_f32_e32 v45, v43, v44
	v_sub_f32_e32 v33, v46, v33
	v_sub_f32_e32 v32, v32, v45
	v_sub_f32_e32 v42, v42, v44
	v_add_f32_e32 v32, v42, v32
	v_add_f32_e32 v42, v33, v31
	v_sub_f32_e32 v44, v42, v33
	v_sub_f32_e32 v45, v42, v44
	v_sub_f32_e32 v33, v33, v45
	v_sub_f32_e32 v31, v31, v44
	v_add_f32_e32 v32, v42, v32
	v_add_f32_e32 v31, v31, v33
	v_add_f32_e32 v33, v43, v32
	v_sub_f32_e32 v42, v33, v43
	v_sub_f32_e32 v32, v32, v42
	v_add_f32_e32 v31, v31, v32
	v_add_f32_e32 v31, v33, v31
	v_cndmask_b32_e32 v31, v230, v31, vcc
	v_cmp_ngt_f32_e32 vcc, -1.0, v30
	s_nop 1
	v_cndmask_b32_e32 v31, v231, v31, vcc
	v_cmp_neq_f32_e32 vcc, -1.0, v30
	s_nop 1
	v_cndmask_b32_e32 v31, v226, v31, vcc
	v_cmp_lt_f32_e64 vcc, |v30|, s33
	s_nop 1
	v_cndmask_b32_e32 v30, v31, v30, vcc
	v_sub_f32_e32 v120, v29, v30
	v_mul_f32_e32 v121, v121, v26
	v_add_f32_e32 v30, v121, v13
	v_min_f32_e32 v29, 0, v30
	v_mul_f32_e64 v30, |v30|, s3
	v_exp_f32_e32 v30, v30
	s_nop 0
	v_add_f32_e32 v32, 1.0, v30
	v_add_f32_e32 v31, -1.0, v32
	v_sub_f32_e32 v33, v31, v32
	v_add_f32_e32 v33, 1.0, v33
	v_sub_f32_e32 v31, v30, v31
	v_add_f32_e32 v33, v31, v33
	v_frexp_mant_f32_e32 v31, v32
	v_cvt_f64_f32_e32 v[42:43], v32
	v_cmp_gt_f32_e32 vcc, s19, v31
	v_frexp_exp_i32_f64_e32 v31, v[42:43]
	s_nop 0
	v_subbrev_co_u32_e32 v31, vcc, 0, v31, vcc
	v_sub_u32_e32 v42, 0, v31
	v_ldexp_f32 v32, v32, v42
	v_ldexp_f32 v33, v33, v42
	v_add_f32_e32 v42, -1.0, v32
	v_add_f32_e32 v43, 1.0, v42
	v_sub_f32_e32 v43, v32, v43
	v_add_f32_e32 v43, v33, v43
	v_add_f32_e32 v44, v42, v43
	v_sub_f32_e32 v42, v44, v42
	v_sub_f32_e32 v42, v43, v42
	v_add_f32_e32 v43, 1.0, v32
	v_add_f32_e32 v45, -1.0, v43
	v_sub_f32_e32 v32, v32, v45
	v_add_f32_e32 v32, v33, v32
	v_add_f32_e32 v33, v43, v32
	v_sub_f32_e32 v43, v33, v43
	v_sub_f32_e32 v32, v32, v43
	v_rcp_f32_e32 v43, v33
	v_cvt_f32_i32_e32 v31, v31
	v_cmp_neq_f32_e32 vcc, s27, v30
	v_mul_f32_e32 v45, v44, v43
	v_mul_f32_e32 v46, v33, v45
	v_fma_f32 v47, v45, v33, -v46
	v_fmac_f32_e32 v47, v45, v32
	v_add_f32_e32 v48, v46, v47
	v_sub_f32_e32 v49, v44, v48
	v_sub_f32_e32 v44, v44, v49
	v_sub_f32_e32 v46, v48, v46
	v_sub_f32_e32 v44, v44, v48
	v_add_f32_e32 v42, v42, v44
	v_sub_f32_e32 v44, v46, v47
	v_add_f32_e32 v42, v44, v42
	v_add_f32_e32 v44, v49, v42
	v_mul_f32_e32 v46, v43, v44
	v_mul_f32_e32 v47, v33, v46
	v_fma_f32 v33, v46, v33, -v47
	v_fmac_f32_e32 v33, v46, v32
	v_sub_f32_e32 v32, v49, v44
	v_add_f32_e32 v32, v42, v32
	v_add_f32_e32 v42, v47, v33
	v_sub_f32_e32 v48, v44, v42
	v_sub_f32_e32 v44, v44, v48
	v_sub_f32_e32 v47, v42, v47
	v_sub_f32_e32 v42, v44, v42
	v_add_f32_e32 v32, v32, v42
	v_sub_f32_e32 v33, v47, v33
	v_add_f32_e32 v32, v33, v32
	v_add_f32_e32 v33, v45, v46
	v_add_f32_e32 v32, v48, v32
	v_sub_f32_e32 v42, v33, v45
	v_mul_f32_e32 v32, v43, v32
	v_sub_f32_e32 v42, v46, v42
	v_add_f32_e32 v32, v42, v32
	v_mul_f32_e32 v45, 0x3f317218, v31
	v_add_f32_e32 v42, v33, v32
	v_fma_f32 v46, v31, s21, -v45
	v_mul_f32_e32 v43, v42, v42
	v_fmac_f32_e32 v46, 0xb102e308, v31
	v_sub_f32_e32 v31, v42, v33
	v_fmamk_f32 v44, v43, 0x3e9b6dac, v217
; #define PG8_PACK8(y0, y1) (u32x4){cvt_pk_bf16((y0)[0], (y0)[1]), cvt_pk_bf16((y0)[2], (y0)[3]), cvt_pk_bf16((y1)[0], (y1)[1]), cvt_pk_bf16((y1)[2], (y1)[3])}
;     __device__ __forceinline__ void operator()(const f32x4 (&acc)[2][2][4][2], const Unit& u, int ui, int wr, int wc, int fr, int fq) const {
;     ...
;                         const f32x4 y0 = acc[ai][bj][m][0] * rs, y1 = acc[ai][bj][m][1] * rs;
;                         if (pn == 12 || bj == 0) {
;                             const unsigned gcol = (unsigned)((pn == 12 ? 0 : 256) + 128 * bj + 32 * wc + 8 * fq);
;                             f32x4 s0, s1;
; #pragma unroll
;                             for (int e = 0; e < 4; ++e) { s0[e] = __builtin_amdgcn_rcpf(1.0f + __builtin_amdgcn_exp2f(y0[e] * -1.4426950408889634f)); s1[e] = __builtin_amdgcn_rcpf(1.0f + __builtin_amdgcn_exp2f(y1[e] * -1.4426950408889634f)); }
;                             *(u32x4*)(ws + E_GF + (size_t)((row * 384u + gcol) * 2u)) = PG8_PACK8(s0, s1);
;                         } else if (wc == 0 && fq == 0) {
;                             float z[6] = {y0[0], y0[1], y0[2], y0[3], y1[0], y1[1]};
; #pragma unroll
;                             for (int e = 0; e < 6; ++e) { const float zz = z[e] + bfg[e]; z[e] = fminf(zz, 0.f) - log1pf(__expf(-fabsf(zz))); }
	v_sub_f32_e32 v31, v32, v31
	v_add_f32_e32 v32, v45, v46
	v_fmaak_f32 v44, v43, v44, 0x3f2aaada
	v_sub_f32_e32 v33, v32, v45
	v_ldexp_f32 v45, v42, 1
	v_mul_f32_e32 v42, v42, v43
	v_mul_f32_e32 v42, v42, v44
	v_add_f32_e32 v43, v45, v42
	v_sub_f32_e32 v44, v43, v45
	v_ldexp_f32 v31, v31, 1
	v_sub_f32_e32 v42, v42, v44
	v_add_f32_e32 v31, v31, v42
	v_add_f32_e32 v42, v43, v31
	v_sub_f32_e32 v43, v42, v43
	v_sub_f32_e32 v31, v31, v43
	v_add_f32_e32 v43, v32, v42
	v_sub_f32_e32 v44, v43, v32
	v_sub_f32_e32 v45, v43, v44
	v_sub_f32_e32 v33, v46, v33
	v_sub_f32_e32 v32, v32, v45
	v_sub_f32_e32 v42, v42, v44
	v_add_f32_e32 v32, v42, v32
	v_add_f32_e32 v42, v33, v31
	v_sub_f32_e32 v44, v42, v33
	v_sub_f32_e32 v45, v42, v44
	v_sub_f32_e32 v33, v33, v45
	v_sub_f32_e32 v31, v31, v44
	v_add_f32_e32 v32, v42, v32
	v_add_f32_e32 v31, v31, v33
	v_add_f32_e32 v33, v43, v32
	v_sub_f32_e32 v42, v33, v43
	v_sub_f32_e32 v32, v32, v42
	v_add_f32_e32 v31, v31, v32
	v_add_f32_e32 v31, v33, v31
	v_cndmask_b32_e32 v31, v230, v31, vcc
	v_cmp_ngt_f32_e32 vcc, -1.0, v30
	s_nop 1
	v_cndmask_b32_e32 v31, v231, v31, vcc
	v_cmp_neq_f32_e32 vcc, -1.0, v30
	s_nop 1
	v_cndmask_b32_e32 v31, v226, v31, vcc
	v_cmp_lt_f32_e64 vcc, |v30|, s33
	s_nop 1
	v_cndmask_b32_e32 v30, v31, v30, vcc
	v_sub_f32_e32 v121, v29, v30
	v_mul_f32_e32 v114, v114, v26
	v_add_f32_e32 v30, v114, v14
	v_min_f32_e32 v29, 0, v30
	v_mul_f32_e64 v30, |v30|, s3
	v_exp_f32_e32 v30, v30
	s_nop 0
	v_add_f32_e32 v32, 1.0, v30
	v_add_f32_e32 v31, -1.0, v32
	v_sub_f32_e32 v33, v31, v32
	v_add_f32_e32 v33, 1.0, v33
	v_sub_f32_e32 v31, v30, v31
	v_add_f32_e32 v33, v31, v33
	v_frexp_mant_f32_e32 v31, v32
	v_cvt_f64_f32_e32 v[42:43], v32
	v_cmp_gt_f32_e32 vcc, s19, v31
	v_frexp_exp_i32_f64_e32 v31, v[42:43]
	s_nop 0
	v_subbrev_co_u32_e32 v31, vcc, 0, v31, vcc
	v_sub_u32_e32 v42, 0, v31
	v_ldexp_f32 v32, v32, v42
	v_ldexp_f32 v33, v33, v42
	v_add_f32_e32 v42, -1.0, v32
	v_add_f32_e32 v43, 1.0, v42
	v_sub_f32_e32 v43, v32, v43
	v_add_f32_e32 v43, v33, v43
	v_add_f32_e32 v44, v42, v43
	v_sub_f32_e32 v42, v44, v42
	v_sub_f32_e32 v42, v43, v42
	v_add_f32_e32 v43, 1.0, v32
	v_add_f32_e32 v45, -1.0, v43
	v_sub_f32_e32 v32, v32, v45
	v_add_f32_e32 v32, v33, v32
	v_add_f32_e32 v33, v43, v32
	v_sub_f32_e32 v43, v33, v43
	v_sub_f32_e32 v32, v32, v43
	v_rcp_f32_e32 v43, v33
	v_cvt_f32_i32_e32 v31, v31
	v_cmp_neq_f32_e32 vcc, s27, v30
	v_mul_f32_e32 v45, v44, v43
	v_mul_f32_e32 v46, v33, v45
	v_fma_f32 v47, v45, v33, -v46
	v_fmac_f32_e32 v47, v45, v32
	v_add_f32_e32 v48, v46, v47
	v_sub_f32_e32 v49, v44, v48
	v_sub_f32_e32 v44, v44, v49
	v_sub_f32_e32 v46, v48, v46
	v_sub_f32_e32 v44, v44, v48
	v_add_f32_e32 v42, v42, v44
	v_sub_f32_e32 v44, v46, v47
	v_add_f32_e32 v42, v44, v42
	v_add_f32_e32 v44, v49, v42
	v_mul_f32_e32 v46, v43, v44
	v_mul_f32_e32 v47, v33, v46
	v_fma_f32 v33, v46, v33, -v47
	v_fmac_f32_e32 v33, v46, v32
	v_sub_f32_e32 v32, v49, v44
	v_add_f32_e32 v32, v42, v32
	v_add_f32_e32 v42, v47, v33
	v_sub_f32_e32 v48, v44, v42
	v_sub_f32_e32 v44, v44, v48
	v_sub_f32_e32 v47, v42, v47
	v_sub_f32_e32 v42, v44, v42
	v_add_f32_e32 v32, v32, v42
	v_sub_f32_e32 v33, v47, v33
	v_add_f32_e32 v32, v33, v32
	v_add_f32_e32 v33, v45, v46
	v_add_f32_e32 v32, v48, v32
	v_sub_f32_e32 v42, v33, v45
	v_mul_f32_e32 v32, v43, v32
	v_sub_f32_e32 v42, v46, v42
	v_add_f32_e32 v32, v42, v32
	v_mul_f32_e32 v45, 0x3f317218, v31
	v_add_f32_e32 v42, v33, v32
	v_fma_f32 v46, v31, s21, -v45
	v_mul_f32_e32 v43, v42, v42
	v_fmac_f32_e32 v46, 0xb102e308, v31
	v_sub_f32_e32 v31, v42, v33
	v_fmamk_f32 v44, v43, 0x3e9b6dac, v217
	v_sub_f32_e32 v31, v32, v31
	v_add_f32_e32 v32, v45, v46
	v_fmaak_f32 v44, v43, v44, 0x3f2aaada
	v_sub_f32_e32 v33, v32, v45
	v_ldexp_f32 v45, v42, 1
	v_mul_f32_e32 v42, v42, v43
	v_mul_f32_e32 v42, v42, v44
	v_add_f32_e32 v43, v45, v42
	v_sub_f32_e32 v44, v43, v45
	v_ldexp_f32 v31, v31, 1
	v_sub_f32_e32 v42, v42, v44
	v_add_f32_e32 v31, v31, v42
	v_add_f32_e32 v42, v43, v31
	v_sub_f32_e32 v43, v42, v43
	v_sub_f32_e32 v31, v31, v43
	v_add_f32_e32 v43, v32, v42
	v_sub_f32_e32 v44, v43, v32
	v_sub_f32_e32 v45, v43, v44
	v_sub_f32_e32 v33, v46, v33
	v_sub_f32_e32 v32, v32, v45
	v_sub_f32_e32 v42, v42, v44
	v_add_f32_e32 v32, v42, v32
	v_add_f32_e32 v42, v33, v31
	v_sub_f32_e32 v44, v42, v33
	v_sub_f32_e32 v45, v42, v44
	v_sub_f32_e32 v33, v33, v45
	v_sub_f32_e32 v31, v31, v44
	v_add_f32_e32 v32, v42, v32
	v_add_f32_e32 v31, v31, v33
	v_add_f32_e32 v33, v43, v32
	v_sub_f32_e32 v42, v33, v43
	v_sub_f32_e32 v32, v32, v42
	v_add_f32_e32 v31, v31, v32
	v_add_f32_e32 v31, v33, v31
	v_cndmask_b32_e32 v31, v230, v31, vcc
	v_cmp_ngt_f32_e32 vcc, -1.0, v30
	s_nop 1
	v_cndmask_b32_e32 v31, v231, v31, vcc
	v_cmp_neq_f32_e32 vcc, -1.0, v30
	s_nop 1
	v_cndmask_b32_e32 v31, v226, v31, vcc
	v_cmp_lt_f32_e64 vcc, |v30|, s33
	s_nop 1
	v_cndmask_b32_e32 v30, v31, v30, vcc
	v_sub_f32_e32 v114, v29, v30
	v_mul_f32_e32 v115, v115, v26
	v_add_f32_e32 v30, v115, v15
	v_min_f32_e32 v29, 0, v30
	v_mul_f32_e64 v30, |v30|, s3
	v_exp_f32_e32 v30, v30
	s_nop 0
	v_add_f32_e32 v32, 1.0, v30
	v_add_f32_e32 v31, -1.0, v32
	v_sub_f32_e32 v33, v31, v32
	v_add_f32_e32 v33, 1.0, v33
	v_sub_f32_e32 v31, v30, v31
	v_add_f32_e32 v33, v31, v33
	v_frexp_mant_f32_e32 v31, v32
	v_cvt_f64_f32_e32 v[42:43], v32
	v_cmp_gt_f32_e32 vcc, s19, v31
	v_frexp_exp_i32_f64_e32 v31, v[42:43]
	s_nop 0
	v_subbrev_co_u32_e32 v31, vcc, 0, v31, vcc
	v_sub_u32_e32 v42, 0, v31
	v_ldexp_f32 v32, v32, v42
	v_ldexp_f32 v33, v33, v42
	v_add_f32_e32 v42, -1.0, v32
	v_add_f32_e32 v43, 1.0, v42
	v_sub_f32_e32 v43, v32, v43
	v_add_f32_e32 v43, v33, v43
	v_add_f32_e32 v44, v42, v43
; #define PG8_PACK8(y0, y1) (u32x4){cvt_pk_bf16((y0)[0], (y0)[1]), cvt_pk_bf16((y0)[2], (y0)[3]), cvt_pk_bf16((y1)[0], (y1)[1]), cvt_pk_bf16((y1)[2], (y1)[3])}
;     __device__ __forceinline__ void operator()(const f32x4 (&acc)[2][2][4][2], const Unit& u, int ui, int wr, int wc, int fr, int fq) const {
;     ...
;                         const f32x4 y0 = acc[ai][bj][m][0] * rs, y1 = acc[ai][bj][m][1] * rs;
;                         if (pn == 12 || bj == 0) {
;                             const unsigned gcol = (unsigned)((pn == 12 ? 0 : 256) + 128 * bj + 32 * wc + 8 * fq);
;                             f32x4 s0, s1;
; #pragma unroll
;                             for (int e = 0; e < 4; ++e) { s0[e] = __builtin_amdgcn_rcpf(1.0f + __builtin_amdgcn_exp2f(y0[e] * -1.4426950408889634f)); s1[e] = __builtin_amdgcn_rcpf(1.0f + __builtin_amdgcn_exp2f(y1[e] * -1.4426950408889634f)); }
;                             *(u32x4*)(ws + E_GF + (size_t)((row * 384u + gcol) * 2u)) = PG8_PACK8(s0, s1);
;                         } else if (wc == 0 && fq == 0) {
;                             float z[6] = {y0[0], y0[1], y0[2], y0[3], y1[0], y1[1]};
; #pragma unroll
;                             for (int e = 0; e < 6; ++e) { const float zz = z[e] + bfg[e]; z[e] = fminf(zz, 0.f) - log1pf(__expf(-fabsf(zz))); }
	v_sub_f32_e32 v42, v44, v42
	v_sub_f32_e32 v42, v43, v42
	v_add_f32_e32 v43, 1.0, v32
	v_add_f32_e32 v45, -1.0, v43
	v_sub_f32_e32 v32, v32, v45
	v_add_f32_e32 v32, v33, v32
	v_add_f32_e32 v33, v43, v32
	v_sub_f32_e32 v43, v33, v43
	v_sub_f32_e32 v32, v32, v43
	v_rcp_f32_e32 v43, v33
	v_cvt_f32_i32_e32 v31, v31
	v_cmp_neq_f32_e32 vcc, s27, v30
	v_mul_f32_e32 v45, v44, v43
	v_mul_f32_e32 v46, v33, v45
	v_fma_f32 v47, v45, v33, -v46
	v_fmac_f32_e32 v47, v45, v32
	v_add_f32_e32 v48, v46, v47
	v_sub_f32_e32 v49, v44, v48
	v_sub_f32_e32 v44, v44, v49
	v_sub_f32_e32 v46, v48, v46
	v_sub_f32_e32 v44, v44, v48
	v_add_f32_e32 v42, v42, v44
	v_sub_f32_e32 v44, v46, v47
	v_add_f32_e32 v42, v44, v42
	v_add_f32_e32 v44, v49, v42
	v_mul_f32_e32 v46, v43, v44
	v_mul_f32_e32 v47, v33, v46
	v_fma_f32 v33, v46, v33, -v47
	v_fmac_f32_e32 v33, v46, v32
	v_sub_f32_e32 v32, v49, v44
	v_add_f32_e32 v32, v42, v32
	v_add_f32_e32 v42, v47, v33
	v_sub_f32_e32 v48, v44, v42
	v_sub_f32_e32 v44, v44, v48
	v_sub_f32_e32 v47, v42, v47
	v_sub_f32_e32 v42, v44, v42
	v_add_f32_e32 v32, v32, v42
	v_sub_f32_e32 v33, v47, v33
	v_add_f32_e32 v32, v33, v32
	v_add_f32_e32 v33, v45, v46
	v_add_f32_e32 v32, v48, v32
	v_sub_f32_e32 v42, v33, v45
	v_mul_f32_e32 v32, v43, v32
	v_sub_f32_e32 v42, v46, v42
	v_add_f32_e32 v32, v42, v32
	v_mul_f32_e32 v45, 0x3f317218, v31
	v_add_f32_e32 v42, v33, v32
	v_fma_f32 v46, v31, s21, -v45
	v_mul_f32_e32 v43, v42, v42
	v_fmac_f32_e32 v46, 0xb102e308, v31
	v_sub_f32_e32 v31, v42, v33
	v_fmamk_f32 v44, v43, 0x3e9b6dac, v217
	v_sub_f32_e32 v31, v32, v31
	v_add_f32_e32 v32, v45, v46
	v_fmaak_f32 v44, v43, v44, 0x3f2aaada
	v_sub_f32_e32 v33, v32, v45
	v_ldexp_f32 v45, v42, 1
	v_mul_f32_e32 v42, v42, v43
	v_mul_f32_e32 v42, v42, v44
	v_add_f32_e32 v43, v45, v42
	v_sub_f32_e32 v44, v43, v45
	v_ldexp_f32 v31, v31, 1
	v_sub_f32_e32 v42, v42, v44
	v_add_f32_e32 v31, v31, v42
	v_add_f32_e32 v42, v43, v31
	v_sub_f32_e32 v43, v42, v43
	v_sub_f32_e32 v31, v31, v43
	v_add_f32_e32 v43, v32, v42
	v_sub_f32_e32 v44, v43, v32
	v_sub_f32_e32 v45, v43, v44
	v_sub_f32_e32 v33, v46, v33
	v_sub_f32_e32 v32, v32, v45
	v_sub_f32_e32 v42, v42, v44
	v_add_f32_e32 v32, v42, v32
	v_add_f32_e32 v42, v33, v31
	v_sub_f32_e32 v44, v42, v33
	v_sub_f32_e32 v45, v42, v44
	v_sub_f32_e32 v33, v33, v45
	v_sub_f32_e32 v31, v31, v44
	v_add_f32_e32 v32, v42, v32
	v_add_f32_e32 v31, v31, v33
	v_add_f32_e32 v33, v43, v32
	v_sub_f32_e32 v42, v33, v43
	v_sub_f32_e32 v32, v32, v42
	v_add_f32_e32 v31, v31, v32
	v_add_f32_e32 v31, v33, v31
	v_cndmask_b32_e32 v31, v230, v31, vcc
	v_cmp_ngt_f32_e32 vcc, -1.0, v30
	s_nop 1
	v_cndmask_b32_e32 v31, v231, v31, vcc
	v_cmp_neq_f32_e32 vcc, -1.0, v30
	s_nop 1
	v_cndmask_b32_e32 v31, v226, v31, vcc
	v_cmp_lt_f32_e64 vcc, |v30|, s33
	s_nop 1
	v_cndmask_b32_e32 v30, v31, v30, vcc
	v_sub_f32_e32 v115, v29, v30
	v_mul_f32_e32 v102, v102, v27
	v_add_f32_e32 v30, v102, v10
	v_min_f32_e32 v29, 0, v30
	v_mul_f32_e64 v30, |v30|, s3
	v_exp_f32_e32 v30, v30
	s_nop 0
	v_add_f32_e32 v32, 1.0, v30
	v_add_f32_e32 v31, -1.0, v32
	v_sub_f32_e32 v33, v31, v32
	v_add_f32_e32 v33, 1.0, v33
	v_sub_f32_e32 v31, v30, v31
	v_add_f32_e32 v33, v31, v33
	v_frexp_mant_f32_e32 v31, v32
	v_cvt_f64_f32_e32 v[42:43], v32
	v_cmp_gt_f32_e32 vcc, s19, v31
	v_frexp_exp_i32_f64_e32 v31, v[42:43]
	s_nop 0
	v_subbrev_co_u32_e32 v31, vcc, 0, v31, vcc
	v_sub_u32_e32 v42, 0, v31
	v_ldexp_f32 v32, v32, v42
	v_ldexp_f32 v33, v33, v42
	v_add_f32_e32 v42, -1.0, v32
	v_add_f32_e32 v43, 1.0, v42
	v_sub_f32_e32 v43, v32, v43
	v_add_f32_e32 v43, v33, v43
	v_add_f32_e32 v44, v42, v43
	v_sub_f32_e32 v42, v44, v42
	v_sub_f32_e32 v42, v43, v42
	v_add_f32_e32 v43, 1.0, v32
	v_add_f32_e32 v45, -1.0, v43
	v_sub_f32_e32 v32, v32, v45
	v_add_f32_e32 v32, v33, v32
	v_add_f32_e32 v33, v43, v32
	v_sub_f32_e32 v43, v33, v43
	v_sub_f32_e32 v32, v32, v43
	v_rcp_f32_e32 v43, v33
	v_cvt_f32_i32_e32 v31, v31
	v_cmp_neq_f32_e32 vcc, s27, v30
	v_mul_f32_e32 v45, v44, v43
	v_mul_f32_e32 v46, v33, v45
	v_fma_f32 v47, v45, v33, -v46
	v_fmac_f32_e32 v47, v45, v32
	v_add_f32_e32 v48, v46, v47
	v_sub_f32_e32 v49, v44, v48
	v_sub_f32_e32 v44, v44, v49
	v_sub_f32_e32 v46, v48, v46
	v_sub_f32_e32 v44, v44, v48
	v_add_f32_e32 v42, v42, v44
	v_sub_f32_e32 v44, v46, v47
	v_add_f32_e32 v42, v44, v42
	v_add_f32_e32 v44, v49, v42
	v_mul_f32_e32 v46, v43, v44
	v_mul_f32_e32 v47, v33, v46
	v_fma_f32 v33, v46, v33, -v47
	v_fmac_f32_e32 v33, v46, v32
	v_sub_f32_e32 v32, v49, v44
	v_add_f32_e32 v32, v42, v32
	v_add_f32_e32 v42, v47, v33
	v_sub_f32_e32 v48, v44, v42
	v_sub_f32_e32 v44, v44, v48
	v_sub_f32_e32 v47, v42, v47
	v_sub_f32_e32 v42, v44, v42
	v_add_f32_e32 v32, v32, v42
	v_sub_f32_e32 v33, v47, v33
	v_add_f32_e32 v32, v33, v32
	v_add_f32_e32 v33, v45, v46
	v_add_f32_e32 v32, v48, v32
	v_sub_f32_e32 v42, v33, v45
	v_mul_f32_e32 v32, v43, v32
	v_sub_f32_e32 v42, v46, v42
	v_add_f32_e32 v32, v42, v32
	v_mul_f32_e32 v45, 0x3f317218, v31
	v_add_f32_e32 v42, v33, v32
	v_fma_f32 v46, v31, s21, -v45
	v_mul_f32_e32 v43, v42, v42
	v_fmac_f32_e32 v46, 0xb102e308, v31
	v_sub_f32_e32 v31, v42, v33
	v_fmamk_f32 v44, v43, 0x3e9b6dac, v217
	v_sub_f32_e32 v31, v32, v31
	v_add_f32_e32 v32, v45, v46
	v_fmaak_f32 v44, v43, v44, 0x3f2aaada
	v_sub_f32_e32 v33, v32, v45
	v_ldexp_f32 v45, v42, 1
	v_mul_f32_e32 v42, v42, v43
	v_mul_f32_e32 v42, v42, v44
	v_add_f32_e32 v43, v45, v42
	v_sub_f32_e32 v44, v43, v45
	v_ldexp_f32 v31, v31, 1
	v_sub_f32_e32 v42, v42, v44
	v_add_f32_e32 v31, v31, v42
	v_add_f32_e32 v42, v43, v31
	v_sub_f32_e32 v43, v42, v43
	v_sub_f32_e32 v31, v31, v43
	v_add_f32_e32 v43, v32, v42
	v_sub_f32_e32 v44, v43, v32
	v_sub_f32_e32 v45, v43, v44
; #define PG8_PACK8(y0, y1) (u32x4){cvt_pk_bf16((y0)[0], (y0)[1]), cvt_pk_bf16((y0)[2], (y0)[3]), cvt_pk_bf16((y1)[0], (y1)[1]), cvt_pk_bf16((y1)[2], (y1)[3])}
;     __device__ __forceinline__ void operator()(const f32x4 (&acc)[2][2][4][2], const Unit& u, int ui, int wr, int wc, int fr, int fq) const {
;     ...
;                         const f32x4 y0 = acc[ai][bj][m][0] * rs, y1 = acc[ai][bj][m][1] * rs;
;                         if (pn == 12 || bj == 0) {
;                             const unsigned gcol = (unsigned)((pn == 12 ? 0 : 256) + 128 * bj + 32 * wc + 8 * fq);
;                             f32x4 s0, s1;
; #pragma unroll
;                             for (int e = 0; e < 4; ++e) { s0[e] = __builtin_amdgcn_rcpf(1.0f + __builtin_amdgcn_exp2f(y0[e] * -1.4426950408889634f)); s1[e] = __builtin_amdgcn_rcpf(1.0f + __builtin_amdgcn_exp2f(y1[e] * -1.4426950408889634f)); }
;                             *(u32x4*)(ws + E_GF + (size_t)((row * 384u + gcol) * 2u)) = PG8_PACK8(s0, s1);
;                         } else if (wc == 0 && fq == 0) {
;                             float z[6] = {y0[0], y0[1], y0[2], y0[3], y1[0], y1[1]};
; #pragma unroll
;                             for (int e = 0; e < 6; ++e) { const float zz = z[e] + bfg[e]; z[e] = fminf(zz, 0.f) - log1pf(__expf(-fabsf(zz))); }
	v_sub_f32_e32 v33, v46, v33
	v_sub_f32_e32 v32, v32, v45
	v_sub_f32_e32 v42, v42, v44
	v_add_f32_e32 v32, v42, v32
	v_add_f32_e32 v42, v33, v31
	v_sub_f32_e32 v44, v42, v33
	v_sub_f32_e32 v45, v42, v44
	v_sub_f32_e32 v33, v33, v45
	v_sub_f32_e32 v31, v31, v44
	v_add_f32_e32 v32, v42, v32
	v_add_f32_e32 v31, v31, v33
	v_add_f32_e32 v33, v43, v32
	v_sub_f32_e32 v42, v33, v43
	v_sub_f32_e32 v32, v32, v42
	v_add_f32_e32 v31, v31, v32
	v_add_f32_e32 v31, v33, v31
	v_cndmask_b32_e32 v31, v230, v31, vcc
	v_cmp_ngt_f32_e32 vcc, -1.0, v30
	s_nop 1
	v_cndmask_b32_e32 v31, v231, v31, vcc
	v_cmp_neq_f32_e32 vcc, -1.0, v30
	s_nop 1
	v_cndmask_b32_e32 v31, v226, v31, vcc
	v_cmp_lt_f32_e64 vcc, |v30|, s33
	s_nop 1
	v_cndmask_b32_e32 v30, v31, v30, vcc
	v_sub_f32_e32 v102, v29, v30
	v_mul_f32_e32 v103, v103, v27
	v_add_f32_e32 v30, v103, v11
	v_min_f32_e32 v29, 0, v30
	v_mul_f32_e64 v30, |v30|, s3
	v_exp_f32_e32 v30, v30
	s_nop 0
	v_add_f32_e32 v32, 1.0, v30
	v_add_f32_e32 v31, -1.0, v32
	v_sub_f32_e32 v33, v31, v32
	v_add_f32_e32 v33, 1.0, v33
	v_sub_f32_e32 v31, v30, v31
	v_add_f32_e32 v33, v31, v33
	v_frexp_mant_f32_e32 v31, v32
	v_cvt_f64_f32_e32 v[42:43], v32
	v_cmp_gt_f32_e32 vcc, s19, v31
	v_frexp_exp_i32_f64_e32 v31, v[42:43]
	s_nop 0
	v_subbrev_co_u32_e32 v31, vcc, 0, v31, vcc
	v_sub_u32_e32 v42, 0, v31
	v_ldexp_f32 v32, v32, v42
	v_ldexp_f32 v33, v33, v42
	v_add_f32_e32 v42, -1.0, v32
	v_add_f32_e32 v43, 1.0, v42
	v_sub_f32_e32 v43, v32, v43
	v_add_f32_e32 v43, v33, v43
	v_add_f32_e32 v44, v42, v43
	v_sub_f32_e32 v42, v44, v42
	v_sub_f32_e32 v42, v43, v42
	v_add_f32_e32 v43, 1.0, v32
	v_add_f32_e32 v45, -1.0, v43
	v_sub_f32_e32 v32, v32, v45
	v_add_f32_e32 v32, v33, v32
	v_add_f32_e32 v33, v43, v32
	v_sub_f32_e32 v43, v33, v43
	v_sub_f32_e32 v32, v32, v43
	v_rcp_f32_e32 v43, v33
	v_cvt_f32_i32_e32 v31, v31
	v_cmp_neq_f32_e32 vcc, s27, v30
	v_mul_f32_e32 v45, v44, v43
	v_mul_f32_e32 v46, v33, v45
	v_fma_f32 v47, v45, v33, -v46
	v_fmac_f32_e32 v47, v45, v32
	v_add_f32_e32 v48, v46, v47
	v_sub_f32_e32 v49, v44, v48
	v_sub_f32_e32 v44, v44, v49
	v_sub_f32_e32 v46, v48, v46
	v_sub_f32_e32 v44, v44, v48
	v_add_f32_e32 v42, v42, v44
	v_sub_f32_e32 v44, v46, v47
	v_add_f32_e32 v42, v44, v42
	v_add_f32_e32 v44, v49, v42
	v_mul_f32_e32 v46, v43, v44
	v_mul_f32_e32 v47, v33, v46
	v_fma_f32 v33, v46, v33, -v47
	v_fmac_f32_e32 v33, v46, v32
	v_sub_f32_e32 v32, v49, v44
	v_add_f32_e32 v32, v42, v32
	v_add_f32_e32 v42, v47, v33
	v_sub_f32_e32 v48, v44, v42
	v_sub_f32_e32 v44, v44, v48
	v_sub_f32_e32 v47, v42, v47
	v_sub_f32_e32 v42, v44, v42
	v_add_f32_e32 v32, v32, v42
	v_sub_f32_e32 v33, v47, v33
	v_add_f32_e32 v32, v33, v32
	v_add_f32_e32 v33, v45, v46
	v_add_f32_e32 v32, v48, v32
	v_sub_f32_e32 v42, v33, v45
	v_mul_f32_e32 v32, v43, v32
	v_sub_f32_e32 v42, v46, v42
	v_add_f32_e32 v32, v42, v32
	v_mul_f32_e32 v45, 0x3f317218, v31
	v_add_f32_e32 v42, v33, v32
	v_fma_f32 v46, v31, s21, -v45
	v_mul_f32_e32 v43, v42, v42
	v_fmac_f32_e32 v46, 0xb102e308, v31
	v_sub_f32_e32 v31, v42, v33
	v_fmamk_f32 v44, v43, 0x3e9b6dac, v217
	v_sub_f32_e32 v31, v32, v31
	v_add_f32_e32 v32, v45, v46
	v_fmaak_f32 v44, v43, v44, 0x3f2aaada
	v_sub_f32_e32 v33, v32, v45
	v_ldexp_f32 v45, v42, 1
	v_mul_f32_e32 v42, v42, v43
	v_mul_f32_e32 v42, v42, v44
	v_add_f32_e32 v43, v45, v42
	v_sub_f32_e32 v44, v43, v45
	v_ldexp_f32 v31, v31, 1
	v_sub_f32_e32 v42, v42, v44
	v_add_f32_e32 v31, v31, v42
	v_add_f32_e32 v42, v43, v31
	v_sub_f32_e32 v43, v42, v43
	v_sub_f32_e32 v31, v31, v43
	v_add_f32_e32 v43, v32, v42
	v_sub_f32_e32 v44, v43, v32
	v_sub_f32_e32 v45, v43, v44
	v_sub_f32_e32 v33, v46, v33
	v_sub_f32_e32 v32, v32, v45
	v_sub_f32_e32 v42, v42, v44
	v_add_f32_e32 v32, v42, v32
	v_add_f32_e32 v42, v33, v31
	v_sub_f32_e32 v44, v42, v33
	v_sub_f32_e32 v45, v42, v44
	v_sub_f32_e32 v33, v33, v45
	v_sub_f32_e32 v31, v31, v44
	v_add_f32_e32 v32, v42, v32
	v_add_f32_e32 v31, v31, v33
	v_add_f32_e32 v33, v43, v32
	v_sub_f32_e32 v42, v33, v43
	v_sub_f32_e32 v32, v32, v42
	v_add_f32_e32 v31, v31, v32
	v_add_f32_e32 v31, v33, v31
	v_cndmask_b32_e32 v31, v230, v31, vcc
	v_cmp_ngt_f32_e32 vcc, -1.0, v30
	s_nop 1
	v_cndmask_b32_e32 v31, v231, v31, vcc
	v_cmp_neq_f32_e32 vcc, -1.0, v30
	s_nop 1
	v_cndmask_b32_e32 v31, v226, v31, vcc
	v_cmp_lt_f32_e64 vcc, |v30|, s33
	s_nop 1
	v_cndmask_b32_e32 v30, v31, v30, vcc
	v_sub_f32_e32 v103, v29, v30
	v_mul_f32_e32 v104, v104, v27
	v_add_f32_e32 v30, v104, v12
	v_min_f32_e32 v29, 0, v30
	v_mul_f32_e64 v30, |v30|, s3
	v_exp_f32_e32 v30, v30
	s_nop 0
	v_add_f32_e32 v32, 1.0, v30
	v_add_f32_e32 v31, -1.0, v32
	v_sub_f32_e32 v33, v31, v32
	v_add_f32_e32 v33, 1.0, v33
	v_sub_f32_e32 v31, v30, v31
	v_add_f32_e32 v33, v31, v33
	v_frexp_mant_f32_e32 v31, v32
	v_cvt_f64_f32_e32 v[42:43], v32
	v_cmp_gt_f32_e32 vcc, s19, v31
	v_frexp_exp_i32_f64_e32 v31, v[42:43]
	s_nop 0
	v_subbrev_co_u32_e32 v31, vcc, 0, v31, vcc
	v_sub_u32_e32 v42, 0, v31
	v_ldexp_f32 v32, v32, v42
	v_ldexp_f32 v33, v33, v42
	v_add_f32_e32 v42, -1.0, v32
	v_add_f32_e32 v43, 1.0, v42
	v_sub_f32_e32 v43, v32, v43
	v_add_f32_e32 v43, v33, v43
	v_add_f32_e32 v44, v42, v43
	v_sub_f32_e32 v42, v44, v42
	v_sub_f32_e32 v42, v43, v42
	v_add_f32_e32 v43, 1.0, v32
	v_add_f32_e32 v45, -1.0, v43
	v_sub_f32_e32 v32, v32, v45
	v_add_f32_e32 v32, v33, v32
	v_add_f32_e32 v33, v43, v32
	v_sub_f32_e32 v43, v33, v43
	v_sub_f32_e32 v32, v32, v43
	v_rcp_f32_e32 v43, v33
	v_cvt_f32_i32_e32 v31, v31
	v_cmp_neq_f32_e32 vcc, s27, v30
	v_mul_f32_e32 v45, v44, v43
	v_mul_f32_e32 v46, v33, v45
	v_fma_f32 v47, v45, v33, -v46
	v_fmac_f32_e32 v47, v45, v32
	v_add_f32_e32 v48, v46, v47
	v_sub_f32_e32 v49, v44, v48
; #define PG8_PACK8(y0, y1) (u32x4){cvt_pk_bf16((y0)[0], (y0)[1]), cvt_pk_bf16((y0)[2], (y0)[3]), cvt_pk_bf16((y1)[0], (y1)[1]), cvt_pk_bf16((y1)[2], (y1)[3])}
;     __device__ __forceinline__ void operator()(const f32x4 (&acc)[2][2][4][2], const Unit& u, int ui, int wr, int wc, int fr, int fq) const {
;     ...
;                         const f32x4 y0 = acc[ai][bj][m][0] * rs, y1 = acc[ai][bj][m][1] * rs;
;                         if (pn == 12 || bj == 0) {
;                             const unsigned gcol = (unsigned)((pn == 12 ? 0 : 256) + 128 * bj + 32 * wc + 8 * fq);
;                             f32x4 s0, s1;
; #pragma unroll
;                             for (int e = 0; e < 4; ++e) { s0[e] = __builtin_amdgcn_rcpf(1.0f + __builtin_amdgcn_exp2f(y0[e] * -1.4426950408889634f)); s1[e] = __builtin_amdgcn_rcpf(1.0f + __builtin_amdgcn_exp2f(y1[e] * -1.4426950408889634f)); }
;                             *(u32x4*)(ws + E_GF + (size_t)((row * 384u + gcol) * 2u)) = PG8_PACK8(s0, s1);
;                         } else if (wc == 0 && fq == 0) {
;                             float z[6] = {y0[0], y0[1], y0[2], y0[3], y1[0], y1[1]};
; #pragma unroll
;                             for (int e = 0; e < 6; ++e) { const float zz = z[e] + bfg[e]; z[e] = fminf(zz, 0.f) - log1pf(__expf(-fabsf(zz))); }
	v_sub_f32_e32 v44, v44, v49
	v_sub_f32_e32 v46, v48, v46
	v_sub_f32_e32 v44, v44, v48
	v_add_f32_e32 v42, v42, v44
	v_sub_f32_e32 v44, v46, v47
	v_add_f32_e32 v42, v44, v42
	v_add_f32_e32 v44, v49, v42
	v_mul_f32_e32 v46, v43, v44
	v_mul_f32_e32 v47, v33, v46
	v_fma_f32 v33, v46, v33, -v47
	v_fmac_f32_e32 v33, v46, v32
	v_sub_f32_e32 v32, v49, v44
	v_add_f32_e32 v32, v42, v32
	v_add_f32_e32 v42, v47, v33
	v_sub_f32_e32 v48, v44, v42
	v_sub_f32_e32 v44, v44, v48
	v_sub_f32_e32 v47, v42, v47
	v_sub_f32_e32 v42, v44, v42
	v_add_f32_e32 v32, v32, v42
	v_sub_f32_e32 v33, v47, v33
	v_add_f32_e32 v32, v33, v32
	v_add_f32_e32 v33, v45, v46
	v_add_f32_e32 v32, v48, v32
	v_sub_f32_e32 v42, v33, v45
	v_mul_f32_e32 v32, v43, v32
	v_sub_f32_e32 v42, v46, v42
	v_add_f32_e32 v32, v42, v32
	v_mul_f32_e32 v45, 0x3f317218, v31
	v_add_f32_e32 v42, v33, v32
	v_fma_f32 v46, v31, s21, -v45
	v_mul_f32_e32 v43, v42, v42
	v_fmac_f32_e32 v46, 0xb102e308, v31
	v_sub_f32_e32 v31, v42, v33
	v_fmamk_f32 v44, v43, 0x3e9b6dac, v217
	v_sub_f32_e32 v31, v32, v31
	v_add_f32_e32 v32, v45, v46
	v_fmaak_f32 v44, v43, v44, 0x3f2aaada
	v_sub_f32_e32 v33, v32, v45
	v_ldexp_f32 v45, v42, 1
	v_mul_f32_e32 v42, v42, v43
	v_mul_f32_e32 v42, v42, v44
	v_add_f32_e32 v43, v45, v42
	v_sub_f32_e32 v44, v43, v45
	v_ldexp_f32 v31, v31, 1
	v_sub_f32_e32 v42, v42, v44
	v_add_f32_e32 v31, v31, v42
	v_add_f32_e32 v42, v43, v31
	v_sub_f32_e32 v43, v42, v43
	v_sub_f32_e32 v31, v31, v43
	v_add_f32_e32 v43, v32, v42
	v_sub_f32_e32 v44, v43, v32
	v_sub_f32_e32 v45, v43, v44
	v_sub_f32_e32 v33, v46, v33
	v_sub_f32_e32 v32, v32, v45
	v_sub_f32_e32 v42, v42, v44
	v_add_f32_e32 v32, v42, v32
	v_add_f32_e32 v42, v33, v31
	v_sub_f32_e32 v44, v42, v33
	v_sub_f32_e32 v45, v42, v44
	v_sub_f32_e32 v33, v33, v45
	v_sub_f32_e32 v31, v31, v44
	v_add_f32_e32 v32, v42, v32
	v_add_f32_e32 v31, v31, v33
	v_add_f32_e32 v33, v43, v32
	v_sub_f32_e32 v42, v33, v43
	v_sub_f32_e32 v32, v32, v42
	v_add_f32_e32 v31, v31, v32
	v_add_f32_e32 v31, v33, v31
	v_cndmask_b32_e32 v31, v230, v31, vcc
	v_cmp_ngt_f32_e32 vcc, -1.0, v30
	s_nop 1
	v_cndmask_b32_e32 v31, v231, v31, vcc
	v_cmp_neq_f32_e32 vcc, -1.0, v30
	s_nop 1
	v_cndmask_b32_e32 v31, v226, v31, vcc
	v_cmp_lt_f32_e64 vcc, |v30|, s33
	s_nop 1
	v_cndmask_b32_e32 v30, v31, v30, vcc
	v_sub_f32_e32 v104, v29, v30
	v_mul_f32_e32 v105, v105, v27
	v_add_f32_e32 v30, v105, v13
	v_min_f32_e32 v29, 0, v30
	v_mul_f32_e64 v30, |v30|, s3
	v_exp_f32_e32 v30, v30
	s_nop 0
	v_add_f32_e32 v32, 1.0, v30
	v_add_f32_e32 v31, -1.0, v32
	v_sub_f32_e32 v33, v31, v32
	v_add_f32_e32 v33, 1.0, v33
	v_sub_f32_e32 v31, v30, v31
	v_add_f32_e32 v33, v31, v33
	v_frexp_mant_f32_e32 v31, v32
	v_cvt_f64_f32_e32 v[42:43], v32
	v_cmp_gt_f32_e32 vcc, s19, v31
	v_frexp_exp_i32_f64_e32 v31, v[42:43]
	s_nop 0
	v_subbrev_co_u32_e32 v31, vcc, 0, v31, vcc
	v_sub_u32_e32 v42, 0, v31
	v_ldexp_f32 v32, v32, v42
	v_ldexp_f32 v33, v33, v42
	v_add_f32_e32 v42, -1.0, v32
	v_add_f32_e32 v43, 1.0, v42
	v_sub_f32_e32 v43, v32, v43
	v_add_f32_e32 v43, v33, v43
	v_add_f32_e32 v44, v42, v43
	v_sub_f32_e32 v42, v44, v42
	v_sub_f32_e32 v42, v43, v42
	v_add_f32_e32 v43, 1.0, v32
	v_add_f32_e32 v45, -1.0, v43
	v_sub_f32_e32 v32, v32, v45
	v_add_f32_e32 v32, v33, v32
	v_add_f32_e32 v33, v43, v32
	v_sub_f32_e32 v43, v33, v43
	v_sub_f32_e32 v32, v32, v43
	v_rcp_f32_e32 v43, v33
	v_cvt_f32_i32_e32 v31, v31
	v_cmp_neq_f32_e32 vcc, s27, v30
	v_mul_f32_e32 v45, v44, v43
	v_mul_f32_e32 v46, v33, v45
	v_fma_f32 v47, v45, v33, -v46
	v_fmac_f32_e32 v47, v45, v32
	v_add_f32_e32 v48, v46, v47
	v_sub_f32_e32 v49, v44, v48
	v_sub_f32_e32 v44, v44, v49
	v_sub_f32_e32 v46, v48, v46
	v_sub_f32_e32 v44, v44, v48
	v_add_f32_e32 v42, v42, v44
	v_sub_f32_e32 v44, v46, v47
	v_add_f32_e32 v42, v44, v42
	v_add_f32_e32 v44, v49, v42
	v_mul_f32_e32 v46, v43, v44
	v_mul_f32_e32 v47, v33, v46
	v_fma_f32 v33, v46, v33, -v47
	v_fmac_f32_e32 v33, v46, v32
	v_sub_f32_e32 v32, v49, v44
	v_add_f32_e32 v32, v42, v32
	v_add_f32_e32 v42, v47, v33
	v_sub_f32_e32 v48, v44, v42
	v_sub_f32_e32 v44, v44, v48
	v_sub_f32_e32 v47, v42, v47
	v_sub_f32_e32 v42, v44, v42
	v_add_f32_e32 v32, v32, v42
	v_sub_f32_e32 v33, v47, v33
	v_add_f32_e32 v32, v33, v32
	v_add_f32_e32 v33, v45, v46
	v_add_f32_e32 v32, v48, v32
	v_sub_f32_e32 v42, v33, v45
	v_mul_f32_e32 v32, v43, v32
	v_sub_f32_e32 v42, v46, v42
	v_add_f32_e32 v32, v42, v32
	v_mul_f32_e32 v45, 0x3f317218, v31
	v_add_f32_e32 v42, v33, v32
	v_fma_f32 v46, v31, s21, -v45
	v_mul_f32_e32 v43, v42, v42
	v_fmac_f32_e32 v46, 0xb102e308, v31
	v_sub_f32_e32 v31, v42, v33
	v_fmamk_f32 v44, v43, 0x3e9b6dac, v217
	v_sub_f32_e32 v31, v32, v31
	v_add_f32_e32 v32, v45, v46
	v_fmaak_f32 v44, v43, v44, 0x3f2aaada
	v_sub_f32_e32 v33, v32, v45
	v_ldexp_f32 v45, v42, 1
	v_mul_f32_e32 v42, v42, v43
	v_mul_f32_e32 v42, v42, v44
	v_add_f32_e32 v43, v45, v42
	v_sub_f32_e32 v44, v43, v45
	v_ldexp_f32 v31, v31, 1
	v_sub_f32_e32 v42, v42, v44
	v_add_f32_e32 v31, v31, v42
	v_add_f32_e32 v42, v43, v31
	v_sub_f32_e32 v43, v42, v43
	v_sub_f32_e32 v31, v31, v43
	v_add_f32_e32 v43, v32, v42
	v_sub_f32_e32 v44, v43, v32
	v_sub_f32_e32 v45, v43, v44
	v_sub_f32_e32 v33, v46, v33
	v_sub_f32_e32 v32, v32, v45
	v_sub_f32_e32 v42, v42, v44
	v_add_f32_e32 v32, v42, v32
	v_add_f32_e32 v42, v33, v31
	v_sub_f32_e32 v44, v42, v33
	v_sub_f32_e32 v45, v42, v44
	v_sub_f32_e32 v33, v33, v45
	v_sub_f32_e32 v31, v31, v44
	v_add_f32_e32 v32, v42, v32
	v_add_f32_e32 v31, v31, v33
	v_add_f32_e32 v33, v43, v32
	v_sub_f32_e32 v42, v33, v43
	v_sub_f32_e32 v32, v32, v42
	v_add_f32_e32 v31, v31, v32
	v_add_f32_e32 v31, v33, v31
	v_cndmask_b32_e32 v31, v230, v31, vcc
; #define PG8_PACK8(y0, y1) (u32x4){cvt_pk_bf16((y0)[0], (y0)[1]), cvt_pk_bf16((y0)[2], (y0)[3]), cvt_pk_bf16((y1)[0], (y1)[1]), cvt_pk_bf16((y1)[2], (y1)[3])}
;     __device__ __forceinline__ void operator()(const f32x4 (&acc)[2][2][4][2], const Unit& u, int ui, int wr, int wc, int fr, int fq) const {
;     ...
;                         const f32x4 y0 = acc[ai][bj][m][0] * rs, y1 = acc[ai][bj][m][1] * rs;
;                         if (pn == 12 || bj == 0) {
;                             const unsigned gcol = (unsigned)((pn == 12 ? 0 : 256) + 128 * bj + 32 * wc + 8 * fq);
;                             f32x4 s0, s1;
; #pragma unroll
;                             for (int e = 0; e < 4; ++e) { s0[e] = __builtin_amdgcn_rcpf(1.0f + __builtin_amdgcn_exp2f(y0[e] * -1.4426950408889634f)); s1[e] = __builtin_amdgcn_rcpf(1.0f + __builtin_amdgcn_exp2f(y1[e] * -1.4426950408889634f)); }
;                             *(u32x4*)(ws + E_GF + (size_t)((row * 384u + gcol) * 2u)) = PG8_PACK8(s0, s1);
;                         } else if (wc == 0 && fq == 0) {
;                             float z[6] = {y0[0], y0[1], y0[2], y0[3], y1[0], y1[1]};
; #pragma unroll
;                             for (int e = 0; e < 6; ++e) { const float zz = z[e] + bfg[e]; z[e] = fminf(zz, 0.f) - log1pf(__expf(-fabsf(zz))); }
	v_cmp_ngt_f32_e32 vcc, -1.0, v30
	s_nop 1
	v_cndmask_b32_e32 v31, v231, v31, vcc
	v_cmp_neq_f32_e32 vcc, -1.0, v30
	s_nop 1
	v_cndmask_b32_e32 v31, v226, v31, vcc
	v_cmp_lt_f32_e64 vcc, |v30|, s33
	s_nop 1
	v_cndmask_b32_e32 v30, v31, v30, vcc
	v_sub_f32_e32 v105, v29, v30
	v_mul_f32_e32 v98, v98, v27
	v_add_f32_e32 v30, v98, v14
	v_min_f32_e32 v29, 0, v30
	v_mul_f32_e64 v30, |v30|, s3
	v_exp_f32_e32 v30, v30
	s_nop 0
	v_add_f32_e32 v32, 1.0, v30
	v_add_f32_e32 v31, -1.0, v32
	v_sub_f32_e32 v33, v31, v32
	v_add_f32_e32 v33, 1.0, v33
	v_sub_f32_e32 v31, v30, v31
	v_add_f32_e32 v33, v31, v33
	v_frexp_mant_f32_e32 v31, v32
	v_cvt_f64_f32_e32 v[42:43], v32
	v_cmp_gt_f32_e32 vcc, s19, v31
	v_frexp_exp_i32_f64_e32 v31, v[42:43]
	s_nop 0
	v_subbrev_co_u32_e32 v31, vcc, 0, v31, vcc
	v_sub_u32_e32 v42, 0, v31
	v_ldexp_f32 v32, v32, v42
	v_ldexp_f32 v33, v33, v42
	v_add_f32_e32 v42, -1.0, v32
	v_add_f32_e32 v43, 1.0, v42
	v_sub_f32_e32 v43, v32, v43
	v_add_f32_e32 v43, v33, v43
	v_add_f32_e32 v44, v42, v43
	v_sub_f32_e32 v42, v44, v42
	v_sub_f32_e32 v42, v43, v42
	v_add_f32_e32 v43, 1.0, v32
	v_add_f32_e32 v45, -1.0, v43
	v_sub_f32_e32 v32, v32, v45
	v_add_f32_e32 v32, v33, v32
	v_add_f32_e32 v33, v43, v32
	v_sub_f32_e32 v43, v33, v43
	v_sub_f32_e32 v32, v32, v43
	v_rcp_f32_e32 v43, v33
	v_cvt_f32_i32_e32 v31, v31
	v_cmp_neq_f32_e32 vcc, s27, v30
	v_mul_f32_e32 v45, v44, v43
	v_mul_f32_e32 v46, v33, v45
	v_fma_f32 v47, v45, v33, -v46
	v_fmac_f32_e32 v47, v45, v32
	v_add_f32_e32 v48, v46, v47
	v_sub_f32_e32 v49, v44, v48
	v_sub_f32_e32 v44, v44, v49
	v_sub_f32_e32 v46, v48, v46
	v_sub_f32_e32 v44, v44, v48
	v_add_f32_e32 v42, v42, v44
	v_sub_f32_e32 v44, v46, v47
	v_add_f32_e32 v42, v44, v42
	v_add_f32_e32 v44, v49, v42
	v_mul_f32_e32 v46, v43, v44
	v_mul_f32_e32 v47, v33, v46
	v_fma_f32 v33, v46, v33, -v47
	v_fmac_f32_e32 v33, v46, v32
	v_sub_f32_e32 v32, v49, v44
	v_add_f32_e32 v32, v42, v32
	v_add_f32_e32 v42, v47, v33
	v_sub_f32_e32 v48, v44, v42
	v_sub_f32_e32 v44, v44, v48
	v_sub_f32_e32 v47, v42, v47
	v_sub_f32_e32 v42, v44, v42
	v_add_f32_e32 v32, v32, v42
	v_sub_f32_e32 v33, v47, v33
	v_add_f32_e32 v32, v33, v32
	v_add_f32_e32 v33, v45, v46
	v_add_f32_e32 v32, v48, v32
	v_sub_f32_e32 v42, v33, v45
	v_mul_f32_e32 v32, v43, v32
	v_sub_f32_e32 v42, v46, v42
	v_add_f32_e32 v32, v42, v32
	v_mul_f32_e32 v45, 0x3f317218, v31
	v_add_f32_e32 v42, v33, v32
	v_fma_f32 v46, v31, s21, -v45
	v_mul_f32_e32 v43, v42, v42
	v_fmac_f32_e32 v46, 0xb102e308, v31
	v_sub_f32_e32 v31, v42, v33
	v_fmamk_f32 v44, v43, 0x3e9b6dac, v217
	v_sub_f32_e32 v31, v32, v31
	v_add_f32_e32 v32, v45, v46
	v_fmaak_f32 v44, v43, v44, 0x3f2aaada
	v_sub_f32_e32 v33, v32, v45
	v_ldexp_f32 v45, v42, 1
	v_mul_f32_e32 v42, v42, v43
	v_mul_f32_e32 v42, v42, v44
	v_add_f32_e32 v43, v45, v42
	v_sub_f32_e32 v44, v43, v45
	v_ldexp_f32 v31, v31, 1
	v_sub_f32_e32 v42, v42, v44
	v_add_f32_e32 v31, v31, v42
	v_add_f32_e32 v42, v43, v31
	v_sub_f32_e32 v43, v42, v43
	v_sub_f32_e32 v31, v31, v43
	v_add_f32_e32 v43, v32, v42
	v_sub_f32_e32 v44, v43, v32
	v_sub_f32_e32 v45, v43, v44
	v_sub_f32_e32 v33, v46, v33
	v_sub_f32_e32 v32, v32, v45
	v_sub_f32_e32 v42, v42, v44
	v_add_f32_e32 v32, v42, v32
	v_add_f32_e32 v42, v33, v31
	v_sub_f32_e32 v44, v42, v33
	v_sub_f32_e32 v45, v42, v44
	v_sub_f32_e32 v33, v33, v45
	v_sub_f32_e32 v31, v31, v44
	v_add_f32_e32 v32, v42, v32
	v_add_f32_e32 v31, v31, v33
	v_add_f32_e32 v33, v43, v32
	v_sub_f32_e32 v42, v33, v43
	v_sub_f32_e32 v32, v32, v42
	v_add_f32_e32 v31, v31, v32
	v_add_f32_e32 v31, v33, v31
	v_cndmask_b32_e32 v31, v230, v31, vcc
	v_cmp_ngt_f32_e32 vcc, -1.0, v30
	s_nop 1
	v_cndmask_b32_e32 v31, v231, v31, vcc
	v_cmp_neq_f32_e32 vcc, -1.0, v30
	s_nop 1
	v_cndmask_b32_e32 v31, v226, v31, vcc
	v_cmp_lt_f32_e64 vcc, |v30|, s33
	s_nop 1
	v_cndmask_b32_e32 v30, v31, v30, vcc
	v_sub_f32_e32 v98, v29, v30
	v_mul_f32_e32 v99, v99, v27
	v_add_f32_e32 v30, v99, v15
	v_min_f32_e32 v29, 0, v30
	v_mul_f32_e64 v30, |v30|, s3
	v_exp_f32_e32 v30, v30
	s_nop 0
	v_add_f32_e32 v32, 1.0, v30
	v_add_f32_e32 v31, -1.0, v32
	v_sub_f32_e32 v33, v31, v32
	v_add_f32_e32 v33, 1.0, v33
;     __device__ __forceinline__ void operator()(const f32x4 (&acc)[2][2][4][2], const Unit& u, int ui, int wr, int wc, int fr, int fq) const {
;     ...
;                             for (int e = 0; e < 6; ++e) { const float zz = z[e] + bfg[e]; z[e] = fminf(zz, 0.f) - log1pf(__expf(-fabsf(zz))); }
;                             float* lp = (float*)(ws + E_LS) + (size_t)row;
; #pragma unroll
;                             for (int e = 0; e < 6; ++e) lp[(size_t)(e * 32768u)] = z[e];
	v_sub_f32_e32 v31, v30, v31
	v_add_f32_e32 v33, v31, v33
	v_frexp_mant_f32_e32 v31, v32
	v_cvt_f64_f32_e32 v[42:43], v32
	v_cmp_gt_f32_e32 vcc, s19, v31
	v_frexp_exp_i32_f64_e32 v31, v[42:43]
	s_nop 0
	v_subbrev_co_u32_e32 v31, vcc, 0, v31, vcc
	v_sub_u32_e32 v42, 0, v31
	v_ldexp_f32 v32, v32, v42
	v_ldexp_f32 v33, v33, v42
	v_add_f32_e32 v42, -1.0, v32
	v_add_f32_e32 v43, 1.0, v42
	v_sub_f32_e32 v43, v32, v43
	v_add_f32_e32 v43, v33, v43
	v_add_f32_e32 v44, v42, v43
	v_sub_f32_e32 v42, v44, v42
	v_sub_f32_e32 v42, v43, v42
	v_add_f32_e32 v43, 1.0, v32
	v_add_f32_e32 v45, -1.0, v43
	v_sub_f32_e32 v32, v32, v45
	v_add_f32_e32 v32, v33, v32
	v_add_f32_e32 v33, v43, v32
	v_sub_f32_e32 v43, v33, v43
	v_sub_f32_e32 v32, v32, v43
	v_rcp_f32_e32 v43, v33
	v_cvt_f32_i32_e32 v31, v31
	v_cmp_neq_f32_e32 vcc, s27, v30
	v_mul_f32_e32 v45, v44, v43
	v_mul_f32_e32 v46, v33, v45
	v_fma_f32 v47, v45, v33, -v46
	v_fmac_f32_e32 v47, v45, v32
	v_add_f32_e32 v48, v46, v47
	v_sub_f32_e32 v49, v44, v48
	v_sub_f32_e32 v44, v44, v49
	v_sub_f32_e32 v46, v48, v46
	v_sub_f32_e32 v44, v44, v48
	v_add_f32_e32 v42, v42, v44
	v_sub_f32_e32 v44, v46, v47
	v_add_f32_e32 v42, v44, v42
	v_add_f32_e32 v44, v49, v42
	v_mul_f32_e32 v46, v43, v44
	v_mul_f32_e32 v47, v33, v46
	v_fma_f32 v33, v46, v33, -v47
	v_fmac_f32_e32 v33, v46, v32
	v_sub_f32_e32 v32, v49, v44
	v_add_f32_e32 v32, v42, v32
	v_add_f32_e32 v42, v47, v33
	v_sub_f32_e32 v48, v44, v42
	v_sub_f32_e32 v44, v44, v48
	v_sub_f32_e32 v47, v42, v47
	v_sub_f32_e32 v42, v44, v42
	v_add_f32_e32 v32, v32, v42
	v_sub_f32_e32 v33, v47, v33
	v_add_f32_e32 v32, v33, v32
	v_add_f32_e32 v33, v45, v46
	v_add_f32_e32 v32, v48, v32
	v_sub_f32_e32 v42, v33, v45
	v_mul_f32_e32 v32, v43, v32
	v_sub_f32_e32 v42, v46, v42
	v_add_f32_e32 v32, v42, v32
	v_mul_f32_e32 v45, 0x3f317218, v31
	v_add_f32_e32 v42, v33, v32
	v_fma_f32 v46, v31, s21, -v45
	v_mul_f32_e32 v43, v42, v42
	v_fmac_f32_e32 v46, 0xb102e308, v31
	v_sub_f32_e32 v31, v42, v33
	v_fmamk_f32 v44, v43, 0x3e9b6dac, v217
	v_sub_f32_e32 v31, v32, v31
	v_add_f32_e32 v32, v45, v46
	v_fmaak_f32 v44, v43, v44, 0x3f2aaada
	v_sub_f32_e32 v33, v32, v45
	v_ldexp_f32 v45, v42, 1
	v_mul_f32_e32 v42, v42, v43
	v_mul_f32_e32 v42, v42, v44
	v_add_f32_e32 v43, v45, v42
	v_sub_f32_e32 v44, v43, v45
	v_ldexp_f32 v31, v31, 1
	v_sub_f32_e32 v42, v42, v44
	v_add_f32_e32 v31, v31, v42
	v_add_f32_e32 v42, v43, v31
	v_sub_f32_e32 v43, v42, v43
	v_sub_f32_e32 v31, v31, v43
	v_add_f32_e32 v43, v32, v42
	v_sub_f32_e32 v44, v43, v32
	v_sub_f32_e32 v45, v43, v44
	v_sub_f32_e32 v33, v46, v33
	v_sub_f32_e32 v32, v32, v45
	v_sub_f32_e32 v42, v42, v44
	v_add_f32_e32 v32, v42, v32
	v_add_f32_e32 v42, v33, v31
	v_sub_f32_e32 v44, v42, v33
	v_sub_f32_e32 v45, v42, v44
	v_sub_f32_e32 v33, v33, v45
	v_sub_f32_e32 v31, v31, v44
	v_add_f32_e32 v32, v42, v32
	v_add_f32_e32 v31, v31, v33
	v_add_f32_e32 v33, v43, v32
	v_sub_f32_e32 v42, v33, v43
	v_sub_f32_e32 v32, v32, v42
	v_add_f32_e32 v31, v31, v32
	v_add_f32_e32 v31, v33, v31
	v_cndmask_b32_e32 v31, v230, v31, vcc
	v_cmp_ngt_f32_e32 vcc, -1.0, v30
	s_nop 1
	v_cndmask_b32_e32 v31, v231, v31, vcc
	v_cmp_neq_f32_e32 vcc, -1.0, v30
	s_nop 1
	v_cndmask_b32_e32 v31, v226, v31, vcc
	v_cmp_lt_f32_e64 vcc, |v30|, s33
	s_nop 1
	v_cndmask_b32_e32 v30, v31, v30, vcc
	v_sub_f32_e32 v99, v29, v30
	s_mov_b64 s[30:31], s[12:13]
	global_store_dword v28, v118, s[30:31]
	global_store_dword v28, v102, s[30:31] offset:64
	s_add_u32 s30, s30, 0x20000
	s_addc_u32 s31, s31, 0
	global_store_dword v28, v119, s[30:31]
	global_store_dword v28, v103, s[30:31] offset:64
	s_add_u32 s30, s30, 0x20000
	s_addc_u32 s31, s31, 0
	global_store_dword v28, v120, s[30:31]
	global_store_dword v28, v104, s[30:31] offset:64
	s_add_u32 s30, s30, 0x20000
	s_addc_u32 s31, s31, 0
	global_store_dword v28, v121, s[30:31]
	global_store_dword v28, v105, s[30:31] offset:64
	s_add_u32 s30, s30, 0x20000
	s_addc_u32 s31, s31, 0
	global_store_dword v28, v114, s[30:31]
	global_store_dword v28, v98, s[30:31] offset:64
	s_add_u32 s30, s30, 0x20000
	s_addc_u32 s31, s31, 0
	global_store_dword v28, v115, s[30:31]
	global_store_dword v28, v99, s[30:31] offset:64

; #define PG8_PACK8(y0, y1) (u32x4){cvt_pk_bf16((y0)[0], (y0)[1]), cvt_pk_bf16((y0)[2], (y0)[3]), cvt_pk_bf16((y1)[0], (y1)[1]), cvt_pk_bf16((y1)[2], (y1)[3])}
;     __device__ __forceinline__ void operator()(const f32x4 (&acc)[2][2][4][2], const Unit& u, int ui, int wr, int wc, int fr, int fq) const {
;     ...
;         } else if (pn < 12) {
;             unsigned char* dst = ws + E_QKVO + (size_t)((unsigned)(u.pm >> 4) * (24u << 20) + (16u << 20) + (unsigned)(((pn & 3) * 256 + wc * 64 + 8 * fq) * 2));
; #pragma unroll
;             for (int ai = 0; ai < 2; ++ai)
; #pragma unroll
;                 for (int m = 0; m < 4; ++m) {
;                     const unsigned row = row0 + ai * HALF + m * 16; const float rs = rsp[ai * HALF + m * 16];
; #pragma unroll
;                     for (int bj = 0; bj < 2; ++bj) { const f32x4 y0 = acc[ai][bj][m][0] * rs, y1 = acc[ai][bj][m][1] * rs;
;                         *(u32x4*)(dst + (size_t)(row * 2048u + 64u * bj)) = PG8_PACK8(y0, y1); }
;                 }
.LBB0_610:
	s_and_b64 vcc, exec, s[28:29]
	s_cbranch_vccz .LBB0_612
	s_lshr_b32 s19, s4, 4
	s_lshl_b32 s21, s26, 9
	ds_read_b32 v136, v160
	s_mul_i32 s19, s19, 0x1800000
	s_and_b32 s21, s21, 0x600
	s_or_b32 s19, s19, s21
	s_add_i32 s19, s19, 0x1000000
	v_or_b32_e32 v0, s19, v175
	v_lshl_add_u64 v[130:131], s[14:15], 0, v[0:1]
	v_lshlrev_b32_e32 v0, 11, v158
	s_waitcnt lgkmcnt(0)
	v_mul_f32_e32 v134, v128, v136
	v_mul_f32_e32 v135, v129, v136
	v_mul_f32_e32 v132, v126, v136
	v_mul_f32_e32 v133, v127, v136
	v_mul_f32_e32 v138, v124, v136
	v_mul_f32_e32 v139, v125, v136
	v_mul_f32_e32 v140, v122, v136
	v_mul_f32_e32 v141, v123, v136
	v_cvt_pk_bf16_f32 v132, v132, v133
	v_cvt_pk_bf16_f32 v133, v134, v135
	s_nop 0
	v_cvt_pk_bf16_f32 v134, v140, v141
	v_cvt_pk_bf16_f32 v135, v138, v139
	v_lshl_add_u64 v[138:139], v[130:131], 0, v[0:1]
	flat_store_dwordx4 v[138:139], v[132:135]
	v_mul_f32_e32 v140, v116, v136
	v_mul_f32_e32 v141, v117, v136
	s_nop 0
	v_mul_f32_e32 v134, v120, v136
	v_mul_f32_e32 v135, v121, v136
	v_mul_f32_e32 v132, v118, v136
	v_mul_f32_e32 v133, v119, v136
	v_mul_f32_e32 v137, v115, v136
	v_mul_f32_e32 v136, v114, v136
	v_cvt_pk_bf16_f32 v132, v132, v133
	v_cvt_pk_bf16_f32 v133, v134, v135
	s_nop 0
	v_cvt_pk_bf16_f32 v134, v136, v137
	v_cvt_pk_bf16_f32 v135, v140, v141
	flat_store_dwordx4 v[138:139], v[132:135] offset:64
	ds_read_b32 v136, v160 offset:64
	v_or_b32_e32 v138, 0x8000, v0
	v_mov_b32_e32 v139, v1
	v_lshl_add_u64 v[138:139], v[130:131], 0, v[138:139]
	s_waitcnt lgkmcnt(0)
	v_mul_f32_e32 v134, v112, v136
	v_mul_f32_e32 v135, v113, v136
	v_mul_f32_e32 v132, v110, v136
	v_mul_f32_e32 v133, v111, v136
	v_mul_f32_e32 v140, v108, v136
	v_mul_f32_e32 v141, v109, v136
	v_mul_f32_e32 v142, v106, v136
	v_mul_f32_e32 v143, v107, v136
	v_cvt_pk_bf16_f32 v132, v132, v133
	v_cvt_pk_bf16_f32 v133, v134, v135
	s_nop 0
	v_cvt_pk_bf16_f32 v134, v142, v143
	v_cvt_pk_bf16_f32 v135, v140, v141
	flat_store_dwordx4 v[138:139], v[132:135]
	v_mul_f32_e32 v138, v100, v136
	v_mul_f32_e32 v139, v101, v136
	s_nop 0
	v_mul_f32_e32 v134, v104, v136
	v_mul_f32_e32 v135, v105, v136
	v_mul_f32_e32 v132, v102, v136
	v_mul_f32_e32 v133, v103, v136
	v_mul_f32_e32 v137, v99, v136
	v_mul_f32_e32 v136, v98, v136
	v_cvt_pk_bf16_f32 v132, v132, v133
	v_cvt_pk_bf16_f32 v133, v134, v135
	s_nop 0
	v_cvt_pk_bf16_f32 v134, v136, v137
	v_or_b32_e32 v136, 0x8040, v0
	v_mov_b32_e32 v137, v1
	v_lshl_add_u64 v[136:137], v[130:131], 0, v[136:137]
	v_cvt_pk_bf16_f32 v135, v138, v139
	flat_store_dwordx4 v[136:137], v[132:135]
	ds_read_b32 v136, v160 offset:128
	v_or_b32_e32 v138, 0x10000, v0
	v_mov_b32_e32 v139, v1
	v_lshl_add_u64 v[138:139], v[130:131], 0, v[138:139]
	s_waitcnt lgkmcnt(0)
	v_mul_f32_e32 v134, v96, v136
	v_mul_f32_e32 v135, v97, v136
	v_mul_f32_e32 v132, v94, v136
	v_mul_f32_e32 v133, v95, v136
	v_mul_f32_e32 v140, v92, v136
	v_mul_f32_e32 v141, v93, v136
	v_mul_f32_e32 v142, v90, v136
	v_mul_f32_e32 v143, v91, v136
	v_cvt_pk_bf16_f32 v132, v132, v133
	v_cvt_pk_bf16_f32 v133, v134, v135
	s_nop 0
	v_cvt_pk_bf16_f32 v134, v142, v143
	v_cvt_pk_bf16_f32 v135, v140, v141
	flat_store_dwordx4 v[138:139], v[132:135]
	v_mul_f32_e32 v138, v84, v136
	v_mul_f32_e32 v139, v85, v136
	s_nop 0
	v_mul_f32_e32 v134, v88, v136
	v_mul_f32_e32 v135, v89, v136
	v_mul_f32_e32 v132, v86, v136
	v_mul_f32_e32 v133, v87, v136
	v_mul_f32_e32 v137, v83, v136
	v_mul_f32_e32 v136, v82, v136
	v_cvt_pk_bf16_f32 v132, v132, v133
	v_cvt_pk_bf16_f32 v133, v134, v135
	s_nop 0
	v_cvt_pk_bf16_f32 v134, v136, v137
	v_or_b32_e32 v136, 0x10040, v0
	v_mov_b32_e32 v137, v1
	v_lshl_add_u64 v[136:137], v[130:131], 0, v[136:137]
	v_cvt_pk_bf16_f32 v135, v138, v139
	flat_store_dwordx4 v[136:137], v[132:135]
	ds_read_b32 v136, v160 offset:192
	v_or_b32_e32 v138, 0x18000, v0
	v_mov_b32_e32 v139, v1
	v_lshl_add_u64 v[138:139], v[130:131], 0, v[138:139]
	s_waitcnt lgkmcnt(0)
	v_mul_f32_e32 v134, v80, v136
	v_mul_f32_e32 v135, v81, v136
	v_mul_f32_e32 v132, v78, v136
	v_mul_f32_e32 v133, v79, v136
	v_mul_f32_e32 v140, v76, v136
	v_mul_f32_e32 v141, v77, v136
	v_mul_f32_e32 v142, v74, v136
	v_mul_f32_e32 v143, v75, v136
	v_cvt_pk_bf16_f32 v132, v132, v133
	v_cvt_pk_bf16_f32 v133, v134, v135
	s_nop 0
	v_cvt_pk_bf16_f32 v134, v142, v143
	v_cvt_pk_bf16_f32 v135, v140, v141
	flat_store_dwordx4 v[138:139], v[132:135]
	v_mul_f32_e32 v138, v68, v136
	v_mul_f32_e32 v139, v69, v136
	s_nop 0
	v_mul_f32_e32 v134, v72, v136
	v_mul_f32_e32 v135, v73, v136
	v_mul_f32_e32 v132, v70, v136
	v_mul_f32_e32 v133, v71, v136
	v_mul_f32_e32 v137, v67, v136
	v_mul_f32_e32 v136, v66, v136
	v_cvt_pk_bf16_f32 v132, v132, v133
	v_cvt_pk_bf16_f32 v133, v134, v135
	s_nop 0
	v_cvt_pk_bf16_f32 v134, v136, v137
	v_or_b32_e32 v136, 0x18040, v0
	v_mov_b32_e32 v137, v1
	v_lshl_add_u64 v[136:137], v[130:131], 0, v[136:137]
	v_cvt_pk_bf16_f32 v135, v138, v139
	flat_store_dwordx4 v[136:137], v[132:135]
	ds_read_b32 v136, v160 offset:512
	v_add_u32_e32 v138, 0x40000, v0
	v_mov_b32_e32 v139, v1
	v_lshl_add_u64 v[138:139], v[130:131], 0, v[138:139]
	s_waitcnt lgkmcnt(0)
; #define PG8_PACK8(y0, y1) (u32x4){cvt_pk_bf16((y0)[0], (y0)[1]), cvt_pk_bf16((y0)[2], (y0)[3]), cvt_pk_bf16((y1)[0], (y1)[1]), cvt_pk_bf16((y1)[2], (y1)[3])}
;     __device__ __forceinline__ void operator()(const f32x4 (&acc)[2][2][4][2], const Unit& u, int ui, int wr, int wc, int fr, int fq) const {
;     ...
;         } else if (pn < 12) {
;             unsigned char* dst = ws + E_QKVO + (size_t)((unsigned)(u.pm >> 4) * (24u << 20) + (16u << 20) + (unsigned)(((pn & 3) * 256 + wc * 64 + 8 * fq) * 2));
; #pragma unroll
;             for (int ai = 0; ai < 2; ++ai)
; #pragma unroll
;                 for (int m = 0; m < 4; ++m) {
;                     const unsigned row = row0 + ai * HALF + m * 16; const float rs = rsp[ai * HALF + m * 16];
; #pragma unroll
;                     for (int bj = 0; bj < 2; ++bj) { const f32x4 y0 = acc[ai][bj][m][0] * rs, y1 = acc[ai][bj][m][1] * rs;
;                         *(u32x4*)(dst + (size_t)(row * 2048u + 64u * bj)) = PG8_PACK8(y0, y1); }
;                 }
	v_mul_f32_e32 v134, v64, v136
	v_mul_f32_e32 v135, v65, v136
	v_mul_f32_e32 v132, v62, v136
	v_mul_f32_e32 v133, v63, v136
	v_mul_f32_e32 v140, v60, v136
	v_mul_f32_e32 v141, v61, v136
	v_mul_f32_e32 v142, v58, v136
	v_mul_f32_e32 v143, v59, v136
	v_cvt_pk_bf16_f32 v132, v132, v133
	v_cvt_pk_bf16_f32 v133, v134, v135
	s_nop 0
	v_cvt_pk_bf16_f32 v134, v142, v143
	v_cvt_pk_bf16_f32 v135, v140, v141
	flat_store_dwordx4 v[138:139], v[132:135]
	v_mul_f32_e32 v140, v52, v136
	v_mul_f32_e32 v141, v53, v136
	s_nop 0
	v_mul_f32_e32 v134, v56, v136
	v_mul_f32_e32 v135, v57, v136
	v_mul_f32_e32 v132, v54, v136
	v_mul_f32_e32 v133, v55, v136
	v_mul_f32_e32 v137, v51, v136
	v_mul_f32_e32 v136, v50, v136
	v_cvt_pk_bf16_f32 v132, v132, v133
	v_cvt_pk_bf16_f32 v133, v134, v135
	s_nop 0
	v_cvt_pk_bf16_f32 v134, v136, v137
	v_cvt_pk_bf16_f32 v135, v140, v141
	flat_store_dwordx4 v[138:139], v[132:135] offset:64
	ds_read_b32 v136, v160 offset:576
	v_add_u32_e32 v138, 0x48000, v0
	v_mov_b32_e32 v139, v1
	v_lshl_add_u64 v[138:139], v[130:131], 0, v[138:139]
	s_waitcnt lgkmcnt(0)
	v_mul_f32_e32 v134, v48, v136
	v_mul_f32_e32 v135, v49, v136
	v_mul_f32_e32 v132, v46, v136
	v_mul_f32_e32 v133, v47, v136
	v_mul_f32_e32 v140, v44, v136
	v_mul_f32_e32 v141, v45, v136
	v_mul_f32_e32 v142, v42, v136
	v_mul_f32_e32 v143, v43, v136
	v_cvt_pk_bf16_f32 v132, v132, v133
	v_cvt_pk_bf16_f32 v133, v134, v135
	s_nop 0
	v_cvt_pk_bf16_f32 v134, v142, v143
	v_cvt_pk_bf16_f32 v135, v140, v141
	flat_store_dwordx4 v[138:139], v[132:135]
	v_mul_f32_e32 v138, v36, v136
	v_mul_f32_e32 v139, v37, v136
	s_nop 0
	v_mul_f32_e32 v134, v40, v136
	v_mul_f32_e32 v135, v41, v136
	v_mul_f32_e32 v132, v38, v136
	v_mul_f32_e32 v133, v39, v136
	v_mul_f32_e32 v137, v35, v136
	v_mul_f32_e32 v136, v34, v136
	v_cvt_pk_bf16_f32 v132, v132, v133
	v_cvt_pk_bf16_f32 v133, v134, v135
	s_nop 0
	v_cvt_pk_bf16_f32 v134, v136, v137
	v_add_u32_e32 v136, 0x48040, v0
	v_mov_b32_e32 v137, v1
	v_lshl_add_u64 v[136:137], v[130:131], 0, v[136:137]
	v_cvt_pk_bf16_f32 v135, v138, v139
	flat_store_dwordx4 v[136:137], v[132:135]
	ds_read_b32 v136, v160 offset:640
	v_add_u32_e32 v138, 0x50000, v0
	v_mov_b32_e32 v139, v1
	v_lshl_add_u64 v[138:139], v[130:131], 0, v[138:139]
	s_waitcnt lgkmcnt(0)
	v_mul_f32_e32 v134, v32, v136
	v_mul_f32_e32 v135, v33, v136
	v_mul_f32_e32 v132, v30, v136
	v_mul_f32_e32 v133, v31, v136
	v_mul_f32_e32 v140, v28, v136
	v_mul_f32_e32 v141, v29, v136
	v_mul_f32_e32 v142, v26, v136
	v_mul_f32_e32 v143, v27, v136
	v_cvt_pk_bf16_f32 v132, v132, v133
	v_cvt_pk_bf16_f32 v133, v134, v135
	s_nop 0
	v_cvt_pk_bf16_f32 v134, v142, v143
	v_cvt_pk_bf16_f32 v135, v140, v141
	flat_store_dwordx4 v[138:139], v[132:135]
	v_mul_f32_e32 v138, v20, v136
	v_mul_f32_e32 v139, v21, v136
	s_nop 0
	v_mul_f32_e32 v134, v24, v136
	v_mul_f32_e32 v135, v25, v136
	v_mul_f32_e32 v132, v22, v136
	v_mul_f32_e32 v133, v23, v136
	v_mul_f32_e32 v137, v19, v136
	v_mul_f32_e32 v136, v18, v136
	v_cvt_pk_bf16_f32 v132, v132, v133
	v_cvt_pk_bf16_f32 v133, v134, v135
	s_nop 0
	v_cvt_pk_bf16_f32 v134, v136, v137
	v_add_u32_e32 v136, 0x50040, v0
	v_mov_b32_e32 v137, v1
	v_lshl_add_u64 v[136:137], v[130:131], 0, v[136:137]
	v_cvt_pk_bf16_f32 v135, v138, v139
	flat_store_dwordx4 v[136:137], v[132:135]
	ds_read_b32 v136, v160 offset:704
	v_add_u32_e32 v138, 0x58000, v0
	v_mov_b32_e32 v139, v1
	v_lshl_add_u64 v[138:139], v[130:131], 0, v[138:139]
	v_add_u32_e32 v0, 0x58040, v0
	s_waitcnt lgkmcnt(0)
	v_mul_f32_e32 v134, v16, v136
	v_mul_f32_e32 v135, v17, v136
	v_mul_f32_e32 v132, v14, v136
	v_mul_f32_e32 v133, v15, v136
	v_mul_f32_e32 v140, v12, v136
	v_mul_f32_e32 v141, v13, v136
	v_mul_f32_e32 v142, v10, v136
	v_mul_f32_e32 v143, v11, v136
	v_cvt_pk_bf16_f32 v132, v132, v133
	v_cvt_pk_bf16_f32 v133, v134, v135
	v_lshl_add_u64 v[130:131], v[130:131], 0, v[0:1]
	v_cvt_pk_bf16_f32 v134, v142, v143
	v_cvt_pk_bf16_f32 v135, v140, v141
	flat_store_dwordx4 v[138:139], v[132:135]
	v_mul_f32_e32 v138, v4, v136
	v_mul_f32_e32 v139, v5, v136
	s_nop 0
	v_mul_f32_e32 v134, v8, v136
	v_mul_f32_e32 v135, v9, v136
	v_mul_f32_e32 v132, v6, v136
	v_mul_f32_e32 v133, v7, v136
	v_mul_f32_e32 v137, v3, v136
	v_mul_f32_e32 v136, v2, v136
	v_cvt_pk_bf16_f32 v132, v132, v133
	v_cvt_pk_bf16_f32 v133, v134, v135
	s_nop 0
	v_cvt_pk_bf16_f32 v134, v136, v137
	v_cvt_pk_bf16_f32 v135, v138, v139
	flat_store_dwordx4 v[130:131], v[132:135]

; #define PG8_LAS __attribute__((address_space(3)))
;     __device__ __forceinline__ void operator()(const f32x4 (&acc)[2][2][4][2], const Unit& u, int ui, int wr, int wc, int fr, int fq) const {
;     ...
;             const PG8_LAS float* gp = tab + TAB_G + ui * 256 + 64 * wc + 8 * fq;
;             f32x4 g[2][2];
; #pragma unroll
;             for (int bj = 0; bj < 2; ++bj)
; #pragma unroll
;                 for (int n = 0; n < 2; ++n) g[bj][n] = *(const PG8_LAS f32x4*)(gp + 32 * bj + 4 * n);
;             unsigned char* dst = ws + E_QKVO + (size_t)((unsigned)(u.pm >> 4) * (24u << 20) + (pn < 4 ? 0u : (8u << 20)) + (unsigned)(((pn & 3) * 256 + wc * 64 + 8 * fq) * 2));
;             float ss[2][4], e2[2][4];
; #pragma unroll
;             for (int ai = 0; ai < 2; ++ai)
; #pragma unroll
;                 for (int m = 0; m < 4; ++m) {
;                     const float rs = rsp[ai * HALF + m * 16]; e2[ai][m] = RMS_EPS * __builtin_amdgcn_rcpf(rs * rs);
;                     f32x4 s4 = acc[ai][0][m][0] * acc[ai][0][m][0]; s4 += acc[ai][0][m][1] * acc[ai][0][m][1]; s4 += acc[ai][1][m][0] * acc[ai][1][m][0]; s4 += acc[ai][1][m][1] * acc[ai][1][m][1];
;                     ss[ai][m] = (s4[0] + s4[1]) + (s4[2] + s4[3]);
;                 }
.LBB0_613:
	s_andn2_b64 vcc, exec, s[28:29]
	s_cbranch_vccnz .LBB0_620
	v_lshl_add_u32 v0, s5, 10, v187
	ds_read_b128 v[142:145], v0
	ds_read_b128 v[138:141], v0 offset:16
	ds_read_b128 v[134:137], v0 offset:128
	ds_read_b128 v[130:133], v0 offset:144
	ds_read2_b32 v[168:169], v160 offset1:16
	v_mul_f32_e32 v172, v124, v124
	v_mul_f32_e32 v173, v125, v125
	v_mul_f32_e32 v176, v122, v122
	v_mul_f32_e32 v177, v123, v123
	v_fma_f32 v172, v128, v128, v172
	v_fma_f32 v173, v129, v129, v173
	v_fma_f32 v176, v126, v126, v176
	v_fma_f32 v177, v127, v127, v177
	v_fma_f32 v172, v120, v120, v172
	v_fma_f32 v173, v121, v121, v173
	v_fma_f32 v176, v118, v118, v176
	v_fma_f32 v177, v119, v119, v177
	v_fma_f32 v172, v116, v116, v172
	v_fma_f32 v173, v117, v117, v173
	v_fma_f32 v176, v114, v114, v176
	v_fma_f32 v177, v115, v115, v177
	s_waitcnt lgkmcnt(0)
	v_mul_f32_e32 v159, v168, v168
	v_pk_mov_b32 v[178:179], v[176:177], v[172:173] op_sel:[1,0]
	v_mov_b32_e32 v177, v173
	v_add_f32_e32 v172, v178, v176
	v_add_f32_e32 v173, v179, v177
	v_rcp_f32_e32 v168, v159
	v_add_f32_e32 v159, v172, v173
	v_mul_f32_e32 v172, v108, v108
	v_mul_f32_e32 v173, v109, v109
	v_mul_f32_e32 v176, v106, v106
	v_mul_f32_e32 v177, v107, v107
	v_fma_f32 v172, v112, v112, v172
	v_fma_f32 v173, v113, v113, v173
	v_fma_f32 v176, v110, v110, v176
	v_fma_f32 v177, v111, v111, v177
	v_fma_f32 v172, v104, v104, v172
	v_fma_f32 v173, v105, v105, v173
	v_fma_f32 v176, v102, v102, v176
	v_fma_f32 v177, v103, v103, v177
	ds_read2_b32 v[178:179], v160 offset0:32 offset1:48
	v_mul_f32_e32 v161, v169, v169
	v_fma_f32 v172, v100, v100, v172
	v_fma_f32 v173, v101, v101, v173
	v_fma_f32 v176, v98, v98, v176
	v_fma_f32 v177, v99, v99, v177
	v_rcp_f32_e32 v162, v161
	v_add_f32_e32 v161, v176, v177
	v_add_f32_e32 v164, v172, v173
	v_mul_f32_e32 v172, v92, v92
	v_mul_f32_e32 v173, v93, v93
	v_mul_f32_e32 v176, v90, v90
	v_mul_f32_e32 v177, v91, v91
	v_fma_f32 v172, v96, v96, v172
	v_fma_f32 v173, v97, v97, v173
	v_fma_f32 v176, v94, v94, v176
	v_fma_f32 v177, v95, v95, v177
	v_fma_f32 v172, v88, v88, v172
	v_fma_f32 v173, v89, v89, v173
	v_fma_f32 v176, v86, v86, v176
	v_fma_f32 v177, v87, v87, v177
	v_add_f32_e32 v164, v161, v164
	s_waitcnt lgkmcnt(0)
	v_mul_f32_e32 v161, v178, v178
	v_fma_f32 v172, v84, v84, v172
	v_fma_f32 v173, v85, v85, v173
	v_fma_f32 v176, v82, v82, v176
	v_fma_f32 v177, v83, v83, v177
	v_rcp_f32_e32 v166, v161
	v_add_f32_e32 v161, v176, v177
	v_add_f32_e32 v169, v172, v173
	v_mul_f32_e32 v172, v76, v76
	v_mul_f32_e32 v173, v77, v77
	v_mul_f32_e32 v176, v74, v74
	v_mul_f32_e32 v177, v75, v75
	v_fma_f32 v172, v80, v80, v172
	v_fma_f32 v173, v81, v81, v173
	v_fma_f32 v176, v78, v78, v176
	v_fma_f32 v177, v79, v79, v177
	v_add_f32_e32 v170, v161, v169
	v_mul_f32_e32 v161, v179, v179
	v_fma_f32 v172, v72, v72, v172
	v_fma_f32 v173, v73, v73, v173
	v_fma_f32 v176, v70, v70, v176
	v_fma_f32 v177, v71, v71, v177
	ds_read2_b32 v[178:179], v160 offset0:128 offset1:144
	v_fma_f32 v172, v68, v68, v172
	v_fma_f32 v173, v69, v69, v173
	v_fma_f32 v176, v66, v66, v176
	v_fma_f32 v177, v67, v67, v177
	v_rcp_f32_e32 v174, v161
	v_add_f32_e32 v161, v176, v177
	v_add_f32_e32 v169, v172, v173
	v_mul_f32_e32 v172, v60, v60
	v_mul_f32_e32 v173, v61, v61
	v_mul_f32_e32 v176, v58, v58
	v_mul_f32_e32 v177, v59, v59
	v_fma_f32 v172, v64, v64, v172
	v_fma_f32 v173, v65, v65, v173
	v_fma_f32 v176, v62, v62, v176
	v_fma_f32 v177, v63, v63, v177
	v_fma_f32 v172, v56, v56, v172
	v_fma_f32 v173, v57, v57, v173
	v_fma_f32 v176, v54, v54, v176
	v_fma_f32 v177, v55, v55, v177
	v_add_f32_e32 v180, v161, v169
	s_waitcnt lgkmcnt(0)
	v_mul_f32_e32 v161, v178, v178
	v_fma_f32 v172, v52, v52, v172
	v_fma_f32 v173, v53, v53, v173
	v_fma_f32 v176, v50, v50, v176
	v_fma_f32 v177, v51, v51, v177
	v_rcp_f32_e32 v178, v161
	v_add_f32_e32 v161, v176, v177
	v_add_f32_e32 v169, v172, v173
	v_mul_f32_e32 v172, v44, v44
	v_mul_f32_e32 v173, v45, v45
	v_mul_f32_e32 v176, v42, v42
	v_mul_f32_e32 v177, v43, v43
	v_fma_f32 v172, v48, v48, v172
	v_fma_f32 v173, v49, v49, v173
	v_fma_f32 v176, v46, v46, v176
	v_fma_f32 v177, v47, v47, v177
	v_add_f32_e32 v182, v161, v169
	v_mul_f32_e32 v161, v179, v179
	v_fma_f32 v172, v40, v40, v172
	v_fma_f32 v173, v41, v41, v173
	v_fma_f32 v176, v38, v38, v176
	v_fma_f32 v177, v39, v39, v177
	v_rcp_f32_e32 v179, v161
	v_fma_f32 v172, v36, v36, v172
	v_fma_f32 v173, v37, v37, v173
	ds_read2_b32 v[160:161], v160 offset0:160 offset1:176
	v_fma_f32 v176, v34, v34, v176
	v_fma_f32 v177, v35, v35, v177
	v_add_f32_e32 v172, v172, v173
	v_add_f32_e32 v169, v176, v177
	v_add_f32_e32 v183, v169, v172
	v_mul_f32_e32 v172, v28, v28
	v_mul_f32_e32 v173, v29, v29
	v_mul_f32_e32 v176, v26, v26
	v_mul_f32_e32 v177, v27, v27
	v_fma_f32 v172, v32, v32, v172
	v_fma_f32 v173, v33, v33, v173
	v_fma_f32 v176, v30, v30, v176
	v_fma_f32 v177, v31, v31, v177
	v_fma_f32 v172, v24, v24, v172
	v_fma_f32 v173, v25, v25, v173
	v_fma_f32 v176, v22, v22, v176
	v_fma_f32 v177, v23, v23, v177
	s_waitcnt lgkmcnt(0)
	v_mul_f32_e32 v160, v160, v160
	v_fma_f32 v172, v20, v20, v172
	v_fma_f32 v173, v21, v21, v173
	v_fma_f32 v176, v18, v18, v176
	v_fma_f32 v177, v19, v19, v177
	v_rcp_f32_e32 v184, v160
	v_add_f32_e32 v160, v176, v177
	v_add_f32_e32 v169, v172, v173
	v_add_f32_e32 v176, v160, v169
	v_mul_f32_e32 v160, v161, v161
	v_rcp_f32_e32 v177, v160
	v_mul_f32_e32 v160, v12, v12
	v_mul_f32_e32 v161, v13, v13
	v_mul_f32_e32 v172, v10, v10
	v_mul_f32_e32 v173, v11, v11
	v_fma_f32 v160, v16, v16, v160
	v_fma_f32 v161, v17, v17, v161
	v_fma_f32 v172, v14, v14, v172
	v_fma_f32 v173, v15, v15, v173
	v_fma_f32 v160, v8, v8, v160
	v_fma_f32 v161, v9, v9, v161
	v_fma_f32 v172, v6, v6, v172
	v_fma_f32 v173, v7, v7, v173
	v_fma_f32 v160, v4, v4, v160
	v_fma_f32 v161, v5, v5, v161
	v_fma_f32 v172, v2, v2, v172
	v_fma_f32 v173, v3, v3, v173
	v_add_f32_e32 v160, v160, v161
	v_add_f32_e32 v169, v172, v173
	v_add_f32_e32 v172, v169, v160
	ds_swizzle_b32 v160, v159 offset:swizzle(SWAP,16)
	ds_swizzle_b32 v161, v164 offset:swizzle(SWAP,16)
	s_mov_b32 s28, 0x358637bd
	s_mov_b32 s29, 0x3c800000
	ds_swizzle_b32 v173, v170 offset:swizzle(SWAP,16)
	s_waitcnt lgkmcnt(0)
; #define PG8_PACK8(y0, y1) (u32x4){cvt_pk_bf16((y0)[0], (y0)[1]), cvt_pk_bf16((y0)[2], (y0)[3]), cvt_pk_bf16((y1)[0], (y1)[1]), cvt_pk_bf16((y1)[2], (y1)[3])}
;     __device__ __forceinline__ void operator()(const f32x4 (&acc)[2][2][4][2], const Unit& u, int ui, int wr, int wc, int fr, int fq) const {
;     ...
;             float sw[2][4];
; #pragma unroll
;             for (int ai = 0; ai < 2; ++ai)
; #pragma unroll
;                 for (int m = 0; m < 4; ++m) sw[ai][m] = __builtin_bit_cast(float, __builtin_amdgcn_ds_swizzle(__builtin_bit_cast(int, ss[ai][m]), 0x401F));
; #pragma unroll
;             for (int ai = 0; ai < 2; ++ai)
; #pragma unroll
;                 for (int m = 0; m < 4; ++m) { float s = ss[ai][m] + sw[ai][m]; s += __shfl_xor(s, 32);
;                     ss[ai][m] = __builtin_amdgcn_rsqf(s * (1.0f / 64.0f) + e2[ai][m]); }
;             if (pn != 4) {
; #pragma unroll
;                 for (int ai = 0; ai < 2; ++ai)
; #pragma unroll
;                     for (int m = 0; m < 4; ++m) {
;                         const unsigned row = row0 + ai * HALF + m * 16; const float r2 = ss[ai][m];
; #pragma unroll
;                         for (int bj = 0; bj < 2; ++bj) {
;                             const f32x4 z0 = acc[ai][bj][m][0] * (g[bj][0] * r2), z1 = acc[ai][bj][m][1] * (g[bj][1] * r2);
;                             *(u32x4*)(dst + (size_t)(row * 2048u + 64u * bj)) = PG8_PACK8(z0, z1);
	v_add_f32_e32 v159, v159, v160
	ds_bpermute_b32 v160, v195, v159
	v_add_f32_e32 v164, v164, v161
	ds_bpermute_b32 v186, v195, v164
	ds_swizzle_b32 v185, v180 offset:swizzle(SWAP,16)
	ds_swizzle_b32 v188, v182 offset:swizzle(SWAP,16)
	s_waitcnt lgkmcnt(0)
	v_add_f32_e32 v169, v159, v160
	v_mul_f32_e32 v160, s28, v168
	v_mul_f32_e32 v161, s29, v169
	ds_swizzle_b32 v189, v183 offset:swizzle(SWAP,16)
	v_add_f32_e32 v159, v160, v161
	v_rsq_f32_e32 v198, v159
	v_add_f32_e32 v159, v164, v186
	v_mul_f32_e32 v159, 0x3c800000, v159
	v_fmac_f32_e32 v159, 0x358637bd, v162
	v_add_f32_e32 v160, v170, v173
	v_rsq_f32_e32 v186, v159
	v_add_f32_e32 v159, v180, v185
	ds_bpermute_b32 v161, v195, v160
	ds_bpermute_b32 v162, v195, v159
	ds_swizzle_b32 v190, v176 offset:swizzle(SWAP,16)
	ds_swizzle_b32 v191, v172 offset:swizzle(SWAP,16)
	s_lshr_b32 s5, s4, 4
	s_waitcnt lgkmcnt(0)
	v_add_f32_e32 v160, v160, v161
	v_add_f32_e32 v159, v159, v162
	v_mul_f32_e32 v160, 0x3c800000, v160
	v_mul_f32_e32 v159, 0x3c800000, v159
	v_fmac_f32_e32 v160, 0x358637bd, v166
	v_fmac_f32_e32 v159, 0x358637bd, v174
	v_rsq_f32_e32 v180, v160
	v_add_f32_e32 v160, v182, v188
	v_rsq_f32_e32 v174, v159
	v_add_f32_e32 v159, v183, v189
	ds_bpermute_b32 v161, v195, v160
	ds_bpermute_b32 v162, v195, v159
	s_cmp_lt_i32 s26, 4
	s_mul_i32 s5, s5, 0x1800000
	s_cselect_b32 s19, 0, 0x800000
	s_waitcnt lgkmcnt(0)
	v_add_f32_e32 v160, v160, v161
	v_add_f32_e32 v159, v159, v162
	v_mul_f32_e32 v160, 0x3c800000, v160
	v_mul_f32_e32 v159, 0x3c800000, v159
	v_fmac_f32_e32 v160, 0x358637bd, v178
	v_fmac_f32_e32 v159, 0x358637bd, v179
	v_rsq_f32_e32 v170, v160
	v_add_f32_e32 v160, v176, v190
	v_rsq_f32_e32 v166, v159
	v_add_f32_e32 v159, v172, v191
	ds_bpermute_b32 v161, v195, v160
	ds_bpermute_b32 v162, v195, v159
	s_add_i32 s5, s5, s19
	s_lshl_b32 s19, s26, 8
	s_and_b32 s19, s19, 0x300
	s_waitcnt lgkmcnt(0)
	v_add_f32_e32 v160, v160, v161
	v_add_f32_e32 v159, v159, v162
	v_mul_f32_e32 v160, 0x3c800000, v160
	v_mul_f32_e32 v159, 0x3c800000, v159
	v_or_b32_e32 v0, s19, v238
	v_fmac_f32_e32 v160, 0x358637bd, v184
	v_fmac_f32_e32 v159, 0x358637bd, v177
	v_lshl_or_b32 v0, v0, 1, s5
	v_rsq_f32_e32 v164, v160
	v_rsq_f32_e32 v162, v159
	v_mov_b32_e32 v199, v198
	v_lshl_add_u64 v[160:161], s[14:15], 0, v[0:1]
	v_lshlrev_b32_e32 v0, 11, v158
	v_mul_f32_e32 v158, v142, v198
	v_mul_f32_e32 v159, v143, v198
	v_mul_f32_e32 v168, v144, v198
	v_mul_f32_e32 v169, v145, v198
	v_mul_f32_e32 v208, v126, v158
	v_mul_f32_e32 v209, v127, v159
	v_mul_f32_e32 v206, v128, v168
	v_mul_f32_e32 v207, v129, v169
	v_mul_f32_e32 v126, v138, v198
	v_mul_f32_e32 v127, v139, v198
	v_mul_f32_e32 v128, v140, v198
	v_mul_f32_e32 v129, v141, v198
	s_cmp_eq_u32 s26, 4
	v_mul_f32_e32 v210, v124, v128
	v_mul_f32_e32 v211, v125, v129
	v_mul_f32_e32 v212, v122, v126
	v_mul_f32_e32 v213, v123, v127
	s_mov_b64 s[26:27], -1
	v_or_b32_e32 v200, 0x8000, v0
	v_or_b32_e32 v196, 0x8040, v0
	v_or_b32_e32 v188, 0x10000, v0
	v_or_b32_e32 v184, 0x10040, v0
	v_or_b32_e32 v182, 0x18000, v0
	v_or_b32_e32 v178, 0x18040, v0
	v_add_u32_e32 v176, 0x40000, v0
	v_add_u32_e32 v172, 0x40040, v0
	v_add_u32_e32 v168, 0x48000, v0
	v_add_u32_e32 v158, 0x48040, v0
	v_add_u32_e32 v128, 0x50000, v0
	v_add_u32_e32 v126, 0x50040, v0
	v_add_u32_e32 v124, 0x58000, v0
	v_mul_f32_e32 v204, v134, v198
	v_mul_f32_e32 v205, v135, v199
	v_mul_f32_e32 v202, v130, v198
	v_mul_f32_e32 v203, v131, v199
	v_add_u32_e32 v122, 0x58040, v0
	s_cbranch_scc1 .LBB0_616
	v_cvt_pk_bf16_f32 v218, v208, v209
	v_cvt_pk_bf16_f32 v219, v206, v207
	v_lshl_add_u64 v[190:191], v[160:161], 0, v[0:1]
	v_mov_b32_e32 v199, v198
	v_cvt_pk_bf16_f32 v220, v212, v213
	v_cvt_pk_bf16_f32 v221, v210, v211
	flat_store_dwordx4 v[190:191], v[218:221]
	v_mul_f32_e32 v222, v132, v198
	v_mul_f32_e32 v223, v133, v199
	v_mul_f32_e32 v228, v114, v202
	v_mul_f32_e32 v229, v115, v203
	v_mul_f32_e32 v218, v136, v198
	v_mul_f32_e32 v219, v137, v199
	v_mul_f32_e32 v222, v116, v222
	v_mul_f32_e32 v223, v117, v223
	v_mul_f32_e32 v220, v120, v218
	v_mul_f32_e32 v221, v121, v219
	v_mul_f32_e32 v218, v118, v204
	v_mul_f32_e32 v219, v119, v205
	v_mov_b32_e32 v201, v1
	v_cvt_pk_bf16_f32 v218, v218, v219
	v_cvt_pk_bf16_f32 v219, v220, v221
	v_cvt_pk_bf16_f32 v220, v228, v229
	v_cvt_pk_bf16_f32 v221, v222, v223
	flat_store_dwordx4 v[190:191], v[218:221] offset:64
	v_mul_f32_e32 v190, v144, v186
	v_mul_f32_e32 v191, v145, v186
	v_mul_f32_e32 v222, v138, v186
	v_mul_f32_e32 v223, v139, v186
	v_mul_f32_e32 v218, v142, v186
	v_mul_f32_e32 v219, v143, v186
	v_mul_f32_e32 v190, v112, v190
	v_mul_f32_e32 v191, v113, v191
	v_mul_f32_e32 v218, v110, v218
	v_mul_f32_e32 v219, v111, v219
	v_mul_f32_e32 v220, v140, v186
	v_mul_f32_e32 v221, v141, v186
	v_cvt_pk_bf16_f32 v218, v218, v219
	v_cvt_pk_bf16_f32 v219, v190, v191
	v_lshl_add_u64 v[190:191], v[160:161], 0, v[200:201]
	v_mul_f32_e32 v228, v108, v220
	v_mul_f32_e32 v229, v109, v221
	v_mul_f32_e32 v220, v106, v222
	v_mul_f32_e32 v221, v107, v223
	v_mul_f32_e32 v222, v130, v186
	v_mul_f32_e32 v223, v131, v186
	v_cvt_pk_bf16_f32 v220, v220, v221
	v_cvt_pk_bf16_f32 v221, v228, v229
	flat_store_dwordx4 v[190:191], v[218:221]
	v_mul_f32_e32 v190, v136, v186
	v_mul_f32_e32 v191, v137, v186
	v_mov_b32_e32 v197, v1
	v_mul_f32_e32 v218, v134, v186
	v_mul_f32_e32 v219, v135, v186
	v_mul_f32_e32 v190, v104, v190
	v_mul_f32_e32 v191, v105, v191
	v_mul_f32_e32 v218, v102, v218
	v_mul_f32_e32 v219, v103, v219
	v_mul_f32_e32 v220, v132, v186
	v_mul_f32_e32 v221, v133, v186
	v_cvt_pk_bf16_f32 v218, v218, v219
	v_cvt_pk_bf16_f32 v219, v190, v191
	v_lshl_add_u64 v[190:191], v[160:161], 0, v[196:197]
; #define PG8_PACK8(y0, y1) (u32x4){cvt_pk_bf16((y0)[0], (y0)[1]), cvt_pk_bf16((y0)[2], (y0)[3]), cvt_pk_bf16((y1)[0], (y1)[1]), cvt_pk_bf16((y1)[2], (y1)[3])}
;     __device__ __forceinline__ void operator()(const f32x4 (&acc)[2][2][4][2], const Unit& u, int ui, int wr, int wc, int fr, int fq) const {
;     ...
;             if (pn != 4) {
; #pragma unroll
;                 for (int ai = 0; ai < 2; ++ai)
; #pragma unroll
;                     for (int m = 0; m < 4; ++m) {
;                         const unsigned row = row0 + ai * HALF + m * 16; const float r2 = ss[ai][m];
; #pragma unroll
;                         for (int bj = 0; bj < 2; ++bj) {
;                             const f32x4 z0 = acc[ai][bj][m][0] * (g[bj][0] * r2), z1 = acc[ai][bj][m][1] * (g[bj][1] * r2);
;                             *(u32x4*)(dst + (size_t)(row * 2048u + 64u * bj)) = PG8_PACK8(z0, z1);
;                         }
;                     }
	v_mul_f32_e32 v228, v100, v220
	v_mul_f32_e32 v229, v101, v221
	v_mul_f32_e32 v220, v98, v222
	v_mul_f32_e32 v221, v99, v223
	v_mul_f32_e32 v222, v138, v180
	v_mul_f32_e32 v223, v139, v180
	v_cvt_pk_bf16_f32 v220, v220, v221
	v_cvt_pk_bf16_f32 v221, v228, v229
	flat_store_dwordx4 v[190:191], v[218:221]
	v_mul_f32_e32 v190, v144, v180
	v_mul_f32_e32 v191, v145, v180
	v_mov_b32_e32 v189, v1
	v_mul_f32_e32 v218, v142, v180
	v_mul_f32_e32 v219, v143, v180
	v_mul_f32_e32 v190, v96, v190
	v_mul_f32_e32 v191, v97, v191
	v_mul_f32_e32 v218, v94, v218
	v_mul_f32_e32 v219, v95, v219
	v_mul_f32_e32 v220, v140, v180
	v_mul_f32_e32 v221, v141, v180
	v_cvt_pk_bf16_f32 v218, v218, v219
	v_cvt_pk_bf16_f32 v219, v190, v191
	v_lshl_add_u64 v[190:191], v[160:161], 0, v[188:189]
	v_mul_f32_e32 v228, v92, v220
	v_mul_f32_e32 v229, v93, v221
	v_mul_f32_e32 v220, v90, v222
	v_mul_f32_e32 v221, v91, v223
	v_mul_f32_e32 v222, v130, v180
	v_mul_f32_e32 v223, v131, v180
	v_cvt_pk_bf16_f32 v220, v220, v221
	v_cvt_pk_bf16_f32 v221, v228, v229
	flat_store_dwordx4 v[190:191], v[218:221]
	v_mul_f32_e32 v190, v136, v180
	v_mul_f32_e32 v191, v137, v180
	v_mov_b32_e32 v185, v1
	v_mul_f32_e32 v218, v134, v180
	v_mul_f32_e32 v219, v135, v180
	v_mul_f32_e32 v190, v88, v190
	v_mul_f32_e32 v191, v89, v191
	v_mul_f32_e32 v218, v86, v218
	v_mul_f32_e32 v219, v87, v219
	v_mul_f32_e32 v220, v132, v180
	v_mul_f32_e32 v221, v133, v180
	v_cvt_pk_bf16_f32 v218, v218, v219
	v_cvt_pk_bf16_f32 v219, v190, v191
	v_lshl_add_u64 v[190:191], v[160:161], 0, v[184:185]
	v_mul_f32_e32 v228, v84, v220
	v_mul_f32_e32 v229, v85, v221
	v_mul_f32_e32 v220, v82, v222
	v_mul_f32_e32 v221, v83, v223
	v_mul_f32_e32 v222, v138, v174
	v_mul_f32_e32 v223, v139, v174
	v_cvt_pk_bf16_f32 v220, v220, v221
	v_cvt_pk_bf16_f32 v221, v228, v229
	flat_store_dwordx4 v[190:191], v[218:221]
	v_mul_f32_e32 v190, v144, v174
	v_mul_f32_e32 v191, v145, v174
	v_mov_b32_e32 v183, v1
	v_mul_f32_e32 v218, v142, v174
	v_mul_f32_e32 v219, v143, v174
	v_mul_f32_e32 v190, v80, v190
	v_mul_f32_e32 v191, v81, v191
	v_mul_f32_e32 v218, v78, v218
	v_mul_f32_e32 v219, v79, v219
	v_mul_f32_e32 v220, v140, v174
	v_mul_f32_e32 v221, v141, v174
	v_cvt_pk_bf16_f32 v218, v218, v219
	v_cvt_pk_bf16_f32 v219, v190, v191
	v_lshl_add_u64 v[190:191], v[160:161], 0, v[182:183]
	v_mul_f32_e32 v228, v76, v220
	v_mul_f32_e32 v229, v77, v221
	v_mul_f32_e32 v220, v74, v222
	v_mul_f32_e32 v221, v75, v223
	v_mul_f32_e32 v222, v130, v174
	v_mul_f32_e32 v223, v131, v174
	v_cvt_pk_bf16_f32 v220, v220, v221
	v_cvt_pk_bf16_f32 v221, v228, v229
	flat_store_dwordx4 v[190:191], v[218:221]
	v_mul_f32_e32 v190, v136, v174
	v_mul_f32_e32 v191, v137, v174
	v_mov_b32_e32 v179, v1
	v_mul_f32_e32 v218, v134, v174
	v_mul_f32_e32 v219, v135, v174
	v_mul_f32_e32 v190, v72, v190
	v_mul_f32_e32 v191, v73, v191
	v_mul_f32_e32 v218, v70, v218
	v_mul_f32_e32 v219, v71, v219
	v_mul_f32_e32 v220, v132, v174
	v_mul_f32_e32 v221, v133, v174
	v_cvt_pk_bf16_f32 v218, v218, v219
	v_cvt_pk_bf16_f32 v219, v190, v191
	v_lshl_add_u64 v[190:191], v[160:161], 0, v[178:179]
	v_mul_f32_e32 v228, v68, v220
	v_mul_f32_e32 v229, v69, v221
	v_mul_f32_e32 v220, v66, v222
	v_mul_f32_e32 v221, v67, v223
	v_mul_f32_e32 v222, v138, v170
	v_mul_f32_e32 v223, v139, v170
	v_cvt_pk_bf16_f32 v220, v220, v221
	v_cvt_pk_bf16_f32 v221, v228, v229
	flat_store_dwordx4 v[190:191], v[218:221]
	v_mul_f32_e32 v190, v144, v170
	v_mul_f32_e32 v191, v145, v170
	v_mov_b32_e32 v177, v1
	v_mul_f32_e32 v218, v142, v170
	v_mul_f32_e32 v219, v143, v170
	v_mul_f32_e32 v190, v64, v190
	v_mul_f32_e32 v191, v65, v191
	v_mul_f32_e32 v218, v62, v218
	v_mul_f32_e32 v219, v63, v219
	v_mul_f32_e32 v220, v140, v170
	v_mul_f32_e32 v221, v141, v170
	v_cvt_pk_bf16_f32 v218, v218, v219
	v_cvt_pk_bf16_f32 v219, v190, v191
	v_lshl_add_u64 v[190:191], v[160:161], 0, v[176:177]
	v_mul_f32_e32 v228, v60, v220
	v_mul_f32_e32 v229, v61, v221
	v_mul_f32_e32 v220, v58, v222
	v_mul_f32_e32 v221, v59, v223
	v_mul_f32_e32 v222, v130, v170
	v_mul_f32_e32 v223, v131, v170
	v_cvt_pk_bf16_f32 v220, v220, v221
	v_cvt_pk_bf16_f32 v221, v228, v229
	flat_store_dwordx4 v[190:191], v[218:221]
	v_mul_f32_e32 v190, v136, v170
	v_mul_f32_e32 v191, v137, v170
	v_mov_b32_e32 v173, v1
	v_mul_f32_e32 v218, v134, v170
	v_mul_f32_e32 v219, v135, v170
	v_mul_f32_e32 v190, v56, v190
	v_mul_f32_e32 v191, v57, v191
	v_mul_f32_e32 v218, v54, v218
	v_mul_f32_e32 v219, v55, v219
	v_mul_f32_e32 v220, v132, v170
	v_mul_f32_e32 v221, v133, v170
	v_cvt_pk_bf16_f32 v218, v218, v219
	v_cvt_pk_bf16_f32 v219, v190, v191
	v_lshl_add_u64 v[190:191], v[160:161], 0, v[172:173]
	v_mul_f32_e32 v228, v52, v220
	v_mul_f32_e32 v229, v53, v221
	v_mul_f32_e32 v220, v50, v222
	v_mul_f32_e32 v221, v51, v223
	v_mul_f32_e32 v222, v138, v166
	v_mul_f32_e32 v223, v139, v166
	v_cvt_pk_bf16_f32 v220, v220, v221
	v_cvt_pk_bf16_f32 v221, v228, v229
	flat_store_dwordx4 v[190:191], v[218:221]
	v_mul_f32_e32 v190, v144, v166
	v_mul_f32_e32 v191, v145, v166
	v_mov_b32_e32 v169, v1
	v_mul_f32_e32 v218, v142, v166
	v_mul_f32_e32 v219, v143, v166
	v_mul_f32_e32 v190, v48, v190
	v_mul_f32_e32 v191, v49, v191
	v_mul_f32_e32 v218, v46, v218
	v_mul_f32_e32 v219, v47, v219
	v_mul_f32_e32 v220, v140, v166
	v_mul_f32_e32 v221, v141, v166
	v_cvt_pk_bf16_f32 v218, v218, v219
	v_cvt_pk_bf16_f32 v219, v190, v191
	v_lshl_add_u64 v[190:191], v[160:161], 0, v[168:169]
	v_mul_f32_e32 v228, v44, v220
	v_mul_f32_e32 v229, v45, v221
	v_mul_f32_e32 v220, v42, v222
	v_mul_f32_e32 v221, v43, v223
	v_mul_f32_e32 v222, v130, v166
	v_mul_f32_e32 v223, v131, v166
	v_cvt_pk_bf16_f32 v220, v220, v221
	v_cvt_pk_bf16_f32 v221, v228, v229
; #define PG8_PACK8(y0, y1) (u32x4){cvt_pk_bf16((y0)[0], (y0)[1]), cvt_pk_bf16((y0)[2], (y0)[3]), cvt_pk_bf16((y1)[0], (y1)[1]), cvt_pk_bf16((y1)[2], (y1)[3])}
;     __device__ __forceinline__ void operator()(const f32x4 (&acc)[2][2][4][2], const Unit& u, int ui, int wr, int wc, int fr, int fq) const {
;     ...
;             if (pn != 4) {
; #pragma unroll
;                 for (int ai = 0; ai < 2; ++ai)
; #pragma unroll
;                     for (int m = 0; m < 4; ++m) {
;                         const unsigned row = row0 + ai * HALF + m * 16; const float r2 = ss[ai][m];
; #pragma unroll
;                         for (int bj = 0; bj < 2; ++bj) {
;                             const f32x4 z0 = acc[ai][bj][m][0] * (g[bj][0] * r2), z1 = acc[ai][bj][m][1] * (g[bj][1] * r2);
;                             *(u32x4*)(dst + (size_t)(row * 2048u + 64u * bj)) = PG8_PACK8(z0, z1);
;                         }
;                     }
;             } else {
;                 f32x4 ks[2][2];
; #pragma unroll
;                 for (int bj = 0; bj < 2; ++bj)
; #pragma unroll
;                     for (int n = 0; n < 2; ++n) ks[bj][n] = (f32x4){0.f, 0.f, 0.f, 0.f};
; #pragma unroll
;                 for (int ai = 0; ai < 2; ++ai)
; #pragma unroll
;                     for (int m = 0; m < 4; ++m) {
;                         const unsigned row = row0 + ai * HALF + m * 16; const float r2 = ss[ai][m];
; #pragma unroll
;                         for (int bj = 0; bj < 2; ++bj) {
;                             const f32x4 z0 = acc[ai][bj][m][0] * (g[bj][0] * r2), z1 = acc[ai][bj][m][1] * (g[bj][1] * r2);
;                             ks[bj][0] += z0; ks[bj][1] += z1;
;                             *(u32x4*)(dst + (size_t)(row * 2048u + 64u * bj)) = PG8_PACK8(z0, z1);
	flat_store_dwordx4 v[190:191], v[218:221]
	v_mul_f32_e32 v190, v136, v166
	v_mul_f32_e32 v191, v137, v166
	v_mov_b32_e32 v159, v1
	v_mul_f32_e32 v218, v134, v166
	v_mul_f32_e32 v219, v135, v166
	v_mul_f32_e32 v190, v40, v190
	v_mul_f32_e32 v191, v41, v191
	v_mul_f32_e32 v218, v38, v218
	v_mul_f32_e32 v219, v39, v219
	v_mul_f32_e32 v220, v132, v166
	v_mul_f32_e32 v221, v133, v166
	v_cvt_pk_bf16_f32 v218, v218, v219
	v_cvt_pk_bf16_f32 v219, v190, v191
	v_lshl_add_u64 v[190:191], v[160:161], 0, v[158:159]
	v_mul_f32_e32 v228, v36, v220
	v_mul_f32_e32 v229, v37, v221
	v_mul_f32_e32 v220, v34, v222
	v_mul_f32_e32 v221, v35, v223
	v_mul_f32_e32 v222, v138, v164
	v_mul_f32_e32 v223, v139, v164
	v_cvt_pk_bf16_f32 v220, v220, v221
	v_cvt_pk_bf16_f32 v221, v228, v229
	flat_store_dwordx4 v[190:191], v[218:221]
	v_mul_f32_e32 v190, v144, v164
	v_mul_f32_e32 v191, v145, v164
	v_mov_b32_e32 v129, v1
	v_mul_f32_e32 v218, v142, v164
	v_mul_f32_e32 v219, v143, v164
	v_mul_f32_e32 v190, v32, v190
	v_mul_f32_e32 v191, v33, v191
	v_mul_f32_e32 v218, v30, v218
	v_mul_f32_e32 v219, v31, v219
	v_mul_f32_e32 v220, v140, v164
	v_mul_f32_e32 v221, v141, v164
	v_cvt_pk_bf16_f32 v218, v218, v219
	v_cvt_pk_bf16_f32 v219, v190, v191
	v_lshl_add_u64 v[190:191], v[160:161], 0, v[128:129]
	v_mul_f32_e32 v228, v28, v220
	v_mul_f32_e32 v229, v29, v221
	v_mul_f32_e32 v220, v26, v222
	v_mul_f32_e32 v221, v27, v223
	v_mul_f32_e32 v222, v130, v164
	v_mul_f32_e32 v223, v131, v164
	v_cvt_pk_bf16_f32 v220, v220, v221
	v_cvt_pk_bf16_f32 v221, v228, v229
	flat_store_dwordx4 v[190:191], v[218:221]
	v_mul_f32_e32 v190, v136, v164
	v_mul_f32_e32 v191, v137, v164
	v_mov_b32_e32 v127, v1
	v_mul_f32_e32 v218, v134, v164
	v_mul_f32_e32 v219, v135, v164
	v_mul_f32_e32 v190, v24, v190
	v_mul_f32_e32 v191, v25, v191
	v_mul_f32_e32 v218, v22, v218
	v_mul_f32_e32 v219, v23, v219
	v_mul_f32_e32 v220, v132, v164
	v_mul_f32_e32 v221, v133, v164
	v_cvt_pk_bf16_f32 v218, v218, v219
	v_cvt_pk_bf16_f32 v219, v190, v191
	v_lshl_add_u64 v[190:191], v[160:161], 0, v[126:127]
	v_mul_f32_e32 v228, v20, v220
	v_mul_f32_e32 v229, v21, v221
	v_mul_f32_e32 v220, v18, v222
	v_mul_f32_e32 v221, v19, v223
	v_mul_f32_e32 v222, v138, v162
	v_mul_f32_e32 v223, v139, v162
	v_cvt_pk_bf16_f32 v220, v220, v221
	v_cvt_pk_bf16_f32 v221, v228, v229
	flat_store_dwordx4 v[190:191], v[218:221]
	v_mul_f32_e32 v190, v144, v162
	v_mul_f32_e32 v191, v145, v162
	v_mov_b32_e32 v125, v1
	v_mul_f32_e32 v218, v142, v162
	v_mul_f32_e32 v219, v143, v162
	v_mul_f32_e32 v190, v16, v190
	v_mul_f32_e32 v191, v17, v191
	v_mul_f32_e32 v218, v14, v218
	v_mul_f32_e32 v219, v15, v219
	v_mul_f32_e32 v220, v140, v162
	v_mul_f32_e32 v221, v141, v162
	v_cvt_pk_bf16_f32 v218, v218, v219
	v_cvt_pk_bf16_f32 v219, v190, v191
	v_lshl_add_u64 v[190:191], v[160:161], 0, v[124:125]
	v_mul_f32_e32 v228, v12, v220
	v_mul_f32_e32 v229, v13, v221
	v_mul_f32_e32 v220, v10, v222
	v_mul_f32_e32 v221, v11, v223
	v_mul_f32_e32 v222, v130, v162
	v_mul_f32_e32 v223, v131, v162
	v_cvt_pk_bf16_f32 v220, v220, v221
	v_cvt_pk_bf16_f32 v221, v228, v229
	flat_store_dwordx4 v[190:191], v[218:221]
	v_mul_f32_e32 v190, v136, v162
	v_mul_f32_e32 v191, v137, v162
	v_mov_b32_e32 v123, v1
	v_mul_f32_e32 v218, v134, v162
	v_mul_f32_e32 v219, v135, v162
	v_mul_f32_e32 v190, v8, v190
	v_mul_f32_e32 v191, v9, v191
	v_mul_f32_e32 v218, v6, v218
	v_mul_f32_e32 v219, v7, v219
	v_mul_f32_e32 v220, v132, v162
	v_mul_f32_e32 v221, v133, v162
	v_cvt_pk_bf16_f32 v218, v218, v219
	v_cvt_pk_bf16_f32 v219, v190, v191
	v_lshl_add_u64 v[190:191], v[160:161], 0, v[122:123]
	v_mul_f32_e32 v228, v4, v220
	v_mul_f32_e32 v229, v5, v221
	v_mul_f32_e32 v220, v2, v222
	v_mul_f32_e32 v221, v3, v223
	s_mov_b64 s[26:27], 0
	v_cvt_pk_bf16_f32 v220, v220, v221
	v_cvt_pk_bf16_f32 v221, v228, v229
	flat_store_dwordx4 v[190:191], v[218:221]
.LBB0_616:
	s_andn2_b64 vcc, exec, s[26:27]
	s_cbranch_vccnz .LBB0_620
	v_mov_b32_e32 v199, v198
	v_add_f32_e32 v190, 0, v206
	v_add_f32_e32 v191, 0, v207
	v_add_f32_e32 v222, 0, v208
	v_add_f32_e32 v223, 0, v209
	v_cvt_pk_bf16_f32 v218, v208, v209
	v_cvt_pk_bf16_f32 v219, v206, v207
	v_cvt_pk_bf16_f32 v220, v212, v213
	v_cvt_pk_bf16_f32 v221, v210, v211
	v_lshl_add_u64 v[206:207], v[160:161], 0, v[0:1]
	v_mul_f32_e32 v208, v136, v198
	v_mul_f32_e32 v209, v137, v199
	v_mul_f32_e32 v198, v132, v198
	v_mul_f32_e32 v199, v133, v199
	v_add_f32_e32 v228, 0, v210
	v_add_f32_e32 v229, 0, v211
	v_add_f32_e32 v240, 0, v212
	v_add_f32_e32 v241, 0, v213
	flat_store_dwordx4 v[206:207], v[218:221]
	v_mul_f32_e32 v210, v120, v208
	v_mul_f32_e32 v211, v121, v209
	v_mul_f32_e32 v212, v118, v204
	v_mul_f32_e32 v213, v119, v205
	v_mul_f32_e32 v218, v116, v198
	v_mul_f32_e32 v219, v117, v199
	v_mul_f32_e32 v220, v114, v202
	v_mul_f32_e32 v221, v115, v203
	v_fma_f32 v198, v116, v198, 0
	v_fma_f32 v199, v117, v199, 0
	v_fma_f32 v202, v114, v202, 0
	v_fma_f32 v203, v115, v203, 0
	v_cvt_pk_bf16_f32 v114, v212, v213
	v_cvt_pk_bf16_f32 v115, v210, v211
	v_cvt_pk_bf16_f32 v116, v220, v221
	v_cvt_pk_bf16_f32 v117, v218, v219
	v_fma_f32 v120, v120, v208, 0
	v_fma_f32 v121, v121, v209, 0
	flat_store_dwordx4 v[206:207], v[114:117] offset:64
	v_mul_f32_e32 v208, v140, v186
	v_mul_f32_e32 v209, v141, v186
	v_mul_f32_e32 v210, v138, v186
	v_mul_f32_e32 v211, v139, v186
	v_mul_f32_e32 v114, v144, v186
	v_mul_f32_e32 v115, v145, v186
	v_mul_f32_e32 v116, v142, v186
	v_mul_f32_e32 v117, v143, v186
	v_mov_b32_e32 v201, v1
	v_fma_f32 v118, v118, v204, 0
	v_fma_f32 v119, v119, v205, 0
	v_mul_f32_e32 v204, v112, v114
	v_mul_f32_e32 v205, v113, v115
	v_mul_f32_e32 v206, v110, v116
	v_mul_f32_e32 v207, v111, v117
; #define PG8_PACK8(y0, y1) (u32x4){cvt_pk_bf16((y0)[0], (y0)[1]), cvt_pk_bf16((y0)[2], (y0)[3]), cvt_pk_bf16((y1)[0], (y1)[1]), cvt_pk_bf16((y1)[2], (y1)[3])}
;     __device__ __forceinline__ void operator()(const f32x4 (&acc)[2][2][4][2], const Unit& u, int ui, int wr, int wc, int fr, int fq) const {
;     ...
;                 for (int ai = 0; ai < 2; ++ai)
; #pragma unroll
;                     for (int m = 0; m < 4; ++m) {
;                         const unsigned row = row0 + ai * HALF + m * 16; const float r2 = ss[ai][m];
; #pragma unroll
;                         for (int bj = 0; bj < 2; ++bj) {
;                             const f32x4 z0 = acc[ai][bj][m][0] * (g[bj][0] * r2), z1 = acc[ai][bj][m][1] * (g[bj][1] * r2);
;                             ks[bj][0] += z0; ks[bj][1] += z1;
;                             *(u32x4*)(dst + (size_t)(row * 2048u + 64u * bj)) = PG8_PACK8(z0, z1);
;                         }
;                     }
	v_mul_f32_e32 v212, v108, v208
	v_mul_f32_e32 v213, v109, v209
	v_mul_f32_e32 v218, v106, v210
	v_mul_f32_e32 v219, v107, v211
	v_fma_f32 v112, v112, v114, v190
	v_fma_f32 v113, v113, v115, v191
	v_fma_f32 v110, v110, v116, v222
	v_fma_f32 v111, v111, v117, v223
	v_fma_f32 v114, v108, v208, v228
	v_fma_f32 v115, v109, v209, v229
	v_fma_f32 v116, v106, v210, v240
	v_fma_f32 v117, v107, v211, v241
	v_cvt_pk_bf16_f32 v106, v206, v207
	v_cvt_pk_bf16_f32 v107, v204, v205
	v_cvt_pk_bf16_f32 v108, v218, v219
	v_cvt_pk_bf16_f32 v109, v212, v213
	v_lshl_add_u64 v[190:191], v[160:161], 0, v[200:201]
	flat_store_dwordx4 v[190:191], v[106:109]
	v_mul_f32_e32 v204, v132, v186
	v_mul_f32_e32 v205, v133, v186
	v_mul_f32_e32 v206, v130, v186
	v_mul_f32_e32 v207, v131, v186
	v_mul_f32_e32 v106, v136, v186
	v_mul_f32_e32 v107, v137, v186
	v_mul_f32_e32 v108, v134, v186
	v_mul_f32_e32 v109, v135, v186
	v_mov_b32_e32 v197, v1
	v_mul_f32_e32 v190, v104, v106
	v_mul_f32_e32 v191, v105, v107
	v_mul_f32_e32 v200, v102, v108
	v_mul_f32_e32 v201, v103, v109
	v_mul_f32_e32 v208, v100, v204
	v_mul_f32_e32 v209, v101, v205
	v_mul_f32_e32 v210, v98, v206
	v_mul_f32_e32 v211, v99, v207
	v_fma_f32 v104, v104, v106, v120
	v_fma_f32 v105, v105, v107, v121
	v_fma_f32 v102, v102, v108, v118
	v_fma_f32 v103, v103, v109, v119
	v_fma_f32 v106, v100, v204, v198
	v_fma_f32 v107, v101, v205, v199
	v_fma_f32 v108, v98, v206, v202
	v_fma_f32 v109, v99, v207, v203
	v_cvt_pk_bf16_f32 v98, v200, v201
	v_cvt_pk_bf16_f32 v99, v190, v191
	v_cvt_pk_bf16_f32 v100, v210, v211
	v_cvt_pk_bf16_f32 v101, v208, v209
	v_lshl_add_u64 v[118:119], v[160:161], 0, v[196:197]
	flat_store_dwordx4 v[118:119], v[98:101]
	v_mul_f32_e32 v190, v140, v180
	v_mul_f32_e32 v191, v141, v180
	v_mul_f32_e32 v196, v138, v180
	v_mul_f32_e32 v197, v139, v180
	v_mul_f32_e32 v98, v144, v180
	v_mul_f32_e32 v99, v145, v180
	v_mul_f32_e32 v100, v142, v180
	v_mul_f32_e32 v101, v143, v180
	v_mov_b32_e32 v189, v1
	v_mul_f32_e32 v118, v96, v98
	v_mul_f32_e32 v119, v97, v99
	v_mul_f32_e32 v120, v94, v100
	v_mul_f32_e32 v121, v95, v101
	v_mul_f32_e32 v198, v92, v190
	v_mul_f32_e32 v199, v93, v191
	v_mul_f32_e32 v200, v90, v196
	v_mul_f32_e32 v201, v91, v197
	v_fma_f32 v96, v96, v98, v112
	v_fma_f32 v97, v97, v99, v113
	v_fma_f32 v94, v94, v100, v110
	v_fma_f32 v95, v95, v101, v111
	v_fma_f32 v98, v92, v190, v114
	v_fma_f32 v99, v93, v191, v115
	v_fma_f32 v100, v90, v196, v116
	v_fma_f32 v101, v91, v197, v117
	v_cvt_pk_bf16_f32 v90, v120, v121
	v_cvt_pk_bf16_f32 v91, v118, v119
	v_cvt_pk_bf16_f32 v92, v200, v201
	v_cvt_pk_bf16_f32 v93, v198, v199
	v_lshl_add_u64 v[110:111], v[160:161], 0, v[188:189]
	flat_store_dwordx4 v[110:111], v[90:93]
	v_mul_f32_e32 v114, v132, v180
	v_mul_f32_e32 v115, v133, v180
	v_mul_f32_e32 v116, v130, v180
	v_mul_f32_e32 v117, v131, v180
	v_mul_f32_e32 v90, v136, v180
	v_mul_f32_e32 v91, v137, v180
	v_mul_f32_e32 v92, v134, v180
	v_mul_f32_e32 v93, v135, v180
	v_mov_b32_e32 v185, v1
	v_mul_f32_e32 v110, v88, v90
	v_mul_f32_e32 v111, v89, v91
	v_mul_f32_e32 v112, v86, v92
	v_mul_f32_e32 v113, v87, v93
	v_mul_f32_e32 v118, v84, v114
	v_mul_f32_e32 v119, v85, v115
	v_mul_f32_e32 v120, v82, v116
	v_mul_f32_e32 v121, v83, v117
	v_fma_f32 v88, v88, v90, v104
	v_fma_f32 v89, v89, v91, v105
	v_fma_f32 v86, v86, v92, v102
	v_fma_f32 v87, v87, v93, v103
	v_fma_f32 v90, v84, v114, v106
	v_fma_f32 v91, v85, v115, v107
	v_fma_f32 v92, v82, v116, v108
	v_fma_f32 v93, v83, v117, v109
	v_cvt_pk_bf16_f32 v82, v112, v113
	v_cvt_pk_bf16_f32 v83, v110, v111
	v_cvt_pk_bf16_f32 v84, v120, v121
	v_cvt_pk_bf16_f32 v85, v118, v119
	v_lshl_add_u64 v[102:103], v[160:161], 0, v[184:185]
	flat_store_dwordx4 v[102:103], v[82:85]
	v_mul_f32_e32 v106, v140, v174
	v_mul_f32_e32 v107, v141, v174
	v_mul_f32_e32 v108, v138, v174
	v_mul_f32_e32 v109, v139, v174
	v_mul_f32_e32 v82, v144, v174
	v_mul_f32_e32 v83, v145, v174
	v_mul_f32_e32 v84, v142, v174
	v_mul_f32_e32 v85, v143, v174
	v_mov_b32_e32 v183, v1
	v_mul_f32_e32 v102, v80, v82
	v_mul_f32_e32 v103, v81, v83
	v_mul_f32_e32 v104, v78, v84
	v_mul_f32_e32 v105, v79, v85
	v_mul_f32_e32 v110, v76, v106
	v_mul_f32_e32 v111, v77, v107
	v_mul_f32_e32 v112, v74, v108
	v_mul_f32_e32 v113, v75, v109
	v_fma_f32 v80, v80, v82, v96
	v_fma_f32 v81, v81, v83, v97
	v_fma_f32 v78, v78, v84, v94
	v_fma_f32 v79, v79, v85, v95
	v_fma_f32 v82, v76, v106, v98
	v_fma_f32 v83, v77, v107, v99
	v_fma_f32 v84, v74, v108, v100
	v_fma_f32 v85, v75, v109, v101
	v_cvt_pk_bf16_f32 v74, v104, v105
	v_cvt_pk_bf16_f32 v75, v102, v103
	v_cvt_pk_bf16_f32 v76, v112, v113
	v_cvt_pk_bf16_f32 v77, v110, v111
	v_lshl_add_u64 v[94:95], v[160:161], 0, v[182:183]
	flat_store_dwordx4 v[94:95], v[74:77]
	v_mul_f32_e32 v98, v132, v174
	v_mul_f32_e32 v99, v133, v174
	v_mul_f32_e32 v100, v130, v174
	v_mul_f32_e32 v101, v131, v174
	v_mul_f32_e32 v74, v136, v174
	v_mul_f32_e32 v75, v137, v174
	v_mul_f32_e32 v76, v134, v174
	v_mul_f32_e32 v77, v135, v174
	v_mov_b32_e32 v179, v1
	v_mul_f32_e32 v94, v72, v74
	v_mul_f32_e32 v95, v73, v75
	v_mul_f32_e32 v96, v70, v76
	v_mul_f32_e32 v97, v71, v77
	v_mul_f32_e32 v102, v68, v98
	v_mul_f32_e32 v103, v69, v99
	v_mul_f32_e32 v104, v66, v100
	v_mul_f32_e32 v105, v67, v101
	v_fma_f32 v72, v72, v74, v88
	v_fma_f32 v73, v73, v75, v89
	v_fma_f32 v70, v70, v76, v86
	v_fma_f32 v71, v71, v77, v87
	v_fma_f32 v74, v68, v98, v90
	v_fma_f32 v75, v69, v99, v91
	v_fma_f32 v76, v66, v100, v92
	v_fma_f32 v77, v67, v101, v93
	v_cvt_pk_bf16_f32 v66, v96, v97
	v_cvt_pk_bf16_f32 v67, v94, v95
	v_cvt_pk_bf16_f32 v68, v104, v105
	v_cvt_pk_bf16_f32 v69, v102, v103
	v_lshl_add_u64 v[86:87], v[160:161], 0, v[178:179]
; #define PG8_PACK8(y0, y1) (u32x4){cvt_pk_bf16((y0)[0], (y0)[1]), cvt_pk_bf16((y0)[2], (y0)[3]), cvt_pk_bf16((y1)[0], (y1)[1]), cvt_pk_bf16((y1)[2], (y1)[3])}
;     __device__ __forceinline__ void operator()(const f32x4 (&acc)[2][2][4][2], const Unit& u, int ui, int wr, int wc, int fr, int fq) const {
;     ...
;                 for (int ai = 0; ai < 2; ++ai)
; #pragma unroll
;                     for (int m = 0; m < 4; ++m) {
;                         const unsigned row = row0 + ai * HALF + m * 16; const float r2 = ss[ai][m];
; #pragma unroll
;                         for (int bj = 0; bj < 2; ++bj) {
;                             const f32x4 z0 = acc[ai][bj][m][0] * (g[bj][0] * r2), z1 = acc[ai][bj][m][1] * (g[bj][1] * r2);
;                             ks[bj][0] += z0; ks[bj][1] += z1;
;                             *(u32x4*)(dst + (size_t)(row * 2048u + 64u * bj)) = PG8_PACK8(z0, z1);
;                         }
;                     }
; #pragma unroll
;                 for (int bj = 0; bj < 2; ++bj)
; #pragma unroll
;                     for (int n = 0; n < 2; ++n)
; #pragma unroll
;                         for (int e = 0; e < 4; ++e) { float s = ks[bj][n][e]; s += __shfl_xor(s, 1); s += __shfl_xor(s, 2); s += __shfl_xor(s, 4); s += __shfl_xor(s, 8); ks[bj][n][e] = s; }
	flat_store_dwordx4 v[86:87], v[66:69]
	v_mul_f32_e32 v90, v140, v170
	v_mul_f32_e32 v91, v141, v170
	v_mul_f32_e32 v92, v138, v170
	v_mul_f32_e32 v93, v139, v170
	v_mul_f32_e32 v66, v144, v170
	v_mul_f32_e32 v67, v145, v170
	v_mul_f32_e32 v68, v142, v170
	v_mul_f32_e32 v69, v143, v170
	v_mov_b32_e32 v177, v1
	v_mul_f32_e32 v86, v64, v66
	v_mul_f32_e32 v87, v65, v67
	v_mul_f32_e32 v88, v62, v68
	v_mul_f32_e32 v89, v63, v69
	v_mul_f32_e32 v94, v60, v90
	v_mul_f32_e32 v95, v61, v91
	v_mul_f32_e32 v96, v58, v92
	v_mul_f32_e32 v97, v59, v93
	v_fma_f32 v64, v64, v66, v80
	v_fma_f32 v65, v65, v67, v81
	v_fma_f32 v62, v62, v68, v78
	v_fma_f32 v63, v63, v69, v79
	v_fma_f32 v66, v60, v90, v82
	v_fma_f32 v67, v61, v91, v83
	v_fma_f32 v68, v58, v92, v84
	v_fma_f32 v69, v59, v93, v85
	v_cvt_pk_bf16_f32 v58, v88, v89
	v_cvt_pk_bf16_f32 v59, v86, v87
	v_cvt_pk_bf16_f32 v60, v96, v97
	v_cvt_pk_bf16_f32 v61, v94, v95
	v_lshl_add_u64 v[78:79], v[160:161], 0, v[176:177]
	flat_store_dwordx4 v[78:79], v[58:61]
	v_mul_f32_e32 v82, v132, v170
	v_mul_f32_e32 v83, v133, v170
	v_mul_f32_e32 v84, v130, v170
	v_mul_f32_e32 v85, v131, v170
	v_mul_f32_e32 v58, v136, v170
	v_mul_f32_e32 v59, v137, v170
	v_mul_f32_e32 v60, v134, v170
	v_mul_f32_e32 v61, v135, v170
	v_mov_b32_e32 v173, v1
	v_mul_f32_e32 v78, v56, v58
	v_mul_f32_e32 v79, v57, v59
	v_mul_f32_e32 v80, v54, v60
	v_mul_f32_e32 v81, v55, v61
	v_mul_f32_e32 v86, v52, v82
	v_mul_f32_e32 v87, v53, v83
	v_mul_f32_e32 v88, v50, v84
	v_mul_f32_e32 v89, v51, v85
	v_fma_f32 v56, v56, v58, v72
	v_fma_f32 v57, v57, v59, v73
	v_fma_f32 v54, v54, v60, v70
	v_fma_f32 v55, v55, v61, v71
	v_fma_f32 v58, v52, v82, v74
	v_fma_f32 v59, v53, v83, v75
	v_fma_f32 v60, v50, v84, v76
	v_fma_f32 v61, v51, v85, v77
	v_cvt_pk_bf16_f32 v50, v80, v81
	v_cvt_pk_bf16_f32 v51, v78, v79
	v_cvt_pk_bf16_f32 v52, v88, v89
	v_cvt_pk_bf16_f32 v53, v86, v87
	v_lshl_add_u64 v[70:71], v[160:161], 0, v[172:173]
	flat_store_dwordx4 v[70:71], v[50:53]
	v_mul_f32_e32 v74, v140, v166
	v_mul_f32_e32 v75, v141, v166
	v_mul_f32_e32 v76, v138, v166
	v_mul_f32_e32 v77, v139, v166
	v_mul_f32_e32 v50, v144, v166
	v_mul_f32_e32 v51, v145, v166
	v_mul_f32_e32 v52, v142, v166
	v_mul_f32_e32 v53, v143, v166
	v_mov_b32_e32 v169, v1
	v_mul_f32_e32 v70, v48, v50
	v_mul_f32_e32 v71, v49, v51
	v_mul_f32_e32 v72, v46, v52
	v_mul_f32_e32 v73, v47, v53
	v_mul_f32_e32 v78, v44, v74
	v_mul_f32_e32 v79, v45, v75
	v_mul_f32_e32 v80, v42, v76
	v_mul_f32_e32 v81, v43, v77
	v_fma_f32 v48, v48, v50, v64
	v_fma_f32 v49, v49, v51, v65
	v_fma_f32 v46, v46, v52, v62
	v_fma_f32 v47, v47, v53, v63
	v_fma_f32 v50, v44, v74, v66
	v_fma_f32 v51, v45, v75, v67
	v_fma_f32 v52, v42, v76, v68
	v_fma_f32 v53, v43, v77, v69
	v_cvt_pk_bf16_f32 v42, v72, v73
	v_cvt_pk_bf16_f32 v43, v70, v71
	v_cvt_pk_bf16_f32 v44, v80, v81
	v_cvt_pk_bf16_f32 v45, v78, v79
	v_lshl_add_u64 v[62:63], v[160:161], 0, v[168:169]
	flat_store_dwordx4 v[62:63], v[42:45]
	v_mul_f32_e32 v66, v132, v166
	v_mul_f32_e32 v67, v133, v166
	v_mul_f32_e32 v68, v130, v166
	v_mul_f32_e32 v69, v131, v166
	v_mul_f32_e32 v42, v136, v166
	v_mul_f32_e32 v43, v137, v166
	v_mul_f32_e32 v44, v134, v166
	v_mul_f32_e32 v45, v135, v166
	v_mov_b32_e32 v159, v1
	v_mul_f32_e32 v62, v40, v42
	v_mul_f32_e32 v63, v41, v43
	v_mul_f32_e32 v64, v38, v44
	v_mul_f32_e32 v65, v39, v45
	v_mul_f32_e32 v70, v36, v66
	v_mul_f32_e32 v71, v37, v67
	v_mul_f32_e32 v72, v34, v68
	v_mul_f32_e32 v73, v35, v69
	v_fma_f32 v40, v40, v42, v56
	v_fma_f32 v41, v41, v43, v57
	v_fma_f32 v38, v38, v44, v54
	v_fma_f32 v39, v39, v45, v55
	v_fma_f32 v42, v36, v66, v58
	v_fma_f32 v43, v37, v67, v59
	v_fma_f32 v44, v34, v68, v60
	v_fma_f32 v45, v35, v69, v61
	v_cvt_pk_bf16_f32 v34, v64, v65
	v_cvt_pk_bf16_f32 v35, v62, v63
	v_cvt_pk_bf16_f32 v36, v72, v73
	v_cvt_pk_bf16_f32 v37, v70, v71
	v_lshl_add_u64 v[54:55], v[160:161], 0, v[158:159]
	flat_store_dwordx4 v[54:55], v[34:37]
	v_mul_f32_e32 v58, v140, v164
	v_mul_f32_e32 v59, v141, v164
	v_mul_f32_e32 v60, v138, v164
	v_mul_f32_e32 v61, v139, v164
	v_mul_f32_e32 v34, v144, v164
	v_mul_f32_e32 v35, v145, v164
	v_mul_f32_e32 v36, v142, v164
	v_mul_f32_e32 v37, v143, v164
	v_mov_b32_e32 v129, v1
	v_mul_f32_e32 v54, v32, v34
	v_mul_f32_e32 v55, v33, v35
	v_mul_f32_e32 v56, v30, v36
	v_mul_f32_e32 v57, v31, v37
	v_mul_f32_e32 v62, v28, v58
	v_mul_f32_e32 v63, v29, v59
	v_mul_f32_e32 v64, v26, v60
	v_mul_f32_e32 v65, v27, v61
	v_fma_f32 v32, v32, v34, v48
	v_fma_f32 v33, v33, v35, v49
	v_fma_f32 v30, v30, v36, v46
	v_fma_f32 v31, v31, v37, v47
	v_fma_f32 v34, v28, v58, v50
	v_fma_f32 v35, v29, v59, v51
	v_fma_f32 v36, v26, v60, v52
	v_fma_f32 v37, v27, v61, v53
	v_cvt_pk_bf16_f32 v26, v56, v57
	v_cvt_pk_bf16_f32 v27, v54, v55
	v_cvt_pk_bf16_f32 v28, v64, v65
	v_cvt_pk_bf16_f32 v29, v62, v63
	v_lshl_add_u64 v[46:47], v[160:161], 0, v[128:129]
	flat_store_dwordx4 v[46:47], v[26:29]
	v_mul_f32_e32 v50, v132, v164
	v_mul_f32_e32 v51, v133, v164
	v_mul_f32_e32 v52, v130, v164
	v_mul_f32_e32 v53, v131, v164
	v_mul_f32_e32 v26, v136, v164
	v_mul_f32_e32 v27, v137, v164
	v_mul_f32_e32 v28, v134, v164
	v_mul_f32_e32 v29, v135, v164
	v_mov_b32_e32 v127, v1
	v_mul_f32_e32 v46, v24, v26
	v_mul_f32_e32 v47, v25, v27
	v_mul_f32_e32 v48, v22, v28
	v_mul_f32_e32 v49, v23, v29
	v_mul_f32_e32 v54, v20, v50
	v_mul_f32_e32 v55, v21, v51
	v_mul_f32_e32 v56, v18, v52
	v_mul_f32_e32 v57, v19, v53
	v_fma_f32 v24, v24, v26, v40
	v_fma_f32 v25, v25, v27, v41
	v_fma_f32 v22, v22, v28, v38
	v_fma_f32 v23, v23, v29, v39
	v_fma_f32 v26, v20, v50, v42
	v_fma_f32 v27, v21, v51, v43
	v_fma_f32 v28, v18, v52, v44
	v_fma_f32 v29, v19, v53, v45
	v_cvt_pk_bf16_f32 v18, v48, v49
	v_cvt_pk_bf16_f32 v19, v46, v47
	v_cvt_pk_bf16_f32 v20, v56, v57
	v_cvt_pk_bf16_f32 v21, v54, v55
	v_lshl_add_u64 v[38:39], v[160:161], 0, v[126:127]
	flat_store_dwordx4 v[38:39], v[18:21]
	v_mul_f32_e32 v42, v140, v162
	v_mul_f32_e32 v43, v141, v162
	v_mul_f32_e32 v44, v138, v162
	v_mul_f32_e32 v45, v139, v162
	v_mul_f32_e32 v20, v142, v162
	v_mul_f32_e32 v21, v143, v162
	v_mul_f32_e32 v18, v144, v162
	v_mul_f32_e32 v19, v145, v162
	v_mul_f32_e32 v40, v14, v20
	v_mul_f32_e32 v41, v15, v21
	v_fma_f32 v14, v14, v20, v30
	v_fma_f32 v15, v15, v21, v31
	v_mul_f32_e32 v38, v16, v18
	v_mul_f32_e32 v39, v17, v19
	v_mul_f32_e32 v46, v12, v42
	v_mul_f32_e32 v47, v13, v43
	v_fma_f32 v16, v16, v18, v32
	v_fma_f32 v17, v17, v19, v33
	v_fma_f32 v18, v12, v42, v34
	v_fma_f32 v19, v13, v43, v35
	ds_bpermute_b32 v42, v233, v14
	ds_bpermute_b32 v43, v233, v15
	v_fma_f32 v20, v10, v44, v36
	v_fma_f32 v21, v11, v45, v37
	v_mul_f32_e32 v36, v130, v162
	v_mul_f32_e32 v37, v131, v162
	v_mul_f32_e32 v48, v10, v44
	v_mul_f32_e32 v49, v11, v45
	v_cvt_pk_bf16_f32 v10, v40, v41
	v_mul_f32_e32 v40, v2, v36
	v_mul_f32_e32 v41, v3, v37
	v_fma_f32 v28, v2, v36, v28
	v_fma_f32 v29, v3, v37, v29
	s_waitcnt lgkmcnt(0)
;     __device__ __forceinline__ void operator()(const f32x4 (&acc)[2][2][4][2], const Unit& u, int ui, int wr, int wc, int fr, int fq) const {
;     ...
; #pragma unroll
;                 for (int bj = 0; bj < 2; ++bj)
; #pragma unroll
;                     for (int n = 0; n < 2; ++n)
; #pragma unroll
;                         for (int e = 0; e < 4; ++e) { float s = ks[bj][n][e]; s += __shfl_xor(s, 1); s += __shfl_xor(s, 2); s += __shfl_xor(s, 4); s += __shfl_xor(s, 8); ks[bj][n][e] = s; }
;                 if (fr == 0) { float* kp = (float*)(ws + E_KMP) + (size_t)(unsigned)((((u.pm * 4 + wc) * 2 + wr) * 64 + 8 * fq));
; #pragma unroll
;                     for (int bj = 0; bj < 2; ++bj)
; #pragma unroll
;                         for (int n = 0; n < 2; ++n) *(f32x4*)(kp + 32 * bj + 4 * n) = ks[bj][n]; }
	v_add_f32_e32 v2, v14, v42
	v_add_f32_e32 v3, v15, v43
	ds_bpermute_b32 v14, v233, v18
	ds_bpermute_b32 v15, v233, v19
	v_mov_b32_e32 v125, v1
	v_cvt_pk_bf16_f32 v11, v38, v39
	v_cvt_pk_bf16_f32 v12, v48, v49
	v_cvt_pk_bf16_f32 v13, v46, v47
	v_lshl_add_u64 v[30:31], v[160:161], 0, v[124:125]
	flat_store_dwordx4 v[30:31], v[10:13]
	s_waitcnt lgkmcnt(0)
	v_add_f32_e32 v14, v18, v14
	v_add_f32_e32 v15, v19, v15
	v_mul_f32_e32 v34, v132, v162
	v_mul_f32_e32 v35, v133, v162
	v_mul_f32_e32 v12, v134, v162
	v_mul_f32_e32 v13, v135, v162
	v_mul_f32_e32 v10, v136, v162
	v_mul_f32_e32 v11, v137, v162
	v_fma_f32 v22, v6, v12, v22
	v_fma_f32 v23, v7, v13, v23
	ds_bpermute_b32 v18, v233, v22
	ds_bpermute_b32 v19, v233, v23
	v_mul_f32_e32 v30, v8, v10
	v_mul_f32_e32 v31, v9, v11
	v_mul_f32_e32 v32, v6, v12
	v_mul_f32_e32 v33, v7, v13
	v_fma_f32 v24, v8, v10, v24
	v_fma_f32 v25, v9, v11, v25
	v_fma_f32 v26, v4, v34, v26
	v_fma_f32 v27, v5, v35, v27
	v_mul_f32_e32 v38, v4, v34
	v_mul_f32_e32 v39, v5, v35
	v_cvt_pk_bf16_f32 v34, v32, v33
	v_cvt_pk_bf16_f32 v35, v30, v31
	ds_bpermute_b32 v6, v233, v16
	ds_bpermute_b32 v7, v233, v17
	ds_bpermute_b32 v10, v233, v20
	ds_bpermute_b32 v11, v233, v21
	s_waitcnt lgkmcnt(0)
	v_add_f32_e32 v18, v22, v18
	v_add_f32_e32 v19, v23, v19
	ds_bpermute_b32 v22, v233, v24
	ds_bpermute_b32 v23, v233, v25
	ds_bpermute_b32 v30, v233, v28
	ds_bpermute_b32 v31, v233, v29
	ds_bpermute_b32 v32, v233, v26
	ds_bpermute_b32 v33, v233, v27
	v_add_f32_e32 v6, v16, v6
	v_add_f32_e32 v7, v17, v7
	v_add_f32_e32 v10, v20, v10
	v_add_f32_e32 v11, v21, v11
	s_waitcnt lgkmcnt(0)
	v_add_f32_e32 v22, v24, v22
	v_add_f32_e32 v23, v25, v23
	v_add_f32_e32 v28, v28, v30
	v_add_f32_e32 v29, v29, v31
	v_add_f32_e32 v26, v26, v32
	v_add_f32_e32 v27, v27, v33
	ds_bpermute_b32 v4, v234, v2
	ds_bpermute_b32 v5, v234, v3
	ds_bpermute_b32 v8, v234, v6
	ds_bpermute_b32 v9, v234, v7
	ds_bpermute_b32 v12, v234, v10
	ds_bpermute_b32 v13, v234, v11
	ds_bpermute_b32 v16, v234, v14
	ds_bpermute_b32 v17, v234, v15
	ds_bpermute_b32 v20, v234, v18
	ds_bpermute_b32 v21, v234, v19
	ds_bpermute_b32 v24, v234, v22
	ds_bpermute_b32 v25, v234, v23
	ds_bpermute_b32 v30, v234, v28
	ds_bpermute_b32 v31, v234, v29
	ds_bpermute_b32 v32, v234, v26
	ds_bpermute_b32 v33, v234, v27
	s_waitcnt lgkmcnt(0)
	v_add_f32_e32 v2, v2, v4
	v_add_f32_e32 v3, v3, v5
	v_add_f32_e32 v6, v6, v8
	v_add_f32_e32 v7, v7, v9
	v_add_f32_e32 v10, v10, v12
	v_add_f32_e32 v11, v11, v13
	v_add_f32_e32 v14, v14, v16
	v_add_f32_e32 v15, v15, v17
	v_add_f32_e32 v18, v18, v20
	v_add_f32_e32 v19, v19, v21
	v_add_f32_e32 v22, v22, v24
	v_add_f32_e32 v23, v23, v25
	v_add_f32_e32 v28, v28, v30
	v_add_f32_e32 v29, v29, v31
	v_add_f32_e32 v32, v26, v32
	v_add_f32_e32 v33, v27, v33
	ds_bpermute_b32 v4, v235, v2
	ds_bpermute_b32 v5, v235, v3
	v_cvt_pk_bf16_f32 v36, v40, v41
	ds_bpermute_b32 v8, v235, v6
	ds_bpermute_b32 v9, v235, v7
	ds_bpermute_b32 v12, v235, v10
	ds_bpermute_b32 v13, v235, v11
	ds_bpermute_b32 v16, v235, v14
	ds_bpermute_b32 v17, v235, v15
	ds_bpermute_b32 v20, v235, v18
	ds_bpermute_b32 v21, v235, v19
	ds_bpermute_b32 v24, v235, v22
	ds_bpermute_b32 v25, v235, v23
	ds_bpermute_b32 v30, v235, v28
	ds_bpermute_b32 v31, v235, v29
	ds_bpermute_b32 v40, v235, v32
	ds_bpermute_b32 v41, v235, v33
	s_waitcnt lgkmcnt(0)
	v_add_f32_e32 v2, v2, v4
	v_add_f32_e32 v3, v3, v5
	v_add_f32_e32 v6, v6, v8
	v_add_f32_e32 v7, v7, v9
	v_add_f32_e32 v10, v10, v12
	v_add_f32_e32 v11, v11, v13
	v_add_f32_e32 v14, v14, v16
	v_add_f32_e32 v15, v15, v17
	v_add_f32_e32 v18, v18, v20
	v_add_f32_e32 v19, v19, v21
	v_add_f32_e32 v22, v22, v24
	v_add_f32_e32 v23, v23, v25
	v_add_f32_e32 v26, v28, v30
	v_add_f32_e32 v27, v29, v31
	v_add_f32_e32 v30, v32, v40
	v_add_f32_e32 v31, v33, v41
	ds_bpermute_b32 v4, v236, v2
	ds_bpermute_b32 v5, v236, v3
	ds_bpermute_b32 v8, v236, v6
	ds_bpermute_b32 v9, v236, v7
	ds_bpermute_b32 v12, v236, v10
	ds_bpermute_b32 v13, v236, v11
	ds_bpermute_b32 v16, v236, v14
	ds_bpermute_b32 v17, v236, v15
	ds_bpermute_b32 v20, v236, v18
	ds_bpermute_b32 v21, v236, v19
	ds_bpermute_b32 v24, v236, v22
	ds_bpermute_b32 v25, v236, v23
	ds_bpermute_b32 v28, v236, v26
	ds_bpermute_b32 v29, v236, v27
	ds_bpermute_b32 v32, v236, v30
	ds_bpermute_b32 v33, v236, v31
	v_mov_b32_e32 v123, v1
	v_cvt_pk_bf16_f32 v37, v38, v39
	v_lshl_add_u64 v[38:39], v[160:161], 0, v[122:123]
	flat_store_dwordx4 v[38:39], v[34:37]
	s_and_saveexec_b64 s[26:27], s[36:37]
	s_cbranch_execz .LBB0_619
	v_lshl_add_u32 v0, s4, 9, v171
	s_waitcnt lgkmcnt(0)
	v_add_f32_e32 v6, v6, v8
	v_add_f32_e32 v7, v7, v9
	v_add_f32_e32 v4, v2, v4
	v_add_f32_e32 v5, v3, v5
	v_lshl_add_u64 v[2:3], v[0:1], 2, s[16:17]
	v_add_f32_e32 v30, v30, v32
	v_add_f32_e32 v31, v31, v33
	v_add_f32_e32 v28, v26, v28
	v_add_f32_e32 v29, v27, v29
	v_add_f32_e32 v22, v22, v24
	v_add_f32_e32 v23, v23, v25
	v_add_f32_e32 v20, v18, v20
	v_add_f32_e32 v21, v19, v21
	v_add_f32_e32 v14, v14, v16
	v_add_f32_e32 v15, v15, v17
	v_add_f32_e32 v12, v10, v12
	v_add_f32_e32 v13, v11, v13
	flat_store_dwordx4 v[2:3], v[4:7]
	flat_store_dwordx4 v[2:3], v[12:15] offset:16
	flat_store_dwordx4 v[2:3], v[20:23] offset:128
	flat_store_dwordx4 v[2:3], v[28:31] offset:144

; #define GAS __attribute__((address_space(1)))
; #define LAS __attribute__((address_space(3)))
; #define LDS_WAIT() asm volatile("s_waitcnt lgkmcnt(0)" ::: "memory")
; __device__ __forceinline__ unsigned pk2(float lo, float hi) { return f2bf(lo) | (f2bf(hi) << 16); }
; __device__ __forceinline__ void tr_finish(const TrItem& d, int lane, LAS float* scr, const float (&v)[32], const float keep) {
;     const int kb = d.item / d.nblk, nb = d.item % d.nblk, k0 = 64 * kb, n0 = 32 * nb;
;     const int c = lane & 7;
;     f32x4 g0 = (f32x4){1.f, 1.f, 1.f, 1.f}, g1 = g0;
;     if (d.gain) { g0 = *(const GAS f32x4*)(d.gain + k0 + 8 * c); g1 = *(const GAS f32x4*)(d.gain + k0 + 8 * c + 4); }
; #pragma unroll
;     for (int i = 0; i < 32; ++i) scr[(2 * i + (lane >> 5)) * 33 + (lane & 31)] = v[i] * keep;
;     LDS_WAIT(); asm volatile("" ::: "memory");
; #pragma unroll
;     for (int j = 0; j < 4; ++j) { const int n = (lane >> 3) + 8 * j; const LAS float* s = scr + (8 * c) * 33 + n;
;         v4u o; o.x = pk2(s[0 * 33] * g0[0], s[1 * 33] * g0[1]); o.y = pk2(s[2 * 33] * g0[2], s[3 * 33] * g0[3]); o.z = pk2(s[4 * 33] * g1[0], s[5 * 33] * g1[1]); o.w = pk2(s[6 * 33] * g1[2], s[7 * 33] * g1[3]);
;         *(GAS v4u*)(d.WT + (size_t)(n0 + n) * d.K + k0 + 8 * c) = o; }
.LBB0_662:
	v_mul_f32_e32 v40, v55, v54
	v_mul_f32_e32 v41, v56, v54
	ds_write2_b32 v52, v40, v41 offset1:66
	v_mul_f32_e32 v40, v57, v54
	v_mul_f32_e32 v41, v58, v54
	ds_write2_b32 v52, v40, v41 offset0:132 offset1:198
	v_mul_f32_e32 v40, v59, v54
	v_mul_f32_e32 v41, v60, v54
	ds_write2_b32 v87, v40, v41 offset0:8 offset1:74
	v_mul_f32_e32 v40, v61, v54
	v_mul_f32_e32 v41, v62, v54
	ds_write2_b32 v87, v40, v41 offset0:140 offset1:206
	v_mul_f32_e32 v40, v63, v54
	v_mul_f32_e32 v41, v64, v54
	ds_write2_b32 v88, v40, v41 offset0:16 offset1:82
	v_mul_f32_e32 v40, v65, v54
	v_mul_f32_e32 v41, v66, v54
	ds_write2_b32 v88, v40, v41 offset0:148 offset1:214
	v_mul_f32_e32 v40, v67, v54
	v_mul_f32_e32 v41, v68, v54
	ds_write2_b32 v89, v40, v41 offset0:24 offset1:90
	v_mul_f32_e32 v40, v69, v54
	v_mul_f32_e32 v41, v70, v54
	ds_write2_b32 v89, v40, v41 offset0:156 offset1:222
	v_mul_f32_e32 v40, v71, v54
	v_mul_f32_e32 v41, v72, v54
	ds_write2_b32 v90, v40, v41 offset0:32 offset1:98
	v_mul_f32_e32 v40, v73, v54
	v_mul_f32_e32 v41, v74, v54
	ds_write2_b32 v90, v40, v41 offset0:164 offset1:230
	v_mul_f32_e32 v40, v75, v54
	v_mul_f32_e32 v41, v76, v54
	ds_write2_b32 v91, v40, v41 offset0:40 offset1:106
	v_mul_f32_e32 v40, v77, v54
	v_mul_f32_e32 v41, v78, v54
	ds_write2_b32 v91, v40, v41 offset0:172 offset1:238
	v_mul_f32_e32 v40, v79, v54
	v_mul_f32_e32 v41, v80, v54
	ds_write2_b32 v92, v40, v41 offset0:48 offset1:114
	v_mul_f32_e32 v40, v81, v54
	v_mul_f32_e32 v41, v82, v54
	ds_write2_b32 v92, v40, v41 offset0:180 offset1:246
	v_mul_f32_e32 v40, v83, v54
	v_mul_f32_e32 v41, v84, v54
	ds_write2_b32 v93, v40, v41 offset0:56 offset1:122
	v_mul_f32_e32 v40, v85, v54
	v_mul_f32_e32 v41, v86, v54
	ds_write2_b32 v93, v40, v41 offset0:188 offset1:254
	s_waitcnt lgkmcnt(0)
	ds_read2_b32 v[40:41], v48 offset1:8
	ds_read2_b32 v[92:93], v48 offset0:66 offset1:74
	ds_read2_b32 v[94:95], v48 offset0:33 offset1:41
	ds_read2_b32 v[96:97], v48 offset0:99 offset1:107
	ds_read2_b32 v[98:99], v48 offset0:132 offset1:140
	ds_read2_b32 v[100:101], v48 offset0:198 offset1:206
	ds_read2_b32 v[102:103], v48 offset0:165 offset1:173
	ds_read2_b32 v[104:105], v48 offset0:231 offset1:239
	s_waitcnt lgkmcnt(7)
	v_mov_b32_e32 v88, v40
	s_waitcnt lgkmcnt(5)
	v_mov_b32_e32 v90, v94
	s_waitcnt lgkmcnt(4)
	v_mov_b32_e32 v91, v96
	s_waitcnt lgkmcnt(3)
	v_mov_b32_e32 v106, v98
	s_waitcnt lgkmcnt(2)
	v_mov_b32_e32 v107, v100
	v_mov_b32_e32 v89, v92
	v_mul_f32_e32 v90, v36, v90
	v_mul_f32_e32 v91, v37, v91
	v_mul_f32_e32 v106, v34, v106
	v_mul_f32_e32 v107, v35, v107
	s_waitcnt lgkmcnt(1)
	v_mov_b32_e32 v108, v102
	s_waitcnt lgkmcnt(0)
	v_mov_b32_e32 v109, v104
	s_mul_i32 s14, s14, s35
	v_mul_f32_e32 v88, v38, v88
	v_mul_f32_e32 v89, v39, v89
	v_mul_f32_e32 v108, v44, v108
	v_mul_f32_e32 v109, v45, v109
	v_bfe_u32 v92, v91, 16, 1
	s_movk_i32 s15, 0x7fff
	v_bfe_u32 v98, v107, 16, 1
	s_sub_i32 s14, s34, s14
	v_bfe_u32 v40, v109, 16, 1
	v_add3_u32 v92, v91, v92, s15
	v_bfe_u32 v91, v89, 16, 1
	v_add3_u32 v98, v107, v98, s15
	s_lshl_b32 s14, s14, 5
	v_add3_u32 v40, v109, v40, s15
	v_add3_u32 v89, v89, v91, s15
	v_lshrrev_b32_e32 v91, 16, v98
	s_mov_b32 s3, 0xffff0000
	v_bfe_u32 v94, v90, 16, 1
	v_bfe_u32 v96, v106, 16, 1
	v_and_or_b32 v91, v40, s3, v91
	v_or_b32_e32 v40, s14, v47
	v_add3_u32 v94, v90, v94, s15
	v_bfe_u32 v90, v88, 16, 1
	v_add3_u32 v96, v106, v96, s15
	v_lshrrev_b32_e32 v89, 16, v89
	v_mad_i64_i32 v[106:107], s[16:17], v40, s36, 0
	v_bfe_u32 v87, v108, 16, 1
	v_add3_u32 v88, v88, v90, s15
	v_and_or_b32 v89, v92, s3, v89
	v_lshl_add_u64 v[106:107], v[106:107], 1, s[8:9]
	s_lshl_b64 s[12:13], s[12:13], 1
	v_mov_b32_e32 v92, v41
	v_mov_b32_e32 v104, v103
	v_add3_u32 v87, v108, v87, s15
	v_lshrrev_b32_e32 v88, 16, v88
	v_lshrrev_b32_e32 v90, 16, v96
	v_lshl_add_u64 v[106:107], v[106:107], 0, s[12:13]
	v_mul_f32_e32 v40, v38, v92
	v_mul_f32_e32 v41, v39, v93
	v_mul_f32_e32 v92, v44, v104
	v_mul_f32_e32 v93, v45, v105
	v_and_or_b32 v90, v87, s3, v90
	v_and_or_b32 v88, v94, s3, v88
	v_lshl_add_u64 v[106:107], v[106:107], 0, v[0:1]
	v_mov_b32_e32 v96, v95
	v_bfe_u32 v87, v93, 16, 1
	global_store_dwordx4 v[106:107], v[88:91], off
	v_bfe_u32 v94, v92, 16, 1
	v_add3_u32 v87, v93, v87, s15
	v_mul_f32_e32 v88, v36, v96
	v_mul_f32_e32 v89, v37, v97
	v_bfe_u32 v93, v40, 16, 1
	v_bfe_u32 v96, v88, 16, 1
	v_add3_u32 v92, v92, v94, s15
	v_bfe_u32 v94, v41, 16, 1
	v_add3_u32 v40, v40, v93, s15
	v_mov_b32_e32 v100, v99
	v_bfe_u32 v95, v89, 16, 1
	v_add3_u32 v88, v88, v96, s15
	v_add3_u32 v41, v41, v94, s15
	v_lshrrev_b32_e32 v40, 16, v40
	v_mul_f32_e32 v90, v34, v100
	v_mul_f32_e32 v91, v35, v101
	v_add3_u32 v89, v89, v95, s15
	v_lshrrev_b32_e32 v41, 16, v41
	v_and_or_b32 v88, v88, s3, v40
	v_or_b32_e32 v40, s14, v49
	v_bfe_u32 v95, v90, 16, 1
	v_bfe_u32 v96, v91, 16, 1
	v_and_or_b32 v89, v89, s3, v41
	v_mad_i64_i32 v[40:41], s[16:17], v40, s36, 0
	v_add3_u32 v91, v91, v96, s15
	v_add3_u32 v90, v90, v95, s15
	v_lshl_add_u64 v[40:41], v[40:41], 1, s[8:9]
	v_lshrrev_b32_e32 v90, 16, v90
	v_lshrrev_b32_e32 v91, 16, v91
	v_lshl_add_u64 v[40:41], v[40:41], 0, s[12:13]
	v_and_or_b32 v91, v87, s3, v91
	v_and_or_b32 v90, v92, s3, v90
	v_lshl_add_u64 v[40:41], v[40:41], 0, v[0:1]
	ds_read2_b32 v[92:93], v48 offset0:16 offset1:24
	ds_read2_b32 v[94:95], v48 offset0:82 offset1:90
	global_store_dwordx4 v[40:41], v[88:91], off
	ds_read2_b32 v[40:41], v48 offset0:49 offset1:57
	ds_read2_b32 v[96:97], v48 offset0:115 offset1:123
	ds_read2_b32 v[98:99], v48 offset0:148 offset1:156
	ds_read2_b32 v[100:101], v48 offset0:214 offset1:222
	ds_read2_b32 v[102:103], v48 offset0:181 offset1:189
	ds_read2_b32 v[104:105], v48 offset0:247 offset1:255
	s_waitcnt lgkmcnt(7)
; #define GAS __attribute__((address_space(1)))
; #define LAS __attribute__((address_space(3)))
; #define LDS_WAIT() asm volatile("s_waitcnt lgkmcnt(0)" ::: "memory")
; __device__ __forceinline__ unsigned pk2(float lo, float hi) { return f2bf(lo) | (f2bf(hi) << 16); }
; __device__ __forceinline__ void tr_finish(const TrItem& d, int lane, LAS float* scr, const float (&v)[32], const float keep) {
;     ...
;     for (int j = 0; j < 4; ++j) { const int n = (lane >> 3) + 8 * j; const LAS float* s = scr + (8 * c) * 33 + n;
;         v4u o; o.x = pk2(s[0 * 33] * g0[0], s[1 * 33] * g0[1]); o.y = pk2(s[2 * 33] * g0[2], s[3 * 33] * g0[3]); o.z = pk2(s[4 * 33] * g1[0], s[5 * 33] * g1[1]); o.w = pk2(s[6 * 33] * g1[2], s[7 * 33] * g1[3]);
;         *(GAS v4u*)(d.WT + (size_t)(n0 + n) * d.K + k0 + 8 * c) = o; }
;     LDS_WAIT(); asm volatile("" ::: "memory");
	v_mov_b32_e32 v88, v92
	s_waitcnt lgkmcnt(5)
	v_mov_b32_e32 v90, v40
	s_waitcnt lgkmcnt(4)
	v_mov_b32_e32 v91, v96
	s_waitcnt lgkmcnt(3)
	v_mov_b32_e32 v106, v98
	s_waitcnt lgkmcnt(2)
	v_mov_b32_e32 v107, v100
	v_mov_b32_e32 v89, v94
	v_mul_f32_e32 v90, v36, v90
	v_mul_f32_e32 v91, v37, v91
	v_mul_f32_e32 v106, v34, v106
	v_mul_f32_e32 v107, v35, v107
	s_waitcnt lgkmcnt(1)
	v_mov_b32_e32 v108, v102
	s_waitcnt lgkmcnt(0)
	v_mov_b32_e32 v109, v104
	v_mul_f32_e32 v88, v38, v88
	v_mul_f32_e32 v89, v39, v89
	v_mul_f32_e32 v108, v44, v108
	v_mul_f32_e32 v109, v45, v109
	v_bfe_u32 v92, v91, 16, 1
	v_bfe_u32 v98, v107, 16, 1
	v_bfe_u32 v40, v109, 16, 1
	v_add3_u32 v92, v91, v92, s15
	v_bfe_u32 v91, v89, 16, 1
	v_add3_u32 v98, v107, v98, s15
	v_add3_u32 v40, v109, v40, s15
	v_add3_u32 v89, v89, v91, s15
	v_lshrrev_b32_e32 v91, 16, v98
	v_bfe_u32 v94, v90, 16, 1
	v_bfe_u32 v96, v106, 16, 1
	v_and_or_b32 v91, v40, s3, v91
	v_or_b32_e32 v40, s14, v50
	v_add3_u32 v94, v90, v94, s15
	v_bfe_u32 v90, v88, 16, 1
	v_add3_u32 v96, v106, v96, s15
	v_mad_i64_i32 v[106:107], s[16:17], v40, s36, 0
	v_bfe_u32 v87, v108, 16, 1
	v_add3_u32 v88, v88, v90, s15
	v_lshl_add_u64 v[106:107], v[106:107], 1, s[8:9]
	v_add3_u32 v87, v108, v87, s15
	v_lshrrev_b32_e32 v88, 16, v88
	v_lshrrev_b32_e32 v89, 16, v89
	v_lshrrev_b32_e32 v90, 16, v96
	v_lshl_add_u64 v[106:107], v[106:107], 0, s[12:13]
	v_mov_b32_e32 v96, v41
	v_mov_b32_e32 v104, v103
	v_and_or_b32 v90, v87, s3, v90
	v_and_or_b32 v89, v92, s3, v89
	v_and_or_b32 v88, v94, s3, v88
	v_lshl_add_u64 v[106:107], v[106:107], 0, v[0:1]
	v_mov_b32_e32 v94, v93
	v_mul_f32_e32 v36, v36, v96
	v_mul_f32_e32 v37, v37, v97
	v_mov_b32_e32 v100, v99
	v_mul_f32_e32 v40, v44, v104
	v_mul_f32_e32 v41, v45, v105
	global_store_dwordx4 v[106:107], v[88:91], off
	v_mul_f32_e32 v38, v38, v94
	v_mul_f32_e32 v39, v39, v95
	v_mul_f32_e32 v34, v34, v100
	v_mul_f32_e32 v35, v35, v101
	v_bfe_u32 v44, v41, 16, 1
	v_bfe_u32 v45, v40, 16, 1
	v_bfe_u32 v87, v37, 16, 1
	v_bfe_u32 v88, v36, 16, 1
	v_add3_u32 v88, v36, v88, s15
	v_add3_u32 v87, v37, v87, s15
	v_add3_u32 v36, v40, v45, s15
	v_add3_u32 v37, v41, v44, s15
	v_bfe_u32 v40, v38, 16, 1
	v_bfe_u32 v44, v34, 16, 1
	v_bfe_u32 v41, v39, 16, 1
	v_bfe_u32 v45, v35, 16, 1
	v_add3_u32 v34, v34, v44, s15
	v_add3_u32 v38, v38, v40, s15
	v_add3_u32 v35, v35, v45, s15
	v_add3_u32 v39, v39, v41, s15
	v_lshrrev_b32_e32 v38, 16, v38
	v_lshrrev_b32_e32 v34, 16, v34
	v_lshrrev_b32_e32 v39, 16, v39
	v_lshrrev_b32_e32 v35, 16, v35
	v_and_or_b32 v36, v36, s3, v34
	v_and_or_b32 v34, v88, s3, v38
	v_or_b32_e32 v38, s14, v51
	v_and_or_b32 v37, v37, s3, v35
	v_and_or_b32 v35, v87, s3, v39
	v_mad_i64_i32 v[38:39], s[14:15], v38, s36, 0
	v_lshl_add_u64 v[38:39], v[38:39], 1, s[8:9]
	v_lshl_add_u64 v[38:39], v[38:39], 0, s[12:13]
	v_lshl_add_u64 v[38:39], v[38:39], 0, v[0:1]
	global_store_dwordx4 v[38:39], v[34:37], off
	s_waitcnt lgkmcnt(0)
	s_add_i32 s38, s37, s28
	s_cmpk_gt_i32 s38, 0x31ff
	s_cselect_b64 s[12:13], -1, 0

; #define GAS __attribute__((address_space(1)))
; #define LAS __attribute__((address_space(3)))
; #define LDS_WAIT() asm volatile("s_waitcnt lgkmcnt(0)" ::: "memory")
; __device__ __forceinline__ unsigned pk2(float lo, float hi) { return f2bf(lo) | (f2bf(hi) << 16); }
; __device__ __forceinline__ void tr_finish(const TrItem& d, int lane, LAS float* scr, const float (&v)[32], const float keep) {
;     const int kb = d.item / d.nblk, nb = d.item % d.nblk, k0 = 64 * kb, n0 = 32 * nb;
;     const int c = lane & 7;
;     f32x4 g0 = (f32x4){1.f, 1.f, 1.f, 1.f}, g1 = g0;
;     if (d.gain) { g0 = *(const GAS f32x4*)(d.gain + k0 + 8 * c); g1 = *(const GAS f32x4*)(d.gain + k0 + 8 * c + 4); }
; #pragma unroll
;     for (int i = 0; i < 32; ++i) scr[(2 * i + (lane >> 5)) * 33 + (lane & 31)] = v[i] * keep;
;     LDS_WAIT(); asm volatile("" ::: "memory");
; #pragma unroll
;     for (int j = 0; j < 4; ++j) { const int n = (lane >> 3) + 8 * j; const LAS float* s = scr + (8 * c) * 33 + n;
;         v4u o; o.x = pk2(s[0 * 33] * g0[0], s[1 * 33] * g0[1]); o.y = pk2(s[2 * 33] * g0[2], s[3 * 33] * g0[3]); o.z = pk2(s[4 * 33] * g1[0], s[5 * 33] * g1[1]); o.w = pk2(s[6 * 33] * g1[2], s[7 * 33] * g1[3]);
;         *(GAS v4u*)(d.WT + (size_t)(n0 + n) * d.K + k0 + 8 * c) = o; }
.LBB0_694:
	s_waitcnt vmcnt(0)
	v_mul_f32_e32 v40, v2, v53
	v_mul_f32_e32 v41, v3, v53
	ds_write2_b32 v52, v40, v41 offset1:66
	v_mul_f32_e32 v40, v4, v53
	v_mul_f32_e32 v41, v5, v53
	ds_write2_b32 v52, v40, v41 offset0:132 offset1:198
	v_mul_f32_e32 v40, v6, v53
	v_mul_f32_e32 v41, v7, v53
	v_add_u32_e32 v87, 0x400, v52
	ds_write2_b32 v87, v40, v41 offset0:8 offset1:74
	v_mul_f32_e32 v40, v8, v53
	v_mul_f32_e32 v41, v9, v53
	ds_write2_b32 v87, v40, v41 offset0:140 offset1:206
	v_mul_f32_e32 v40, v10, v53
	v_mul_f32_e32 v41, v11, v53
	v_add_u32_e32 v88, 0x800, v52
	ds_write2_b32 v88, v40, v41 offset0:16 offset1:82
	v_mul_f32_e32 v40, v12, v53
	v_mul_f32_e32 v41, v13, v53
	ds_write2_b32 v88, v40, v41 offset0:148 offset1:214
	v_mul_f32_e32 v40, v14, v53
	v_mul_f32_e32 v41, v15, v53
	v_add_u32_e32 v89, 0xc00, v52
	ds_write2_b32 v89, v40, v41 offset0:24 offset1:90
	v_mul_f32_e32 v40, v16, v53
	v_mul_f32_e32 v41, v17, v53
	ds_write2_b32 v89, v40, v41 offset0:156 offset1:222
	v_mul_f32_e32 v40, v18, v53
	v_mul_f32_e32 v41, v19, v53
	v_add_u32_e32 v90, 0x1000, v52
	ds_write2_b32 v90, v40, v41 offset0:32 offset1:98
	v_mul_f32_e32 v40, v20, v53
	v_mul_f32_e32 v41, v21, v53
	ds_write2_b32 v90, v40, v41 offset0:164 offset1:230
	v_mul_f32_e32 v40, v22, v53
	v_mul_f32_e32 v41, v23, v53
	v_add_u32_e32 v91, 0x1400, v52
	ds_write2_b32 v91, v40, v41 offset0:40 offset1:106
	v_mul_f32_e32 v40, v24, v53
	v_mul_f32_e32 v41, v25, v53
	ds_write2_b32 v91, v40, v41 offset0:172 offset1:238
	v_mul_f32_e32 v40, v26, v53
	v_mul_f32_e32 v41, v27, v53
	v_add_u32_e32 v92, 0x1800, v52
	ds_write2_b32 v92, v40, v41 offset0:48 offset1:114
	v_mul_f32_e32 v40, v28, v53
	v_mul_f32_e32 v41, v29, v53
	ds_write2_b32 v92, v40, v41 offset0:180 offset1:246
	v_mul_f32_e32 v40, v30, v53
	v_mul_f32_e32 v41, v31, v53
	v_add_u32_e32 v93, 0x1c00, v52
	ds_write2_b32 v93, v40, v41 offset0:56 offset1:122
	v_mul_f32_e32 v40, v32, v53
	v_mul_f32_e32 v41, v33, v53
	ds_write2_b32 v93, v40, v41 offset0:188 offset1:254
	s_waitcnt lgkmcnt(0)
	ds_read2_b32 v[40:41], v48 offset1:8
	ds_read2_b32 v[98:99], v48 offset0:66 offset1:74
	ds_read2_b32 v[100:101], v48 offset0:33 offset1:41
	ds_read2_b32 v[102:103], v48 offset0:99 offset1:107
	ds_read2_b32 v[104:105], v48 offset0:132 offset1:140
	ds_read2_b32 v[106:107], v48 offset0:198 offset1:206
	ds_read2_b32 v[108:109], v48 offset0:165 offset1:173
	ds_read2_b32 v[110:111], v48 offset0:231 offset1:239
	s_waitcnt lgkmcnt(7)
	v_mov_b32_e32 v94, v40
	s_waitcnt lgkmcnt(5)
	v_mov_b32_e32 v96, v100
	s_waitcnt lgkmcnt(4)
	v_mov_b32_e32 v97, v102
	s_waitcnt lgkmcnt(3)
	v_mov_b32_e32 v112, v104
	s_waitcnt lgkmcnt(2)
	v_mov_b32_e32 v113, v106
	v_mov_b32_e32 v95, v98
	v_mul_f32_e32 v96, v36, v96
	v_mul_f32_e32 v97, v37, v97
	v_mul_f32_e32 v112, v34, v112
	v_mul_f32_e32 v113, v35, v113
	s_waitcnt lgkmcnt(1)
	v_mov_b32_e32 v114, v108
	s_waitcnt lgkmcnt(0)
	v_mov_b32_e32 v115, v110
	s_mul_i32 s16, s16, s27
	v_mul_f32_e32 v94, v38, v94
	v_mul_f32_e32 v95, v39, v95
	v_mul_f32_e32 v114, v44, v114
	v_mul_f32_e32 v115, v45, v115
	v_bfe_u32 v100, v97, 16, 1
	s_movk_i32 s17, 0x7fff
	v_bfe_u32 v106, v113, 16, 1
	s_sub_i32 s16, s26, s16
	v_bfe_u32 v40, v115, 16, 1
	v_add3_u32 v100, v97, v100, s17
	v_bfe_u32 v97, v94, 16, 1
	v_add3_u32 v106, v113, v106, s17
	s_lshl_b32 s16, s16, 5
	v_bfe_u32 v98, v114, 16, 1
	v_bfe_u32 v102, v96, 16, 1
	v_add3_u32 v40, v115, v40, s17
	v_bfe_u32 v104, v112, 16, 1
	v_add3_u32 v94, v94, v97, s17
	v_lshrrev_b32_e32 v97, 16, v106
	s_mov_b32 s3, 0xffff0000
	v_add3_u32 v102, v96, v102, s17
	v_add3_u32 v96, v114, v98, s17
	v_bfe_u32 v98, v95, 16, 1
	v_add3_u32 v104, v112, v104, s17
	v_and_or_b32 v97, v40, s3, v97
	v_or_b32_e32 v40, s16, v47
	v_add3_u32 v95, v95, v98, s17
	v_lshrrev_b32_e32 v98, 16, v104
	v_mad_i64_i32 v[112:113], s[18:19], v40, s29, 0
	v_and_or_b32 v96, v96, s3, v98
	v_lshl_add_u64 v[112:113], v[112:113], 1, s[0:1]
	s_lshl_b64 s[14:15], s[14:15], 1
	v_mov_b32_e32 v98, v41
	v_mov_b32_e32 v110, v109
	v_lshrrev_b32_e32 v94, 16, v94
	v_lshrrev_b32_e32 v95, 16, v95
	v_lshl_add_u64 v[112:113], v[112:113], 0, s[14:15]
	v_mul_f32_e32 v40, v38, v98
	v_mul_f32_e32 v41, v39, v99
	v_mul_f32_e32 v98, v44, v110
	v_mul_f32_e32 v99, v45, v111
	v_and_or_b32 v95, v100, s3, v95
	v_and_or_b32 v94, v102, s3, v94
	v_lshl_add_u64 v[112:113], v[112:113], 0, v[0:1]
	v_mov_b32_e32 v102, v101
	v_bfe_u32 v100, v99, 16, 1
	global_store_dwordx4 v[112:113], v[94:97], off
	v_bfe_u32 v101, v98, 16, 1
	v_add3_u32 v99, v99, v100, s17
	v_mul_f32_e32 v94, v36, v102
	v_mul_f32_e32 v95, v37, v103
	v_bfe_u32 v100, v40, 16, 1
	v_bfe_u32 v103, v94, 16, 1
	v_add3_u32 v98, v98, v101, s17
	v_bfe_u32 v101, v41, 16, 1
	v_add3_u32 v40, v40, v100, s17
	v_mov_b32_e32 v106, v105
	v_bfe_u32 v102, v95, 16, 1
	v_add3_u32 v94, v94, v103, s17
	v_add3_u32 v41, v41, v101, s17
	v_lshrrev_b32_e32 v40, 16, v40
	v_mul_f32_e32 v96, v34, v106
	v_mul_f32_e32 v97, v35, v107
	v_add3_u32 v95, v95, v102, s17
	v_lshrrev_b32_e32 v41, 16, v41
	v_and_or_b32 v94, v94, s3, v40
	v_or_b32_e32 v40, s16, v49
	v_bfe_u32 v102, v96, 16, 1
	v_bfe_u32 v103, v97, 16, 1
	v_and_or_b32 v95, v95, s3, v41
	v_mad_i64_i32 v[40:41], s[18:19], v40, s29, 0
	v_add3_u32 v97, v97, v103, s17
	v_add3_u32 v96, v96, v102, s17
	v_lshl_add_u64 v[40:41], v[40:41], 1, s[0:1]
	v_lshrrev_b32_e32 v96, 16, v96
	v_lshrrev_b32_e32 v97, 16, v97
	v_lshl_add_u64 v[40:41], v[40:41], 0, s[14:15]
	v_and_or_b32 v97, v99, s3, v97
	v_and_or_b32 v96, v98, s3, v96
	v_lshl_add_u64 v[40:41], v[40:41], 0, v[0:1]
	ds_read2_b32 v[98:99], v48 offset0:16 offset1:24
	ds_read2_b32 v[100:101], v48 offset0:82 offset1:90
	global_store_dwordx4 v[40:41], v[94:97], off
	ds_read2_b32 v[40:41], v48 offset0:49 offset1:57
	ds_read2_b32 v[102:103], v48 offset0:115 offset1:123
	ds_read2_b32 v[104:105], v48 offset0:148 offset1:156
	ds_read2_b32 v[106:107], v48 offset0:214 offset1:222
	ds_read2_b32 v[108:109], v48 offset0:181 offset1:189
	ds_read2_b32 v[110:111], v48 offset0:247 offset1:255
	s_waitcnt lgkmcnt(7)
; #define GAS __attribute__((address_space(1)))
; #define LAS __attribute__((address_space(3)))
; __device__ __forceinline__ unsigned pk2(float lo, float hi) { return f2bf(lo) | (f2bf(hi) << 16); }
; __device__ __forceinline__ void tr_finish(const TrItem& d, int lane, LAS float* scr, const float (&v)[32], const float keep) {
;     ...
;     for (int j = 0; j < 4; ++j) { const int n = (lane >> 3) + 8 * j; const LAS float* s = scr + (8 * c) * 33 + n;
;         v4u o; o.x = pk2(s[0 * 33] * g0[0], s[1 * 33] * g0[1]); o.y = pk2(s[2 * 33] * g0[2], s[3 * 33] * g0[3]); o.z = pk2(s[4 * 33] * g1[0], s[5 * 33] * g1[1]); o.w = pk2(s[6 * 33] * g1[2], s[7 * 33] * g1[3]);
;         *(GAS v4u*)(d.WT + (size_t)(n0 + n) * d.K + k0 + 8 * c) = o; }
; __device__ __forceinline__ void p0_prologue(Frame& F, const Ptrs& P) {
;     ...
;         const int l = it / I_LAYER; int r = it % I_LAYER;
;         unsigned char* wl = P.ws + WS_W + (size_t)l * W_LAYER;
;         if (r < I_IN) { d = TrItem{P.w_in + (size_t)l * DM * NIN, DM, NIN, P.attn_norm + l * DM, (bf16*)(wl + W_IN), r, NINP / 32, 0}; return; } r -= I_IN;
;         if (r < I_OUT) { d = TrItem{P.w_out + (size_t)l * DM * DM, DM, DM, P.out_gain + l * DM, (bf16*)(wl + W_OUT), r, DM / 32, 1}; return; } r -= I_OUT;
;         if (r < I_UP) { d = TrItem{P.w_up + (size_t)l * DM * FF, DM, FF, P.mlp_norm + l * DM, (bf16*)(wl + W_UP), r, FF / 32, 1}; return; } r -= I_UP;
;         d = TrItem{P.w_down + (size_t)l * FF * DM, FF, DM, nullptr, (bf16*)(wl + W_DOWN), r, DM / 32, 1};
	v_mov_b32_e32 v94, v98
	s_waitcnt lgkmcnt(5)
	v_mov_b32_e32 v96, v40
	s_waitcnt lgkmcnt(4)
	v_mov_b32_e32 v97, v102
	s_waitcnt lgkmcnt(3)
	v_mov_b32_e32 v112, v104
	s_waitcnt lgkmcnt(2)
	v_mov_b32_e32 v113, v106
	v_mov_b32_e32 v95, v100
	v_mul_f32_e32 v96, v36, v96
	v_mul_f32_e32 v97, v37, v97
	v_mul_f32_e32 v112, v34, v112
	v_mul_f32_e32 v113, v35, v113
	s_waitcnt lgkmcnt(1)
	v_mov_b32_e32 v114, v108
	s_waitcnt lgkmcnt(0)
	v_mov_b32_e32 v115, v110
	v_mul_f32_e32 v94, v38, v94
	v_mul_f32_e32 v95, v39, v95
	v_mul_f32_e32 v114, v44, v114
	v_mul_f32_e32 v115, v45, v115
	v_bfe_u32 v100, v97, 16, 1
	v_bfe_u32 v106, v113, 16, 1
	v_bfe_u32 v40, v115, 16, 1
	v_add3_u32 v100, v97, v100, s17
	v_bfe_u32 v97, v94, 16, 1
	v_add3_u32 v106, v113, v106, s17
	v_add3_u32 v40, v115, v40, s17
	v_add3_u32 v94, v94, v97, s17
	v_lshrrev_b32_e32 v97, 16, v106
	v_bfe_u32 v98, v114, 16, 1
	v_bfe_u32 v102, v96, 16, 1
	v_bfe_u32 v104, v112, 16, 1
	v_and_or_b32 v97, v40, s3, v97
	v_or_b32_e32 v40, s16, v50
	v_add3_u32 v102, v96, v102, s17
	v_add3_u32 v96, v114, v98, s17
	v_bfe_u32 v98, v95, 16, 1
	v_add3_u32 v104, v112, v104, s17
	v_mad_i64_i32 v[112:113], s[18:19], v40, s29, 0
	v_add3_u32 v95, v95, v98, s17
	v_lshrrev_b32_e32 v94, 16, v94
	v_lshl_add_u64 v[112:113], v[112:113], 1, s[0:1]
	v_lshrrev_b32_e32 v95, 16, v95
	v_lshrrev_b32_e32 v98, 16, v104
	v_and_or_b32 v94, v102, s3, v94
	v_lshl_add_u64 v[112:113], v[112:113], 0, s[14:15]
	v_mov_b32_e32 v102, v41
	v_mov_b32_e32 v110, v109
	v_and_or_b32 v96, v96, s3, v98
	v_and_or_b32 v95, v100, s3, v95
	v_lshl_add_u64 v[112:113], v[112:113], 0, v[0:1]
	v_mov_b32_e32 v100, v99
	v_mul_f32_e32 v36, v36, v102
	v_mul_f32_e32 v37, v37, v103
	v_mov_b32_e32 v106, v105
	v_mul_f32_e32 v40, v44, v110
	v_mul_f32_e32 v41, v45, v111
	global_store_dwordx4 v[112:113], v[94:97], off
	v_mul_f32_e32 v38, v38, v100
	v_mul_f32_e32 v39, v39, v101
	v_mul_f32_e32 v34, v34, v106
	v_mul_f32_e32 v35, v35, v107
	v_bfe_u32 v44, v41, 16, 1
	v_bfe_u32 v45, v40, 16, 1
	v_bfe_u32 v94, v37, 16, 1
	v_bfe_u32 v95, v36, 16, 1
	v_add3_u32 v95, v36, v95, s17
	v_add3_u32 v94, v37, v94, s17
	v_add3_u32 v36, v40, v45, s17
	v_add3_u32 v37, v41, v44, s17
	v_bfe_u32 v40, v38, 16, 1
	v_bfe_u32 v44, v34, 16, 1
	v_bfe_u32 v41, v39, 16, 1
	v_bfe_u32 v45, v35, 16, 1
	v_add3_u32 v34, v34, v44, s17
	v_add3_u32 v38, v38, v40, s17
	v_add3_u32 v35, v35, v45, s17
	v_add3_u32 v39, v39, v41, s17
	v_lshrrev_b32_e32 v38, 16, v38
	v_lshrrev_b32_e32 v34, 16, v34
	v_lshrrev_b32_e32 v39, 16, v39
	v_lshrrev_b32_e32 v35, 16, v35
	v_and_or_b32 v36, v36, s3, v34
	v_and_or_b32 v34, v95, s3, v38
	v_or_b32_e32 v38, s16, v51
	v_and_or_b32 v37, v37, s3, v35
	v_and_or_b32 v35, v94, s3, v39
	v_mad_i64_i32 v[38:39], s[16:17], v38, s29, 0
	v_lshl_add_u64 v[38:39], v[38:39], 1, s[0:1]
	v_lshl_add_u64 v[38:39], v[38:39], 0, s[14:15]
	v_lshl_add_u64 v[38:39], v[38:39], 0, v[0:1]
	global_store_dwordx4 v[38:39], v[34:37], off
	s_waitcnt lgkmcnt(0)
	s_andn2_b64 vcc, exec, s[12:13]
	s_mov_b64 s[12:13], -1
	s_cbranch_vccnz .LBB0_663
	s_add_i32 s12, s33, s38
	s_cmpk_gt_i32 s12, 0x31ff
	s_cbranch_scc1 .LBB0_660
	s_mul_hi_i32 s0, s12, 0x51eb851f
	s_lshr_b32 s1, s0, 31
	s_ashr_i32 s0, s0, 11
	s_add_i32 s20, s0, s1
	s_mul_i32 s0, s20, 0x1900
	s_sub_i32 s24, s12, s0
	s_ashr_i32 s21, s20, 31
	s_mul_i32 s1, s20, 0x1900000
	s_mul_hi_i32 s0, s20, 0x1900000
	s_add_u32 s18, s30, s1
	s_addc_u32 s19, s31, s0
	s_cmpk_lt_i32 s24, 0x700
	s_cselect_b64 s[16:17], -1, 0
	s_cmpk_gt_i32 s24, 0x6ff
	s_mov_b64 s[22:23], -1
	s_cbranch_scc0 .LBB0_705
	s_cmpk_gt_u32 s24, 0x8ff
	s_cbranch_scc0 .LBB0_702
	s_lshl_b64 s[4:5], s[20:21], 24
	s_cmpk_gt_u32 s24, 0x10ff
	s_mov_b64 s[14:15], -1
	s_cbranch_scc0 .LBB0_700
	v_readlane_b32 s40, v253, 2
	s_add_i32 s26, s24, 0xffffef00
	v_readlane_b32 s44, v253, 6
	v_readlane_b32 s45, v253, 7
	s_add_u32 s12, s44, s4
	s_addc_u32 s13, s45, s5
	s_add_u32 s0, s18, 0x1100000
	v_readlane_b32 s41, v253, 3
	v_readlane_b32 s42, v253, 4
	v_readlane_b32 s43, v253, 5
	v_readlane_b32 s46, v253, 8
	v_readlane_b32 s47, v253, 9
	s_addc_u32 s1, s19, 0
	s_mov_b64 s[14:15], 0
